# only the dead zero-init v_mov before fp8 pack pairs replaced by s_nop (no rider move)
# speedup vs baseline: 1.0020x; 1.0020x over previous
; DI unsigned pk4_fp8(float a, float b, float c, float d) { int r = 0; r = __builtin_amdgcn_cvt_pk_fp8_f32(a, b, r, false); r = __builtin_amdgcn_cvt_pk_fp8_f32(c, d, r, true); return (unsigned)r; }
; DI void phase_prep(unsigned char* lds, const Params& P, int G) {
;     ...
;       for (int u = blk; u < DEPTH * 64; u += G) { const int li = u >> 6, k0 = (u & 63) * 16;
;           for (int idx = tid; idx < 16 * 64; idx += 512) { const int row = idx >> 6, c4 = (idx & 63) * 4;
;               *(f32x4*)(wv + row * 256 + c4) = *(const f32x4*)(P.w_in + ((size_t)li * 1024 + k0 + row) * 2048 + 1024 + c4); }
;           __syncthreads();
;           const int ch = tid & 255, part = tid >> 8, g = ch >> 6, cp = ch & 63;
;           float acc[16];
; #pragma unroll
;           for (int kk = 0; kk < 16; ++kk) acc[kk] = 0.f;
;           const float* tw = part ? ls : lc;
;           for (int c = 0; c < 64; ++c) { const float t = tw[((c * cp) & 63) * 64];
; #pragma unroll
;               for (int kk = 0; kk < 16; ++kk) acc[kk] += wv[kk * 256 + 64 * g + c] * t; }
;           unsigned char* d = ws + WS_WCH + (size_t)li * SZ_WCH + (size_t)(256 + 256 * part + ch) * 1024 + k0;
;           { const float sc8 = 0.125f * W8_SCALE; u32x4 w;
;             w.x = pk4_fp8(acc[0] * sc8, acc[1] * sc8, acc[2] * sc8, acc[3] * sc8); w.y = pk4_fp8(acc[4] * sc8, acc[5] * sc8, acc[6] * sc8, acc[7] * sc8);
;             w.z = pk4_fp8(acc[8] * sc8, acc[9] * sc8, acc[10] * sc8, acc[11] * sc8); w.w = pk4_fp8(acc[12] * sc8, acc[13] * sc8, acc[14] * sc8, acc[15] * sc8);
;             *(u32x4*)d = w; }
;           __syncthreads(); } }
.LBB0_101:
	v_add_u32_e32 v88, s11, v25
	v_and_b32_e32 v92, 0xf00, v4
	ds_read_b128 v[28:31], v88
	ds_read_b128 v[32:35], v88 offset:1024
	ds_read_b128 v[36:39], v88 offset:2048
	ds_read_b128 v[40:43], v88 offset:3072
	ds_read_b128 v[44:47], v88 offset:4096
	ds_read_b128 v[48:51], v88 offset:5120
	ds_read_b128 v[52:55], v88 offset:6144
	ds_read_b128 v[56:59], v88 offset:7168
	ds_read_b128 v[60:63], v88 offset:8192
	ds_read_b128 v[64:67], v88 offset:9216
	ds_read_b128 v[68:71], v88 offset:10240
	ds_read_b128 v[72:75], v88 offset:11264
	ds_read_b128 v[76:79], v88 offset:12288
	ds_read_b128 v[80:83], v88 offset:13312
	ds_read_b128 v[84:87], v88 offset:14336
	ds_read_b128 v[88:91], v88 offset:15360
	v_lshl_add_u32 v92, v92, 2, v1
	v_add_u32_e32 v93, v24, v4
	v_add_u32_e32 v94, v22, v4
	ds_read_b32 v92, v92
	v_add_u32_e32 v95, v27, v4
	v_and_b32_e32 v93, 0xfc0, v93
	v_and_b32_e32 v94, 0xf80, v94
	v_and_b32_e32 v95, 0xfc0, v95
	v_lshl_add_u32 v93, v93, 2, v1
	v_lshl_add_u32 v96, v94, 2, v1
	v_lshl_add_u32 v95, v95, 2, v1
	ds_read_b32 v94, v93
	ds_read_b32 v96, v96
	ds_read_b32 v98, v95
	s_waitcnt lgkmcnt(14)
	v_mov_b32_e32 v100, v28
	v_mov_b32_e32 v101, v32
	v_mov_b32_e32 v32, v29
	v_mov_b32_e32 v28, v30
	v_mov_b32_e32 v29, v34
	v_mov_b32_e32 v34, v31
	v_mov_b32_e32 v30, v36
	v_mov_b32_e32 v31, v40
	v_mov_b32_e32 v40, v37
	v_mov_b32_e32 v36, v38
	v_mov_b32_e32 v37, v42
	v_mov_b32_e32 v42, v39
	v_mov_b32_e32 v38, v44
	v_mov_b32_e32 v39, v48
	v_mov_b32_e32 v48, v45
	v_mov_b32_e32 v44, v46
	v_mov_b32_e32 v45, v50
	v_mov_b32_e32 v50, v47
	s_waitcnt lgkmcnt(13)
	v_mov_b32_e32 v46, v52
	s_waitcnt lgkmcnt(12)
	v_mov_b32_e32 v47, v56
	v_mov_b32_e32 v56, v53
	v_mov_b32_e32 v52, v54
	v_mov_b32_e32 v53, v58
	v_mov_b32_e32 v58, v55
	s_waitcnt lgkmcnt(11)
	v_mov_b32_e32 v54, v60
	s_waitcnt lgkmcnt(10)
	v_mov_b32_e32 v55, v64
	v_mov_b32_e32 v64, v61
	v_mov_b32_e32 v60, v62
	v_mov_b32_e32 v61, v66
	v_mov_b32_e32 v66, v63
	s_waitcnt lgkmcnt(9)
	v_mov_b32_e32 v62, v68
	s_waitcnt lgkmcnt(8)
	v_mov_b32_e32 v63, v72
	v_mov_b32_e32 v72, v69
	v_mov_b32_e32 v68, v70
	v_mov_b32_e32 v69, v74
	v_mov_b32_e32 v74, v71
	s_waitcnt lgkmcnt(7)
	v_mov_b32_e32 v70, v76
	s_waitcnt lgkmcnt(6)
	v_mov_b32_e32 v71, v80
	v_mov_b32_e32 v80, v77
	v_mov_b32_e32 v76, v78
	v_mov_b32_e32 v77, v82
	v_mov_b32_e32 v82, v79
	s_waitcnt lgkmcnt(5)
	v_mov_b32_e32 v78, v84
	s_waitcnt lgkmcnt(4)
	v_mov_b32_e32 v79, v88
	v_mov_b32_e32 v88, v85
	s_waitcnt lgkmcnt(3)
	v_pk_fma_f32 v[20:21], v[92:93], v[100:101], v[20:21] op_sel_hi:[0,1,1]
	v_pk_fma_f32 v[18:19], v[92:93], v[30:31], v[18:19] op_sel_hi:[0,1,1]
	v_pk_fma_f32 v[16:17], v[92:93], v[38:39], v[16:17] op_sel_hi:[0,1,1]
	v_pk_fma_f32 v[14:15], v[92:93], v[46:47], v[14:15] op_sel_hi:[0,1,1]
	v_pk_fma_f32 v[12:13], v[92:93], v[54:55], v[12:13] op_sel_hi:[0,1,1]
	v_pk_fma_f32 v[10:11], v[92:93], v[62:63], v[10:11] op_sel_hi:[0,1,1]
	v_pk_fma_f32 v[8:9], v[92:93], v[70:71], v[8:9] op_sel_hi:[0,1,1]
	v_pk_fma_f32 v[6:7], v[92:93], v[78:79], v[6:7] op_sel_hi:[0,1,1]
	v_mov_b32_e32 v84, v86
	v_mov_b32_e32 v85, v90
	s_waitcnt lgkmcnt(2)
	v_pk_fma_f32 v[20:21], v[94:95], v[32:33], v[20:21] op_sel_hi:[0,1,1]
	v_pk_fma_f32 v[18:19], v[94:95], v[40:41], v[18:19] op_sel_hi:[0,1,1]
	v_pk_fma_f32 v[16:17], v[94:95], v[48:49], v[16:17] op_sel_hi:[0,1,1]
	v_pk_fma_f32 v[14:15], v[94:95], v[56:57], v[14:15] op_sel_hi:[0,1,1]
	v_pk_fma_f32 v[12:13], v[94:95], v[64:65], v[12:13] op_sel_hi:[0,1,1]
	v_pk_fma_f32 v[10:11], v[94:95], v[72:73], v[10:11] op_sel_hi:[0,1,1]
	v_pk_fma_f32 v[8:9], v[94:95], v[80:81], v[8:9] op_sel_hi:[0,1,1]
	v_pk_fma_f32 v[6:7], v[94:95], v[88:89], v[6:7] op_sel_hi:[0,1,1]
	s_add_i32 s11, s11, 16
	v_mov_b32_e32 v90, v87
	s_waitcnt lgkmcnt(1)
	v_pk_fma_f32 v[20:21], v[96:97], v[28:29], v[20:21] op_sel_hi:[0,1,1]
	v_pk_fma_f32 v[18:19], v[96:97], v[36:37], v[18:19] op_sel_hi:[0,1,1]
	v_pk_fma_f32 v[16:17], v[96:97], v[44:45], v[16:17] op_sel_hi:[0,1,1]
	v_pk_fma_f32 v[14:15], v[96:97], v[52:53], v[14:15] op_sel_hi:[0,1,1]
	v_pk_fma_f32 v[12:13], v[96:97], v[60:61], v[12:13] op_sel_hi:[0,1,1]
	v_pk_fma_f32 v[10:11], v[96:97], v[68:69], v[10:11] op_sel_hi:[0,1,1]
	v_pk_fma_f32 v[8:9], v[96:97], v[76:77], v[8:9] op_sel_hi:[0,1,1]
	v_pk_fma_f32 v[6:7], v[96:97], v[84:85], v[6:7] op_sel_hi:[0,1,1]
	v_add_u32_e32 v4, v4, v26
	s_cmpk_eq_i32 s11, 0x100
	s_waitcnt lgkmcnt(0)
	v_pk_fma_f32 v[20:21], v[98:99], v[34:35], v[20:21] op_sel_hi:[0,1,1]
	v_pk_fma_f32 v[18:19], v[98:99], v[42:43], v[18:19] op_sel_hi:[0,1,1]
	v_pk_fma_f32 v[16:17], v[98:99], v[50:51], v[16:17] op_sel_hi:[0,1,1]
	v_pk_fma_f32 v[14:15], v[98:99], v[58:59], v[14:15] op_sel_hi:[0,1,1]
	v_pk_fma_f32 v[12:13], v[98:99], v[66:67], v[12:13] op_sel_hi:[0,1,1]
	v_pk_fma_f32 v[10:11], v[98:99], v[74:75], v[10:11] op_sel_hi:[0,1,1]
	v_pk_fma_f32 v[8:9], v[98:99], v[82:83], v[8:9] op_sel_hi:[0,1,1]
	v_pk_fma_f32 v[6:7], v[98:99], v[90:91], v[6:7] op_sel_hi:[0,1,1]
	s_cbranch_scc0 .LBB0_101
	v_mul_f32_e32 v4, 0x41000000, v20
	v_mul_f32_e32 v20, 0x41000000, v21
	v_mul_f32_e32 v21, 0x41000000, v18
	s_nop 0
	v_mul_f32_e32 v28, 0x41000000, v19
	v_cvt_pk_fp8_f32 v18, v4, v20
	v_mul_f32_e32 v4, 0x41000000, v16
	v_mul_f32_e32 v16, 0x41000000, v17
	s_nop 0
	v_cvt_pk_fp8_f32 v19, v4, v16
	v_mul_f32_e32 v4, 0x41000000, v14
	v_mul_f32_e32 v14, 0x41000000, v15
	s_nop 0
	v_cvt_pk_fp8_f32 v19, v4, v14 op_sel:[0,0,1]
	v_mul_f32_e32 v4, 0x41000000, v12
	v_mul_f32_e32 v12, 0x41000000, v13
	v_cvt_pk_fp8_f32 v18, v21, v28 op_sel:[0,0,1]
	v_cvt_pk_fp8_f32 v20, v4, v12
	v_mul_f32_e32 v4, 0x41000000, v8
	v_mul_f32_e32 v8, 0x41000000, v9
	s_nop 0
	v_cvt_pk_fp8_f32 v21, v4, v8
	v_mul_f32_e32 v10, 0x41000000, v10
	v_mul_f32_e32 v11, 0x41000000, v11
	v_mul_f32_e32 v4, 0x41000000, v6
	v_mul_f32_e32 v6, 0x41000000, v7
	s_ashr_i32 s11, s10, 31
	v_cvt_pk_fp8_f32 v20, v10, v11 op_sel:[0,0,1]
	v_cvt_pk_fp8_f32 v21, v4, v6 op_sel:[0,0,1]
	s_lshl_b64 s[10:11], s[10:11], 21
	v_lshl_add_u64 v[6:7], v[2:3], 0, s[10:11]
	s_add_i32 s29, s29, s3
	v_lshl_add_u64 v[6:7], v[6:7], 0, s[8:9]
	s_cmpk_gt_i32 s29, 0x7f
	global_store_dwordx4 v[6:7], v[18:21], off
	s_barrier
	s_cbranch_scc0 .LBB0_97
	v_mov_b32_e32 v1, v23

; DI int ld_tid() { int t = threadIdx.x; asm volatile("" : "+v"(t)); return t; }
; DI unsigned pk4_fp8(float a, float b, float c, float d) { int r = 0; r = __builtin_amdgcn_cvt_pk_fp8_f32(a, b, r, false); r = __builtin_amdgcn_cvt_pk_fp8_f32(c, d, r, true); return (unsigned)r; }
; DI float clamp448(float x) { return __builtin_amdgcn_fmed3f(x, -448.0f, 448.0f); }
; DI void modnorm_row(f32x4 (&v)[4], int lane, const float* g, const float* sh, const float* sc) {
;     float ss = 0.f;
; #pragma unroll
;     for (int j = 0; j < 4; ++j)
; #pragma unroll
;         for (int i = 0; i < 4; ++i) ss += v[j][i] * v[j][i];
;     ss = wave_sum(ss);
;     const float rinv = rsqrtf(ss * (1.0f / 1024.0f) + EPS);
; #pragma unroll
;     for (int j = 0; j < 4; ++j) { const int k = (j >> 1) * 512 + 8 * lane + 4 * (j & 1);
;         const f32x4 gg = *(const f32x4*)(g + k), s1 = *(const f32x4*)(sc + k), s0 = *(const f32x4*)(sh + k);
;         v[j] = v[j] * rinv * gg * (s1 + 1.0f) + s0; }
; }
; DI void store_row_bf16(bf16_t* hr, int lane, const f32x4 (&v)[4]) { store16(hr + 8 * lane, v[0], v[1]); store16(hr + 512 + 8 * lane, v[2], v[3]); }
; DI void store_row_fp8(unsigned char* hr, int lane, const f32x4 (&v)[4]) { u32x2 w0, w1;
;     w0.x = pk4_fp8(clamp448(v[0][0]), clamp448(v[0][1]), clamp448(v[0][2]), clamp448(v[0][3])); w0.y = pk4_fp8(clamp448(v[1][0]), clamp448(v[1][1]), clamp448(v[1][2]), clamp448(v[1][3]));
;     w1.x = pk4_fp8(clamp448(v[2][0]), clamp448(v[2][1]), clamp448(v[2][2]), clamp448(v[2][3])); w1.y = pk4_fp8(clamp448(v[3][0]), clamp448(v[3][1]), clamp448(v[3][2]), clamp448(v[3][3]));
;     *(u32x2*)(hr + 8 * lane) = w0; *(u32x2*)(hr + 512 + 8 * lane) = w1; }
; DI void phase_norm1(const Params& P, unsigned char* H, const float* mod0, int G) {
;     const int tid_ = ld_tid(); const int lane = tid_ & 63, gw = blockIdx.x * 8 + (tid_ >> 6);
;     for (int row = gw; row < NTOK; row += G * 8) {
;         const float* xr = row < NLAT ? P.x + (size_t)row * 1024 : P.ctx + (size_t)(row - NLAT) * 1024;
;         const float* md = mod0 + (row < NLAT ? (row >> 12) : 8) * 6144;
;         f32x4 v[4]; load_row(xr, lane, v);
;         modnorm_row(v, lane, P.norm1_g, md, md + 1024);
;         store_row_fp8(H + (size_t)row * 1024, lane, v);
;     }
; }
.LBB0_324:
	s_or_b64 exec, exec, s[20:21]
	v_lshl_add_u64 v[18:19], v[18:19], 0, v[12:13]
	global_load_dwordx4 v[28:31], v[18:19], off
	global_load_dwordx4 v[32:35], v[18:19], off offset:2064
	global_load_dwordx4 v[36:39], v[18:19], off offset:16
	global_load_dwordx4 v[40:43], v[18:19], off offset:2048
	v_min_i32_e32 v4, 0x8000, v2
	v_ashrrev_i32_e32 v4, 12, v4
	v_mul_i32_i24_e32 v18, 0x1800, v4
	v_ashrrev_i32_e32 v19, 31, v18
	v_lshl_add_u64 v[18:19], v[18:19], 2, s[10:11]
	v_lshl_add_u64 v[52:53], v[18:19], 0, s[18:19]
	v_lshl_add_u64 v[54:55], v[52:53], 0, v[12:13]
	global_load_dwordx4 v[44:47], v[54:55], off
	global_load_dwordx4 v[48:51], v[54:55], off offset:16
	v_lshl_add_u64 v[76:77], v[52:53], 0, v[14:15]
	global_load_dwordx4 v[52:55], v[76:77], off
	global_load_dwordx4 v[56:59], v[76:77], off offset:16
	global_load_dwordx4 v[60:63], v[6:7], off offset:16
	global_load_dwordx4 v[64:67], v[6:7], off
	global_load_dwordx4 v[68:71], v[6:7], off offset:2064
	global_load_dwordx4 v[72:75], v[6:7], off offset:2048
	v_lshl_add_u64 v[18:19], v[18:19], 0, v[12:13]
	global_load_dwordx4 v[76:79], v[18:19], off offset:16
	global_load_dwordx4 v[80:83], v[18:19], off
	global_load_dwordx4 v[84:87], v[18:19], off offset:2064
	global_load_dwordx4 v[88:91], v[18:19], off offset:2048
	v_lshl_add_u64 v[2:3], v[2:3], 0, s[12:13]
	v_lshlrev_b64 v[16:17], 10, v[16:17]
	v_lshl_add_u64 v[16:17], v[8:9], 0, v[16:17]
	v_lshl_add_u64 v[10:11], v[10:11], 0, s[14:15]
	s_waitcnt vmcnt(15)
	v_mul_f32_e32 v4, v29, v29
	v_fmac_f32_e32 v4, v28, v28
	v_fmac_f32_e32 v4, v30, v30
	v_fmac_f32_e32 v4, v31, v31
	s_waitcnt vmcnt(13)
	v_fmac_f32_e32 v4, v36, v36
	v_fmac_f32_e32 v4, v37, v37
	v_fmac_f32_e32 v4, v38, v38
	v_fmac_f32_e32 v4, v39, v39
	s_waitcnt vmcnt(12)
	v_fmac_f32_e32 v4, v40, v40
	v_fmac_f32_e32 v4, v41, v41
	v_fmac_f32_e32 v4, v42, v42
	v_pk_mul_f32 v[92:93], v[32:33], v[32:33]
	v_fmac_f32_e32 v4, v43, v43
	v_add_f32_e32 v4, v92, v4
	v_pk_mul_f32 v[18:19], v[34:35], v[34:35]
	v_add_f32_e32 v4, v93, v4
	v_add_f32_e32 v4, v18, v4
	v_add_f32_e32 v4, v19, v4
	ds_bpermute_b32 v18, v1, v4
	s_waitcnt vmcnt(11)
	v_pk_add_f32 v[46:47], v[46:47], 1.0 op_sel_hi:[1,0]
	v_pk_add_f32 v[44:45], v[44:45], 1.0 op_sel_hi:[1,0]
	s_waitcnt vmcnt(10)
	v_pk_add_f32 v[48:49], v[48:49], 1.0 op_sel_hi:[1,0]
	v_pk_add_f32 v[50:51], v[50:51], 1.0 op_sel_hi:[1,0]
	s_waitcnt lgkmcnt(0)
	v_add_f32_e32 v4, v4, v18
	ds_bpermute_b32 v18, v20, v4
	s_waitcnt vmcnt(9)
	v_pk_add_f32 v[52:53], v[52:53], 1.0 op_sel_hi:[1,0]
	s_waitcnt vmcnt(8)
	v_pk_add_f32 v[56:57], v[56:57], 1.0 op_sel_hi:[1,0]
	s_nop 0
	s_nop 0
	s_waitcnt lgkmcnt(0)
	v_add_f32_e32 v4, v4, v18
	ds_bpermute_b32 v18, v21, v4
	s_nop 0
	v_pk_add_f32 v[54:55], v[54:55], 1.0 op_sel_hi:[1,0]
	v_pk_add_f32 v[58:59], v[58:59], 1.0 op_sel_hi:[1,0]
	s_waitcnt lgkmcnt(0)
	v_add_f32_e32 v4, v4, v18
	ds_bpermute_b32 v27, v22, v4
	s_nop 0
	s_waitcnt lgkmcnt(0)
	v_add_f32_e32 v4, v4, v27
	ds_bpermute_b32 v27, v23, v4
	s_waitcnt lgkmcnt(0)
	v_add_f32_e32 v4, v4, v27
	ds_bpermute_b32 v27, v24, v4
	s_waitcnt lgkmcnt(0)
	v_add_f32_e32 v4, v4, v27
	v_fmamk_f32 v4, v4, 0x3a800000, v25
	v_mul_f32_e32 v27, 0x4b800000, v4
	v_cmp_gt_f32_e32 vcc, s22, v4
	s_nop 1
	v_cndmask_b32_e32 v4, v4, v27, vcc
	v_rsq_f32_e32 v4, v4
	s_nop 0
	v_mul_f32_e32 v27, 0x45800000, v4
	v_cndmask_b32_e32 v4, v4, v27, vcc
	v_pk_mul_f32 v[30:31], v[30:31], v[4:5] op_sel_hi:[1,0]
	v_pk_mul_f32 v[28:29], v[28:29], v[4:5] op_sel_hi:[1,0]
	v_pk_mul_f32 v[36:37], v[36:37], v[4:5] op_sel_hi:[1,0]
	v_pk_mul_f32 v[38:39], v[38:39], v[4:5] op_sel_hi:[1,0]
	v_pk_mul_f32 v[40:41], v[40:41], v[4:5] op_sel_hi:[1,0]
	v_pk_mul_f32 v[32:33], v[32:33], v[4:5] op_sel_hi:[1,0]
	s_waitcnt vmcnt(6)
	v_pk_mul_f32 v[28:29], v[64:65], v[28:29]
	v_pk_mul_f32 v[30:31], v[66:67], v[30:31]
	v_pk_mul_f32 v[36:37], v[60:61], v[36:37]
	v_pk_mul_f32 v[38:39], v[62:63], v[38:39]
	s_waitcnt vmcnt(4)
	v_pk_mul_f32 v[40:41], v[72:73], v[40:41]
	v_pk_mul_f32 v[32:33], v[68:69], v[32:33]
	s_waitcnt vmcnt(2)
	v_pk_fma_f32 v[30:31], v[46:47], v[30:31], v[82:83]
	v_pk_fma_f32 v[28:29], v[44:45], v[28:29], v[80:81]
	v_pk_fma_f32 v[36:37], v[48:49], v[36:37], v[76:77]
	v_pk_mul_f32 v[42:43], v[42:43], v[4:5] op_sel_hi:[1,0]
	v_pk_mul_f32 v[34:35], v[34:35], v[4:5] op_sel_hi:[1,0]
	v_pk_fma_f32 v[38:39], v[50:51], v[38:39], v[78:79]
	s_waitcnt vmcnt(0)
	v_pk_fma_f32 v[40:41], v[52:53], v[40:41], v[88:89]
	v_pk_fma_f32 v[32:33], v[56:57], v[32:33], v[84:85]
	v_med3_f32 v4, v28, s23, v26
	v_med3_f32 v27, v29, s23, v26
	v_med3_f32 v28, v30, s23, v26
	v_med3_f32 v29, v31, s23, v26
	v_med3_f32 v30, v36, s23, v26
	v_med3_f32 v31, v37, s23, v26
	v_med3_f32 v36, v38, s23, v26
	v_med3_f32 v37, v39, s23, v26
	v_med3_f32 v38, v40, s23, v26
	v_med3_f32 v39, v41, s23, v26
	v_med3_f32 v32, v32, s23, v26
	v_med3_f32 v33, v33, s23, v26
	v_cvt_pk_fp8_f32 v18, v4, v27
	v_cvt_pk_fp8_f32 v19, v30, v31
	v_cvt_pk_fp8_f32 v92, v38, v39
	v_cvt_pk_fp8_f32 v93, v32, v33
	v_pk_mul_f32 v[42:43], v[74:75], v[42:43]
	v_pk_mul_f32 v[34:35], v[70:71], v[34:35]
	v_pk_fma_f32 v[42:43], v[54:55], v[42:43], v[90:91]
	v_pk_fma_f32 v[34:35], v[58:59], v[34:35], v[86:87]
	v_med3_f32 v40, v42, s23, v26
	v_med3_f32 v41, v43, s23, v26
	v_med3_f32 v34, v34, s23, v26
	v_med3_f32 v35, v35, s23, v26
	v_cvt_pk_fp8_f32 v18, v28, v29 op_sel:[0,0,1]
	v_cvt_pk_fp8_f32 v19, v36, v37 op_sel:[0,0,1]
	v_cvt_pk_fp8_f32 v92, v40, v41 op_sel:[0,0,1]
	v_cvt_pk_fp8_f32 v93, v34, v35 op_sel:[0,0,1]
	v_cmp_lt_i32_e32 vcc, s24, v2
	s_or_b64 s[16:17], vcc, s[16:17]
	global_store_dwordx2 v[16:17], v[18:19], off
	global_store_dwordx2 v[16:17], v[92:93], off offset:512
	s_andn2_b64 exec, exec, s[16:17]
	s_cbranch_execz .LBB0_327

; #define LAS __attribute__((address_space(3)))
; DI unsigned pk4_fp8(float a, float b, float c, float d) { int r = 0; r = __builtin_amdgcn_cvt_pk_fp8_f32(a, b, r, false); r = __builtin_amdgcn_cvt_pk_fp8_f32(c, d, r, true); return (unsigned)r; }
;     DI void head32x2(const AccT& acc, int rbase, int wc, int fq, bf16_t* dst, const float* gain, float scale, const bool F8) const {
;         LAS const float* cs8 = rope + 2 * 65 * 16; LAS const float* sn8 = cs8 + 65 * 8;
;         const int dbase = 16 * (fq >> 1) + 4 * (fq & 1);
;         const f32x4 g0 = *(const f32x4*)(gain + dbase), g1 = *(const f32x4*)(gain + dbase + 8);
; #pragma unroll
;         for (int ai = 0; ai < 2; ++ai)
; #pragma unroll
;             for (int m = 0; m < 4; ++m) {
;                 const int row = rbase + 128 * ai + 16 * m;
;                 const bool lat = row < NLAT; const int t = row & (SEQ - 1);
;                 const int pos = lat ? ((fq >> 1) ? (t & 63) : (t >> 6)) : 64;
;                 const f32x4 c = *(LAS const f32x4*)(cs8 + pos * 8 + 4 * (fq & 1)), sn = *(LAS const f32x4*)(sn8 + pos * 8 + 4 * (fq & 1));
; #pragma unroll
;                 for (int bj = 0; bj < 2; ++bj) {
;                     float ss = 0.f;
; #pragma unroll
;                     for (int n = 0; n < 2; ++n)
; #pragma unroll
;                         for (int i = 0; i < 4; ++i) ss += acc[ai][bj][m][n][i] * acc[ai][bj][m][n][i];
;                     ss = sum_x16_x32(ss);
;                     const float rinv = __builtin_amdgcn_rsqf(ss * (W8_INV * W8_INV / 32.0f) + EPS) * (scale * W8_INV);
;                     const f32x4 x1 = acc[ai][bj][m][0] * rinv * g0, x2 = acc[ai][bj][m][1] * rinv * g1;
;                     if (F8) { unsigned char* p8 = (unsigned char*)dst + (size_t)row * 256 + wc * 64 + 32 * bj + dbase; const f32x4 y1 = x1 * c - x2 * sn, y2 = x1 * sn + x2 * c;
;                         *(unsigned*)p8 = pk4_fp8(y1[0], y1[1], y1[2], y1[3]); *(unsigned*)(p8 + 8) = pk4_fp8(y2[0], y2[1], y2[2], y2[3]); }
.LBB0_415:
	s_load_dwordx2 s[4:5], s[4:5], 0x0
	v_lshlrev_b32_e32 v131, 2, v158
	v_lshlrev_b32_e32 v130, 3, v158
	v_and_b32_e32 v138, 4, v131
	v_and_or_b32 v148, v130, -16, v138
	v_ashrrev_i32_e32 v149, 31, v148
	s_waitcnt lgkmcnt(0)
	v_lshl_add_u64 v[130:131], v[148:149], 2, s[4:5]
	global_load_dwordx4 v[134:137], v[130:131], off
	s_nop 0
	global_load_dwordx4 v[130:133], v[130:131], off offset:32
	v_mul_f32_e32 v152, v127, v127
	v_fmac_f32_e32 v152, v126, v126
	v_fmac_f32_e32 v152, v128, v128
	v_fmac_f32_e32 v152, v129, v129
	v_fmac_f32_e32 v152, v122, v122
	v_fmac_f32_e32 v152, v123, v123
	v_fmac_f32_e32 v152, v124, v124
	s_and_b64 s[52:53], exec, s[52:53]
	v_fmac_f32_e32 v152, v125, v125
	v_lshlrev_b32_e32 v138, 2, v138
	v_readlane_b32 s52, v254, 4
	v_mov_b32_e32 v153, v152
	s_nop 1
	v_permlane16_swap_b32_e32 v152, v153
	v_add_u32_e32 v174, s52, v138
	v_readlane_b32 s52, v254, 5
	v_cmp_gt_u32_e64 s[4:5], 2, v158
	v_add_f32_e32 v152, v152, v153
	v_add_u32_e32 v175, s52, v138
	v_lshrrev_b32_e32 v138, 6, v160
	v_cndmask_b32_e64 v138, v190, v138, s[4:5]
	v_mov_b32_e32 v153, v152
	v_lshlrev_b32_e32 v138, 3, v138
	s_nop 0
	v_permlane32_swap_b32_e32 v152, v153
	v_cmp_gt_i32_e32 vcc, s80, v160
	v_and_b32_e32 v138, 0x1f8, v138
	v_add_f32_e32 v152, v152, v153
	s_mov_b32 s41, 0x25054000
	v_cndmask_b32_e32 v138, v188, v138, vcc
	v_fmamk_f32 v152, v152, 0x37000000, v187
	s_cselect_b32 s41, s41, 0x26154000
	v_lshlrev_b32_e32 v138, 2, v138
	v_rsq_f32_e32 v152, v152
	s_add_u32 s41, s10, s41
	v_add_u32_e32 v139, v174, v138
	v_add_u32_e32 v138, v175, v138
	s_addc_u32 s55, s11, 0
	s_lshl_b32 s52, s81, 1
	ds_read_b128 v[142:145], v139
	ds_read_b128 v[138:141], v138
	s_add_u32 s52, s41, s52
	s_addc_u32 s53, s55, 0
	v_mul_f32_e32 v164, s40, v152
	s_add_u32 s54, s41, s81
	v_pk_mul_f32 v[166:167], v[124:125], v[164:165] op_sel_hi:[1,0]
	v_pk_mul_f32 v[168:169], v[122:123], v[164:165] op_sel_hi:[1,0]
	s_addc_u32 s55, s55, 0
	v_ashrrev_i32_e32 v161, 31, v160
	v_pk_mul_f32 v[152:153], v[128:129], v[164:165] op_sel_hi:[1,0]
	v_pk_mul_f32 v[162:163], v[126:127], v[164:165] op_sel_hi:[1,0]
	v_lshl_add_u64 v[146:147], s[54:55], 0, v[148:149]
	v_lshlrev_b64 v[150:151], 8, v[160:161]
	v_lshl_add_u64 v[150:151], v[146:147], 0, v[150:151]
	s_mov_b64 s[54:55], -1
	s_andn2_b64 vcc, exec, s[6:7]
	s_waitcnt vmcnt(0)
	v_pk_mul_f32 v[152:153], v[136:137], v[152:153]
	v_pk_mul_f32 v[164:165], v[132:133], v[166:167]
	v_pk_mul_f32 v[170:171], v[130:131], v[168:169]
	v_pk_mul_f32 v[162:163], v[134:135], v[162:163]
	s_waitcnt lgkmcnt(0)
	v_pk_mul_f32 v[166:167], v[140:141], v[164:165]
	v_pk_mul_f32 v[168:169], v[138:139], v[170:171]
	v_pk_fma_f32 v[166:167], v[144:145], v[152:153], v[166:167] neg_lo:[0,0,1] neg_hi:[0,0,1]
	v_pk_fma_f32 v[168:169], v[142:143], v[162:163], v[168:169] neg_lo:[0,0,1] neg_hi:[0,0,1]
	v_pk_mul_f32 v[172:173], v[142:143], v[170:171]
	s_cbranch_vccnz .LBB0_417
	s_nop 0
	v_cvt_pk_fp8_f32 v178, v168, v169
	v_pk_fma_f32 v[176:177], v[138:139], v[162:163], v[172:173]
	v_pk_mul_f32 v[170:171], v[144:145], v[164:165]
	s_mov_b64 s[54:55], 0
	v_cvt_pk_fp8_f32 v178, v166, v167 op_sel:[0,0,1]
	v_pk_fma_f32 v[170:171], v[140:141], v[152:153], v[170:171]
	global_store_dword v[150:151], v178, off
	s_nop 0
	v_cvt_pk_fp8_f32 v178, v176, v177
	v_cvt_pk_fp8_f32 v178, v170, v171 op_sel:[0,0,1]
	global_store_dword v[150:151], v178, off offset:8

; DI unsigned pk4_fp8(float a, float b, float c, float d) { int r = 0; r = __builtin_amdgcn_cvt_pk_fp8_f32(a, b, r, false); r = __builtin_amdgcn_cvt_pk_fp8_f32(c, d, r, true); return (unsigned)r; }
; DI void store8(bf16_t* p, f32x4 a) { u32x2 w; w.x = pk2(a[0], a[1]); w.y = pk2(a[2], a[3]); *(u32x2*)p = w; }
;     DI void head32x2(const AccT& acc, int rbase, int wc, int fq, bf16_t* dst, const float* gain, float scale, const bool F8) const {
;     ...
;                 for (int bj = 0; bj < 2; ++bj) {
;                     float ss = 0.f;
; #pragma unroll
;                     for (int n = 0; n < 2; ++n)
; #pragma unroll
;                         for (int i = 0; i < 4; ++i) ss += acc[ai][bj][m][n][i] * acc[ai][bj][m][n][i];
;                     ss = sum_x16_x32(ss);
;                     const float rinv = __builtin_amdgcn_rsqf(ss * (W8_INV * W8_INV / 32.0f) + EPS) * (scale * W8_INV);
;                     const f32x4 x1 = acc[ai][bj][m][0] * rinv * g0, x2 = acc[ai][bj][m][1] * rinv * g1;
;                     if (F8) { unsigned char* p8 = (unsigned char*)dst + (size_t)row * 256 + wc * 64 + 32 * bj + dbase; const f32x4 y1 = x1 * c - x2 * sn, y2 = x1 * sn + x2 * c;
;                         *(unsigned*)p8 = pk4_fp8(y1[0], y1[1], y1[2], y1[3]); *(unsigned*)(p8 + 8) = pk4_fp8(y2[0], y2[1], y2[2], y2[3]); }
;                     else { bf16_t* p = dst + (size_t)row * 256 + wc * 64 + 32 * bj + dbase;
;                         store8(p, x1 * c - x2 * sn); store8(p + 8, x1 * sn + x2 * c); }
.LBB0_419:
	v_mul_f32_e32 v152, v119, v119
	v_fmac_f32_e32 v152, v118, v118
	v_fmac_f32_e32 v152, v120, v120
	v_fmac_f32_e32 v152, v121, v121
	v_fmac_f32_e32 v152, v114, v114
	v_fmac_f32_e32 v152, v115, v115
	v_fmac_f32_e32 v152, v116, v116
	v_fmac_f32_e32 v152, v117, v117
	v_mov_b32_e32 v153, v152
	s_nop 1
	v_permlane16_swap_b32_e32 v152, v153
	v_add_f32_e32 v152, v152, v153
	v_mov_b32_e32 v153, v152
	s_nop 1
	v_permlane32_swap_b32_e32 v152, v153
	v_add_f32_e32 v152, v152, v153
	v_fmamk_f32 v152, v152, 0x37000000, v187
	v_rsq_f32_e32 v152, v152
	s_mov_b64 s[52:53], -1
	s_and_b64 vcc, exec, s[6:7]
	v_mul_f32_e32 v164, s40, v152
	v_pk_mul_f32 v[166:167], v[116:117], v[164:165] op_sel_hi:[1,0]
	v_pk_mul_f32 v[168:169], v[114:115], v[164:165] op_sel_hi:[1,0]
	v_pk_mul_f32 v[152:153], v[120:121], v[164:165] op_sel_hi:[1,0]
	v_pk_mul_f32 v[162:163], v[118:119], v[164:165] op_sel_hi:[1,0]
	v_pk_mul_f32 v[164:165], v[132:133], v[166:167]
	v_pk_mul_f32 v[172:173], v[130:131], v[168:169]
	v_pk_mul_f32 v[152:153], v[136:137], v[152:153]
	v_pk_mul_f32 v[162:163], v[134:135], v[162:163]
	v_pk_mul_f32 v[166:167], v[140:141], v[164:165]
	v_pk_mul_f32 v[168:169], v[138:139], v[172:173]
	v_pk_fma_f32 v[166:167], v[144:145], v[152:153], v[166:167] neg_lo:[0,0,1] neg_hi:[0,0,1]
	v_pk_fma_f32 v[168:169], v[142:143], v[162:163], v[168:169] neg_lo:[0,0,1] neg_hi:[0,0,1]
	v_pk_mul_f32 v[142:143], v[142:143], v[172:173]
	s_cbranch_vccz .LBB0_421
	s_nop 0
	v_cvt_pk_fp8_f32 v161, v168, v169
	v_pk_fma_f32 v[176:177], v[138:139], v[162:163], v[142:143]
	v_pk_mul_f32 v[172:173], v[144:145], v[164:165]
	s_mov_b64 s[52:53], 0
	v_cvt_pk_fp8_f32 v161, v166, v167 op_sel:[0,0,1]
	v_pk_fma_f32 v[172:173], v[140:141], v[152:153], v[172:173]
	global_store_dword v[150:151], v161, off offset:32
	s_nop 0
	v_cvt_pk_fp8_f32 v161, v176, v177
	v_cvt_pk_fp8_f32 v161, v172, v173 op_sel:[0,0,1]
	global_store_dword v[150:151], v161, off offset:40

; #define LAS __attribute__((address_space(3)))
; DI unsigned pk4_fp8(float a, float b, float c, float d) { int r = 0; r = __builtin_amdgcn_cvt_pk_fp8_f32(a, b, r, false); r = __builtin_amdgcn_cvt_pk_fp8_f32(c, d, r, true); return (unsigned)r; }
; DI void store8(bf16_t* p, f32x4 a) { u32x2 w; w.x = pk2(a[0], a[1]); w.y = pk2(a[2], a[3]); *(u32x2*)p = w; }
;     DI void head32x2(const AccT& acc, int rbase, int wc, int fq, bf16_t* dst, const float* gain, float scale, const bool F8) const {
;     ...
;             for (int m = 0; m < 4; ++m) {
;                 const int row = rbase + 128 * ai + 16 * m;
;                 const bool lat = row < NLAT; const int t = row & (SEQ - 1);
;                 const int pos = lat ? ((fq >> 1) ? (t & 63) : (t >> 6)) : 64;
;                 const f32x4 c = *(LAS const f32x4*)(cs8 + pos * 8 + 4 * (fq & 1)), sn = *(LAS const f32x4*)(sn8 + pos * 8 + 4 * (fq & 1));
; #pragma unroll
;                 for (int bj = 0; bj < 2; ++bj) {
;                     float ss = 0.f;
; #pragma unroll
;                     for (int n = 0; n < 2; ++n)
; #pragma unroll
;                         for (int i = 0; i < 4; ++i) ss += acc[ai][bj][m][n][i] * acc[ai][bj][m][n][i];
;                     ss = sum_x16_x32(ss);
;                     const float rinv = __builtin_amdgcn_rsqf(ss * (W8_INV * W8_INV / 32.0f) + EPS) * (scale * W8_INV);
;                     const f32x4 x1 = acc[ai][bj][m][0] * rinv * g0, x2 = acc[ai][bj][m][1] * rinv * g1;
;                     if (F8) { unsigned char* p8 = (unsigned char*)dst + (size_t)row * 256 + wc * 64 + 32 * bj + dbase; const f32x4 y1 = x1 * c - x2 * sn, y2 = x1 * sn + x2 * c;
;                         *(unsigned*)p8 = pk4_fp8(y1[0], y1[1], y1[2], y1[3]); *(unsigned*)(p8 + 8) = pk4_fp8(y2[0], y2[1], y2[2], y2[3]); }
;                     else { bf16_t* p = dst + (size_t)row * 256 + wc * 64 + 32 * bj + dbase;
;                         store8(p, x1 * c - x2 * sn); store8(p + 8, x1 * sn + x2 * c); }
.LBB0_423:
	v_mul_f32_e32 v150, v111, v111
	v_fmac_f32_e32 v150, v110, v110
	v_fmac_f32_e32 v150, v112, v112
	v_fmac_f32_e32 v150, v113, v113
	v_fmac_f32_e32 v150, v106, v106
	v_fmac_f32_e32 v150, v107, v107
	v_fmac_f32_e32 v150, v108, v108
	v_fmac_f32_e32 v150, v109, v109
	v_mov_b32_e32 v151, v150
	v_add_u32_e32 v152, 16, v160
	s_nop 0
	v_permlane16_swap_b32_e32 v150, v151
	v_lshrrev_b32_e32 v138, 6, v152
	v_add_f32_e32 v150, v150, v151
	v_cndmask_b32_e64 v138, v152, v138, s[4:5]
	v_mov_b32_e32 v151, v150
	v_lshlrev_b32_e32 v138, 3, v138
	s_nop 0
	v_permlane32_swap_b32_e32 v150, v151
	v_and_b32_e32 v138, 0x1f8, v138
	v_cmp_gt_i32_e32 vcc, s85, v160
	v_add_f32_e32 v150, v150, v151
	v_fmamk_f32 v150, v150, 0x37000000, v187
	v_cndmask_b32_e32 v138, v188, v138, vcc
	v_lshlrev_b32_e32 v138, 2, v138
	v_rsq_f32_e32 v161, v150
	v_add_u32_e32 v139, v174, v138
	v_add_u32_e32 v138, v175, v138
	ds_read_b128 v[142:145], v139
	ds_read_b128 v[138:141], v138
	v_mul_f32_e32 v166, s40, v161
	v_pk_mul_f32 v[168:169], v[108:109], v[166:167] op_sel_hi:[1,0]
	v_pk_mul_f32 v[170:171], v[106:107], v[166:167] op_sel_hi:[1,0]
	v_ashrrev_i32_e32 v153, 31, v152
	v_pk_mul_f32 v[162:163], v[112:113], v[166:167] op_sel_hi:[1,0]
	v_pk_mul_f32 v[164:165], v[110:111], v[166:167] op_sel_hi:[1,0]
	v_pk_mul_f32 v[166:167], v[132:133], v[168:169]
	v_pk_mul_f32 v[168:169], v[130:131], v[170:171]
	v_lshlrev_b64 v[150:151], 8, v[152:153]
	v_pk_mul_f32 v[162:163], v[136:137], v[162:163]
	v_pk_mul_f32 v[164:165], v[134:135], v[164:165]
	s_waitcnt lgkmcnt(0)
	v_pk_mul_f32 v[170:171], v[140:141], v[166:167]
	v_pk_mul_f32 v[172:173], v[138:139], v[168:169]
	v_lshl_add_u64 v[150:151], v[146:147], 0, v[150:151]
	v_pk_fma_f32 v[170:171], v[144:145], v[162:163], v[170:171] neg_lo:[0,0,1] neg_hi:[0,0,1]
	v_pk_fma_f32 v[172:173], v[142:143], v[164:165], v[172:173] neg_lo:[0,0,1] neg_hi:[0,0,1]
	s_mov_b64 s[52:53], -1
	s_and_b64 vcc, exec, s[6:7]
	v_pk_mul_f32 v[168:169], v[142:143], v[168:169]
	s_cbranch_vccz .LBB0_425
	s_nop 0
	v_cvt_pk_fp8_f32 v161, v172, v173
	v_pk_fma_f32 v[178:179], v[138:139], v[164:165], v[168:169]
	v_pk_mul_f32 v[176:177], v[144:145], v[166:167]
	s_mov_b64 s[52:53], 0
	v_cvt_pk_fp8_f32 v161, v170, v171 op_sel:[0,0,1]
	v_pk_fma_f32 v[176:177], v[140:141], v[162:163], v[176:177]
	global_store_dword v[150:151], v161, off
	s_nop 0
	v_cvt_pk_fp8_f32 v161, v178, v179
	v_cvt_pk_fp8_f32 v161, v176, v177 op_sel:[0,0,1]
	global_store_dword v[150:151], v161, off offset:8

; DI unsigned pk4_fp8(float a, float b, float c, float d) { int r = 0; r = __builtin_amdgcn_cvt_pk_fp8_f32(a, b, r, false); r = __builtin_amdgcn_cvt_pk_fp8_f32(c, d, r, true); return (unsigned)r; }
; DI void store8(bf16_t* p, f32x4 a) { u32x2 w; w.x = pk2(a[0], a[1]); w.y = pk2(a[2], a[3]); *(u32x2*)p = w; }
;     DI void head32x2(const AccT& acc, int rbase, int wc, int fq, bf16_t* dst, const float* gain, float scale, const bool F8) const {
;     ...
;                 for (int bj = 0; bj < 2; ++bj) {
;                     float ss = 0.f;
; #pragma unroll
;                     for (int n = 0; n < 2; ++n)
; #pragma unroll
;                         for (int i = 0; i < 4; ++i) ss += acc[ai][bj][m][n][i] * acc[ai][bj][m][n][i];
;                     ss = sum_x16_x32(ss);
;                     const float rinv = __builtin_amdgcn_rsqf(ss * (W8_INV * W8_INV / 32.0f) + EPS) * (scale * W8_INV);
;                     const f32x4 x1 = acc[ai][bj][m][0] * rinv * g0, x2 = acc[ai][bj][m][1] * rinv * g1;
;                     if (F8) { unsigned char* p8 = (unsigned char*)dst + (size_t)row * 256 + wc * 64 + 32 * bj + dbase; const f32x4 y1 = x1 * c - x2 * sn, y2 = x1 * sn + x2 * c;
;                         *(unsigned*)p8 = pk4_fp8(y1[0], y1[1], y1[2], y1[3]); *(unsigned*)(p8 + 8) = pk4_fp8(y2[0], y2[1], y2[2], y2[3]); }
;                     else { bf16_t* p = dst + (size_t)row * 256 + wc * 64 + 32 * bj + dbase;
;                         store8(p, x1 * c - x2 * sn); store8(p + 8, x1 * sn + x2 * c); }
.LBB0_427:
	v_mul_f32_e32 v161, v103, v103
	v_fmac_f32_e32 v161, v102, v102
	v_fmac_f32_e32 v161, v104, v104
	v_fmac_f32_e32 v161, v105, v105
	v_fmac_f32_e32 v161, v98, v98
	v_fmac_f32_e32 v161, v99, v99
	v_fmac_f32_e32 v161, v100, v100
	v_fmac_f32_e32 v161, v101, v101
	v_mov_b32_e32 v162, v161
	s_nop 1
	v_permlane16_swap_b32_e32 v161, v162
	v_add_f32_e32 v161, v161, v162
	v_mov_b32_e32 v162, v161
	s_nop 1
	v_permlane32_swap_b32_e32 v161, v162
	v_add_f32_e32 v161, v161, v162
	v_fmamk_f32 v161, v161, 0x37000000, v187
	v_rsq_f32_e32 v161, v161
	s_mov_b64 s[52:53], -1
	s_and_b64 vcc, exec, s[6:7]
	v_mul_f32_e32 v166, s40, v161
	v_pk_mul_f32 v[168:169], v[100:101], v[166:167] op_sel_hi:[1,0]
	v_pk_mul_f32 v[170:171], v[98:99], v[166:167] op_sel_hi:[1,0]
	v_pk_mul_f32 v[162:163], v[104:105], v[166:167] op_sel_hi:[1,0]
	v_pk_mul_f32 v[164:165], v[102:103], v[166:167] op_sel_hi:[1,0]
	v_pk_mul_f32 v[166:167], v[132:133], v[168:169]
	v_pk_mul_f32 v[172:173], v[130:131], v[170:171]
	v_pk_mul_f32 v[162:163], v[136:137], v[162:163]
	v_pk_mul_f32 v[164:165], v[134:135], v[164:165]
	v_pk_mul_f32 v[168:169], v[140:141], v[166:167]
	v_pk_mul_f32 v[170:171], v[138:139], v[172:173]
	v_pk_fma_f32 v[168:169], v[144:145], v[162:163], v[168:169] neg_lo:[0,0,1] neg_hi:[0,0,1]
	v_pk_fma_f32 v[170:171], v[142:143], v[164:165], v[170:171] neg_lo:[0,0,1] neg_hi:[0,0,1]
	v_pk_mul_f32 v[142:143], v[142:143], v[172:173]
	s_cbranch_vccz .LBB0_429
	s_nop 0
	v_cvt_pk_fp8_f32 v161, v170, v171
	v_pk_fma_f32 v[176:177], v[138:139], v[164:165], v[142:143]
	v_pk_mul_f32 v[172:173], v[144:145], v[166:167]
	s_mov_b64 s[52:53], 0
	v_cvt_pk_fp8_f32 v161, v168, v169 op_sel:[0,0,1]
	v_pk_fma_f32 v[172:173], v[140:141], v[162:163], v[172:173]
	global_store_dword v[150:151], v161, off offset:32
	s_nop 0
	v_cvt_pk_fp8_f32 v161, v176, v177
	v_cvt_pk_fp8_f32 v161, v172, v173 op_sel:[0,0,1]
	global_store_dword v[150:151], v161, off offset:40

; #define LAS __attribute__((address_space(3)))
; DI unsigned pk4_fp8(float a, float b, float c, float d) { int r = 0; r = __builtin_amdgcn_cvt_pk_fp8_f32(a, b, r, false); r = __builtin_amdgcn_cvt_pk_fp8_f32(c, d, r, true); return (unsigned)r; }
; DI void store8(bf16_t* p, f32x4 a) { u32x2 w; w.x = pk2(a[0], a[1]); w.y = pk2(a[2], a[3]); *(u32x2*)p = w; }
;     DI void head32x2(const AccT& acc, int rbase, int wc, int fq, bf16_t* dst, const float* gain, float scale, const bool F8) const {
;     ...
;             for (int m = 0; m < 4; ++m) {
;                 const int row = rbase + 128 * ai + 16 * m;
;                 const bool lat = row < NLAT; const int t = row & (SEQ - 1);
;                 const int pos = lat ? ((fq >> 1) ? (t & 63) : (t >> 6)) : 64;
;                 const f32x4 c = *(LAS const f32x4*)(cs8 + pos * 8 + 4 * (fq & 1)), sn = *(LAS const f32x4*)(sn8 + pos * 8 + 4 * (fq & 1));
; #pragma unroll
;                 for (int bj = 0; bj < 2; ++bj) {
;                     float ss = 0.f;
; #pragma unroll
;                     for (int n = 0; n < 2; ++n)
; #pragma unroll
;                         for (int i = 0; i < 4; ++i) ss += acc[ai][bj][m][n][i] * acc[ai][bj][m][n][i];
;                     ss = sum_x16_x32(ss);
;                     const float rinv = __builtin_amdgcn_rsqf(ss * (W8_INV * W8_INV / 32.0f) + EPS) * (scale * W8_INV);
;                     const f32x4 x1 = acc[ai][bj][m][0] * rinv * g0, x2 = acc[ai][bj][m][1] * rinv * g1;
;                     if (F8) { unsigned char* p8 = (unsigned char*)dst + (size_t)row * 256 + wc * 64 + 32 * bj + dbase; const f32x4 y1 = x1 * c - x2 * sn, y2 = x1 * sn + x2 * c;
;                         *(unsigned*)p8 = pk4_fp8(y1[0], y1[1], y1[2], y1[3]); *(unsigned*)(p8 + 8) = pk4_fp8(y2[0], y2[1], y2[2], y2[3]); }
;                     else { bf16_t* p = dst + (size_t)row * 256 + wc * 64 + 32 * bj + dbase;
;                         store8(p, x1 * c - x2 * sn); store8(p + 8, x1 * sn + x2 * c); }
.LBB0_431:
	v_mul_f32_e32 v150, v95, v95
	v_fmac_f32_e32 v150, v94, v94
	v_fmac_f32_e32 v150, v96, v96
	v_fmac_f32_e32 v150, v97, v97
	v_fmac_f32_e32 v150, v90, v90
	v_fmac_f32_e32 v150, v91, v91
	v_fmac_f32_e32 v150, v92, v92
	v_fmac_f32_e32 v150, v93, v93
	v_mov_b32_e32 v151, v150
	v_add_u32_e32 v152, 32, v160
	s_nop 0
	v_permlane16_swap_b32_e32 v150, v151
	v_lshrrev_b32_e32 v138, 6, v152
	v_add_f32_e32 v150, v150, v151
	v_cndmask_b32_e64 v138, v152, v138, s[4:5]
	v_mov_b32_e32 v151, v150
	v_lshlrev_b32_e32 v138, 3, v138
	s_nop 0
	v_permlane32_swap_b32_e32 v150, v151
	v_and_b32_e32 v138, 0x1f8, v138
	v_cmp_gt_i32_e32 vcc, s86, v160
	v_add_f32_e32 v150, v150, v151
	v_fmamk_f32 v150, v150, 0x37000000, v187
	v_cndmask_b32_e32 v138, v188, v138, vcc
	v_lshlrev_b32_e32 v138, 2, v138
	v_rsq_f32_e32 v161, v150
	v_add_u32_e32 v139, v174, v138
	v_add_u32_e32 v138, v175, v138
	ds_read_b128 v[142:145], v139
	ds_read_b128 v[138:141], v138
	v_mul_f32_e32 v166, s40, v161
	v_pk_mul_f32 v[168:169], v[92:93], v[166:167] op_sel_hi:[1,0]
	v_pk_mul_f32 v[170:171], v[90:91], v[166:167] op_sel_hi:[1,0]
	v_ashrrev_i32_e32 v153, 31, v152
	v_pk_mul_f32 v[162:163], v[96:97], v[166:167] op_sel_hi:[1,0]
	v_pk_mul_f32 v[164:165], v[94:95], v[166:167] op_sel_hi:[1,0]
	v_pk_mul_f32 v[166:167], v[132:133], v[168:169]
	v_pk_mul_f32 v[168:169], v[130:131], v[170:171]
	v_lshlrev_b64 v[150:151], 8, v[152:153]
	v_pk_mul_f32 v[162:163], v[136:137], v[162:163]
	v_pk_mul_f32 v[164:165], v[134:135], v[164:165]
	s_waitcnt lgkmcnt(0)
	v_pk_mul_f32 v[170:171], v[140:141], v[166:167]
	v_pk_mul_f32 v[172:173], v[138:139], v[168:169]
	v_lshl_add_u64 v[150:151], v[146:147], 0, v[150:151]
	v_pk_fma_f32 v[170:171], v[144:145], v[162:163], v[170:171] neg_lo:[0,0,1] neg_hi:[0,0,1]
	v_pk_fma_f32 v[172:173], v[142:143], v[164:165], v[172:173] neg_lo:[0,0,1] neg_hi:[0,0,1]
	s_mov_b64 s[52:53], -1
	s_and_b64 vcc, exec, s[6:7]
	v_pk_mul_f32 v[168:169], v[142:143], v[168:169]
	s_cbranch_vccz .LBB0_433
	s_nop 0
	v_cvt_pk_fp8_f32 v161, v172, v173
	v_pk_fma_f32 v[178:179], v[138:139], v[164:165], v[168:169]
	v_pk_mul_f32 v[176:177], v[144:145], v[166:167]
	s_mov_b64 s[52:53], 0
	v_cvt_pk_fp8_f32 v161, v170, v171 op_sel:[0,0,1]
	v_pk_fma_f32 v[176:177], v[140:141], v[162:163], v[176:177]
	global_store_dword v[150:151], v161, off
	s_nop 0
	v_cvt_pk_fp8_f32 v161, v178, v179
	v_cvt_pk_fp8_f32 v161, v176, v177 op_sel:[0,0,1]
	global_store_dword v[150:151], v161, off offset:8

; DI unsigned pk4_fp8(float a, float b, float c, float d) { int r = 0; r = __builtin_amdgcn_cvt_pk_fp8_f32(a, b, r, false); r = __builtin_amdgcn_cvt_pk_fp8_f32(c, d, r, true); return (unsigned)r; }
; DI void store8(bf16_t* p, f32x4 a) { u32x2 w; w.x = pk2(a[0], a[1]); w.y = pk2(a[2], a[3]); *(u32x2*)p = w; }
;     DI void head32x2(const AccT& acc, int rbase, int wc, int fq, bf16_t* dst, const float* gain, float scale, const bool F8) const {
;     ...
;                 for (int bj = 0; bj < 2; ++bj) {
;                     float ss = 0.f;
; #pragma unroll
;                     for (int n = 0; n < 2; ++n)
; #pragma unroll
;                         for (int i = 0; i < 4; ++i) ss += acc[ai][bj][m][n][i] * acc[ai][bj][m][n][i];
;                     ss = sum_x16_x32(ss);
;                     const float rinv = __builtin_amdgcn_rsqf(ss * (W8_INV * W8_INV / 32.0f) + EPS) * (scale * W8_INV);
;                     const f32x4 x1 = acc[ai][bj][m][0] * rinv * g0, x2 = acc[ai][bj][m][1] * rinv * g1;
;                     if (F8) { unsigned char* p8 = (unsigned char*)dst + (size_t)row * 256 + wc * 64 + 32 * bj + dbase; const f32x4 y1 = x1 * c - x2 * sn, y2 = x1 * sn + x2 * c;
;                         *(unsigned*)p8 = pk4_fp8(y1[0], y1[1], y1[2], y1[3]); *(unsigned*)(p8 + 8) = pk4_fp8(y2[0], y2[1], y2[2], y2[3]); }
;                     else { bf16_t* p = dst + (size_t)row * 256 + wc * 64 + 32 * bj + dbase;
;                         store8(p, x1 * c - x2 * sn); store8(p + 8, x1 * sn + x2 * c); }
.LBB0_435:
	v_mul_f32_e32 v161, v87, v87
	v_fmac_f32_e32 v161, v86, v86
	v_fmac_f32_e32 v161, v88, v88
	v_fmac_f32_e32 v161, v89, v89
	v_fmac_f32_e32 v161, v82, v82
	v_fmac_f32_e32 v161, v83, v83
	v_fmac_f32_e32 v161, v84, v84
	v_fmac_f32_e32 v161, v85, v85
	v_mov_b32_e32 v162, v161
	s_nop 1
	v_permlane16_swap_b32_e32 v161, v162
	v_add_f32_e32 v161, v161, v162
	v_mov_b32_e32 v162, v161
	s_nop 1
	v_permlane32_swap_b32_e32 v161, v162
	v_add_f32_e32 v161, v161, v162
	v_fmamk_f32 v161, v161, 0x37000000, v187
	v_rsq_f32_e32 v161, v161
	s_mov_b64 s[52:53], -1
	s_and_b64 vcc, exec, s[6:7]
	v_mul_f32_e32 v166, s40, v161
	v_pk_mul_f32 v[168:169], v[84:85], v[166:167] op_sel_hi:[1,0]
	v_pk_mul_f32 v[170:171], v[82:83], v[166:167] op_sel_hi:[1,0]
	v_pk_mul_f32 v[162:163], v[88:89], v[166:167] op_sel_hi:[1,0]
	v_pk_mul_f32 v[164:165], v[86:87], v[166:167] op_sel_hi:[1,0]
	v_pk_mul_f32 v[166:167], v[132:133], v[168:169]
	v_pk_mul_f32 v[172:173], v[130:131], v[170:171]
	v_pk_mul_f32 v[162:163], v[136:137], v[162:163]
	v_pk_mul_f32 v[164:165], v[134:135], v[164:165]
	v_pk_mul_f32 v[168:169], v[140:141], v[166:167]
	v_pk_mul_f32 v[170:171], v[138:139], v[172:173]
	v_pk_fma_f32 v[168:169], v[144:145], v[162:163], v[168:169] neg_lo:[0,0,1] neg_hi:[0,0,1]
	v_pk_fma_f32 v[170:171], v[142:143], v[164:165], v[170:171] neg_lo:[0,0,1] neg_hi:[0,0,1]
	v_pk_mul_f32 v[142:143], v[142:143], v[172:173]
	s_cbranch_vccz .LBB0_437
	s_nop 0
	v_cvt_pk_fp8_f32 v161, v170, v171
	v_pk_fma_f32 v[176:177], v[138:139], v[164:165], v[142:143]
	v_pk_mul_f32 v[172:173], v[144:145], v[166:167]
	s_mov_b64 s[52:53], 0
	v_cvt_pk_fp8_f32 v161, v168, v169 op_sel:[0,0,1]
	v_pk_fma_f32 v[172:173], v[140:141], v[162:163], v[172:173]
	global_store_dword v[150:151], v161, off offset:32
	s_nop 0
	v_cvt_pk_fp8_f32 v161, v176, v177
	v_cvt_pk_fp8_f32 v161, v172, v173 op_sel:[0,0,1]
	global_store_dword v[150:151], v161, off offset:40

; #define LAS __attribute__((address_space(3)))
; DI unsigned pk4_fp8(float a, float b, float c, float d) { int r = 0; r = __builtin_amdgcn_cvt_pk_fp8_f32(a, b, r, false); r = __builtin_amdgcn_cvt_pk_fp8_f32(c, d, r, true); return (unsigned)r; }
; DI void store8(bf16_t* p, f32x4 a) { u32x2 w; w.x = pk2(a[0], a[1]); w.y = pk2(a[2], a[3]); *(u32x2*)p = w; }
;     DI void head32x2(const AccT& acc, int rbase, int wc, int fq, bf16_t* dst, const float* gain, float scale, const bool F8) const {
;     ...
;             for (int m = 0; m < 4; ++m) {
;                 const int row = rbase + 128 * ai + 16 * m;
;                 const bool lat = row < NLAT; const int t = row & (SEQ - 1);
;                 const int pos = lat ? ((fq >> 1) ? (t & 63) : (t >> 6)) : 64;
;                 const f32x4 c = *(LAS const f32x4*)(cs8 + pos * 8 + 4 * (fq & 1)), sn = *(LAS const f32x4*)(sn8 + pos * 8 + 4 * (fq & 1));
; #pragma unroll
;                 for (int bj = 0; bj < 2; ++bj) {
;                     float ss = 0.f;
; #pragma unroll
;                     for (int n = 0; n < 2; ++n)
; #pragma unroll
;                         for (int i = 0; i < 4; ++i) ss += acc[ai][bj][m][n][i] * acc[ai][bj][m][n][i];
;                     ss = sum_x16_x32(ss);
;                     const float rinv = __builtin_amdgcn_rsqf(ss * (W8_INV * W8_INV / 32.0f) + EPS) * (scale * W8_INV);
;                     const f32x4 x1 = acc[ai][bj][m][0] * rinv * g0, x2 = acc[ai][bj][m][1] * rinv * g1;
;                     if (F8) { unsigned char* p8 = (unsigned char*)dst + (size_t)row * 256 + wc * 64 + 32 * bj + dbase; const f32x4 y1 = x1 * c - x2 * sn, y2 = x1 * sn + x2 * c;
;                         *(unsigned*)p8 = pk4_fp8(y1[0], y1[1], y1[2], y1[3]); *(unsigned*)(p8 + 8) = pk4_fp8(y2[0], y2[1], y2[2], y2[3]); }
;                     else { bf16_t* p = dst + (size_t)row * 256 + wc * 64 + 32 * bj + dbase;
;                         store8(p, x1 * c - x2 * sn); store8(p + 8, x1 * sn + x2 * c); }
.LBB0_439:
	v_mul_f32_e32 v150, v79, v79
	v_fmac_f32_e32 v150, v78, v78
	v_fmac_f32_e32 v150, v80, v80
	v_fmac_f32_e32 v150, v81, v81
	v_fmac_f32_e32 v150, v74, v74
	v_fmac_f32_e32 v150, v75, v75
	v_fmac_f32_e32 v150, v76, v76
	v_fmac_f32_e32 v150, v77, v77
	v_mov_b32_e32 v151, v150
	v_add_u32_e32 v152, 48, v160
	s_nop 0
	v_permlane16_swap_b32_e32 v150, v151
	v_lshrrev_b32_e32 v138, 6, v152
	v_add_f32_e32 v150, v150, v151
	v_cndmask_b32_e64 v138, v152, v138, s[4:5]
	v_mov_b32_e32 v151, v150
	v_lshlrev_b32_e32 v138, 3, v138
	s_nop 0
	v_permlane32_swap_b32_e32 v150, v151
	v_and_b32_e32 v138, 0x1f8, v138
	v_cmp_gt_i32_e32 vcc, s87, v160
	v_add_f32_e32 v150, v150, v151
	v_fmamk_f32 v150, v150, 0x37000000, v187
	v_cndmask_b32_e32 v138, v188, v138, vcc
	v_lshlrev_b32_e32 v138, 2, v138
	v_rsq_f32_e32 v161, v150
	v_add_u32_e32 v139, v174, v138
	v_add_u32_e32 v138, v175, v138
	ds_read_b128 v[142:145], v139
	ds_read_b128 v[138:141], v138
	v_mul_f32_e32 v166, s40, v161
	v_pk_mul_f32 v[168:169], v[76:77], v[166:167] op_sel_hi:[1,0]
	v_pk_mul_f32 v[170:171], v[74:75], v[166:167] op_sel_hi:[1,0]
	v_ashrrev_i32_e32 v153, 31, v152
	v_pk_mul_f32 v[162:163], v[80:81], v[166:167] op_sel_hi:[1,0]
	v_pk_mul_f32 v[164:165], v[78:79], v[166:167] op_sel_hi:[1,0]
	v_pk_mul_f32 v[166:167], v[132:133], v[168:169]
	v_pk_mul_f32 v[168:169], v[130:131], v[170:171]
	v_lshlrev_b64 v[150:151], 8, v[152:153]
	v_pk_mul_f32 v[162:163], v[136:137], v[162:163]
	v_pk_mul_f32 v[164:165], v[134:135], v[164:165]
	s_waitcnt lgkmcnt(0)
	v_pk_mul_f32 v[170:171], v[140:141], v[166:167]
	v_pk_mul_f32 v[172:173], v[138:139], v[168:169]
	v_lshl_add_u64 v[150:151], v[146:147], 0, v[150:151]
	v_pk_fma_f32 v[170:171], v[144:145], v[162:163], v[170:171] neg_lo:[0,0,1] neg_hi:[0,0,1]
	v_pk_fma_f32 v[172:173], v[142:143], v[164:165], v[172:173] neg_lo:[0,0,1] neg_hi:[0,0,1]
	s_mov_b64 s[52:53], -1
	s_and_b64 vcc, exec, s[6:7]
	v_pk_mul_f32 v[168:169], v[142:143], v[168:169]
	s_cbranch_vccz .LBB0_441
	s_nop 0
	v_cvt_pk_fp8_f32 v161, v172, v173
	v_pk_fma_f32 v[178:179], v[138:139], v[164:165], v[168:169]
	v_pk_mul_f32 v[176:177], v[144:145], v[166:167]
	s_mov_b64 s[52:53], 0
	v_cvt_pk_fp8_f32 v161, v170, v171 op_sel:[0,0,1]
	v_pk_fma_f32 v[176:177], v[140:141], v[162:163], v[176:177]
	global_store_dword v[150:151], v161, off
	s_nop 0
	v_cvt_pk_fp8_f32 v161, v178, v179
	v_cvt_pk_fp8_f32 v161, v176, v177 op_sel:[0,0,1]
	global_store_dword v[150:151], v161, off offset:8

; DI unsigned pk4_fp8(float a, float b, float c, float d) { int r = 0; r = __builtin_amdgcn_cvt_pk_fp8_f32(a, b, r, false); r = __builtin_amdgcn_cvt_pk_fp8_f32(c, d, r, true); return (unsigned)r; }
; DI void store8(bf16_t* p, f32x4 a) { u32x2 w; w.x = pk2(a[0], a[1]); w.y = pk2(a[2], a[3]); *(u32x2*)p = w; }
;     DI void head32x2(const AccT& acc, int rbase, int wc, int fq, bf16_t* dst, const float* gain, float scale, const bool F8) const {
;     ...
;                 for (int bj = 0; bj < 2; ++bj) {
;                     float ss = 0.f;
; #pragma unroll
;                     for (int n = 0; n < 2; ++n)
; #pragma unroll
;                         for (int i = 0; i < 4; ++i) ss += acc[ai][bj][m][n][i] * acc[ai][bj][m][n][i];
;                     ss = sum_x16_x32(ss);
;                     const float rinv = __builtin_amdgcn_rsqf(ss * (W8_INV * W8_INV / 32.0f) + EPS) * (scale * W8_INV);
;                     const f32x4 x1 = acc[ai][bj][m][0] * rinv * g0, x2 = acc[ai][bj][m][1] * rinv * g1;
;                     if (F8) { unsigned char* p8 = (unsigned char*)dst + (size_t)row * 256 + wc * 64 + 32 * bj + dbase; const f32x4 y1 = x1 * c - x2 * sn, y2 = x1 * sn + x2 * c;
;                         *(unsigned*)p8 = pk4_fp8(y1[0], y1[1], y1[2], y1[3]); *(unsigned*)(p8 + 8) = pk4_fp8(y2[0], y2[1], y2[2], y2[3]); }
;                     else { bf16_t* p = dst + (size_t)row * 256 + wc * 64 + 32 * bj + dbase;
;                         store8(p, x1 * c - x2 * sn); store8(p + 8, x1 * sn + x2 * c); }
.LBB0_443:
	v_mul_f32_e32 v161, v71, v71
	v_fmac_f32_e32 v161, v70, v70
	v_fmac_f32_e32 v161, v72, v72
	v_fmac_f32_e32 v161, v73, v73
	v_fmac_f32_e32 v161, v66, v66
	v_fmac_f32_e32 v161, v67, v67
	v_fmac_f32_e32 v161, v68, v68
	v_fmac_f32_e32 v161, v69, v69
	v_mov_b32_e32 v162, v161
	s_nop 1
	v_permlane16_swap_b32_e32 v161, v162
	v_add_f32_e32 v161, v161, v162
	v_mov_b32_e32 v162, v161
	s_nop 1
	v_permlane32_swap_b32_e32 v161, v162
	v_add_f32_e32 v161, v161, v162
	v_fmamk_f32 v161, v161, 0x37000000, v187
	v_rsq_f32_e32 v161, v161
	s_mov_b64 s[52:53], -1
	s_and_b64 vcc, exec, s[6:7]
	v_mul_f32_e32 v166, s40, v161
	v_pk_mul_f32 v[168:169], v[68:69], v[166:167] op_sel_hi:[1,0]
	v_pk_mul_f32 v[170:171], v[66:67], v[166:167] op_sel_hi:[1,0]
	v_pk_mul_f32 v[162:163], v[72:73], v[166:167] op_sel_hi:[1,0]
	v_pk_mul_f32 v[164:165], v[70:71], v[166:167] op_sel_hi:[1,0]
	v_pk_mul_f32 v[166:167], v[132:133], v[168:169]
	v_pk_mul_f32 v[172:173], v[130:131], v[170:171]
	v_pk_mul_f32 v[162:163], v[136:137], v[162:163]
	v_pk_mul_f32 v[164:165], v[134:135], v[164:165]
	v_pk_mul_f32 v[168:169], v[140:141], v[166:167]
	v_pk_mul_f32 v[170:171], v[138:139], v[172:173]
	v_pk_fma_f32 v[168:169], v[144:145], v[162:163], v[168:169] neg_lo:[0,0,1] neg_hi:[0,0,1]
	v_pk_fma_f32 v[170:171], v[142:143], v[164:165], v[170:171] neg_lo:[0,0,1] neg_hi:[0,0,1]
	v_pk_mul_f32 v[142:143], v[142:143], v[172:173]
	s_cbranch_vccz .LBB0_445
	s_nop 0
	v_cvt_pk_fp8_f32 v161, v170, v171
	v_pk_fma_f32 v[176:177], v[138:139], v[164:165], v[142:143]
	v_pk_mul_f32 v[172:173], v[144:145], v[166:167]
	s_mov_b64 s[52:53], 0
	v_cvt_pk_fp8_f32 v161, v168, v169 op_sel:[0,0,1]
	v_pk_fma_f32 v[172:173], v[140:141], v[162:163], v[172:173]
	global_store_dword v[150:151], v161, off offset:32
	s_nop 0
	v_cvt_pk_fp8_f32 v161, v176, v177
	v_cvt_pk_fp8_f32 v161, v172, v173 op_sel:[0,0,1]
	global_store_dword v[150:151], v161, off offset:40

; #define LAS __attribute__((address_space(3)))
; DI unsigned pk4_fp8(float a, float b, float c, float d) { int r = 0; r = __builtin_amdgcn_cvt_pk_fp8_f32(a, b, r, false); r = __builtin_amdgcn_cvt_pk_fp8_f32(c, d, r, true); return (unsigned)r; }
; DI void store8(bf16_t* p, f32x4 a) { u32x2 w; w.x = pk2(a[0], a[1]); w.y = pk2(a[2], a[3]); *(u32x2*)p = w; }
;     DI void head32x2(const AccT& acc, int rbase, int wc, int fq, bf16_t* dst, const float* gain, float scale, const bool F8) const {
;     ...
;             for (int m = 0; m < 4; ++m) {
;                 const int row = rbase + 128 * ai + 16 * m;
;                 const bool lat = row < NLAT; const int t = row & (SEQ - 1);
;                 const int pos = lat ? ((fq >> 1) ? (t & 63) : (t >> 6)) : 64;
;                 const f32x4 c = *(LAS const f32x4*)(cs8 + pos * 8 + 4 * (fq & 1)), sn = *(LAS const f32x4*)(sn8 + pos * 8 + 4 * (fq & 1));
; #pragma unroll
;                 for (int bj = 0; bj < 2; ++bj) {
;                     float ss = 0.f;
; #pragma unroll
;                     for (int n = 0; n < 2; ++n)
; #pragma unroll
;                         for (int i = 0; i < 4; ++i) ss += acc[ai][bj][m][n][i] * acc[ai][bj][m][n][i];
;                     ss = sum_x16_x32(ss);
;                     const float rinv = __builtin_amdgcn_rsqf(ss * (W8_INV * W8_INV / 32.0f) + EPS) * (scale * W8_INV);
;                     const f32x4 x1 = acc[ai][bj][m][0] * rinv * g0, x2 = acc[ai][bj][m][1] * rinv * g1;
;                     if (F8) { unsigned char* p8 = (unsigned char*)dst + (size_t)row * 256 + wc * 64 + 32 * bj + dbase; const f32x4 y1 = x1 * c - x2 * sn, y2 = x1 * sn + x2 * c;
;                         *(unsigned*)p8 = pk4_fp8(y1[0], y1[1], y1[2], y1[3]); *(unsigned*)(p8 + 8) = pk4_fp8(y2[0], y2[1], y2[2], y2[3]); }
;                     else { bf16_t* p = dst + (size_t)row * 256 + wc * 64 + 32 * bj + dbase;
;                         store8(p, x1 * c - x2 * sn); store8(p + 8, x1 * sn + x2 * c); }
.LBB0_447:
	v_mul_f32_e32 v150, v63, v63
	v_fmac_f32_e32 v150, v62, v62
	v_fmac_f32_e32 v150, v64, v64
	v_fmac_f32_e32 v150, v65, v65
	v_fmac_f32_e32 v150, v58, v58
	v_fmac_f32_e32 v150, v59, v59
	v_fmac_f32_e32 v150, v60, v60
	v_fmac_f32_e32 v150, v61, v61
	v_mov_b32_e32 v151, v150
	v_add_u32_e32 v152, 0x80, v160
	s_nop 0
	v_permlane16_swap_b32_e32 v150, v151
	v_lshrrev_b32_e32 v138, 6, v152
	v_add_f32_e32 v150, v150, v151
	v_cndmask_b32_e64 v138, v190, v138, s[4:5]
	v_mov_b32_e32 v151, v150
	v_lshlrev_b32_e32 v138, 3, v138
	s_nop 0
	v_permlane32_swap_b32_e32 v150, v151
	v_and_b32_e32 v138, 0x1f8, v138
	v_cmp_gt_i32_e32 vcc, s88, v160
	v_add_f32_e32 v150, v150, v151
	v_fmamk_f32 v150, v150, 0x37000000, v187
	v_cndmask_b32_e32 v138, v188, v138, vcc
	v_lshlrev_b32_e32 v138, 2, v138
	v_rsq_f32_e32 v161, v150
	v_add_u32_e32 v139, v174, v138
	v_add_u32_e32 v138, v175, v138
	ds_read_b128 v[142:145], v139
	ds_read_b128 v[138:141], v138
	v_mul_f32_e32 v166, s40, v161
	v_pk_mul_f32 v[168:169], v[60:61], v[166:167] op_sel_hi:[1,0]
	v_pk_mul_f32 v[170:171], v[58:59], v[166:167] op_sel_hi:[1,0]
	v_ashrrev_i32_e32 v153, 31, v152
	v_pk_mul_f32 v[162:163], v[64:65], v[166:167] op_sel_hi:[1,0]
	v_pk_mul_f32 v[164:165], v[62:63], v[166:167] op_sel_hi:[1,0]
	v_pk_mul_f32 v[166:167], v[132:133], v[168:169]
	v_pk_mul_f32 v[168:169], v[130:131], v[170:171]
	v_lshlrev_b64 v[150:151], 8, v[152:153]
	v_pk_mul_f32 v[162:163], v[136:137], v[162:163]
	v_pk_mul_f32 v[164:165], v[134:135], v[164:165]
	s_waitcnt lgkmcnt(0)
	v_pk_mul_f32 v[170:171], v[140:141], v[166:167]
	v_pk_mul_f32 v[172:173], v[138:139], v[168:169]
	v_lshl_add_u64 v[150:151], v[146:147], 0, v[150:151]
	v_pk_fma_f32 v[170:171], v[144:145], v[162:163], v[170:171] neg_lo:[0,0,1] neg_hi:[0,0,1]
	v_pk_fma_f32 v[172:173], v[142:143], v[164:165], v[172:173] neg_lo:[0,0,1] neg_hi:[0,0,1]
	s_mov_b64 s[52:53], -1
	s_and_b64 vcc, exec, s[6:7]
	v_pk_mul_f32 v[168:169], v[142:143], v[168:169]
	s_cbranch_vccz .LBB0_449
	s_nop 0
	v_cvt_pk_fp8_f32 v161, v172, v173
	v_pk_fma_f32 v[178:179], v[138:139], v[164:165], v[168:169]
	v_pk_mul_f32 v[176:177], v[144:145], v[166:167]
	s_mov_b64 s[52:53], 0
	v_cvt_pk_fp8_f32 v161, v170, v171 op_sel:[0,0,1]
	v_pk_fma_f32 v[176:177], v[140:141], v[162:163], v[176:177]
	global_store_dword v[150:151], v161, off
	s_nop 0
	v_cvt_pk_fp8_f32 v161, v178, v179
	v_cvt_pk_fp8_f32 v161, v176, v177 op_sel:[0,0,1]
	global_store_dword v[150:151], v161, off offset:8

; DI unsigned pk4_fp8(float a, float b, float c, float d) { int r = 0; r = __builtin_amdgcn_cvt_pk_fp8_f32(a, b, r, false); r = __builtin_amdgcn_cvt_pk_fp8_f32(c, d, r, true); return (unsigned)r; }
; DI void store8(bf16_t* p, f32x4 a) { u32x2 w; w.x = pk2(a[0], a[1]); w.y = pk2(a[2], a[3]); *(u32x2*)p = w; }
;     DI void head32x2(const AccT& acc, int rbase, int wc, int fq, bf16_t* dst, const float* gain, float scale, const bool F8) const {
;     ...
;                 for (int bj = 0; bj < 2; ++bj) {
;                     float ss = 0.f;
; #pragma unroll
;                     for (int n = 0; n < 2; ++n)
; #pragma unroll
;                         for (int i = 0; i < 4; ++i) ss += acc[ai][bj][m][n][i] * acc[ai][bj][m][n][i];
;                     ss = sum_x16_x32(ss);
;                     const float rinv = __builtin_amdgcn_rsqf(ss * (W8_INV * W8_INV / 32.0f) + EPS) * (scale * W8_INV);
;                     const f32x4 x1 = acc[ai][bj][m][0] * rinv * g0, x2 = acc[ai][bj][m][1] * rinv * g1;
;                     if (F8) { unsigned char* p8 = (unsigned char*)dst + (size_t)row * 256 + wc * 64 + 32 * bj + dbase; const f32x4 y1 = x1 * c - x2 * sn, y2 = x1 * sn + x2 * c;
;                         *(unsigned*)p8 = pk4_fp8(y1[0], y1[1], y1[2], y1[3]); *(unsigned*)(p8 + 8) = pk4_fp8(y2[0], y2[1], y2[2], y2[3]); }
;                     else { bf16_t* p = dst + (size_t)row * 256 + wc * 64 + 32 * bj + dbase;
;                         store8(p, x1 * c - x2 * sn); store8(p + 8, x1 * sn + x2 * c); }
.LBB0_451:
	v_mul_f32_e32 v161, v55, v55
	v_fmac_f32_e32 v161, v54, v54
	v_fmac_f32_e32 v161, v56, v56
	v_fmac_f32_e32 v161, v57, v57
	v_fmac_f32_e32 v161, v50, v50
	v_fmac_f32_e32 v161, v51, v51
	v_fmac_f32_e32 v161, v52, v52
	v_fmac_f32_e32 v161, v53, v53
	v_mov_b32_e32 v162, v161
	s_nop 1
	v_permlane16_swap_b32_e32 v161, v162
	v_add_f32_e32 v161, v161, v162
	v_mov_b32_e32 v162, v161
	s_nop 1
	v_permlane32_swap_b32_e32 v161, v162
	v_add_f32_e32 v161, v161, v162
	v_fmamk_f32 v161, v161, 0x37000000, v187
	v_rsq_f32_e32 v161, v161
	s_mov_b64 s[52:53], -1
	s_and_b64 vcc, exec, s[6:7]
	v_mul_f32_e32 v166, s40, v161
	v_pk_mul_f32 v[168:169], v[52:53], v[166:167] op_sel_hi:[1,0]
	v_pk_mul_f32 v[170:171], v[50:51], v[166:167] op_sel_hi:[1,0]
	v_pk_mul_f32 v[162:163], v[56:57], v[166:167] op_sel_hi:[1,0]
	v_pk_mul_f32 v[164:165], v[54:55], v[166:167] op_sel_hi:[1,0]
	v_pk_mul_f32 v[166:167], v[132:133], v[168:169]
	v_pk_mul_f32 v[172:173], v[130:131], v[170:171]
	v_pk_mul_f32 v[162:163], v[136:137], v[162:163]
	v_pk_mul_f32 v[164:165], v[134:135], v[164:165]
	v_pk_mul_f32 v[168:169], v[140:141], v[166:167]
	v_pk_mul_f32 v[170:171], v[138:139], v[172:173]
	v_pk_fma_f32 v[168:169], v[144:145], v[162:163], v[168:169] neg_lo:[0,0,1] neg_hi:[0,0,1]
	v_pk_fma_f32 v[170:171], v[142:143], v[164:165], v[170:171] neg_lo:[0,0,1] neg_hi:[0,0,1]
	v_pk_mul_f32 v[142:143], v[142:143], v[172:173]
	s_cbranch_vccz .LBB0_453
	s_nop 0
	v_cvt_pk_fp8_f32 v161, v170, v171
	v_pk_fma_f32 v[176:177], v[138:139], v[164:165], v[142:143]
	v_pk_mul_f32 v[172:173], v[144:145], v[166:167]
	s_mov_b64 s[52:53], 0
	v_cvt_pk_fp8_f32 v161, v168, v169 op_sel:[0,0,1]
	v_pk_fma_f32 v[172:173], v[140:141], v[162:163], v[172:173]
	global_store_dword v[150:151], v161, off offset:32
	s_nop 0
	v_cvt_pk_fp8_f32 v161, v176, v177
	v_cvt_pk_fp8_f32 v161, v172, v173 op_sel:[0,0,1]
	global_store_dword v[150:151], v161, off offset:40

; #define LAS __attribute__((address_space(3)))
; DI unsigned pk4_fp8(float a, float b, float c, float d) { int r = 0; r = __builtin_amdgcn_cvt_pk_fp8_f32(a, b, r, false); r = __builtin_amdgcn_cvt_pk_fp8_f32(c, d, r, true); return (unsigned)r; }
; DI void store8(bf16_t* p, f32x4 a) { u32x2 w; w.x = pk2(a[0], a[1]); w.y = pk2(a[2], a[3]); *(u32x2*)p = w; }
;     DI void head32x2(const AccT& acc, int rbase, int wc, int fq, bf16_t* dst, const float* gain, float scale, const bool F8) const {
;     ...
;             for (int m = 0; m < 4; ++m) {
;                 const int row = rbase + 128 * ai + 16 * m;
;                 const bool lat = row < NLAT; const int t = row & (SEQ - 1);
;                 const int pos = lat ? ((fq >> 1) ? (t & 63) : (t >> 6)) : 64;
;                 const f32x4 c = *(LAS const f32x4*)(cs8 + pos * 8 + 4 * (fq & 1)), sn = *(LAS const f32x4*)(sn8 + pos * 8 + 4 * (fq & 1));
; #pragma unroll
;                 for (int bj = 0; bj < 2; ++bj) {
;                     float ss = 0.f;
; #pragma unroll
;                     for (int n = 0; n < 2; ++n)
; #pragma unroll
;                         for (int i = 0; i < 4; ++i) ss += acc[ai][bj][m][n][i] * acc[ai][bj][m][n][i];
;                     ss = sum_x16_x32(ss);
;                     const float rinv = __builtin_amdgcn_rsqf(ss * (W8_INV * W8_INV / 32.0f) + EPS) * (scale * W8_INV);
;                     const f32x4 x1 = acc[ai][bj][m][0] * rinv * g0, x2 = acc[ai][bj][m][1] * rinv * g1;
;                     if (F8) { unsigned char* p8 = (unsigned char*)dst + (size_t)row * 256 + wc * 64 + 32 * bj + dbase; const f32x4 y1 = x1 * c - x2 * sn, y2 = x1 * sn + x2 * c;
;                         *(unsigned*)p8 = pk4_fp8(y1[0], y1[1], y1[2], y1[3]); *(unsigned*)(p8 + 8) = pk4_fp8(y2[0], y2[1], y2[2], y2[3]); }
;                     else { bf16_t* p = dst + (size_t)row * 256 + wc * 64 + 32 * bj + dbase;
;                         store8(p, x1 * c - x2 * sn); store8(p + 8, x1 * sn + x2 * c); }
.LBB0_455:
	v_mul_f32_e32 v150, v47, v47
	v_fmac_f32_e32 v150, v46, v46
	v_fmac_f32_e32 v150, v48, v48
	v_fmac_f32_e32 v150, v49, v49
	v_fmac_f32_e32 v150, v42, v42
	v_fmac_f32_e32 v150, v43, v43
	v_fmac_f32_e32 v150, v44, v44
	v_fmac_f32_e32 v150, v45, v45
	v_mov_b32_e32 v151, v150
	v_add_u32_e32 v152, 0x90, v160
	s_nop 0
	v_permlane16_swap_b32_e32 v150, v151
	v_lshrrev_b32_e32 v138, 6, v152
	v_add_f32_e32 v150, v150, v151
	v_cndmask_b32_e64 v138, v152, v138, s[4:5]
	v_mov_b32_e32 v151, v150
	v_lshlrev_b32_e32 v138, 3, v138
	s_nop 0
	v_permlane32_swap_b32_e32 v150, v151
	v_and_b32_e32 v138, 0x1f8, v138
	v_cmp_gt_i32_e32 vcc, s89, v160
	v_add_f32_e32 v150, v150, v151
	v_fmamk_f32 v150, v150, 0x37000000, v187
	v_cndmask_b32_e32 v138, v188, v138, vcc
	v_lshlrev_b32_e32 v138, 2, v138
	v_rsq_f32_e32 v161, v150
	v_add_u32_e32 v139, v174, v138
	v_add_u32_e32 v138, v175, v138
	ds_read_b128 v[142:145], v139
	ds_read_b128 v[138:141], v138
	v_mul_f32_e32 v166, s40, v161
	v_pk_mul_f32 v[168:169], v[44:45], v[166:167] op_sel_hi:[1,0]
	v_pk_mul_f32 v[170:171], v[42:43], v[166:167] op_sel_hi:[1,0]
	v_ashrrev_i32_e32 v153, 31, v152
	v_pk_mul_f32 v[162:163], v[48:49], v[166:167] op_sel_hi:[1,0]
	v_pk_mul_f32 v[164:165], v[46:47], v[166:167] op_sel_hi:[1,0]
	v_pk_mul_f32 v[166:167], v[132:133], v[168:169]
	v_pk_mul_f32 v[168:169], v[130:131], v[170:171]
	v_lshlrev_b64 v[150:151], 8, v[152:153]
	v_pk_mul_f32 v[162:163], v[136:137], v[162:163]
	v_pk_mul_f32 v[164:165], v[134:135], v[164:165]
	s_waitcnt lgkmcnt(0)
	v_pk_mul_f32 v[170:171], v[140:141], v[166:167]
	v_pk_mul_f32 v[172:173], v[138:139], v[168:169]
	v_lshl_add_u64 v[150:151], v[146:147], 0, v[150:151]
	v_pk_fma_f32 v[170:171], v[144:145], v[162:163], v[170:171] neg_lo:[0,0,1] neg_hi:[0,0,1]
	v_pk_fma_f32 v[172:173], v[142:143], v[164:165], v[172:173] neg_lo:[0,0,1] neg_hi:[0,0,1]
	s_mov_b64 s[52:53], -1
	s_and_b64 vcc, exec, s[6:7]
	v_pk_mul_f32 v[168:169], v[142:143], v[168:169]
	s_cbranch_vccz .LBB0_457
	s_nop 0
	v_cvt_pk_fp8_f32 v161, v172, v173
	v_pk_fma_f32 v[178:179], v[138:139], v[164:165], v[168:169]
	v_pk_mul_f32 v[176:177], v[144:145], v[166:167]
	s_mov_b64 s[52:53], 0
	v_cvt_pk_fp8_f32 v161, v170, v171 op_sel:[0,0,1]
	v_pk_fma_f32 v[176:177], v[140:141], v[162:163], v[176:177]
	global_store_dword v[150:151], v161, off
	s_nop 0
	v_cvt_pk_fp8_f32 v161, v178, v179
	v_cvt_pk_fp8_f32 v161, v176, v177 op_sel:[0,0,1]
	global_store_dword v[150:151], v161, off offset:8

; DI unsigned pk4_fp8(float a, float b, float c, float d) { int r = 0; r = __builtin_amdgcn_cvt_pk_fp8_f32(a, b, r, false); r = __builtin_amdgcn_cvt_pk_fp8_f32(c, d, r, true); return (unsigned)r; }
; DI void store8(bf16_t* p, f32x4 a) { u32x2 w; w.x = pk2(a[0], a[1]); w.y = pk2(a[2], a[3]); *(u32x2*)p = w; }
;     DI void head32x2(const AccT& acc, int rbase, int wc, int fq, bf16_t* dst, const float* gain, float scale, const bool F8) const {
;     ...
;                 for (int bj = 0; bj < 2; ++bj) {
;                     float ss = 0.f;
; #pragma unroll
;                     for (int n = 0; n < 2; ++n)
; #pragma unroll
;                         for (int i = 0; i < 4; ++i) ss += acc[ai][bj][m][n][i] * acc[ai][bj][m][n][i];
;                     ss = sum_x16_x32(ss);
;                     const float rinv = __builtin_amdgcn_rsqf(ss * (W8_INV * W8_INV / 32.0f) + EPS) * (scale * W8_INV);
;                     const f32x4 x1 = acc[ai][bj][m][0] * rinv * g0, x2 = acc[ai][bj][m][1] * rinv * g1;
;                     if (F8) { unsigned char* p8 = (unsigned char*)dst + (size_t)row * 256 + wc * 64 + 32 * bj + dbase; const f32x4 y1 = x1 * c - x2 * sn, y2 = x1 * sn + x2 * c;
;                         *(unsigned*)p8 = pk4_fp8(y1[0], y1[1], y1[2], y1[3]); *(unsigned*)(p8 + 8) = pk4_fp8(y2[0], y2[1], y2[2], y2[3]); }
;                     else { bf16_t* p = dst + (size_t)row * 256 + wc * 64 + 32 * bj + dbase;
;                         store8(p, x1 * c - x2 * sn); store8(p + 8, x1 * sn + x2 * c); }
.LBB0_459:
	v_mul_f32_e32 v161, v39, v39
	v_fmac_f32_e32 v161, v38, v38
	v_fmac_f32_e32 v161, v40, v40
	v_fmac_f32_e32 v161, v41, v41
	v_fmac_f32_e32 v161, v34, v34
	v_fmac_f32_e32 v161, v35, v35
	v_fmac_f32_e32 v161, v36, v36
	v_fmac_f32_e32 v161, v37, v37
	v_mov_b32_e32 v162, v161
	s_nop 1
	v_permlane16_swap_b32_e32 v161, v162
	v_add_f32_e32 v161, v161, v162
	v_mov_b32_e32 v162, v161
	s_nop 1
	v_permlane32_swap_b32_e32 v161, v162
	v_add_f32_e32 v161, v161, v162
	v_fmamk_f32 v161, v161, 0x37000000, v187
	v_rsq_f32_e32 v161, v161
	s_mov_b64 s[52:53], -1
	s_and_b64 vcc, exec, s[6:7]
	v_mul_f32_e32 v166, s40, v161
	v_pk_mul_f32 v[168:169], v[36:37], v[166:167] op_sel_hi:[1,0]
	v_pk_mul_f32 v[170:171], v[34:35], v[166:167] op_sel_hi:[1,0]
	v_pk_mul_f32 v[162:163], v[40:41], v[166:167] op_sel_hi:[1,0]
	v_pk_mul_f32 v[164:165], v[38:39], v[166:167] op_sel_hi:[1,0]
	v_pk_mul_f32 v[166:167], v[132:133], v[168:169]
	v_pk_mul_f32 v[172:173], v[130:131], v[170:171]
	v_pk_mul_f32 v[162:163], v[136:137], v[162:163]
	v_pk_mul_f32 v[164:165], v[134:135], v[164:165]
	v_pk_mul_f32 v[168:169], v[140:141], v[166:167]
	v_pk_mul_f32 v[170:171], v[138:139], v[172:173]
	v_pk_fma_f32 v[168:169], v[144:145], v[162:163], v[168:169] neg_lo:[0,0,1] neg_hi:[0,0,1]
	v_pk_fma_f32 v[170:171], v[142:143], v[164:165], v[170:171] neg_lo:[0,0,1] neg_hi:[0,0,1]
	v_pk_mul_f32 v[142:143], v[142:143], v[172:173]
	s_cbranch_vccz .LBB0_461
	s_nop 0
	v_cvt_pk_fp8_f32 v161, v170, v171
	v_pk_fma_f32 v[176:177], v[138:139], v[164:165], v[142:143]
	v_pk_mul_f32 v[172:173], v[144:145], v[166:167]
	s_mov_b64 s[52:53], 0
	v_cvt_pk_fp8_f32 v161, v168, v169 op_sel:[0,0,1]
	v_pk_fma_f32 v[172:173], v[140:141], v[162:163], v[172:173]
	global_store_dword v[150:151], v161, off offset:32
	s_nop 0
	v_cvt_pk_fp8_f32 v161, v176, v177
	v_cvt_pk_fp8_f32 v161, v172, v173 op_sel:[0,0,1]
	global_store_dword v[150:151], v161, off offset:40

; #define LAS __attribute__((address_space(3)))
; DI unsigned pk4_fp8(float a, float b, float c, float d) { int r = 0; r = __builtin_amdgcn_cvt_pk_fp8_f32(a, b, r, false); r = __builtin_amdgcn_cvt_pk_fp8_f32(c, d, r, true); return (unsigned)r; }
; DI void store8(bf16_t* p, f32x4 a) { u32x2 w; w.x = pk2(a[0], a[1]); w.y = pk2(a[2], a[3]); *(u32x2*)p = w; }
;     DI void head32x2(const AccT& acc, int rbase, int wc, int fq, bf16_t* dst, const float* gain, float scale, const bool F8) const {
;     ...
;             for (int m = 0; m < 4; ++m) {
;                 const int row = rbase + 128 * ai + 16 * m;
;                 const bool lat = row < NLAT; const int t = row & (SEQ - 1);
;                 const int pos = lat ? ((fq >> 1) ? (t & 63) : (t >> 6)) : 64;
;                 const f32x4 c = *(LAS const f32x4*)(cs8 + pos * 8 + 4 * (fq & 1)), sn = *(LAS const f32x4*)(sn8 + pos * 8 + 4 * (fq & 1));
; #pragma unroll
;                 for (int bj = 0; bj < 2; ++bj) {
;                     float ss = 0.f;
; #pragma unroll
;                     for (int n = 0; n < 2; ++n)
; #pragma unroll
;                         for (int i = 0; i < 4; ++i) ss += acc[ai][bj][m][n][i] * acc[ai][bj][m][n][i];
;                     ss = sum_x16_x32(ss);
;                     const float rinv = __builtin_amdgcn_rsqf(ss * (W8_INV * W8_INV / 32.0f) + EPS) * (scale * W8_INV);
;                     const f32x4 x1 = acc[ai][bj][m][0] * rinv * g0, x2 = acc[ai][bj][m][1] * rinv * g1;
;                     if (F8) { unsigned char* p8 = (unsigned char*)dst + (size_t)row * 256 + wc * 64 + 32 * bj + dbase; const f32x4 y1 = x1 * c - x2 * sn, y2 = x1 * sn + x2 * c;
;                         *(unsigned*)p8 = pk4_fp8(y1[0], y1[1], y1[2], y1[3]); *(unsigned*)(p8 + 8) = pk4_fp8(y2[0], y2[1], y2[2], y2[3]); }
;                     else { bf16_t* p = dst + (size_t)row * 256 + wc * 64 + 32 * bj + dbase;
;                         store8(p, x1 * c - x2 * sn); store8(p + 8, x1 * sn + x2 * c); }
.LBB0_463:
	v_mul_f32_e32 v150, v31, v31
	v_fmac_f32_e32 v150, v30, v30
	v_fmac_f32_e32 v150, v32, v32
	v_fmac_f32_e32 v150, v33, v33
	v_fmac_f32_e32 v150, v26, v26
	v_fmac_f32_e32 v150, v27, v27
	v_fmac_f32_e32 v150, v28, v28
	v_fmac_f32_e32 v150, v29, v29
	v_mov_b32_e32 v151, v150
	v_add_u32_e32 v152, 0xa0, v160
	s_nop 0
	v_permlane16_swap_b32_e32 v150, v151
	v_lshrrev_b32_e32 v138, 6, v152
	v_add_f32_e32 v150, v150, v151
	v_cndmask_b32_e64 v138, v152, v138, s[4:5]
	v_mov_b32_e32 v151, v150
	v_lshlrev_b32_e32 v138, 3, v138
	s_nop 0
	v_permlane32_swap_b32_e32 v150, v151
	v_and_b32_e32 v138, 0x1f8, v138
	v_cmp_gt_i32_e32 vcc, s90, v160
	v_add_f32_e32 v150, v150, v151
	v_fmamk_f32 v150, v150, 0x37000000, v187
	v_cndmask_b32_e32 v138, v188, v138, vcc
	v_lshlrev_b32_e32 v138, 2, v138
	v_rsq_f32_e32 v161, v150
	v_add_u32_e32 v139, v174, v138
	v_add_u32_e32 v138, v175, v138
	ds_read_b128 v[142:145], v139
	ds_read_b128 v[138:141], v138
	v_mul_f32_e32 v166, s40, v161
	v_pk_mul_f32 v[168:169], v[28:29], v[166:167] op_sel_hi:[1,0]
	v_pk_mul_f32 v[170:171], v[26:27], v[166:167] op_sel_hi:[1,0]
	v_ashrrev_i32_e32 v153, 31, v152
	v_pk_mul_f32 v[162:163], v[32:33], v[166:167] op_sel_hi:[1,0]
	v_pk_mul_f32 v[164:165], v[30:31], v[166:167] op_sel_hi:[1,0]
	v_pk_mul_f32 v[166:167], v[132:133], v[168:169]
	v_pk_mul_f32 v[168:169], v[130:131], v[170:171]
	v_lshlrev_b64 v[150:151], 8, v[152:153]
	v_pk_mul_f32 v[162:163], v[136:137], v[162:163]
	v_pk_mul_f32 v[164:165], v[134:135], v[164:165]
	s_waitcnt lgkmcnt(0)
	v_pk_mul_f32 v[170:171], v[140:141], v[166:167]
	v_pk_mul_f32 v[172:173], v[138:139], v[168:169]
	v_lshl_add_u64 v[150:151], v[146:147], 0, v[150:151]
	v_pk_fma_f32 v[170:171], v[144:145], v[162:163], v[170:171] neg_lo:[0,0,1] neg_hi:[0,0,1]
	v_pk_fma_f32 v[172:173], v[142:143], v[164:165], v[172:173] neg_lo:[0,0,1] neg_hi:[0,0,1]
	s_mov_b64 s[52:53], -1
	s_and_b64 vcc, exec, s[6:7]
	v_pk_mul_f32 v[168:169], v[142:143], v[168:169]
	s_cbranch_vccz .LBB0_465
	s_nop 0
	v_cvt_pk_fp8_f32 v161, v172, v173
	v_pk_fma_f32 v[178:179], v[138:139], v[164:165], v[168:169]
	v_pk_mul_f32 v[176:177], v[144:145], v[166:167]
	s_mov_b64 s[52:53], 0
	v_cvt_pk_fp8_f32 v161, v170, v171 op_sel:[0,0,1]
	v_pk_fma_f32 v[176:177], v[140:141], v[162:163], v[176:177]
	global_store_dword v[150:151], v161, off
	s_nop 0
	v_cvt_pk_fp8_f32 v161, v178, v179
	v_cvt_pk_fp8_f32 v161, v176, v177 op_sel:[0,0,1]
	global_store_dword v[150:151], v161, off offset:8

; DI unsigned pk4_fp8(float a, float b, float c, float d) { int r = 0; r = __builtin_amdgcn_cvt_pk_fp8_f32(a, b, r, false); r = __builtin_amdgcn_cvt_pk_fp8_f32(c, d, r, true); return (unsigned)r; }
; DI void store8(bf16_t* p, f32x4 a) { u32x2 w; w.x = pk2(a[0], a[1]); w.y = pk2(a[2], a[3]); *(u32x2*)p = w; }
;     DI void head32x2(const AccT& acc, int rbase, int wc, int fq, bf16_t* dst, const float* gain, float scale, const bool F8) const {
;     ...
;                 for (int bj = 0; bj < 2; ++bj) {
;                     float ss = 0.f;
; #pragma unroll
;                     for (int n = 0; n < 2; ++n)
; #pragma unroll
;                         for (int i = 0; i < 4; ++i) ss += acc[ai][bj][m][n][i] * acc[ai][bj][m][n][i];
;                     ss = sum_x16_x32(ss);
;                     const float rinv = __builtin_amdgcn_rsqf(ss * (W8_INV * W8_INV / 32.0f) + EPS) * (scale * W8_INV);
;                     const f32x4 x1 = acc[ai][bj][m][0] * rinv * g0, x2 = acc[ai][bj][m][1] * rinv * g1;
;                     if (F8) { unsigned char* p8 = (unsigned char*)dst + (size_t)row * 256 + wc * 64 + 32 * bj + dbase; const f32x4 y1 = x1 * c - x2 * sn, y2 = x1 * sn + x2 * c;
;                         *(unsigned*)p8 = pk4_fp8(y1[0], y1[1], y1[2], y1[3]); *(unsigned*)(p8 + 8) = pk4_fp8(y2[0], y2[1], y2[2], y2[3]); }
;                     else { bf16_t* p = dst + (size_t)row * 256 + wc * 64 + 32 * bj + dbase;
;                         store8(p, x1 * c - x2 * sn); store8(p + 8, x1 * sn + x2 * c); }
.LBB0_467:
	v_mul_f32_e32 v161, v23, v23
	v_fmac_f32_e32 v161, v22, v22
	v_fmac_f32_e32 v161, v24, v24
	v_fmac_f32_e32 v161, v25, v25
	v_fmac_f32_e32 v161, v18, v18
	v_fmac_f32_e32 v161, v19, v19
	v_fmac_f32_e32 v161, v20, v20
	v_fmac_f32_e32 v161, v21, v21
	v_mov_b32_e32 v162, v161
	s_nop 1
	v_permlane16_swap_b32_e32 v161, v162
	v_add_f32_e32 v161, v161, v162
	v_mov_b32_e32 v162, v161
	s_nop 1
	v_permlane32_swap_b32_e32 v161, v162
	v_add_f32_e32 v161, v161, v162
	v_fmamk_f32 v161, v161, 0x37000000, v187
	v_rsq_f32_e32 v161, v161
	s_mov_b64 s[52:53], -1
	s_and_b64 vcc, exec, s[6:7]
	v_mul_f32_e32 v166, s40, v161
	v_pk_mul_f32 v[168:169], v[20:21], v[166:167] op_sel_hi:[1,0]
	v_pk_mul_f32 v[170:171], v[18:19], v[166:167] op_sel_hi:[1,0]
	v_pk_mul_f32 v[162:163], v[24:25], v[166:167] op_sel_hi:[1,0]
	v_pk_mul_f32 v[164:165], v[22:23], v[166:167] op_sel_hi:[1,0]
	v_pk_mul_f32 v[166:167], v[132:133], v[168:169]
	v_pk_mul_f32 v[172:173], v[130:131], v[170:171]
	v_pk_mul_f32 v[162:163], v[136:137], v[162:163]
	v_pk_mul_f32 v[164:165], v[134:135], v[164:165]
	v_pk_mul_f32 v[168:169], v[140:141], v[166:167]
	v_pk_mul_f32 v[170:171], v[138:139], v[172:173]
	v_pk_fma_f32 v[168:169], v[144:145], v[162:163], v[168:169] neg_lo:[0,0,1] neg_hi:[0,0,1]
	v_pk_fma_f32 v[170:171], v[142:143], v[164:165], v[170:171] neg_lo:[0,0,1] neg_hi:[0,0,1]
	v_pk_mul_f32 v[142:143], v[142:143], v[172:173]
	s_cbranch_vccz .LBB0_469
	s_nop 0
	v_cvt_pk_fp8_f32 v161, v170, v171
	v_pk_fma_f32 v[176:177], v[138:139], v[164:165], v[142:143]
	v_pk_mul_f32 v[172:173], v[144:145], v[166:167]
	s_mov_b64 s[52:53], 0
	v_cvt_pk_fp8_f32 v161, v168, v169 op_sel:[0,0,1]
	v_pk_fma_f32 v[172:173], v[140:141], v[162:163], v[172:173]
	global_store_dword v[150:151], v161, off offset:32
	s_nop 0
	v_cvt_pk_fp8_f32 v161, v176, v177
	v_cvt_pk_fp8_f32 v161, v172, v173 op_sel:[0,0,1]
	global_store_dword v[150:151], v161, off offset:40

; #define LAS __attribute__((address_space(3)))
; DI unsigned pk4_fp8(float a, float b, float c, float d) { int r = 0; r = __builtin_amdgcn_cvt_pk_fp8_f32(a, b, r, false); r = __builtin_amdgcn_cvt_pk_fp8_f32(c, d, r, true); return (unsigned)r; }
; DI void store8(bf16_t* p, f32x4 a) { u32x2 w; w.x = pk2(a[0], a[1]); w.y = pk2(a[2], a[3]); *(u32x2*)p = w; }
;     DI void head32x2(const AccT& acc, int rbase, int wc, int fq, bf16_t* dst, const float* gain, float scale, const bool F8) const {
;     ...
;             for (int m = 0; m < 4; ++m) {
;                 const int row = rbase + 128 * ai + 16 * m;
;                 const bool lat = row < NLAT; const int t = row & (SEQ - 1);
;                 const int pos = lat ? ((fq >> 1) ? (t & 63) : (t >> 6)) : 64;
;                 const f32x4 c = *(LAS const f32x4*)(cs8 + pos * 8 + 4 * (fq & 1)), sn = *(LAS const f32x4*)(sn8 + pos * 8 + 4 * (fq & 1));
; #pragma unroll
;                 for (int bj = 0; bj < 2; ++bj) {
;                     float ss = 0.f;
; #pragma unroll
;                     for (int n = 0; n < 2; ++n)
; #pragma unroll
;                         for (int i = 0; i < 4; ++i) ss += acc[ai][bj][m][n][i] * acc[ai][bj][m][n][i];
;                     ss = sum_x16_x32(ss);
;                     const float rinv = __builtin_amdgcn_rsqf(ss * (W8_INV * W8_INV / 32.0f) + EPS) * (scale * W8_INV);
;                     const f32x4 x1 = acc[ai][bj][m][0] * rinv * g0, x2 = acc[ai][bj][m][1] * rinv * g1;
;                     if (F8) { unsigned char* p8 = (unsigned char*)dst + (size_t)row * 256 + wc * 64 + 32 * bj + dbase; const f32x4 y1 = x1 * c - x2 * sn, y2 = x1 * sn + x2 * c;
;                         *(unsigned*)p8 = pk4_fp8(y1[0], y1[1], y1[2], y1[3]); *(unsigned*)(p8 + 8) = pk4_fp8(y2[0], y2[1], y2[2], y2[3]); }
;                     else { bf16_t* p = dst + (size_t)row * 256 + wc * 64 + 32 * bj + dbase;
;                         store8(p, x1 * c - x2 * sn); store8(p + 8, x1 * sn + x2 * c); }
.LBB0_471:
	v_mul_f32_e32 v151, v15, v15
	v_fmac_f32_e32 v151, v14, v14
	v_fmac_f32_e32 v151, v16, v16
	v_fmac_f32_e32 v151, v17, v17
	v_fmac_f32_e32 v151, v10, v10
	v_fmac_f32_e32 v151, v11, v11
	v_fmac_f32_e32 v151, v12, v12
	v_fmac_f32_e32 v151, v13, v13
	v_mov_b32_e32 v152, v151
	v_add_u32_e32 v150, 0xb0, v160
	s_nop 0
	v_permlane16_swap_b32_e32 v151, v152
	v_lshrrev_b32_e32 v138, 6, v150
	v_add_f32_e32 v151, v151, v152
	v_cndmask_b32_e64 v138, v150, v138, s[4:5]
	v_mov_b32_e32 v152, v151
	v_lshlrev_b32_e32 v138, 3, v138
	s_nop 0
	v_permlane32_swap_b32_e32 v151, v152
	v_and_b32_e32 v138, 0x1f8, v138
	v_cmp_gt_i32_e32 vcc, s91, v160
	v_add_f32_e32 v151, v151, v152
	v_fmamk_f32 v151, v151, 0x37000000, v187
	v_cndmask_b32_e32 v138, v188, v138, vcc
	v_lshlrev_b32_e32 v138, 2, v138
	v_rsq_f32_e32 v161, v151
	v_add_u32_e32 v139, v174, v138
	v_add_u32_e32 v138, v175, v138
	ds_read_b128 v[142:145], v139
	ds_read_b128 v[138:141], v138
	v_ashrrev_i32_e32 v151, 31, v150
	v_mul_f32_e32 v164, s40, v161
	v_lshlrev_b64 v[152:153], 8, v[150:151]
	v_pk_mul_f32 v[166:167], v[12:13], v[164:165] op_sel_hi:[1,0]
	v_pk_mul_f32 v[168:169], v[10:11], v[164:165] op_sel_hi:[1,0]
	v_lshl_add_u64 v[146:147], v[146:147], 0, v[152:153]
	v_pk_mul_f32 v[152:153], v[16:17], v[164:165] op_sel_hi:[1,0]
	v_pk_mul_f32 v[162:163], v[14:15], v[164:165] op_sel_hi:[1,0]
	v_pk_mul_f32 v[164:165], v[132:133], v[166:167]
	v_pk_mul_f32 v[166:167], v[130:131], v[168:169]
	v_pk_mul_f32 v[152:153], v[136:137], v[152:153]
	v_pk_mul_f32 v[162:163], v[134:135], v[162:163]
	s_waitcnt lgkmcnt(0)
	v_pk_mul_f32 v[168:169], v[140:141], v[164:165]
	v_pk_mul_f32 v[170:171], v[138:139], v[166:167]
	v_pk_fma_f32 v[168:169], v[144:145], v[152:153], v[168:169] neg_lo:[0,0,1] neg_hi:[0,0,1]
	v_pk_fma_f32 v[170:171], v[142:143], v[162:163], v[170:171] neg_lo:[0,0,1] neg_hi:[0,0,1]
	s_mov_b64 s[4:5], -1
	s_and_b64 vcc, exec, s[6:7]
	v_pk_mul_f32 v[166:167], v[142:143], v[166:167]
	s_cbranch_vccz .LBB0_473
	s_nop 0
	v_cvt_pk_fp8_f32 v161, v170, v171
	v_pk_fma_f32 v[174:175], v[138:139], v[162:163], v[166:167]
	v_pk_mul_f32 v[172:173], v[144:145], v[164:165]
	s_mov_b64 s[4:5], 0
	v_cvt_pk_fp8_f32 v161, v168, v169 op_sel:[0,0,1]
	v_pk_fma_f32 v[172:173], v[140:141], v[152:153], v[172:173]
	global_store_dword v[146:147], v161, off
	s_nop 0
	v_cvt_pk_fp8_f32 v161, v174, v175
	v_cvt_pk_fp8_f32 v161, v172, v173 op_sel:[0,0,1]
	global_store_dword v[146:147], v161, off offset:8

; DI unsigned pk4_fp8(float a, float b, float c, float d) { int r = 0; r = __builtin_amdgcn_cvt_pk_fp8_f32(a, b, r, false); r = __builtin_amdgcn_cvt_pk_fp8_f32(c, d, r, true); return (unsigned)r; }
; DI void store8(bf16_t* p, f32x4 a) { u32x2 w; w.x = pk2(a[0], a[1]); w.y = pk2(a[2], a[3]); *(u32x2*)p = w; }
;     DI void head32x2(const AccT& acc, int rbase, int wc, int fq, bf16_t* dst, const float* gain, float scale, const bool F8) const {
;     ...
;                 for (int bj = 0; bj < 2; ++bj) {
;                     float ss = 0.f;
; #pragma unroll
;                     for (int n = 0; n < 2; ++n)
; #pragma unroll
;                         for (int i = 0; i < 4; ++i) ss += acc[ai][bj][m][n][i] * acc[ai][bj][m][n][i];
;                     ss = sum_x16_x32(ss);
;                     const float rinv = __builtin_amdgcn_rsqf(ss * (W8_INV * W8_INV / 32.0f) + EPS) * (scale * W8_INV);
;                     const f32x4 x1 = acc[ai][bj][m][0] * rinv * g0, x2 = acc[ai][bj][m][1] * rinv * g1;
;                     if (F8) { unsigned char* p8 = (unsigned char*)dst + (size_t)row * 256 + wc * 64 + 32 * bj + dbase; const f32x4 y1 = x1 * c - x2 * sn, y2 = x1 * sn + x2 * c;
;                         *(unsigned*)p8 = pk4_fp8(y1[0], y1[1], y1[2], y1[3]); *(unsigned*)(p8 + 8) = pk4_fp8(y2[0], y2[1], y2[2], y2[3]); }
;                     else { bf16_t* p = dst + (size_t)row * 256 + wc * 64 + 32 * bj + dbase;
;                         store8(p, x1 * c - x2 * sn); store8(p + 8, x1 * sn + x2 * c); }
.LBB0_475:
	v_mul_f32_e32 v150, v7, v7
	v_fmac_f32_e32 v150, v6, v6
	v_fmac_f32_e32 v150, v8, v8
	v_fmac_f32_e32 v150, v9, v9
	v_fmac_f32_e32 v150, v2, v2
	v_fmac_f32_e32 v150, v3, v3
	v_fmac_f32_e32 v150, v4, v4
	v_fmac_f32_e32 v150, v5, v5
	v_mov_b32_e32 v151, v150
	s_nop 1
	v_permlane16_swap_b32_e32 v150, v151
	v_add_f32_e32 v150, v150, v151
	v_mov_b32_e32 v151, v150
	s_nop 1
	v_permlane32_swap_b32_e32 v150, v151
	v_add_f32_e32 v150, v150, v151
	v_fmamk_f32 v150, v150, 0x37000000, v187
	v_rsq_f32_e32 v150, v150
	s_mov_b64 s[4:5], -1
	s_and_b64 vcc, exec, s[6:7]
	v_mul_f32_e32 v150, s40, v150
	v_pk_mul_f32 v[152:153], v[8:9], v[150:151] op_sel_hi:[1,0]
	v_pk_mul_f32 v[162:163], v[6:7], v[150:151] op_sel_hi:[1,0]
	v_pk_mul_f32 v[136:137], v[136:137], v[152:153]
	v_pk_mul_f32 v[152:153], v[4:5], v[150:151] op_sel_hi:[1,0]
	v_pk_mul_f32 v[150:151], v[2:3], v[150:151] op_sel_hi:[1,0]
	v_pk_mul_f32 v[132:133], v[132:133], v[152:153]
	v_pk_mul_f32 v[130:131], v[130:131], v[150:151]
	v_pk_mul_f32 v[134:135], v[134:135], v[162:163]
	v_pk_mul_f32 v[150:151], v[140:141], v[132:133]
	v_pk_mul_f32 v[152:153], v[138:139], v[130:131]
	v_pk_fma_f32 v[150:151], v[144:145], v[136:137], v[150:151] neg_lo:[0,0,1] neg_hi:[0,0,1]
	v_pk_fma_f32 v[152:153], v[142:143], v[134:135], v[152:153] neg_lo:[0,0,1] neg_hi:[0,0,1]
	v_pk_mul_f32 v[130:131], v[142:143], v[130:131]
	s_cbranch_vccz .LBB0_477
	s_nop 0
	v_cvt_pk_fp8_f32 v161, v152, v153
	v_pk_fma_f32 v[162:163], v[138:139], v[134:135], v[130:131]
	v_pk_mul_f32 v[142:143], v[144:145], v[132:133]
	s_mov_b64 s[4:5], 0
	v_cvt_pk_fp8_f32 v161, v150, v151 op_sel:[0,0,1]
	v_pk_fma_f32 v[142:143], v[140:141], v[136:137], v[142:143]
	global_store_dword v[146:147], v161, off offset:32
	s_nop 0
	v_cvt_pk_fp8_f32 v161, v162, v163
	v_cvt_pk_fp8_f32 v161, v142, v143 op_sel:[0,0,1]
	global_store_dword v[146:147], v161, off offset:40

; #define LAS __attribute__((address_space(3)))
; DI unsigned pk4_fp8(float a, float b, float c, float d) { int r = 0; r = __builtin_amdgcn_cvt_pk_fp8_f32(a, b, r, false); r = __builtin_amdgcn_cvt_pk_fp8_f32(c, d, r, true); return (unsigned)r; }
; DI void store8(bf16_t* p, f32x4 a) { u32x2 w; w.x = pk2(a[0], a[1]); w.y = pk2(a[2], a[3]); *(u32x2*)p = w; }
;     DI void head64(const AccT& acc, int rbase, int wc, int fq, bf16_t* dst, int pitch, const float* gain, float scale, const bool F8) const {
;     ...
;                 const float rinv = __builtin_amdgcn_rsqf(ss * (W8_INV * W8_INV / 64.0f) + EPS) * (scale * W8_INV);
;                 const bool lat = row < NLAT; const int t = row & (SEQ - 1);
; #pragma unroll
;                 for (int bj = 0; bj < 2; ++bj) {
;                     const f32x4 x1 = acc[ai][bj][m][0] * rinv * g[bj][0], x2 = acc[ai][bj][m][1] * rinv * g[bj][1];
;                     const int pos = lat ? (bj ? (t & 63) : (t >> 6)) : 64;
;                     const f32x4 c = *(LAS const f32x4*)(cs16 + pos * 16 + 4 * fq), sn = *(LAS const f32x4*)(sn16 + pos * 16 + 4 * fq);
;                     if (F8) { unsigned char* p8 = (unsigned char*)dst + (size_t)row * pitch + wc * 64 + 32 * bj + 4 * fq; const f32x4 y1 = x1 * c - x2 * sn, y2 = x1 * sn + x2 * c;
;                         *(unsigned*)p8 = pk4_fp8(y1[0], y1[1], y1[2], y1[3]); *(unsigned*)(p8 + 16) = pk4_fp8(y2[0], y2[1], y2[2], y2[3]); }
;                     else { bf16_t* p = dst + (size_t)row * pitch + wc * 64 + 32 * bj + 4 * fq;
;                         store8(p, x1 * c - x2 * sn); store8(p + 16, x1 * sn + x2 * c); }
.LBB0_495:
	v_lshl_add_u64 v[164:165], s[52:53], 0, v[164:165]
	s_andn2_b64 vcc, exec, s[54:55]
	v_lshl_add_u64 v[176:177], v[164:165], 0, v[176:177]
	s_cbranch_vccnz .LBB0_497
	v_pk_fma_f32 v[146:147], v[146:147], v[174:175], v[150:151]
	s_nop 0
	v_cvt_pk_fp8_f32 v150, v182, v183
	s_nop 0
	v_cvt_pk_fp8_f32 v151, v146, v147
	v_pk_mul_f32 v[146:147], v[152:153], v[170:171]
	v_cvt_pk_fp8_f32 v150, v178, v179 op_sel:[0,0,1]
	v_pk_fma_f32 v[146:147], v[148:149], v[172:173], v[146:147]
	s_nop 0
	v_cvt_pk_fp8_f32 v151, v146, v147 op_sel:[0,0,1]
	global_store_dword v[176:177], v150, off
	global_store_dword v[176:177], v151, off offset:16

; #define LAS __attribute__((address_space(3)))
; DI unsigned pk4_fp8(float a, float b, float c, float d) { int r = 0; r = __builtin_amdgcn_cvt_pk_fp8_f32(a, b, r, false); r = __builtin_amdgcn_cvt_pk_fp8_f32(c, d, r, true); return (unsigned)r; }
; DI void store8(bf16_t* p, f32x4 a) { u32x2 w; w.x = pk2(a[0], a[1]); w.y = pk2(a[2], a[3]); *(u32x2*)p = w; }
;     DI void head64(const AccT& acc, int rbase, int wc, int fq, bf16_t* dst, int pitch, const float* gain, float scale, const bool F8) const {
;     ...
;                 const float rinv = __builtin_amdgcn_rsqf(ss * (W8_INV * W8_INV / 64.0f) + EPS) * (scale * W8_INV);
;                 const bool lat = row < NLAT; const int t = row & (SEQ - 1);
; #pragma unroll
;                 for (int bj = 0; bj < 2; ++bj) {
;                     const f32x4 x1 = acc[ai][bj][m][0] * rinv * g[bj][0], x2 = acc[ai][bj][m][1] * rinv * g[bj][1];
;                     const int pos = lat ? (bj ? (t & 63) : (t >> 6)) : 64;
;                     const f32x4 c = *(LAS const f32x4*)(cs16 + pos * 16 + 4 * fq), sn = *(LAS const f32x4*)(sn16 + pos * 16 + 4 * fq);
;                     if (F8) { unsigned char* p8 = (unsigned char*)dst + (size_t)row * pitch + wc * 64 + 32 * bj + 4 * fq; const f32x4 y1 = x1 * c - x2 * sn, y2 = x1 * sn + x2 * c;
;                         *(unsigned*)p8 = pk4_fp8(y1[0], y1[1], y1[2], y1[3]); *(unsigned*)(p8 + 16) = pk4_fp8(y2[0], y2[1], y2[2], y2[3]); }
;                     else { bf16_t* p = dst + (size_t)row * pitch + wc * 64 + 32 * bj + 4 * fq;
;                         store8(p, x1 * c - x2 * sn); store8(p + 16, x1 * sn + x2 * c); }
.LBB0_499:
	s_andn2_b64 vcc, exec, s[52:53]
	s_mov_b64 s[6:7], 8
	s_cbranch_vccnz .LBB0_501
	v_pk_fma_f32 v[146:147], v[174:175], v[146:147], v[150:151]
	s_nop 0
	v_cvt_pk_fp8_f32 v150, v178, v179
	s_nop 0
	v_cvt_pk_fp8_f32 v151, v146, v147
	v_pk_mul_f32 v[146:147], v[170:171], v[152:153]
	v_cvt_pk_fp8_f32 v150, v172, v173 op_sel:[0,0,1]
	v_pk_fma_f32 v[146:147], v[166:167], v[148:149], v[146:147]
	s_mov_b64 s[6:7], 7
	v_cvt_pk_fp8_f32 v151, v146, v147 op_sel:[0,0,1]
	global_store_dword v[176:177], v150, off offset:32
	global_store_dword v[176:177], v151, off offset:48

; #define LAS __attribute__((address_space(3)))
; DI unsigned pk4_fp8(float a, float b, float c, float d) { int r = 0; r = __builtin_amdgcn_cvt_pk_fp8_f32(a, b, r, false); r = __builtin_amdgcn_cvt_pk_fp8_f32(c, d, r, true); return (unsigned)r; }
; DI void store8(bf16_t* p, f32x4 a) { u32x2 w; w.x = pk2(a[0], a[1]); w.y = pk2(a[2], a[3]); *(u32x2*)p = w; }
;     DI void head64(const AccT& acc, int rbase, int wc, int fq, bf16_t* dst, int pitch, const float* gain, float scale, const bool F8) const {
;     ...
;                 const float rinv = __builtin_amdgcn_rsqf(ss * (W8_INV * W8_INV / 64.0f) + EPS) * (scale * W8_INV);
;                 const bool lat = row < NLAT; const int t = row & (SEQ - 1);
; #pragma unroll
;                 for (int bj = 0; bj < 2; ++bj) {
;                     const f32x4 x1 = acc[ai][bj][m][0] * rinv * g[bj][0], x2 = acc[ai][bj][m][1] * rinv * g[bj][1];
;                     const int pos = lat ? (bj ? (t & 63) : (t >> 6)) : 64;
;                     const f32x4 c = *(LAS const f32x4*)(cs16 + pos * 16 + 4 * fq), sn = *(LAS const f32x4*)(sn16 + pos * 16 + 4 * fq);
;                     if (F8) { unsigned char* p8 = (unsigned char*)dst + (size_t)row * pitch + wc * 64 + 32 * bj + 4 * fq; const f32x4 y1 = x1 * c - x2 * sn, y2 = x1 * sn + x2 * c;
;                         *(unsigned*)p8 = pk4_fp8(y1[0], y1[1], y1[2], y1[3]); *(unsigned*)(p8 + 16) = pk4_fp8(y2[0], y2[1], y2[2], y2[3]); }
;                     else { bf16_t* p = dst + (size_t)row * pitch + wc * 64 + 32 * bj + 4 * fq;
;                         store8(p, x1 * c - x2 * sn); store8(p + 16, x1 * sn + x2 * c); }
.LBB0_503:
	s_andn2_b64 vcc, exec, s[52:53]
	v_lshl_add_u64 v[172:173], v[164:165], 0, v[172:173]
	s_cbranch_vccnz .LBB0_505
	v_pk_fma_f32 v[146:147], v[146:147], v[180:181], v[150:151]
	s_nop 0
	v_cvt_pk_fp8_f32 v150, v182, v183
	s_nop 0
	v_cvt_pk_fp8_f32 v151, v146, v147
	v_pk_mul_f32 v[146:147], v[152:153], v[174:175]
	v_cvt_pk_fp8_f32 v150, v178, v179 op_sel:[0,0,1]
	v_pk_fma_f32 v[146:147], v[148:149], v[176:177], v[146:147]
	s_nop 0
	v_cvt_pk_fp8_f32 v151, v146, v147 op_sel:[0,0,1]
	global_store_dword v[172:173], v150, off
	global_store_dword v[172:173], v151, off offset:16

; #define LAS __attribute__((address_space(3)))
; DI unsigned pk4_fp8(float a, float b, float c, float d) { int r = 0; r = __builtin_amdgcn_cvt_pk_fp8_f32(a, b, r, false); r = __builtin_amdgcn_cvt_pk_fp8_f32(c, d, r, true); return (unsigned)r; }
; DI void store8(bf16_t* p, f32x4 a) { u32x2 w; w.x = pk2(a[0], a[1]); w.y = pk2(a[2], a[3]); *(u32x2*)p = w; }
;     DI void head64(const AccT& acc, int rbase, int wc, int fq, bf16_t* dst, int pitch, const float* gain, float scale, const bool F8) const {
;     ...
;                 const float rinv = __builtin_amdgcn_rsqf(ss * (W8_INV * W8_INV / 64.0f) + EPS) * (scale * W8_INV);
;                 const bool lat = row < NLAT; const int t = row & (SEQ - 1);
; #pragma unroll
;                 for (int bj = 0; bj < 2; ++bj) {
;                     const f32x4 x1 = acc[ai][bj][m][0] * rinv * g[bj][0], x2 = acc[ai][bj][m][1] * rinv * g[bj][1];
;                     const int pos = lat ? (bj ? (t & 63) : (t >> 6)) : 64;
;                     const f32x4 c = *(LAS const f32x4*)(cs16 + pos * 16 + 4 * fq), sn = *(LAS const f32x4*)(sn16 + pos * 16 + 4 * fq);
;                     if (F8) { unsigned char* p8 = (unsigned char*)dst + (size_t)row * pitch + wc * 64 + 32 * bj + 4 * fq; const f32x4 y1 = x1 * c - x2 * sn, y2 = x1 * sn + x2 * c;
;                         *(unsigned*)p8 = pk4_fp8(y1[0], y1[1], y1[2], y1[3]); *(unsigned*)(p8 + 16) = pk4_fp8(y2[0], y2[1], y2[2], y2[3]); }
;                     else { bf16_t* p = dst + (size_t)row * pitch + wc * 64 + 32 * bj + 4 * fq;
;                         store8(p, x1 * c - x2 * sn); store8(p + 16, x1 * sn + x2 * c); }
.LBB0_507:
	s_andn2_b64 vcc, exec, s[6:7]
	s_mov_b64 s[6:7], 8
	s_cbranch_vccnz .LBB0_509
	v_pk_fma_f32 v[146:147], v[176:177], v[146:147], v[150:151]
	s_nop 0
	v_cvt_pk_fp8_f32 v150, v178, v179
	s_nop 0
	v_cvt_pk_fp8_f32 v151, v146, v147
	v_pk_mul_f32 v[146:147], v[174:175], v[152:153]
	v_cvt_pk_fp8_f32 v150, v170, v171 op_sel:[0,0,1]
	v_pk_fma_f32 v[146:147], v[168:169], v[148:149], v[146:147]
	s_mov_b64 s[6:7], 7
	v_cvt_pk_fp8_f32 v151, v146, v147 op_sel:[0,0,1]
	global_store_dword v[172:173], v150, off offset:32
	global_store_dword v[172:173], v151, off offset:48

; #define LAS __attribute__((address_space(3)))
; DI unsigned pk4_fp8(float a, float b, float c, float d) { int r = 0; r = __builtin_amdgcn_cvt_pk_fp8_f32(a, b, r, false); r = __builtin_amdgcn_cvt_pk_fp8_f32(c, d, r, true); return (unsigned)r; }
; DI void store8(bf16_t* p, f32x4 a) { u32x2 w; w.x = pk2(a[0], a[1]); w.y = pk2(a[2], a[3]); *(u32x2*)p = w; }
;     DI void head64(const AccT& acc, int rbase, int wc, int fq, bf16_t* dst, int pitch, const float* gain, float scale, const bool F8) const {
;     ...
;                 const float rinv = __builtin_amdgcn_rsqf(ss * (W8_INV * W8_INV / 64.0f) + EPS) * (scale * W8_INV);
;                 const bool lat = row < NLAT; const int t = row & (SEQ - 1);
; #pragma unroll
;                 for (int bj = 0; bj < 2; ++bj) {
;                     const f32x4 x1 = acc[ai][bj][m][0] * rinv * g[bj][0], x2 = acc[ai][bj][m][1] * rinv * g[bj][1];
;                     const int pos = lat ? (bj ? (t & 63) : (t >> 6)) : 64;
;                     const f32x4 c = *(LAS const f32x4*)(cs16 + pos * 16 + 4 * fq), sn = *(LAS const f32x4*)(sn16 + pos * 16 + 4 * fq);
;                     if (F8) { unsigned char* p8 = (unsigned char*)dst + (size_t)row * pitch + wc * 64 + 32 * bj + 4 * fq; const f32x4 y1 = x1 * c - x2 * sn, y2 = x1 * sn + x2 * c;
;                         *(unsigned*)p8 = pk4_fp8(y1[0], y1[1], y1[2], y1[3]); *(unsigned*)(p8 + 16) = pk4_fp8(y2[0], y2[1], y2[2], y2[3]); }
;                     else { bf16_t* p = dst + (size_t)row * pitch + wc * 64 + 32 * bj + 4 * fq;
;                         store8(p, x1 * c - x2 * sn); store8(p + 16, x1 * sn + x2 * c); }
.LBB0_527:
	s_andn2_b64 vcc, exec, s[52:53]
	v_lshl_add_u64 v[170:171], v[164:165], 0, v[170:171]
	s_cbranch_vccnz .LBB0_529
	v_pk_fma_f32 v[146:147], v[146:147], v[178:179], v[150:151]
	s_nop 0
	v_cvt_pk_fp8_f32 v150, v180, v181
	s_nop 0
	v_cvt_pk_fp8_f32 v151, v146, v147
	v_pk_mul_f32 v[146:147], v[152:153], v[172:173]
	v_cvt_pk_fp8_f32 v150, v176, v177 op_sel:[0,0,1]
	v_pk_fma_f32 v[146:147], v[148:149], v[174:175], v[146:147]
	s_nop 0
	v_cvt_pk_fp8_f32 v151, v146, v147 op_sel:[0,0,1]
	global_store_dword v[170:171], v150, off
	global_store_dword v[170:171], v151, off offset:16

; #define LAS __attribute__((address_space(3)))
; DI unsigned pk4_fp8(float a, float b, float c, float d) { int r = 0; r = __builtin_amdgcn_cvt_pk_fp8_f32(a, b, r, false); r = __builtin_amdgcn_cvt_pk_fp8_f32(c, d, r, true); return (unsigned)r; }
; DI void store8(bf16_t* p, f32x4 a) { u32x2 w; w.x = pk2(a[0], a[1]); w.y = pk2(a[2], a[3]); *(u32x2*)p = w; }
;     DI void head64(const AccT& acc, int rbase, int wc, int fq, bf16_t* dst, int pitch, const float* gain, float scale, const bool F8) const {
;     ...
;                 const float rinv = __builtin_amdgcn_rsqf(ss * (W8_INV * W8_INV / 64.0f) + EPS) * (scale * W8_INV);
;                 const bool lat = row < NLAT; const int t = row & (SEQ - 1);
; #pragma unroll
;                 for (int bj = 0; bj < 2; ++bj) {
;                     const f32x4 x1 = acc[ai][bj][m][0] * rinv * g[bj][0], x2 = acc[ai][bj][m][1] * rinv * g[bj][1];
;                     const int pos = lat ? (bj ? (t & 63) : (t >> 6)) : 64;
;                     const f32x4 c = *(LAS const f32x4*)(cs16 + pos * 16 + 4 * fq), sn = *(LAS const f32x4*)(sn16 + pos * 16 + 4 * fq);
;                     if (F8) { unsigned char* p8 = (unsigned char*)dst + (size_t)row * pitch + wc * 64 + 32 * bj + 4 * fq; const f32x4 y1 = x1 * c - x2 * sn, y2 = x1 * sn + x2 * c;
;                         *(unsigned*)p8 = pk4_fp8(y1[0], y1[1], y1[2], y1[3]); *(unsigned*)(p8 + 16) = pk4_fp8(y2[0], y2[1], y2[2], y2[3]); }
;                     else { bf16_t* p = dst + (size_t)row * pitch + wc * 64 + 32 * bj + 4 * fq;
;                         store8(p, x1 * c - x2 * sn); store8(p + 16, x1 * sn + x2 * c); }
.LBB0_531:
	s_andn2_b64 vcc, exec, s[6:7]
	s_mov_b64 s[6:7], 8
	s_cbranch_vccnz .LBB0_533
	v_pk_fma_f32 v[146:147], v[176:177], v[146:147], v[150:151]
	s_nop 0
	v_cvt_pk_fp8_f32 v150, v178, v179
	s_nop 0
	v_cvt_pk_fp8_f32 v151, v146, v147
	v_pk_mul_f32 v[146:147], v[172:173], v[152:153]
	v_cvt_pk_fp8_f32 v150, v174, v175 op_sel:[0,0,1]
	v_pk_fma_f32 v[146:147], v[168:169], v[148:149], v[146:147]
	s_mov_b64 s[6:7], 7
	v_cvt_pk_fp8_f32 v151, v146, v147 op_sel:[0,0,1]
	global_store_dword v[170:171], v150, off offset:32
	global_store_dword v[170:171], v151, off offset:48

; #define LAS __attribute__((address_space(3)))
; DI unsigned pk4_fp8(float a, float b, float c, float d) { int r = 0; r = __builtin_amdgcn_cvt_pk_fp8_f32(a, b, r, false); r = __builtin_amdgcn_cvt_pk_fp8_f32(c, d, r, true); return (unsigned)r; }
; DI void store8(bf16_t* p, f32x4 a) { u32x2 w; w.x = pk2(a[0], a[1]); w.y = pk2(a[2], a[3]); *(u32x2*)p = w; }
;     DI void head64(const AccT& acc, int rbase, int wc, int fq, bf16_t* dst, int pitch, const float* gain, float scale, const bool F8) const {
;     ...
;                 const float rinv = __builtin_amdgcn_rsqf(ss * (W8_INV * W8_INV / 64.0f) + EPS) * (scale * W8_INV);
;                 const bool lat = row < NLAT; const int t = row & (SEQ - 1);
; #pragma unroll
;                 for (int bj = 0; bj < 2; ++bj) {
;                     const f32x4 x1 = acc[ai][bj][m][0] * rinv * g[bj][0], x2 = acc[ai][bj][m][1] * rinv * g[bj][1];
;                     const int pos = lat ? (bj ? (t & 63) : (t >> 6)) : 64;
;                     const f32x4 c = *(LAS const f32x4*)(cs16 + pos * 16 + 4 * fq), sn = *(LAS const f32x4*)(sn16 + pos * 16 + 4 * fq);
;                     if (F8) { unsigned char* p8 = (unsigned char*)dst + (size_t)row * pitch + wc * 64 + 32 * bj + 4 * fq; const f32x4 y1 = x1 * c - x2 * sn, y2 = x1 * sn + x2 * c;
;                         *(unsigned*)p8 = pk4_fp8(y1[0], y1[1], y1[2], y1[3]); *(unsigned*)(p8 + 16) = pk4_fp8(y2[0], y2[1], y2[2], y2[3]); }
;                     else { bf16_t* p = dst + (size_t)row * pitch + wc * 64 + 32 * bj + 4 * fq;
;                         store8(p, x1 * c - x2 * sn); store8(p + 16, x1 * sn + x2 * c); }
.LBB0_551:
	s_andn2_b64 vcc, exec, s[52:53]
	v_lshl_add_u64 v[146:147], v[164:165], 0, v[168:169]
	s_cbranch_vccnz .LBB0_553
	s_nop 0
	v_pk_fma_f32 v[142:143], v[142:143], v[170:171], v[174:175]
	v_cvt_pk_fp8_f32 v153, v172, v173
	s_nop 0
	v_cvt_pk_fp8_f32 v161, v142, v143
	v_pk_mul_f32 v[142:143], v[148:149], v[162:163]
	v_cvt_pk_fp8_f32 v153, v138, v139 op_sel:[0,0,1]
	v_pk_fma_f32 v[140:141], v[144:145], v[140:141], v[142:143]
	s_nop 0
	v_cvt_pk_fp8_f32 v161, v140, v141 op_sel:[0,0,1]
	global_store_dword v[146:147], v153, off
	global_store_dword v[146:147], v161, off offset:16

; #define LAS __attribute__((address_space(3)))
; DI unsigned pk4_fp8(float a, float b, float c, float d) { int r = 0; r = __builtin_amdgcn_cvt_pk_fp8_f32(a, b, r, false); r = __builtin_amdgcn_cvt_pk_fp8_f32(c, d, r, true); return (unsigned)r; }
; DI void store8(bf16_t* p, f32x4 a) { u32x2 w; w.x = pk2(a[0], a[1]); w.y = pk2(a[2], a[3]); *(u32x2*)p = w; }
;     DI void head64(const AccT& acc, int rbase, int wc, int fq, bf16_t* dst, int pitch, const float* gain, float scale, const bool F8) const {
;     ...
;                 const float rinv = __builtin_amdgcn_rsqf(ss * (W8_INV * W8_INV / 64.0f) + EPS) * (scale * W8_INV);
;                 const bool lat = row < NLAT; const int t = row & (SEQ - 1);
; #pragma unroll
;                 for (int bj = 0; bj < 2; ++bj) {
;                     const f32x4 x1 = acc[ai][bj][m][0] * rinv * g[bj][0], x2 = acc[ai][bj][m][1] * rinv * g[bj][1];
;                     const int pos = lat ? (bj ? (t & 63) : (t >> 6)) : 64;
;                     const f32x4 c = *(LAS const f32x4*)(cs16 + pos * 16 + 4 * fq), sn = *(LAS const f32x4*)(sn16 + pos * 16 + 4 * fq);
;                     if (F8) { unsigned char* p8 = (unsigned char*)dst + (size_t)row * pitch + wc * 64 + 32 * bj + 4 * fq; const f32x4 y1 = x1 * c - x2 * sn, y2 = x1 * sn + x2 * c;
;                         *(unsigned*)p8 = pk4_fp8(y1[0], y1[1], y1[2], y1[3]); *(unsigned*)(p8 + 16) = pk4_fp8(y2[0], y2[1], y2[2], y2[3]); }
;                     else { bf16_t* p = dst + (size_t)row * pitch + wc * 64 + 32 * bj + 4 * fq;
;                         store8(p, x1 * c - x2 * sn); store8(p + 16, x1 * sn + x2 * c); }
.LBB0_555:
	s_andn2_b64 vcc, exec, s[6:7]
	s_cbranch_vccnz .LBB0_557
	v_pk_fma_f32 v[134:135], v[144:145], v[134:135], v[138:139]
	s_nop 0
	v_cvt_pk_fp8_f32 v138, v148, v149
	s_nop 0
	v_cvt_pk_fp8_f32 v139, v134, v135
	v_pk_mul_f32 v[134:135], v[142:143], v[140:141]
	v_cvt_pk_fp8_f32 v138, v130, v131 op_sel:[0,0,1]
	v_pk_fma_f32 v[132:133], v[132:133], v[136:137], v[134:135]
	s_nop 0
	v_cvt_pk_fp8_f32 v139, v132, v133 op_sel:[0,0,1]
	global_store_dword v[146:147], v138, off offset:32
	global_store_dword v[146:147], v139, off offset:48

; DI unsigned pk4_fp8(float a, float b, float c, float d) { int r = 0; r = __builtin_amdgcn_cvt_pk_fp8_f32(a, b, r, false); r = __builtin_amdgcn_cvt_pk_fp8_f32(c, d, r, true); return (unsigned)r; }
;     DI void operator()(EPI_ARGS) const {
;     ...
;         const bool ctx = u.pn >= 128; const int b = ctx ? (u.pn - 128) : (u.pn >> 4); const int t0 = ctx ? 0 : (u.pn & 15) * 256;
;         bf16_t* base; size_t pitch; int tokoff;
;         if (u.pm == 0) {
;             unsigned char* vb = WSB(unsigned char, WS_VTD) + (size_t)b * 4 * 64 * KEYS; const int tko = ctx ? SEQ : t0;
; #pragma unroll
;             for (int ai = 0; ai < 2; ++ai)
; #pragma unroll
;                 for (int m = 0; m < 4; ++m) { const int lrow = 128 * ai + 64 * wr + 16 * m + fr;
; #pragma unroll
;                     for (int bj = 0; bj < 2; ++bj) { const f32x4 x0 = acc[ai][bj][m][0] * W8_INV, x1 = acc[ai][bj][m][1] * W8_INV;
;                         *(u32x2*)(vb + (size_t)lrow * KEYS + tko + 128 * bj + 32 * wc + 8 * fq) = (u32x2){pk4_fp8(x0[0], x0[1], x0[2], x0[3]), pk4_fp8(x1[0], x1[1], x1[2], x1[3])}; } }
;             return; }
.LBB0_582:
	v_pk_mul_f32 v[126:127], v[126:127], s[14:15] op_sel_hi:[1,0]
	s_nop 0
	v_cvt_pk_fp8_f32 v132, v126, v127
	s_and_b64 s[18:19], s[18:19], exec
	s_cselect_b32 s18, s20, s22
	v_pk_mul_f32 v[122:123], v[122:123], s[14:15] op_sel_hi:[1,0]
	s_nop 0
	s_mul_hi_i32 s19, s18, 0x110000
	s_mul_i32 s18, s18, 0x110000
	v_cvt_pk_fp8_f32 v133, v122, v123
	v_pk_mul_f32 v[122:123], v[128:129], s[14:15] op_sel_hi:[1,0]
	s_cselect_b32 s10, 0x1000, s67
	s_add_u32 s18, s57, s18
	v_cvt_pk_fp8_f32 v132, v122, v123 op_sel:[0,0,1]
	v_pk_mul_f32 v[118:119], v[118:119], s[14:15] op_sel_hi:[1,0]
	v_pk_mul_f32 v[110:111], v[110:111], s[14:15] op_sel_hi:[1,0]
	s_nop 0
	s_nop 0
	s_addc_u32 s19, s58, s19
	v_cvt_pk_fp8_f32 v122, v118, v119
	v_cvt_pk_fp8_f32 v123, v110, v111
	s_add_u32 s10, s18, s10
	s_addc_u32 s19, s19, 0
	v_pk_mul_f32 v[124:125], v[124:125], s[14:15] op_sel_hi:[1,0]
	s_add_u32 s18, s10, s28
	v_lshlrev_b32_e32 v130, 3, v143
	v_cvt_pk_fp8_f32 v133, v124, v125 op_sel:[0,0,1]
	v_pk_mul_f32 v[110:111], v[120:121], s[14:15] op_sel_hi:[1,0]
	v_pk_mul_f32 v[112:113], v[112:113], s[14:15] op_sel_hi:[1,0]
	s_addc_u32 s19, s19, 0
	v_ashrrev_i32_e32 v131, 31, v130
	v_cvt_pk_fp8_f32 v122, v110, v111 op_sel:[0,0,1]
	v_cvt_pk_fp8_f32 v123, v112, v113 op_sel:[0,0,1]
	v_add_u32_e32 v144, s45, v144
	v_lshl_add_u64 v[130:131], s[18:19], 0, v[130:131]
	v_mad_i64_i32 v[110:111], s[18:19], v144, s61, v[130:131]
	global_store_dwordx2 v[110:111], v[132:133], off
	global_store_dwordx2 v[110:111], v[122:123], off offset:128
	v_pk_mul_f32 v[110:111], v[114:115], s[14:15] op_sel_hi:[1,0]
	s_nop 0
	v_cvt_pk_fp8_f32 v112, v110, v111
	v_pk_mul_f32 v[106:107], v[106:107], s[14:15] op_sel_hi:[1,0]
	s_nop 0
	v_cvt_pk_fp8_f32 v113, v106, v107
	v_pk_mul_f32 v[106:107], v[116:117], s[14:15] op_sel_hi:[1,0]
	v_pk_mul_f32 v[102:103], v[102:103], s[14:15] op_sel_hi:[1,0]
	v_cvt_pk_fp8_f32 v112, v106, v107 op_sel:[0,0,1]
	v_pk_mul_f32 v[94:95], v[94:95], s[14:15] op_sel_hi:[1,0]
	s_nop 0
	s_nop 0
	v_cvt_pk_fp8_f32 v106, v102, v103
	v_cvt_pk_fp8_f32 v107, v94, v95
	v_pk_mul_f32 v[108:109], v[108:109], s[14:15] op_sel_hi:[1,0]
	v_pk_mul_f32 v[94:95], v[104:105], s[14:15] op_sel_hi:[1,0]
	v_cvt_pk_fp8_f32 v113, v108, v109 op_sel:[0,0,1]
	v_pk_mul_f32 v[96:97], v[96:97], s[14:15] op_sel_hi:[1,0]
	v_cvt_pk_fp8_f32 v106, v94, v95 op_sel:[0,0,1]
	v_cvt_pk_fp8_f32 v107, v96, v97 op_sel:[0,0,1]
	v_add_u32_e32 v118, 16, v144
	v_mad_i64_i32 v[94:95], s[18:19], v118, s61, v[130:131]
	global_store_dwordx2 v[94:95], v[112:113], off
	global_store_dwordx2 v[94:95], v[106:107], off offset:128
	v_pk_mul_f32 v[94:95], v[98:99], s[14:15] op_sel_hi:[1,0]
	s_nop 0
	v_cvt_pk_fp8_f32 v96, v94, v95
	v_pk_mul_f32 v[90:91], v[90:91], s[14:15] op_sel_hi:[1,0]
	s_nop 0
	v_cvt_pk_fp8_f32 v97, v90, v91
	v_pk_mul_f32 v[90:91], v[100:101], s[14:15] op_sel_hi:[1,0]
	v_pk_mul_f32 v[86:87], v[86:87], s[14:15] op_sel_hi:[1,0]
	v_cvt_pk_fp8_f32 v96, v90, v91 op_sel:[0,0,1]
	v_pk_mul_f32 v[78:79], v[78:79], s[14:15] op_sel_hi:[1,0]
	s_nop 0
	s_nop 0
	v_cvt_pk_fp8_f32 v90, v86, v87
	v_cvt_pk_fp8_f32 v91, v78, v79
	v_pk_mul_f32 v[92:93], v[92:93], s[14:15] op_sel_hi:[1,0]
	v_pk_mul_f32 v[78:79], v[88:89], s[14:15] op_sel_hi:[1,0]
	v_cvt_pk_fp8_f32 v97, v92, v93 op_sel:[0,0,1]
	v_pk_mul_f32 v[80:81], v[80:81], s[14:15] op_sel_hi:[1,0]
	v_cvt_pk_fp8_f32 v90, v78, v79 op_sel:[0,0,1]
	v_cvt_pk_fp8_f32 v91, v80, v81 op_sel:[0,0,1]
	v_add_u32_e32 v102, 32, v144
	v_mad_i64_i32 v[78:79], s[18:19], v102, s61, v[130:131]
	global_store_dwordx2 v[78:79], v[96:97], off
	global_store_dwordx2 v[78:79], v[90:91], off offset:128
	v_pk_mul_f32 v[78:79], v[82:83], s[14:15] op_sel_hi:[1,0]
	s_nop 0
	v_cvt_pk_fp8_f32 v80, v78, v79
	v_pk_mul_f32 v[74:75], v[74:75], s[14:15] op_sel_hi:[1,0]
	s_nop 0
	v_cvt_pk_fp8_f32 v81, v74, v75
	v_pk_mul_f32 v[74:75], v[84:85], s[14:15] op_sel_hi:[1,0]
	v_pk_mul_f32 v[70:71], v[70:71], s[14:15] op_sel_hi:[1,0]
	v_cvt_pk_fp8_f32 v80, v74, v75 op_sel:[0,0,1]
	v_pk_mul_f32 v[66:67], v[66:67], s[14:15] op_sel_hi:[1,0]
	s_nop 0
	s_nop 0
	v_cvt_pk_fp8_f32 v74, v70, v71
	v_cvt_pk_fp8_f32 v75, v66, v67
	v_pk_mul_f32 v[76:77], v[76:77], s[14:15] op_sel_hi:[1,0]
	v_pk_mul_f32 v[66:67], v[72:73], s[14:15] op_sel_hi:[1,0]
	v_cvt_pk_fp8_f32 v81, v76, v77 op_sel:[0,0,1]
	v_pk_mul_f32 v[68:69], v[68:69], s[14:15] op_sel_hi:[1,0]
; DI unsigned pk4_fp8(float a, float b, float c, float d) { int r = 0; r = __builtin_amdgcn_cvt_pk_fp8_f32(a, b, r, false); r = __builtin_amdgcn_cvt_pk_fp8_f32(c, d, r, true); return (unsigned)r; }
;     DI void operator()(EPI_ARGS) const {
;     ...
;             for (int ai = 0; ai < 2; ++ai)
; #pragma unroll
;                 for (int m = 0; m < 4; ++m) { const int lrow = 128 * ai + 64 * wr + 16 * m + fr;
; #pragma unroll
;                     for (int bj = 0; bj < 2; ++bj) { const f32x4 x0 = acc[ai][bj][m][0] * W8_INV, x1 = acc[ai][bj][m][1] * W8_INV;
;                         *(u32x2*)(vb + (size_t)lrow * KEYS + tko + 128 * bj + 32 * wc + 8 * fq) = (u32x2){pk4_fp8(x0[0], x0[1], x0[2], x0[3]), pk4_fp8(x1[0], x1[1], x1[2], x1[3])}; } }
;             return; }
	v_cvt_pk_fp8_f32 v74, v66, v67 op_sel:[0,0,1]
	v_cvt_pk_fp8_f32 v75, v68, v69 op_sel:[0,0,1]
	v_add_u32_e32 v86, 48, v144
	v_mad_i64_i32 v[66:67], s[18:19], v86, s61, v[130:131]
	global_store_dwordx2 v[66:67], v[80:81], off
	global_store_dwordx2 v[66:67], v[74:75], off offset:128
	v_pk_mul_f32 v[62:63], v[62:63], s[14:15] op_sel_hi:[1,0]
	s_nop 0
	v_cvt_pk_fp8_f32 v66, v62, v63
	v_pk_mul_f32 v[58:59], v[58:59], s[14:15] op_sel_hi:[1,0]
	s_nop 0
	v_cvt_pk_fp8_f32 v67, v58, v59
	v_pk_mul_f32 v[58:59], v[64:65], s[14:15] op_sel_hi:[1,0]
	v_pk_mul_f32 v[54:55], v[54:55], s[14:15] op_sel_hi:[1,0]
	v_cvt_pk_fp8_f32 v66, v58, v59 op_sel:[0,0,1]
	v_pk_mul_f32 v[46:47], v[46:47], s[14:15] op_sel_hi:[1,0]
	s_nop 0
	s_nop 0
	v_cvt_pk_fp8_f32 v58, v54, v55
	v_cvt_pk_fp8_f32 v59, v46, v47
	v_pk_mul_f32 v[60:61], v[60:61], s[14:15] op_sel_hi:[1,0]
	v_pk_mul_f32 v[46:47], v[56:57], s[14:15] op_sel_hi:[1,0]
	v_cvt_pk_fp8_f32 v67, v60, v61 op_sel:[0,0,1]
	v_pk_mul_f32 v[48:49], v[48:49], s[14:15] op_sel_hi:[1,0]
	v_cvt_pk_fp8_f32 v58, v46, v47 op_sel:[0,0,1]
	v_cvt_pk_fp8_f32 v59, v48, v49 op_sel:[0,0,1]
	v_add_u32_e32 v68, 0x80, v144
	v_mad_i64_i32 v[46:47], s[18:19], v68, s61, v[130:131]
	global_store_dwordx2 v[46:47], v[66:67], off
	global_store_dwordx2 v[46:47], v[58:59], off offset:128
	v_pk_mul_f32 v[46:47], v[50:51], s[14:15] op_sel_hi:[1,0]
	s_nop 0
	v_cvt_pk_fp8_f32 v48, v46, v47
	v_pk_mul_f32 v[42:43], v[42:43], s[14:15] op_sel_hi:[1,0]
	s_nop 0
	v_cvt_pk_fp8_f32 v49, v42, v43
	v_pk_mul_f32 v[42:43], v[52:53], s[14:15] op_sel_hi:[1,0]
	v_pk_mul_f32 v[38:39], v[38:39], s[14:15] op_sel_hi:[1,0]
	v_cvt_pk_fp8_f32 v48, v42, v43 op_sel:[0,0,1]
	v_pk_mul_f32 v[30:31], v[30:31], s[14:15] op_sel_hi:[1,0]
	s_nop 0
	s_nop 0
	v_cvt_pk_fp8_f32 v42, v38, v39
	v_cvt_pk_fp8_f32 v43, v30, v31
	v_pk_mul_f32 v[44:45], v[44:45], s[14:15] op_sel_hi:[1,0]
	v_pk_mul_f32 v[30:31], v[40:41], s[14:15] op_sel_hi:[1,0]
	v_cvt_pk_fp8_f32 v49, v44, v45 op_sel:[0,0,1]
	v_pk_mul_f32 v[32:33], v[32:33], s[14:15] op_sel_hi:[1,0]
	v_cvt_pk_fp8_f32 v42, v30, v31 op_sel:[0,0,1]
	v_cvt_pk_fp8_f32 v43, v32, v33 op_sel:[0,0,1]
	v_add_u32_e32 v54, 0x90, v144
	v_mad_i64_i32 v[30:31], s[18:19], v54, s61, v[130:131]
	global_store_dwordx2 v[30:31], v[48:49], off
	global_store_dwordx2 v[30:31], v[42:43], off offset:128
	v_pk_mul_f32 v[30:31], v[34:35], s[14:15] op_sel_hi:[1,0]
	s_nop 0
	v_cvt_pk_fp8_f32 v32, v30, v31
	v_pk_mul_f32 v[26:27], v[26:27], s[14:15] op_sel_hi:[1,0]
	s_nop 0
	v_cvt_pk_fp8_f32 v33, v26, v27
	v_pk_mul_f32 v[26:27], v[36:37], s[14:15] op_sel_hi:[1,0]
	v_pk_mul_f32 v[22:23], v[22:23], s[14:15] op_sel_hi:[1,0]
	v_cvt_pk_fp8_f32 v32, v26, v27 op_sel:[0,0,1]
	v_pk_mul_f32 v[14:15], v[14:15], s[14:15] op_sel_hi:[1,0]
	s_nop 0
	s_nop 0
	v_cvt_pk_fp8_f32 v26, v22, v23
	v_cvt_pk_fp8_f32 v27, v14, v15
	v_pk_mul_f32 v[28:29], v[28:29], s[14:15] op_sel_hi:[1,0]
	v_pk_mul_f32 v[14:15], v[24:25], s[14:15] op_sel_hi:[1,0]
	v_cvt_pk_fp8_f32 v33, v28, v29 op_sel:[0,0,1]
	v_pk_mul_f32 v[16:17], v[16:17], s[14:15] op_sel_hi:[1,0]
	v_cvt_pk_fp8_f32 v26, v14, v15 op_sel:[0,0,1]
	v_cvt_pk_fp8_f32 v27, v16, v17 op_sel:[0,0,1]
	v_add_u32_e32 v38, 0xa0, v144
	v_mad_i64_i32 v[14:15], s[18:19], v38, s61, v[130:131]
	global_store_dwordx2 v[14:15], v[32:33], off
	global_store_dwordx2 v[14:15], v[26:27], off offset:128
	v_pk_mul_f32 v[14:15], v[18:19], s[14:15] op_sel_hi:[1,0]
	s_nop 0
	v_cvt_pk_fp8_f32 v16, v14, v15
	v_pk_mul_f32 v[10:11], v[10:11], s[14:15] op_sel_hi:[1,0]
	s_nop 0
	v_cvt_pk_fp8_f32 v17, v10, v11
	v_pk_mul_f32 v[10:11], v[20:21], s[14:15] op_sel_hi:[1,0]
	v_pk_mul_f32 v[6:7], v[6:7], s[14:15] op_sel_hi:[1,0]
	v_cvt_pk_fp8_f32 v16, v10, v11 op_sel:[0,0,1]
	v_pk_mul_f32 v[2:3], v[2:3], s[14:15] op_sel_hi:[1,0]
	s_nop 0
	s_nop 0
	v_cvt_pk_fp8_f32 v10, v6, v7
	v_cvt_pk_fp8_f32 v11, v2, v3
	v_pk_mul_f32 v[12:13], v[12:13], s[14:15] op_sel_hi:[1,0]
	v_pk_mul_f32 v[2:3], v[8:9], s[14:15] op_sel_hi:[1,0]
	v_cvt_pk_fp8_f32 v17, v12, v13 op_sel:[0,0,1]
	v_pk_mul_f32 v[4:5], v[4:5], s[14:15] op_sel_hi:[1,0]
	v_cvt_pk_fp8_f32 v10, v2, v3 op_sel:[0,0,1]
	v_cvt_pk_fp8_f32 v11, v4, v5 op_sel:[0,0,1]
	v_add_u32_e32 v22, 0xb0, v144
	v_mad_i64_i32 v[2:3], s[18:19], v22, s61, v[130:131]
	global_store_dwordx2 v[2:3], v[16:17], off
	global_store_dwordx2 v[2:3], v[10:11], off offset:128

; DI void attn_unit_d8(unsigned char* lds, const AttnArgs& a) {
;     ...
;     const int lane = tid & 63, r = lane & 31, h = lane >> 5; const int wid = __builtin_amdgcn_readfirstlane(tid >> 6);
;     v8i qfa, qfb;
;     { const bf16_t* qp = a.q + (size_t)(wid * 32 + r) * 256 + 32 * h;
;       const u32x4 q0 = *(const u32x4*)qp, q1 = *(const u32x4*)(qp + 8), q2 = *(const u32x4*)(qp + 16), q3 = *(const u32x4*)(qp + 24);
;       const u32x2 c0 = bf8_to_fp8(q0), c1 = bf8_to_fp8(q1), c2 = bf8_to_fp8(q2), c3 = bf8_to_fp8(q3);
;       const v8i qv = (v8i){(int)c0.x, (int)c0.y, (int)c1.x, (int)c1.y, (int)c2.x, (int)c2.y, (int)c3.x, (int)c3.y}, zz = (v8i){0, 0, 0, 0, 0, 0, 0, 0};
;       qfa = h == 0 ? qv : zz; qfb = h == 1 ? qv : zz; }
;     const int lrow = tid >> 3, lch = tid & 7;
;     const unsigned char* vsrc = a.vt8 + (size_t)lrow * KEYS + 8 * lch;
;     const int ldst = lrow * A8_PITCH + lch * 8;
;     const int ldv = A8_VOFF + lrow * A8_PITCH + (lch >> 2) * 16 + (lch & 3) * 4;
;     const int koff = r * A8_PITCH + 32 * h, voff = A8_VOFF + r * A8_PITCH + 32 * h;
;     f32x16 o0[2], o1[2];
; #pragma unroll
;     for (int d = 0; d < 2; ++d) { o0[d] = (f32x16){}; o1[d] = (f32x16){}; }
;     f32x4 l0 = {0.f, 0.f, 0.f, 0.f}, l1 = {0.f, 0.f, 0.f, 0.f};
;     constexpr int D8_SLOT = 2 * 64 * A8_PITCH;
;     u32x2 kreg0, vreg0, kreg1, vreg1;
;     auto gload = [&](int t, u32x2& kreg, u32x2& vreg) __attribute__((always_inline)) {
;         const unsigned char* kp = (t < 64) ? a.klat8 + (size_t)(t * 64 + lrow) * 256 : a.kctx8 + (size_t)((t - 64) * 64 + lrow) * 256;
;         kreg = *(const u32x2*)(kp + 8 * lch);
;         vreg = *(const u32x2*)(vsrc + (size_t)t * 64);
;     };
;     auto lstore = [&](int slot, const u32x2& kreg, const u32x2& vreg) __attribute__((always_inline)) { unsigned char* b = lds + slot * D8_SLOT;
;         *(u32x2*)(b + ldst) = kreg; *(unsigned*)(b + ldv) = vreg.x; *(unsigned*)(b + ldv + 32) = vreg.y; };
;     auto rd32 = [&](const unsigned char* p) __attribute__((always_inline)) -> v8i { const u32x4 lo = *(const u32x4*)p, hi = *(const u32x4*)(p + 16);
;         return (v8i){(int)lo.x, (int)lo.y, (int)lo.z, (int)lo.w, (int)hi.x, (int)hi.y, (int)hi.z, (int)hi.w}; };
;     auto expsum = [&](f32x16& sc, f32x4& l) __attribute__((always_inline)) {
; #pragma unroll
;         for (int i = 0; i < 16; ++i) sc[i] = __builtin_amdgcn_exp2f(sc[i]);
; #pragma unroll
.LBB0_660:
	s_ashr_i32 s15, s14, 31
	s_lshl_b64 s[48:49], s[14:15], 9
	s_add_u32 s21, s22, s48
	s_addc_u32 s47, s23, s49
	s_lshl_b32 s19, s19, 6
	s_and_b32 s43, s19, 0xc0
	s_lshl_b32 s19, s43, 1
	s_add_u32 s52, s21, s19
	s_addc_u32 s53, s47, 0
	s_ashr_i32 s19, s18, 31
	s_ashr_i32 s21, s20, 31
	s_or_b32 s6, s43, s6
	s_lshl_b64 s[48:49], s[18:19], 8
	s_lshl_b64 s[54:55], s[20:21], 8
	s_mul_hi_i32 s19, s6, 0x1100
	s_mulk_i32 s6, 0x1100
	s_add_u32 s18, s28, s6
	s_addc_u32 s19, s29, s19
	s_add_u32 s6, s24, s48
	s_addc_u32 s21, s25, s49
	s_add_u32 s20, s6, s43
	s_addc_u32 s21, s21, 0
	s_add_u32 s6, s24, s54
	s_addc_u32 s48, s25, s55
	v_mov_b32_e32 v18, v0
	s_add_u32 s47, s6, s43
	s_addc_u32 s48, s48, 0
	v_readfirstlane_b32 s6, v18
	v_and_b32_e32 v30, 31, v18
	s_ashr_i32 s49, s6, 6
	v_lshl_or_b32 v180, s49, 5, v30
	v_ashrrev_i32_e32 v181, 31, v180
	v_bfe_u32 v214, v18, 5, 1
	v_lshlrev_b64 v[2:3], 9, v[180:181]
	v_lshl_add_u64 v[2:3], s[52:53], 0, v[2:3]
	v_lshlrev_b32_e32 v178, 6, v214
	v_lshl_add_u64 v[14:15], v[2:3], 0, v[178:179]
	global_load_dwordx4 v[2:5], v[14:15], off
	global_load_dwordx4 v[6:9], v[14:15], off offset:16
	global_load_dwordx4 v[10:13], v[14:15], off offset:32
	s_nop 0
	global_load_dwordx4 v[14:17], v[14:15], off offset:48
	s_lshl_b32 s6, s46, 6
	v_bfe_i32 v34, v18, 5, 1
	v_ashrrev_i32_e32 v215, 3, v18
	v_and_b32_e32 v35, 7, v18
	v_mov_b64_e32 v[18:19], s[18:19]
	s_add_i32 s52, s6, 0xfffff000
	v_mad_i64_i32 v[18:19], s[18:19], v215, s37, v[18:19]
	s_and_b64 s[18:19], s[16:17], exec
	s_cselect_b32 s52, s6, s52
	s_cselect_b32 s19, s21, s48
	s_cselect_b32 s18, s20, s47
	s_or_b32 s54, s6, 64
	s_add_i32 s55, s6, 0xfffff040
	v_add_u32_e32 v20, s52, v215
	s_and_b64 s[52:53], s[16:17], exec
	v_lshlrev_b32_e32 v178, 3, v35
	s_cselect_b32 s52, s54, s55
	s_or_b32 s53, s6, 0x80
	s_add_i32 s54, s6, 0xfffff080
	v_lshl_add_u64 v[182:183], v[18:19], 0, v[178:179]
	s_and_b64 s[16:17], s[16:17], exec
	v_ashrrev_i32_e32 v21, 31, v20
	v_lshl_add_u64 v[22:23], v[182:183], 0, s[6:7]
	s_cselect_b32 s6, s53, s54
	v_lshlrev_b64 v[18:19], 8, v[20:21]
	v_add_u32_e32 v20, s52, v215
	v_add_u32_e32 v24, s6, v215
	v_ashrrev_i32_e32 v21, 31, v20
	v_ashrrev_i32_e32 v25, 31, v24
	v_lshl_add_u64 v[18:19], s[18:19], 0, v[18:19]
	v_lshlrev_b64 v[20:21], 8, v[20:21]
	v_lshlrev_b64 v[24:25], 8, v[24:25]
	v_lshl_add_u64 v[18:19], v[18:19], 0, v[178:179]
	v_lshl_add_u64 v[20:21], s[18:19], 0, v[20:21]
	v_lshl_add_u64 v[24:25], s[18:19], 0, v[24:25]
	global_load_dwordx2 v[26:27], v[22:23], off
	global_load_dwordx2 v[28:29], v[22:23], off offset:64
	s_nop 0
	global_load_dwordx2 v[22:23], v[22:23], off offset:128
	s_nop 0
	global_load_dwordx2 v[18:19], v[18:19], off
	v_lshl_add_u64 v[20:21], v[20:21], 0, v[178:179]
	v_lshl_add_u64 v[24:25], v[24:25], 0, v[178:179]
	global_load_dwordx2 v[20:21], v[20:21], off
	s_nop 0
	global_load_dwordx2 v[24:25], v[24:25], off
	s_nop 0
	s_nop 0
	s_nop 0
	v_cmp_eq_u32_e32 vcc, 0, v214
	v_lshlrev_b32_e32 v36, 5, v214
	s_cmp_lt_i32 s49, 4
	s_waitcnt vmcnt(9)
	v_lshlrev_b32_e32 v37, 16, v2
	v_and_b32_e32 v2, 0xffff0000, v2
	v_lshlrev_b32_e32 v39, 16, v4
	v_and_b32_e32 v4, 0xffff0000, v4
	s_waitcnt vmcnt(8)
	v_lshlrev_b32_e32 v41, 16, v6
	v_and_b32_e32 v6, 0xffff0000, v6
	v_cvt_pk_fp8_f32 v31, v37, v2
	v_cvt_pk_fp8_f32 v32, v39, v4
	v_cvt_pk_fp8_f32 v33, v41, v6
	v_lshlrev_b32_e32 v38, 16, v3
	v_and_b32_e32 v3, 0xffff0000, v3
	v_lshlrev_b32_e32 v40, 16, v5
	v_and_b32_e32 v5, 0xffff0000, v5
	v_lshlrev_b32_e32 v42, 16, v7
	v_and_b32_e32 v7, 0xffff0000, v7
	v_lshlrev_b32_e32 v43, 16, v8
	v_and_b32_e32 v2, 0xffff0000, v8
	v_cvt_pk_fp8_f32 v31, v38, v3 op_sel:[0,0,1]
	s_nop 0
	v_cvt_pk_fp8_f32 v32, v40, v5 op_sel:[0,0,1]
	v_cvt_pk_fp8_f32 v33, v42, v7 op_sel:[0,0,1]
	v_cvt_pk_fp8_f32 v3, v43, v2
	s_waitcnt vmcnt(7)
	v_lshlrev_b32_e32 v5, 16, v10
	v_and_b32_e32 v6, 0xffff0000, v10
	s_nop 0
	v_cvt_pk_fp8_f32 v7, v5, v6
	v_lshlrev_b32_e32 v2, 16, v9
	v_and_b32_e32 v4, 0xffff0000, v9
	v_cvt_pk_fp8_f32 v3, v2, v4 op_sel:[0,0,1]
	v_lshlrev_b32_e32 v2, 16, v11
	v_and_b32_e32 v4, 0xffff0000, v11
	v_cvt_pk_fp8_f32 v7, v2, v4 op_sel:[0,0,1]
	v_lshlrev_b32_e32 v2, 16, v12
	v_and_b32_e32 v4, 0xffff0000, v12
	s_nop 0
	v_cvt_pk_fp8_f32 v5, v2, v4
	s_waitcnt vmcnt(6)
	v_lshlrev_b32_e32 v6, 16, v14
	v_and_b32_e32 v8, 0xffff0000, v14
	s_nop 0
	v_cvt_pk_fp8_f32 v9, v6, v8
	v_lshlrev_b32_e32 v8, 16, v16
	v_and_b32_e32 v10, 0xffff0000, v16
	s_nop 0
	v_cvt_pk_fp8_f32 v11, v8, v10
	v_lshlrev_b32_e32 v2, 16, v13
	v_and_b32_e32 v4, 0xffff0000, v13
	v_lshlrev_b32_e32 v6, 16, v15
	v_and_b32_e32 v8, 0xffff0000, v15
	v_cvt_pk_fp8_f32 v5, v2, v4 op_sel:[0,0,1]
	v_lshlrev_b32_e32 v4, 2, v35
	v_lshlrev_b32_e32 v10, 16, v17
	v_and_b32_e32 v12, 0xffff0000, v17
	v_cvt_pk_fp8_f32 v9, v6, v8 op_sel:[0,0,1]
	v_mul_lo_u32 v2, v215, s38
	v_and_b32_e32 v6, 16, v4
	v_cvt_pk_fp8_f32 v11, v10, v12 op_sel:[0,0,1]
	v_add_u32_e32 v216, v2, v178
	v_add_u32_e32 v2, v2, v6
	v_and_or_b32 v217, v4, 12, v2
	v_add_u32_e32 v2, 0, v217
	v_cndmask_b32_e32 v117, 0, v3, vcc
	v_mul_u32_u24_e32 v8, 0x50, v30
	v_and_b32_e32 v125, v34, v3
	v_add_u32_e32 v3, 0, v216
	v_add_u32_e32 v4, 0x1400, v2
	v_cndmask_b32_e32 v121, 0, v11, vcc
	v_cndmask_b32_e32 v120, 0, v9, vcc
	v_cndmask_b32_e32 v119, 0, v5, vcc
	v_cndmask_b32_e32 v118, 0, v7, vcc
	v_cndmask_b32_e32 v116, 0, v33, vcc
	v_cndmask_b32_e32 v115, 0, v32, vcc
	v_cndmask_b32_e32 v114, 0, v31, vcc
	v_and_b32_e32 v129, v34, v11
	v_and_b32_e32 v128, v34, v9
	v_and_b32_e32 v127, v34, v5
	v_and_b32_e32 v126, v34, v7
	v_and_b32_e32 v124, v34, v33
	v_and_b32_e32 v123, v34, v32
	v_and_b32_e32 v122, v34, v31
	s_waitcnt vmcnt(2)
	ds_write_b64 v3, v[18:19]
	ds_write2_b32 v4, v26, v27 offset1:8
	s_waitcnt vmcnt(1)
	ds_write_b64 v3, v[20:21] offset:10240
	v_add_u32_e32 v4, 0x3c00, v2
	v_add_u32_e32 v2, 0x6400, v2
	v_add3_u32 v218, v36, v8, 0
	ds_write2_b32 v4, v28, v29 offset1:8
	s_waitcnt vmcnt(0)
	ds_write_b64 v3, v[24:25] offset:20480
	ds_write2_b32 v2, v22, v23 offset1:8
	s_waitcnt lgkmcnt(0)
	s_barrier
	ds_read_b128 v[2:5], v218
	ds_read_b128 v[6:9], v218 offset:16
	s_waitcnt lgkmcnt(0)
	v_mfma_f32_32x32x64_f8f6f4 v[82:97], v[2:9], v[114:121], 0
	v_mfma_f32_32x32x64_f8f6f4 v[66:81], v[2:9], v[122:129], 0
	s_cbranch_scc1 .LBB0_662
	s_setprio 1

; DI f32x16 mfma8(v8i a, v8i b, f32x16 c) { return __builtin_amdgcn_mfma_scale_f32_32x32x64_f8f6f4(a, b, c, 0, 0, 0, 0, 0, 0); }
; DI void attn_unit_d8(unsigned char* lds, const AttnArgs& a) {
;     ...
;     auto tile = [&](const unsigned char* Kb, const unsigned char* Kn, v8i& Pa, v8i& Pb, v8i& v0, v8i& v1, const v8i& Qa, const v8i& Qb, const v8i& w0, const v8i& w1) __attribute__((always_inline)) {
;         qk(Kb, 1, s1a, s1b);
;         v0 = rd32(Kb + voff); v1 = rd32(Kb + voff + 32 * A8_PITCH);
;         o0[0] = mfma8(w0, Qa, o0[0]); o1[0] = mfma8(w0, Qb, o1[0]); o0[1] = mfma8(w1, Qa, o0[1]); o1[1] = mfma8(w1, Qb, o1[1]);
;         expsum(s0a, l0); expsum(s0b, l1); pack4(s0a, Pa, 0); pack4(s0b, Pb, 0);
;         qk(Kn, 0, s0a, s0b);
;         expsum(s1a, l0); expsum(s1b, l1); pack4(s1a, Pa, 4); pack4(s1b, Pb, 4);
; #pragma unroll
;         for (int i = 0; i < 8; ++i) { __builtin_amdgcn_sched_group_barrier(0x008, 1, 0); __builtin_amdgcn_sched_group_barrier(0x402, 22, 0); }
;     };
;     for (int t = a.t0; t < a.t1; t += 2) {
;         const int s1 = sb + 1 >= 5 ? sb - 4 : sb + 1, s2 = sb + 2 >= 5 ? sb - 3 : sb + 2, s3 = sb + 3 >= 5 ? sb - 2 : sb + 3, s4 = sb + 4 >= 5 ? sb - 1 : sb + 4;
;         { const int ta = t + 3, tb = t + 4; gload(ta < a.t1 ? ta : a.t1 - 1, kreg0, vreg0); gload(tb < a.t1 ? tb : a.t1 - 1, kreg1, vreg1); }
;         tile(lds + sb * D8_SLOT, lds + s1 * D8_SLOT, PaX, PbX, vX0, vX1, PaY, PbY, vY0, vY1);
;         tile(lds + s1 * D8_SLOT, lds + s2 * D8_SLOT, PaY, PbY, vY0, vY1, PaX, PbX, vX0, vX1);
;         lstore(s3, kreg0, vreg0); lstore(s4, kreg1, vreg1);
;         __syncthreads();
;         sb = s2;
;     }
.LBB0_663:
	s_cmp_gt_i32 s16, 3
	s_cselect_b32 s17, -4, 1
	s_add_i32 s18, s17, s16
	s_mul_i32 s6, s16, 0x2800
	s_cmp_gt_i32 s16, 2
	v_mfma_f32_32x32x64_f8f6f4 v[50:65], v[154:161], v[138:145], v[50:65]
	v_exp_f32_e32 v192, v90
	v_add_u32_e32 v90, s6, v218
	s_cselect_b32 s6, -3, 2
	s_add_i32 s6, s6, s16
	s_cmp_gt_i32 s16, 1
	s_cselect_b32 s19, -2, 3
	s_add_i32 s19, s19, s16
	s_cmp_gt_i32 s16, 0
	s_cselect_b32 s49, -1, 4
	s_min_u32 s54, s46, 64
	s_add_i32 s49, s49, s16
	s_cmp_lt_u32 s46, 61
	s_mul_i32 s17, s6, 0x2800
	s_mov_b32 s16, s6
	s_cselect_b64 s[52:53], -1, 0
	s_lshl_b32 s6, s54, 6
	s_add_i32 s54, s6, 0xc0
	s_add_i32 s55, s6, 0xfffff0c0
	s_and_b64 s[52:53], s[52:53], exec
	v_lshl_add_u64 v[98:99], v[182:183], 0, s[6:7]
	s_cselect_b32 s6, s54, s55
	s_cselect_b32 s53, s21, s48
	s_cselect_b32 s52, s20, s47
	s_min_u32 s56, s46, 63
	v_exp_f32_e32 v198, v82
	v_exp_f32_e32 v199, v83
	v_exp_f32_e32 v196, v84
	v_exp_f32_e32 v197, v85
	v_exp_f32_e32 v200, v86
	v_exp_f32_e32 v201, v87
	v_exp_f32_e32 v194, v88
	v_exp_f32_e32 v195, v89
	ds_read_b128 v[82:85], v90 offset:2560
	ds_read_b128 v[86:89], v90 offset:2576
	global_load_dwordx2 v[202:203], v[98:99], off offset:192
	v_add_u32_e32 v98, s6, v215
	s_cmp_lt_u32 s46, 60
	v_ashrrev_i32_e32 v99, 31, v98
	s_cselect_b64 s[54:55], -1, 0
	s_lshl_b32 s6, s56, 6
	v_lshlrev_b64 v[98:99], 8, v[98:99]
	s_add_i32 s56, s6, 0x100
	s_add_i32 s57, s6, 0xfffff100
	v_lshl_add_u64 v[98:99], s[52:53], 0, v[98:99]
	s_and_b64 s[52:53], s[54:55], exec
	s_cselect_b32 s54, s56, s57
	v_lshl_add_u64 v[220:221], v[98:99], 0, v[178:179]
	v_add_u32_e32 v98, s54, v215
	v_ashrrev_i32_e32 v99, 31, v98
	s_cselect_b32 s53, s21, s48
	s_cselect_b32 s52, s20, s47
	v_lshlrev_b64 v[98:99], 8, v[98:99]
	v_lshl_add_u64 v[100:101], v[182:183], 0, s[6:7]
	v_lshl_add_u64 v[98:99], s[52:53], 0, v[98:99]
	global_load_dwordx2 v[204:205], v[100:101], off offset:256
	v_lshl_add_u64 v[222:223], v[98:99], 0, v[178:179]
	s_waitcnt lgkmcnt(0)
	v_mfma_f32_32x32x64_f8f6f4 v[98:113], v[82:89], v[114:121], 0
	v_exp_f32_e32 v193, v91
	v_exp_f32_e32 v224, v92
	v_exp_f32_e32 v225, v93
	v_exp_f32_e32 v226, v94
	v_exp_f32_e32 v227, v95
	v_exp_f32_e32 v228, v96
	v_exp_f32_e32 v229, v97
	ds_read_b128 v[170:173], v90 offset:5120
	ds_read_b128 v[174:177], v90 offset:5136
	ds_read_b128 v[162:165], v90 offset:7680
	ds_read_b128 v[166:169], v90 offset:7696
	v_pk_add_f32 v[90:91], v[186:187], v[198:199]
	v_pk_add_f32 v[92:93], v[184:185], v[196:197]
	v_pk_add_f32 v[90:91], v[200:201], v[90:91]
	v_pk_add_f32 v[92:93], v[194:195], v[92:93]
	v_pk_add_f32 v[90:91], v[192:193], v[90:91]
	v_pk_add_f32 v[92:93], v[224:225], v[92:93]
	v_exp_f32_e32 v66, v66
	v_exp_f32_e32 v67, v67
	v_exp_f32_e32 v68, v68
	v_exp_f32_e32 v69, v69
	v_exp_f32_e32 v70, v70
	v_exp_f32_e32 v71, v71
	v_exp_f32_e32 v72, v72
	v_pk_add_f32 v[230:231], v[228:229], v[92:93]
	v_pk_add_f32 v[232:233], v[226:227], v[90:91]
	v_mfma_f32_32x32x64_f8f6f4 v[82:97], v[82:89], v[122:129], 0
	v_exp_f32_e32 v73, v73
	v_exp_f32_e32 v74, v74
	v_exp_f32_e32 v75, v75
	v_exp_f32_e32 v76, v76
	v_exp_f32_e32 v77, v77
	v_exp_f32_e32 v78, v78
	v_exp_f32_e32 v79, v79
	v_exp_f32_e32 v80, v80
	v_exp_f32_e32 v81, v81
	v_pk_add_f32 v[186:187], v[190:191], v[66:67]
	v_pk_add_f32 v[188:189], v[188:189], v[68:69]
	s_nop 0
	v_pk_add_f32 v[186:187], v[70:71], v[186:187]
	v_pk_add_f32 v[188:189], v[72:73], v[188:189]
	s_nop 0
	v_cvt_scalef32_pk_fp8_f32 v184, v198, v199, s36
	v_pk_add_f32 v[186:187], v[74:75], v[186:187]
	v_pk_add_f32 v[188:189], v[76:77], v[188:189]
	v_cvt_scalef32_pk_fp8_f32 v185, v200, v201, s36
	v_cvt_scalef32_pk_fp8_f32 v184, v196, v197, s36 op_sel:[0,0,0,1]
	v_pk_add_f32 v[190:191], v[78:79], v[186:187]
	v_pk_add_f32 v[188:189], v[80:81], v[188:189]
	v_mfma_f32_32x32x64_f8f6f4 v[2:17], v[154:161], v[130:137], v[2:17]
	s_nop 0
	s_nop 0
	s_nop 0
	s_nop 0
	s_nop 0
	s_nop 0
	s_mulk_i32 s18, 0x2800
	v_cvt_scalef32_pk_fp8_f32 v186, v192, v193, s36
	v_cvt_scalef32_pk_fp8_f32 v187, v226, v227, s36
	v_cvt_scalef32_pk_fp8_f32 v154, v66, v67, s36
	v_cvt_scalef32_pk_fp8_f32 v155, v70, v71, s36
	v_cvt_scalef32_pk_fp8_f32 v156, v74, v75, s36
	v_cvt_scalef32_pk_fp8_f32 v157, v78, v79, s36
	v_cvt_scalef32_pk_fp8_f32 v185, v194, v195, s36 op_sel:[0,0,0,1]
	v_add_u32_e32 v219, s18, v218
	v_cvt_scalef32_pk_fp8_f32 v186, v224, v225, s36 op_sel:[0,0,0,1]
	v_cvt_scalef32_pk_fp8_f32 v187, v228, v229, s36 op_sel:[0,0,0,1]
	v_cvt_scalef32_pk_fp8_f32 v154, v68, v69, s36 op_sel:[0,0,0,1]
	v_cvt_scalef32_pk_fp8_f32 v155, v72, v73, s36 op_sel:[0,0,0,1]
	v_cvt_scalef32_pk_fp8_f32 v156, v76, v77, s36 op_sel:[0,0,0,1]
	v_cvt_scalef32_pk_fp8_f32 v157, v80, v81, s36 op_sel:[0,0,0,1]
	v_exp_f32_e32 v98, v98
	v_exp_f32_e32 v99, v99
	v_mfma_f32_32x32x64_f8f6f4 v[34:49], v[146:153], v[138:145], v[34:49]
	v_exp_f32_e32 v100, v100
	v_exp_f32_e32 v101, v101
	v_exp_f32_e32 v102, v102
	v_exp_f32_e32 v103, v103
	v_exp_f32_e32 v104, v104
	v_exp_f32_e32 v105, v105
	v_exp_f32_e32 v106, v106
	v_exp_f32_e32 v107, v107
	v_exp_f32_e32 v108, v108
	v_exp_f32_e32 v109, v109
	v_exp_f32_e32 v110, v110
	v_exp_f32_e32 v111, v111
	v_exp_f32_e32 v112, v112
	v_exp_f32_e32 v113, v113
	ds_read_b128 v[192:195], v219
	ds_read_b128 v[196:199], v219 offset:16
	v_pk_add_f32 v[66:67], v[232:233], v[98:99]
	v_pk_add_f32 v[68:69], v[230:231], v[100:101]
	v_pk_add_f32 v[66:67], v[102:103], v[66:67]
	v_pk_add_f32 v[68:69], v[104:105], v[68:69]
	v_pk_add_f32 v[66:67], v[106:107], v[66:67]
	v_pk_add_f32 v[68:69], v[108:109], v[68:69]
	v_pk_add_f32 v[140:141], v[110:111], v[66:67]
	v_pk_add_f32 v[138:139], v[112:113], v[68:69]
	v_mfma_f32_32x32x64_f8f6f4 v[18:33], v[146:153], v[130:137], v[18:33]
	v_exp_f32_e32 v82, v82
	v_exp_f32_e32 v83, v83
	v_exp_f32_e32 v84, v84
	v_exp_f32_e32 v85, v85
	v_exp_f32_e32 v86, v86
	v_exp_f32_e32 v87, v87
	v_exp_f32_e32 v88, v88
	v_exp_f32_e32 v89, v89
	v_exp_f32_e32 v90, v90
	v_exp_f32_e32 v91, v91
	v_exp_f32_e32 v92, v92
	v_exp_f32_e32 v93, v93
	v_exp_f32_e32 v94, v94
	v_exp_f32_e32 v95, v95
	v_exp_f32_e32 v96, v96
	v_exp_f32_e32 v97, v97
	v_pk_add_f32 v[66:67], v[190:191], v[82:83]
	v_pk_add_f32 v[68:69], v[188:189], v[84:85]
	v_pk_add_f32 v[66:67], v[86:87], v[66:67]
	v_pk_add_f32 v[68:69], v[88:89], v[68:69]
	v_pk_add_f32 v[130:131], v[90:91], v[66:67]
	v_pk_add_f32 v[132:133], v[92:93], v[68:69]
	s_waitcnt lgkmcnt(0)
; DI f32x16 mfma8(v8i a, v8i b, f32x16 c) { return __builtin_amdgcn_mfma_scale_f32_32x32x64_f8f6f4(a, b, c, 0, 0, 0, 0, 0, 0); }
; DI void attn_unit_d8(unsigned char* lds, const AttnArgs& a) {
;     ...
;     auto tile = [&](const unsigned char* Kb, const unsigned char* Kn, v8i& Pa, v8i& Pb, v8i& v0, v8i& v1, const v8i& Qa, const v8i& Qb, const v8i& w0, const v8i& w1) __attribute__((always_inline)) {
;         qk(Kb, 1, s1a, s1b);
;         v0 = rd32(Kb + voff); v1 = rd32(Kb + voff + 32 * A8_PITCH);
;         o0[0] = mfma8(w0, Qa, o0[0]); o1[0] = mfma8(w0, Qb, o1[0]); o0[1] = mfma8(w1, Qa, o0[1]); o1[1] = mfma8(w1, Qb, o1[1]);
;         expsum(s0a, l0); expsum(s0b, l1); pack4(s0a, Pa, 0); pack4(s0b, Pb, 0);
;         qk(Kn, 0, s0a, s0b);
;         expsum(s1a, l0); expsum(s1b, l1); pack4(s1a, Pa, 4); pack4(s1b, Pb, 4);
; #pragma unroll
;         for (int i = 0; i < 8; ++i) { __builtin_amdgcn_sched_group_barrier(0x008, 1, 0); __builtin_amdgcn_sched_group_barrier(0x402, 22, 0); }
;     };
;     for (int t = a.t0; t < a.t1; t += 2) {
;         const int s1 = sb + 1 >= 5 ? sb - 4 : sb + 1, s2 = sb + 2 >= 5 ? sb - 3 : sb + 2, s3 = sb + 3 >= 5 ? sb - 2 : sb + 3, s4 = sb + 4 >= 5 ? sb - 1 : sb + 4;
;         { const int ta = t + 3, tb = t + 4; gload(ta < a.t1 ? ta : a.t1 - 1, kreg0, vreg0); gload(tb < a.t1 ? tb : a.t1 - 1, kreg1, vreg1); }
;         tile(lds + sb * D8_SLOT, lds + s1 * D8_SLOT, PaX, PbX, vX0, vX1, PaY, PbY, vY0, vY1);
;         tile(lds + s1 * D8_SLOT, lds + s2 * D8_SLOT, PaY, PbY, vY0, vY1, PaX, PbX, vX0, vX1);
;         lstore(s3, kreg0, vreg0); lstore(s4, kreg1, vreg1);
;         __syncthreads();
;         sb = s2;
;     }
	v_mfma_f32_32x32x64_f8f6f4 v[66:81], v[192:199], v[114:121], 0
	s_nop 0
	s_nop 0
	s_nop 0
	s_nop 0
	s_nop 0
	s_nop 0
	s_nop 0
	v_cvt_scalef32_pk_fp8_f32 v188, v98, v99, s36
	v_cvt_scalef32_pk_fp8_f32 v189, v102, v103, s36
	v_cvt_scalef32_pk_fp8_f32 v190, v106, v107, s36
	v_cvt_scalef32_pk_fp8_f32 v191, v110, v111, s36
	v_cvt_scalef32_pk_fp8_f32 v158, v82, v83, s36
	v_cvt_scalef32_pk_fp8_f32 v159, v86, v87, s36
	v_pk_add_f32 v[142:143], v[96:97], v[132:133]
	v_pk_add_f32 v[144:145], v[94:95], v[130:131]
	v_cvt_scalef32_pk_fp8_f32 v160, v90, v91, s36
	v_cvt_scalef32_pk_fp8_f32 v188, v100, v101, s36 op_sel:[0,0,0,1]
	v_cvt_scalef32_pk_fp8_f32 v189, v104, v105, s36 op_sel:[0,0,0,1]
	v_cvt_scalef32_pk_fp8_f32 v190, v108, v109, s36 op_sel:[0,0,0,1]
	v_cvt_scalef32_pk_fp8_f32 v191, v112, v113, s36 op_sel:[0,0,0,1]
	v_cvt_scalef32_pk_fp8_f32 v158, v84, v85, s36 op_sel:[0,0,0,1]
	v_cvt_scalef32_pk_fp8_f32 v159, v88, v89, s36 op_sel:[0,0,0,1]
	v_mfma_f32_32x32x64_f8f6f4 v[98:113], v[192:199], v[122:129], 0
	global_load_dwordx2 v[192:193], v[220:221], off
	global_load_dwordx2 v[194:195], v[222:223], off
	ds_read_b128 v[130:133], v219 offset:2560
	ds_read_b128 v[134:137], v219 offset:2576
	s_mulk_i32 s19, 0x2800
	s_nop 0
	v_exp_f32_e32 v146, v66
	v_exp_f32_e32 v147, v67
	v_exp_f32_e32 v148, v68
	v_exp_f32_e32 v149, v69
	s_add_i32 s19, s19, 0
	v_cvt_scalef32_pk_fp8_f32 v161, v94, v95, s36
	v_exp_f32_e32 v150, v70
	v_exp_f32_e32 v151, v71
	v_exp_f32_e32 v152, v72
	v_exp_f32_e32 v153, v73
	v_add_u32_e32 v224, s19, v216
	v_add_u32_e32 v225, s19, v217
	v_cvt_scalef32_pk_fp8_f32 v160, v92, v93, s36 op_sel:[0,0,0,1]
	v_cvt_scalef32_pk_fp8_f32 v161, v96, v97, s36 op_sel:[0,0,0,1]
	v_exp_f32_e32 v196, v74
	v_exp_f32_e32 v197, v75
	v_exp_f32_e32 v198, v76
	v_exp_f32_e32 v199, v77
	v_exp_f32_e32 v200, v78
	v_exp_f32_e32 v201, v79
	v_exp_f32_e32 v220, v80
	v_exp_f32_e32 v221, v81
	s_waitcnt lgkmcnt(0)
	v_mfma_f32_32x32x64_f8f6f4 v[82:97], v[130:137], v[114:121], 0
	v_add_f32_e64 v66, v140, v146
	v_add_f32_e64 v67, v141, v147
	v_add_f32_e64 v68, v138, v148
	v_add_f32_e64 v69, v139, v149
	v_add_f32_e64 v66, v150, v66
	v_add_f32_e64 v67, v151, v67
	v_add_f32_e64 v68, v152, v68
	v_add_f32_e64 v69, v153, v69
	v_add_f32_e64 v138, v196, v66
	v_add_f32_e64 v139, v197, v67
	v_add_f32_e64 v140, v198, v68
	v_add_f32_e64 v141, v199, v69
	v_exp_f32_e32 v98, v98
	v_exp_f32_e32 v99, v99
	v_exp_f32_e32 v100, v100
	v_exp_f32_e32 v101, v101
	v_exp_f32_e32 v102, v102
	v_exp_f32_e32 v103, v103
	v_exp_f32_e32 v104, v104
	v_exp_f32_e32 v105, v105
	v_exp_f32_e32 v106, v106
	v_exp_f32_e32 v107, v107
	v_exp_f32_e32 v108, v108
	v_exp_f32_e32 v109, v109
	v_exp_f32_e32 v110, v110
	v_exp_f32_e32 v111, v111
	v_exp_f32_e32 v112, v112
	v_exp_f32_e32 v113, v113
	v_mfma_f32_32x32x64_f8f6f4 v[66:81], v[130:137], v[122:129], 0
	v_add_f32_e64 v130, v144, v98
	v_add_f32_e64 v131, v145, v99
	v_add_f32_e64 v132, v142, v100
	v_add_f32_e64 v133, v143, v101
	v_add_f32_e64 v142, v102, v130
	v_add_f32_e64 v143, v103, v131
	v_add_f32_e64 v132, v104, v132
	v_add_f32_e64 v133, v105, v133
	v_add_f32_e64 v134, v220, v140
	v_add_f32_e64 v135, v221, v141
	v_add_f32_e64 v136, v200, v138
	v_add_f32_e64 v137, v201, v139
	s_nop 0
	s_nop 0
	s_nop 0
	s_nop 0
	s_nop 0
	s_nop 0
	v_pk_add_f32 v[142:143], v[106:107], v[142:143]
	v_pk_add_f32 v[132:133], v[108:109], v[132:133]
	v_cvt_scalef32_pk_fp8_f32 v138, v146, v147, s36
	v_cvt_scalef32_pk_fp8_f32 v139, v150, v151, s36
	v_cvt_scalef32_pk_fp8_f32 v140, v196, v197, s36
	v_cvt_scalef32_pk_fp8_f32 v141, v200, v201, s36
	v_cvt_scalef32_pk_fp8_f32 v130, v98, v99, s36
	v_cvt_scalef32_pk_fp8_f32 v131, v102, v103, s36
	v_pk_add_f32 v[146:147], v[112:113], v[132:133]
	v_pk_add_f32 v[150:151], v[110:111], v[142:143]
	v_mfma_f32_32x32x64_f8f6f4 v[50:65], v[170:177], v[184:191], v[50:65]
	v_exp_f32_e32 v82, v82
	v_exp_f32_e32 v83, v83
	v_exp_f32_e32 v84, v84
	v_exp_f32_e32 v85, v85
	v_add_u32_e32 v102, s17, v218
	v_exp_f32_e32 v86, v86
	v_exp_f32_e32 v87, v87
	v_exp_f32_e32 v88, v88
	v_exp_f32_e32 v89, v89
	v_cvt_scalef32_pk_fp8_f32 v130, v100, v101, s36 op_sel:[0,0,0,1]
	v_cvt_scalef32_pk_fp8_f32 v131, v104, v105, s36 op_sel:[0,0,0,1]
	v_exp_f32_e32 v90, v90
	v_exp_f32_e32 v91, v91
	v_exp_f32_e32 v92, v92
	v_exp_f32_e32 v93, v93
	ds_read_b128 v[98:101], v102
	ds_read_b128 v[102:105], v102 offset:16
	s_nop 0
	v_cvt_scalef32_pk_fp8_f32 v138, v148, v149, s36 op_sel:[0,0,0,1]
	v_cvt_scalef32_pk_fp8_f32 v139, v152, v153, s36 op_sel:[0,0,0,1]
	v_cvt_scalef32_pk_fp8_f32 v140, v198, v199, s36 op_sel:[0,0,0,1]
	v_cvt_scalef32_pk_fp8_f32 v141, v220, v221, s36 op_sel:[0,0,0,1]
	s_nop 0
	v_exp_f32_e32 v94, v94
	v_mfma_f32_32x32x64_f8f6f4 v[2:17], v[170:177], v[154:161], v[2:17]
	v_exp_f32_e32 v148, v96
	v_cvt_scalef32_pk_fp8_f32 v132, v106, v107, s36
	v_exp_f32_e32 v149, v97
	v_pk_add_f32 v[96:97], v[136:137], v[82:83]
	v_pk_add_f32 v[106:107], v[134:135], v[84:85]
	v_exp_f32_e32 v66, v66
	v_exp_f32_e32 v67, v67
	v_exp_f32_e32 v68, v68
	v_exp_f32_e32 v69, v69
	v_exp_f32_e32 v95, v95
	v_cvt_scalef32_pk_fp8_f32 v133, v110, v111, s36
	v_pk_add_f32 v[106:107], v[88:89], v[106:107]
	v_pk_add_f32 v[96:97], v[86:87], v[96:97]
	v_exp_f32_e32 v70, v70
	v_exp_f32_e32 v71, v71
	v_exp_f32_e32 v72, v72
	v_exp_f32_e32 v73, v73
	v_cvt_scalef32_pk_fp8_f32 v132, v108, v109, s36 op_sel:[0,0,0,1]
	v_cvt_scalef32_pk_fp8_f32 v133, v112, v113, s36 op_sel:[0,0,0,1]
	v_pk_add_f32 v[96:97], v[90:91], v[96:97]
	v_pk_add_f32 v[106:107], v[92:93], v[106:107]
	v_exp_f32_e32 v74, v74
	v_mfma_f32_32x32x64_f8f6f4 v[34:49], v[162:169], v[184:191], v[34:49]
	v_exp_f32_e32 v75, v75
	v_exp_f32_e32 v76, v76
	v_exp_f32_e32 v77, v77
; DI void attn_unit_d8(unsigned char* lds, const AttnArgs& a) {
;     ...
;     auto tile = [&](const unsigned char* Kb, const unsigned char* Kn, v8i& Pa, v8i& Pb, v8i& v0, v8i& v1, const v8i& Qa, const v8i& Qb, const v8i& w0, const v8i& w1) __attribute__((always_inline)) {
;         qk(Kb, 1, s1a, s1b);
;         v0 = rd32(Kb + voff); v1 = rd32(Kb + voff + 32 * A8_PITCH);
;         o0[0] = mfma8(w0, Qa, o0[0]); o1[0] = mfma8(w0, Qb, o1[0]); o0[1] = mfma8(w1, Qa, o0[1]); o1[1] = mfma8(w1, Qb, o1[1]);
;         expsum(s0a, l0); expsum(s0b, l1); pack4(s0a, Pa, 0); pack4(s0b, Pb, 0);
;         qk(Kn, 0, s0a, s0b);
;         expsum(s1a, l0); expsum(s1b, l1); pack4(s1a, Pa, 4); pack4(s1b, Pb, 4);
; #pragma unroll
;         for (int i = 0; i < 8; ++i) { __builtin_amdgcn_sched_group_barrier(0x008, 1, 0); __builtin_amdgcn_sched_group_barrier(0x402, 22, 0); }
;     };
;     for (int t = a.t0; t < a.t1; t += 2) {
;         const int s1 = sb + 1 >= 5 ? sb - 4 : sb + 1, s2 = sb + 2 >= 5 ? sb - 3 : sb + 2, s3 = sb + 3 >= 5 ? sb - 2 : sb + 3, s4 = sb + 4 >= 5 ? sb - 1 : sb + 4;
;         { const int ta = t + 3, tb = t + 4; gload(ta < a.t1 ? ta : a.t1 - 1, kreg0, vreg0); gload(tb < a.t1 ? tb : a.t1 - 1, kreg1, vreg1); }
;         tile(lds + sb * D8_SLOT, lds + s1 * D8_SLOT, PaX, PbX, vX0, vX1, PaY, PbY, vY0, vY1);
;         tile(lds + s1 * D8_SLOT, lds + s2 * D8_SLOT, PaY, PbY, vY0, vY1, PaX, PbX, vX0, vX1);
;         lstore(s3, kreg0, vreg0); lstore(s4, kreg1, vreg1);
;         __syncthreads();
;         sb = s2;
;     }
;     o0[0] = mfma8(vY0, PaY, o0[0]); o1[0] = mfma8(vY0, PbY, o1[0]); o0[1] = mfma8(vY1, PaY, o0[1]); o1[1] = mfma8(vY1, PbY, o1[1]);
;     __builtin_amdgcn_s_setprio(0);
;     float lt0 = l0[0] + l0[1] + l0[2] + l0[3]; lt0 += __shfl_xor(lt0, 32);
;     float lt1 = l1[0] + l1[1] + l1[2] + l1[3]; lt1 += __shfl_xor(lt1, 32);
;     unsigned char* op = a.out8 + (size_t)(wid * 32 + r) * 1024 + 4 * h;
;     const float r0 = 16.0f / lt0, r1 = 16.0f * a.lam / lt1;
;     float ss = 0.f;
; #pragma unroll
;     for (int d = 0; d < 2; ++d)
; #pragma unroll
;         for (int i = 0; i < 16; ++i) { const float v = o0[d][i] * r0 - o1[d][i] * r1; o0[d][i] = v; ss += v * v; }
;     ss += __shfl_xor(ss, 32);
;     const float rinv = rsqrtf(ss * (1.0f / 64.0f) + EPS) * a.oscale * CAT_SCALE;
;     f32x4 ggv[2][4];
; #pragma unroll
;     for (int d = 0; d < 2; ++d)
; #pragma unroll
	v_exp_f32_e32 v78, v78
	v_exp_f32_e32 v79, v79
	s_nop 0
	v_exp_f32_e32 v80, v80
	v_exp_f32_e32 v81, v81
	s_nop 0
	s_nop 0
	v_cvt_scalef32_pk_fp8_f32 v142, v82, v83, s36
	s_nop 0
	v_cvt_scalef32_pk_fp8_f32 v143, v86, v87, s36
	v_cvt_scalef32_pk_fp8_f32 v144, v90, v91, s36
	v_cvt_scalef32_pk_fp8_f32 v142, v84, v85, s36 op_sel:[0,0,0,1]
	v_pk_add_f32 v[82:83], v[150:151], v[66:67]
	v_pk_add_f32 v[84:85], v[146:147], v[68:69]
	s_mulk_i32 s49, 0x2800
	v_pk_add_f32 v[184:185], v[148:149], v[106:107]
	v_pk_add_f32 v[186:187], v[94:95], v[96:97]
	v_cvt_scalef32_pk_fp8_f32 v145, v94, v95, s36
	v_cvt_scalef32_pk_fp8_f32 v143, v88, v89, s36 op_sel:[0,0,0,1]
	v_cvt_scalef32_pk_fp8_f32 v144, v92, v93, s36 op_sel:[0,0,0,1]
	v_mfma_f32_32x32x64_f8f6f4 v[18:33], v[162:169], v[154:161], v[18:33]
	v_add_f32_e64 v84, v72, v84
	v_add_f32_e64 v85, v73, v85
	v_add_f32_e64 v82, v70, v82
	v_add_f32_e64 v83, v71, v83
	s_nop 0
	s_nop 0
	s_nop 0
	s_nop 0
	s_add_i32 s6, s49, 0
	v_add_f32_e64 v82, v74, v82
	v_add_f32_e64 v83, v75, v83
	v_add_f32_e64 v84, v76, v84
	v_add_f32_e64 v85, v77, v85
	v_cvt_scalef32_pk_fp8_f32 v134, v66, v67, s36
	v_cvt_scalef32_pk_fp8_f32 v135, v70, v71, s36
	v_cvt_scalef32_pk_fp8_f32 v136, v74, v75, s36
	v_cvt_scalef32_pk_fp8_f32 v137, v78, v79, s36
	v_pk_add_f32 v[188:189], v[80:81], v[84:85]
	v_pk_add_f32 v[190:191], v[78:79], v[82:83]
	v_add_u32_e32 v106, s6, v216
	v_add_u32_e32 v107, s6, v217
	v_cvt_scalef32_pk_fp8_f32 v145, v148, v149, s36 op_sel:[0,0,0,1]
	v_cvt_scalef32_pk_fp8_f32 v134, v68, v69, s36 op_sel:[0,0,0,1]
	v_cvt_scalef32_pk_fp8_f32 v135, v72, v73, s36 op_sel:[0,0,0,1]
	v_cvt_scalef32_pk_fp8_f32 v136, v76, v77, s36 op_sel:[0,0,0,1]
	v_cvt_scalef32_pk_fp8_f32 v137, v80, v81, s36 op_sel:[0,0,0,1]
	s_waitcnt lgkmcnt(0)
	v_mfma_f32_32x32x64_f8f6f4 v[82:97], v[98:105], v[114:121], 0
	ds_read_b128 v[154:157], v219 offset:5120
	ds_read_b128 v[158:161], v219 offset:5136
	ds_read_b128 v[146:149], v219 offset:7680
	ds_read_b128 v[150:153], v219 offset:7696
	s_add_i32 s18, s46, 2
	s_cmpk_lt_u32 s46, 0x42
	s_mov_b32 s46, s18
	s_waitcnt vmcnt(1)
	ds_write_b64 v224, v[192:193]
	v_mfma_f32_32x32x64_f8f6f4 v[66:81], v[98:105], v[122:129], 0
	v_add_u32_e32 v98, 0x1400, v225
	v_add_u32_e32 v99, 0x1400, v107
	ds_write2_b32 v98, v202, v203 offset1:8
	s_waitcnt vmcnt(0)
	ds_write_b64 v106, v[194:195]
	ds_write2_b32 v99, v204, v205 offset1:8
	s_waitcnt lgkmcnt(0)
	s_barrier
	s_cbranch_scc1 .LBB0_663
	s_lshl_b64 s[14:15], s[14:15], 10
	s_add_u32 s6, s8, s14
	s_addc_u32 s15, s9, s15
	s_add_u32 s14, s6, s43
	v_mfma_f32_32x32x64_f8f6f4 v[50:65], v[154:161], v[138:145], v[50:65]
	s_addc_u32 s15, s15, 0
	v_mfma_f32_32x32x64_f8f6f4 v[2:17], v[154:161], v[130:137], v[2:17]
	v_mfma_f32_32x32x64_f8f6f4 v[34:49], v[146:153], v[138:145], v[34:49]
	v_mfma_f32_32x32x64_f8f6f4 v[18:33], v[146:153], v[130:137], v[18:33]
	s_setprio 0
	v_add_f32_e32 v66, v186, v187
	v_add_f32_e32 v66, v184, v66
	v_add_f32_e32 v66, v185, v66
	ds_bpermute_b32 v67, v1, v66
	v_add_f32_e32 v68, v190, v191
	v_add_f32_e32 v68, v188, v68
	v_add_f32_e32 v68, v189, v68
	ds_bpermute_b32 v69, v1, v68
	s_waitcnt lgkmcnt(1)
	v_add_f32_e32 v66, v66, v67
	v_div_scale_f32 v67, s[16:17], v66, v66, s36
	v_rcp_f32_e32 v70, v67
	s_waitcnt lgkmcnt(0)
	v_add_f32_e32 v68, v68, v69
	v_lshlrev_b32_e32 v178, 2, v214
	s_add_i32 s42, s42, s64
	v_fma_f32 v69, -v67, v70, 1.0
	v_fmac_f32_e32 v70, v69, v70
	v_div_scale_f32 v69, vcc, s36, v66, s36
	v_mul_f32_e32 v71, v69, v70
	v_fma_f32 v72, -v67, v71, v69
	v_fmac_f32_e32 v71, v72, v70
	v_fma_f32 v67, -v67, v71, v69
	v_div_scale_f32 v69, s[16:17], v68, v68, v211
	v_rcp_f32_e32 v72, v69
	v_div_fmas_f32 v67, v67, v70, v71
	v_div_fixup_f32 v66, v67, v66, s36
	s_cmpk_gt_i32 s42, 0x21f
	v_fma_f32 v67, -v69, v72, 1.0
	v_fmac_f32_e32 v72, v67, v72
	v_div_scale_f32 v67, vcc, v211, v68, v211
	v_mul_f32_e32 v70, v67, v72
	v_fma_f32 v71, -v69, v70, v67
	v_fmac_f32_e32 v70, v71, v72
	v_fma_f32 v67, -v69, v70, v67
	v_div_fmas_f32 v67, v67, v72, v70
	v_div_fixup_f32 v68, v67, v68, v211
	v_mul_f32_e32 v2, v2, v68
	v_fma_f32 v50, v50, v66, -v2
	v_mul_f32_e32 v2, v3, v68
	v_fma_f32 v51, v51, v66, -v2
	v_mul_f32_e32 v67, v51, v51
	v_mul_f32_e32 v2, v4, v68
	v_fmac_f32_e32 v67, v50, v50
	v_fma_f32 v52, v52, v66, -v2
	v_mul_f32_e32 v2, v5, v68
	v_fmac_f32_e32 v67, v52, v52
	v_fma_f32 v53, v53, v66, -v2
	v_mul_f32_e32 v2, v6, v68
	v_fmac_f32_e32 v67, v53, v53
	v_fma_f32 v54, v54, v66, -v2
	v_mul_f32_e32 v2, v7, v68
	v_fmac_f32_e32 v67, v54, v54
	v_fma_f32 v55, v55, v66, -v2
	v_mul_f32_e32 v2, v8, v68
	v_fmac_f32_e32 v67, v55, v55
	v_fma_f32 v56, v56, v66, -v2
	v_mul_f32_e32 v2, v9, v68
	v_fmac_f32_e32 v67, v56, v56
	v_fma_f32 v57, v57, v66, -v2
	v_mul_f32_e32 v2, v10, v68
	v_fmac_f32_e32 v67, v57, v57
	v_fma_f32 v58, v58, v66, -v2
	v_mul_f32_e32 v2, v11, v68
	v_fmac_f32_e32 v67, v58, v58
	v_fma_f32 v59, v59, v66, -v2
	v_mul_f32_e32 v2, v12, v68
	v_fmac_f32_e32 v67, v59, v59
	v_fma_f32 v60, v60, v66, -v2
	v_mul_f32_e32 v2, v13, v68
	v_fmac_f32_e32 v67, v60, v60
	v_fma_f32 v61, v61, v66, -v2
	v_mul_f32_e32 v14, v14, v68
	v_fmac_f32_e32 v67, v61, v61
	v_fma_f32 v62, v62, v66, -v14
	v_mul_f32_e32 v14, v15, v68
	v_fmac_f32_e32 v67, v62, v62
	v_fma_f32 v63, v63, v66, -v14
	v_mul_f32_e32 v14, v16, v68
	v_lshlrev_b32_e32 v69, 4, v214
	v_fmac_f32_e32 v67, v63, v63
	v_fma_f32 v64, v64, v66, -v14
	v_mul_f32_e32 v14, v17, v68
	global_load_dwordx4 v[2:5], v69, s[10:11] offset:224
	global_load_dwordx4 v[6:9], v69, s[10:11] offset:32
	global_load_dwordx4 v[10:13], v69, s[10:11]
	v_fmac_f32_e32 v67, v64, v64
	v_fma_f32 v65, v65, v66, -v14
	v_mul_f32_e32 v14, v18, v68
	v_fmac_f32_e32 v67, v65, v65
; DI unsigned pk4_fp8(float a, float b, float c, float d) { int r = 0; r = __builtin_amdgcn_cvt_pk_fp8_f32(a, b, r, false); r = __builtin_amdgcn_cvt_pk_fp8_f32(c, d, r, true); return (unsigned)r; }
; DI float clamp448(float x) { return __builtin_amdgcn_fmed3f(x, -448.0f, 448.0f); }
; DI void attn_unit_d8(unsigned char* lds, const AttnArgs& a) {
;     ...
;     float lt1 = l1[0] + l1[1] + l1[2] + l1[3]; lt1 += __shfl_xor(lt1, 32);
;     unsigned char* op = a.out8 + (size_t)(wid * 32 + r) * 1024 + 4 * h;
;     const float r0 = 16.0f / lt0, r1 = 16.0f * a.lam / lt1;
;     float ss = 0.f;
; #pragma unroll
;     for (int d = 0; d < 2; ++d)
; #pragma unroll
;         for (int i = 0; i < 16; ++i) { const float v = o0[d][i] * r0 - o1[d][i] * r1; o0[d][i] = v; ss += v * v; }
;     ss += __shfl_xor(ss, 32);
;     const float rinv = rsqrtf(ss * (1.0f / 64.0f) + EPS) * a.oscale * CAT_SCALE;
;     f32x4 ggv[2][4];
; #pragma unroll
;     for (int d = 0; d < 2; ++d)
; #pragma unroll
;         for (int g = 0; g < 4; ++g) ggv[d][g] = *(const f32x4*)(a.subg + 32 * d + 8 * g + 4 * h);
;     asm volatile("" : "+v"(ggv[0][0]), "+v"(ggv[1][3]));
; #pragma unroll
;     for (int d = 0; d < 2; ++d)
; #pragma unroll
;         for (int g = 0; g < 4; ++g) { const f32x4 gg = ggv[d][g];
;             *(unsigned*)(op + 32 * d + 8 * g) = pk4_fp8(clamp448(o0[d][4 * g] * rinv * gg[0]), clamp448(o0[d][4 * g + 1] * rinv * gg[1]), clamp448(o0[d][4 * g + 2] * rinv * gg[2]), clamp448(o0[d][4 * g + 3] * rinv * gg[3])); }
	v_fma_f32 v70, v34, v66, -v14
	v_mul_f32_e32 v14, v19, v68
	v_fmac_f32_e32 v67, v70, v70
	v_fma_f32 v71, v35, v66, -v14
	v_mul_f32_e32 v14, v20, v68
	v_fmac_f32_e32 v67, v71, v71
	v_fma_f32 v72, v36, v66, -v14
	v_mul_f32_e32 v14, v21, v68
	v_fmac_f32_e32 v67, v72, v72
	v_fma_f32 v73, v37, v66, -v14
	v_mul_f32_e32 v14, v22, v68
	v_fmac_f32_e32 v67, v73, v73
	v_fma_f32 v74, v38, v66, -v14
	v_mul_f32_e32 v14, v23, v68
	v_fmac_f32_e32 v67, v74, v74
	v_fma_f32 v75, v39, v66, -v14
	v_fmac_f32_e32 v67, v75, v75
	v_pk_mul_f32 v[14:15], v[24:25], v[68:69] op_sel_hi:[1,0]
	v_pk_mul_f32 v[22:23], v[32:33], v[68:69] op_sel_hi:[1,0]
	v_pk_fma_f32 v[34:35], v[40:41], v[66:67], v[14:15] op_sel_hi:[1,0,1] neg_lo:[0,0,1] neg_hi:[0,0,1]
	s_nop 0
	v_pk_mul_f32 v[14:15], v[34:35], v[34:35]
	s_nop 0
	v_add_f32_e32 v14, v14, v67
	v_add_f32_e32 v20, v15, v14
	v_pk_mul_f32 v[14:15], v[26:27], v[68:69] op_sel_hi:[1,0]
	s_nop 0
	v_pk_fma_f32 v[36:37], v[42:43], v[66:67], v[14:15] op_sel_hi:[1,0,1] neg_lo:[0,0,1] neg_hi:[0,0,1]
	global_load_dwordx4 v[14:17], v69, s[10:11] offset:64
	v_pk_mul_f32 v[18:19], v[36:37], v[36:37]
	v_pk_fma_f32 v[42:43], v[48:49], v[66:67], v[22:23] op_sel_hi:[1,0,1] neg_lo:[0,0,1] neg_hi:[0,0,1]
	v_add_f32_e32 v18, v18, v20
	v_add_f32_e32 v20, v19, v18
	v_pk_mul_f32 v[18:19], v[28:29], v[68:69] op_sel_hi:[1,0]
	v_pk_mul_f32 v[22:23], v[42:43], v[42:43]
	v_pk_fma_f32 v[38:39], v[44:45], v[66:67], v[18:19] op_sel_hi:[1,0,1] neg_lo:[0,0,1] neg_hi:[0,0,1]
	s_nop 0
	v_pk_mul_f32 v[18:19], v[38:39], v[38:39]
	s_nop 0
	v_add_f32_e32 v18, v18, v20
	v_add_f32_e32 v20, v19, v18
	v_pk_mul_f32 v[18:19], v[30:31], v[68:69] op_sel_hi:[1,0]
	s_nop 0
	v_pk_fma_f32 v[40:41], v[46:47], v[66:67], v[18:19] op_sel_hi:[1,0,1] neg_lo:[0,0,1] neg_hi:[0,0,1]
	s_nop 0
	v_pk_mul_f32 v[18:19], v[40:41], v[40:41]
	s_nop 0
	v_add_f32_e32 v18, v18, v20
	v_add_f32_e32 v24, v19, v18
	v_add_f32_e32 v22, v22, v24
	v_add_f32_e32 v26, v23, v22
	ds_bpermute_b32 v27, v1, v26
	global_load_dwordx4 v[18:21], v69, s[10:11] offset:96
	global_load_dwordx4 v[22:25], v69, s[10:11] offset:192
	s_waitcnt lgkmcnt(0)
	v_add_f32_e32 v26, v26, v27
	v_fmamk_f32 v26, v26, 0x3c800000, v212
	v_mul_f32_e32 v27, 0x4b800000, v26
	v_cmp_gt_f32_e32 vcc, s39, v26
	s_nop 1
	v_cndmask_b32_e32 v30, v26, v27, vcc
	global_load_dwordx4 v[26:29], v69, s[10:11] offset:128
	v_rsq_f32_e32 v32, v30
	v_lshlrev_b64 v[30:31], 10, v[180:181]
	v_lshl_add_u64 v[44:45], s[14:15], 0, v[30:31]
	v_lshl_add_u64 v[44:45], v[44:45], 0, v[178:179]
	v_mul_f32_e32 v30, 0x45800000, v32
	v_cndmask_b32_e32 v30, v32, v30, vcc
	v_mul_f32_e32 v48, 0x3f4ccccd, v30
	global_load_dwordx4 v[30:33], v69, s[10:11] offset:160
	v_mul_f32_e32 v48, 0x41800000, v48
	s_waitcnt vmcnt(5)
	v_mul_f32_e32 v49, v50, v48
	v_mul_f32_e32 v10, v10, v49
	v_mul_f32_e32 v49, v51, v48
	v_mul_f32_e32 v11, v11, v49
	v_mul_f32_e32 v49, v52, v48
	v_med3_f32 v10, v10, s40, v213
	v_med3_f32 v11, v11, s40, v213
	v_mul_f32_e32 v12, v12, v49
	s_nop 0
	v_cvt_pk_fp8_f32 v49, v10, v11
	v_mul_f32_e32 v10, v53, v48
	v_mul_f32_e32 v10, v13, v10
	v_med3_f32 v12, v12, s40, v213
	v_med3_f32 v10, v10, s40, v213
	v_cvt_pk_fp8_f32 v49, v12, v10 op_sel:[0,0,1]
	v_mul_f32_e32 v10, v54, v48
	v_mul_f32_e32 v6, v6, v10
	v_mul_f32_e32 v10, v55, v48
	v_mul_f32_e32 v7, v7, v10
	v_mul_f32_e32 v10, v56, v48
	v_med3_f32 v6, v6, s40, v213
	v_med3_f32 v7, v7, s40, v213
	v_mul_f32_e32 v8, v8, v10
	s_nop 0
	v_cvt_pk_fp8_f32 v10, v6, v7
	v_mul_f32_e32 v6, v57, v48
	v_mul_f32_e32 v6, v9, v6
	v_med3_f32 v8, v8, s40, v213
	v_med3_f32 v6, v6, s40, v213
	v_cvt_pk_fp8_f32 v10, v8, v6 op_sel:[0,0,1]
	v_add_co_u32_e32 v6, vcc, s41, v44
	v_lshl_add_u64 v[46:47], v[44:45], 0, s[12:13]
	s_nop 0
	v_addc_co_u32_e32 v7, vcc, 0, v45, vcc
	global_store_dword v[6:7], v49, off offset:768
	global_store_dword v[46:47], v10, off offset:8
	v_mul_f32_e32 v6, v58, v48
	v_mul_f32_e32 v7, v59, v48
	s_waitcnt vmcnt(6)
	v_mul_f32_e32 v6, v14, v6
	v_mul_f32_e32 v7, v15, v7
	v_med3_f32 v6, v6, s40, v213
	v_med3_f32 v7, v7, s40, v213
	s_nop 0
	v_cvt_pk_fp8_f32 v9, v6, v7
	v_mul_f32_e32 v8, v60, v48
	v_mul_f32_e32 v6, v61, v48
	v_mul_f32_e32 v8, v16, v8
	v_mul_f32_e32 v6, v17, v6
	v_med3_f32 v8, v8, s40, v213
	v_med3_f32 v6, v6, s40, v213
	v_cvt_pk_fp8_f32 v9, v8, v6 op_sel:[0,0,1]
	v_mul_f32_e32 v6, v62, v48
	v_mul_f32_e32 v7, v63, v48
	s_nop 0
	v_mul_f32_e32 v8, v64, v48
	s_nop 0
	s_waitcnt vmcnt(5)
	v_mul_f32_e32 v6, v18, v6
	v_mul_f32_e32 v7, v19, v7
	v_med3_f32 v6, v6, s40, v213
	v_med3_f32 v7, v7, s40, v213
	v_cvt_pk_fp8_f32 v10, v6, v7
	v_mul_f32_e32 v6, v65, v48
	v_mul_f32_e32 v8, v20, v8
	v_mul_f32_e32 v6, v21, v6
	v_med3_f32 v8, v8, s40, v213
	v_med3_f32 v6, v6, s40, v213
	v_cvt_pk_fp8_f32 v10, v8, v6 op_sel:[0,0,1]
	v_mul_f32_e32 v6, v70, v48
	v_mul_f32_e32 v7, v71, v48
	s_waitcnt vmcnt(3)
	v_mul_f32_e32 v6, v26, v6
	v_mul_f32_e32 v7, v27, v7
	v_med3_f32 v6, v6, s40, v213
	v_med3_f32 v7, v7, s40, v213
	v_cvt_pk_fp8_f32 v11, v6, v7
	v_mul_f32_e32 v8, v72, v48
	v_mul_f32_e32 v6, v73, v48
	v_mul_f32_e32 v8, v28, v8
	v_mul_f32_e32 v6, v29, v6
	v_med3_f32 v8, v8, s40, v213
	v_med3_f32 v6, v6, s40, v213
	v_cvt_pk_fp8_f32 v11, v8, v6 op_sel:[0,0,1]
	v_mul_f32_e32 v6, v74, v48
	v_mul_f32_e32 v7, v75, v48
	s_waitcnt vmcnt(2)
	v_mul_f32_e32 v6, v30, v6
	v_mul_f32_e32 v7, v31, v7
	v_med3_f32 v6, v6, s40, v213
	v_med3_f32 v7, v7, s40, v213
	s_nop 0
	v_cvt_pk_fp8_f32 v12, v6, v7
	v_mul_f32_e32 v8, v34, v48
	v_mul_f32_e32 v6, v35, v48
	v_mul_f32_e32 v8, v32, v8
	v_mul_f32_e32 v6, v33, v6
	v_med3_f32 v8, v8, s40, v213
	v_med3_f32 v6, v6, s40, v213
	v_cvt_pk_fp8_f32 v12, v8, v6 op_sel:[0,0,1]
	v_mul_f32_e32 v6, v36, v48
	v_mul_f32_e32 v7, v37, v48
	v_mul_f32_e32 v6, v22, v6
	v_mul_f32_e32 v7, v23, v7
	global_store_dword v[46:47], v9, off offset:16
	global_store_dword v[46:47], v10, off offset:24
	global_store_dword v[46:47], v11, off offset:32
	global_store_dword v[46:47], v12, off offset:40
	v_med3_f32 v6, v6, s40, v213
	v_med3_f32 v7, v7, s40, v213
	s_nop 0
	v_cvt_pk_fp8_f32 v9, v6, v7
	v_mul_f32_e32 v8, v38, v48
	v_mul_f32_e32 v6, v39, v48
	v_mul_f32_e32 v8, v24, v8
	v_mul_f32_e32 v6, v25, v6
	v_med3_f32 v8, v8, s40, v213
	v_med3_f32 v6, v6, s40, v213
	v_cvt_pk_fp8_f32 v9, v8, v6 op_sel:[0,0,1]
	v_mul_f32_e32 v6, v40, v48
	v_mul_f32_e32 v2, v2, v6
	v_mul_f32_e32 v6, v41, v48
	v_mul_f32_e32 v3, v3, v6
	v_mul_f32_e32 v6, v42, v48
	v_med3_f32 v2, v2, s40, v213
	v_med3_f32 v3, v3, s40, v213
	v_mul_f32_e32 v4, v4, v6
	s_nop 0
	v_cvt_pk_fp8_f32 v6, v2, v3
	v_mul_f32_e32 v2, v43, v48
	v_mul_f32_e32 v2, v5, v2
	v_med3_f32 v4, v4, s40, v213
	v_med3_f32 v2, v2, s40, v213
	v_cvt_pk_fp8_f32 v6, v4, v2 op_sel:[0,0,1]
	global_store_dword v[46:47], v9, off offset:48
	global_store_dword v[46:47], v6, off offset:56
	s_cbranch_scc0 .LBB0_656

; DI unsigned pk4_fp8(float a, float b, float c, float d) { int r = 0; r = __builtin_amdgcn_cvt_pk_fp8_f32(a, b, r, false); r = __builtin_amdgcn_cvt_pk_fp8_f32(c, d, r, true); return (unsigned)r; }
; DI float clamp448(float x) { return __builtin_amdgcn_fmed3f(x, -448.0f, 448.0f); }
; DI void attn_unit_a8(unsigned char* lds, const AttnArgs& a) {
;     ...
;     float lt0 = l0[0] + l0[1] + l0[2] + l0[3];
;     lt0 += __shfl_xor(lt0, 32);
;     unsigned char* op = a.out8 + (size_t)(wid * 32 + r) * 1024 + 4 * h;
;     const float rl = 16.0f * CAT_SCALE / lt0;
; #pragma unroll
;     for (int d = 0; d < 2; ++d)
; #pragma unroll
;         for (int g = 0; g < 4; ++g) *(unsigned*)(op + 32 * d + 8 * g) = pk4_fp8(clamp448(o0[d][4 * g] * rl), clamp448(o0[d][4 * g + 1] * rl), clamp448(o0[d][4 * g + 2] * rl), clamp448(o0[d][4 * g + 3] * rl));
; template <int li>
; DI void layer_phases(unsigned char* smem, LAS unsigned char* ldsL, const int lo, const int hi) {
;     ...
;               for (int it = 0; ; ++it) {
;                 int L = (int)blockIdx.x + it * G;
;                 if (G == 256 && it == 2) { const int j = (int)blockIdx.x - 32; if (j < 0 || j >= 32) break; L = 512 + j; }
;                 if (L >= (li == DEPTH - 1 ? 512 : 512 + 32)) break;
.LBB0_688:
	v_add_f32_e32 v34, v108, v109
	v_add_f32_e32 v34, v110, v34
	v_add_f32_e32 v34, v111, v34
	ds_bpermute_b32 v35, v1, v34
	v_lshrrev_b32_e32 v39, 3, v153
	v_and_b32_e32 v106, 4, v39
	s_lshl_b64 s[6:7], s[22:23], 10
	s_add_u32 s4, s42, s6
	s_waitcnt lgkmcnt(0)
	v_add_f32_e32 v36, v34, v35
	v_div_scale_f32 v37, s[8:9], v36, v36, s49
	v_rcp_f32_e32 v38, v37
	s_addc_u32 s7, s43, s7
	s_add_u32 s6, s4, s57
	s_addc_u32 s7, s7, 0
	v_fma_f32 v39, -v37, v38, 1.0
	v_fmac_f32_e32 v38, v39, v38
	v_div_scale_f32 v39, vcc, s49, v36, s49
	v_mul_f32_e32 v40, v39, v38
	v_fma_f32 v41, -v37, v40, v39
	v_fmac_f32_e32 v40, v41, v38
	v_fma_f32 v37, -v37, v40, v39
	v_div_fmas_f32 v37, v37, v38, v40
	v_div_fixup_f32 v36, v37, v36, s49
	v_mul_f32_e32 v18, v18, v36
	v_mul_f32_e32 v19, v19, v36
	v_med3_f32 v18, v18, s54, v152
	v_med3_f32 v19, v19, s54, v152
	s_nop 0
	v_cvt_pk_fp8_f32 v37, v18, v19
	v_mul_f32_e32 v20, v20, v36
	v_mul_f32_e32 v19, v21, v36
	v_med3_f32 v18, v20, s54, v152
	v_med3_f32 v19, v19, s54, v152
	v_cvt_pk_fp8_f32 v37, v18, v19 op_sel:[0,0,1]
	v_mul_f32_e32 v18, v22, v36
	v_mul_f32_e32 v19, v23, v36
	v_med3_f32 v18, v18, s54, v152
	v_med3_f32 v19, v19, s54, v152
	s_nop 0
	v_cvt_pk_fp8_f32 v21, v18, v19
	v_mul_f32_e32 v20, v24, v36
	v_mul_f32_e32 v19, v25, v36
	v_med3_f32 v18, v20, s54, v152
	v_med3_f32 v19, v19, s54, v152
	v_cvt_pk_fp8_f32 v21, v18, v19 op_sel:[0,0,1]
	v_mul_f32_e32 v18, v26, v36
	v_mul_f32_e32 v19, v27, v36
	v_med3_f32 v18, v18, s54, v152
	v_med3_f32 v19, v19, s54, v152
	s_nop 0
	v_cvt_pk_fp8_f32 v22, v18, v19
	v_mul_f32_e32 v20, v28, v36
	v_mul_f32_e32 v19, v29, v36
	v_lshlrev_b64 v[34:35], 10, v[128:129]
	v_med3_f32 v18, v20, s54, v152
	v_med3_f32 v19, v19, s54, v152
	v_lshl_add_u64 v[34:35], s[6:7], 0, v[34:35]
	v_cvt_pk_fp8_f32 v22, v18, v19 op_sel:[0,0,1]
	v_lshl_add_u64 v[18:19], v[34:35], 0, v[106:107]
	global_store_dword v[18:19], v37, off
	global_store_dword v[18:19], v21, off offset:8
	global_store_dword v[18:19], v22, off offset:16
	v_mul_f32_e32 v20, v30, v36
	v_mul_f32_e32 v21, v31, v36
	v_med3_f32 v20, v20, s54, v152
	v_med3_f32 v21, v21, s54, v152
	s_nop 0
	v_cvt_pk_fp8_f32 v23, v20, v21
	v_mul_f32_e32 v22, v32, v36
	v_mul_f32_e32 v21, v33, v36
	v_med3_f32 v20, v22, s54, v152
	v_med3_f32 v21, v21, s54, v152
	v_mul_f32_e32 v2, v2, v36
	v_mul_f32_e32 v3, v3, v36
	v_cvt_pk_fp8_f32 v23, v20, v21 op_sel:[0,0,1]
	v_med3_f32 v2, v2, s54, v152
	v_med3_f32 v3, v3, s54, v152
	s_nop 0
	v_cvt_pk_fp8_f32 v20, v2, v3
	v_mul_f32_e32 v4, v4, v36
	v_mul_f32_e32 v3, v5, v36
	v_med3_f32 v2, v4, s54, v152
	v_med3_f32 v3, v3, s54, v152
	v_cvt_pk_fp8_f32 v20, v2, v3 op_sel:[0,0,1]
	v_mul_f32_e32 v2, v6, v36
	v_mul_f32_e32 v3, v7, v36
	v_med3_f32 v2, v2, s54, v152
	v_med3_f32 v3, v3, s54, v152
	s_nop 0
	v_cvt_pk_fp8_f32 v5, v2, v3
	v_mul_f32_e32 v4, v8, v36
	v_mul_f32_e32 v3, v9, v36
	v_med3_f32 v2, v4, s54, v152
	v_med3_f32 v3, v3, s54, v152
	v_cvt_pk_fp8_f32 v5, v2, v3 op_sel:[0,0,1]
	v_mul_f32_e32 v2, v10, v36
	v_mul_f32_e32 v3, v11, v36
	v_med3_f32 v2, v2, s54, v152
	v_med3_f32 v3, v3, s54, v152
	s_nop 0
	v_cvt_pk_fp8_f32 v6, v2, v3
	v_mul_f32_e32 v4, v12, v36
	v_mul_f32_e32 v3, v13, v36
	s_add_i32 s55, s55, 1
	v_med3_f32 v2, v4, s54, v152
	v_med3_f32 v3, v3, s54, v152
	s_cmp_eq_u32 s55, 2
	v_cvt_pk_fp8_f32 v6, v2, v3 op_sel:[0,0,1]
	v_mul_f32_e32 v2, v14, v36
	v_mul_f32_e32 v3, v15, v36
	s_cselect_b64 s[6:7], -1, 0
	global_store_dword v[18:19], v23, off offset:24
	global_store_dword v[18:19], v20, off offset:32
	global_store_dword v[18:19], v5, off offset:40
	global_store_dword v[18:19], v6, off offset:48
	v_med3_f32 v2, v2, s54, v152
	v_med3_f32 v3, v3, s54, v152
	s_nop 0
	s_and_b64 s[6:7], s[52:53], s[6:7]
	v_cvt_pk_fp8_f32 v5, v2, v3
	s_and_b64 s[8:9], s[26:27], s[6:7]
	s_mul_i32 s4, s55, s64
	s_and_b64 s[6:7], s[6:7], exec
	v_mul_f32_e32 v4, v16, v36
	v_mul_f32_e32 v3, v17, v36
	s_cselect_b32 s4, 0x1e0, s4
	v_med3_f32 v2, v4, s54, v152
	v_med3_f32 v3, v3, s54, v152
	s_add_i32 s4, s4, s2
	v_cvt_pk_fp8_f32 v5, v2, v3 op_sel:[0,0,1]
	s_cmpk_gt_i32 s4, 0x21f
	s_cselect_b64 s[6:7], -1, 0
	s_or_b64 s[6:7], s[8:9], s[6:7]
	s_andn2_b64 vcc, exec, s[6:7]
	global_store_dword v[18:19], v5, off offset:56
	s_cbranch_vccz .LBB0_718

; DI void attn_unit_a8(unsigned char* lds, const AttnArgs& a) {
;     ...
;     { const bf16_t* qp = a.q + (size_t)(wid * 32 + r) * 256 + 32 * h;
;       const u32x4 q0 = *(const u32x4*)qp, q1 = *(const u32x4*)(qp + 8), q2 = *(const u32x4*)(qp + 16), q3 = *(const u32x4*)(qp + 24);
;       const u32x2 c0 = bf8_to_fp8(q0), c1 = bf8_to_fp8(q1), c2 = bf8_to_fp8(q2), c3 = bf8_to_fp8(q3);
;       qf8 = (v8i){(int)c0.x, (int)c0.y, (int)c1.x, (int)c1.y, (int)c2.x, (int)c2.y, (int)c3.x, (int)c3.y}; }
;     const int lrow = tid >> 3, lch = tid & 7;
;     const unsigned char* vsrc = a.vt8 + (size_t)lrow * KEYS + 8 * lch;
;     const int ldk = lrow * A8_PITCH + 8 * lch;
;     const int ldv = A8_VOFF + lrow * A8_PITCH + (lch >> 2) * 16 + (lch & 3) * 4;
;     const int koff = r * A8_PITCH + 32 * h, voff = A8_VOFF + r * A8_PITCH + 32 * h;
;     f32x16 o0[2]; o0[0] = (f32x16){}; o0[1] = (f32x16){};
;     f32x4 l0 = {0.f, 0.f, 0.f, 0.f};
;     u32x2 kregA, vregA, kregB, vregB;
;     auto gload = [&](int t, u32x2& kreg, u32x2& vreg) __attribute__((always_inline)) {
;         const unsigned char* kp = (t < 64) ? a.klat8 + (size_t)(t * 64 + lrow) * 128 : a.kctx8 + (size_t)((t - 64) * 64 + lrow) * 128;
;         kreg = *(const u32x2*)(kp + 8 * lch);
;         vreg = *(const u32x2*)(vsrc + (size_t)t * 64);
;     };
;     auto lstore = [&](int slot, const u32x2& kreg, const u32x2& vreg) __attribute__((always_inline)) { unsigned char* b = lds + slot * AT_BUFB;
;         *(u32x2*)(b + ldk) = kreg; *(unsigned*)(b + ldv) = vreg.x; *(unsigned*)(b + ldv + 32) = vreg.y; };
;     auto rd32 = [&](const unsigned char* p) __attribute__((always_inline)) -> v8i { const u32x4 lo = *(const u32x4*)p, hi = *(const u32x4*)(p + 16);
;         return (v8i){(int)lo.x, (int)lo.y, (int)lo.z, (int)lo.w, (int)hi.x, (int)hi.y, (int)hi.z, (int)hi.w}; };
;     ...
;     const int wcol = tid >> 1, whalf = tid & 1;
;     const unsigned wper_gu = (unsigned)((wcol >> 7) * 256 + (wcol & 96) + invperm32(wcol & 31)) * 1024u + 16u * whalf;
;     const unsigned wper_dn = (unsigned)fwd_lane16(wcol) * 1024u + 16u * whalf;
;     auto w_store = [&](int j) __attribute__((always_inline)) { const float* src; unsigned char* dst; int ld, n0, k0; bool gu; w_decode(j, src, dst, ld, n0, k0, gu);
;         const int nb = n0 >> 8; const unsigned uni = (unsigned)(gu ? (nb & 3) * 512 + (nb >> 2) * 128 : nb * 256) * 1024u + (unsigned)k0;
.LBB0_700:
	s_lshl_b32 s4, s9, 5
	s_and_b32 s4, s4, 64
	s_lshl_b32 s12, s58, 7
	s_lshl_b32 s57, s9, 6
	s_ashr_i32 s11, s10, 31
	s_ashr_i32 s9, s8, 31
	s_or_b32 s12, s4, s12
	s_lshl_b64 s[10:11], s[10:11], 7
	s_lshl_b64 s[8:9], s[8:9], 7
	s_mul_hi_i32 s13, s12, 0x1100
	s_mulk_i32 s12, 0x1100
	s_add_u32 s12, s40, s12
	s_addc_u32 s13, s41, s13
	s_add_u32 s10, s38, s10
	s_addc_u32 s11, s39, s11
	s_add_u32 s58, s10, s4
	s_addc_u32 s59, s11, 0
	s_add_u32 s8, s38, s8
	s_addc_u32 s9, s39, s9
	s_add_u32 s60, s8, s4
	s_addc_u32 s61, s9, 0
	s_lshl_b32 s4, s56, 6
	v_ashrrev_i32_e32 v154, 3, v153
	v_mov_b64_e32 v[22:23], s[12:13]
	s_add_i32 s10, s4, 0xfffff000
	v_and_b32_e32 v21, 7, v153
	v_mad_i64_i32 v[22:23], s[8:9], v154, s28, v[22:23]
	s_and_b64 s[8:9], s[6:7], exec
	v_lshlrev_b32_e32 v130, 3, v21
	v_mov_b32_e32 v131, v107
	s_cselect_b32 s8, s4, s10
	v_lshl_add_u64 v[132:133], v[22:23], 0, v[130:131]
	v_add_u32_e32 v22, s8, v154
	s_cselect_b32 s9, s59, s61
	s_cselect_b32 s8, s58, s60
	s_or_b32 s12, s4, 64
	s_add_i32 s13, s4, 0xfffff040
	s_and_b64 s[10:11], s[6:7], exec
	s_cselect_b32 s10, s12, s13
	v_add_u32_e32 v28, s10, v154
	v_ashrrev_i32_e32 v23, 31, v22
	v_ashrrev_i32_e32 v29, 31, v28
	v_lshlrev_b64 v[22:23], 7, v[22:23]
	v_lshlrev_b64 v[28:29], 7, v[28:29]
	v_lshl_add_u64 v[22:23], s[8:9], 0, v[22:23]
	v_lshl_add_u64 v[28:29], s[8:9], 0, v[28:29]
	v_lshl_add_u64 v[22:23], v[22:23], 0, v[130:131]
	v_lshl_add_u64 v[24:25], v[132:133], 0, s[4:5]
	v_lshl_add_u64 v[28:29], v[28:29], 0, v[130:131]
	global_load_dwordx2 v[22:23], v[22:23], off
	s_waitcnt vmcnt(1)
	v_lshlrev_b32_e32 v32, 16, v14
	global_load_dwordx2 v[26:27], v[24:25], off
	s_nop 0
	global_load_dwordx2 v[28:29], v[28:29], off
	s_nop 0
	global_load_dwordx2 v[30:31], v[24:25], off offset:64
	v_and_b32_e32 v14, 0xffff0000, v14
	s_nop 0
	v_cvt_pk_fp8_f32 v98, v32, v14
	v_lshlrev_b32_e32 v32, 16, v16
	v_and_b32_e32 v16, 0xffff0000, v16
	s_nop 0
	v_cvt_pk_fp8_f32 v99, v32, v16
	v_lshlrev_b32_e32 v14, 16, v15
	v_and_b32_e32 v15, 0xffff0000, v15
	v_cvt_pk_fp8_f32 v98, v14, v15 op_sel:[0,0,1]
	v_lshlrev_b32_e32 v14, 16, v17
	v_and_b32_e32 v15, 0xffff0000, v17
	v_cvt_pk_fp8_f32 v99, v14, v15 op_sel:[0,0,1]
	v_lshlrev_b32_e32 v14, 16, v10
	v_and_b32_e32 v10, 0xffff0000, v10
	s_nop 0
	v_cvt_pk_fp8_f32 v100, v14, v10
	v_lshlrev_b32_e32 v14, 16, v12
	v_and_b32_e32 v12, 0xffff0000, v12
	s_nop 0
	v_cvt_pk_fp8_f32 v101, v14, v12
	v_lshlrev_b32_e32 v10, 16, v11
	v_and_b32_e32 v11, 0xffff0000, v11
	v_cvt_pk_fp8_f32 v100, v10, v11 op_sel:[0,0,1]
	v_lshlrev_b32_e32 v10, 16, v13
	v_and_b32_e32 v11, 0xffff0000, v13
	v_cvt_pk_fp8_f32 v101, v10, v11 op_sel:[0,0,1]
	v_lshlrev_b32_e32 v10, 16, v6
	v_and_b32_e32 v6, 0xffff0000, v6
	s_nop 0
	v_cvt_pk_fp8_f32 v102, v10, v6
	v_lshlrev_b32_e32 v10, 16, v8
	v_and_b32_e32 v8, 0xffff0000, v8
	s_nop 0
	v_cvt_pk_fp8_f32 v103, v10, v8
	v_lshlrev_b32_e32 v6, 16, v7
	v_and_b32_e32 v7, 0xffff0000, v7
	v_cvt_pk_fp8_f32 v102, v6, v7 op_sel:[0,0,1]
	v_lshlrev_b32_e32 v6, 16, v9
	v_and_b32_e32 v7, 0xffff0000, v9
	v_cvt_pk_fp8_f32 v103, v6, v7 op_sel:[0,0,1]
	v_lshlrev_b32_e32 v6, 16, v2
	v_and_b32_e32 v2, 0xffff0000, v2
	s_nop 0
	v_cvt_pk_fp8_f32 v104, v6, v2
	v_lshlrev_b32_e32 v6, 16, v4
	v_and_b32_e32 v4, 0xffff0000, v4
	s_nop 0
	v_cvt_pk_fp8_f32 v105, v6, v4
	v_lshlrev_b32_e32 v2, 16, v3
	v_and_b32_e32 v3, 0xffff0000, v3
	v_cvt_pk_fp8_f32 v104, v2, v3 op_sel:[0,0,1]
	v_lshlrev_b32_e32 v2, 16, v5
	v_and_b32_e32 v3, 0xffff0000, v5
	v_cvt_pk_fp8_f32 v105, v2, v3 op_sel:[0,0,1]
	v_lshlrev_b32_e32 v3, 2, v21
	v_mul_lo_u32 v2, v154, s29
	v_and_b32_e32 v4, 16, v3
	v_add_u32_e32 v155, v2, v130
	v_add_u32_e32 v2, v2, v4
	v_and_or_b32 v156, v3, 12, v2
	s_or_b32 s10, s4, 0x80
	s_addk_i32 s4, 0xf080
	v_add_u32_e32 v2, 0, v156
	s_and_b64 s[6:7], s[6:7], exec
	v_add_u32_e32 v5, 0, v155
	v_add_u32_e32 v3, 0x1400, v2
	v_add_u32_e32 v2, 0x5800, v2
	s_cselect_b32 s4, s10, s4
	s_andn2_b64 vcc, exec, s[24:25]
	s_waitcnt vmcnt(3)
	ds_write_b64 v5, v[22:23]
	s_waitcnt vmcnt(2)
	ds_write2_b32 v3, v26, v27 offset1:8
	s_waitcnt vmcnt(1)
	ds_write_b64 v5, v[28:29] offset:18048
	s_waitcnt vmcnt(0)
	ds_write2_b32 v2, v30, v31 offset0:160 offset1:168
	v_add_u32_e32 v2, s4, v154
	v_ashrrev_i32_e32 v3, 31, v2
	v_lshlrev_b64 v[2:3], 7, v[2:3]
	v_lshl_add_u64 v[2:3], s[8:9], 0, v[2:3]
	v_lshl_add_u64 v[2:3], v[2:3], 0, v[130:131]
	s_waitcnt lgkmcnt(0)
	s_barrier
	global_load_dwordx2 v[134:135], v[2:3], off
	global_load_dwordx2 v[136:137], v[24:25], off offset:128
	v_mul_u32_u24_e32 v2, 0x50, v18
	v_add3_u32 v157, v2, v19, 0
	ds_read_b128 v[2:5], v157
	ds_read_b128 v[6:9], v157 offset:16
	s_waitcnt lgkmcnt(0)
	v_mfma_f32_32x32x64_f8f6f4 v[50:65], v[2:9], v[98:105], 0
	ds_read_b128 v[2:5], v157 offset:2560
	ds_read_b128 v[6:9], v157 offset:2576
	s_waitcnt lgkmcnt(0)
	v_mfma_f32_32x32x64_f8f6f4 v[34:49], v[2:9], v[98:105], 0
	s_cbranch_vccnz .LBB0_711
	v_ashrrev_i32_e32 v3, 1, v153
	v_lshlrev_b32_e32 v4, 2, v3
	v_and_b32_e32 v158, 16, v4
	v_lshrrev_b32_e32 v4, 1, v3
	v_and_b32_e32 v2, 0x3fff00, v153
	v_and_b32_e32 v5, 12, v4
	v_and_b32_e32 v6, 0x63, v3
	v_or3_b32 v159, v6, v2, v5
	v_lshlrev_b32_e32 v2, 4, v153
	v_and_b32_e32 v160, 16, v2
	v_lshlrev_b32_e32 v2, 4, v3
	v_lshrrev_b32_e32 v5, 2, v3
	v_and_b32_e32 v6, 0x3fff03, v3
	v_and_b32_e32 v4, 0x60, v4
	v_and_b32_e32 v5, 12, v5
	v_and_or_b32 v2, v2, s46, v6
	v_or3_b32 v161, v2, v4, v5
	v_mov_b32_e32 v2, v107
	s_lshl_b32 s16, s63, 2
	v_mad_u32_u24 v4, v20, 36, 0
	s_lshl_b32 s4, s62, 8
	v_mad_u64_u32 v[2:3], s[6:7], v3, 36, v[2:3]
	v_mov_b32_e32 v18, 0
	s_and_b32 s17, s4, 0x300
	s_and_b32 s18, s4, 0x700
	s_mov_b32 s19, 0
	v_add_u32_e32 v162, s16, v4
	v_lshlrev_b32_e32 v106, 2, v20
	v_add_u32_e32 v163, v2, v160
	s_mov_b32 s24, 0
	s_mov_b32 s14, 0
	v_mov_b32_e32 v19, v18
	v_mov_b32_e32 v20, v18
	v_mov_b32_e32 v21, v18
	v_mov_b32_e32 v22, v18
	v_mov_b32_e32 v23, v18
	v_mov_b32_e32 v24, v18
	v_mov_b32_e32 v25, v18
	v_mov_b32_e32 v26, v18
	v_mov_b32_e32 v27, v18
	v_mov_b32_e32 v28, v18
	v_mov_b32_e32 v29, v18
	v_mov_b32_e32 v30, v18
	v_mov_b32_e32 v31, v18
	v_mov_b32_e32 v32, v18
	v_mov_b32_e32 v33, v18
	v_mov_b32_e32 v2, v18
	v_mov_b32_e32 v3, v18
	v_mov_b32_e32 v4, v18
	v_mov_b32_e32 v5, v18
	v_mov_b32_e32 v6, v18
	v_mov_b32_e32 v7, v18
	v_mov_b32_e32 v8, v18
	v_mov_b32_e32 v9, v18
	v_mov_b32_e32 v10, v18
	v_mov_b32_e32 v11, v18
	v_mov_b32_e32 v12, v18
	v_mov_b32_e32 v13, v18
	v_mov_b32_e32 v14, v18
	v_mov_b32_e32 v15, v18
	v_mov_b32_e32 v16, v18
	v_mov_b32_e32 v17, v18
	v_mov_b32_e32 v108, v18
	v_mov_b32_e32 v109, v18
	v_mov_b32_e32 v110, v18
	v_mov_b32_e32 v111, v18
	s_branch .LBB0_703
; DI void attn_unit_a8(unsigned char* lds, const AttnArgs& a) {
;     ...
;     auto w_cvt = [&]() __attribute__((always_inline)) { unsigned char* t8 = lds + AT_WT + wn4 * WPITCH + 4 * wid;
; #pragma unroll
;         for (int j = 0; j < 4; ++j) *(unsigned*)(t8 + j * WPITCH) = pk4_fp8_mul64(wq[0][j], wq[1][j], wq[2][j], wq[3][j]); };
;     const int wcol = tid >> 1, whalf = tid & 1;
;     const unsigned wper_gu = (unsigned)((wcol >> 7) * 256 + (wcol & 96) + invperm32(wcol & 31)) * 1024u + 16u * whalf;
;     const unsigned wper_dn = (unsigned)fwd_lane16(wcol) * 1024u + 16u * whalf;
;     auto w_store = [&](int j) __attribute__((always_inline)) { const float* src; unsigned char* dst; int ld, n0, k0; bool gu; w_decode(j, src, dst, ld, n0, k0, gu);
;         const int nb = n0 >> 8; const unsigned uni = (unsigned)(gu ? (nb & 3) * 512 + (nb >> 2) * 128 : nb * 256) * 1024u + (unsigned)k0;
;         const unsigned off = (gu ? wper_gu : wper_dn) + uni;
;         const unsigned* t = (const unsigned*)(lds + AT_WT + wcol * WPITCH + 16 * whalf);
;         *(u32x4*)(dst + off) = (u32x4){t[0], t[1], t[2], t[3]}; };
;     const bool wrider = a.wl >= 0;
;     if (wrider) w_issue(0);
;     gload(a.t0, kregA, vregA); gload(a.t0 + 1 < a.t1 ? a.t0 + 1 : a.t0, kregB, vregB);
;     lstore(0, kregA, vregA); lstore(1, kregB, vregB);
;     __syncthreads();
;     asm volatile("" : "+v"(qf8));
;     if (a.t0 + 2 < a.t1) gload(a.t0 + 2, kregA, vregA);
;     f32x16 sx0, sx1, sy0, sy1;
;     sx0 = mfma8(kread(lds, 0), qf8, cinit); sx1 = mfma8(kread(lds, 1), qf8, cinit);
;     int slot = 0;
;     auto step = [&](int t, u32x2& kl, u32x2& vl, const u32x2& ks, const u32x2& vs, f32x16& c0, f32x16& c1, f32x16& n0, f32x16& n1, const int hk, const int wj) __attribute__((always_inline)) {
;         const int slot1 = slot == 2 ? 0 : slot + 1, slot2 = slot1 == 2 ? 0 : slot1 + 1;
;         if (hk == 1) { w_cvt(); w_issue(wj + 1 < AT_NWT ? wj + 1 : AT_NWT - 1); }
;         if (hk == 2) w_store(wj);
;         { const int tn = t + 3; gload(tn < a.t1 ? tn : a.t1 - 1, kl, vl); }
;         const unsigned char* Kb = lds + slot * AT_BUFB; const unsigned char* Kn = lds + slot1 * AT_BUFB;
;         const v8i k0 = kread(Kn, 0), k1 = kread(Kn, 1), v0 = vread(Kb, 0), v1 = vread(Kb, 1);
;         n0 = mfma8(k0, qf8, cinit); n1 = mfma8(k1, qf8, cinit);
;         expsum(c0); expsum(c1);
;         const v8i P = pack8(c0, c1);
.LBB0_702:
	s_lshl_b32 s4, s14, 1
	s_waitcnt lgkmcnt(0)
	s_lshr_b32 s12, s14, 3
	s_and_b32 s4, s4, 0x600
	s_and_b32 s12, s12, 0x80
	s_or_b32 s4, s4, s12
	s_and_b64 s[10:11], s[10:11], exec
	s_cselect_b32 s4, s4, s14
	s_and_b32 s10, s24, 3
	s_add_i32 s10, s63, s10
	s_lshl_b32 s10, s10, 5
	s_lshl_b32 s4, s4, 10
	s_add_i32 s15, s4, s10
	s_min_i32 s4, s56, 63
	s_cmp_lt_u32 s56, 60
	s_cselect_b64 s[10:11], -1, 0
	s_lshl_b32 s4, s4, 6
	v_pk_add_f32 v[48:49], v[146:147], v[110:111]
	s_add_i32 s14, s4, 0x100
	s_add_i32 s63, s4, 0xfffff100
	v_pk_add_f32 v[46:47], v[150:151], v[108:109]
	v_pk_add_f32 v[48:49], v[148:149], v[48:49]
	s_and_b64 s[12:13], s[10:11], exec
	v_pk_add_f32 v[46:47], v[142:143], v[46:47]
	v_pk_add_f32 v[48:49], v[58:59], v[48:49]
	s_cselect_b32 s12, s14, s63
	s_add_i32 s25, s25, 1
	v_pk_add_f32 v[46:47], v[144:145], v[46:47]
	v_pk_add_f32 v[48:49], v[60:61], v[48:49]
	s_and_b64 s[6:7], s[6:7], exec
	v_pk_add_f32 v[46:47], v[52:53], v[46:47]
	v_pk_add_f32 v[48:49], v[50:51], v[48:49]
	s_cselect_b32 s14, 0, s25
	v_pk_add_f32 v[46:47], v[56:57], v[46:47]
	v_pk_add_f32 v[48:49], v[54:55], v[48:49]
	s_mul_i32 s6, s14, 0x4680
	v_pk_add_f32 v[38:39], v[38:39], v[46:47]
	v_pk_add_f32 v[36:37], v[36:37], v[48:49]
	v_add_u32_e32 v48, 0xd808, v163
	v_add_u32_e32 v134, s6, v157
	v_pk_add_f32 v[50:51], v[42:43], v[38:39]
	v_pk_add_f32 v[108:109], v[40:41], v[36:37]
	v_add_u32_e32 v45, 0xd800, v163
	ds_read_b128 v[36:39], v134
	ds_read_b128 v[40:43], v134 offset:16
	ds_read2_b32 v[46:47], v45 offset1:1
	ds_read2_b32 v[48:49], v48 offset1:1
	v_pk_add_f32 v[110:111], v[34:35], v[50:51]
	v_add_u32_e32 v34, v44, v158
	v_lshl_or_b32 v34, v34, 10, v160
	v_add_u32_e32 v34, s15, v34
	s_waitcnt lgkmcnt(0)
	global_store_dwordx4 v34, v[46:49], s[8:9]
	v_add_u32_e32 v34, s12, v154
	s_and_b64 s[8:9], s[10:11], exec
	v_ashrrev_i32_e32 v35, 31, v34
	s_cselect_b32 s9, s59, s61
	s_cselect_b32 s8, s58, s60
	v_lshlrev_b64 v[34:35], 7, v[34:35]
	v_mfma_f32_32x32x64_f8f6f4 v[50:65], v[36:43], v[98:105], 0
	v_lshl_add_u64 v[42:43], s[8:9], 0, v[34:35]
	v_lshl_add_u64 v[42:43], v[42:43], 0, v[130:131]
	ds_read_b128 v[34:37], v134 offset:2560
	ds_read_b128 v[38:41], v134 offset:2576
	global_load_dwordx2 v[134:135], v[42:43], off
	v_lshl_add_u64 v[42:43], v[132:133], 0, s[4:5]
	global_load_dwordx2 v[136:137], v[42:43], off offset:256
	v_exp_f32_e32 v82, v82
	v_exp_f32_e32 v83, v83
	v_exp_f32_e32 v86, v86
	v_exp_f32_e32 v87, v87
	v_exp_f32_e32 v90, v90
	v_exp_f32_e32 v91, v91
	v_exp_f32_e32 v94, v94
	v_exp_f32_e32 v95, v95
	v_exp_f32_e32 v150, v66
	v_exp_f32_e32 v151, v67
	v_exp_f32_e32 v174, v70
	v_exp_f32_e32 v175, v71
	v_exp_f32_e32 v74, v74
	v_exp_f32_e32 v75, v75
	v_exp_f32_e32 v78, v78
	v_exp_f32_e32 v79, v79
	ds_read_b128 v[142:145], v164 offset:5120
	ds_read_b128 v[146:149], v164 offset:5136
	ds_read_b128 v[166:169], v164 offset:7680
	ds_read_b128 v[170:173], v164 offset:7696
	v_exp_f32_e32 v84, v84
	v_exp_f32_e32 v85, v85
	v_exp_f32_e32 v88, v88
	v_exp_f32_e32 v89, v89
	v_exp_f32_e32 v92, v92
	v_exp_f32_e32 v93, v93
	v_exp_f32_e32 v96, v96
	v_exp_f32_e32 v97, v97
	v_exp_f32_e32 v164, v68
	v_exp_f32_e32 v165, v69
	v_exp_f32_e32 v176, v72
	v_exp_f32_e32 v177, v73
	v_exp_f32_e32 v76, v76
	v_exp_f32_e32 v77, v77
	v_exp_f32_e32 v80, v80
	v_exp_f32_e32 v81, v81
	s_nop 0
	s_nop 0
	s_nop 0
	s_nop 0
	s_nop 0
	s_nop 0
	s_nop 0
	s_nop 0
	v_cvt_scalef32_pk_fp8_f32 v66, v82, v83, s48
	v_cvt_scalef32_pk_fp8_f32 v70, v150, v151, s48
	v_cvt_scalef32_pk_fp8_f32 v67, v86, v87, s48
	v_cvt_scalef32_pk_fp8_f32 v71, v174, v175, s48
	v_cvt_scalef32_pk_fp8_f32 v68, v90, v91, s48
	v_cvt_scalef32_pk_fp8_f32 v72, v74, v75, s48
	v_cvt_scalef32_pk_fp8_f32 v69, v94, v95, s48
	v_cvt_scalef32_pk_fp8_f32 v73, v78, v79, s48
	v_cvt_scalef32_pk_fp8_f32 v66, v84, v85, s48 op_sel:[0,0,0,1]
	v_cvt_scalef32_pk_fp8_f32 v70, v164, v165, s48 op_sel:[0,0,0,1]
	v_cvt_scalef32_pk_fp8_f32 v67, v88, v89, s48 op_sel:[0,0,0,1]
	v_cvt_scalef32_pk_fp8_f32 v71, v176, v177, s48 op_sel:[0,0,0,1]
	v_cvt_scalef32_pk_fp8_f32 v68, v92, v93, s48 op_sel:[0,0,0,1]
	v_cvt_scalef32_pk_fp8_f32 v72, v76, v77, s48 op_sel:[0,0,0,1]
	v_cvt_scalef32_pk_fp8_f32 v69, v96, v97, s48 op_sel:[0,0,0,1]
	v_cvt_scalef32_pk_fp8_f32 v73, v80, v81, s48 op_sel:[0,0,0,1]
	s_waitcnt lgkmcnt(4)
	v_mfma_f32_32x32x64_f8f6f4 v[34:49], v[34:41], v[98:105], 0
	v_add_f32_e64 v110, v110, v82
	v_add_f32_e64 v111, v111, v83
	v_add_f32_e64 v82, v108, v84
	v_add_f32_e64 v83, v109, v85
	v_add_f32_e64 v84, v86, v110
	v_add_f32_e64 v85, v87, v111
	v_add_f32_e64 v82, v88, v82
	v_add_f32_e64 v83, v89, v83
	s_addk_i32 s6, 0x4680
	v_add_f32_e64 v84, v90, v84
	v_add_f32_e64 v85, v91, v85
	v_add_f32_e64 v82, v92, v82
	v_add_f32_e64 v83, v93, v83
	s_cmp_lg_u32 s14, 2
	v_pk_add_f32 v[82:83], v[96:97], v[82:83]
	v_pk_add_f32 v[84:85], v[94:95], v[84:85]
	s_cselect_b32 s4, s6, 0
	v_pk_add_f32 v[84:85], v[150:151], v[84:85]
	v_pk_add_f32 v[82:83], v[164:165], v[82:83]
	s_add_i32 s4, s4, 0
	v_pk_add_f32 v[82:83], v[176:177], v[82:83]
	s_waitcnt lgkmcnt(2)
	v_mfma_f32_32x32x64_f8f6f4 v[18:33], v[142:149], v[66:73], v[18:33]
	v_add_f32_e64 v84, v174, v84
	v_add_f32_e64 v85, v175, v85
	v_add_f32_e64 v76, v76, v82
	v_add_f32_e64 v77, v77, v83
	v_add_f32_e64 v74, v74, v84
	v_add_f32_e64 v75, v75, v85
	s_add_i32 s24, s24, 1
	s_add_i32 s56, s56, 2
	s_addk_i32 s19, 0x80
	v_add_f32_e64 v110, v80, v76
	v_add_f32_e64 v111, v81, v77
	v_add_f32_e64 v108, v78, v74
	v_add_f32_e64 v109, v79, v75
	s_cmp_lg_u32 s24, 24
	s_waitcnt lgkmcnt(0)
	v_mfma_f32_32x32x64_f8f6f4 v[2:17], v[166:173], v[66:73], v[2:17]
	v_add_u32_e32 v66, s4, v155
	s_waitcnt vmcnt(4)
	ds_write_b64 v66, v[138:139]
	v_add_u32_e32 v66, s4, v156
	v_add_u32_e32 v66, 0x1400, v66
	s_waitcnt vmcnt(3)
	ds_write2_b32 v66, v140, v141 offset1:8
	s_waitcnt lgkmcnt(0)
	s_barrier
	s_cbranch_scc0 .LBB0_712
.LBB0_703:
	s_min_u32 s15, s24, 22
	s_add_i32 s15, s15, 1
	s_lshl_b32 s4, s15, 7
	s_and_b32 s4, s4, 0x1e00
	s_nop 0
	s_nop 0
	s_add_i32 s6, s4, s62
	v_cvt_scalef32_pk_fp8_f32 v66, v116, v112, s47
	v_cvt_scalef32_pk_fp8_f32 v67, v117, v113, s47
	s_mul_hi_u32 s4, s6, 0xaaaaaaab
	v_cvt_scalef32_pk_fp8_f32 v66, v120, v124, s47 op_sel:[0,0,0,1]
	v_cvt_scalef32_pk_fp8_f32 v67, v121, v125, s47 op_sel:[0,0,0,1]
	v_add_u32_e32 v68, 0xd800, v162
	s_lshr_b32 s4, s4, 6
	ds_write2_b32 v68, v66, v67 offset1:9
	s_nop 0
	s_nop 0
	s_mul_i32 s63, s4, 0xffffffa0
	v_cvt_scalef32_pk_fp8_f32 v66, v118, v114, s47
	v_cvt_scalef32_pk_fp8_f32 v67, v119, v115, s47
	s_add_i32 s63, s63, s6
	v_cvt_scalef32_pk_fp8_f32 v66, v122, v126, s47 op_sel:[0,0,0,1]
	v_cvt_scalef32_pk_fp8_f32 v67, v123, v127, s47 op_sel:[0,0,0,1]
	s_mov_b64 s[10:11], s[0:1]
	s_cmp_gt_i32 s63, 63
	s_mov_b64 s[12:13], -1
	ds_write2_b32 v68, v66, v67 offset0:18 offset1:27
	s_cbranch_scc0 .LBB0_705
	s_load_dwordx2 s[6:7], s[10:11], 0xc0
	s_lshl_b64 s[8:9], s[4:5], 22
	s_mov_b64 s[12:13], 0
	s_waitcnt lgkmcnt(0)
	s_add_u32 s6, s6, s8
	s_addc_u32 s7, s7, s9
	s_and_b32 s8, s63, 0x7ffffffc
	s_sub_i32 s25, s8, 64

; DI void attn_unit_a8(unsigned char* lds, const AttnArgs& a) {
;     ...
;     auto w_issue = [&](int j) __attribute__((always_inline)) { const float* src; unsigned char* dst; int ld, n0, k0; bool gu; w_decode(j, src, dst, ld, n0, k0, gu);
;         const float* p = src + (size_t)(k0 + 4 * wid) * ld + n0 + wn4;
;         wq[0] = __builtin_nontemporal_load((const f32x4*)p); wq[1] = __builtin_nontemporal_load((const f32x4*)(p + ld));
;         wq[2] = __builtin_nontemporal_load((const f32x4*)(p + (size_t)2 * ld)); wq[3] = __builtin_nontemporal_load((const f32x4*)(p + (size_t)3 * ld)); };
;     auto w_cvt = [&]() __attribute__((always_inline)) { unsigned char* t8 = lds + AT_WT + wn4 * WPITCH + 4 * wid;
; #pragma unroll
;         for (int j = 0; j < 4; ++j) *(unsigned*)(t8 + j * WPITCH) = pk4_fp8_mul64(wq[0][j], wq[1][j], wq[2][j], wq[3][j]); };
;     const int wcol = tid >> 1, whalf = tid & 1;
;     const unsigned wper_gu = (unsigned)((wcol >> 7) * 256 + (wcol & 96) + invperm32(wcol & 31)) * 1024u + 16u * whalf;
;     const unsigned wper_dn = (unsigned)fwd_lane16(wcol) * 1024u + 16u * whalf;
;     auto w_store = [&](int j) __attribute__((always_inline)) { const float* src; unsigned char* dst; int ld, n0, k0; bool gu; w_decode(j, src, dst, ld, n0, k0, gu);
;         const int nb = n0 >> 8; const unsigned uni = (unsigned)(gu ? (nb & 3) * 512 + (nb >> 2) * 128 : nb * 256) * 1024u + (unsigned)k0;
;         const unsigned off = (gu ? wper_gu : wper_dn) + uni;
;         const unsigned* t = (const unsigned*)(lds + AT_WT + wcol * WPITCH + 16 * whalf);
;         *(u32x4*)(dst + off) = (u32x4){t[0], t[1], t[2], t[3]}; };
;     const bool wrider = a.wl >= 0;
;     if (wrider) w_issue(0);
;     gload(a.t0, kregA, vregA); gload(a.t0 + 1 < a.t1 ? a.t0 + 1 : a.t0, kregB, vregB);
;     lstore(0, kregA, vregA); lstore(1, kregB, vregB);
;     __syncthreads();
;     asm volatile("" : "+v"(qf8));
;     if (a.t0 + 2 < a.t1) gload(a.t0 + 2, kregA, vregA);
;     f32x16 sx0, sx1, sy0, sy1;
;     sx0 = mfma8(kread(lds, 0), qf8, cinit); sx1 = mfma8(kread(lds, 1), qf8, cinit);
;     int slot = 0;
;     auto step = [&](int t, u32x2& kl, u32x2& vl, const u32x2& ks, const u32x2& vs, f32x16& c0, f32x16& c1, f32x16& n0, f32x16& n1, const int hk, const int wj) __attribute__((always_inline)) {
;         const int slot1 = slot == 2 ? 0 : slot + 1, slot2 = slot1 == 2 ? 0 : slot1 + 1;
.LBB0_707:
	s_and_b32 s4, s15, 3
	s_add_i32 s4, s25, s4
	s_lshl_b32 s4, s4, 5
	s_add_i32 s4, s4, s16
	s_mul_hi_i32 s11, s8, s4
	s_mul_i32 s10, s8, s4
	s_lshl_b64 s[10:11], s[10:11], 2
	s_add_u32 s4, s6, s10
	s_addc_u32 s7, s7, s11
	s_lshl_b32 s6, s9, 2
	s_add_u32 s6, s4, s6
	s_addc_u32 s7, s7, 0
	v_lshl_add_u64 v[66:67], s[6:7], 0, v[106:107]
	s_lshl_b32 s4, s8, 2
	v_lshl_add_u64 v[74:75], v[66:67], 0, s[4:5]
	v_lshl_add_u64 v[76:77], v[74:75], 0, s[4:5]
	v_lshl_add_u64 v[78:79], v[76:77], 0, s[4:5]
	s_min_i32 s4, s56, 64
	s_cmp_lt_u32 s56, 61
	s_cselect_b64 s[8:9], -1, 0
	s_lshl_b32 s4, s4, 6
	s_add_i32 s12, s4, 0xc0
	s_add_i32 s13, s4, 0xfffff0c0
	s_and_b64 s[10:11], s[8:9], exec
	s_cselect_b32 s10, s12, s13
	s_add_i32 s11, s14, 1
	s_cmp_lg_u32 s14, 2
	s_cselect_b32 s25, s11, 0
	s_mul_i32 s11, s25, 0x4680
	v_add_u32_e32 v164, s11, v157
	ds_read_b128 v[66:69], v164
	ds_read_b128 v[70:73], v164 offset:16
	global_load_dwordx4 v[116:119], v106, s[6:7] nt
	global_load_dwordx4 v[112:115], v[74:75], off nt
	global_load_dwordx4 v[120:123], v[76:77], off nt
	global_load_dwordx4 v[124:127], v[78:79], off nt
	v_add_u32_e32 v74, s10, v154
	s_and_b64 s[6:7], s[8:9], exec
	v_ashrrev_i32_e32 v75, 31, v74
	s_cselect_b32 s6, s58, s60
	s_cselect_b32 s7, s59, s61
	v_lshlrev_b64 v[74:75], 7, v[74:75]
	v_lshl_add_u64 v[74:75], s[6:7], 0, v[74:75]
	v_lshl_add_u64 v[140:141], v[132:133], 0, s[4:5]
	s_mul_i32 s4, s14, 0x4680
	v_lshl_add_u64 v[74:75], v[74:75], 0, v[130:131]
	v_add_u32_e32 v165, s4, v157
	s_waitcnt lgkmcnt(0)
	v_mfma_f32_32x32x64_f8f6f4 v[82:97], v[66:73], v[98:105], 0
	ds_read_b128 v[66:69], v164 offset:2560
	ds_read_b128 v[70:73], v164 offset:2576
	global_load_dwordx2 v[138:139], v[74:75], off
	ds_read_b128 v[166:169], v165 offset:5120
	ds_read_b128 v[170:173], v165 offset:5136
	global_load_dwordx2 v[140:141], v[140:141], off offset:192
	v_exp_f32_e32 v150, v50
	v_exp_f32_e32 v151, v51
	v_exp_f32_e32 v146, v52
	v_exp_f32_e32 v147, v53
	v_exp_f32_e32 v142, v54
	v_exp_f32_e32 v143, v55
	v_exp_f32_e32 v148, v56
	v_exp_f32_e32 v149, v57
	v_exp_f32_e32 v144, v58
	v_exp_f32_e32 v145, v59
	v_exp_f32_e32 v52, v62
	v_exp_f32_e32 v53, v63
	v_exp_f32_e32 v56, v34
	v_exp_f32_e32 v57, v35
	v_exp_f32_e32 v38, v38
	v_exp_f32_e32 v39, v39
	v_exp_f32_e32 v42, v42
	v_exp_f32_e32 v43, v43
	v_exp_f32_e32 v34, v46
	v_exp_f32_e32 v35, v47
	v_exp_f32_e32 v58, v60
	v_exp_f32_e32 v59, v61
	v_exp_f32_e32 v60, v64
	v_exp_f32_e32 v61, v65
	v_exp_f32_e32 v50, v36
	v_exp_f32_e32 v51, v37
	v_exp_f32_e32 v54, v40
	v_exp_f32_e32 v55, v41
	v_exp_f32_e32 v36, v44
	v_exp_f32_e32 v37, v45
	v_exp_f32_e32 v40, v48
	v_exp_f32_e32 v41, v49
	s_nop 0
	s_nop 0
	s_nop 0
	s_nop 0
	s_nop 0
	s_nop 0
	s_nop 0
	s_nop 0
	v_cvt_scalef32_pk_fp8_f32 v174, v150, v151, s48
	v_cvt_scalef32_pk_fp8_f32 v178, v56, v57, s48
	v_cvt_scalef32_pk_fp8_f32 v175, v142, v143, s48
	v_cvt_scalef32_pk_fp8_f32 v179, v38, v39, s48
	v_cvt_scalef32_pk_fp8_f32 v176, v144, v145, s48
	v_cvt_scalef32_pk_fp8_f32 v180, v42, v43, s48
	v_cvt_scalef32_pk_fp8_f32 v177, v52, v53, s48
	v_cvt_scalef32_pk_fp8_f32 v181, v34, v35, s48
	v_cvt_scalef32_pk_fp8_f32 v174, v146, v147, s48 op_sel:[0,0,0,1]
	v_cvt_scalef32_pk_fp8_f32 v178, v50, v51, s48 op_sel:[0,0,0,1]
	v_cvt_scalef32_pk_fp8_f32 v175, v148, v149, s48 op_sel:[0,0,0,1]
	v_cvt_scalef32_pk_fp8_f32 v179, v54, v55, s48 op_sel:[0,0,0,1]
	v_cvt_scalef32_pk_fp8_f32 v176, v58, v59, s48 op_sel:[0,0,0,1]
	v_cvt_scalef32_pk_fp8_f32 v180, v36, v37, s48 op_sel:[0,0,0,1]
	v_cvt_scalef32_pk_fp8_f32 v177, v60, v61, s48 op_sel:[0,0,0,1]
	v_cvt_scalef32_pk_fp8_f32 v181, v40, v41, s48 op_sel:[0,0,0,1]
	s_addk_i32 s11, 0x4680
	s_cmp_eq_u32 s25, 2
	s_waitcnt lgkmcnt(0)
	v_mfma_f32_32x32x64_f8f6f4 v[18:33], v[166:173], v[174:181], v[18:33]
	ds_read_b128 v[166:169], v165 offset:7680
	ds_read_b128 v[170:173], v165 offset:7696
	s_cselect_b64 s[6:7], -1, 0
	s_and_b64 s[8:9], s[6:7], exec
	s_cselect_b32 s4, 0, s11
	s_add_i32 s4, s4, 0
	v_add_u32_e32 v44, s4, v155
	s_waitcnt vmcnt(7)
	ds_write_b64 v44, v[134:135]
	v_add_u32_e32 v44, s4, v156
	s_and_b32 s4, s19, 0xe00
	s_add_i32 s8, s4, s62
	s_mul_hi_u32 s4, s8, 0xaaaaaaab
	s_lshr_b32 s4, s4, 6
	s_mul_i32 s65, s4, 0xffffffa0
	v_add_u32_e32 v44, 0x1400, v44
	s_add_i32 s65, s65, s8
	v_mfma_f32_32x32x64_f8f6f4 v[66:81], v[66:73], v[98:105], 0
	s_mov_b64 s[8:9], s[0:1]
	s_waitcnt vmcnt(6)
	ds_write2_b32 v44, v136, v137 offset1:8
	s_waitcnt lgkmcnt(0)
	s_barrier
	s_load_dwordx2 s[12:13], s[8:9], 0xd8
	s_cmp_lt_i32 s65, 64
	s_cselect_b64 s[10:11], -1, 0
	s_cmp_gt_i32 s65, 63
	s_mov_b64 s[14:15], -1
	v_mfma_f32_32x32x64_f8f6f4 v[2:17], v[166:173], v[174:181], v[2:17]
	s_cbranch_scc0 .LBB0_709
	s_lshl_b64 s[8:9], s[4:5], 20
	s_waitcnt lgkmcnt(0)
	s_add_u32 s8, s12, s8
	s_addc_u32 s9, s13, s9
	s_add_u32 s8, s8, 0x11094000
	s_addc_u32 s9, s9, 0
	s_and_b32 s14, s65, 0x7ffffffc
	s_sub_i32 s63, s14, 64
	s_mov_b64 s[14:15], 0

; DI unsigned pk4_fp8_div16(float a, float b, float c, float d) { v2s_t r = {0, 0}; r = __builtin_amdgcn_cvt_scalef32_pk_fp8_f32(r, a, b, 16.0f, false); r = __builtin_amdgcn_cvt_scalef32_pk_fp8_f32(r, c, d, 16.0f, true); return __builtin_bit_cast(unsigned, r); }
; DI f32x16 mfma8(v8i a, v8i b, f32x16 c) { return __builtin_amdgcn_mfma_scale_f32_32x32x64_f8f6f4(a, b, c, 0, 0, 0, 0, 0, 0); }
; DI void attn_unit_a8(unsigned char* lds, const AttnArgs& a) {
;     ...
;     auto expsum = [&](f32x16& sc) __attribute__((always_inline)) {
; #pragma unroll
;         for (int i = 0; i < 16; ++i) sc[i] = __builtin_amdgcn_exp2f(sc[i]);
; #pragma unroll
;         for (int i = 0; i < 4; ++i) l0 += (f32x4){sc[4 * i], sc[4 * i + 1], sc[4 * i + 2], sc[4 * i + 3]};
;     };
;     auto pack8 = [&](const f32x16& s0, const f32x16& s1) __attribute__((always_inline)) -> v8i { v8i p;
; #pragma unroll
;         for (int g = 0; g < 4; ++g) { p[g] = (int)pk4_fp8_div16(s0[4 * g], s0[4 * g + 1], s0[4 * g + 2], s0[4 * g + 3]); p[4 + g] = (int)pk4_fp8_div16(s1[4 * g], s1[4 * g + 1], s1[4 * g + 2], s1[4 * g + 3]); }
;         return p; };
;     ...
;     auto step = [&](int t, u32x2& kl, u32x2& vl, const u32x2& ks, const u32x2& vs, f32x16& c0, f32x16& c1, f32x16& n0, f32x16& n1, const int hk, const int wj) __attribute__((always_inline)) {
;         const int slot1 = slot == 2 ? 0 : slot + 1, slot2 = slot1 == 2 ? 0 : slot1 + 1;
;         if (hk == 1) { w_cvt(); w_issue(wj + 1 < AT_NWT ? wj + 1 : AT_NWT - 1); }
;         if (hk == 2) w_store(wj);
;         { const int tn = t + 3; gload(tn < a.t1 ? tn : a.t1 - 1, kl, vl); }
;         const unsigned char* Kb = lds + slot * AT_BUFB; const unsigned char* Kn = lds + slot1 * AT_BUFB;
;         const v8i k0 = kread(Kn, 0), k1 = kread(Kn, 1), v0 = vread(Kb, 0), v1 = vread(Kb, 1);
;         n0 = mfma8(k0, qf8, cinit); n1 = mfma8(k1, qf8, cinit);
;         expsum(c0); expsum(c1);
;         const v8i P = pack8(c0, c1);
;         o0[0] = mfma8(v0, P, o0[0]); o0[1] = mfma8(v1, P, o0[1]);
;         lstore(slot2, ks, vs);
;         __syncthreads();
;         slot = slot1;
;     };
.LBB0_714:
	s_min_i32 s4, s56, 64
	s_add_i32 s6, s4, 3
	s_cmp_lt_u32 s56, 61
	s_cselect_b64 s[10:11], -1, 0
	s_lshl_b32 s4, s6, 6
	s_add_i32 s7, s4, 0xfffff000
	s_and_b64 s[12:13], s[10:11], exec
	v_mov_b64_e32 v[80:81], v[48:49]
	s_cselect_b32 s4, s4, s7
	v_mov_b64_e32 v[78:79], v[46:47]
	v_mov_b64_e32 v[76:77], v[44:45]
	v_mov_b64_e32 v[74:75], v[42:43]
	v_mov_b64_e32 v[72:73], v[40:41]
	v_mov_b64_e32 v[70:71], v[38:39]
	v_mov_b64_e32 v[68:69], v[36:37]
	v_mov_b64_e32 v[66:67], v[34:35]
	v_add_u32_e32 v42, s4, v154
	s_add_i32 s4, s8, 1
	s_cmp_lg_u32 s8, 2
	s_mov_b32 s9, s8
	s_cselect_b32 s8, s4, 0
	s_mul_i32 s4, s8, 0x4680
	v_add_u32_e32 v106, s4, v157
	ds_read_b128 v[34:37], v106
	ds_read_b128 v[38:41], v106 offset:16
	v_mov_b64_e32 v[96:97], v[64:65]
	s_and_b64 s[10:11], s[10:11], exec
	v_ashrrev_i32_e32 v43, 31, v42
	v_mov_b64_e32 v[94:95], v[62:63]
	v_mov_b64_e32 v[92:93], v[60:61]
	v_mov_b64_e32 v[90:91], v[58:59]
	v_mov_b64_e32 v[88:89], v[56:57]
	v_mov_b64_e32 v[86:87], v[54:55]
	v_mov_b64_e32 v[84:85], v[52:53]
	v_mov_b64_e32 v[82:83], v[50:51]
	s_cselect_b32 s10, s58, s60
	s_cselect_b32 s11, s59, s61
	s_ashr_i32 s7, s6, 31
	s_waitcnt lgkmcnt(0)
	v_mfma_f32_32x32x64_f8f6f4 v[50:65], v[34:41], v[98:105], 0
	v_lshlrev_b64 v[34:35], 7, v[42:43]
	s_lshl_b64 s[12:13], s[6:7], 6
	v_lshl_add_u64 v[34:35], s[10:11], 0, v[34:35]
	v_lshl_add_u64 v[34:35], v[34:35], 0, v[130:131]
	v_lshl_add_u64 v[42:43], v[132:133], 0, s[12:13]
	global_load_dwordx2 v[112:113], v[34:35], off
	ds_read_b128 v[34:37], v106 offset:2560
	ds_read_b128 v[38:41], v106 offset:2576
	global_load_dwordx2 v[114:115], v[42:43], off
	s_mulk_i32 s9, 0x4680
	v_add_u32_e32 v42, s9, v157
	v_exp_f32_e32 v82, v82
	v_exp_f32_e32 v83, v83
	v_exp_f32_e32 v86, v86
	v_exp_f32_e32 v87, v87
	v_exp_f32_e32 v90, v90
	v_exp_f32_e32 v91, v91
	v_exp_f32_e32 v94, v94
	v_exp_f32_e32 v95, v95
	v_exp_f32_e32 v124, v66
	v_exp_f32_e32 v125, v67
	v_exp_f32_e32 v146, v70
	v_exp_f32_e32 v147, v71
	v_exp_f32_e32 v74, v74
	v_exp_f32_e32 v75, v75
	v_exp_f32_e32 v78, v78
	v_exp_f32_e32 v79, v79
	ds_read_b128 v[116:119], v42 offset:5120
	ds_read_b128 v[120:123], v42 offset:5136
	ds_read_b128 v[138:141], v42 offset:7680
	ds_read_b128 v[142:145], v42 offset:7696
	v_exp_f32_e32 v84, v84
	v_exp_f32_e32 v85, v85
	v_exp_f32_e32 v88, v88
	v_exp_f32_e32 v89, v89
	v_exp_f32_e32 v92, v92
	v_exp_f32_e32 v93, v93
	v_exp_f32_e32 v96, v96
	v_exp_f32_e32 v97, v97
	v_exp_f32_e32 v126, v68
	v_exp_f32_e32 v127, v69
	v_exp_f32_e32 v148, v72
	v_exp_f32_e32 v149, v73
	v_exp_f32_e32 v76, v76
	v_exp_f32_e32 v77, v77
	v_exp_f32_e32 v80, v80
	v_exp_f32_e32 v81, v81
	s_nop 0
	s_nop 0
	s_nop 0
	s_nop 0
	s_nop 0
	s_nop 0
	s_nop 0
	s_nop 0
	v_cvt_scalef32_pk_fp8_f32 v66, v82, v83, s48
	v_cvt_scalef32_pk_fp8_f32 v70, v124, v125, s48
	v_cvt_scalef32_pk_fp8_f32 v67, v86, v87, s48
	v_cvt_scalef32_pk_fp8_f32 v71, v146, v147, s48
	v_cvt_scalef32_pk_fp8_f32 v68, v90, v91, s48
	v_cvt_scalef32_pk_fp8_f32 v72, v74, v75, s48
	v_cvt_scalef32_pk_fp8_f32 v69, v94, v95, s48
	v_cvt_scalef32_pk_fp8_f32 v73, v78, v79, s48
	v_cvt_scalef32_pk_fp8_f32 v66, v84, v85, s48 op_sel:[0,0,0,1]
	v_cvt_scalef32_pk_fp8_f32 v70, v126, v127, s48 op_sel:[0,0,0,1]
	v_cvt_scalef32_pk_fp8_f32 v67, v88, v89, s48 op_sel:[0,0,0,1]
	v_cvt_scalef32_pk_fp8_f32 v71, v148, v149, s48 op_sel:[0,0,0,1]
	v_cvt_scalef32_pk_fp8_f32 v68, v92, v93, s48 op_sel:[0,0,0,1]
	v_cvt_scalef32_pk_fp8_f32 v72, v76, v77, s48 op_sel:[0,0,0,1]
	v_cvt_scalef32_pk_fp8_f32 v69, v96, v97, s48 op_sel:[0,0,0,1]
	v_cvt_scalef32_pk_fp8_f32 v73, v80, v81, s48 op_sel:[0,0,0,1]
	s_waitcnt lgkmcnt(4)
	v_mfma_f32_32x32x64_f8f6f4 v[34:49], v[34:41], v[98:105], 0
	s_addk_i32 s4, 0x4680
	s_cmp_eq_u32 s8, 2
	v_add_f32_e64 v110, v110, v84
	v_add_f32_e64 v111, v111, v85
	v_add_f32_e64 v82, v108, v82
	v_add_f32_e64 v83, v109, v83
	s_cselect_b64 s[6:7], -1, 0
	v_add_f32_e64 v84, v88, v110
	v_add_f32_e64 v85, v89, v111
	v_add_f32_e64 v82, v86, v82
	v_add_f32_e64 v83, v87, v83
	v_add_f32_e64 v84, v92, v84
	v_add_f32_e64 v85, v93, v85
	v_pk_add_f32 v[82:83], v[90:91], v[82:83]
	s_and_b64 s[10:11], s[6:7], exec
	v_pk_add_f32 v[84:85], v[96:97], v[84:85]
	v_pk_add_f32 v[82:83], v[94:95], v[82:83]
	s_cselect_b32 s4, 0, s4
	v_pk_add_f32 v[82:83], v[124:125], v[82:83]
	v_pk_add_f32 v[84:85], v[126:127], v[84:85]
	s_waitcnt lgkmcnt(2)
	v_mfma_f32_32x32x64_f8f6f4 v[18:33], v[116:123], v[66:73], v[18:33]
	s_add_i32 s4, s4, 0
	v_add_f32_e64 v84, v148, v84
	v_add_f32_e64 v85, v149, v85
	v_add_f32_e64 v82, v146, v82
	v_add_f32_e64 v83, v147, v83
	v_add_f32_e64 v76, v76, v84
	v_add_f32_e64 v77, v77, v85
	v_add_f32_e64 v74, v74, v82
	v_add_f32_e64 v75, v75, v83
	v_add_f32_e64 v110, v80, v76
	v_add_f32_e64 v111, v81, v77
	v_add_f32_e64 v108, v78, v74
	v_add_f32_e64 v109, v79, v75
	s_cmpk_gt_u32 s56, 0x42
	s_waitcnt lgkmcnt(0)
	v_mfma_f32_32x32x64_f8f6f4 v[2:17], v[138:145], v[66:73], v[2:17]
	v_add_u32_e32 v66, s4, v155
	s_waitcnt vmcnt(3)
	ds_write_b64 v66, v[134:135]
	v_add_u32_e32 v66, s4, v156
	v_add_u32_e32 v66, 0x1400, v66
	s_waitcnt vmcnt(2)
	ds_write2_b32 v66, v136, v137 offset1:8
	s_waitcnt lgkmcnt(0)
	s_barrier
; DI unsigned pk4_fp8_div16(float a, float b, float c, float d) { v2s_t r = {0, 0}; r = __builtin_amdgcn_cvt_scalef32_pk_fp8_f32(r, a, b, 16.0f, false); r = __builtin_amdgcn_cvt_scalef32_pk_fp8_f32(r, c, d, 16.0f, true); return __builtin_bit_cast(unsigned, r); }
; DI f32x16 mfma8(v8i a, v8i b, f32x16 c) { return __builtin_amdgcn_mfma_scale_f32_32x32x64_f8f6f4(a, b, c, 0, 0, 0, 0, 0, 0); }
; DI void attn_unit_a8(unsigned char* lds, const AttnArgs& a) {
;     ...
;     auto expsum = [&](f32x16& sc) __attribute__((always_inline)) {
; #pragma unroll
;         for (int i = 0; i < 16; ++i) sc[i] = __builtin_amdgcn_exp2f(sc[i]);
; #pragma unroll
;         for (int i = 0; i < 4; ++i) l0 += (f32x4){sc[4 * i], sc[4 * i + 1], sc[4 * i + 2], sc[4 * i + 3]};
;     };
;     auto pack8 = [&](const f32x16& s0, const f32x16& s1) __attribute__((always_inline)) -> v8i { v8i p;
; #pragma unroll
;         for (int g = 0; g < 4; ++g) { p[g] = (int)pk4_fp8_div16(s0[4 * g], s0[4 * g + 1], s0[4 * g + 2], s0[4 * g + 3]); p[4 + g] = (int)pk4_fp8_div16(s1[4 * g], s1[4 * g + 1], s1[4 * g + 2], s1[4 * g + 3]); }
;         return p; };
;     ...
;     auto step = [&](int t, u32x2& kl, u32x2& vl, const u32x2& ks, const u32x2& vs, f32x16& c0, f32x16& c1, f32x16& n0, f32x16& n1, const int hk, const int wj) __attribute__((always_inline)) {
;         const int slot1 = slot == 2 ? 0 : slot + 1, slot2 = slot1 == 2 ? 0 : slot1 + 1;
;         if (hk == 1) { w_cvt(); w_issue(wj + 1 < AT_NWT ? wj + 1 : AT_NWT - 1); }
;         if (hk == 2) w_store(wj);
;         { const int tn = t + 3; gload(tn < a.t1 ? tn : a.t1 - 1, kl, vl); }
;         const unsigned char* Kb = lds + slot * AT_BUFB; const unsigned char* Kn = lds + slot1 * AT_BUFB;
;         const v8i k0 = kread(Kn, 0), k1 = kread(Kn, 1), v0 = vread(Kb, 0), v1 = vread(Kb, 1);
;         n0 = mfma8(k0, qf8, cinit); n1 = mfma8(k1, qf8, cinit);
;         expsum(c0); expsum(c1);
;         const v8i P = pack8(c0, c1);
;         o0[0] = mfma8(v0, P, o0[0]); o0[1] = mfma8(v1, P, o0[1]);
;         lstore(slot2, ks, vs);
;         __syncthreads();
;         slot = slot1;
;     };
	s_cbranch_scc1 .LBB0_716
	s_min_u32 s4, s56, 63
	s_cmp_lt_u32 s56, 60
	s_cselect_b64 s[10:11], -1, 0
	s_lshl_b32 s4, s4, 6
	s_add_i32 s9, s4, 0x100
	s_add_i32 s14, s4, 0xfffff100
	s_and_b64 s[12:13], s[10:11], exec
	s_cselect_b32 s9, s9, s14
	s_add_i32 s8, s8, 1
	s_and_b64 s[6:7], s[6:7], exec
	v_add_u32_e32 v82, s9, v154
	s_cselect_b32 s8, 0, s8
	s_and_b64 s[10:11], s[10:11], exec
	v_ashrrev_i32_e32 v83, 31, v82
	s_cselect_b32 s11, s59, s61
	s_cselect_b32 s10, s58, s60
	v_lshlrev_b64 v[82:83], 7, v[82:83]
	s_mul_i32 s6, s8, 0x4680
	v_lshl_add_u64 v[90:91], s[10:11], 0, v[82:83]
	v_add_u32_e32 v86, s6, v157
	v_lshl_add_u64 v[90:91], v[90:91], 0, v[130:131]
	ds_read_b128 v[66:69], v86
	ds_read_b128 v[70:73], v86 offset:16
	ds_read_b128 v[82:85], v86 offset:2560
	ds_read_b128 v[86:89], v86 offset:2576
	global_load_dwordx2 v[134:135], v[90:91], off
	v_lshl_add_u64 v[90:91], v[132:133], 0, s[4:5]
	global_load_dwordx2 v[136:137], v[90:91], off offset:256
	v_exp_f32_e32 v50, v50
	v_exp_f32_e32 v51, v51
	v_exp_f32_e32 v54, v54
	v_exp_f32_e32 v55, v55
	v_exp_f32_e32 v58, v58
	v_exp_f32_e32 v59, v59
	v_exp_f32_e32 v62, v62
	v_exp_f32_e32 v63, v63
	v_exp_f32_e32 v124, v34
	v_exp_f32_e32 v125, v35
	v_exp_f32_e32 v146, v38
	v_exp_f32_e32 v147, v39
	v_exp_f32_e32 v42, v42
	v_exp_f32_e32 v43, v43
	v_exp_f32_e32 v46, v46
	v_exp_f32_e32 v47, v47
	ds_read_b128 v[116:119], v106 offset:5120
	ds_read_b128 v[120:123], v106 offset:5136
	ds_read_b128 v[138:141], v106 offset:7680
	ds_read_b128 v[142:145], v106 offset:7696
	v_exp_f32_e32 v52, v52
	v_exp_f32_e32 v53, v53
	v_exp_f32_e32 v56, v56
	v_exp_f32_e32 v57, v57
	v_exp_f32_e32 v60, v60
	v_exp_f32_e32 v61, v61
	v_exp_f32_e32 v64, v64
	v_exp_f32_e32 v65, v65
	v_exp_f32_e32 v126, v36
	v_exp_f32_e32 v127, v37
	v_exp_f32_e32 v148, v40
	v_exp_f32_e32 v149, v41
	v_exp_f32_e32 v44, v44
	v_exp_f32_e32 v45, v45
	v_exp_f32_e32 v48, v48
	v_exp_f32_e32 v49, v49
	s_nop 0
	s_nop 0
	s_nop 0
	s_nop 0
	s_nop 0
	s_nop 0
	s_nop 0
	s_nop 0
	s_waitcnt lgkmcnt(6)
	v_mfma_f32_32x32x64_f8f6f4 v[66:81], v[66:73], v[98:105], 0
	v_cvt_scalef32_pk_fp8_f32 v34, v50, v51, s48
	v_cvt_scalef32_pk_fp8_f32 v38, v124, v125, s48
	v_cvt_scalef32_pk_fp8_f32 v35, v54, v55, s48
	v_cvt_scalef32_pk_fp8_f32 v39, v146, v147, s48
	v_cvt_scalef32_pk_fp8_f32 v36, v58, v59, s48
	v_cvt_scalef32_pk_fp8_f32 v40, v42, v43, s48
	v_cvt_scalef32_pk_fp8_f32 v37, v62, v63, s48
	v_cvt_scalef32_pk_fp8_f32 v41, v46, v47, s48
	v_cvt_scalef32_pk_fp8_f32 v34, v52, v53, s48 op_sel:[0,0,0,1]
	v_cvt_scalef32_pk_fp8_f32 v38, v126, v127, s48 op_sel:[0,0,0,1]
	v_cvt_scalef32_pk_fp8_f32 v35, v56, v57, s48 op_sel:[0,0,0,1]
	v_cvt_scalef32_pk_fp8_f32 v39, v148, v149, s48 op_sel:[0,0,0,1]
	v_cvt_scalef32_pk_fp8_f32 v36, v60, v61, s48 op_sel:[0,0,0,1]
	v_cvt_scalef32_pk_fp8_f32 v40, v44, v45, s48 op_sel:[0,0,0,1]
	v_cvt_scalef32_pk_fp8_f32 v37, v64, v65, s48 op_sel:[0,0,0,1]
	s_waitcnt lgkmcnt(4)
	v_mfma_f32_32x32x64_f8f6f4 v[82:97], v[82:89], v[98:105], 0
	v_cvt_scalef32_pk_fp8_f32 v41, v48, v49, s48 op_sel:[0,0,0,1]
	v_add_f32_e64 v110, v110, v52
	v_add_f32_e64 v111, v111, v53
	v_add_f32_e64 v50, v108, v50
	v_add_f32_e64 v51, v109, v51
	s_addk_i32 s6, 0x4680
	v_add_f32_e64 v52, v56, v110
	v_add_f32_e64 v53, v57, v111
	v_add_f32_e64 v50, v54, v50
	v_add_f32_e64 v51, v55, v51
	s_cmp_lg_u32 s8, 2
	v_add_f32_e64 v50, v58, v50
	v_add_f32_e64 v51, v59, v51
	v_pk_add_f32 v[52:53], v[60:61], v[52:53]
	s_cselect_b32 s4, s6, 0
	v_pk_add_f32 v[52:53], v[64:65], v[52:53]
	v_pk_add_f32 v[50:51], v[62:63], v[50:51]
	s_add_i32 s4, s4, 0
	v_pk_add_f32 v[50:51], v[124:125], v[50:51]
	v_pk_add_f32 v[52:53], v[126:127], v[52:53]
	s_waitcnt lgkmcnt(2)
	v_mfma_f32_32x32x64_f8f6f4 v[18:33], v[116:123], v[34:41], v[18:33]
	v_add_f32_e64 v52, v148, v52
	v_add_f32_e64 v53, v149, v53
	v_add_f32_e64 v50, v146, v50
	v_add_f32_e64 v51, v147, v51
	v_add_f32_e64 v44, v44, v52
	v_add_f32_e64 v45, v45, v53
	v_add_f32_e64 v42, v42, v50
	v_add_f32_e64 v43, v43, v51
	v_add_f32_e64 v110, v48, v44
	v_add_f32_e64 v111, v49, v45
	v_add_f32_e64 v108, v46, v42
	v_add_f32_e64 v109, v47, v43
	v_mov_b64_e32 v[50:51], v[66:67]
	v_mov_b64_e32 v[52:53], v[68:69]
	v_mov_b64_e32 v[54:55], v[70:71]
	v_mov_b64_e32 v[56:57], v[72:73]
	v_mov_b64_e32 v[58:59], v[74:75]
	v_mov_b64_e32 v[60:61], v[76:77]
	v_mov_b64_e32 v[62:63], v[78:79]
	v_mov_b64_e32 v[64:65], v[80:81]
	s_waitcnt lgkmcnt(0)
	v_mfma_f32_32x32x64_f8f6f4 v[2:17], v[138:145], v[34:41], v[2:17]
	v_add_u32_e32 v34, s4, v155
	s_waitcnt vmcnt(3)
	ds_write_b64 v34, v[112:113]
	v_add_u32_e32 v34, s4, v156
	v_add_u32_e32 v34, 0x1400, v34
	s_waitcnt vmcnt(2)
	ds_write2_b32 v34, v114, v115 offset1:8
	v_mov_b64_e32 v[34:35], v[82:83]
	v_mov_b64_e32 v[36:37], v[84:85]
	v_mov_b64_e32 v[38:39], v[86:87]
	v_mov_b64_e32 v[40:41], v[88:89]
	v_mov_b64_e32 v[42:43], v[90:91]
	v_mov_b64_e32 v[44:45], v[92:93]
	v_mov_b64_e32 v[46:47], v[94:95]
	v_mov_b64_e32 v[48:49], v[96:97]
	s_waitcnt lgkmcnt(0)
	s_barrier

; DI unsigned pk4_fp8(float a, float b, float c, float d) { int r = 0; r = __builtin_amdgcn_cvt_pk_fp8_f32(a, b, r, false); r = __builtin_amdgcn_cvt_pk_fp8_f32(c, d, r, true); return (unsigned)r; }
; DI float clamp448(float x) { return __builtin_amdgcn_fmed3f(x, -448.0f, 448.0f); }
;     DI void operator()(EPI_ARGS) const {
;     ...
;         unsigned char* CAT = WSB(unsigned char, WS_CAT);
;         const int rbase = u.e + wr * 64 + fr;
; #pragma unroll
;         for (int ai = 0; ai < 2; ++ai)
; #pragma unroll
;             for (int m = 0; m < 4; ++m) {
;                 const int row = rbase + 128 * ai + 16 * m;
; #pragma unroll
;                 for (int bj = 0; bj < 2; ++bj) { const f32x4 x0 = acc[ai][bj][m][0] * FOUR_SCALE, x1 = acc[ai][bj][m][1] * FOUR_SCALE; u32x2 w;
;                     w.x = pk4_fp8(clamp448(x0[0]), clamp448(x0[1]), clamp448(x0[2]), clamp448(x0[3])); w.y = pk4_fp8(clamp448(x1[0]), clamp448(x1[1]), clamp448(x1[2]), clamp448(x1[3]));
;                     *(u32x2*)(CAT + (size_t)row * 1024 + 512 + 128 * bj + 32 * wc + 8 * fq) = w; }
;             }
.LBB0_728:
	v_pk_add_f32 v[126:127], v[126:127], v[126:127]
	v_pk_add_f32 v[122:123], v[122:123], v[122:123]
	v_med3_f32 v149, v126, s70, v148
	v_med3_f32 v127, v127, s70, v148
	v_mov_b32_e32 v126, 0
	v_cvt_pk_fp8_f32 v126, v149, v127
	v_med3_f32 v122, v122, s70, v148
	v_med3_f32 v123, v123, s70, v148
	s_nop 0
	v_cvt_pk_fp8_f32 v127, v122, v123
	v_pk_add_f32 v[124:125], v[124:125], v[124:125]
	v_pk_add_f32 v[118:119], v[118:119], v[118:119]
	v_med3_f32 v122, v124, s70, v148
	v_med3_f32 v123, v125, s70, v148
	v_cvt_pk_fp8_f32 v127, v122, v123 op_sel:[0,0,1]
	v_pk_add_f32 v[114:115], v[114:115], v[114:115]
	v_med3_f32 v122, v118, s70, v148
	v_med3_f32 v119, v119, s70, v148
	v_mov_b32_e32 v118, 0
	v_pk_add_f32 v[116:117], v[116:117], v[116:117]
	v_cvt_pk_fp8_f32 v118, v122, v119
	v_med3_f32 v114, v114, s70, v148
	v_med3_f32 v115, v115, s70, v148
	s_nop 0
	v_pk_add_f32 v[110:111], v[110:111], v[110:111]
	v_cvt_pk_fp8_f32 v119, v114, v115
	v_med3_f32 v114, v116, s70, v148
	v_pk_add_f32 v[106:107], v[106:107], v[106:107]
	v_med3_f32 v116, v110, s70, v148
	v_med3_f32 v111, v111, s70, v148
	v_mov_b32_e32 v110, 0
	v_cvt_pk_fp8_f32 v110, v116, v111
	v_med3_f32 v106, v106, s70, v148
	v_med3_f32 v107, v107, s70, v148
	s_nop 0
	v_cvt_pk_fp8_f32 v111, v106, v107
	v_pk_add_f32 v[108:109], v[108:109], v[108:109]
	v_pk_add_f32 v[102:103], v[102:103], v[102:103]
	v_med3_f32 v106, v108, s70, v148
	v_med3_f32 v107, v109, s70, v148
	v_cvt_pk_fp8_f32 v111, v106, v107 op_sel:[0,0,1]
	v_pk_add_f32 v[98:99], v[98:99], v[98:99]
	v_med3_f32 v106, v102, s70, v148
	v_med3_f32 v103, v103, s70, v148
	v_mov_b32_e32 v102, 0
	v_pk_add_f32 v[100:101], v[100:101], v[100:101]
	v_cvt_pk_fp8_f32 v102, v106, v103
	v_med3_f32 v98, v98, s70, v148
	v_med3_f32 v99, v99, s70, v148
	s_nop 0
	v_pk_add_f32 v[94:95], v[94:95], v[94:95]
	v_cvt_pk_fp8_f32 v103, v98, v99
	v_med3_f32 v98, v100, s70, v148
	v_pk_add_f32 v[90:91], v[90:91], v[90:91]
	v_med3_f32 v100, v94, s70, v148
	v_med3_f32 v95, v95, s70, v148
	v_mov_b32_e32 v94, 0
	v_cvt_pk_fp8_f32 v94, v100, v95
	v_med3_f32 v90, v90, s70, v148
	v_med3_f32 v91, v91, s70, v148
	s_nop 0
	v_cvt_pk_fp8_f32 v95, v90, v91
	v_pk_add_f32 v[92:93], v[92:93], v[92:93]
	v_pk_add_f32 v[86:87], v[86:87], v[86:87]
	v_med3_f32 v90, v92, s70, v148
	v_med3_f32 v91, v93, s70, v148
	v_cvt_pk_fp8_f32 v95, v90, v91 op_sel:[0,0,1]
	v_pk_add_f32 v[82:83], v[82:83], v[82:83]
	v_med3_f32 v90, v86, s70, v148
	v_med3_f32 v87, v87, s70, v148
	v_mov_b32_e32 v86, 0
	v_pk_add_f32 v[84:85], v[84:85], v[84:85]
	v_cvt_pk_fp8_f32 v86, v90, v87
	v_med3_f32 v82, v82, s70, v148
	v_med3_f32 v83, v83, s70, v148
	s_nop 0
	v_pk_add_f32 v[78:79], v[78:79], v[78:79]
	v_cvt_pk_fp8_f32 v87, v82, v83
	v_med3_f32 v82, v84, s70, v148
	v_pk_add_f32 v[74:75], v[74:75], v[74:75]
	v_med3_f32 v84, v78, s70, v148
	v_med3_f32 v79, v79, s70, v148
	v_mov_b32_e32 v78, 0
	v_cvt_pk_fp8_f32 v78, v84, v79
	v_med3_f32 v74, v74, s70, v148
	v_med3_f32 v75, v75, s70, v148
	s_nop 0
	v_cvt_pk_fp8_f32 v79, v74, v75
	v_pk_add_f32 v[76:77], v[76:77], v[76:77]
	v_pk_add_f32 v[70:71], v[70:71], v[70:71]
	v_med3_f32 v74, v76, s70, v148
	v_med3_f32 v75, v77, s70, v148
	v_cvt_pk_fp8_f32 v79, v74, v75 op_sel:[0,0,1]
	v_pk_add_f32 v[66:67], v[66:67], v[66:67]
	v_med3_f32 v74, v70, s70, v148
	v_med3_f32 v71, v71, s70, v148
	v_mov_b32_e32 v70, 0
	v_pk_add_f32 v[68:69], v[68:69], v[68:69]
	v_cvt_pk_fp8_f32 v70, v74, v71
	v_med3_f32 v66, v66, s70, v148
	v_med3_f32 v67, v67, s70, v148
	s_nop 0
	v_pk_add_f32 v[62:63], v[62:63], v[62:63]
	v_cvt_pk_fp8_f32 v71, v66, v67
	v_med3_f32 v66, v68, s70, v148
	v_pk_add_f32 v[58:59], v[58:59], v[58:59]
	v_med3_f32 v68, v62, s70, v148
	v_med3_f32 v63, v63, s70, v148
	s_nop 0
	v_cvt_pk_fp8_f32 v62, v68, v63
	v_med3_f32 v58, v58, s70, v148
	v_med3_f32 v59, v59, s70, v148
	s_nop 0
	v_cvt_pk_fp8_f32 v63, v58, v59
	v_pk_add_f32 v[60:61], v[60:61], v[60:61]
	v_pk_add_f32 v[54:55], v[54:55], v[54:55]
	v_med3_f32 v58, v60, s70, v148
	v_med3_f32 v59, v61, s70, v148
	v_cvt_pk_fp8_f32 v63, v58, v59 op_sel:[0,0,1]
	v_pk_add_f32 v[50:51], v[50:51], v[50:51]
	v_med3_f32 v58, v54, s70, v148
	v_med3_f32 v55, v55, s70, v148
	s_nop 0
	v_pk_add_f32 v[52:53], v[52:53], v[52:53]
	v_cvt_pk_fp8_f32 v54, v58, v55
	v_med3_f32 v50, v50, s70, v148
	v_med3_f32 v51, v51, s70, v148
	s_nop 0
	v_pk_add_f32 v[46:47], v[46:47], v[46:47]
	v_cvt_pk_fp8_f32 v55, v50, v51
	v_med3_f32 v50, v52, s70, v148
	v_pk_add_f32 v[42:43], v[42:43], v[42:43]
	v_med3_f32 v52, v46, s70, v148
	v_med3_f32 v47, v47, s70, v148
	s_nop 0
	v_cvt_pk_fp8_f32 v46, v52, v47
	v_med3_f32 v42, v42, s70, v148
	v_med3_f32 v43, v43, s70, v148
	s_nop 0
	v_cvt_pk_fp8_f32 v47, v42, v43
	v_pk_add_f32 v[44:45], v[44:45], v[44:45]
	v_pk_add_f32 v[38:39], v[38:39], v[38:39]
	v_med3_f32 v42, v44, s70, v148
	v_med3_f32 v43, v45, s70, v148
	s_lshl_b32 s42, s81, 8
	v_mov_b32_e32 v143, v145
	v_mov_b32_e32 v142, v144
	v_cvt_pk_fp8_f32 v47, v42, v43 op_sel:[0,0,1]
	v_pk_add_f32 v[34:35], v[34:35], v[34:35]
	v_med3_f32 v42, v38, s70, v148
	v_med3_f32 v39, v39, s70, v148
	s_nop 0
	s_add_i32 s42, s67, s42
	v_pk_add_f32 v[36:37], v[36:37], v[36:37]
	v_cvt_pk_fp8_f32 v38, v42, v39
	v_med3_f32 v34, v34, s70, v148
	v_med3_f32 v35, v35, s70, v148
	s_nop 0
	v_pk_add_f32 v[30:31], v[30:31], v[30:31]
	v_add_u32_e32 v142, s42, v142
	v_cvt_pk_fp8_f32 v39, v34, v35
	v_med3_f32 v34, v36, s70, v148
	v_pk_add_f32 v[26:27], v[26:27], v[26:27]
	v_med3_f32 v36, v30, s70, v148
	v_med3_f32 v31, v31, s70, v148
	s_nop 0
	v_lshlrev_b32_e32 v150, 3, v143
	v_ashrrev_i32_e32 v143, 31, v142
	v_cvt_pk_fp8_f32 v30, v36, v31
	v_med3_f32 v26, v26, s70, v148
	v_med3_f32 v27, v27, s70, v148
	s_nop 0
; DI unsigned pk4_fp8(float a, float b, float c, float d) { int r = 0; r = __builtin_amdgcn_cvt_pk_fp8_f32(a, b, r, false); r = __builtin_amdgcn_cvt_pk_fp8_f32(c, d, r, true); return (unsigned)r; }
; DI float clamp448(float x) { return __builtin_amdgcn_fmed3f(x, -448.0f, 448.0f); }
;     DI void operator()(EPI_ARGS) const {
;     ...
;         unsigned char* CAT = WSB(unsigned char, WS_CAT);
;         const int rbase = u.e + wr * 64 + fr;
; #pragma unroll
;         for (int ai = 0; ai < 2; ++ai)
; #pragma unroll
;             for (int m = 0; m < 4; ++m) {
;                 const int row = rbase + 128 * ai + 16 * m;
; #pragma unroll
;                 for (int bj = 0; bj < 2; ++bj) { const f32x4 x0 = acc[ai][bj][m][0] * FOUR_SCALE, x1 = acc[ai][bj][m][1] * FOUR_SCALE; u32x2 w;
;                     w.x = pk4_fp8(clamp448(x0[0]), clamp448(x0[1]), clamp448(x0[2]), clamp448(x0[3])); w.y = pk4_fp8(clamp448(x1[0]), clamp448(x1[1]), clamp448(x1[2]), clamp448(x1[3]));
;                     *(u32x2*)(CAT + (size_t)row * 1024 + 512 + 128 * bj + 32 * wc + 8 * fq) = w; }
;             }
	v_lshlrev_b64 v[142:143], 10, v[142:143]
	v_cvt_pk_fp8_f32 v31, v26, v27
	v_lshl_add_u64 v[142:143], s[6:7], 0, v[142:143]
	v_ashrrev_i32_e32 v151, 31, v150
	v_lshl_add_u64 v[142:143], v[142:143], 0, s[4:5]
	v_pk_add_f32 v[28:29], v[28:29], v[28:29]
	v_lshl_add_u64 v[142:143], v[142:143], 0, v[150:151]
	v_med3_f32 v115, v117, s70, v148
	v_med3_f32 v26, v28, s70, v148
	v_med3_f32 v27, v29, s70, v148
	v_pk_add_f32 v[22:23], v[22:23], v[22:23]
	v_cvt_pk_fp8_f32 v119, v114, v115 op_sel:[0,0,1]
	v_add_co_u32_e32 v114, vcc, s71, v142
	v_cvt_pk_fp8_f32 v31, v26, v27 op_sel:[0,0,1]
	v_pk_add_f32 v[18:19], v[18:19], v[18:19]
	v_med3_f32 v26, v22, s70, v148
	v_med3_f32 v23, v23, s70, v148
	s_nop 0
	v_addc_co_u32_e32 v115, vcc, 0, v143, vcc
	v_med3_f32 v99, v101, s70, v148
	v_pk_add_f32 v[20:21], v[20:21], v[20:21]
	v_cvt_pk_fp8_f32 v22, v26, v23
	v_med3_f32 v18, v18, s70, v148
	v_med3_f32 v19, v19, s70, v148
	s_nop 0
	v_pk_add_f32 v[14:15], v[14:15], v[14:15]
	v_cvt_pk_fp8_f32 v103, v98, v99 op_sel:[0,0,1]
	v_add_co_u32_e32 v98, vcc, s72, v142
	v_cvt_pk_fp8_f32 v23, v18, v19
	v_med3_f32 v18, v20, s70, v148
	v_pk_add_f32 v[10:11], v[10:11], v[10:11]
	v_med3_f32 v20, v14, s70, v148
	v_med3_f32 v15, v15, s70, v148
	s_nop 0
	v_addc_co_u32_e32 v99, vcc, 0, v143, vcc
	v_med3_f32 v83, v85, s70, v148
	v_cvt_pk_fp8_f32 v14, v20, v15
	v_med3_f32 v10, v10, s70, v148
	v_med3_f32 v11, v11, s70, v148
	s_nop 0
	v_cvt_pk_fp8_f32 v87, v82, v83 op_sel:[0,0,1]
	v_add_co_u32_e32 v82, vcc, s73, v142
	v_cvt_pk_fp8_f32 v15, v10, v11
	s_nop 0
	v_addc_co_u32_e32 v83, vcc, 0, v143, vcc
	v_med3_f32 v67, v69, s70, v148
	v_cvt_pk_fp8_f32 v71, v66, v67 op_sel:[0,0,1]
	v_add_co_u32_e32 v66, vcc, s74, v142
	v_pk_add_f32 v[12:13], v[12:13], v[12:13]
	s_nop 0
	v_addc_co_u32_e32 v67, vcc, 0, v143, vcc
	v_med3_f32 v51, v53, s70, v148
	v_med3_f32 v10, v12, s70, v148
	v_med3_f32 v11, v13, s70, v148
	v_pk_add_f32 v[6:7], v[6:7], v[6:7]
	v_cvt_pk_fp8_f32 v55, v50, v51 op_sel:[0,0,1]
	v_add_co_u32_e32 v50, vcc, s75, v142
	v_cvt_pk_fp8_f32 v15, v10, v11 op_sel:[0,0,1]
	v_pk_add_f32 v[2:3], v[2:3], v[2:3]
	v_med3_f32 v10, v6, s70, v148
	v_med3_f32 v7, v7, s70, v148
	s_nop 0
	v_addc_co_u32_e32 v51, vcc, 0, v143, vcc
	v_med3_f32 v35, v37, s70, v148
	v_cvt_pk_fp8_f32 v6, v10, v7
	v_med3_f32 v2, v2, s70, v148
	v_med3_f32 v3, v3, s70, v148
	s_nop 0
	v_cvt_pk_fp8_f32 v39, v34, v35 op_sel:[0,0,1]
	v_add_co_u32_e32 v34, vcc, s76, v142
	v_cvt_pk_fp8_f32 v7, v2, v3
	v_pk_add_f32 v[128:129], v[128:129], v[128:129]
	v_pk_add_f32 v[112:113], v[112:113], v[112:113]
	v_pk_add_f32 v[96:97], v[96:97], v[96:97]
	v_pk_add_f32 v[80:81], v[80:81], v[80:81]
	v_pk_add_f32 v[64:65], v[64:65], v[64:65]
	v_pk_add_f32 v[48:49], v[48:49], v[48:49]
	v_addc_co_u32_e32 v35, vcc, 0, v143, vcc
	v_pk_add_f32 v[32:33], v[32:33], v[32:33]
	v_med3_f32 v19, v21, s70, v148
	v_pk_add_f32 v[16:17], v[16:17], v[16:17]
	v_med3_f32 v128, v128, s70, v148
	v_med3_f32 v129, v129, s70, v148
	v_pk_add_f32 v[120:121], v[120:121], v[120:121]
	v_med3_f32 v112, v112, s70, v148
	v_med3_f32 v113, v113, s70, v148
	v_pk_add_f32 v[104:105], v[104:105], v[104:105]
	v_med3_f32 v96, v96, s70, v148
	v_med3_f32 v97, v97, s70, v148
	v_pk_add_f32 v[88:89], v[88:89], v[88:89]
	v_med3_f32 v80, v80, s70, v148
	v_med3_f32 v81, v81, s70, v148
	v_pk_add_f32 v[72:73], v[72:73], v[72:73]
	v_med3_f32 v64, v64, s70, v148
	v_med3_f32 v65, v65, s70, v148
	v_pk_add_f32 v[56:57], v[56:57], v[56:57]
	v_med3_f32 v48, v48, s70, v148
	v_med3_f32 v49, v49, s70, v148
	v_pk_add_f32 v[40:41], v[40:41], v[40:41]
	v_med3_f32 v32, v32, s70, v148
	v_med3_f32 v33, v33, s70, v148
	v_pk_add_f32 v[24:25], v[24:25], v[24:25]
	v_cvt_pk_fp8_f32 v23, v18, v19 op_sel:[0,0,1]
	v_add_co_u32_e32 v18, vcc, s77, v142
	v_med3_f32 v16, v16, s70, v148
	v_med3_f32 v17, v17, s70, v148
	v_pk_add_f32 v[8:9], v[8:9], v[8:9]
	v_pk_add_f32 v[4:5], v[4:5], v[4:5]
	v_cvt_pk_fp8_f32 v126, v128, v129 op_sel:[0,0,1]
	v_med3_f32 v120, v120, s70, v148
	v_med3_f32 v121, v121, s70, v148
	v_cvt_pk_fp8_f32 v110, v112, v113 op_sel:[0,0,1]
	v_med3_f32 v104, v104, s70, v148
	v_med3_f32 v105, v105, s70, v148
	v_cvt_pk_fp8_f32 v94, v96, v97 op_sel:[0,0,1]
	v_med3_f32 v88, v88, s70, v148
	v_med3_f32 v89, v89, s70, v148
	v_cvt_pk_fp8_f32 v78, v80, v81 op_sel:[0,0,1]
	v_med3_f32 v72, v72, s70, v148
	v_med3_f32 v73, v73, s70, v148
	v_cvt_pk_fp8_f32 v62, v64, v65 op_sel:[0,0,1]
	v_med3_f32 v56, v56, s70, v148
	v_med3_f32 v57, v57, s70, v148
	v_cvt_pk_fp8_f32 v46, v48, v49 op_sel:[0,0,1]
	v_med3_f32 v40, v40, s70, v148
	v_med3_f32 v41, v41, s70, v148
	v_cvt_pk_fp8_f32 v30, v32, v33 op_sel:[0,0,1]
	v_med3_f32 v24, v24, s70, v148
	v_med3_f32 v25, v25, s70, v148
	v_addc_co_u32_e32 v19, vcc, 0, v143, vcc
	v_cvt_pk_fp8_f32 v14, v16, v17 op_sel:[0,0,1]
	v_med3_f32 v8, v8, s70, v148
	v_med3_f32 v9, v9, s70, v148
	v_med3_f32 v2, v4, s70, v148
	v_med3_f32 v3, v5, s70, v148
	v_cvt_pk_fp8_f32 v118, v120, v121 op_sel:[0,0,1]
	v_cvt_pk_fp8_f32 v102, v104, v105 op_sel:[0,0,1]
	v_cvt_pk_fp8_f32 v86, v88, v89 op_sel:[0,0,1]
	v_cvt_pk_fp8_f32 v70, v72, v73 op_sel:[0,0,1]
	v_cvt_pk_fp8_f32 v54, v56, v57 op_sel:[0,0,1]
	v_cvt_pk_fp8_f32 v38, v40, v41 op_sel:[0,0,1]
	v_cvt_pk_fp8_f32 v22, v24, v25 op_sel:[0,0,1]
	v_cvt_pk_fp8_f32 v6, v8, v9 op_sel:[0,0,1]
	v_cvt_pk_fp8_f32 v7, v2, v3 op_sel:[0,0,1]
	v_add_co_u32_e32 v2, vcc, s78, v142
	v_lshl_add_u64 v[150:151], v[142:143], 0, s[12:13]
	s_nop 0
	v_addc_co_u32_e32 v3, vcc, 0, v143, vcc
	s_andn2_b64 vcc, exec, s[40:41]
	s_mov_b64 s[40:41], -1
	global_store_dwordx2 v[114:115], v[126:127], off offset:512
	global_store_dwordx2 v[150:151], v[118:119], off offset:128
	v_lshl_add_u64 v[114:115], v[142:143], 0, s[14:15]
	global_store_dwordx2 v[98:99], v[110:111], off offset:512
	global_store_dwordx2 v[114:115], v[102:103], off offset:128
	v_lshl_add_u64 v[98:99], v[142:143], 0, s[16:17]
	global_store_dwordx2 v[82:83], v[94:95], off offset:512
	global_store_dwordx2 v[98:99], v[86:87], off offset:128
	v_lshl_add_u64 v[82:83], v[142:143], 0, s[18:19]
	global_store_dwordx2 v[66:67], v[78:79], off offset:512
	global_store_dwordx2 v[82:83], v[70:71], off offset:128
	v_lshl_add_u64 v[66:67], v[142:143], 0, s[22:23]
	global_store_dwordx2 v[50:51], v[62:63], off offset:512
	global_store_dwordx2 v[66:67], v[54:55], off offset:128
	v_lshl_add_u64 v[50:51], v[142:143], 0, s[24:25]
	global_store_dwordx2 v[34:35], v[46:47], off offset:512
	global_store_dwordx2 v[50:51], v[38:39], off offset:128
	v_lshl_add_u64 v[34:35], v[142:143], 0, s[36:37]
	global_store_dwordx2 v[18:19], v[30:31], off offset:512
	global_store_dwordx2 v[34:35], v[22:23], off offset:128
	v_lshl_add_u64 v[18:19], v[142:143], 0, s[38:39]
	global_store_dwordx2 v[2:3], v[14:15], off offset:512
	global_store_dwordx2 v[18:19], v[6:7], off offset:128
	s_cbranch_vccnz .LBB0_723
	s_andn2_b64 vcc, exec, s[8:9]
	s_cbranch_vccnz .LBB0_722
	s_barrier
	s_branch .LBB0_722

; DI unsigned pk4_fp8(float a, float b, float c, float d) { int r = 0; r = __builtin_amdgcn_cvt_pk_fp8_f32(a, b, r, false); r = __builtin_amdgcn_cvt_pk_fp8_f32(c, d, r, true); return (unsigned)r; }
; DI float clamp448(float x) { return __builtin_amdgcn_fmed3f(x, -448.0f, 448.0f); }
; DI float sigmoidf_(float x) { return 1.0f / (1.0f + __expf(-x)); }
; DI void conv_unit(unsigned char* lds, int seqrow, int L, int t0, const bf16_t* BU, const bf16_t* BG, const float* cw, const float* cb, const float* lg, const float* lb, unsigned char* CAT) {
;     ...
;     const int lane = tid & 63, wv = tid >> 6;
;     const f32x4 g4 = *(const f32x4*)(lg + 4 * lane), b4 = *(const f32x4*)(lb + 4 * lane);
;     for (int tt = wv; tt < 64; tt += 8) {
;         const f32x4 v = *(const f32x4*)(z + tt * 256 + 4 * lane);
;         const float mean = wave_sum(v[0] + v[1] + v[2] + v[3]) * (1.0f / 256.0f);
;         const f32x4 d = v - mean;
;         const float var = wave_sum(d[0] * d[0] + d[1] * d[1] + d[2] * d[2] + d[3] * d[3]) * (1.0f / 256.0f);
;         const f32x4 y = d * rsqrtf(var + EPS) * g4 + b4;
;         f32x4 o;
; #pragma unroll
;         for (int e = 0; e < 4; ++e) o[e] = y[e] * sigmoidf_(y[e]);
;         *(unsigned*)(CAT + (size_t)(seqrow + t0 + tt) * 1024 + 256 + 4 * lane) = pk4_fp8(clamp448(o[0] * CAT_SCALE), clamp448(o[1] * CAT_SCALE), clamp448(o[2] * CAT_SCALE), clamp448(o[3] * CAT_SCALE));
;     }
.LBB0_845:
	ds_read_b128 v[12:15], v11
	v_add_u32_e32 v18, 8, v10
	v_add_u32_e32 v16, s70, v10
	v_cmp_lt_i32_e32 vcc, 55, v10
	v_mov_b32_e32 v10, v18
	s_waitcnt lgkmcnt(0)
	v_add_f32_e32 v18, v12, v13
	v_add_f32_e32 v18, v14, v18
	v_add_f32_e32 v18, v15, v18
	ds_bpermute_b32 v19, v1, v18
	s_or_b64 s[12:13], vcc, s[12:13]
	v_ashrrev_i32_e32 v17, 31, v16
	v_lshlrev_b64 v[16:17], 10, v[16:17]
	v_lshl_add_u64 v[16:17], s[54:55], 0, v[16:17]
	s_waitcnt lgkmcnt(0)
	v_add_f32_e32 v18, v18, v19
	ds_bpermute_b32 v19, v206, v18
	s_nop 0
	v_lshl_add_u64 v[16:17], v[16:17], 0, v[58:59]
	v_add_u32_e32 v11, 0x2000, v11
	s_waitcnt lgkmcnt(0)
	v_add_f32_e32 v18, v18, v19
	ds_bpermute_b32 v19, v207, v18
	s_waitcnt lgkmcnt(0)
	v_add_f32_e32 v18, v18, v19
	ds_bpermute_b32 v19, v208, v18
	s_waitcnt lgkmcnt(0)
	v_add_f32_e32 v18, v18, v19
	ds_bpermute_b32 v19, v209, v18
	s_waitcnt lgkmcnt(0)
	v_add_f32_e32 v18, v18, v19
	ds_bpermute_b32 v19, v210, v18
	s_waitcnt lgkmcnt(0)
	v_add_f32_e32 v18, v18, v19
	v_fmamk_f32 v13, v18, 0xbb800000, v13
	v_fmamk_f32 v12, v18, 0xbb800000, v12
	v_fmamk_f32 v15, v18, 0xbb800000, v15
	v_fmac_f32_e32 v14, 0xbb800000, v18
	v_pk_mul_f32 v[20:21], v[12:13], v[12:13]
	v_pk_mul_f32 v[18:19], v[14:15], v[14:15]
	v_add_f32_e32 v20, v20, v21
	v_add_f32_e32 v18, v18, v20
	v_add_f32_e32 v18, v19, v18
	ds_bpermute_b32 v19, v1, v18
	s_waitcnt lgkmcnt(0)
	v_add_f32_e32 v18, v18, v19
	ds_bpermute_b32 v19, v206, v18
	s_waitcnt lgkmcnt(0)
	v_add_f32_e32 v18, v18, v19
	ds_bpermute_b32 v19, v207, v18
	s_waitcnt lgkmcnt(0)
	v_add_f32_e32 v18, v18, v19
	ds_bpermute_b32 v19, v208, v18
	s_waitcnt lgkmcnt(0)
	v_add_f32_e32 v18, v18, v19
	ds_bpermute_b32 v19, v209, v18
	s_waitcnt lgkmcnt(0)
	v_add_f32_e32 v18, v18, v19
	ds_bpermute_b32 v19, v210, v18
	s_waitcnt lgkmcnt(0)
	v_add_f32_e32 v18, v18, v19
	v_fmamk_f32 v18, v18, 0x3b800000, v62
	v_mul_f32_e32 v19, 0x4b800000, v18
	v_cmp_gt_f32_e32 vcc, s68, v18
	s_nop 1
	v_cndmask_b32_e32 v18, v18, v19, vcc
	v_rsq_f32_e32 v18, v18
	s_nop 0
	v_mul_f32_e32 v19, 0x45800000, v18
	v_cndmask_b32_e32 v18, v18, v19, vcc
	v_pk_mul_f32 v[12:13], v[12:13], v[18:19] op_sel_hi:[1,0]
	v_pk_mul_f32 v[14:15], v[14:15], v[18:19] op_sel_hi:[1,0]
	v_fma_f32 v12, v6, v12, v2
	v_fma_f32 v13, v7, v13, v3
	v_mul_f32_e32 v18, 0xbfb8aa3b, v12
	v_mul_f32_e32 v19, 0xbfb8aa3b, v13
	v_exp_f32_e32 v18, v18
	v_fma_f32 v14, v8, v14, v4
	v_exp_f32_e32 v19, v19
	v_mul_f32_e32 v20, 0xbfb8aa3b, v14
	v_fma_f32 v15, v9, v15, v5
	v_exp_f32_e32 v20, v20
	v_mul_f32_e32 v21, 0xbfb8aa3b, v15
	v_add_f32_e32 v18, 1.0, v18
	v_exp_f32_e32 v21, v21
	v_add_f32_e32 v19, 1.0, v19
	v_div_scale_f32 v23, s[4:5], v18, v18, 1.0
	v_div_scale_f32 v25, s[4:5], v19, v19, 1.0
	v_rcp_f32_e32 v31, v23
	v_add_f32_e32 v20, 1.0, v20
	v_rcp_f32_e32 v32, v25
	v_div_scale_f32 v27, s[6:7], v20, v20, 1.0
	v_add_f32_e32 v21, 1.0, v21
	v_rcp_f32_e32 v33, v27
	v_div_scale_f32 v29, s[8:9], v21, v21, 1.0
	v_fma_f32 v35, -v23, v31, 1.0
	v_div_scale_f32 v24, vcc, 1.0, v18, 1.0
	v_rcp_f32_e32 v34, v29
	v_fma_f32 v36, -v25, v32, 1.0
	v_fmac_f32_e32 v31, v35, v31
	v_div_scale_f32 v26, s[4:5], 1.0, v19, 1.0
	v_fmac_f32_e32 v32, v36, v32
	v_mul_f32_e32 v35, v24, v31
	v_fma_f32 v37, -v27, v33, 1.0
	v_mul_f32_e32 v36, v26, v32
	v_fma_f32 v39, -v23, v35, v24
	v_div_scale_f32 v28, s[6:7], 1.0, v20, 1.0
	v_fmac_f32_e32 v33, v37, v33
	v_fma_f32 v40, -v25, v36, v26
	v_fmac_f32_e32 v35, v39, v31
	v_fma_f32 v38, -v29, v34, 1.0
	v_mul_f32_e32 v37, v28, v33
	v_fmac_f32_e32 v36, v40, v32
	v_fma_f32 v23, -v23, v35, v24
	v_div_scale_f32 v30, s[8:9], 1.0, v21, 1.0
	v_fmac_f32_e32 v34, v38, v34
	v_fma_f32 v41, -v27, v37, v28
	v_fma_f32 v24, -v25, v36, v26
	v_div_fmas_f32 v23, v23, v31, v35
	s_mov_b64 vcc, s[4:5]
	v_mul_f32_e32 v38, v30, v34
	v_fmac_f32_e32 v37, v41, v33
	v_div_fixup_f32 v18, v23, v18, 1.0
	v_div_fmas_f32 v23, v24, v32, v36
	v_fma_f32 v42, -v29, v38, v30
	v_fma_f32 v25, -v27, v37, v28
	v_mul_f32_e32 v12, v12, v18
	v_div_fixup_f32 v18, v23, v19, 1.0
	s_mov_b64 vcc, s[6:7]
	v_fmac_f32_e32 v38, v42, v34
	v_div_fmas_f32 v19, v25, v33, v37
	v_mul_f32_e32 v13, v13, v18
	v_fma_f32 v26, -v29, v38, v30
	v_div_fixup_f32 v18, v19, v20, 1.0
	s_mov_b64 vcc, s[8:9]
	v_mul_f32_e32 v20, 0x41800000, v12
	v_mul_f32_e32 v13, 0x41800000, v13
	v_div_fmas_f32 v19, v26, v34, v38
	v_mul_f32_e32 v14, v14, v18
	v_med3_f32 v18, v20, s69, v63
	v_med3_f32 v13, v13, s69, v63
	v_add_co_u32_e32 v12, vcc, 0x2add4000, v16
	v_div_fixup_f32 v16, v19, v21, 1.0
	v_cvt_pk_fp8_f32 v22, v18, v13
	v_mul_f32_e32 v15, v15, v16
	v_mul_f32_e32 v14, 0x41800000, v14
	v_med3_f32 v13, v14, s69, v63
	v_mul_f32_e32 v14, 0x41800000, v15
	v_med3_f32 v14, v14, s69, v63
	v_cvt_pk_fp8_f32 v22, v13, v14 op_sel:[0,0,1]
	v_addc_co_u32_e32 v13, vcc, 0, v17, vcc
	global_store_dword v[12:13], v22, off offset:256
	s_andn2_b64 exec, exec, s[12:13]
	s_cbranch_execnz .LBB0_845
	s_branch .LBB0_734

; DI unsigned pk4_fp8(float a, float b, float c, float d) { int r = 0; r = __builtin_amdgcn_cvt_pk_fp8_f32(a, b, r, false); r = __builtin_amdgcn_cvt_pk_fp8_f32(c, d, r, true); return (unsigned)r; }
; DI float clamp448(float x) { return __builtin_amdgcn_fmed3f(x, -448.0f, 448.0f); }
; DI float bflo(unsigned u) { return __uint_as_float(u << 16); }
; DI float bfhi(unsigned u) { return __uint_as_float(u & 0xffff0000u); }
; DI void phase_router(unsigned char* lds, const Params& P, int li, const bf16_t* X1, unsigned char* H8, const float* modl, unsigned* cnt, int* tok_e, int* tok_pos, float* tok_gate, int* tok_list, int G, int ntok, int chsz) {
;     ...
;                 if (tl < chsz) {
;                     const u32x4 a = ra[rr], b = rbv[rr];
;                     v[0] = (f32x4){bflo(a[0]), bfhi(a[0]), bflo(a[1]), bfhi(a[1])}; v[1] = (f32x4){bflo(a[2]), bfhi(a[2]), bflo(a[3]), bfhi(a[3])};
;                     v[2] = (f32x4){bflo(b[0]), bfhi(b[0]), bflo(b[1]), bfhi(b[1])}; v[3] = (f32x4){bflo(b[2]), bfhi(b[2]), bflo(b[3]), bfhi(b[3])};
;                     const int b9 = tok < NLAT ? (tok >> 12) : 8; if (b9 != cur_b9) load_mod(b9);
;                     float ss = 0.f;
; #pragma unroll
;                     for (int j = 0; j < 4; ++j)
; #pragma unroll
;                         for (int i = 0; i < 4; ++i) ss += v[j][i] * v[j][i];
;                     ss = wave_sum(ss);
;                     const float rinv = __builtin_amdgcn_rsqf(ss * (1.0f / 1024.0f) + EPS);
; #pragma unroll
;                     for (int j = 0; j < 4; ++j) v[j] = v[j] * rinv * ma[j] + mb[j];
;                     { unsigned char* hr = H8 + (size_t)tok * 1024; u32x2 w0, w1;
;                       w0.x = pk4_fp8(clamp448(v[0][0]), clamp448(v[0][1]), clamp448(v[0][2]), clamp448(v[0][3])); w0.y = pk4_fp8(clamp448(v[1][0]), clamp448(v[1][1]), clamp448(v[1][2]), clamp448(v[1][3]));
;                       w1.x = pk4_fp8(clamp448(v[2][0]), clamp448(v[2][1]), clamp448(v[2][2]), clamp448(v[2][3])); w1.y = pk4_fp8(clamp448(v[3][0]), clamp448(v[3][1]), clamp448(v[3][2]), clamp448(v[3][3]));
;                       *(u32x2*)(hr + 8 * lane) = w0; *(u32x2*)(hr + 512 + 8 * lane) = w1; } }
.LBB0_982:
	s_or_b64 exec, exec, s[38:39]
	s_waitcnt vmcnt(1)
	v_and_b32_e32 v107, 0xffff0000, v102
	v_lshlrev_b32_e32 v106, 16, v102
	v_mul_f32_e32 v112, v107, v107
	v_lshlrev_b32_e32 v102, 16, v103
	v_fmac_f32_e32 v112, v106, v106
	v_and_b32_e32 v103, 0xffff0000, v103
	v_fmac_f32_e32 v112, v102, v102
	v_lshlrev_b32_e32 v110, 16, v104
	v_fmac_f32_e32 v112, v103, v103
	v_and_b32_e32 v111, 0xffff0000, v104
	v_fmac_f32_e32 v112, v110, v110
	v_lshlrev_b32_e32 v104, 16, v105
	v_fmac_f32_e32 v112, v111, v111
	v_and_b32_e32 v105, 0xffff0000, v105
	v_fmac_f32_e32 v112, v104, v104
	s_waitcnt vmcnt(0)
	v_lshlrev_b32_e32 v114, 16, v98
	v_fmac_f32_e32 v112, v105, v105
	v_and_b32_e32 v115, 0xffff0000, v98
	v_fmac_f32_e32 v112, v114, v114
	v_lshlrev_b32_e32 v98, 16, v99
	v_fmac_f32_e32 v112, v115, v115
	v_and_b32_e32 v99, 0xffff0000, v99
	v_fmac_f32_e32 v112, v98, v98
	v_lshlrev_b32_e32 v118, 16, v100
	v_fmac_f32_e32 v112, v99, v99
	v_and_b32_e32 v119, 0xffff0000, v100
	v_and_b32_e32 v100, 0xffff0000, v101
	v_lshlrev_b32_e32 v101, 16, v101
	v_fmac_f32_e32 v112, v118, v118
	v_fmac_f32_e32 v112, v119, v119
	v_pk_mul_f32 v[108:109], v[100:101], v[100:101]
	v_ashrrev_i32_e32 v123, 31, v122
	v_add_f32_e32 v109, v109, v112
	v_add_f32_e32 v108, v108, v109
	v_and_b32_e32 v109, 64, v169
	v_add_u32_e32 v109, 64, v109
	v_xor_b32_e32 v112, 32, v169
	v_cmp_lt_i32_e32 vcc, v112, v109
	s_nop 1
	v_cndmask_b32_e32 v112, v169, v112, vcc
	v_lshlrev_b32_e32 v112, 2, v112
	ds_bpermute_b32 v112, v112, v108
	s_waitcnt lgkmcnt(0)
	v_add_f32_e32 v108, v108, v112
	v_xor_b32_e32 v112, 16, v169
	v_cmp_lt_i32_e32 vcc, v112, v109
	s_nop 1
	v_cndmask_b32_e32 v112, v169, v112, vcc
	v_lshlrev_b32_e32 v112, 2, v112
	ds_bpermute_b32 v112, v112, v108
	s_waitcnt lgkmcnt(0)
	v_add_f32_e32 v108, v108, v112
	v_xor_b32_e32 v112, 8, v169
	v_cmp_lt_i32_e32 vcc, v112, v109
	s_nop 1
	v_cndmask_b32_e32 v112, v169, v112, vcc
	v_lshlrev_b32_e32 v112, 2, v112
	ds_bpermute_b32 v112, v112, v108
	s_waitcnt lgkmcnt(0)
	v_add_f32_e32 v108, v108, v112
	v_xor_b32_e32 v112, 4, v169
	v_cmp_lt_i32_e32 vcc, v112, v109
	s_nop 1
	v_cndmask_b32_e32 v112, v169, v112, vcc
	v_lshlrev_b32_e32 v112, 2, v112
	ds_bpermute_b32 v112, v112, v108
	s_waitcnt lgkmcnt(0)
	v_add_f32_e32 v108, v108, v112
	v_xor_b32_e32 v112, 2, v169
	v_cmp_lt_i32_e32 vcc, v112, v109
	s_nop 1
	v_cndmask_b32_e32 v112, v169, v112, vcc
	v_lshlrev_b32_e32 v112, 2, v112
	ds_bpermute_b32 v112, v112, v108
	s_waitcnt lgkmcnt(0)
	v_add_f32_e32 v108, v108, v112
	v_xor_b32_e32 v112, 1, v169
	v_cmp_lt_i32_e32 vcc, v112, v109
	s_nop 1
	v_cndmask_b32_e32 v109, v169, v112, vcc
	v_lshlrev_b32_e32 v109, 2, v109
	ds_bpermute_b32 v109, v109, v108
	s_waitcnt lgkmcnt(0)
	v_add_f32_e32 v108, v108, v109
	v_fmamk_f32 v108, v108, 0x3a800000, v166
	v_rsq_f32_e32 v120, v108
	s_nop 0
	v_pk_mul_f32 v[106:107], v[106:107], v[120:121] op_sel_hi:[1,0]
	v_pk_mul_f32 v[102:103], v[102:103], v[120:121] op_sel_hi:[1,0]
	v_pk_mul_f32 v[98:99], v[98:99], v[120:121] op_sel_hi:[1,0]
	v_pk_fma_f32 v[108:109], v[84:85], v[102:103], v[72:73]
	v_pk_fma_f32 v[106:107], v[82:83], v[106:107], v[70:71]
	v_pk_mul_f32 v[102:103], v[110:111], v[120:121] op_sel_hi:[1,0]
	v_pk_fma_f32 v[116:117], v[92:93], v[98:99], v[80:81]
	v_pk_mul_f32 v[98:99], v[118:119], v[120:121] op_sel_hi:[1,0]
	v_pk_mul_f32 v[100:101], v[100:101], v[120:121] op_sel:[1,0] op_sel_hi:[0,0]
	v_pk_mul_f32 v[104:105], v[104:105], v[120:121] op_sel_hi:[1,0]
	v_pk_fma_f32 v[110:111], v[86:87], v[102:103], v[66:67]
	v_pk_mul_f32 v[102:103], v[114:115], v[120:121] op_sel_hi:[1,0]
	v_pk_fma_f32 v[120:121], v[96:97], v[100:101], v[76:77]
	v_pk_fma_f32 v[118:119], v[94:95], v[98:99], v[74:75]
	v_med3_f32 v99, v106, s50, v170
	v_med3_f32 v100, v107, s50, v170
	s_nop 0
	v_pk_fma_f32 v[114:115], v[90:91], v[102:103], v[78:79]
	v_cvt_pk_fp8_f32 v98, v99, v100
	v_med3_f32 v100, v110, s50, v170
	v_med3_f32 v103, v111, s50, v170
	s_nop 0
	v_cvt_pk_fp8_f32 v99, v100, v103
	v_pk_fma_f32 v[112:113], v[88:89], v[104:105], v[68:69]
	v_med3_f32 v101, v108, s50, v170
	v_med3_f32 v102, v109, s50, v170
	v_cvt_pk_fp8_f32 v98, v101, v102 op_sel:[0,0,1]
	v_med3_f32 v100, v112, s50, v170
	v_med3_f32 v101, v113, s50, v170
	v_cvt_pk_fp8_f32 v99, v100, v101 op_sel:[0,0,1]
	v_med3_f32 v101, v114, s50, v170
	v_med3_f32 v102, v115, s50, v170
	s_nop 0
	v_cvt_pk_fp8_f32 v100, v101, v102
	v_med3_f32 v102, v118, s50, v170
	v_med3_f32 v105, v119, s50, v170
	s_nop 0
	v_cvt_pk_fp8_f32 v101, v102, v105
	v_med3_f32 v103, v116, s50, v170
	v_med3_f32 v104, v117, s50, v170
	v_cvt_pk_fp8_f32 v100, v103, v104 op_sel:[0,0,1]
	v_med3_f32 v102, v120, s50, v170
	v_med3_f32 v103, v121, s50, v170
	v_cvt_pk_fp8_f32 v101, v102, v103 op_sel:[0,0,1]
	v_lshlrev_b64 v[102:103], 10, v[122:123]
	v_lshl_add_u64 v[102:103], v[146:147], 0, v[102:103]
	global_store_dwordx2 v[102:103], v[98:99], off
	global_store_dwordx2 v[102:103], v[100:101], off offset:512

; DI unsigned pk4_fp8(float a, float b, float c, float d) { int r = 0; r = __builtin_amdgcn_cvt_pk_fp8_f32(a, b, r, false); r = __builtin_amdgcn_cvt_pk_fp8_f32(c, d, r, true); return (unsigned)r; }
; DI float clamp448(float x) { return __builtin_amdgcn_fmed3f(x, -448.0f, 448.0f); }
; DI float bflo(unsigned u) { return __uint_as_float(u << 16); }
; DI float bfhi(unsigned u) { return __uint_as_float(u & 0xffff0000u); }
; DI void phase_router(unsigned char* lds, const Params& P, int li, const bf16_t* X1, unsigned char* H8, const float* modl, unsigned* cnt, int* tok_e, int* tok_pos, float* tok_gate, int* tok_list, int G, int ntok, int chsz) {
;     ...
;                 if (tl < chsz) {
;                     const u32x4 a = ra[rr], b = rbv[rr];
;                     v[0] = (f32x4){bflo(a[0]), bfhi(a[0]), bflo(a[1]), bfhi(a[1])}; v[1] = (f32x4){bflo(a[2]), bfhi(a[2]), bflo(a[3]), bfhi(a[3])};
;                     v[2] = (f32x4){bflo(b[0]), bfhi(b[0]), bflo(b[1]), bfhi(b[1])}; v[3] = (f32x4){bflo(b[2]), bfhi(b[2]), bflo(b[3]), bfhi(b[3])};
;                     const int b9 = tok < NLAT ? (tok >> 12) : 8; if (b9 != cur_b9) load_mod(b9);
;                     float ss = 0.f;
; #pragma unroll
;                     for (int j = 0; j < 4; ++j)
; #pragma unroll
;                         for (int i = 0; i < 4; ++i) ss += v[j][i] * v[j][i];
;                     ss = wave_sum(ss);
;                     const float rinv = __builtin_amdgcn_rsqf(ss * (1.0f / 1024.0f) + EPS);
; #pragma unroll
;                     for (int j = 0; j < 4; ++j) v[j] = v[j] * rinv * ma[j] + mb[j];
;                     { unsigned char* hr = H8 + (size_t)tok * 1024; u32x2 w0, w1;
;                       w0.x = pk4_fp8(clamp448(v[0][0]), clamp448(v[0][1]), clamp448(v[0][2]), clamp448(v[0][3])); w0.y = pk4_fp8(clamp448(v[1][0]), clamp448(v[1][1]), clamp448(v[1][2]), clamp448(v[1][3]));
;                       w1.x = pk4_fp8(clamp448(v[2][0]), clamp448(v[2][1]), clamp448(v[2][2]), clamp448(v[2][3])); w1.y = pk4_fp8(clamp448(v[3][0]), clamp448(v[3][1]), clamp448(v[3][2]), clamp448(v[3][3]));
;                       *(u32x2*)(hr + 8 * lane) = w0; *(u32x2*)(hr + 512 + 8 * lane) = w1; } }
.LBB0_987:
	s_or_b64 exec, exec, s[38:39]
	s_waitcnt vmcnt(3)
	v_and_b32_e32 v115, 0xffff0000, v110
	v_lshlrev_b32_e32 v114, 16, v110
	v_mul_f32_e32 v120, v115, v115
	v_lshlrev_b32_e32 v110, 16, v111
	v_fmac_f32_e32 v120, v114, v114
	v_and_b32_e32 v111, 0xffff0000, v111
	v_fmac_f32_e32 v120, v110, v110
	v_lshlrev_b32_e32 v118, 16, v112
	v_fmac_f32_e32 v120, v111, v111
	v_and_b32_e32 v119, 0xffff0000, v112
	v_fmac_f32_e32 v120, v118, v118
	v_lshlrev_b32_e32 v112, 16, v113
	v_fmac_f32_e32 v120, v119, v119
	v_and_b32_e32 v113, 0xffff0000, v113
	v_fmac_f32_e32 v120, v112, v112
	s_waitcnt vmcnt(2)
	v_lshlrev_b32_e32 v122, 16, v106
	v_fmac_f32_e32 v120, v113, v113
	v_and_b32_e32 v123, 0xffff0000, v106
	v_fmac_f32_e32 v120, v122, v122
	v_lshlrev_b32_e32 v106, 16, v107
	v_fmac_f32_e32 v120, v123, v123
	v_and_b32_e32 v107, 0xffff0000, v107
	v_fmac_f32_e32 v120, v106, v106
	v_lshlrev_b32_e32 v126, 16, v108
	v_fmac_f32_e32 v120, v107, v107
	v_and_b32_e32 v127, 0xffff0000, v108
	v_and_b32_e32 v108, 0xffff0000, v109
	v_lshlrev_b32_e32 v109, 16, v109
	v_fmac_f32_e32 v120, v126, v126
	v_fmac_f32_e32 v120, v127, v127
	v_pk_mul_f32 v[116:117], v[108:109], v[108:109]
	v_ashrrev_i32_e32 v151, 31, v150
	v_add_f32_e32 v117, v117, v120
	v_add_f32_e32 v116, v116, v117
	v_and_b32_e32 v117, 64, v169
	v_add_u32_e32 v117, 64, v117
	v_xor_b32_e32 v120, 32, v169
	v_cmp_lt_i32_e32 vcc, v120, v117
	s_nop 1
	v_cndmask_b32_e32 v120, v169, v120, vcc
	v_lshlrev_b32_e32 v120, 2, v120
	ds_bpermute_b32 v120, v120, v116
	s_waitcnt lgkmcnt(0)
	v_add_f32_e32 v116, v116, v120
	v_xor_b32_e32 v120, 16, v169
	v_cmp_lt_i32_e32 vcc, v120, v117
	s_nop 1
	v_cndmask_b32_e32 v120, v169, v120, vcc
	v_lshlrev_b32_e32 v120, 2, v120
	ds_bpermute_b32 v120, v120, v116
	s_waitcnt lgkmcnt(0)
	v_add_f32_e32 v116, v116, v120
	v_xor_b32_e32 v120, 8, v169
	v_cmp_lt_i32_e32 vcc, v120, v117
	s_nop 1
	v_cndmask_b32_e32 v120, v169, v120, vcc
	v_lshlrev_b32_e32 v120, 2, v120
	ds_bpermute_b32 v120, v120, v116
	s_waitcnt lgkmcnt(0)
	v_add_f32_e32 v116, v116, v120
	v_xor_b32_e32 v120, 4, v169
	v_cmp_lt_i32_e32 vcc, v120, v117
	s_nop 1
	v_cndmask_b32_e32 v120, v169, v120, vcc
	v_lshlrev_b32_e32 v120, 2, v120
	ds_bpermute_b32 v120, v120, v116
	s_waitcnt lgkmcnt(0)
	v_add_f32_e32 v116, v116, v120
	v_xor_b32_e32 v120, 2, v169
	v_cmp_lt_i32_e32 vcc, v120, v117
	s_nop 1
	v_cndmask_b32_e32 v120, v169, v120, vcc
	v_lshlrev_b32_e32 v120, 2, v120
	ds_bpermute_b32 v120, v120, v116
	s_waitcnt lgkmcnt(0)
	v_add_f32_e32 v116, v116, v120
	v_xor_b32_e32 v120, 1, v169
	v_cmp_lt_i32_e32 vcc, v120, v117
	s_nop 1
	v_cndmask_b32_e32 v117, v169, v120, vcc
	v_lshlrev_b32_e32 v117, 2, v117
	ds_bpermute_b32 v117, v117, v116
	s_waitcnt lgkmcnt(0)
	v_add_f32_e32 v116, v116, v117
	v_fmamk_f32 v116, v116, 0x3a800000, v166
	v_rsq_f32_e32 v128, v116
	s_nop 0
	v_pk_mul_f32 v[114:115], v[114:115], v[128:129] op_sel_hi:[1,0]
	v_pk_mul_f32 v[110:111], v[110:111], v[128:129] op_sel_hi:[1,0]
	v_pk_mul_f32 v[106:107], v[106:107], v[128:129] op_sel_hi:[1,0]
	v_pk_fma_f32 v[116:117], v[84:85], v[110:111], v[72:73]
	v_pk_fma_f32 v[114:115], v[82:83], v[114:115], v[70:71]
	v_pk_mul_f32 v[110:111], v[118:119], v[128:129] op_sel_hi:[1,0]
	s_waitcnt vmcnt(0)
	v_pk_fma_f32 v[124:125], v[92:93], v[106:107], v[80:81]
	v_pk_mul_f32 v[106:107], v[126:127], v[128:129] op_sel_hi:[1,0]
	v_pk_mul_f32 v[108:109], v[108:109], v[128:129] op_sel:[1,0] op_sel_hi:[0,0]
	v_pk_mul_f32 v[112:113], v[112:113], v[128:129] op_sel_hi:[1,0]
	v_pk_fma_f32 v[118:119], v[86:87], v[110:111], v[66:67]
	v_pk_mul_f32 v[110:111], v[122:123], v[128:129] op_sel_hi:[1,0]
	v_pk_fma_f32 v[128:129], v[96:97], v[108:109], v[76:77]
	v_pk_fma_f32 v[126:127], v[94:95], v[106:107], v[74:75]
	v_med3_f32 v107, v114, s50, v170
	v_med3_f32 v108, v115, s50, v170
	s_nop 0
	v_pk_fma_f32 v[122:123], v[90:91], v[110:111], v[78:79]
	v_cvt_pk_fp8_f32 v106, v107, v108
	v_med3_f32 v108, v118, s50, v170
	v_med3_f32 v111, v119, s50, v170
	s_nop 0
	v_cvt_pk_fp8_f32 v107, v108, v111
	v_pk_fma_f32 v[120:121], v[88:89], v[112:113], v[68:69]
	v_med3_f32 v109, v116, s50, v170
	v_med3_f32 v110, v117, s50, v170
	v_cvt_pk_fp8_f32 v106, v109, v110 op_sel:[0,0,1]
	v_med3_f32 v108, v120, s50, v170
	v_med3_f32 v109, v121, s50, v170
	v_cvt_pk_fp8_f32 v107, v108, v109 op_sel:[0,0,1]
	v_med3_f32 v109, v122, s50, v170
	v_med3_f32 v110, v123, s50, v170
	s_nop 0
	v_cvt_pk_fp8_f32 v108, v109, v110
	v_med3_f32 v110, v126, s50, v170
	v_med3_f32 v113, v127, s50, v170
	s_nop 0
	v_cvt_pk_fp8_f32 v109, v110, v113
	v_med3_f32 v111, v124, s50, v170
	v_med3_f32 v112, v125, s50, v170
	v_cvt_pk_fp8_f32 v108, v111, v112 op_sel:[0,0,1]
	v_med3_f32 v110, v128, s50, v170
	v_med3_f32 v111, v129, s50, v170
	v_cvt_pk_fp8_f32 v109, v110, v111 op_sel:[0,0,1]
	v_lshlrev_b64 v[110:111], 10, v[150:151]
	v_lshl_add_u64 v[110:111], v[146:147], 0, v[110:111]
	global_store_dwordx2 v[110:111], v[106:107], off
	global_store_dwordx2 v[110:111], v[108:109], off offset:512

; DI unsigned pk4_fp8(float a, float b, float c, float d) { int r = 0; r = __builtin_amdgcn_cvt_pk_fp8_f32(a, b, r, false); r = __builtin_amdgcn_cvt_pk_fp8_f32(c, d, r, true); return (unsigned)r; }
; DI float clamp448(float x) { return __builtin_amdgcn_fmed3f(x, -448.0f, 448.0f); }
; DI float bflo(unsigned u) { return __uint_as_float(u << 16); }
; DI float bfhi(unsigned u) { return __uint_as_float(u & 0xffff0000u); }
; DI void phase_router(unsigned char* lds, const Params& P, int li, const bf16_t* X1, unsigned char* H8, const float* modl, unsigned* cnt, int* tok_e, int* tok_pos, float* tok_gate, int* tok_list, int G, int ntok, int chsz) {
;     ...
;                 if (tl < chsz) {
;                     const u32x4 a = ra[rr], b = rbv[rr];
;                     v[0] = (f32x4){bflo(a[0]), bfhi(a[0]), bflo(a[1]), bfhi(a[1])}; v[1] = (f32x4){bflo(a[2]), bfhi(a[2]), bflo(a[3]), bfhi(a[3])};
;                     v[2] = (f32x4){bflo(b[0]), bfhi(b[0]), bflo(b[1]), bfhi(b[1])}; v[3] = (f32x4){bflo(b[2]), bfhi(b[2]), bflo(b[3]), bfhi(b[3])};
;                     const int b9 = tok < NLAT ? (tok >> 12) : 8; if (b9 != cur_b9) load_mod(b9);
;                     float ss = 0.f;
; #pragma unroll
;                     for (int j = 0; j < 4; ++j)
; #pragma unroll
;                         for (int i = 0; i < 4; ++i) ss += v[j][i] * v[j][i];
;                     ss = wave_sum(ss);
;                     const float rinv = __builtin_amdgcn_rsqf(ss * (1.0f / 1024.0f) + EPS);
; #pragma unroll
;                     for (int j = 0; j < 4; ++j) v[j] = v[j] * rinv * ma[j] + mb[j];
;                     { unsigned char* hr = H8 + (size_t)tok * 1024; u32x2 w0, w1;
;                       w0.x = pk4_fp8(clamp448(v[0][0]), clamp448(v[0][1]), clamp448(v[0][2]), clamp448(v[0][3])); w0.y = pk4_fp8(clamp448(v[1][0]), clamp448(v[1][1]), clamp448(v[1][2]), clamp448(v[1][3]));
;                       w1.x = pk4_fp8(clamp448(v[2][0]), clamp448(v[2][1]), clamp448(v[2][2]), clamp448(v[2][3])); w1.y = pk4_fp8(clamp448(v[3][0]), clamp448(v[3][1]), clamp448(v[3][2]), clamp448(v[3][3]));
;                       *(u32x2*)(hr + 8 * lane) = w0; *(u32x2*)(hr + 512 + 8 * lane) = w1; } }
.LBB0_994:
	s_or_b64 exec, exec, s[40:41]
	v_and_b32_e32 v115, 0xffff0000, v110
	v_lshlrev_b32_e32 v114, 16, v110
	v_mul_f32_e32 v120, v115, v115
	v_lshlrev_b32_e32 v110, 16, v111
	v_fmac_f32_e32 v120, v114, v114
	v_and_b32_e32 v111, 0xffff0000, v111
	v_fmac_f32_e32 v120, v110, v110
	v_lshlrev_b32_e32 v118, 16, v112
	v_fmac_f32_e32 v120, v111, v111
	v_and_b32_e32 v119, 0xffff0000, v112
	v_fmac_f32_e32 v120, v118, v118
	v_lshlrev_b32_e32 v112, 16, v113
	v_fmac_f32_e32 v120, v119, v119
	v_and_b32_e32 v113, 0xffff0000, v113
	v_fmac_f32_e32 v120, v112, v112
	v_lshlrev_b32_e32 v122, 16, v106
	v_fmac_f32_e32 v120, v113, v113
	v_and_b32_e32 v123, 0xffff0000, v106
	v_fmac_f32_e32 v120, v122, v122
	v_lshlrev_b32_e32 v106, 16, v107
	v_fmac_f32_e32 v120, v123, v123
	v_and_b32_e32 v107, 0xffff0000, v107
	v_fmac_f32_e32 v120, v106, v106
	v_lshlrev_b32_e32 v126, 16, v108
	v_fmac_f32_e32 v120, v107, v107
	v_and_b32_e32 v127, 0xffff0000, v108
	v_and_b32_e32 v108, 0xffff0000, v109
	v_lshlrev_b32_e32 v109, 16, v109
	v_fmac_f32_e32 v120, v126, v126
	v_fmac_f32_e32 v120, v127, v127
	v_pk_mul_f32 v[116:117], v[108:109], v[108:109]
	v_ashrrev_i32_e32 v151, 31, v150
	v_add_f32_e32 v117, v117, v120
	v_add_f32_e32 v116, v116, v117
	v_and_b32_e32 v117, 64, v169
	v_add_u32_e32 v117, 64, v117
	v_xor_b32_e32 v120, 32, v169
	v_cmp_lt_i32_e64 s[12:13], v120, v117
	s_nop 1
	v_cndmask_b32_e64 v120, v169, v120, s[12:13]
	v_lshlrev_b32_e32 v120, 2, v120
	ds_bpermute_b32 v120, v120, v116
	s_waitcnt lgkmcnt(0)
	v_add_f32_e32 v116, v116, v120
	v_xor_b32_e32 v120, 16, v169
	v_cmp_lt_i32_e64 s[12:13], v120, v117
	s_nop 1
	v_cndmask_b32_e64 v120, v169, v120, s[12:13]
	v_lshlrev_b32_e32 v120, 2, v120
	ds_bpermute_b32 v120, v120, v116
	s_waitcnt lgkmcnt(0)
	v_add_f32_e32 v116, v116, v120
	v_xor_b32_e32 v120, 8, v169
	v_cmp_lt_i32_e64 s[12:13], v120, v117
	s_nop 1
	v_cndmask_b32_e64 v120, v169, v120, s[12:13]
	v_lshlrev_b32_e32 v120, 2, v120
	ds_bpermute_b32 v120, v120, v116
	s_waitcnt lgkmcnt(0)
	v_add_f32_e32 v116, v116, v120
	v_xor_b32_e32 v120, 4, v169
	v_cmp_lt_i32_e64 s[12:13], v120, v117
	s_nop 1
	v_cndmask_b32_e64 v120, v169, v120, s[12:13]
	v_lshlrev_b32_e32 v120, 2, v120
	ds_bpermute_b32 v120, v120, v116
	s_waitcnt lgkmcnt(0)
	v_add_f32_e32 v116, v116, v120
	v_xor_b32_e32 v120, 2, v169
	v_cmp_lt_i32_e64 s[12:13], v120, v117
	s_nop 1
	v_cndmask_b32_e64 v120, v169, v120, s[12:13]
	v_lshlrev_b32_e32 v120, 2, v120
	ds_bpermute_b32 v120, v120, v116
	s_waitcnt lgkmcnt(0)
	v_add_f32_e32 v116, v116, v120
	v_xor_b32_e32 v120, 1, v169
	v_cmp_lt_i32_e64 s[12:13], v120, v117
	s_nop 1
	v_cndmask_b32_e64 v117, v169, v120, s[12:13]
	v_lshlrev_b32_e32 v117, 2, v117
	ds_bpermute_b32 v117, v117, v116
	s_waitcnt lgkmcnt(0)
	v_add_f32_e32 v116, v116, v117
	v_fmamk_f32 v116, v116, 0x3a800000, v166
	v_rsq_f32_e32 v128, v116
	s_nop 0
	v_pk_mul_f32 v[114:115], v[114:115], v[128:129] op_sel_hi:[1,0]
	v_pk_mul_f32 v[110:111], v[110:111], v[128:129] op_sel_hi:[1,0]
	v_pk_mul_f32 v[106:107], v[106:107], v[128:129] op_sel_hi:[1,0]
	s_waitcnt vmcnt(2)
	v_pk_fma_f32 v[116:117], v[84:85], v[110:111], v[72:73]
	v_pk_fma_f32 v[114:115], v[82:83], v[114:115], v[70:71]
	v_pk_mul_f32 v[110:111], v[118:119], v[128:129] op_sel_hi:[1,0]
	s_waitcnt vmcnt(0)
	v_pk_fma_f32 v[124:125], v[92:93], v[106:107], v[80:81]
	v_pk_mul_f32 v[106:107], v[126:127], v[128:129] op_sel_hi:[1,0]
	v_pk_mul_f32 v[108:109], v[108:109], v[128:129] op_sel:[1,0] op_sel_hi:[0,0]
	v_pk_mul_f32 v[112:113], v[112:113], v[128:129] op_sel_hi:[1,0]
	v_pk_fma_f32 v[118:119], v[86:87], v[110:111], v[66:67]
	v_pk_mul_f32 v[110:111], v[122:123], v[128:129] op_sel_hi:[1,0]
	v_pk_fma_f32 v[128:129], v[96:97], v[108:109], v[76:77]
	v_pk_fma_f32 v[126:127], v[94:95], v[106:107], v[74:75]
	v_med3_f32 v107, v114, s50, v170
	v_med3_f32 v108, v115, s50, v170
	s_nop 0
	v_pk_fma_f32 v[122:123], v[90:91], v[110:111], v[78:79]
	v_cvt_pk_fp8_f32 v106, v107, v108
	v_med3_f32 v108, v118, s50, v170
	v_med3_f32 v111, v119, s50, v170
	s_nop 0
	v_cvt_pk_fp8_f32 v107, v108, v111
	v_pk_fma_f32 v[120:121], v[88:89], v[112:113], v[68:69]
	v_med3_f32 v109, v116, s50, v170
	v_med3_f32 v110, v117, s50, v170
	v_cvt_pk_fp8_f32 v106, v109, v110 op_sel:[0,0,1]
	v_med3_f32 v108, v120, s50, v170
	v_med3_f32 v109, v121, s50, v170
	v_cvt_pk_fp8_f32 v107, v108, v109 op_sel:[0,0,1]
	v_med3_f32 v109, v122, s50, v170
	v_med3_f32 v110, v123, s50, v170
	s_nop 0
	v_cvt_pk_fp8_f32 v108, v109, v110
	v_med3_f32 v110, v126, s50, v170
	v_med3_f32 v113, v127, s50, v170
	s_nop 0
	v_cvt_pk_fp8_f32 v109, v110, v113
	v_med3_f32 v111, v124, s50, v170
	v_med3_f32 v112, v125, s50, v170
	v_cvt_pk_fp8_f32 v108, v111, v112 op_sel:[0,0,1]
	v_med3_f32 v110, v128, s50, v170
	v_med3_f32 v111, v129, s50, v170
	v_cvt_pk_fp8_f32 v109, v110, v111 op_sel:[0,0,1]
	v_lshlrev_b64 v[110:111], 10, v[150:151]
	v_lshl_add_u64 v[110:111], v[146:147], 0, v[110:111]
	global_store_dwordx2 v[110:111], v[106:107], off
	global_store_dwordx2 v[110:111], v[108:109], off offset:512

; DI unsigned pk4_fp8(float a, float b, float c, float d) { int r = 0; r = __builtin_amdgcn_cvt_pk_fp8_f32(a, b, r, false); r = __builtin_amdgcn_cvt_pk_fp8_f32(c, d, r, true); return (unsigned)r; }
; DI float clamp448(float x) { return __builtin_amdgcn_fmed3f(x, -448.0f, 448.0f); }
; DI float bflo(unsigned u) { return __uint_as_float(u << 16); }
; DI float bfhi(unsigned u) { return __uint_as_float(u & 0xffff0000u); }
; DI void phase_router(unsigned char* lds, const Params& P, int li, const bf16_t* X1, unsigned char* H8, const float* modl, unsigned* cnt, int* tok_e, int* tok_pos, float* tok_gate, int* tok_list, int G, int ntok, int chsz) {
;     ...
;                 if (tl < chsz) {
;                     const u32x4 a = ra[rr], b = rbv[rr];
;                     v[0] = (f32x4){bflo(a[0]), bfhi(a[0]), bflo(a[1]), bfhi(a[1])}; v[1] = (f32x4){bflo(a[2]), bfhi(a[2]), bflo(a[3]), bfhi(a[3])};
;                     v[2] = (f32x4){bflo(b[0]), bfhi(b[0]), bflo(b[1]), bfhi(b[1])}; v[3] = (f32x4){bflo(b[2]), bfhi(b[2]), bflo(b[3]), bfhi(b[3])};
;                     const int b9 = tok < NLAT ? (tok >> 12) : 8; if (b9 != cur_b9) load_mod(b9);
;                     float ss = 0.f;
; #pragma unroll
;                     for (int j = 0; j < 4; ++j)
; #pragma unroll
;                         for (int i = 0; i < 4; ++i) ss += v[j][i] * v[j][i];
;                     ss = wave_sum(ss);
;                     const float rinv = __builtin_amdgcn_rsqf(ss * (1.0f / 1024.0f) + EPS);
; #pragma unroll
;                     for (int j = 0; j < 4; ++j) v[j] = v[j] * rinv * ma[j] + mb[j];
;                     { unsigned char* hr = H8 + (size_t)tok * 1024; u32x2 w0, w1;
;                       w0.x = pk4_fp8(clamp448(v[0][0]), clamp448(v[0][1]), clamp448(v[0][2]), clamp448(v[0][3])); w0.y = pk4_fp8(clamp448(v[1][0]), clamp448(v[1][1]), clamp448(v[1][2]), clamp448(v[1][3]));
;                       w1.x = pk4_fp8(clamp448(v[2][0]), clamp448(v[2][1]), clamp448(v[2][2]), clamp448(v[2][3])); w1.y = pk4_fp8(clamp448(v[3][0]), clamp448(v[3][1]), clamp448(v[3][2]), clamp448(v[3][3]));
;                       *(u32x2*)(hr + 8 * lane) = w0; *(u32x2*)(hr + 512 + 8 * lane) = w1; } }
.LBB0_998:
	s_or_b64 exec, exec, s[38:39]
	v_and_b32_e32 v107, 0xffff0000, v102
	v_lshlrev_b32_e32 v106, 16, v102
	v_mul_f32_e32 v112, v107, v107
	v_lshlrev_b32_e32 v102, 16, v103
	v_fmac_f32_e32 v112, v106, v106
	v_and_b32_e32 v103, 0xffff0000, v103
	v_fmac_f32_e32 v112, v102, v102
	v_lshlrev_b32_e32 v110, 16, v104
	v_fmac_f32_e32 v112, v103, v103
	v_and_b32_e32 v111, 0xffff0000, v104
	v_fmac_f32_e32 v112, v110, v110
	v_lshlrev_b32_e32 v104, 16, v105
	v_fmac_f32_e32 v112, v111, v111
	v_and_b32_e32 v105, 0xffff0000, v105
	v_fmac_f32_e32 v112, v104, v104
	v_lshlrev_b32_e32 v114, 16, v98
	v_fmac_f32_e32 v112, v105, v105
	v_and_b32_e32 v115, 0xffff0000, v98
	v_fmac_f32_e32 v112, v114, v114
	v_lshlrev_b32_e32 v98, 16, v99
	v_fmac_f32_e32 v112, v115, v115
	v_and_b32_e32 v99, 0xffff0000, v99
	v_fmac_f32_e32 v112, v98, v98
	v_lshlrev_b32_e32 v118, 16, v100
	v_fmac_f32_e32 v112, v99, v99
	v_and_b32_e32 v119, 0xffff0000, v100
	v_and_b32_e32 v100, 0xffff0000, v101
	v_lshlrev_b32_e32 v101, 16, v101
	v_fmac_f32_e32 v112, v118, v118
	v_fmac_f32_e32 v112, v119, v119
	v_pk_mul_f32 v[108:109], v[100:101], v[100:101]
	v_ashrrev_i32_e32 v123, 31, v122
	v_add_f32_e32 v109, v109, v112
	v_add_f32_e32 v108, v108, v109
	v_and_b32_e32 v109, 64, v169
	v_add_u32_e32 v109, 64, v109
	v_xor_b32_e32 v112, 32, v169
	v_cmp_lt_i32_e32 vcc, v112, v109
	s_nop 1
	v_cndmask_b32_e32 v112, v169, v112, vcc
	v_lshlrev_b32_e32 v112, 2, v112
	ds_bpermute_b32 v112, v112, v108
	s_waitcnt lgkmcnt(0)
	v_add_f32_e32 v108, v108, v112
	v_xor_b32_e32 v112, 16, v169
	v_cmp_lt_i32_e32 vcc, v112, v109
	s_nop 1
	v_cndmask_b32_e32 v112, v169, v112, vcc
	v_lshlrev_b32_e32 v112, 2, v112
	ds_bpermute_b32 v112, v112, v108
	s_waitcnt lgkmcnt(0)
	v_add_f32_e32 v108, v108, v112
	v_xor_b32_e32 v112, 8, v169
	v_cmp_lt_i32_e32 vcc, v112, v109
	s_nop 1
	v_cndmask_b32_e32 v112, v169, v112, vcc
	v_lshlrev_b32_e32 v112, 2, v112
	ds_bpermute_b32 v112, v112, v108
	s_waitcnt lgkmcnt(0)
	v_add_f32_e32 v108, v108, v112
	v_xor_b32_e32 v112, 4, v169
	v_cmp_lt_i32_e32 vcc, v112, v109
	s_nop 1
	v_cndmask_b32_e32 v112, v169, v112, vcc
	v_lshlrev_b32_e32 v112, 2, v112
	ds_bpermute_b32 v112, v112, v108
	s_waitcnt lgkmcnt(0)
	v_add_f32_e32 v108, v108, v112
	v_xor_b32_e32 v112, 2, v169
	v_cmp_lt_i32_e32 vcc, v112, v109
	s_nop 1
	v_cndmask_b32_e32 v112, v169, v112, vcc
	v_lshlrev_b32_e32 v112, 2, v112
	ds_bpermute_b32 v112, v112, v108
	s_waitcnt lgkmcnt(0)
	v_add_f32_e32 v108, v108, v112
	v_xor_b32_e32 v112, 1, v169
	v_cmp_lt_i32_e32 vcc, v112, v109
	s_nop 1
	v_cndmask_b32_e32 v109, v169, v112, vcc
	v_lshlrev_b32_e32 v109, 2, v109
	ds_bpermute_b32 v109, v109, v108
	s_waitcnt lgkmcnt(0)
	v_add_f32_e32 v108, v108, v109
	v_fmamk_f32 v108, v108, 0x3a800000, v166
	v_rsq_f32_e32 v120, v108
	s_nop 0
	v_pk_mul_f32 v[106:107], v[106:107], v[120:121] op_sel_hi:[1,0]
	v_pk_mul_f32 v[102:103], v[102:103], v[120:121] op_sel_hi:[1,0]
	v_pk_mul_f32 v[98:99], v[98:99], v[120:121] op_sel_hi:[1,0]
	s_waitcnt vmcnt(2)
	v_pk_fma_f32 v[108:109], v[84:85], v[102:103], v[72:73]
	v_pk_fma_f32 v[106:107], v[82:83], v[106:107], v[70:71]
	v_pk_mul_f32 v[102:103], v[110:111], v[120:121] op_sel_hi:[1,0]
	s_waitcnt vmcnt(0)
	v_pk_fma_f32 v[116:117], v[92:93], v[98:99], v[80:81]
	v_pk_mul_f32 v[98:99], v[118:119], v[120:121] op_sel_hi:[1,0]
	v_pk_mul_f32 v[100:101], v[100:101], v[120:121] op_sel:[1,0] op_sel_hi:[0,0]
	v_pk_mul_f32 v[104:105], v[104:105], v[120:121] op_sel_hi:[1,0]
	v_pk_fma_f32 v[110:111], v[86:87], v[102:103], v[66:67]
	v_pk_mul_f32 v[102:103], v[114:115], v[120:121] op_sel_hi:[1,0]
	v_pk_fma_f32 v[120:121], v[96:97], v[100:101], v[76:77]
	v_pk_fma_f32 v[118:119], v[94:95], v[98:99], v[74:75]
	v_med3_f32 v99, v106, s50, v170
	v_med3_f32 v100, v107, s50, v170
	s_nop 0
	v_pk_fma_f32 v[114:115], v[90:91], v[102:103], v[78:79]
	v_cvt_pk_fp8_f32 v98, v99, v100
	v_med3_f32 v100, v110, s50, v170
	v_med3_f32 v103, v111, s50, v170
	s_nop 0
	v_cvt_pk_fp8_f32 v99, v100, v103
	v_pk_fma_f32 v[112:113], v[88:89], v[104:105], v[68:69]
	v_med3_f32 v101, v108, s50, v170
	v_med3_f32 v102, v109, s50, v170
	v_cvt_pk_fp8_f32 v98, v101, v102 op_sel:[0,0,1]
	v_med3_f32 v100, v112, s50, v170
	v_med3_f32 v101, v113, s50, v170
	v_cvt_pk_fp8_f32 v99, v100, v101 op_sel:[0,0,1]
	v_med3_f32 v101, v114, s50, v170
	v_med3_f32 v102, v115, s50, v170
	s_nop 0
	v_cvt_pk_fp8_f32 v100, v101, v102
	v_med3_f32 v102, v118, s50, v170
	v_med3_f32 v105, v119, s50, v170
	s_nop 0
	v_cvt_pk_fp8_f32 v101, v102, v105
	v_med3_f32 v103, v116, s50, v170
	v_med3_f32 v104, v117, s50, v170
	v_cvt_pk_fp8_f32 v100, v103, v104 op_sel:[0,0,1]
	v_med3_f32 v102, v120, s50, v170
	v_med3_f32 v103, v121, s50, v170
	v_cvt_pk_fp8_f32 v101, v102, v103 op_sel:[0,0,1]
	v_lshlrev_b64 v[102:103], 10, v[122:123]
	v_lshl_add_u64 v[102:103], v[146:147], 0, v[102:103]
	global_store_dwordx2 v[102:103], v[98:99], off
	global_store_dwordx2 v[102:103], v[100:101], off offset:512

; DI KParamsPtr kparams() { KParamsPtr p = (KParamsPtr)__builtin_amdgcn_kernarg_segment_ptr(); asm volatile("" : "+s"(p)); return p; }
; DI unsigned pk4_fp8(float a, float b, float c, float d) { int r = 0; r = __builtin_amdgcn_cvt_pk_fp8_f32(a, b, r, false); r = __builtin_amdgcn_cvt_pk_fp8_f32(c, d, r, true); return (unsigned)r; }
;     DI void operator()(EPI_ARGS) const {
;     ...
;         unsigned char* ACT = WSB(unsigned char, WS_ACT);
;         const int rbase = u.pm * 256 + wr * 64 + fr, cbase = u.pn * 128 + 32 * wc + 8 * fq;
;         const float* bb = kparams()->b_gu + ((size_t)li * NE + u.e) * 2048 + cbase;
;         constexpr float CG = -1.702f * LOG2E;
;         f32x4 bg[2], bu1[2];
; #pragma unroll
;         for (int n = 0; n < 2; ++n) { bg[n] = *(const f32x4*)(bb + 4 * n) * CG; bu1[n] = (*(const f32x4*)(bb + 1024 + 4 * n) + 1.0f) * (1.0f / CG); }
; #pragma unroll
;         for (int ai = 0; ai < 2; ++ai)
; #pragma unroll
;             for (int m = 0; m < 4; ++m) {
;                 const int row = rbase + 128 * ai + 16 * m;
;                 f32x4 o[2];
; #pragma unroll
;                 for (int n = 0; n < 2; ++n) {
;                     const f32x4 gg = acc[ai][0][m][n] * (W8_INV * CG) + bg[n], uu = acc[ai][1][m][n] * (W8_INV / CG) + bu1[n];
;                     f32x4 gv, u1, e;
; #pragma unroll
;                     for (int i = 0; i < 4; ++i) { gv[i] = fmaxf(gg[i], 7.0f * CG); u1[i] = __builtin_amdgcn_fmed3f(uu[i], 8.0f / CG, -6.0f / CG); }
; #pragma unroll
;                     for (int i = 0; i < 4; ++i) e[i] = __builtin_amdgcn_exp2f(gv[i]);
;                     const f32x4 d = e + 1.0f;
;                     f32x4 r;
; #pragma unroll
;                     for (int i = 0; i < 4; ++i) r[i] = __builtin_amdgcn_rcpf(d[i]);
;                     o[n] = gv * u1 * r;
;                 }
;                 u32x2 w; w.x = pk4_fp8(o[0][0], o[0][1], o[0][2], o[0][3]); w.y = pk4_fp8(o[1][0], o[1][1], o[1][2], o[1][3]);
;                 *(u32x2*)(ACT + (size_t)row * 1024 + cbase) = w;
;             }
.LBB0_1347:
	v_mov_b32_e32 v2, v208
	v_mov_b32_e32 v25, v1
	s_mov_b64 s[50:51], s[0:1]
	s_load_dwordx2 s[50:51], s[50:51], 0xb8
	s_lshl_b32 s14, s49, 8
	s_lshl_b32 s49, s82, 7
	s_or_b32 s49, s49, s28
	v_lshl_add_u32 v2, v2, 3, s49
	s_ashr_i32 s49, s48, 31
	s_lshl_b64 s[48:49], s[48:49], 13
	s_waitcnt lgkmcnt(0)
	s_add_u32 s48, s50, s48
	s_addc_u32 s49, s51, s49
	v_ashrrev_i32_e32 v3, 31, v2
	v_lshl_add_u64 v[12:13], v[2:3], 2, s[48:49]
	v_add_co_u32_e32 v14, vcc, s72, v12
	global_load_dwordx4 v[4:7], v[12:13], off offset:16
	global_load_dwordx4 v[8:11], v[12:13], off
	v_addc_co_u32_e32 v15, vcc, 0, v13, vcc
	v_lshl_add_u64 v[12:13], v[12:13], 0, s[36:37]
	global_load_dwordx4 v[16:19], v[14:15], off
	global_load_dwordx4 v[20:23], v[12:13], off offset:16
	v_lshl_add_u64 v[26:27], s[24:25], 0, v[2:3]
	s_add_i32 s14, s14, s60
	v_add_u32_e32 v28, s14, v25
	s_nop 0
	s_waitcnt vmcnt(0)
	v_pk_mul_f32 v[4:5], v[4:5], s[38:39] op_sel_hi:[1,0]
	v_pk_mul_f32 v[14:15], v[8:9], s[38:39] op_sel_hi:[1,0]
	v_pk_mul_f32 v[12:13], v[10:11], s[38:39] op_sel_hi:[1,0]
	v_pk_mul_f32 v[2:3], v[6:7], s[38:39] op_sel_hi:[1,0]
	v_fmamk_f32 v30, v186, 0xbd1d265f, v4
	v_pk_add_f32 v[6:7], v[18:19], 1.0 op_sel_hi:[1,0]
	v_pk_add_f32 v[10:11], v[22:23], 1.0 op_sel_hi:[1,0]
	v_fmamk_f32 v22, v190, 0xbd1d265f, v14
	v_fmamk_f32 v23, v191, 0xbd1d265f, v15
	v_fmamk_f32 v31, v187, 0xbd1d265f, v5
	v_pk_add_f32 v[8:9], v[16:17], 1.0 op_sel_hi:[1,0]
	v_pk_mul_f32 v[16:17], v[6:7], s[40:41] op_sel_hi:[1,0]
	v_pk_mul_f32 v[6:7], v[10:11], s[40:41] op_sel_hi:[1,0]
	v_max_f32_e32 v10, 0xc1898193, v22
	v_max_f32_e32 v11, 0xc1898193, v23
	v_max_f32_e32 v22, 0xc1898193, v30
	v_max_f32_e32 v23, 0xc1898193, v31
	v_pk_add_f32 v[20:21], v[20:21], 1.0 op_sel_hi:[1,0]
	v_exp_f32_e32 v40, v10
	v_exp_f32_e32 v41, v11
	v_exp_f32_e32 v44, v22
	v_exp_f32_e32 v45, v23
	v_pk_mul_f32 v[18:19], v[8:9], s[40:41] op_sel_hi:[1,0]
	v_pk_mul_f32 v[8:9], v[20:21], s[40:41] op_sel_hi:[1,0]
	v_fmamk_f32 v25, v192, 0xbd1d265f, v12
	v_fmamk_f32 v29, v193, 0xbd1d265f, v13
	v_fmamk_f32 v32, v188, 0xbd1d265f, v2
	v_fmamk_f32 v33, v189, 0xbd1d265f, v3
	v_fmamk_f32 v36, v178, 0xbbd083aa, v8
	v_fmamk_f32 v37, v179, 0xbbd083aa, v9
	v_max_f32_e32 v20, 0xc1898193, v25
	v_max_f32_e32 v21, 0xc1898193, v29
	v_max_f32_e32 v30, 0xc1898193, v32
	v_max_f32_e32 v31, 0xc1898193, v33
	v_fmamk_f32 v25, v182, 0xbbd083aa, v18
	v_fmamk_f32 v29, v183, 0xbbd083aa, v19
	v_med3_f32 v36, v36, s73, v203
	v_med3_f32 v37, v37, s73, v203
	v_exp_f32_e32 v42, v20
	v_exp_f32_e32 v43, v21
	v_exp_f32_e32 v46, v30
	v_exp_f32_e32 v47, v31
	v_med3_f32 v32, v25, s73, v203
	v_med3_f32 v33, v29, s73, v203
	v_pk_mul_f32 v[22:23], v[22:23], v[36:37]
	v_add_f32_e32 v25, 1.0, v40
	v_add_f32_e32 v29, 1.0, v41
	v_add_f32_e32 v36, 1.0, v44
	v_add_f32_e32 v37, 1.0, v45
	v_pk_mul_f32 v[10:11], v[10:11], v[32:33]
	v_rcp_f32_e32 v32, v25
	v_rcp_f32_e32 v33, v29
	v_rcp_f32_e32 v36, v36
	v_rcp_f32_e32 v37, v37
	v_fmamk_f32 v34, v184, 0xbbd083aa, v16
	v_fmamk_f32 v35, v185, 0xbbd083aa, v17
	v_med3_f32 v34, v34, s73, v203
	v_med3_f32 v35, v35, s73, v203
	v_pk_mul_f32 v[20:21], v[20:21], v[34:35]
	v_add_f32_e32 v34, 1.0, v42
	v_add_f32_e32 v35, 1.0, v43
	v_add_f32_e32 v40, 1.0, v46
	v_add_f32_e32 v41, 1.0, v47
	v_rcp_f32_e32 v34, v34
	v_rcp_f32_e32 v35, v35
	v_rcp_f32_e32 v40, v40
	v_rcp_f32_e32 v41, v41
	v_pk_mul_f32 v[10:11], v[10:11], v[32:33]
	v_pk_mul_f32 v[22:23], v[22:23], v[36:37]
	s_nop 0
	v_fmamk_f32 v38, v180, 0xbbd083aa, v6
	v_fmamk_f32 v39, v181, 0xbbd083aa, v7
	v_cvt_pk_fp8_f32 v24, v10, v11
	v_cvt_pk_fp8_f32 v25, v22, v23
	v_med3_f32 v38, v38, s73, v203
	v_med3_f32 v39, v39, s73, v203
	v_pk_mul_f32 v[10:11], v[30:31], v[38:39]
	v_pk_mul_f32 v[20:21], v[20:21], v[34:35]
	v_pk_mul_f32 v[10:11], v[10:11], v[40:41]
	v_cvt_pk_fp8_f32 v24, v20, v21 op_sel:[0,0,1]
	v_cvt_pk_fp8_f32 v25, v10, v11 op_sel:[0,0,1]
	v_ashrrev_i32_e32 v29, 31, v28
	v_lshlrev_b64 v[10:11], 10, v[28:29]
	v_lshl_add_u64 v[10:11], v[26:27], 0, v[10:11]
	global_store_dwordx2 v[10:11], v[24:25], off
	v_fmamk_f32 v25, v172, 0xbbd083aa, v16
	v_fmamk_f32 v24, v176, 0xbd1d265f, v12
	v_med3_f32 v26, v25, s73, v203
	v_fmamk_f32 v25, v177, 0xbd1d265f, v13
	v_max_f32_e32 v24, 0xc1898193, v24
	v_max_f32_e32 v25, 0xc1898193, v25
	v_exp_f32_e32 v30, v24
	v_exp_f32_e32 v31, v25
	v_fmamk_f32 v21, v170, 0xbbd083aa, v18
	v_fmamk_f32 v20, v174, 0xbd1d265f, v14
	v_med3_f32 v22, v21, s73, v203
	v_fmamk_f32 v21, v175, 0xbd1d265f, v15
	v_max_f32_e32 v20, 0xc1898193, v20
	v_max_f32_e32 v21, 0xc1898193, v21
	v_exp_f32_e32 v28, v20
	v_exp_f32_e32 v29, v21
	v_add_f32_e32 v30, 1.0, v30
	v_add_f32_e32 v31, 1.0, v31
	v_rcp_f32_e32 v30, v30
	v_rcp_f32_e32 v31, v31
	v_fmamk_f32 v27, v173, 0xbbd083aa, v17
	v_fmamk_f32 v23, v171, 0xbbd083aa, v19
	v_med3_f32 v27, v27, s73, v203
	v_med3_f32 v23, v23, s73, v203
	v_add_f32_e32 v28, 1.0, v28
	v_add_f32_e32 v29, 1.0, v29
	v_pk_mul_f32 v[24:25], v[24:25], v[26:27]
	v_rcp_f32_e32 v28, v28
	v_rcp_f32_e32 v29, v29
	v_pk_mul_f32 v[20:21], v[20:21], v[22:23]
	v_pk_mul_f32 v[22:23], v[24:25], v[30:31]
	v_fmamk_f32 v25, v162, 0xbbd083aa, v8
	v_fmamk_f32 v24, v166, 0xbd1d265f, v4
	v_med3_f32 v26, v25, s73, v203
	v_fmamk_f32 v25, v167, 0xbd1d265f, v5
	v_max_f32_e32 v24, 0xc1898193, v24
	v_max_f32_e32 v25, 0xc1898193, v25
	v_exp_f32_e32 v32, v24
	v_exp_f32_e32 v33, v25
	v_pk_mul_f32 v[20:21], v[20:21], v[28:29]
	v_fmamk_f32 v29, v164, 0xbbd083aa, v6
	v_fmamk_f32 v28, v168, 0xbd1d265f, v2
	v_med3_f32 v30, v29, s73, v203
	v_fmamk_f32 v29, v169, 0xbd1d265f, v3
	v_max_f32_e32 v28, 0xc1898193, v28
	v_max_f32_e32 v29, 0xc1898193, v29
	v_exp_f32_e32 v34, v28
	v_exp_f32_e32 v35, v29
; DI KParamsPtr kparams() { KParamsPtr p = (KParamsPtr)__builtin_amdgcn_kernarg_segment_ptr(); asm volatile("" : "+s"(p)); return p; }
; DI unsigned pk4_fp8(float a, float b, float c, float d) { int r = 0; r = __builtin_amdgcn_cvt_pk_fp8_f32(a, b, r, false); r = __builtin_amdgcn_cvt_pk_fp8_f32(c, d, r, true); return (unsigned)r; }
;     DI void operator()(EPI_ARGS) const {
;     ...
;         unsigned char* ACT = WSB(unsigned char, WS_ACT);
;         const int rbase = u.pm * 256 + wr * 64 + fr, cbase = u.pn * 128 + 32 * wc + 8 * fq;
;         const float* bb = kparams()->b_gu + ((size_t)li * NE + u.e) * 2048 + cbase;
;         constexpr float CG = -1.702f * LOG2E;
;         f32x4 bg[2], bu1[2];
; #pragma unroll
;         for (int n = 0; n < 2; ++n) { bg[n] = *(const f32x4*)(bb + 4 * n) * CG; bu1[n] = (*(const f32x4*)(bb + 1024 + 4 * n) + 1.0f) * (1.0f / CG); }
; #pragma unroll
;         for (int ai = 0; ai < 2; ++ai)
; #pragma unroll
;             for (int m = 0; m < 4; ++m) {
;                 const int row = rbase + 128 * ai + 16 * m;
;                 f32x4 o[2];
; #pragma unroll
;                 for (int n = 0; n < 2; ++n) {
;                     const f32x4 gg = acc[ai][0][m][n] * (W8_INV * CG) + bg[n], uu = acc[ai][1][m][n] * (W8_INV / CG) + bu1[n];
;                     f32x4 gv, u1, e;
; #pragma unroll
;                     for (int i = 0; i < 4; ++i) { gv[i] = fmaxf(gg[i], 7.0f * CG); u1[i] = __builtin_amdgcn_fmed3f(uu[i], 8.0f / CG, -6.0f / CG); }
; #pragma unroll
;                     for (int i = 0; i < 4; ++i) e[i] = __builtin_amdgcn_exp2f(gv[i]);
;                     const f32x4 d = e + 1.0f;
;                     f32x4 r;
; #pragma unroll
;                     for (int i = 0; i < 4; ++i) r[i] = __builtin_amdgcn_rcpf(d[i]);
;                     o[n] = gv * u1 * r;
;                 }
;                 u32x2 w; w.x = pk4_fp8(o[0][0], o[0][1], o[0][2], o[0][3]); w.y = pk4_fp8(o[1][0], o[1][1], o[1][2], o[1][3]);
;                 *(u32x2*)(ACT + (size_t)row * 1024 + cbase) = w;
;             }
	v_add_f32_e32 v32, 1.0, v32
	v_add_f32_e32 v33, 1.0, v33
	v_rcp_f32_e32 v32, v32
	v_rcp_f32_e32 v33, v33
	v_fmamk_f32 v27, v163, 0xbbd083aa, v9
	v_med3_f32 v27, v27, s73, v203
	v_add_f32_e32 v34, 1.0, v34
	v_add_f32_e32 v35, 1.0, v35
	v_pk_mul_f32 v[24:25], v[24:25], v[26:27]
	v_rcp_f32_e32 v34, v34
	v_rcp_f32_e32 v35, v35
	v_pk_mul_f32 v[24:25], v[24:25], v[32:33]
	s_nop 0
	s_nop 0
	v_fmamk_f32 v31, v165, 0xbbd083aa, v7
	v_cvt_pk_fp8_f32 v26, v20, v21
	v_cvt_pk_fp8_f32 v27, v24, v25
	v_med3_f32 v31, v31, s73, v203
	v_pk_mul_f32 v[20:21], v[28:29], v[30:31]
	v_cvt_pk_fp8_f32 v26, v22, v23 op_sel:[0,0,1]
	v_pk_mul_f32 v[20:21], v[20:21], v[34:35]
	v_fmamk_f32 v25, v156, 0xbbd083aa, v16
	v_cvt_pk_fp8_f32 v27, v20, v21 op_sel:[0,0,1]
	v_add_co_u32_e32 v20, vcc, s59, v10
	v_fmamk_f32 v24, v160, 0xbd1d265f, v12
	s_nop 0
	v_addc_co_u32_e32 v21, vcc, 0, v11, vcc
	global_store_dwordx2 v[20:21], v[26:27], off
	v_med3_f32 v26, v25, s73, v203
	v_fmamk_f32 v25, v161, 0xbd1d265f, v13
	v_max_f32_e32 v24, 0xc1898193, v24
	v_max_f32_e32 v25, 0xc1898193, v25
	v_exp_f32_e32 v30, v24
	v_exp_f32_e32 v31, v25
	v_fmamk_f32 v21, v154, 0xbbd083aa, v18
	v_fmamk_f32 v20, v158, 0xbd1d265f, v14
	v_med3_f32 v22, v21, s73, v203
	v_fmamk_f32 v21, v159, 0xbd1d265f, v15
	v_max_f32_e32 v20, 0xc1898193, v20
	v_max_f32_e32 v21, 0xc1898193, v21
	v_exp_f32_e32 v28, v20
	v_exp_f32_e32 v29, v21
	v_add_f32_e32 v30, 1.0, v30
	v_add_f32_e32 v31, 1.0, v31
	v_rcp_f32_e32 v30, v30
	v_rcp_f32_e32 v31, v31
	v_fmamk_f32 v27, v157, 0xbbd083aa, v17
	v_fmamk_f32 v23, v155, 0xbbd083aa, v19
	v_med3_f32 v27, v27, s73, v203
	v_med3_f32 v23, v23, s73, v203
	v_add_f32_e32 v28, 1.0, v28
	v_add_f32_e32 v29, 1.0, v29
	v_pk_mul_f32 v[24:25], v[24:25], v[26:27]
	v_rcp_f32_e32 v28, v28
	v_rcp_f32_e32 v29, v29
	v_pk_mul_f32 v[20:21], v[20:21], v[22:23]
	v_pk_mul_f32 v[22:23], v[24:25], v[30:31]
	v_fmamk_f32 v25, v146, 0xbbd083aa, v8
	v_fmamk_f32 v24, v150, 0xbd1d265f, v4
	v_med3_f32 v26, v25, s73, v203
	v_fmamk_f32 v25, v151, 0xbd1d265f, v5
	v_max_f32_e32 v24, 0xc1898193, v24
	v_max_f32_e32 v25, 0xc1898193, v25
	v_exp_f32_e32 v32, v24
	v_exp_f32_e32 v33, v25
	v_pk_mul_f32 v[20:21], v[20:21], v[28:29]
	v_fmamk_f32 v29, v148, 0xbbd083aa, v6
	v_fmamk_f32 v28, v152, 0xbd1d265f, v2
	v_med3_f32 v30, v29, s73, v203
	v_fmamk_f32 v29, v153, 0xbd1d265f, v3
	v_max_f32_e32 v28, 0xc1898193, v28
	v_max_f32_e32 v29, 0xc1898193, v29
	v_exp_f32_e32 v34, v28
	v_exp_f32_e32 v35, v29
	v_add_f32_e32 v32, 1.0, v32
	v_add_f32_e32 v33, 1.0, v33
	v_rcp_f32_e32 v32, v32
	v_rcp_f32_e32 v33, v33
	v_fmamk_f32 v27, v147, 0xbbd083aa, v9
	v_med3_f32 v27, v27, s73, v203
	v_add_f32_e32 v34, 1.0, v34
	v_add_f32_e32 v35, 1.0, v35
	v_pk_mul_f32 v[24:25], v[24:25], v[26:27]
	v_rcp_f32_e32 v34, v34
	v_rcp_f32_e32 v35, v35
	v_pk_mul_f32 v[24:25], v[24:25], v[32:33]
	s_nop 0
	s_nop 0
	v_fmamk_f32 v31, v149, 0xbbd083aa, v7
	v_cvt_pk_fp8_f32 v26, v20, v21
	v_cvt_pk_fp8_f32 v27, v24, v25
	v_med3_f32 v31, v31, s73, v203
	v_pk_mul_f32 v[20:21], v[28:29], v[30:31]
	v_cvt_pk_fp8_f32 v26, v22, v23 op_sel:[0,0,1]
	v_pk_mul_f32 v[20:21], v[20:21], v[34:35]
	v_fmamk_f32 v25, v140, 0xbbd083aa, v16
	v_cvt_pk_fp8_f32 v27, v20, v21 op_sel:[0,0,1]
	v_add_co_u32_e32 v20, vcc, s68, v10
	v_fmamk_f32 v24, v144, 0xbd1d265f, v12
	s_nop 0
	v_addc_co_u32_e32 v21, vcc, 0, v11, vcc
	global_store_dwordx2 v[20:21], v[26:27], off
	v_med3_f32 v26, v25, s73, v203
	v_fmamk_f32 v25, v145, 0xbd1d265f, v13
	v_max_f32_e32 v24, 0xc1898193, v24
	v_max_f32_e32 v25, 0xc1898193, v25
	v_exp_f32_e32 v30, v24
	v_exp_f32_e32 v31, v25
	v_fmamk_f32 v21, v138, 0xbbd083aa, v18
	v_fmamk_f32 v20, v142, 0xbd1d265f, v14
	v_med3_f32 v22, v21, s73, v203
	v_fmamk_f32 v21, v143, 0xbd1d265f, v15
	v_max_f32_e32 v20, 0xc1898193, v20
	v_max_f32_e32 v21, 0xc1898193, v21
	v_exp_f32_e32 v28, v20
	v_exp_f32_e32 v29, v21
	v_add_f32_e32 v30, 1.0, v30
	v_add_f32_e32 v31, 1.0, v31
	v_rcp_f32_e32 v30, v30
	v_rcp_f32_e32 v31, v31
	v_fmamk_f32 v27, v141, 0xbbd083aa, v17
	v_fmamk_f32 v23, v139, 0xbbd083aa, v19
	v_med3_f32 v27, v27, s73, v203
	v_med3_f32 v23, v23, s73, v203
	v_add_f32_e32 v28, 1.0, v28
	v_add_f32_e32 v29, 1.0, v29
	v_pk_mul_f32 v[24:25], v[24:25], v[26:27]
	v_rcp_f32_e32 v28, v28
	v_rcp_f32_e32 v29, v29
	v_pk_mul_f32 v[20:21], v[20:21], v[22:23]
	v_pk_mul_f32 v[22:23], v[24:25], v[30:31]
	v_fmamk_f32 v25, v130, 0xbbd083aa, v8
	v_fmamk_f32 v24, v134, 0xbd1d265f, v4
	v_med3_f32 v26, v25, s73, v203
	v_fmamk_f32 v25, v135, 0xbd1d265f, v5
	v_max_f32_e32 v24, 0xc1898193, v24
	v_max_f32_e32 v25, 0xc1898193, v25
	v_exp_f32_e32 v32, v24
	v_exp_f32_e32 v33, v25
	v_pk_mul_f32 v[20:21], v[20:21], v[28:29]
	v_fmamk_f32 v29, v132, 0xbbd083aa, v6
	v_fmamk_f32 v28, v136, 0xbd1d265f, v2
	v_med3_f32 v30, v29, s73, v203
	v_fmamk_f32 v29, v137, 0xbd1d265f, v3
	v_max_f32_e32 v28, 0xc1898193, v28
	v_max_f32_e32 v29, 0xc1898193, v29
	v_exp_f32_e32 v34, v28
	v_exp_f32_e32 v35, v29
	v_add_f32_e32 v32, 1.0, v32
	v_add_f32_e32 v33, 1.0, v33
	v_rcp_f32_e32 v32, v32
	v_rcp_f32_e32 v33, v33
	v_fmamk_f32 v27, v131, 0xbbd083aa, v9
	v_med3_f32 v27, v27, s73, v203
	v_add_f32_e32 v34, 1.0, v34
	v_add_f32_e32 v35, 1.0, v35
	v_pk_mul_f32 v[24:25], v[24:25], v[26:27]
	v_rcp_f32_e32 v34, v34
	v_rcp_f32_e32 v35, v35
	v_pk_mul_f32 v[24:25], v[24:25], v[32:33]
	s_nop 0
	s_nop 0
	v_fmamk_f32 v31, v133, 0xbbd083aa, v7
	v_cvt_pk_fp8_f32 v26, v20, v21
	v_cvt_pk_fp8_f32 v27, v24, v25
	v_med3_f32 v31, v31, s73, v203
	v_pk_mul_f32 v[20:21], v[28:29], v[30:31]
	v_cvt_pk_fp8_f32 v26, v22, v23 op_sel:[0,0,1]
	v_pk_mul_f32 v[20:21], v[20:21], v[34:35]
	v_fmamk_f32 v25, v124, 0xbbd083aa, v16
	v_cvt_pk_fp8_f32 v27, v20, v21 op_sel:[0,0,1]
; DI KParamsPtr kparams() { KParamsPtr p = (KParamsPtr)__builtin_amdgcn_kernarg_segment_ptr(); asm volatile("" : "+s"(p)); return p; }
; DI unsigned pk4_fp8(float a, float b, float c, float d) { int r = 0; r = __builtin_amdgcn_cvt_pk_fp8_f32(a, b, r, false); r = __builtin_amdgcn_cvt_pk_fp8_f32(c, d, r, true); return (unsigned)r; }
;     DI void operator()(EPI_ARGS) const {
;     ...
;         unsigned char* ACT = WSB(unsigned char, WS_ACT);
;         const int rbase = u.pm * 256 + wr * 64 + fr, cbase = u.pn * 128 + 32 * wc + 8 * fq;
;         const float* bb = kparams()->b_gu + ((size_t)li * NE + u.e) * 2048 + cbase;
;         constexpr float CG = -1.702f * LOG2E;
;         f32x4 bg[2], bu1[2];
; #pragma unroll
;         for (int n = 0; n < 2; ++n) { bg[n] = *(const f32x4*)(bb + 4 * n) * CG; bu1[n] = (*(const f32x4*)(bb + 1024 + 4 * n) + 1.0f) * (1.0f / CG); }
; #pragma unroll
;         for (int ai = 0; ai < 2; ++ai)
; #pragma unroll
;             for (int m = 0; m < 4; ++m) {
;                 const int row = rbase + 128 * ai + 16 * m;
;                 f32x4 o[2];
; #pragma unroll
;                 for (int n = 0; n < 2; ++n) {
;                     const f32x4 gg = acc[ai][0][m][n] * (W8_INV * CG) + bg[n], uu = acc[ai][1][m][n] * (W8_INV / CG) + bu1[n];
;                     f32x4 gv, u1, e;
; #pragma unroll
;                     for (int i = 0; i < 4; ++i) { gv[i] = fmaxf(gg[i], 7.0f * CG); u1[i] = __builtin_amdgcn_fmed3f(uu[i], 8.0f / CG, -6.0f / CG); }
; #pragma unroll
;                     for (int i = 0; i < 4; ++i) e[i] = __builtin_amdgcn_exp2f(gv[i]);
;                     const f32x4 d = e + 1.0f;
;                     f32x4 r;
; #pragma unroll
;                     for (int i = 0; i < 4; ++i) r[i] = __builtin_amdgcn_rcpf(d[i]);
;                     o[n] = gv * u1 * r;
;                 }
;                 u32x2 w; w.x = pk4_fp8(o[0][0], o[0][1], o[0][2], o[0][3]); w.y = pk4_fp8(o[1][0], o[1][1], o[1][2], o[1][3]);
;                 *(u32x2*)(ACT + (size_t)row * 1024 + cbase) = w;
;             }
	v_add_co_u32_e32 v20, vcc, s71, v10
	v_fmamk_f32 v24, v128, 0xbd1d265f, v12
	s_nop 0
	v_addc_co_u32_e32 v21, vcc, 0, v11, vcc
	global_store_dwordx2 v[20:21], v[26:27], off
	v_med3_f32 v26, v25, s73, v203
	v_fmamk_f32 v25, v129, 0xbd1d265f, v13
	v_max_f32_e32 v24, 0xc1898193, v24
	v_max_f32_e32 v25, 0xc1898193, v25
	v_exp_f32_e32 v30, v24
	v_exp_f32_e32 v31, v25
	v_fmamk_f32 v21, v122, 0xbbd083aa, v18
	v_fmamk_f32 v20, v126, 0xbd1d265f, v14
	v_med3_f32 v22, v21, s73, v203
	v_fmamk_f32 v21, v127, 0xbd1d265f, v15
	v_max_f32_e32 v20, 0xc1898193, v20
	v_max_f32_e32 v21, 0xc1898193, v21
	v_exp_f32_e32 v28, v20
	v_exp_f32_e32 v29, v21
	v_add_f32_e32 v30, 1.0, v30
	v_add_f32_e32 v31, 1.0, v31
	v_rcp_f32_e32 v30, v30
	v_rcp_f32_e32 v31, v31
	v_fmamk_f32 v27, v125, 0xbbd083aa, v17
	v_fmamk_f32 v23, v123, 0xbbd083aa, v19
	v_med3_f32 v27, v27, s73, v203
	v_med3_f32 v23, v23, s73, v203
	v_add_f32_e32 v28, 1.0, v28
	v_add_f32_e32 v29, 1.0, v29
	v_pk_mul_f32 v[24:25], v[24:25], v[26:27]
	v_rcp_f32_e32 v28, v28
	v_rcp_f32_e32 v29, v29
	v_pk_mul_f32 v[20:21], v[20:21], v[22:23]
	v_pk_mul_f32 v[22:23], v[24:25], v[30:31]
	v_fmamk_f32 v25, v114, 0xbbd083aa, v8
	v_fmamk_f32 v24, v118, 0xbd1d265f, v4
	v_med3_f32 v26, v25, s73, v203
	v_fmamk_f32 v25, v119, 0xbd1d265f, v5
	v_max_f32_e32 v24, 0xc1898193, v24
	v_max_f32_e32 v25, 0xc1898193, v25
	v_exp_f32_e32 v32, v24
	v_exp_f32_e32 v33, v25
	v_pk_mul_f32 v[20:21], v[20:21], v[28:29]
	v_fmamk_f32 v29, v116, 0xbbd083aa, v6
	v_fmamk_f32 v28, v120, 0xbd1d265f, v2
	v_med3_f32 v30, v29, s73, v203
	v_fmamk_f32 v29, v121, 0xbd1d265f, v3
	v_max_f32_e32 v28, 0xc1898193, v28
	v_max_f32_e32 v29, 0xc1898193, v29
	v_exp_f32_e32 v34, v28
	v_exp_f32_e32 v35, v29
	v_add_f32_e32 v32, 1.0, v32
	v_add_f32_e32 v33, 1.0, v33
	v_rcp_f32_e32 v32, v32
	v_rcp_f32_e32 v33, v33
	v_fmamk_f32 v27, v115, 0xbbd083aa, v9
	v_med3_f32 v27, v27, s73, v203
	v_add_f32_e32 v34, 1.0, v34
	v_add_f32_e32 v35, 1.0, v35
	v_pk_mul_f32 v[24:25], v[24:25], v[26:27]
	v_rcp_f32_e32 v34, v34
	v_rcp_f32_e32 v35, v35
	v_pk_mul_f32 v[24:25], v[24:25], v[32:33]
	s_nop 0
	s_nop 0
	v_fmamk_f32 v31, v117, 0xbbd083aa, v7
	v_cvt_pk_fp8_f32 v26, v20, v21
	v_cvt_pk_fp8_f32 v27, v24, v25
	v_med3_f32 v31, v31, s73, v203
	v_pk_mul_f32 v[20:21], v[28:29], v[30:31]
	v_cvt_pk_fp8_f32 v26, v22, v23 op_sel:[0,0,1]
	v_pk_mul_f32 v[20:21], v[20:21], v[34:35]
	v_fmamk_f32 v25, v108, 0xbbd083aa, v16
	v_cvt_pk_fp8_f32 v27, v20, v21 op_sel:[0,0,1]
	v_add_co_u32_e32 v20, vcc, s58, v10
	v_fmamk_f32 v24, v112, 0xbd1d265f, v12
	s_nop 0
	v_addc_co_u32_e32 v21, vcc, 0, v11, vcc
	global_store_dwordx2 v[20:21], v[26:27], off
	v_med3_f32 v26, v25, s73, v203
	v_fmamk_f32 v25, v113, 0xbd1d265f, v13
	v_max_f32_e32 v24, 0xc1898193, v24
	v_max_f32_e32 v25, 0xc1898193, v25
	v_exp_f32_e32 v30, v24
	v_exp_f32_e32 v31, v25
	v_fmamk_f32 v21, v106, 0xbbd083aa, v18
	v_fmamk_f32 v20, v110, 0xbd1d265f, v14
	v_med3_f32 v22, v21, s73, v203
	v_fmamk_f32 v21, v111, 0xbd1d265f, v15
	v_max_f32_e32 v20, 0xc1898193, v20
	v_max_f32_e32 v21, 0xc1898193, v21
	v_exp_f32_e32 v28, v20
	v_exp_f32_e32 v29, v21
	v_add_f32_e32 v30, 1.0, v30
	v_add_f32_e32 v31, 1.0, v31
	v_rcp_f32_e32 v30, v30
	v_rcp_f32_e32 v31, v31
	v_fmamk_f32 v27, v109, 0xbbd083aa, v17
	v_fmamk_f32 v23, v107, 0xbbd083aa, v19
	v_med3_f32 v27, v27, s73, v203
	v_med3_f32 v23, v23, s73, v203
	v_add_f32_e32 v28, 1.0, v28
	v_add_f32_e32 v29, 1.0, v29
	v_pk_mul_f32 v[24:25], v[24:25], v[26:27]
	v_rcp_f32_e32 v28, v28
	v_rcp_f32_e32 v29, v29
	v_pk_mul_f32 v[20:21], v[20:21], v[22:23]
	v_pk_mul_f32 v[22:23], v[24:25], v[30:31]
	v_fmamk_f32 v25, v98, 0xbbd083aa, v8
	v_fmamk_f32 v24, v102, 0xbd1d265f, v4
	v_med3_f32 v26, v25, s73, v203
	v_fmamk_f32 v25, v103, 0xbd1d265f, v5
	v_max_f32_e32 v24, 0xc1898193, v24
	v_max_f32_e32 v25, 0xc1898193, v25
	v_exp_f32_e32 v32, v24
	v_exp_f32_e32 v33, v25
	v_pk_mul_f32 v[20:21], v[20:21], v[28:29]
	v_fmamk_f32 v29, v100, 0xbbd083aa, v6
	v_fmamk_f32 v28, v104, 0xbd1d265f, v2
	v_med3_f32 v30, v29, s73, v203
	v_fmamk_f32 v29, v105, 0xbd1d265f, v3
	v_max_f32_e32 v28, 0xc1898193, v28
	v_max_f32_e32 v29, 0xc1898193, v29
	v_exp_f32_e32 v34, v28
	v_exp_f32_e32 v35, v29
	v_add_f32_e32 v32, 1.0, v32
	v_add_f32_e32 v33, 1.0, v33
	v_rcp_f32_e32 v32, v32
	v_rcp_f32_e32 v33, v33
	v_fmamk_f32 v27, v99, 0xbbd083aa, v9
	v_med3_f32 v27, v27, s73, v203
	v_add_f32_e32 v34, 1.0, v34
	v_add_f32_e32 v35, 1.0, v35
	v_pk_mul_f32 v[24:25], v[24:25], v[26:27]
	v_rcp_f32_e32 v34, v34
	v_rcp_f32_e32 v35, v35
	v_pk_mul_f32 v[24:25], v[24:25], v[32:33]
	s_nop 0
	s_nop 0
	v_fmamk_f32 v31, v101, 0xbbd083aa, v7
	v_cvt_pk_fp8_f32 v26, v20, v21
	v_cvt_pk_fp8_f32 v27, v24, v25
	v_med3_f32 v31, v31, s73, v203
	v_pk_mul_f32 v[20:21], v[28:29], v[30:31]
	v_cvt_pk_fp8_f32 v26, v22, v23 op_sel:[0,0,1]
	v_pk_mul_f32 v[20:21], v[20:21], v[34:35]
	v_fmamk_f32 v25, v92, 0xbbd083aa, v16
	v_cvt_pk_fp8_f32 v27, v20, v21 op_sel:[0,0,1]
	v_add_co_u32_e32 v20, vcc, s74, v10
	v_fmamk_f32 v24, v96, 0xbd1d265f, v12
	s_nop 0
; DI KParamsPtr kparams() { KParamsPtr p = (KParamsPtr)__builtin_amdgcn_kernarg_segment_ptr(); asm volatile("" : "+s"(p)); return p; }
; DI unsigned pk4_fp8(float a, float b, float c, float d) { int r = 0; r = __builtin_amdgcn_cvt_pk_fp8_f32(a, b, r, false); r = __builtin_amdgcn_cvt_pk_fp8_f32(c, d, r, true); return (unsigned)r; }
;     DI void operator()(EPI_ARGS) const {
;     ...
;         unsigned char* ACT = WSB(unsigned char, WS_ACT);
;         const int rbase = u.pm * 256 + wr * 64 + fr, cbase = u.pn * 128 + 32 * wc + 8 * fq;
;         const float* bb = kparams()->b_gu + ((size_t)li * NE + u.e) * 2048 + cbase;
;         constexpr float CG = -1.702f * LOG2E;
;         f32x4 bg[2], bu1[2];
; #pragma unroll
;         for (int n = 0; n < 2; ++n) { bg[n] = *(const f32x4*)(bb + 4 * n) * CG; bu1[n] = (*(const f32x4*)(bb + 1024 + 4 * n) + 1.0f) * (1.0f / CG); }
; #pragma unroll
;         for (int ai = 0; ai < 2; ++ai)
; #pragma unroll
;             for (int m = 0; m < 4; ++m) {
;                 const int row = rbase + 128 * ai + 16 * m;
;                 f32x4 o[2];
; #pragma unroll
;                 for (int n = 0; n < 2; ++n) {
;                     const f32x4 gg = acc[ai][0][m][n] * (W8_INV * CG) + bg[n], uu = acc[ai][1][m][n] * (W8_INV / CG) + bu1[n];
;                     f32x4 gv, u1, e;
; #pragma unroll
;                     for (int i = 0; i < 4; ++i) { gv[i] = fmaxf(gg[i], 7.0f * CG); u1[i] = __builtin_amdgcn_fmed3f(uu[i], 8.0f / CG, -6.0f / CG); }
; #pragma unroll
;                     for (int i = 0; i < 4; ++i) e[i] = __builtin_amdgcn_exp2f(gv[i]);
;                     const f32x4 d = e + 1.0f;
;                     f32x4 r;
; #pragma unroll
;                     for (int i = 0; i < 4; ++i) r[i] = __builtin_amdgcn_rcpf(d[i]);
;                     o[n] = gv * u1 * r;
;                 }
;                 u32x2 w; w.x = pk4_fp8(o[0][0], o[0][1], o[0][2], o[0][3]); w.y = pk4_fp8(o[1][0], o[1][1], o[1][2], o[1][3]);
;                 *(u32x2*)(ACT + (size_t)row * 1024 + cbase) = w;
;             }
	v_addc_co_u32_e32 v21, vcc, 0, v11, vcc
	global_store_dwordx2 v[20:21], v[26:27], off
	v_med3_f32 v26, v25, s73, v203
	v_fmamk_f32 v25, v97, 0xbd1d265f, v13
	v_max_f32_e32 v24, 0xc1898193, v24
	v_max_f32_e32 v25, 0xc1898193, v25
	v_exp_f32_e32 v30, v24
	v_exp_f32_e32 v31, v25
	v_fmamk_f32 v21, v90, 0xbbd083aa, v18
	v_fmamk_f32 v20, v94, 0xbd1d265f, v14
	v_med3_f32 v22, v21, s73, v203
	v_fmamk_f32 v21, v95, 0xbd1d265f, v15
	v_max_f32_e32 v20, 0xc1898193, v20
	v_max_f32_e32 v21, 0xc1898193, v21
	v_exp_f32_e32 v28, v20
	v_exp_f32_e32 v29, v21
	v_add_f32_e32 v30, 1.0, v30
	v_add_f32_e32 v31, 1.0, v31
	v_rcp_f32_e32 v30, v30
	v_rcp_f32_e32 v31, v31
	v_fmamk_f32 v27, v93, 0xbbd083aa, v17
	v_fmamk_f32 v23, v91, 0xbbd083aa, v19
	v_med3_f32 v27, v27, s73, v203
	v_med3_f32 v23, v23, s73, v203
	v_add_f32_e32 v28, 1.0, v28
	v_add_f32_e32 v29, 1.0, v29
	v_pk_mul_f32 v[24:25], v[24:25], v[26:27]
	v_rcp_f32_e32 v28, v28
	v_rcp_f32_e32 v29, v29
	v_pk_mul_f32 v[20:21], v[20:21], v[22:23]
	v_pk_mul_f32 v[22:23], v[24:25], v[30:31]
	v_fmamk_f32 v25, v82, 0xbbd083aa, v8
	v_fmamk_f32 v24, v86, 0xbd1d265f, v4
	v_med3_f32 v26, v25, s73, v203
	v_fmamk_f32 v25, v87, 0xbd1d265f, v5
	v_max_f32_e32 v24, 0xc1898193, v24
	v_max_f32_e32 v25, 0xc1898193, v25
	v_exp_f32_e32 v32, v24
	v_exp_f32_e32 v33, v25
	v_pk_mul_f32 v[20:21], v[20:21], v[28:29]
	v_fmamk_f32 v29, v84, 0xbbd083aa, v6
	v_fmamk_f32 v28, v88, 0xbd1d265f, v2
	v_med3_f32 v30, v29, s73, v203
	v_fmamk_f32 v29, v89, 0xbd1d265f, v3
	v_max_f32_e32 v28, 0xc1898193, v28
	v_max_f32_e32 v29, 0xc1898193, v29
	v_exp_f32_e32 v34, v28
	v_exp_f32_e32 v35, v29
	v_add_f32_e32 v32, 1.0, v32
	v_add_f32_e32 v33, 1.0, v33
	v_rcp_f32_e32 v32, v32
	v_rcp_f32_e32 v33, v33
	v_fmamk_f32 v27, v83, 0xbbd083aa, v9
	v_med3_f32 v27, v27, s73, v203
	v_add_f32_e32 v34, 1.0, v34
	v_add_f32_e32 v35, 1.0, v35
	v_pk_mul_f32 v[24:25], v[24:25], v[26:27]
	v_rcp_f32_e32 v34, v34
	v_rcp_f32_e32 v35, v35
	v_pk_mul_f32 v[24:25], v[24:25], v[32:33]
	s_nop 0
	s_nop 0
	v_fmamk_f32 v31, v85, 0xbbd083aa, v7
	v_cvt_pk_fp8_f32 v26, v20, v21
	v_cvt_pk_fp8_f32 v27, v24, v25
	v_med3_f32 v31, v31, s73, v203
	v_pk_mul_f32 v[20:21], v[28:29], v[30:31]
	v_cvt_pk_fp8_f32 v26, v22, v23 op_sel:[0,0,1]
	v_pk_mul_f32 v[20:21], v[20:21], v[34:35]
	v_fmamk_f32 v14, v78, 0xbd1d265f, v14
	v_cvt_pk_fp8_f32 v27, v20, v21 op_sel:[0,0,1]
	v_add_co_u32_e32 v20, vcc, s75, v10
	v_fmac_f32_e32 v15, 0xbd1d265f, v79
	v_fmamk_f32 v12, v80, 0xbd1d265f, v12
	v_fmamk_f32 v16, v76, 0xbbd083aa, v16
	v_fmac_f32_e32 v13, 0xbd1d265f, v81
	v_fmac_f32_e32 v17, 0xbbd083aa, v77
	v_fmamk_f32 v4, v70, 0xbd1d265f, v4
	v_fmac_f32_e32 v5, 0xbd1d265f, v71
	v_addc_co_u32_e32 v21, vcc, 0, v11, vcc
	v_max_f32_e32 v14, 0xc1898193, v14
	v_max_f32_e32 v15, 0xc1898193, v15
	v_max_f32_e32 v12, 0xc1898193, v12
	v_med3_f32 v16, v16, s73, v203
	v_max_f32_e32 v13, 0xc1898193, v13
	v_med3_f32 v17, v17, s73, v203
	v_max_f32_e32 v4, 0xc1898193, v4
	v_max_f32_e32 v5, 0xc1898193, v5
	global_store_dwordx2 v[20:21], v[26:27], off
	v_exp_f32_e32 v20, v14
	v_exp_f32_e32 v21, v15
	v_exp_f32_e32 v22, v12
	v_exp_f32_e32 v23, v13
	v_pk_mul_f32 v[12:13], v[12:13], v[16:17]
	v_exp_f32_e32 v16, v4
	v_exp_f32_e32 v17, v5
	v_fmamk_f32 v18, v74, 0xbbd083aa, v18
	v_fmac_f32_e32 v19, 0xbbd083aa, v75
	v_fmamk_f32 v2, v72, 0xbd1d265f, v2
	v_fmac_f32_e32 v3, 0xbd1d265f, v73
	v_med3_f32 v18, v18, s73, v203
	v_med3_f32 v19, v19, s73, v203
	v_max_f32_e32 v2, 0xc1898193, v2
	v_max_f32_e32 v3, 0xc1898193, v3
	v_add_f32_e32 v20, 1.0, v20
	v_add_f32_e32 v21, 1.0, v21
	v_pk_mul_f32 v[14:15], v[14:15], v[18:19]
	v_exp_f32_e32 v18, v2
	v_exp_f32_e32 v19, v3
	v_add_f32_e32 v16, 1.0, v16
	v_add_f32_e32 v17, 1.0, v17
	v_rcp_f32_e32 v20, v20
	v_rcp_f32_e32 v21, v21
	v_rcp_f32_e32 v16, v16
	v_rcp_f32_e32 v17, v17
	v_fmamk_f32 v8, v66, 0xbbd083aa, v8
	v_fmac_f32_e32 v9, 0xbbd083aa, v67
	v_med3_f32 v8, v8, s73, v203
	v_med3_f32 v9, v9, s73, v203
	v_add_f32_e32 v22, 1.0, v22
	v_add_f32_e32 v23, 1.0, v23
	v_add_f32_e32 v18, 1.0, v18
	v_add_f32_e32 v19, 1.0, v19
	v_pk_mul_f32 v[4:5], v[4:5], v[8:9]
	v_rcp_f32_e32 v22, v22
	v_rcp_f32_e32 v23, v23
	v_pk_mul_f32 v[14:15], v[14:15], v[20:21]
	v_rcp_f32_e32 v18, v18
	v_rcp_f32_e32 v19, v19
	v_pk_mul_f32 v[4:5], v[4:5], v[16:17]
	s_nop 0
	s_nop 0
	v_fmamk_f32 v6, v68, 0xbbd083aa, v6
	v_fmac_f32_e32 v7, 0xbbd083aa, v69
	v_cvt_pk_fp8_f32 v8, v14, v15
	v_cvt_pk_fp8_f32 v9, v4, v5
	v_med3_f32 v6, v6, s73, v203
	v_med3_f32 v7, v7, s73, v203
	v_pk_mul_f32 v[2:3], v[2:3], v[6:7]
	v_pk_mul_f32 v[12:13], v[12:13], v[22:23]
	v_pk_mul_f32 v[2:3], v[2:3], v[18:19]
	v_cvt_pk_fp8_f32 v8, v12, v13 op_sel:[0,0,1]
	v_cvt_pk_fp8_f32 v9, v2, v3 op_sel:[0,0,1]
	v_add_co_u32_e32 v2, vcc, 0x2c000, v10
	s_nop 1
	v_addc_co_u32_e32 v3, vcc, 0, v11, vcc
	s_andn2_b64 vcc, exec, s[42:43]
	s_mov_b64 s[42:43], -1
	global_store_dwordx2 v[2:3], v[8:9], off
	s_cbranch_vccnz .LBB0_1333
	s_andn2_b64 vcc, exec, s[16:17]
	s_cbranch_vccnz .LBB0_1332
	s_barrier
	s_branch .LBB0_1332

; DI KParamsPtr kparams() { KParamsPtr p = (KParamsPtr)__builtin_amdgcn_kernarg_segment_ptr(); asm volatile("" : "+s"(p)); return p; }
; DI unsigned pk4_fp8(float a, float b, float c, float d) { int r = 0; r = __builtin_amdgcn_cvt_pk_fp8_f32(a, b, r, false); r = __builtin_amdgcn_cvt_pk_fp8_f32(c, d, r, true); return (unsigned)r; }
; DI float clamp448(float x) { return __builtin_amdgcn_fmed3f(x, -448.0f, 448.0f); }
;     DI void operator()(EPI_ARGS) const {
;     ...
;         unsigned char* YB = WSB(unsigned char, WS_XP) + (size_t)MAXMT * 256 * 1024;
;         const int rbase = u.pm * 256 + wr * 64 + fr, cbase = u.pn * 256 + 64 * wc + 16 * fq;
;         const float* bb = kparams()->b_dn + ((size_t)li * NE + u.e) * 1024 + cbase;
;         f32x4 bv[2][2];
; #pragma unroll
;         for (int bj = 0; bj < 2; ++bj)
; #pragma unroll
;             for (int n = 0; n < 2; ++n) bv[bj][n] = *(const f32x4*)(bb + 8 * bj + 4 * n);
; #pragma unroll
;         for (int ai = 0; ai < 2; ++ai)
; #pragma unroll
;             for (int m = 0; m < 4; ++m) {
;                 const int row = rbase + 128 * ai + 16 * m;
;                 u32x4 w;
; #pragma unroll
;                 for (int bj = 0; bj < 2; ++bj)
; #pragma unroll
;                     for (int n = 0; n < 2; ++n) { const f32x4 a = acc[ai][bj][m][n] * W8_INV + bv[bj][n]; w[2 * bj + n] = pk4_fp8(clamp448(a[0]), clamp448(a[1]), clamp448(a[2]), clamp448(a[3])); }
;                 *(u32x4*)(YB + (size_t)row * 1024 + cbase) = w;
;             }
.LBB0_1453:
	v_mov_b32_e32 v157, v1
	v_mov_b32_e32 v130, v152
	s_mov_b64 s[24:25], s[0:1]
	s_load_dwordx2 s[24:25], s[24:25], 0xc8
	s_lshl_b32 s67, s23, 8
	s_lshl_b32 s23, s66, 8
	s_or_b32 s23, s23, s52
	v_lshl_add_u32 v150, v130, 4, s23
	s_ashr_i32 s23, s22, 31
	s_lshl_b64 s[22:23], s[22:23], 12
	s_waitcnt lgkmcnt(0)
	s_add_u32 s22, s24, s22
	s_addc_u32 s23, s25, s23
	v_ashrrev_i32_e32 v151, 31, v150
	v_lshl_add_u64 v[130:131], v[150:151], 2, s[22:23]
	global_load_dwordx4 v[142:145], v[130:131], off
	global_load_dwordx4 v[138:141], v[130:131], off offset:16
	global_load_dwordx4 v[134:137], v[130:131], off offset:32
	s_nop 0
	global_load_dwordx4 v[130:133], v[130:131], off offset:48
	s_nop 0
	s_nop 0
	s_nop 0
	s_nop 0
	s_add_i32 s67, s67, s42
	v_add_u32_e32 v166, s67, v157
	v_ashrrev_i32_e32 v167, 31, v166
	v_lshl_add_u64 v[150:151], s[16:17], 0, v[150:151]
	v_lshlrev_b64 v[166:167], 10, v[166:167]
	v_lshl_add_u64 v[150:151], v[150:151], 0, v[166:167]
	v_mov_b32_e32 v158, 0
	v_mov_b32_e32 v159, 0
	v_mov_b32_e32 v160, 0
	v_mov_b32_e32 v161, 0
	s_waitcnt vmcnt(0)
	v_pk_fma_f32 v[118:119], v[118:119], s[18:19], v[142:143] op_sel_hi:[1,0,1]
	v_pk_fma_f32 v[114:115], v[114:115], s[18:19], v[138:139] op_sel_hi:[1,0,1]
	v_pk_fma_f32 v[102:103], v[102:103], s[18:19], v[134:135] op_sel_hi:[1,0,1]
	v_pk_fma_f32 v[98:99], v[98:99], s[18:19], v[130:131] op_sel_hi:[1,0,1]
	v_med3_f32 v118, v118, s56, v156
	v_med3_f32 v119, v119, s56, v156
	v_med3_f32 v114, v114, s56, v156
	v_med3_f32 v115, v115, s56, v156
	v_med3_f32 v102, v102, s56, v156
	v_med3_f32 v103, v103, s56, v156
	v_med3_f32 v98, v98, s56, v156
	v_med3_f32 v99, v99, s56, v156
	v_cvt_pk_fp8_f32 v162, v118, v119
	v_cvt_pk_fp8_f32 v163, v114, v115
	v_cvt_pk_fp8_f32 v164, v102, v103
	v_cvt_pk_fp8_f32 v165, v98, v99
	v_pk_fma_f32 v[120:121], v[120:121], s[18:19], v[144:145] op_sel_hi:[1,0,1]
	v_pk_fma_f32 v[116:117], v[116:117], s[18:19], v[140:141] op_sel_hi:[1,0,1]
	v_pk_fma_f32 v[104:105], v[104:105], s[18:19], v[136:137] op_sel_hi:[1,0,1]
	v_pk_fma_f32 v[100:101], v[100:101], s[18:19], v[132:133] op_sel_hi:[1,0,1]
	v_med3_f32 v120, v120, s56, v156
	v_med3_f32 v121, v121, s56, v156
	v_med3_f32 v116, v116, s56, v156
	v_med3_f32 v117, v117, s56, v156
	v_med3_f32 v104, v104, s56, v156
	v_med3_f32 v105, v105, s56, v156
	v_med3_f32 v100, v100, s56, v156
	v_med3_f32 v101, v101, s56, v156
	v_cvt_pk_fp8_f32 v162, v120, v121 op_sel:[0,0,1]
	v_cvt_pk_fp8_f32 v163, v116, v117 op_sel:[0,0,1]
	v_cvt_pk_fp8_f32 v164, v104, v105 op_sel:[0,0,1]
	v_cvt_pk_fp8_f32 v165, v100, v101 op_sel:[0,0,1]
	v_add_co_u32_e32 v98, vcc, s41, v150
	v_pk_fma_f32 v[94:95], v[94:95], s[18:19], v[142:143] op_sel_hi:[1,0,1]
	s_nop 0
	v_addc_co_u32_e32 v99, vcc, 0, v151, vcc
	global_store_dwordx4 v[98:99], v[162:165], off
	v_med3_f32 v98, v94, s56, v156
	v_med3_f32 v95, v95, s56, v156
	s_nop 0
	v_cvt_pk_fp8_f32 v94, v98, v95
	v_pk_fma_f32 v[96:97], v[96:97], s[18:19], v[144:145] op_sel_hi:[1,0,1]
	v_pk_fma_f32 v[90:91], v[90:91], s[18:19], v[138:139] op_sel_hi:[1,0,1]
	v_med3_f32 v95, v96, s56, v156
	v_med3_f32 v96, v97, s56, v156
	v_pk_fma_f32 v[86:87], v[86:87], s[18:19], v[134:135] op_sel_hi:[1,0,1]
	v_pk_fma_f32 v[78:79], v[78:79], s[18:19], v[130:131] op_sel_hi:[1,0,1]
	v_cvt_pk_fp8_f32 v94, v95, v96 op_sel:[0,0,1]
	v_med3_f32 v90, v90, s56, v156
	v_med3_f32 v91, v91, s56, v156
	s_nop 0
	v_med3_f32 v86, v86, s56, v156
	v_med3_f32 v87, v87, s56, v156
	s_nop 0
	v_med3_f32 v78, v78, s56, v156
	v_med3_f32 v79, v79, s56, v156
	s_nop 0
	v_cvt_pk_fp8_f32 v95, v90, v91
	v_cvt_pk_fp8_f32 v96, v86, v87
	v_cvt_pk_fp8_f32 v97, v78, v79
	v_pk_fma_f32 v[90:91], v[92:93], s[18:19], v[140:141] op_sel_hi:[1,0,1]
	v_pk_fma_f32 v[86:87], v[88:89], s[18:19], v[136:137] op_sel_hi:[1,0,1]
	v_pk_fma_f32 v[78:79], v[80:81], s[18:19], v[132:133] op_sel_hi:[1,0,1]
	v_med3_f32 v90, v90, s56, v156
	v_med3_f32 v91, v91, s56, v156
	v_med3_f32 v86, v86, s56, v156
	v_med3_f32 v87, v87, s56, v156
	v_med3_f32 v78, v78, s56, v156
	v_med3_f32 v79, v79, s56, v156
	v_cvt_pk_fp8_f32 v95, v90, v91 op_sel:[0,0,1]
	v_cvt_pk_fp8_f32 v96, v86, v87 op_sel:[0,0,1]
	v_cvt_pk_fp8_f32 v97, v78, v79 op_sel:[0,0,1]
	v_add_co_u32_e32 v78, vcc, s51, v150
	v_pk_fma_f32 v[74:75], v[74:75], s[18:19], v[138:139] op_sel_hi:[1,0,1]
	s_nop 0
	v_addc_co_u32_e32 v79, vcc, 0, v151, vcc
	global_store_dwordx4 v[78:79], v[94:97], off
	v_pk_fma_f32 v[78:79], v[82:83], s[18:19], v[142:143] op_sel_hi:[1,0,1]
	v_pk_fma_f32 v[70:71], v[70:71], s[18:19], v[134:135] op_sel_hi:[1,0,1]
	v_med3_f32 v80, v78, s56, v156
	v_med3_f32 v79, v79, s56, v156
	s_nop 0
	v_cvt_pk_fp8_f32 v78, v80, v79
	v_pk_fma_f32 v[80:81], v[84:85], s[18:19], v[144:145] op_sel_hi:[1,0,1]
	v_pk_fma_f32 v[66:67], v[66:67], s[18:19], v[130:131] op_sel_hi:[1,0,1]
	v_med3_f32 v79, v80, s56, v156
	v_med3_f32 v80, v81, s56, v156
	v_cvt_pk_fp8_f32 v78, v79, v80 op_sel:[0,0,1]
	v_med3_f32 v74, v74, s56, v156
	v_med3_f32 v75, v75, s56, v156
	s_nop 0
	v_med3_f32 v70, v70, s56, v156
	v_med3_f32 v71, v71, s56, v156
	s_nop 0
	v_med3_f32 v66, v66, s56, v156
	v_med3_f32 v67, v67, s56, v156
	s_nop 0
	v_cvt_pk_fp8_f32 v79, v74, v75
	v_cvt_pk_fp8_f32 v80, v70, v71
	v_cvt_pk_fp8_f32 v81, v66, v67
	v_pk_fma_f32 v[74:75], v[76:77], s[18:19], v[140:141] op_sel_hi:[1,0,1]
	v_pk_fma_f32 v[70:71], v[72:73], s[18:19], v[136:137] op_sel_hi:[1,0,1]
	v_pk_fma_f32 v[66:67], v[68:69], s[18:19], v[132:133] op_sel_hi:[1,0,1]
	v_med3_f32 v74, v74, s56, v156
	v_med3_f32 v75, v75, s56, v156
	v_med3_f32 v70, v70, s56, v156
	v_med3_f32 v71, v71, s56, v156
	v_med3_f32 v66, v66, s56, v156
	v_med3_f32 v67, v67, s56, v156
	v_cvt_pk_fp8_f32 v79, v74, v75 op_sel:[0,0,1]
; DI KParamsPtr kparams() { KParamsPtr p = (KParamsPtr)__builtin_amdgcn_kernarg_segment_ptr(); asm volatile("" : "+s"(p)); return p; }
; DI unsigned pk4_fp8(float a, float b, float c, float d) { int r = 0; r = __builtin_amdgcn_cvt_pk_fp8_f32(a, b, r, false); r = __builtin_amdgcn_cvt_pk_fp8_f32(c, d, r, true); return (unsigned)r; }
; DI float clamp448(float x) { return __builtin_amdgcn_fmed3f(x, -448.0f, 448.0f); }
;     DI void operator()(EPI_ARGS) const {
;     ...
;         unsigned char* YB = WSB(unsigned char, WS_XP) + (size_t)MAXMT * 256 * 1024;
;         const int rbase = u.pm * 256 + wr * 64 + fr, cbase = u.pn * 256 + 64 * wc + 16 * fq;
;         const float* bb = kparams()->b_dn + ((size_t)li * NE + u.e) * 1024 + cbase;
;         f32x4 bv[2][2];
; #pragma unroll
;         for (int bj = 0; bj < 2; ++bj)
; #pragma unroll
;             for (int n = 0; n < 2; ++n) bv[bj][n] = *(const f32x4*)(bb + 8 * bj + 4 * n);
; #pragma unroll
;         for (int ai = 0; ai < 2; ++ai)
; #pragma unroll
;             for (int m = 0; m < 4; ++m) {
;                 const int row = rbase + 128 * ai + 16 * m;
;                 u32x4 w;
; #pragma unroll
;                 for (int bj = 0; bj < 2; ++bj)
; #pragma unroll
;                     for (int n = 0; n < 2; ++n) { const f32x4 a = acc[ai][bj][m][n] * W8_INV + bv[bj][n]; w[2 * bj + n] = pk4_fp8(clamp448(a[0]), clamp448(a[1]), clamp448(a[2]), clamp448(a[3])); }
;                 *(u32x4*)(YB + (size_t)row * 1024 + cbase) = w;
;             }
	v_cvt_pk_fp8_f32 v80, v70, v71 op_sel:[0,0,1]
	v_cvt_pk_fp8_f32 v81, v66, v67 op_sel:[0,0,1]
	v_add_co_u32_e32 v66, vcc, s55, v150
	v_pk_fma_f32 v[62:63], v[62:63], s[18:19], v[142:143] op_sel_hi:[1,0,1]
	s_nop 0
	v_addc_co_u32_e32 v67, vcc, 0, v151, vcc
	global_store_dwordx4 v[66:67], v[78:81], off
	v_med3_f32 v66, v62, s56, v156
	v_med3_f32 v63, v63, s56, v156
	s_nop 0
	v_cvt_pk_fp8_f32 v62, v66, v63
	v_pk_fma_f32 v[64:65], v[64:65], s[18:19], v[144:145] op_sel_hi:[1,0,1]
	v_pk_fma_f32 v[58:59], v[58:59], s[18:19], v[138:139] op_sel_hi:[1,0,1]
	v_med3_f32 v63, v64, s56, v156
	v_med3_f32 v64, v65, s56, v156
	v_pk_fma_f32 v[54:55], v[54:55], s[18:19], v[134:135] op_sel_hi:[1,0,1]
	v_pk_fma_f32 v[46:47], v[46:47], s[18:19], v[130:131] op_sel_hi:[1,0,1]
	v_cvt_pk_fp8_f32 v62, v63, v64 op_sel:[0,0,1]
	v_med3_f32 v58, v58, s56, v156
	v_med3_f32 v59, v59, s56, v156
	s_nop 0
	v_med3_f32 v54, v54, s56, v156
	v_med3_f32 v55, v55, s56, v156
	s_nop 0
	v_med3_f32 v46, v46, s56, v156
	v_med3_f32 v47, v47, s56, v156
	s_nop 0
	v_cvt_pk_fp8_f32 v63, v58, v59
	v_cvt_pk_fp8_f32 v64, v54, v55
	v_cvt_pk_fp8_f32 v65, v46, v47
	v_pk_fma_f32 v[58:59], v[60:61], s[18:19], v[140:141] op_sel_hi:[1,0,1]
	v_pk_fma_f32 v[54:55], v[56:57], s[18:19], v[136:137] op_sel_hi:[1,0,1]
	v_pk_fma_f32 v[46:47], v[48:49], s[18:19], v[132:133] op_sel_hi:[1,0,1]
	v_med3_f32 v58, v58, s56, v156
	v_med3_f32 v59, v59, s56, v156
	v_med3_f32 v54, v54, s56, v156
	v_med3_f32 v55, v55, s56, v156
	v_med3_f32 v46, v46, s56, v156
	v_med3_f32 v47, v47, s56, v156
	v_cvt_pk_fp8_f32 v63, v58, v59 op_sel:[0,0,1]
	v_cvt_pk_fp8_f32 v64, v54, v55 op_sel:[0,0,1]
	v_cvt_pk_fp8_f32 v65, v46, v47 op_sel:[0,0,1]
	v_add_co_u32_e32 v46, vcc, s54, v150
	v_pk_fma_f32 v[42:43], v[42:43], s[18:19], v[138:139] op_sel_hi:[1,0,1]
	s_nop 0
	v_addc_co_u32_e32 v47, vcc, 0, v151, vcc
	global_store_dwordx4 v[46:47], v[62:65], off
	v_pk_fma_f32 v[46:47], v[50:51], s[18:19], v[142:143] op_sel_hi:[1,0,1]
	v_pk_fma_f32 v[38:39], v[38:39], s[18:19], v[134:135] op_sel_hi:[1,0,1]
	v_med3_f32 v48, v46, s56, v156
	v_med3_f32 v47, v47, s56, v156
	s_nop 0
	v_cvt_pk_fp8_f32 v46, v48, v47
	v_pk_fma_f32 v[48:49], v[52:53], s[18:19], v[144:145] op_sel_hi:[1,0,1]
	v_pk_fma_f32 v[30:31], v[30:31], s[18:19], v[130:131] op_sel_hi:[1,0,1]
	v_med3_f32 v47, v48, s56, v156
	v_med3_f32 v48, v49, s56, v156
	v_cvt_pk_fp8_f32 v46, v47, v48 op_sel:[0,0,1]
	v_med3_f32 v42, v42, s56, v156
	v_med3_f32 v43, v43, s56, v156
	s_nop 0
	v_med3_f32 v38, v38, s56, v156
	v_med3_f32 v39, v39, s56, v156
	s_nop 0
	v_med3_f32 v30, v30, s56, v156
	v_med3_f32 v31, v31, s56, v156
	s_nop 0
	v_cvt_pk_fp8_f32 v47, v42, v43
	v_cvt_pk_fp8_f32 v48, v38, v39
	v_cvt_pk_fp8_f32 v49, v30, v31
	v_pk_fma_f32 v[42:43], v[44:45], s[18:19], v[140:141] op_sel_hi:[1,0,1]
	v_pk_fma_f32 v[38:39], v[40:41], s[18:19], v[136:137] op_sel_hi:[1,0,1]
	v_pk_fma_f32 v[30:31], v[32:33], s[18:19], v[132:133] op_sel_hi:[1,0,1]
	v_med3_f32 v42, v42, s56, v156
	v_med3_f32 v43, v43, s56, v156
	v_med3_f32 v38, v38, s56, v156
	v_med3_f32 v39, v39, s56, v156
	v_med3_f32 v30, v30, s56, v156
	v_med3_f32 v31, v31, s56, v156
	v_cvt_pk_fp8_f32 v47, v42, v43 op_sel:[0,0,1]
	v_cvt_pk_fp8_f32 v48, v38, v39 op_sel:[0,0,1]
	v_cvt_pk_fp8_f32 v49, v30, v31 op_sel:[0,0,1]
	v_add_co_u32_e32 v30, vcc, s57, v150
	v_pk_fma_f32 v[26:27], v[26:27], s[18:19], v[138:139] op_sel_hi:[1,0,1]
	s_nop 0
	v_addc_co_u32_e32 v31, vcc, 0, v151, vcc
	global_store_dwordx4 v[30:31], v[46:49], off
	v_pk_fma_f32 v[30:31], v[34:35], s[18:19], v[142:143] op_sel_hi:[1,0,1]
	v_pk_fma_f32 v[22:23], v[22:23], s[18:19], v[134:135] op_sel_hi:[1,0,1]
	v_med3_f32 v32, v30, s56, v156
	v_med3_f32 v31, v31, s56, v156
	s_nop 0
	v_cvt_pk_fp8_f32 v30, v32, v31
	v_pk_fma_f32 v[32:33], v[36:37], s[18:19], v[144:145] op_sel_hi:[1,0,1]
	v_pk_fma_f32 v[14:15], v[14:15], s[18:19], v[130:131] op_sel_hi:[1,0,1]
	v_med3_f32 v31, v32, s56, v156
	v_med3_f32 v32, v33, s56, v156
	v_cvt_pk_fp8_f32 v30, v31, v32 op_sel:[0,0,1]
	v_med3_f32 v26, v26, s56, v156
	v_med3_f32 v27, v27, s56, v156
	s_nop 0
	v_med3_f32 v22, v22, s56, v156
	v_med3_f32 v23, v23, s56, v156
	s_nop 0
; DI KParamsPtr kparams() { KParamsPtr p = (KParamsPtr)__builtin_amdgcn_kernarg_segment_ptr(); asm volatile("" : "+s"(p)); return p; }
; DI unsigned pk4_fp8(float a, float b, float c, float d) { int r = 0; r = __builtin_amdgcn_cvt_pk_fp8_f32(a, b, r, false); r = __builtin_amdgcn_cvt_pk_fp8_f32(c, d, r, true); return (unsigned)r; }
; DI float clamp448(float x) { return __builtin_amdgcn_fmed3f(x, -448.0f, 448.0f); }
;     DI void operator()(EPI_ARGS) const {
;     ...
;         unsigned char* YB = WSB(unsigned char, WS_XP) + (size_t)MAXMT * 256 * 1024;
;         const int rbase = u.pm * 256 + wr * 64 + fr, cbase = u.pn * 256 + 64 * wc + 16 * fq;
;         const float* bb = kparams()->b_dn + ((size_t)li * NE + u.e) * 1024 + cbase;
;         f32x4 bv[2][2];
; #pragma unroll
;         for (int bj = 0; bj < 2; ++bj)
; #pragma unroll
;             for (int n = 0; n < 2; ++n) bv[bj][n] = *(const f32x4*)(bb + 8 * bj + 4 * n);
; #pragma unroll
;         for (int ai = 0; ai < 2; ++ai)
; #pragma unroll
;             for (int m = 0; m < 4; ++m) {
;                 const int row = rbase + 128 * ai + 16 * m;
;                 u32x4 w;
; #pragma unroll
;                 for (int bj = 0; bj < 2; ++bj)
; #pragma unroll
;                     for (int n = 0; n < 2; ++n) { const f32x4 a = acc[ai][bj][m][n] * W8_INV + bv[bj][n]; w[2 * bj + n] = pk4_fp8(clamp448(a[0]), clamp448(a[1]), clamp448(a[2]), clamp448(a[3])); }
;                 *(u32x4*)(YB + (size_t)row * 1024 + cbase) = w;
;             }
	v_med3_f32 v14, v14, s56, v156
	v_med3_f32 v15, v15, s56, v156
	s_nop 0
	v_cvt_pk_fp8_f32 v31, v26, v27
	v_cvt_pk_fp8_f32 v32, v22, v23
	v_cvt_pk_fp8_f32 v33, v14, v15
	v_pk_fma_f32 v[26:27], v[28:29], s[18:19], v[140:141] op_sel_hi:[1,0,1]
	v_pk_fma_f32 v[22:23], v[24:25], s[18:19], v[136:137] op_sel_hi:[1,0,1]
	v_pk_fma_f32 v[14:15], v[16:17], s[18:19], v[132:133] op_sel_hi:[1,0,1]
	v_med3_f32 v26, v26, s56, v156
	v_med3_f32 v27, v27, s56, v156
	v_med3_f32 v22, v22, s56, v156
	v_med3_f32 v23, v23, s56, v156
	v_med3_f32 v14, v14, s56, v156
	v_med3_f32 v15, v15, s56, v156
	v_cvt_pk_fp8_f32 v31, v26, v27 op_sel:[0,0,1]
	v_cvt_pk_fp8_f32 v32, v22, v23 op_sel:[0,0,1]
	v_cvt_pk_fp8_f32 v33, v14, v15 op_sel:[0,0,1]
	v_add_co_u32_e32 v14, vcc, s58, v150
	v_pk_fma_f32 v[126:127], v[126:127], s[18:19], v[142:143] op_sel_hi:[1,0,1]
	s_nop 0
	v_addc_co_u32_e32 v15, vcc, 0, v151, vcc
	global_store_dwordx4 v[14:15], v[30:33], off
	v_pk_fma_f32 v[14:15], v[18:19], s[18:19], v[142:143] op_sel_hi:[1,0,1]
	v_pk_fma_f32 v[122:123], v[122:123], s[18:19], v[138:139] op_sel_hi:[1,0,1]
	v_med3_f32 v16, v14, s56, v156
	v_med3_f32 v15, v15, s56, v156
	s_nop 0
	v_cvt_pk_fp8_f32 v14, v16, v15
	v_pk_fma_f32 v[16:17], v[20:21], s[18:19], v[144:145] op_sel_hi:[1,0,1]
	v_pk_fma_f32 v[110:111], v[110:111], s[18:19], v[134:135] op_sel_hi:[1,0,1]
	v_pk_fma_f32 v[106:107], v[106:107], s[18:19], v[130:131] op_sel_hi:[1,0,1]
	v_med3_f32 v15, v16, s56, v156
	v_med3_f32 v16, v17, s56, v156
	v_pk_fma_f32 v[10:11], v[10:11], s[18:19], v[138:139] op_sel_hi:[1,0,1]
	v_pk_fma_f32 v[6:7], v[6:7], s[18:19], v[134:135] op_sel_hi:[1,0,1]
	v_pk_fma_f32 v[2:3], v[2:3], s[18:19], v[130:131] op_sel_hi:[1,0,1]
	v_med3_f32 v126, v126, s56, v156
	v_med3_f32 v127, v127, s56, v156
	v_med3_f32 v122, v122, s56, v156
	v_med3_f32 v123, v123, s56, v156
	v_med3_f32 v110, v110, s56, v156
	v_med3_f32 v111, v111, s56, v156
	v_med3_f32 v106, v106, s56, v156
	v_med3_f32 v107, v107, s56, v156
	v_cvt_pk_fp8_f32 v14, v15, v16 op_sel:[0,0,1]
	v_med3_f32 v10, v10, s56, v156
	v_med3_f32 v11, v11, s56, v156
	s_nop 0
	v_med3_f32 v6, v6, s56, v156
	v_med3_f32 v7, v7, s56, v156
	s_nop 0
	v_med3_f32 v2, v2, s56, v156
	v_med3_f32 v3, v3, s56, v156
	s_nop 0
	v_cvt_pk_fp8_f32 v158, v126, v127
	v_cvt_pk_fp8_f32 v159, v122, v123
	v_cvt_pk_fp8_f32 v160, v110, v111
	v_cvt_pk_fp8_f32 v161, v106, v107
	v_cvt_pk_fp8_f32 v15, v10, v11
	v_cvt_pk_fp8_f32 v16, v6, v7
	v_cvt_pk_fp8_f32 v17, v2, v3
	v_pk_fma_f32 v[128:129], v[128:129], s[18:19], v[144:145] op_sel_hi:[1,0,1]
	v_pk_fma_f32 v[124:125], v[124:125], s[18:19], v[140:141] op_sel_hi:[1,0,1]
	v_pk_fma_f32 v[112:113], v[112:113], s[18:19], v[136:137] op_sel_hi:[1,0,1]
	v_pk_fma_f32 v[108:109], v[108:109], s[18:19], v[132:133] op_sel_hi:[1,0,1]
	v_pk_fma_f32 v[10:11], v[12:13], s[18:19], v[140:141] op_sel_hi:[1,0,1]
	v_pk_fma_f32 v[6:7], v[8:9], s[18:19], v[136:137] op_sel_hi:[1,0,1]
	v_pk_fma_f32 v[2:3], v[4:5], s[18:19], v[132:133] op_sel_hi:[1,0,1]
	v_med3_f32 v128, v128, s56, v156
	v_med3_f32 v129, v129, s56, v156
	v_med3_f32 v124, v124, s56, v156
	v_med3_f32 v125, v125, s56, v156
	v_med3_f32 v112, v112, s56, v156
	v_med3_f32 v113, v113, s56, v156
	v_med3_f32 v108, v108, s56, v156
	v_med3_f32 v109, v109, s56, v156
	v_med3_f32 v10, v10, s56, v156
	v_med3_f32 v11, v11, s56, v156
	v_med3_f32 v6, v6, s56, v156
	v_med3_f32 v7, v7, s56, v156
	v_med3_f32 v2, v2, s56, v156
	v_med3_f32 v3, v3, s56, v156
	v_cvt_pk_fp8_f32 v158, v128, v129 op_sel:[0,0,1]
	v_cvt_pk_fp8_f32 v159, v124, v125 op_sel:[0,0,1]
	v_cvt_pk_fp8_f32 v160, v112, v113 op_sel:[0,0,1]
	v_cvt_pk_fp8_f32 v161, v108, v109 op_sel:[0,0,1]
	v_cvt_pk_fp8_f32 v15, v10, v11 op_sel:[0,0,1]
	v_cvt_pk_fp8_f32 v16, v6, v7 op_sel:[0,0,1]
	v_cvt_pk_fp8_f32 v17, v2, v3 op_sel:[0,0,1]
	v_add_co_u32_e32 v2, vcc, 0x2c000, v150
	global_store_dwordx4 v[150:151], v[158:161], off
	s_nop 0
	v_addc_co_u32_e32 v3, vcc, 0, v151, vcc
	s_andn2_b64 vcc, exec, s[20:21]
	s_mov_b64 s[20:21], -1
	global_store_dwordx4 v[2:3], v[14:17], off
	s_cbranch_vccnz .LBB0_1440
	s_andn2_b64 vcc, exec, s[12:13]
	s_cbranch_vccnz .LBB0_1439
	s_barrier
	s_branch .LBB0_1439

; DI void phase_combine(const Params& P, int li, const bf16_t* X1, bf16_t* X2, const unsigned char* YB, const LAS int* tab, const int* tok_e, const int* tok_pos, const float* tok_gate, const float* modl, const float* modn, unsigned char* H, int G) {
;     ...
;     for (int tok = gw; tok < N; tok += 2 * S) {
;         u32x4 xa[2][2]; u32x2 ya[2][4][2];
; #pragma unroll
;         for (int q = 0; q < 2; ++q) { int t = tok + q * S; t = t < N ? t : tok;
;             xa[q][0] = *(const u32x4*)(X1 + (size_t)t * 1024 + 8 * lane); xa[q][1] = *(const u32x4*)(X1 + (size_t)t * 1024 + 512 + 8 * lane);
; #pragma unroll
;             for (int k = 0; k < 4; ++k) { ya[q][k][0] = *(const u32x2*)(YB + (size_t)sl[q][k] * 1024 + 8 * lane); ya[q][k][1] = *(const u32x2*)(YB + (size_t)sl[q][k] * 1024 + 512 + 8 * lane); } }
;         float gc[2][4];
; #pragma unroll
;         for (int q = 0; q < 2; ++q)
; #pragma unroll
.LBB0_1538:
	v_ashrrev_i32_e32 v65, 31, v64
	v_ashrrev_i32_e32 v23, 31, v22
	v_lshlrev_b64 v[86:87], 11, v[64:65]
	v_lshlrev_b64 v[22:23], 10, v[22:23]
	v_lshl_add_u64 v[6:7], v[48:49], 0, v[86:87]
	v_lshl_add_u64 v[22:23], v[50:51], 0, v[22:23]
	global_load_dwordx4 v[92:95], v[6:7], off
	global_load_dwordx4 v[96:99], v[6:7], off offset:1024
	global_load_dwordx2 v[116:117], v[22:23], off offset:512
	global_load_dwordx2 v[118:119], v[22:23], off
	v_ashrrev_i32_e32 v19, 31, v18
	v_ashrrev_i32_e32 v15, 31, v14
	v_ashrrev_i32_e32 v27, 31, v26
	v_ashrrev_i32_e32 v17, 31, v16
	v_ashrrev_i32_e32 v29, 31, v28
	v_ashrrev_i32_e32 v25, 31, v24
	v_lshlrev_b64 v[18:19], 10, v[18:19]
	v_ashrrev_i32_e32 v21, 31, v20
	v_lshlrev_b64 v[8:9], 10, v[14:15]
	v_lshlrev_b64 v[10:11], 10, v[26:27]
	v_lshlrev_b64 v[12:13], 10, v[16:17]
	v_lshlrev_b64 v[14:15], 10, v[28:29]
	v_lshlrev_b64 v[16:17], 10, v[24:25]
	v_lshl_add_u64 v[18:19], v[50:51], 0, v[18:19]
	v_lshlrev_b64 v[20:21], 10, v[20:21]
	v_lshl_add_u64 v[8:9], v[50:51], 0, v[8:9]
	v_lshl_add_u64 v[10:11], v[50:51], 0, v[10:11]
	v_lshl_add_u64 v[12:13], v[50:51], 0, v[12:13]
	v_lshl_add_u64 v[14:15], v[50:51], 0, v[14:15]
	v_lshl_add_u64 v[16:17], v[50:51], 0, v[16:17]
	global_load_dwordx2 v[120:121], v[18:19], off offset:512
	global_load_dwordx2 v[122:123], v[18:19], off
	global_load_dwordx2 v[80:81], v[8:9], off
	global_load_dwordx2 v[78:79], v[8:9], off offset:512
	global_load_dwordx2 v[76:77], v[10:11], off
	global_load_dwordx2 v[74:75], v[10:11], off offset:512
	global_load_dwordx2 v[72:73], v[12:13], off
	global_load_dwordx2 v[70:71], v[12:13], off offset:512
	global_load_dwordx2 v[68:69], v[14:15], off
	global_load_dwordx2 v[66:67], v[14:15], off offset:512
	v_lshl_add_u64 v[20:21], v[50:51], 0, v[20:21]
	global_load_dwordx2 v[124:125], v[16:17], off offset:512
	global_load_dwordx2 v[126:127], v[20:21], off offset:512
	global_load_dwordx2 v[128:129], v[20:21], off
	global_load_dwordx2 v[130:131], v[16:17], off
	v_add_u32_e32 v3, s29, v64
	v_cmp_gt_i32_e64 s[6:7], s4, v3
	v_add_u32_e32 v58, s5, v64
	v_min_i32_e32 v5, 0x8000, v64
	v_cndmask_b32_e64 v3, v1, v3, s[6:7]
	v_cmp_gt_i32_e64 s[6:7], s4, v3
	v_cmp_gt_i32_e32 vcc, s4, v58
	v_mov_b32_e32 v57, v43
	v_cndmask_b32_e64 v22, v1, v3, s[6:7]
	v_add_u32_e32 v3, s5, v3
	v_cmp_gt_i32_e64 s[6:7], s4, v3
	v_cndmask_b32_e32 v6, v64, v58, vcc
	v_ashrrev_i32_e32 v7, 31, v6
	v_cndmask_b32_e64 v3, v1, v3, s[6:7]
	v_lshlrev_b32_e32 v10, 2, v3
	v_ashrrev_i32_e32 v3, 12, v5
	v_mul_i32_i24_e32 v100, 0x1800, v3
	v_lshlrev_b64 v[6:7], 11, v[6:7]
	v_lshlrev_b32_e32 v8, 2, v22
	v_ashrrev_i32_e32 v101, 31, v100
	v_lshl_add_u64 v[6:7], v[48:49], 0, v[6:7]
	v_ashrrev_i32_e32 v9, 31, v8
	v_lshlrev_b64 v[136:137], 2, v[100:101]
	global_load_dwordx4 v[26:29], v[6:7], off
	global_load_dwordx4 v[22:25], v[6:7], off offset:1024
	v_lshlrev_b64 v[6:7], 2, v[8:9]
	v_ashrrev_i32_e32 v11, 31, v10
	v_lshl_add_u64 v[100:101], s[24:25], 0, v[136:137]
	v_lshl_add_u64 v[8:9], s[12:13], 0, v[6:7]
	v_lshl_add_u64 v[12:13], s[14:15], 0, v[6:7]
	v_lshl_add_u64 v[6:7], s[16:17], 0, v[6:7]
	v_lshlrev_b64 v[10:11], 2, v[10:11]
	v_lshl_add_u64 v[108:109], v[100:101], 0, s[20:21]
	global_load_dwordx4 v[38:41], v[8:9], off
	global_load_dwordx4 v[18:21], v[12:13], off
	s_nop 0
	global_load_dwordx4 v[6:9], v[6:7], off
	v_lshl_add_u64 v[12:13], s[12:13], 0, v[10:11]
	v_lshl_add_u64 v[14:15], s[14:15], 0, v[10:11]
	v_lshl_add_u64 v[10:11], s[16:17], 0, v[10:11]
	v_lshl_add_u64 v[104:105], v[108:109], 0, v[42:43]
	global_load_dwordx4 v[34:37], v[12:13], off
	s_nop 0
	global_load_dwordx4 v[14:17], v[14:15], off
	s_nop 0
	global_load_dwordx4 v[10:13], v[10:11], off
	s_nop 0
	global_load_dwordx4 v[100:103], v[104:105], off offset:16
	s_nop 0
	global_load_dwordx4 v[104:107], v[104:105], off
	v_lshl_add_u64 v[112:113], v[108:109], 0, v[56:57]
	global_load_dwordx4 v[108:111], v[112:113], off offset:16
	s_nop 0
	global_load_dwordx4 v[112:115], v[112:113], off
	v_lshl_add_u64 v[86:87], v[52:53], 0, v[86:87]
	s_waitcnt vmcnt(29)
	v_lshlrev_b32_e32 v132, 16, v92
	s_waitcnt vmcnt(27)
	v_cvt_pk_f32_fp8_e32 v[148:149], v116
	s_waitcnt vmcnt(26)
	v_cvt_pk_f32_fp8_e32 v[142:143], v118
	v_cvt_pk_f32_fp8_sdwa v[144:145], v118 src0_sel:WORD_1
	v_cvt_pk_f32_fp8_e32 v[146:147], v119
	v_cvt_pk_f32_fp8_sdwa v[118:119], v119 src0_sel:WORD_1
	v_cvt_pk_f32_fp8_sdwa v[150:151], v116 src0_sel:WORD_1
	v_cvt_pk_f32_fp8_e32 v[152:153], v117
	v_cvt_pk_f32_fp8_sdwa v[116:117], v117 src0_sel:WORD_1
	v_pk_fma_f32 v[142:143], v[30:31], v[142:143], 0 op_sel_hi:[0,1,0]
	v_pk_fma_f32 v[144:145], v[30:31], v[144:145], 0 op_sel_hi:[0,1,0]
	v_pk_fma_f32 v[146:147], v[30:31], v[146:147], 0 op_sel_hi:[0,1,0]
	v_pk_fma_f32 v[118:119], v[30:31], v[118:119], 0 op_sel_hi:[0,1,0]
	v_pk_fma_f32 v[148:149], v[30:31], v[148:149], 0 op_sel_hi:[0,1,0]
	v_pk_fma_f32 v[150:151], v[30:31], v[150:151], 0 op_sel_hi:[0,1,0]
	v_pk_fma_f32 v[152:153], v[30:31], v[152:153], 0 op_sel_hi:[0,1,0]
	v_pk_fma_f32 v[30:31], v[30:31], v[116:117], 0 op_sel_hi:[0,1,0]
	s_waitcnt vmcnt(24)
	v_cvt_pk_f32_fp8_sdwa v[116:117], v122 src0_sel:WORD_1
	v_cvt_pk_f32_fp8_e32 v[154:155], v122
	v_cvt_pk_f32_fp8_sdwa v[156:157], v123 src0_sel:WORD_1
	v_cvt_pk_f32_fp8_e32 v[122:123], v123
	v_pk_fma_f32 v[116:117], v[84:85], v[116:117], v[144:145] op_sel_hi:[0,1,1]
	v_pk_fma_f32 v[142:143], v[84:85], v[154:155], v[142:143] op_sel_hi:[0,1,1]
	v_cvt_pk_f32_fp8_sdwa v[144:145], v120 src0_sel:WORD_1
	v_pk_fma_f32 v[122:123], v[84:85], v[122:123], v[146:147] op_sel_hi:[0,1,1]
	v_cvt_pk_f32_fp8_e32 v[146:147], v120
	v_cvt_pk_f32_fp8_sdwa v[154:155], v121 src0_sel:WORD_1
	v_cvt_pk_f32_fp8_e32 v[120:121], v121
	v_pk_fma_f32 v[144:145], v[84:85], v[144:145], v[150:151] op_sel_hi:[0,1,1]
	v_pk_fma_f32 v[146:147], v[84:85], v[146:147], v[148:149] op_sel_hi:[0,1,1]
	s_waitcnt vmcnt(13)
; DI void store_row_bf16(bf16_t* hr, int lane, const f32x4 (&v)[4]) { store16(hr + 8 * lane, v[0], v[1]); store16(hr + 512 + 8 * lane, v[2], v[3]); }
; DI void phase_combine(const Params& P, int li, const bf16_t* X1, bf16_t* X2, const unsigned char* YB, const LAS int* tab, const int* tok_e, const int* tok_pos, const float* tok_gate, const float* modl, const float* modn, unsigned char* H, int G) {
;     ...
;                 for (int k = 0; k < 4; ++k) { const float g = gc[q][k]; const u32x2 a = ya[q][k][0], b = ya[q][k][1];
;                     { const f32x2 p0 = __builtin_amdgcn_cvt_pk_f32_fp8((int)a.x, false), p1 = __builtin_amdgcn_cvt_pk_f32_fp8((int)a.x, true), p2 = __builtin_amdgcn_cvt_pk_f32_fp8((int)a.y, false), p3 = __builtin_amdgcn_cvt_pk_f32_fp8((int)a.y, true);
;                       y[0] += g * (f32x4){p0.x, p0.y, p1.x, p1.y}; y[1] += g * (f32x4){p2.x, p2.y, p3.x, p3.y}; }
;                     { const f32x2 p0 = __builtin_amdgcn_cvt_pk_f32_fp8((int)b.x, false), p1 = __builtin_amdgcn_cvt_pk_f32_fp8((int)b.x, true), p2 = __builtin_amdgcn_cvt_pk_f32_fp8((int)b.y, false), p3 = __builtin_amdgcn_cvt_pk_f32_fp8((int)b.y, true);
;                       y[2] += g * (f32x4){p0.x, p0.y, p1.x, p1.y}; y[3] += g * (f32x4){p2.x, p2.y, p3.x, p3.y}; } }
;                 const float* g2 = modl + b9 * 6144 + 5 * 1024;
; #pragma unroll
;                 for (int j = 0; j < 4; ++j) { const int k = (j >> 1) * 512 + 8 * lane + 4 * (j & 1); v[j] += *(const f32x4*)(g2 + k) * y[j]; }
;                 if (last) { float* o = P.out + (size_t)t * 1024; *(f32x4*)(o + 8 * lane) = v[0]; *(f32x4*)(o + 8 * lane + 4) = v[1]; *(f32x4*)(o + 512 + 8 * lane) = v[2]; *(f32x4*)(o + 512 + 8 * lane + 4) = v[3]; }
;                 else { store_row_bf16(X2 + (size_t)t * 1024, lane, v);
;                     const float* md = modn + b9 * 6144;
;                     modnorm_row(v, lane, P.norm1_g + (li + 1) * 1024, md, md + 1024);
;                     store_row_fp8(H + (size_t)t * 1024, lane, v); }
	v_cvt_pk_f32_fp8_e32 v[148:149], v128
	v_pk_fma_f32 v[120:121], v[84:85], v[120:121], v[152:153] op_sel_hi:[0,1,1]
	v_cvt_pk_f32_fp8_sdwa v[150:151], v128 src0_sel:WORD_1
	v_cvt_pk_f32_fp8_e32 v[152:153], v129
	v_cvt_pk_f32_fp8_sdwa v[128:129], v129 src0_sel:WORD_1
	v_pk_fma_f32 v[118:119], v[84:85], v[156:157], v[118:119] op_sel_hi:[0,1,1]
	v_pk_fma_f32 v[142:143], v[32:33], v[148:149], v[142:143] op_sel_hi:[0,1,1]
	v_pk_fma_f32 v[116:117], v[32:33], v[150:151], v[116:117] op_sel_hi:[0,1,1]
	v_pk_fma_f32 v[118:119], v[32:33], v[128:129], v[118:119] op_sel_hi:[0,1,1]
	v_cvt_pk_f32_fp8_e32 v[128:129], v126
	v_cvt_pk_f32_fp8_sdwa v[148:149], v126 src0_sel:WORD_1
	v_cvt_pk_f32_fp8_e32 v[150:151], v127
	v_cvt_pk_f32_fp8_sdwa v[126:127], v127 src0_sel:WORD_1
	v_pk_fma_f32 v[30:31], v[84:85], v[154:155], v[30:31] op_sel_hi:[0,1,1]
	v_pk_fma_f32 v[122:123], v[32:33], v[152:153], v[122:123] op_sel_hi:[0,1,1]
	v_pk_fma_f32 v[128:129], v[32:33], v[128:129], v[146:147] op_sel_hi:[0,1,1]
	v_pk_fma_f32 v[144:145], v[32:33], v[148:149], v[144:145] op_sel_hi:[0,1,1]
	v_pk_fma_f32 v[120:121], v[32:33], v[150:151], v[120:121] op_sel_hi:[0,1,1]
	v_pk_fma_f32 v[30:31], v[32:33], v[126:127], v[30:31] op_sel_hi:[0,1,1]
	s_waitcnt vmcnt(12)
	v_cvt_pk_f32_fp8_sdwa v[32:33], v130 src0_sel:WORD_1
	v_cvt_pk_f32_fp8_e32 v[126:127], v130
	v_cvt_pk_f32_fp8_sdwa v[146:147], v131 src0_sel:WORD_1
	v_cvt_pk_f32_fp8_e32 v[130:131], v131
	v_pk_fma_f32 v[32:33], v[82:83], v[32:33], v[116:117] op_sel_hi:[0,1,1]
	v_pk_fma_f32 v[116:117], v[82:83], v[126:127], v[142:143] op_sel_hi:[0,1,1]
	v_cvt_pk_f32_fp8_sdwa v[126:127], v124 src0_sel:WORD_1
	v_pk_fma_f32 v[122:123], v[82:83], v[130:131], v[122:123] op_sel_hi:[0,1,1]
	v_cvt_pk_f32_fp8_e32 v[130:131], v124
	v_cvt_pk_f32_fp8_sdwa v[142:143], v125 src0_sel:WORD_1
	v_cvt_pk_f32_fp8_e32 v[124:125], v125
	v_and_b32_e32 v133, 0xffff0000, v92
	v_lshlrev_b32_e32 v92, 16, v93
	v_and_b32_e32 v93, 0xffff0000, v93
	v_lshlrev_b32_e32 v134, 16, v94
	v_and_b32_e32 v135, 0xffff0000, v94
	v_lshlrev_b32_e32 v94, 16, v95
	v_and_b32_e32 v95, 0xffff0000, v95
	v_pk_fma_f32 v[118:119], v[82:83], v[146:147], v[118:119] op_sel_hi:[0,1,1]
	v_lshlrev_b32_e32 v138, 16, v96
	v_and_b32_e32 v139, 0xffff0000, v96
	v_lshlrev_b32_e32 v96, 16, v97
	v_and_b32_e32 v97, 0xffff0000, v97
	v_lshlrev_b32_e32 v140, 16, v98
	v_and_b32_e32 v141, 0xffff0000, v98
	v_lshlrev_b32_e32 v98, 16, v99
	v_and_b32_e32 v99, 0xffff0000, v99
	v_pk_fma_f32 v[126:127], v[82:83], v[126:127], v[144:145] op_sel_hi:[0,1,1]
	v_pk_fma_f32 v[128:129], v[82:83], v[130:131], v[128:129] op_sel_hi:[0,1,1]
	v_pk_fma_f32 v[30:31], v[82:83], v[142:143], v[30:31] op_sel_hi:[0,1,1]
	v_pk_fma_f32 v[120:121], v[82:83], v[124:125], v[120:121] op_sel_hi:[0,1,1]
	s_waitcnt vmcnt(2)
	v_pk_fma_f32 v[142:143], v[116:117], v[104:105], v[132:133]
	v_pk_fma_f32 v[144:145], v[32:33], v[106:107], v[92:93]
	v_pk_fma_f32 v[146:147], v[122:123], v[100:101], v[134:135]
	v_pk_fma_f32 v[148:149], v[118:119], v[102:103], v[94:95]
	s_waitcnt vmcnt(0)
	v_pk_fma_f32 v[150:151], v[128:129], v[112:113], v[138:139]
	v_pk_fma_f32 v[152:153], v[126:127], v[114:115], v[96:97]
	v_pk_fma_f32 v[140:141], v[120:121], v[108:109], v[140:141]
	v_pk_fma_f32 v[154:155], v[30:31], v[110:111], v[98:99]
	v_cvt_pk_bf16_f32 v30, v142, v143
	v_cvt_pk_bf16_f32 v31, v144, v145
	v_cvt_pk_bf16_f32 v32, v146, v147
	v_cvt_pk_bf16_f32 v33, v148, v149
	global_store_dwordx4 v[86:87], v[30:33], off
	v_mul_f32_e32 v3, v143, v143
	v_fmac_f32_e32 v3, v142, v142
	v_cvt_pk_bf16_f32 v30, v150, v151
	v_cvt_pk_bf16_f32 v31, v152, v153
	v_cvt_pk_bf16_f32 v32, v140, v141
	v_cvt_pk_bf16_f32 v33, v154, v155
	global_store_dwordx4 v[86:87], v[30:33], off offset:1024
	global_load_dwordx4 v[92:95], v[44:45], off offset:16
	global_load_dwordx4 v[96:99], v[44:45], off
	v_lshl_add_u64 v[30:31], s[18:19], 0, v[136:137]
	v_lshl_add_u64 v[32:33], v[30:31], 0, s[22:23]
	v_lshl_add_u64 v[86:87], v[32:33], 0, v[42:43]
	global_load_dwordx4 v[100:103], v[86:87], off offset:16
	global_load_dwordx4 v[104:107], v[86:87], off
	v_lshl_add_u64 v[30:31], v[30:31], 0, v[42:43]
	global_load_dwordx4 v[108:111], v[30:31], off
	global_load_dwordx4 v[112:115], v[30:31], off offset:16
	global_load_dwordx4 v[116:119], v[46:47], off offset:16
	global_load_dwordx4 v[120:123], v[46:47], off
	v_lshl_add_u64 v[32:33], v[32:33], 0, v[56:57]
	global_load_dwordx4 v[124:127], v[32:33], off offset:16
	global_load_dwordx4 v[128:131], v[32:33], off
	global_load_dwordx4 v[132:135], v[30:31], off offset:2064
	global_load_dwordx4 v[136:139], v[30:31], off offset:2048
	v_fmac_f32_e32 v3, v144, v144
	v_fmac_f32_e32 v3, v145, v145
	v_fmac_f32_e32 v3, v146, v146
	v_fmac_f32_e32 v3, v147, v147
	v_fmac_f32_e32 v3, v148, v148
	v_fmac_f32_e32 v3, v149, v149
	v_fmac_f32_e32 v3, v150, v150
	v_fmac_f32_e32 v3, v151, v151
	v_fmac_f32_e32 v3, v152, v152
	v_fmac_f32_e32 v3, v153, v153
	v_pk_mul_f32 v[30:31], v[140:141], v[140:141]
	v_pk_mul_f32 v[32:33], v[154:155], v[154:155]
	v_add_f32_e32 v3, v30, v3
	v_add_f32_e32 v3, v31, v3
	v_add_f32_e32 v3, v32, v3
	v_add_f32_e32 v3, v33, v3
	ds_bpermute_b32 v5, v61, v3
	v_lshl_add_u32 v32, v39, 2, s28
	v_lshl_add_u32 v33, v40, 2, s28
	v_lshl_add_u32 v30, v38, 2, s28
	v_lshl_add_u32 v38, v41, 2, s28
	s_waitcnt lgkmcnt(0)
	v_add_f32_e32 v3, v3, v5
	ds_bpermute_b32 v5, v63, v3
	v_lshl_add_u32 v34, v34, 2, s28
	v_lshl_add_u32 v36, v36, 2, s28
	v_lshl_add_u32 v37, v37, 2, s28
	s_waitcnt lgkmcnt(0)
	v_add_f32_e32 v3, v3, v5
	ds_bpermute_b32 v5, v83, v3
	s_waitcnt lgkmcnt(0)
	v_add_f32_e32 v3, v3, v5
	ds_bpermute_b32 v5, v85, v3
	s_waitcnt lgkmcnt(0)
; DI void store_row_bf16(bf16_t* hr, int lane, const f32x4 (&v)[4]) { store16(hr + 8 * lane, v[0], v[1]); store16(hr + 512 + 8 * lane, v[2], v[3]); }
; DI void phase_combine(const Params& P, int li, const bf16_t* X1, bf16_t* X2, const unsigned char* YB, const LAS int* tab, const int* tok_e, const int* tok_pos, const float* tok_gate, const float* modl, const float* modn, unsigned char* H, int G) {
;     ...
;                 for (int k = 0; k < 4; ++k) { const float g = gc[q][k]; const u32x2 a = ya[q][k][0], b = ya[q][k][1];
;                     { const f32x2 p0 = __builtin_amdgcn_cvt_pk_f32_fp8((int)a.x, false), p1 = __builtin_amdgcn_cvt_pk_f32_fp8((int)a.x, true), p2 = __builtin_amdgcn_cvt_pk_f32_fp8((int)a.y, false), p3 = __builtin_amdgcn_cvt_pk_f32_fp8((int)a.y, true);
;                       y[0] += g * (f32x4){p0.x, p0.y, p1.x, p1.y}; y[1] += g * (f32x4){p2.x, p2.y, p3.x, p3.y}; }
;                     { const f32x2 p0 = __builtin_amdgcn_cvt_pk_f32_fp8((int)b.x, false), p1 = __builtin_amdgcn_cvt_pk_f32_fp8((int)b.x, true), p2 = __builtin_amdgcn_cvt_pk_f32_fp8((int)b.y, false), p3 = __builtin_amdgcn_cvt_pk_f32_fp8((int)b.y, true);
;                       y[2] += g * (f32x4){p0.x, p0.y, p1.x, p1.y}; y[3] += g * (f32x4){p2.x, p2.y, p3.x, p3.y}; } }
;                 const float* g2 = modl + b9 * 6144 + 5 * 1024;
; #pragma unroll
;                 for (int j = 0; j < 4; ++j) { const int k = (j >> 1) * 512 + 8 * lane + 4 * (j & 1); v[j] += *(const f32x4*)(g2 + k) * y[j]; }
;                 if (last) { float* o = P.out + (size_t)t * 1024; *(f32x4*)(o + 8 * lane) = v[0]; *(f32x4*)(o + 8 * lane + 4) = v[1]; *(f32x4*)(o + 512 + 8 * lane) = v[2]; *(f32x4*)(o + 512 + 8 * lane + 4) = v[3]; }
;                 else { store_row_bf16(X2 + (size_t)t * 1024, lane, v);
;                     const float* md = modn + b9 * 6144;
;                     modnorm_row(v, lane, P.norm1_g + (li + 1) * 1024, md, md + 1024);
;                     store_row_fp8(H + (size_t)t * 1024, lane, v); }
	v_add_f32_e32 v39, v3, v5
	ds_bpermute_b32 v40, v88, v39
	ds_read_b32 v31, v30 offset:128
	ds_read_b32 v30, v32 offset:128
	ds_read_b32 v5, v33 offset:128
	ds_read_b32 v3, v38 offset:128
	v_lshl_add_u32 v38, v35, 2, s28
	s_waitcnt lgkmcnt(4)
	v_add_f32_e32 v32, v39, v40
	ds_bpermute_b32 v33, v89, v32
	s_waitcnt lgkmcnt(0)
	v_add_f32_e32 v32, v32, v33
	v_fmamk_f32 v32, v32, 0x3a800000, v90
	v_mul_f32_e32 v33, 0x4b800000, v32
	v_cmp_gt_f32_e64 s[6:7], s38, v32
	s_waitcnt vmcnt(8)
	v_pk_add_f32 v[86:87], v[106:107], 1.0 op_sel_hi:[1,0]
	v_cndmask_b32_e64 v32, v32, v33, s[6:7]
	v_rsq_f32_e32 v39, v32
	ds_read_b32 v35, v34 offset:128
	ds_read_b32 v34, v38 offset:128
	ds_read_b32 v33, v36 offset:128
	ds_read_b32 v32, v37 offset:128
	v_mul_f32_e32 v36, 0x45800000, v39
	v_cndmask_b32_e64 v36, v39, v36, s[6:7]
	v_pk_mul_f32 v[40:41], v[142:143], v[36:37] op_sel_hi:[1,0]
	v_pk_mul_f32 v[38:39], v[144:145], v[36:37] op_sel_hi:[1,0]
	v_pk_mul_f32 v[40:41], v[96:97], v[40:41]
	v_pk_add_f32 v[96:97], v[104:105], 1.0 op_sel_hi:[1,0]
	v_pk_mul_f32 v[38:39], v[98:99], v[38:39]
	s_waitcnt vmcnt(7)
	v_pk_fma_f32 v[40:41], v[96:97], v[40:41], v[108:109]
	v_pk_mul_f32 v[96:97], v[146:147], v[36:37] op_sel_hi:[1,0]
	v_pk_fma_f32 v[38:39], v[86:87], v[38:39], v[110:111]
	v_pk_mul_f32 v[92:93], v[92:93], v[96:97]
	v_pk_add_f32 v[96:97], v[100:101], 1.0 op_sel_hi:[1,0]
	v_pk_mul_f32 v[86:87], v[148:149], v[36:37] op_sel_hi:[1,0]
	s_waitcnt vmcnt(6)
	v_pk_fma_f32 v[92:93], v[96:97], v[92:93], v[112:113]
	v_med3_f32 v40, v40, s39, v91
	v_med3_f32 v41, v41, s39, v91
	v_med3_f32 v59, v38, s39, v91
	s_nop 0
	v_pk_mul_f32 v[86:87], v[94:95], v[86:87]
	v_pk_add_f32 v[94:95], v[102:103], 1.0 op_sel_hi:[1,0]
	v_med3_f32 v82, v39, s39, v91
	v_cvt_pk_fp8_f32 v38, v40, v41
	v_med3_f32 v40, v92, s39, v91
	v_med3_f32 v41, v93, s39, v91
	s_nop 0
	v_pk_fma_f32 v[86:87], v[94:95], v[86:87], v[114:115]
	v_pk_mul_f32 v[94:95], v[152:153], v[36:37] op_sel_hi:[1,0]
	v_cvt_pk_fp8_f32 v39, v40, v41
	v_pk_mul_f32 v[96:97], v[150:151], v[36:37] op_sel_hi:[1,0]
	s_waitcnt vmcnt(4)
	v_pk_mul_f32 v[94:95], v[122:123], v[94:95]
	s_waitcnt vmcnt(2)
	v_pk_add_f32 v[98:99], v[130:131], 1.0 op_sel_hi:[1,0]
	v_pk_mul_f32 v[96:97], v[120:121], v[96:97]
	v_pk_add_f32 v[100:101], v[128:129], 1.0 op_sel_hi:[1,0]
	s_waitcnt vmcnt(0)
	v_pk_fma_f32 v[94:95], v[98:99], v[94:95], v[138:139]
	v_pk_mul_f32 v[98:99], v[154:155], v[36:37] op_sel_hi:[1,0]
	v_pk_mul_f32 v[36:37], v[140:141], v[36:37] op_sel_hi:[1,0]
	v_pk_fma_f32 v[96:97], v[100:101], v[96:97], v[136:137]
	v_pk_mul_f32 v[36:37], v[116:117], v[36:37]
	v_pk_add_f32 v[102:103], v[124:125], 1.0 op_sel_hi:[1,0]
	v_med3_f32 v40, v86, s39, v91
	v_med3_f32 v41, v87, s39, v91
	v_pk_fma_f32 v[36:37], v[102:103], v[36:37], v[132:133]
	v_cvt_pk_fp8_f32 v38, v59, v82 op_sel:[0,0,1]
	v_cvt_pk_fp8_f32 v39, v40, v41 op_sel:[0,0,1]
	v_med3_f32 v41, v96, s39, v91
	v_med3_f32 v59, v97, s39, v91
	s_nop 0
	v_cvt_pk_fp8_f32 v40, v41, v59
	v_med3_f32 v36, v36, s39, v91
	v_med3_f32 v37, v37, s39, v91
	s_nop 0
	v_cvt_pk_fp8_f32 v41, v36, v37
	v_pk_mul_f32 v[98:99], v[118:119], v[98:99]
	v_pk_add_f32 v[100:101], v[126:127], 1.0 op_sel_hi:[1,0]
	v_med3_f32 v82, v94, s39, v91
	v_pk_fma_f32 v[98:99], v[100:101], v[98:99], v[134:135]
	v_med3_f32 v84, v95, s39, v91
	v_med3_f32 v36, v98, s39, v91
	v_med3_f32 v37, v99, s39, v91
	v_cvt_pk_fp8_f32 v40, v82, v84 op_sel:[0,0,1]
	v_cvt_pk_fp8_f32 v41, v36, v37 op_sel:[0,0,1]
	v_lshlrev_b64 v[36:37], 10, v[64:65]
	v_lshl_add_u64 v[36:37], v[54:55], 0, v[36:37]
	global_store_dwordx2 v[36:37], v[38:39], off
	global_store_dwordx2 v[36:37], v[40:41], off offset:512
	s_and_saveexec_b64 s[6:7], vcc
	s_cbranch_execz .LBB0_1537
	v_min_i32_e32 v36, 0x8000, v58
	v_ashrrev_i32_e32 v36, 12, v36
	v_mul_i32_i24_e32 v36, 0x1800, v36
	v_ashrrev_i32_e32 v37, 31, v36
	v_lshlrev_b64 v[64:65], 2, v[36:37]
	v_lshl_add_u64 v[36:37], s[24:25], 0, v[64:65]
	v_lshl_add_u64 v[86:87], v[36:37], 0, s[20:21]
	v_lshl_add_u64 v[92:93], v[86:87], 0, v[42:43]
	v_lshl_add_u64 v[86:87], v[86:87], 0, v[56:57]
	global_load_dwordx4 v[36:39], v[92:93], off offset:16
	s_nop 0
	global_load_dwordx4 v[92:95], v[92:93], off
	s_nop 0
	global_load_dwordx4 v[96:99], v[86:87], off offset:16
	global_load_dwordx4 v[100:103], v[86:87], off
	v_cvt_pk_f32_fp8_e32 v[108:109], v80
	v_cvt_pk_f32_fp8_sdwa v[110:111], v80 src0_sel:WORD_1
	v_cvt_pk_f32_fp8_e32 v[112:113], v81
	v_cvt_pk_f32_fp8_sdwa v[120:121], v76 src0_sel:WORD_1
	v_cvt_pk_f32_fp8_e32 v[122:123], v76
	v_cvt_pk_f32_fp8_sdwa v[124:125], v77 src0_sel:WORD_1
	v_cvt_pk_f32_fp8_e32 v[76:77], v77
	v_pk_fma_f32 v[108:109], v[2:3], v[108:109], 0 op_sel_hi:[0,1,0]
	v_pk_fma_f32 v[110:111], v[2:3], v[110:111], 0 op_sel_hi:[0,1,0]
	v_pk_fma_f32 v[112:113], v[2:3], v[112:113], 0 op_sel_hi:[0,1,0]
	v_cvt_pk_f32_fp8_e32 v[114:115], v78
	v_cvt_pk_f32_fp8_sdwa v[116:117], v78 src0_sel:WORD_1
	v_cvt_pk_f32_fp8_e32 v[118:119], v79
	v_pk_fma_f32 v[110:111], v[62:63], v[120:121], v[110:111] op_sel_hi:[0,1,1]
	v_pk_fma_f32 v[108:109], v[62:63], v[122:123], v[108:109] op_sel_hi:[0,1,1]
	v_pk_fma_f32 v[76:77], v[62:63], v[76:77], v[112:113] op_sel_hi:[0,1,1]
	v_cvt_pk_f32_fp8_sdwa v[112:113], v74 src0_sel:WORD_1
	v_cvt_pk_f32_fp8_e32 v[120:121], v74
	v_cvt_pk_f32_fp8_sdwa v[122:123], v75 src0_sel:WORD_1
	v_cvt_pk_f32_fp8_e32 v[74:75], v75
	v_cvt_pk_f32_fp8_sdwa v[80:81], v81 src0_sel:WORD_1
	v_pk_fma_f32 v[114:115], v[2:3], v[114:115], 0 op_sel_hi:[0,1,0]
	v_pk_fma_f32 v[116:117], v[2:3], v[116:117], 0 op_sel_hi:[0,1,0]
	v_pk_fma_f32 v[118:119], v[2:3], v[118:119], 0 op_sel_hi:[0,1,0]
	v_pk_fma_f32 v[112:113], v[62:63], v[112:113], v[116:117] op_sel_hi:[0,1,1]
; DI void store_row_bf16(bf16_t* hr, int lane, const f32x4 (&v)[4]) { store16(hr + 8 * lane, v[0], v[1]); store16(hr + 512 + 8 * lane, v[2], v[3]); }
; DI void phase_combine(const Params& P, int li, const bf16_t* X1, bf16_t* X2, const unsigned char* YB, const LAS int* tab, const int* tok_e, const int* tok_pos, const float* tok_gate, const float* modl, const float* modn, unsigned char* H, int G) {
;     ...
;                 for (int k = 0; k < 4; ++k) { const float g = gc[q][k]; const u32x2 a = ya[q][k][0], b = ya[q][k][1];
;                     { const f32x2 p0 = __builtin_amdgcn_cvt_pk_f32_fp8((int)a.x, false), p1 = __builtin_amdgcn_cvt_pk_f32_fp8((int)a.x, true), p2 = __builtin_amdgcn_cvt_pk_f32_fp8((int)a.y, false), p3 = __builtin_amdgcn_cvt_pk_f32_fp8((int)a.y, true);
;                       y[0] += g * (f32x4){p0.x, p0.y, p1.x, p1.y}; y[1] += g * (f32x4){p2.x, p2.y, p3.x, p3.y}; }
;                     { const f32x2 p0 = __builtin_amdgcn_cvt_pk_f32_fp8((int)b.x, false), p1 = __builtin_amdgcn_cvt_pk_f32_fp8((int)b.x, true), p2 = __builtin_amdgcn_cvt_pk_f32_fp8((int)b.y, false), p3 = __builtin_amdgcn_cvt_pk_f32_fp8((int)b.y, true);
;                       y[2] += g * (f32x4){p0.x, p0.y, p1.x, p1.y}; y[3] += g * (f32x4){p2.x, p2.y, p3.x, p3.y}; } }
;                 const float* g2 = modl + b9 * 6144 + 5 * 1024;
; #pragma unroll
;                 for (int j = 0; j < 4; ++j) { const int k = (j >> 1) * 512 + 8 * lane + 4 * (j & 1); v[j] += *(const f32x4*)(g2 + k) * y[j]; }
;                 if (last) { float* o = P.out + (size_t)t * 1024; *(f32x4*)(o + 8 * lane) = v[0]; *(f32x4*)(o + 8 * lane + 4) = v[1]; *(f32x4*)(o + 512 + 8 * lane) = v[2]; *(f32x4*)(o + 512 + 8 * lane + 4) = v[3]; }
;                 else { store_row_bf16(X2 + (size_t)t * 1024, lane, v);
	v_pk_fma_f32 v[114:115], v[62:63], v[120:121], v[114:115] op_sel_hi:[0,1,1]
	v_pk_fma_f32 v[74:75], v[62:63], v[74:75], v[118:119] op_sel_hi:[0,1,1]
	v_cvt_pk_f32_fp8_e32 v[116:117], v72
	v_cvt_pk_f32_fp8_sdwa v[118:119], v72 src0_sel:WORD_1
	v_cvt_pk_f32_fp8_e32 v[120:121], v73
	v_cvt_pk_f32_fp8_sdwa v[72:73], v73 src0_sel:WORD_1
	v_pk_fma_f32 v[80:81], v[2:3], v[80:81], 0 op_sel_hi:[0,1,0]
	v_cvt_pk_f32_fp8_sdwa v[78:79], v79 src0_sel:WORD_1
	v_pk_fma_f32 v[80:81], v[62:63], v[124:125], v[80:81] op_sel_hi:[0,1,1]
	v_pk_fma_f32 v[108:109], v[4:5], v[116:117], v[108:109] op_sel_hi:[0,1,1]
	v_pk_fma_f32 v[110:111], v[4:5], v[118:119], v[110:111] op_sel_hi:[0,1,1]
	v_pk_fma_f32 v[72:73], v[4:5], v[72:73], v[80:81] op_sel_hi:[0,1,1]
	v_cvt_pk_f32_fp8_e32 v[80:81], v70
	v_cvt_pk_f32_fp8_sdwa v[116:117], v70 src0_sel:WORD_1
	v_cvt_pk_f32_fp8_e32 v[118:119], v71
	v_cvt_pk_f32_fp8_sdwa v[70:71], v71 src0_sel:WORD_1
	v_pk_fma_f32 v[78:79], v[2:3], v[78:79], 0 op_sel_hi:[0,1,0]
	v_pk_fma_f32 v[78:79], v[62:63], v[122:123], v[78:79] op_sel_hi:[0,1,1]
	v_pk_fma_f32 v[80:81], v[4:5], v[80:81], v[114:115] op_sel_hi:[0,1,1]
	v_pk_fma_f32 v[112:113], v[4:5], v[116:117], v[112:113] op_sel_hi:[0,1,1]
	v_pk_fma_f32 v[70:71], v[4:5], v[70:71], v[78:79] op_sel_hi:[0,1,1]
	v_cvt_pk_f32_fp8_sdwa v[78:79], v68 src0_sel:WORD_1
	v_cvt_pk_f32_fp8_e32 v[114:115], v68
	v_cvt_pk_f32_fp8_sdwa v[116:117], v69 src0_sel:WORD_1
	v_cvt_pk_f32_fp8_e32 v[68:69], v69
	v_pk_fma_f32 v[76:77], v[4:5], v[120:121], v[76:77] op_sel_hi:[0,1,1]
	v_pk_fma_f32 v[78:79], v[60:61], v[78:79], v[110:111] op_sel_hi:[0,1,1]
	v_cvt_pk_f32_fp8_e32 v[110:111], v66
	v_pk_fma_f32 v[68:69], v[60:61], v[68:69], v[76:77] op_sel_hi:[0,1,1]
	v_cvt_pk_f32_fp8_sdwa v[76:77], v66 src0_sel:WORD_1
	v_pk_fma_f32 v[108:109], v[60:61], v[114:115], v[108:109] op_sel_hi:[0,1,1]
	v_cvt_pk_f32_fp8_sdwa v[114:115], v67 src0_sel:WORD_1
	v_cvt_pk_f32_fp8_e32 v[66:67], v67
	v_lshlrev_b32_e32 v40, 16, v26
	v_and_b32_e32 v41, 0xffff0000, v26
	v_lshlrev_b32_e32 v26, 16, v27
	v_and_b32_e32 v27, 0xffff0000, v27
	v_lshlrev_b32_e32 v104, 16, v28
	v_and_b32_e32 v105, 0xffff0000, v28
	v_lshlrev_b32_e32 v28, 16, v29
	v_and_b32_e32 v29, 0xffff0000, v29
	v_lshlrev_b32_e32 v86, 16, v22
	v_and_b32_e32 v87, 0xffff0000, v22
	v_lshlrev_b32_e32 v22, 16, v23
	v_and_b32_e32 v23, 0xffff0000, v23
	v_pk_fma_f32 v[74:75], v[4:5], v[118:119], v[74:75] op_sel_hi:[0,1,1]
	v_pk_fma_f32 v[72:73], v[60:61], v[116:117], v[72:73] op_sel_hi:[0,1,1]
	v_pk_fma_f32 v[76:77], v[60:61], v[76:77], v[112:113] op_sel_hi:[0,1,1]
	v_pk_fma_f32 v[80:81], v[60:61], v[110:111], v[80:81] op_sel_hi:[0,1,1]
	v_ashrrev_i32_e32 v59, 31, v58
	v_lshlrev_b32_e32 v106, 16, v24
	v_and_b32_e32 v107, 0xffff0000, v24
	v_lshlrev_b32_e32 v24, 16, v25
	v_and_b32_e32 v25, 0xffff0000, v25
	v_pk_fma_f32 v[70:71], v[60:61], v[114:115], v[70:71] op_sel_hi:[0,1,1]
	v_pk_fma_f32 v[66:67], v[60:61], v[66:67], v[74:75] op_sel_hi:[0,1,1]
	s_waitcnt vmcnt(2)
	v_pk_fma_f32 v[40:41], v[108:109], v[92:93], v[40:41]
	v_pk_fma_f32 v[112:113], v[78:79], v[94:95], v[26:27]
	v_pk_fma_f32 v[114:115], v[68:69], v[36:37], v[104:105]
	v_pk_fma_f32 v[116:117], v[72:73], v[38:39], v[28:29]
	s_waitcnt vmcnt(0)
	v_pk_fma_f32 v[80:81], v[80:81], v[100:101], v[86:87]
	v_pk_fma_f32 v[86:87], v[76:77], v[102:103], v[22:23]
	v_lshlrev_b64 v[22:23], 11, v[58:59]
	v_pk_fma_f32 v[118:119], v[66:67], v[96:97], v[106:107]
	v_pk_fma_f32 v[120:121], v[70:71], v[98:99], v[24:25]
	v_lshl_add_u64 v[26:27], v[52:53], 0, v[22:23]
	v_cvt_pk_bf16_f32 v22, v40, v41
	v_cvt_pk_bf16_f32 v23, v112, v113
	v_cvt_pk_bf16_f32 v24, v114, v115
	v_cvt_pk_bf16_f32 v25, v116, v117
	v_lshl_add_u64 v[64:65], s[18:19], 0, v[64:65]
	global_store_dwordx4 v[26:27], v[22:25], off
	v_lshl_add_u64 v[96:97], v[64:65], 0, s[22:23]
	v_lshl_add_u64 v[68:69], v[96:97], 0, v[42:43]
	v_cvt_pk_bf16_f32 v22, v80, v81
	v_cvt_pk_bf16_f32 v23, v86, v87
	v_cvt_pk_bf16_f32 v24, v118, v119
	v_cvt_pk_bf16_f32 v25, v120, v121
	global_store_dwordx4 v[26:27], v[22:25], off offset:1024
	global_load_dwordx4 v[22:25], v[44:45], off offset:16
	s_nop 0
	global_load_dwordx4 v[26:29], v[44:45], off
	global_load_dwordx4 v[36:39], v[68:69], off
	v_lshl_add_u64 v[108:109], v[64:65], 0, v[42:43]
	global_load_dwordx4 v[64:67], v[108:109], off
	s_nop 0
	global_load_dwordx4 v[68:71], v[68:69], off offset:16
	s_nop 0
	global_load_dwordx4 v[72:75], v[108:109], off offset:16
	global_load_dwordx4 v[76:79], v[46:47], off offset:16
	global_load_dwordx4 v[92:95], v[46:47], off
	v_lshl_add_u64 v[100:101], v[96:97], 0, v[56:57]
	global_load_dwordx4 v[96:99], v[100:101], off offset:16
	s_nop 0
	global_load_dwordx4 v[100:103], v[100:101], off
	s_nop 0
	global_load_dwordx4 v[104:107], v[108:109], off offset:2064
	s_nop 0
	global_load_dwordx4 v[108:111], v[108:109], off offset:2048
	v_mul_f32_e32 v2, v41, v41
	v_fmac_f32_e32 v2, v40, v40
	v_fmac_f32_e32 v2, v112, v112
	v_fmac_f32_e32 v2, v113, v113
	v_fmac_f32_e32 v2, v114, v114
	v_fmac_f32_e32 v2, v115, v115
	v_fmac_f32_e32 v2, v116, v116
	v_fmac_f32_e32 v2, v117, v117
	v_fmac_f32_e32 v2, v80, v80
	v_fmac_f32_e32 v2, v81, v81
	v_fmac_f32_e32 v2, v86, v86
	v_fmac_f32_e32 v2, v87, v87
	v_pk_mul_f32 v[122:123], v[118:119], v[118:119]
	v_pk_mul_f32 v[124:125], v[120:121], v[120:121]
	v_add_f32_e32 v2, v122, v2
	v_add_f32_e32 v2, v123, v2
	v_add_f32_e32 v2, v124, v2
	v_add_f32_e32 v2, v125, v2
	ds_bpermute_b32 v4, v61, v2
	s_waitcnt lgkmcnt(0)
; DI void store_row_bf16(bf16_t* hr, int lane, const f32x4 (&v)[4]) { store16(hr + 8 * lane, v[0], v[1]); store16(hr + 512 + 8 * lane, v[2], v[3]); }
; DI void phase_combine(const Params& P, int li, const bf16_t* X1, bf16_t* X2, const unsigned char* YB, const LAS int* tab, const int* tok_e, const int* tok_pos, const float* tok_gate, const float* modl, const float* modn, unsigned char* H, int G) {
;     ...
;                 else { store_row_bf16(X2 + (size_t)t * 1024, lane, v);
;                     const float* md = modn + b9 * 6144;
;                     modnorm_row(v, lane, P.norm1_g + (li + 1) * 1024, md, md + 1024);
;                     store_row_fp8(H + (size_t)t * 1024, lane, v); }
	v_add_f32_e32 v2, v2, v4
	ds_bpermute_b32 v4, v63, v2
	s_waitcnt lgkmcnt(0)
	v_add_f32_e32 v2, v2, v4
	ds_bpermute_b32 v4, v83, v2
	s_waitcnt lgkmcnt(0)
	v_add_f32_e32 v2, v2, v4
	ds_bpermute_b32 v4, v85, v2
	s_waitcnt lgkmcnt(0)
	v_add_f32_e32 v2, v2, v4
	ds_bpermute_b32 v4, v88, v2
	s_waitcnt lgkmcnt(0)
	v_add_f32_e32 v2, v2, v4
	ds_bpermute_b32 v4, v89, v2
	s_waitcnt lgkmcnt(0)
	v_add_f32_e32 v2, v2, v4
	v_fmamk_f32 v2, v2, 0x3a800000, v90
	v_mul_f32_e32 v4, 0x4b800000, v2
	v_cmp_gt_f32_e32 vcc, s38, v2
	s_waitcnt vmcnt(9)
	v_pk_add_f32 v[38:39], v[38:39], 1.0 op_sel_hi:[1,0]
	v_cndmask_b32_e32 v2, v2, v4, vcc
	v_rsq_f32_e32 v2, v2
	v_pk_add_f32 v[36:37], v[36:37], 1.0 op_sel_hi:[1,0]
	v_mul_f32_e32 v4, 0x45800000, v2
	v_cndmask_b32_e32 v2, v2, v4, vcc
	v_pk_mul_f32 v[112:113], v[112:113], v[2:3] op_sel_hi:[1,0]
	v_pk_mul_f32 v[40:41], v[40:41], v[2:3] op_sel_hi:[1,0]
	v_pk_mul_f32 v[28:29], v[28:29], v[112:113]
	v_pk_mul_f32 v[26:27], v[26:27], v[40:41]
	s_waitcnt vmcnt(8)
	v_pk_fma_f32 v[28:29], v[38:39], v[28:29], v[66:67]
	v_pk_fma_f32 v[26:27], v[36:37], v[26:27], v[64:65]
	v_pk_mul_f32 v[36:37], v[116:117], v[2:3] op_sel_hi:[1,0]
	v_pk_mul_f32 v[38:39], v[114:115], v[2:3] op_sel_hi:[1,0]
	v_pk_mul_f32 v[24:25], v[24:25], v[36:37]
	v_pk_mul_f32 v[22:23], v[22:23], v[38:39]
	s_waitcnt vmcnt(7)
	v_pk_add_f32 v[36:37], v[70:71], 1.0 op_sel_hi:[1,0]
	v_pk_add_f32 v[38:39], v[68:69], 1.0 op_sel_hi:[1,0]
	s_waitcnt vmcnt(6)
	v_pk_fma_f32 v[24:25], v[36:37], v[24:25], v[74:75]
	v_pk_fma_f32 v[22:23], v[38:39], v[22:23], v[72:73]
	v_pk_mul_f32 v[36:37], v[86:87], v[2:3] op_sel_hi:[1,0]
	v_pk_mul_f32 v[38:39], v[80:81], v[2:3] op_sel_hi:[1,0]
	s_waitcnt vmcnt(4)
	v_pk_mul_f32 v[36:37], v[94:95], v[36:37]
	v_pk_mul_f32 v[38:39], v[92:93], v[38:39]
	s_waitcnt vmcnt(2)
	v_pk_add_f32 v[40:41], v[102:103], 1.0 op_sel_hi:[1,0]
	v_pk_add_f32 v[64:65], v[100:101], 1.0 op_sel_hi:[1,0]
	s_waitcnt vmcnt(0)
	v_pk_fma_f32 v[36:37], v[40:41], v[36:37], v[110:111]
	v_pk_fma_f32 v[38:39], v[64:65], v[38:39], v[108:109]
	v_pk_mul_f32 v[40:41], v[120:121], v[2:3] op_sel_hi:[1,0]
	v_pk_mul_f32 v[64:65], v[118:119], v[2:3] op_sel_hi:[1,0]
	v_med3_f32 v2, v26, s39, v91
	v_med3_f32 v4, v27, s39, v91
	s_nop 0
	v_cvt_pk_fp8_f32 v26, v2, v4
	v_med3_f32 v2, v22, s39, v91
	v_med3_f32 v4, v23, s39, v91
	s_nop 0
	v_cvt_pk_fp8_f32 v27, v2, v4
	v_pk_mul_f32 v[64:65], v[76:77], v[64:65]
	v_pk_add_f32 v[68:69], v[96:97], 1.0 op_sel_hi:[1,0]
	v_med3_f32 v2, v24, s39, v91
	v_med3_f32 v4, v25, s39, v91
	v_pk_fma_f32 v[64:65], v[68:69], v[64:65], v[104:105]
	v_cvt_pk_fp8_f32 v27, v2, v4 op_sel:[0,0,1]
	v_med3_f32 v2, v38, s39, v91
	v_med3_f32 v4, v39, s39, v91
	s_nop 0
	v_cvt_pk_fp8_f32 v22, v2, v4
	v_med3_f32 v2, v64, s39, v91
	v_med3_f32 v4, v65, s39, v91
	s_nop 0
	v_cvt_pk_fp8_f32 v23, v2, v4
	v_pk_mul_f32 v[40:41], v[78:79], v[40:41]
	v_pk_add_f32 v[66:67], v[98:99], 1.0 op_sel_hi:[1,0]
	v_med3_f32 v28, v28, s39, v91
	v_pk_fma_f32 v[40:41], v[66:67], v[40:41], v[106:107]
	v_med3_f32 v29, v29, s39, v91
	v_cvt_pk_fp8_f32 v26, v28, v29 op_sel:[0,0,1]
	v_med3_f32 v24, v36, s39, v91
	v_med3_f32 v25, v37, s39, v91
	v_med3_f32 v2, v40, s39, v91
	v_med3_f32 v4, v41, s39, v91
	v_cvt_pk_fp8_f32 v22, v24, v25 op_sel:[0,0,1]
	v_cvt_pk_fp8_f32 v23, v2, v4 op_sel:[0,0,1]
	v_lshlrev_b64 v[24:25], 10, v[58:59]
	v_lshl_add_u64 v[24:25], v[54:55], 0, v[24:25]
	global_store_dwordx2 v[24:25], v[26:27], off
	global_store_dwordx2 v[24:25], v[22:23], off offset:512
	s_branch .LBB0_1537

; #define LAS __attribute__((address_space(3)))
; DI unsigned pk4_fp8(float a, float b, float c, float d) { int r = 0; r = __builtin_amdgcn_cvt_pk_fp8_f32(a, b, r, false); r = __builtin_amdgcn_cvt_pk_fp8_f32(c, d, r, true); return (unsigned)r; }
;     DI void head32x2(const AccT& acc, int rbase, int wc, int fq, bf16_t* dst, const float* gain, float scale, const bool F8) const {
;         LAS const float* cs8 = rope + 2 * 65 * 16; LAS const float* sn8 = cs8 + 65 * 8;
;         const int dbase = 16 * (fq >> 1) + 4 * (fq & 1);
;         const f32x4 g0 = *(const f32x4*)(gain + dbase), g1 = *(const f32x4*)(gain + dbase + 8);
; #pragma unroll
;         for (int ai = 0; ai < 2; ++ai)
; #pragma unroll
;             for (int m = 0; m < 4; ++m) {
;                 const int row = rbase + 128 * ai + 16 * m;
;                 const bool lat = row < NLAT; const int t = row & (SEQ - 1);
;                 const int pos = lat ? ((fq >> 1) ? (t & 63) : (t >> 6)) : 64;
;                 const f32x4 c = *(LAS const f32x4*)(cs8 + pos * 8 + 4 * (fq & 1)), sn = *(LAS const f32x4*)(sn8 + pos * 8 + 4 * (fq & 1));
; #pragma unroll
;                 for (int bj = 0; bj < 2; ++bj) {
;                     float ss = 0.f;
; #pragma unroll
;                     for (int n = 0; n < 2; ++n)
; #pragma unroll
;                         for (int i = 0; i < 4; ++i) ss += acc[ai][bj][m][n][i] * acc[ai][bj][m][n][i];
;                     ss = sum_x16_x32(ss);
;                     const float rinv = __builtin_amdgcn_rsqf(ss * (W8_INV * W8_INV / 32.0f) + EPS) * (scale * W8_INV);
;                     const f32x4 x1 = acc[ai][bj][m][0] * rinv * g0, x2 = acc[ai][bj][m][1] * rinv * g1;
;                     if (F8) { unsigned char* p8 = (unsigned char*)dst + (size_t)row * 256 + wc * 64 + 32 * bj + dbase; const f32x4 y1 = x1 * c - x2 * sn, y2 = x1 * sn + x2 * c;
;                         *(unsigned*)p8 = pk4_fp8(y1[0], y1[1], y1[2], y1[3]); *(unsigned*)(p8 + 8) = pk4_fp8(y2[0], y2[1], y2[2], y2[3]); }
.LBB0_1636:
	s_load_dwordx2 s[6:7], s[6:7], 0x0
	v_lshlrev_b32_e32 v131, 2, v158
	v_lshlrev_b32_e32 v130, 3, v158
	v_and_b32_e32 v138, 4, v131
	v_and_or_b32 v148, v130, -16, v138
	v_ashrrev_i32_e32 v149, 31, v148
	s_waitcnt lgkmcnt(0)
	v_lshl_add_u64 v[130:131], v[148:149], 2, s[6:7]
	global_load_dwordx4 v[134:137], v[130:131], off offset:128
	s_nop 0
	global_load_dwordx4 v[130:133], v[130:131], off offset:160
	v_mul_f32_e32 v152, v127, v127
	v_fmac_f32_e32 v152, v126, v126
	v_fmac_f32_e32 v152, v128, v128
	v_fmac_f32_e32 v152, v129, v129
	v_fmac_f32_e32 v152, v122, v122
	v_fmac_f32_e32 v152, v123, v123
	v_fmac_f32_e32 v152, v124, v124
	s_and_b64 s[58:59], exec, s[58:59]
	v_fmac_f32_e32 v152, v125, v125
	v_lshlrev_b32_e32 v138, 2, v138
	v_readlane_b32 s58, v254, 4
	v_mov_b32_e32 v153, v152
	s_nop 1
	v_permlane16_swap_b32_e32 v152, v153
	v_add_u32_e32 v174, s58, v138
	v_readlane_b32 s58, v254, 5
	v_cmp_gt_u32_e64 s[6:7], 2, v158
	v_add_f32_e32 v152, v152, v153
	v_add_u32_e32 v175, s58, v138
	v_lshrrev_b32_e32 v138, 6, v160
	v_cndmask_b32_e64 v138, v190, v138, s[6:7]
	v_mov_b32_e32 v153, v152
	v_lshlrev_b32_e32 v138, 3, v138
	s_nop 0
	v_permlane32_swap_b32_e32 v152, v153
	v_cmp_gt_i32_e32 vcc, s91, v160
	v_and_b32_e32 v138, 0x1f8, v138
	v_add_f32_e32 v152, v152, v153
	s_mov_b32 s53, 0x25054000
	v_cndmask_b32_e32 v138, v188, v138, vcc
	v_fmamk_f32 v152, v152, 0x37000000, v187
	s_cselect_b32 s53, s53, 0x26154000
	v_lshlrev_b32_e32 v138, 2, v138
	v_rsq_f32_e32 v152, v152
	s_add_u32 s53, s12, s53
	v_add_u32_e32 v139, v174, v138
	v_add_u32_e32 v138, v175, v138
	s_addc_u32 s61, s13, 0
	s_lshl_b32 s58, s92, 1
	ds_read_b128 v[142:145], v139
	ds_read_b128 v[138:141], v138
	s_add_u32 s58, s53, s58
	s_addc_u32 s59, s61, 0
	v_mul_f32_e32 v164, s52, v152
	s_add_u32 s60, s53, s92
	v_pk_mul_f32 v[166:167], v[124:125], v[164:165] op_sel_hi:[1,0]
	v_pk_mul_f32 v[168:169], v[122:123], v[164:165] op_sel_hi:[1,0]
	s_addc_u32 s61, s61, 0
	v_ashrrev_i32_e32 v161, 31, v160
	v_pk_mul_f32 v[152:153], v[128:129], v[164:165] op_sel_hi:[1,0]
	v_pk_mul_f32 v[162:163], v[126:127], v[164:165] op_sel_hi:[1,0]
	v_lshl_add_u64 v[146:147], s[60:61], 0, v[148:149]
	v_lshlrev_b64 v[150:151], 8, v[160:161]
	v_lshl_add_u64 v[150:151], v[146:147], 0, v[150:151]
	s_mov_b64 s[60:61], -1
	s_andn2_b64 vcc, exec, s[8:9]
	s_waitcnt vmcnt(0)
	v_pk_mul_f32 v[152:153], v[136:137], v[152:153]
	v_pk_mul_f32 v[164:165], v[132:133], v[166:167]
	v_pk_mul_f32 v[170:171], v[130:131], v[168:169]
	v_pk_mul_f32 v[162:163], v[134:135], v[162:163]
	s_waitcnt lgkmcnt(0)
	v_pk_mul_f32 v[166:167], v[140:141], v[164:165]
	v_pk_mul_f32 v[168:169], v[138:139], v[170:171]
	v_pk_fma_f32 v[166:167], v[144:145], v[152:153], v[166:167] neg_lo:[0,0,1] neg_hi:[0,0,1]
	v_pk_fma_f32 v[168:169], v[142:143], v[162:163], v[168:169] neg_lo:[0,0,1] neg_hi:[0,0,1]
	v_pk_mul_f32 v[172:173], v[142:143], v[170:171]
	s_cbranch_vccnz .LBB0_1638
	s_nop 0
	v_cvt_pk_fp8_f32 v178, v168, v169
	v_pk_fma_f32 v[176:177], v[138:139], v[162:163], v[172:173]
	v_pk_mul_f32 v[170:171], v[144:145], v[164:165]
	s_mov_b64 s[60:61], 0
	v_cvt_pk_fp8_f32 v178, v166, v167 op_sel:[0,0,1]
	v_pk_fma_f32 v[170:171], v[140:141], v[152:153], v[170:171]
	global_store_dword v[150:151], v178, off
	s_nop 0
	v_cvt_pk_fp8_f32 v178, v176, v177
	v_cvt_pk_fp8_f32 v178, v170, v171 op_sel:[0,0,1]
	global_store_dword v[150:151], v178, off offset:8

; #define LAS __attribute__((address_space(3)))
; DI unsigned pk4_fp8(float a, float b, float c, float d) { int r = 0; r = __builtin_amdgcn_cvt_pk_fp8_f32(a, b, r, false); r = __builtin_amdgcn_cvt_pk_fp8_f32(c, d, r, true); return (unsigned)r; }
;     DI void head32x2(const AccT& acc, int rbase, int wc, int fq, bf16_t* dst, const float* gain, float scale, const bool F8) const {
;         LAS const float* cs8 = rope + 2 * 65 * 16; LAS const float* sn8 = cs8 + 65 * 8;
;         const int dbase = 16 * (fq >> 1) + 4 * (fq & 1);
;         const f32x4 g0 = *(const f32x4*)(gain + dbase), g1 = *(const f32x4*)(gain + dbase + 8);
; #pragma unroll
;         for (int ai = 0; ai < 2; ++ai)
; #pragma unroll
;             for (int m = 0; m < 4; ++m) {
;                 const int row = rbase + 128 * ai + 16 * m;
;                 const bool lat = row < NLAT; const int t = row & (SEQ - 1);
;                 const int pos = lat ? ((fq >> 1) ? (t & 63) : (t >> 6)) : 64;
;                 const f32x4 c = *(LAS const f32x4*)(cs8 + pos * 8 + 4 * (fq & 1)), sn = *(LAS const f32x4*)(sn8 + pos * 8 + 4 * (fq & 1));
; #pragma unroll
;                 for (int bj = 0; bj < 2; ++bj) {
;                     float ss = 0.f;
; #pragma unroll
;                     for (int n = 0; n < 2; ++n)
; #pragma unroll
;                         for (int i = 0; i < 4; ++i) ss += acc[ai][bj][m][n][i] * acc[ai][bj][m][n][i];
;                     ss = sum_x16_x32(ss);
;                     const float rinv = __builtin_amdgcn_rsqf(ss * (W8_INV * W8_INV / 32.0f) + EPS) * (scale * W8_INV);
;                     const f32x4 x1 = acc[ai][bj][m][0] * rinv * g0, x2 = acc[ai][bj][m][1] * rinv * g1;
;                     if (F8) { unsigned char* p8 = (unsigned char*)dst + (size_t)row * 256 + wc * 64 + 32 * bj + dbase; const f32x4 y1 = x1 * c - x2 * sn, y2 = x1 * sn + x2 * c;
;                         *(unsigned*)p8 = pk4_fp8(y1[0], y1[1], y1[2], y1[3]); *(unsigned*)(p8 + 8) = pk4_fp8(y2[0], y2[1], y2[2], y2[3]); }
.LBB0_1640:
	v_mul_f32_e32 v152, v119, v119
	v_fmac_f32_e32 v152, v118, v118
	v_fmac_f32_e32 v152, v120, v120
	v_fmac_f32_e32 v152, v121, v121
	v_fmac_f32_e32 v152, v114, v114
	v_fmac_f32_e32 v152, v115, v115
	v_fmac_f32_e32 v152, v116, v116
	v_fmac_f32_e32 v152, v117, v117
	v_mov_b32_e32 v153, v152
	s_nop 1
	v_permlane16_swap_b32_e32 v152, v153
	v_add_f32_e32 v152, v152, v153
	v_mov_b32_e32 v153, v152
	s_nop 1
	v_permlane32_swap_b32_e32 v152, v153
	v_add_f32_e32 v152, v152, v153
	v_fmamk_f32 v152, v152, 0x37000000, v187
	v_rsq_f32_e32 v152, v152
	s_mov_b64 s[58:59], -1
	s_and_b64 vcc, exec, s[8:9]
	v_mul_f32_e32 v164, s52, v152
	v_pk_mul_f32 v[166:167], v[116:117], v[164:165] op_sel_hi:[1,0]
	v_pk_mul_f32 v[168:169], v[114:115], v[164:165] op_sel_hi:[1,0]
	v_pk_mul_f32 v[152:153], v[120:121], v[164:165] op_sel_hi:[1,0]
	v_pk_mul_f32 v[162:163], v[118:119], v[164:165] op_sel_hi:[1,0]
	v_pk_mul_f32 v[164:165], v[132:133], v[166:167]
	v_pk_mul_f32 v[172:173], v[130:131], v[168:169]
	v_pk_mul_f32 v[152:153], v[136:137], v[152:153]
	v_pk_mul_f32 v[162:163], v[134:135], v[162:163]
	v_pk_mul_f32 v[166:167], v[140:141], v[164:165]
	v_pk_mul_f32 v[168:169], v[138:139], v[172:173]
	v_pk_fma_f32 v[166:167], v[144:145], v[152:153], v[166:167] neg_lo:[0,0,1] neg_hi:[0,0,1]
	v_pk_fma_f32 v[168:169], v[142:143], v[162:163], v[168:169] neg_lo:[0,0,1] neg_hi:[0,0,1]
	v_pk_mul_f32 v[142:143], v[142:143], v[172:173]
	s_cbranch_vccz .LBB0_1642
	s_nop 0
	v_cvt_pk_fp8_f32 v161, v168, v169
	v_pk_fma_f32 v[176:177], v[138:139], v[162:163], v[142:143]
	v_pk_mul_f32 v[172:173], v[144:145], v[164:165]
	s_mov_b64 s[58:59], 0
	v_cvt_pk_fp8_f32 v161, v166, v167 op_sel:[0,0,1]
	v_pk_fma_f32 v[172:173], v[140:141], v[152:153], v[172:173]
	global_store_dword v[150:151], v161, off offset:32
	s_nop 0
	v_cvt_pk_fp8_f32 v161, v176, v177
	v_cvt_pk_fp8_f32 v161, v172, v173 op_sel:[0,0,1]
	global_store_dword v[150:151], v161, off offset:40

; #define LAS __attribute__((address_space(3)))
; DI unsigned pk4_fp8(float a, float b, float c, float d) { int r = 0; r = __builtin_amdgcn_cvt_pk_fp8_f32(a, b, r, false); r = __builtin_amdgcn_cvt_pk_fp8_f32(c, d, r, true); return (unsigned)r; }
;     DI void head32x2(const AccT& acc, int rbase, int wc, int fq, bf16_t* dst, const float* gain, float scale, const bool F8) const {
;         LAS const float* cs8 = rope + 2 * 65 * 16; LAS const float* sn8 = cs8 + 65 * 8;
;         const int dbase = 16 * (fq >> 1) + 4 * (fq & 1);
;         const f32x4 g0 = *(const f32x4*)(gain + dbase), g1 = *(const f32x4*)(gain + dbase + 8);
; #pragma unroll
;         for (int ai = 0; ai < 2; ++ai)
; #pragma unroll
;             for (int m = 0; m < 4; ++m) {
;                 const int row = rbase + 128 * ai + 16 * m;
;                 const bool lat = row < NLAT; const int t = row & (SEQ - 1);
;                 const int pos = lat ? ((fq >> 1) ? (t & 63) : (t >> 6)) : 64;
;                 const f32x4 c = *(LAS const f32x4*)(cs8 + pos * 8 + 4 * (fq & 1)), sn = *(LAS const f32x4*)(sn8 + pos * 8 + 4 * (fq & 1));
; #pragma unroll
;                 for (int bj = 0; bj < 2; ++bj) {
;                     float ss = 0.f;
; #pragma unroll
;                     for (int n = 0; n < 2; ++n)
; #pragma unroll
;                         for (int i = 0; i < 4; ++i) ss += acc[ai][bj][m][n][i] * acc[ai][bj][m][n][i];
;                     ss = sum_x16_x32(ss);
;                     const float rinv = __builtin_amdgcn_rsqf(ss * (W8_INV * W8_INV / 32.0f) + EPS) * (scale * W8_INV);
;                     const f32x4 x1 = acc[ai][bj][m][0] * rinv * g0, x2 = acc[ai][bj][m][1] * rinv * g1;
;                     if (F8) { unsigned char* p8 = (unsigned char*)dst + (size_t)row * 256 + wc * 64 + 32 * bj + dbase; const f32x4 y1 = x1 * c - x2 * sn, y2 = x1 * sn + x2 * c;
;                         *(unsigned*)p8 = pk4_fp8(y1[0], y1[1], y1[2], y1[3]); *(unsigned*)(p8 + 8) = pk4_fp8(y2[0], y2[1], y2[2], y2[3]); }
.LBB0_1644:
	v_mul_f32_e32 v150, v111, v111
	v_fmac_f32_e32 v150, v110, v110
	v_fmac_f32_e32 v150, v112, v112
	v_fmac_f32_e32 v150, v113, v113
	v_fmac_f32_e32 v150, v106, v106
	v_fmac_f32_e32 v150, v107, v107
	v_fmac_f32_e32 v150, v108, v108
	v_fmac_f32_e32 v150, v109, v109
	v_mov_b32_e32 v151, v150
	v_add_u32_e32 v152, 16, v160
	s_nop 0
	v_permlane16_swap_b32_e32 v150, v151
	v_lshrrev_b32_e32 v138, 6, v152
	v_add_f32_e32 v150, v150, v151
	v_cndmask_b32_e64 v138, v152, v138, s[6:7]
	v_mov_b32_e32 v151, v150
	v_lshlrev_b32_e32 v138, 3, v138
	s_nop 0
	v_permlane32_swap_b32_e32 v150, v151
	v_and_b32_e32 v138, 0x1f8, v138
	v_cmp_gt_i32_e32 vcc, s96, v160
	v_add_f32_e32 v150, v150, v151
	v_fmamk_f32 v150, v150, 0x37000000, v187
	v_cndmask_b32_e32 v138, v188, v138, vcc
	v_lshlrev_b32_e32 v138, 2, v138
	v_rsq_f32_e32 v161, v150
	v_add_u32_e32 v139, v174, v138
	v_add_u32_e32 v138, v175, v138
	ds_read_b128 v[142:145], v139
	ds_read_b128 v[138:141], v138
	v_mul_f32_e32 v166, s52, v161
	v_pk_mul_f32 v[168:169], v[108:109], v[166:167] op_sel_hi:[1,0]
	v_pk_mul_f32 v[170:171], v[106:107], v[166:167] op_sel_hi:[1,0]
	v_ashrrev_i32_e32 v153, 31, v152
	v_pk_mul_f32 v[162:163], v[112:113], v[166:167] op_sel_hi:[1,0]
	v_pk_mul_f32 v[164:165], v[110:111], v[166:167] op_sel_hi:[1,0]
	v_pk_mul_f32 v[166:167], v[132:133], v[168:169]
	v_pk_mul_f32 v[168:169], v[130:131], v[170:171]
	v_lshlrev_b64 v[150:151], 8, v[152:153]
	v_pk_mul_f32 v[162:163], v[136:137], v[162:163]
	v_pk_mul_f32 v[164:165], v[134:135], v[164:165]
	s_waitcnt lgkmcnt(0)
	v_pk_mul_f32 v[170:171], v[140:141], v[166:167]
	v_pk_mul_f32 v[172:173], v[138:139], v[168:169]
	v_lshl_add_u64 v[150:151], v[146:147], 0, v[150:151]
	v_pk_fma_f32 v[170:171], v[144:145], v[162:163], v[170:171] neg_lo:[0,0,1] neg_hi:[0,0,1]
	v_pk_fma_f32 v[172:173], v[142:143], v[164:165], v[172:173] neg_lo:[0,0,1] neg_hi:[0,0,1]
	s_mov_b64 s[58:59], -1
	s_and_b64 vcc, exec, s[8:9]
	v_pk_mul_f32 v[168:169], v[142:143], v[168:169]
	s_cbranch_vccz .LBB0_1646
	s_nop 0
	v_cvt_pk_fp8_f32 v161, v172, v173
	v_pk_fma_f32 v[178:179], v[138:139], v[164:165], v[168:169]
	v_pk_mul_f32 v[176:177], v[144:145], v[166:167]
	s_mov_b64 s[58:59], 0
	v_cvt_pk_fp8_f32 v161, v170, v171 op_sel:[0,0,1]
	v_pk_fma_f32 v[176:177], v[140:141], v[162:163], v[176:177]
	global_store_dword v[150:151], v161, off
	s_nop 0
	v_cvt_pk_fp8_f32 v161, v178, v179
	v_cvt_pk_fp8_f32 v161, v176, v177 op_sel:[0,0,1]
	global_store_dword v[150:151], v161, off offset:8

; #define LAS __attribute__((address_space(3)))
; DI unsigned pk4_fp8(float a, float b, float c, float d) { int r = 0; r = __builtin_amdgcn_cvt_pk_fp8_f32(a, b, r, false); r = __builtin_amdgcn_cvt_pk_fp8_f32(c, d, r, true); return (unsigned)r; }
;     DI void head32x2(const AccT& acc, int rbase, int wc, int fq, bf16_t* dst, const float* gain, float scale, const bool F8) const {
;         LAS const float* cs8 = rope + 2 * 65 * 16; LAS const float* sn8 = cs8 + 65 * 8;
;         const int dbase = 16 * (fq >> 1) + 4 * (fq & 1);
;         const f32x4 g0 = *(const f32x4*)(gain + dbase), g1 = *(const f32x4*)(gain + dbase + 8);
; #pragma unroll
;         for (int ai = 0; ai < 2; ++ai)
; #pragma unroll
;             for (int m = 0; m < 4; ++m) {
;                 const int row = rbase + 128 * ai + 16 * m;
;                 const bool lat = row < NLAT; const int t = row & (SEQ - 1);
;                 const int pos = lat ? ((fq >> 1) ? (t & 63) : (t >> 6)) : 64;
;                 const f32x4 c = *(LAS const f32x4*)(cs8 + pos * 8 + 4 * (fq & 1)), sn = *(LAS const f32x4*)(sn8 + pos * 8 + 4 * (fq & 1));
; #pragma unroll
;                 for (int bj = 0; bj < 2; ++bj) {
;                     float ss = 0.f;
; #pragma unroll
;                     for (int n = 0; n < 2; ++n)
; #pragma unroll
;                         for (int i = 0; i < 4; ++i) ss += acc[ai][bj][m][n][i] * acc[ai][bj][m][n][i];
;                     ss = sum_x16_x32(ss);
;                     const float rinv = __builtin_amdgcn_rsqf(ss * (W8_INV * W8_INV / 32.0f) + EPS) * (scale * W8_INV);
;                     const f32x4 x1 = acc[ai][bj][m][0] * rinv * g0, x2 = acc[ai][bj][m][1] * rinv * g1;
;                     if (F8) { unsigned char* p8 = (unsigned char*)dst + (size_t)row * 256 + wc * 64 + 32 * bj + dbase; const f32x4 y1 = x1 * c - x2 * sn, y2 = x1 * sn + x2 * c;
;                         *(unsigned*)p8 = pk4_fp8(y1[0], y1[1], y1[2], y1[3]); *(unsigned*)(p8 + 8) = pk4_fp8(y2[0], y2[1], y2[2], y2[3]); }
.LBB0_1648:
	v_mul_f32_e32 v161, v103, v103
	v_fmac_f32_e32 v161, v102, v102
	v_fmac_f32_e32 v161, v104, v104
	v_fmac_f32_e32 v161, v105, v105
	v_fmac_f32_e32 v161, v98, v98
	v_fmac_f32_e32 v161, v99, v99
	v_fmac_f32_e32 v161, v100, v100
	v_fmac_f32_e32 v161, v101, v101
	v_mov_b32_e32 v162, v161
	s_nop 1
	v_permlane16_swap_b32_e32 v161, v162
	v_add_f32_e32 v161, v161, v162
	v_mov_b32_e32 v162, v161
	s_nop 1
	v_permlane32_swap_b32_e32 v161, v162
	v_add_f32_e32 v161, v161, v162
	v_fmamk_f32 v161, v161, 0x37000000, v187
	v_rsq_f32_e32 v161, v161
	s_mov_b64 s[58:59], -1
	s_and_b64 vcc, exec, s[8:9]
	v_mul_f32_e32 v166, s52, v161
	v_pk_mul_f32 v[168:169], v[100:101], v[166:167] op_sel_hi:[1,0]
	v_pk_mul_f32 v[170:171], v[98:99], v[166:167] op_sel_hi:[1,0]
	v_pk_mul_f32 v[162:163], v[104:105], v[166:167] op_sel_hi:[1,0]
	v_pk_mul_f32 v[164:165], v[102:103], v[166:167] op_sel_hi:[1,0]
	v_pk_mul_f32 v[166:167], v[132:133], v[168:169]
	v_pk_mul_f32 v[172:173], v[130:131], v[170:171]
	v_pk_mul_f32 v[162:163], v[136:137], v[162:163]
	v_pk_mul_f32 v[164:165], v[134:135], v[164:165]
	v_pk_mul_f32 v[168:169], v[140:141], v[166:167]
	v_pk_mul_f32 v[170:171], v[138:139], v[172:173]
	v_pk_fma_f32 v[168:169], v[144:145], v[162:163], v[168:169] neg_lo:[0,0,1] neg_hi:[0,0,1]
	v_pk_fma_f32 v[170:171], v[142:143], v[164:165], v[170:171] neg_lo:[0,0,1] neg_hi:[0,0,1]
	v_pk_mul_f32 v[142:143], v[142:143], v[172:173]
	s_cbranch_vccz .LBB0_1650
	s_nop 0
	v_cvt_pk_fp8_f32 v161, v170, v171
	v_pk_fma_f32 v[176:177], v[138:139], v[164:165], v[142:143]
	v_pk_mul_f32 v[172:173], v[144:145], v[166:167]
	s_mov_b64 s[58:59], 0
	v_cvt_pk_fp8_f32 v161, v168, v169 op_sel:[0,0,1]
	v_pk_fma_f32 v[172:173], v[140:141], v[162:163], v[172:173]
	global_store_dword v[150:151], v161, off offset:32
	s_nop 0
	v_cvt_pk_fp8_f32 v161, v176, v177
	v_cvt_pk_fp8_f32 v161, v172, v173 op_sel:[0,0,1]
	global_store_dword v[150:151], v161, off offset:40

; #define LAS __attribute__((address_space(3)))
; DI unsigned pk4_fp8(float a, float b, float c, float d) { int r = 0; r = __builtin_amdgcn_cvt_pk_fp8_f32(a, b, r, false); r = __builtin_amdgcn_cvt_pk_fp8_f32(c, d, r, true); return (unsigned)r; }
;     DI void head32x2(const AccT& acc, int rbase, int wc, int fq, bf16_t* dst, const float* gain, float scale, const bool F8) const {
;         LAS const float* cs8 = rope + 2 * 65 * 16; LAS const float* sn8 = cs8 + 65 * 8;
;         const int dbase = 16 * (fq >> 1) + 4 * (fq & 1);
;         const f32x4 g0 = *(const f32x4*)(gain + dbase), g1 = *(const f32x4*)(gain + dbase + 8);
; #pragma unroll
;         for (int ai = 0; ai < 2; ++ai)
; #pragma unroll
;             for (int m = 0; m < 4; ++m) {
;                 const int row = rbase + 128 * ai + 16 * m;
;                 const bool lat = row < NLAT; const int t = row & (SEQ - 1);
;                 const int pos = lat ? ((fq >> 1) ? (t & 63) : (t >> 6)) : 64;
;                 const f32x4 c = *(LAS const f32x4*)(cs8 + pos * 8 + 4 * (fq & 1)), sn = *(LAS const f32x4*)(sn8 + pos * 8 + 4 * (fq & 1));
; #pragma unroll
;                 for (int bj = 0; bj < 2; ++bj) {
;                     float ss = 0.f;
; #pragma unroll
;                     for (int n = 0; n < 2; ++n)
; #pragma unroll
;                         for (int i = 0; i < 4; ++i) ss += acc[ai][bj][m][n][i] * acc[ai][bj][m][n][i];
;                     ss = sum_x16_x32(ss);
;                     const float rinv = __builtin_amdgcn_rsqf(ss * (W8_INV * W8_INV / 32.0f) + EPS) * (scale * W8_INV);
;                     const f32x4 x1 = acc[ai][bj][m][0] * rinv * g0, x2 = acc[ai][bj][m][1] * rinv * g1;
;                     if (F8) { unsigned char* p8 = (unsigned char*)dst + (size_t)row * 256 + wc * 64 + 32 * bj + dbase; const f32x4 y1 = x1 * c - x2 * sn, y2 = x1 * sn + x2 * c;
;                         *(unsigned*)p8 = pk4_fp8(y1[0], y1[1], y1[2], y1[3]); *(unsigned*)(p8 + 8) = pk4_fp8(y2[0], y2[1], y2[2], y2[3]); }
.LBB0_1652:
	v_mul_f32_e32 v150, v95, v95
	v_fmac_f32_e32 v150, v94, v94
	v_fmac_f32_e32 v150, v96, v96
	v_fmac_f32_e32 v150, v97, v97
	v_fmac_f32_e32 v150, v90, v90
	v_fmac_f32_e32 v150, v91, v91
	v_fmac_f32_e32 v150, v92, v92
	v_fmac_f32_e32 v150, v93, v93
	v_mov_b32_e32 v151, v150
	v_add_u32_e32 v152, 32, v160
	s_nop 0
	v_permlane16_swap_b32_e32 v150, v151
	v_lshrrev_b32_e32 v138, 6, v152
	v_add_f32_e32 v150, v150, v151
	v_cndmask_b32_e64 v138, v152, v138, s[6:7]
	v_mov_b32_e32 v151, v150
	v_lshlrev_b32_e32 v138, 3, v138
	s_nop 0
	v_permlane32_swap_b32_e32 v150, v151
	v_and_b32_e32 v138, 0x1f8, v138
	v_cmp_gt_i32_e32 vcc, s97, v160
	v_add_f32_e32 v150, v150, v151
	v_fmamk_f32 v150, v150, 0x37000000, v187
	v_cndmask_b32_e32 v138, v188, v138, vcc
	v_lshlrev_b32_e32 v138, 2, v138
	v_rsq_f32_e32 v161, v150
	v_add_u32_e32 v139, v174, v138
	v_add_u32_e32 v138, v175, v138
	ds_read_b128 v[142:145], v139
	ds_read_b128 v[138:141], v138
	v_mul_f32_e32 v166, s52, v161
	v_pk_mul_f32 v[168:169], v[92:93], v[166:167] op_sel_hi:[1,0]
	v_pk_mul_f32 v[170:171], v[90:91], v[166:167] op_sel_hi:[1,0]
	v_ashrrev_i32_e32 v153, 31, v152
	v_pk_mul_f32 v[162:163], v[96:97], v[166:167] op_sel_hi:[1,0]
	v_pk_mul_f32 v[164:165], v[94:95], v[166:167] op_sel_hi:[1,0]
	v_pk_mul_f32 v[166:167], v[132:133], v[168:169]
	v_pk_mul_f32 v[168:169], v[130:131], v[170:171]
	v_lshlrev_b64 v[150:151], 8, v[152:153]
	v_pk_mul_f32 v[162:163], v[136:137], v[162:163]
	v_pk_mul_f32 v[164:165], v[134:135], v[164:165]
	s_waitcnt lgkmcnt(0)
	v_pk_mul_f32 v[170:171], v[140:141], v[166:167]
	v_pk_mul_f32 v[172:173], v[138:139], v[168:169]
	v_lshl_add_u64 v[150:151], v[146:147], 0, v[150:151]
	v_pk_fma_f32 v[170:171], v[144:145], v[162:163], v[170:171] neg_lo:[0,0,1] neg_hi:[0,0,1]
	v_pk_fma_f32 v[172:173], v[142:143], v[164:165], v[172:173] neg_lo:[0,0,1] neg_hi:[0,0,1]
	s_mov_b64 s[58:59], -1
	s_and_b64 vcc, exec, s[8:9]
	v_pk_mul_f32 v[168:169], v[142:143], v[168:169]
	s_cbranch_vccz .LBB0_1654
	s_nop 0
	v_cvt_pk_fp8_f32 v161, v172, v173
	v_pk_fma_f32 v[178:179], v[138:139], v[164:165], v[168:169]
	v_pk_mul_f32 v[176:177], v[144:145], v[166:167]
	s_mov_b64 s[58:59], 0
	v_cvt_pk_fp8_f32 v161, v170, v171 op_sel:[0,0,1]
	v_pk_fma_f32 v[176:177], v[140:141], v[162:163], v[176:177]
	global_store_dword v[150:151], v161, off
	s_nop 0
	v_cvt_pk_fp8_f32 v161, v178, v179
	v_cvt_pk_fp8_f32 v161, v176, v177 op_sel:[0,0,1]
	global_store_dword v[150:151], v161, off offset:8

; #define LAS __attribute__((address_space(3)))
; DI unsigned pk4_fp8(float a, float b, float c, float d) { int r = 0; r = __builtin_amdgcn_cvt_pk_fp8_f32(a, b, r, false); r = __builtin_amdgcn_cvt_pk_fp8_f32(c, d, r, true); return (unsigned)r; }
; DI void store8(bf16_t* p, f32x4 a) { u32x2 w; w.x = pk2(a[0], a[1]); w.y = pk2(a[2], a[3]); *(u32x2*)p = w; }
;     DI void head32x2(const AccT& acc, int rbase, int wc, int fq, bf16_t* dst, const float* gain, float scale, const bool F8) const {
;         LAS const float* cs8 = rope + 2 * 65 * 16; LAS const float* sn8 = cs8 + 65 * 8;
;         const int dbase = 16 * (fq >> 1) + 4 * (fq & 1);
;         const f32x4 g0 = *(const f32x4*)(gain + dbase), g1 = *(const f32x4*)(gain + dbase + 8);
; #pragma unroll
;         for (int ai = 0; ai < 2; ++ai)
; #pragma unroll
;             for (int m = 0; m < 4; ++m) {
;                 const int row = rbase + 128 * ai + 16 * m;
;                 const bool lat = row < NLAT; const int t = row & (SEQ - 1);
;                 const int pos = lat ? ((fq >> 1) ? (t & 63) : (t >> 6)) : 64;
;                 const f32x4 c = *(LAS const f32x4*)(cs8 + pos * 8 + 4 * (fq & 1)), sn = *(LAS const f32x4*)(sn8 + pos * 8 + 4 * (fq & 1));
; #pragma unroll
;                 for (int bj = 0; bj < 2; ++bj) {
;                     float ss = 0.f;
; #pragma unroll
;                     for (int n = 0; n < 2; ++n)
; #pragma unroll
;                         for (int i = 0; i < 4; ++i) ss += acc[ai][bj][m][n][i] * acc[ai][bj][m][n][i];
;                     ss = sum_x16_x32(ss);
;                     const float rinv = __builtin_amdgcn_rsqf(ss * (W8_INV * W8_INV / 32.0f) + EPS) * (scale * W8_INV);
;                     const f32x4 x1 = acc[ai][bj][m][0] * rinv * g0, x2 = acc[ai][bj][m][1] * rinv * g1;
;                     if (F8) { unsigned char* p8 = (unsigned char*)dst + (size_t)row * 256 + wc * 64 + 32 * bj + dbase; const f32x4 y1 = x1 * c - x2 * sn, y2 = x1 * sn + x2 * c;
;                         *(unsigned*)p8 = pk4_fp8(y1[0], y1[1], y1[2], y1[3]); *(unsigned*)(p8 + 8) = pk4_fp8(y2[0], y2[1], y2[2], y2[3]); }
;                     else { bf16_t* p = dst + (size_t)row * 256 + wc * 64 + 32 * bj + dbase;
;                         store8(p, x1 * c - x2 * sn); store8(p + 8, x1 * sn + x2 * c); }
;                 }
.LBB0_1656:
	v_mul_f32_e32 v161, v87, v87
	v_fmac_f32_e32 v161, v86, v86
	v_fmac_f32_e32 v161, v88, v88
	v_fmac_f32_e32 v161, v89, v89
	v_fmac_f32_e32 v161, v82, v82
	v_fmac_f32_e32 v161, v83, v83
	v_fmac_f32_e32 v161, v84, v84
	v_fmac_f32_e32 v161, v85, v85
	v_mov_b32_e32 v162, v161
	s_nop 1
	v_permlane16_swap_b32_e32 v161, v162
	v_add_f32_e32 v161, v161, v162
	v_mov_b32_e32 v162, v161
	s_nop 1
	v_permlane32_swap_b32_e32 v161, v162
	v_add_f32_e32 v161, v161, v162
	v_fmamk_f32 v161, v161, 0x37000000, v187
	v_rsq_f32_e32 v161, v161
	s_mov_b64 s[58:59], -1
	s_and_b64 vcc, exec, s[8:9]
	v_mul_f32_e32 v166, s52, v161
	v_pk_mul_f32 v[168:169], v[84:85], v[166:167] op_sel_hi:[1,0]
	v_pk_mul_f32 v[170:171], v[82:83], v[166:167] op_sel_hi:[1,0]
	v_pk_mul_f32 v[162:163], v[88:89], v[166:167] op_sel_hi:[1,0]
	v_pk_mul_f32 v[164:165], v[86:87], v[166:167] op_sel_hi:[1,0]
	v_pk_mul_f32 v[166:167], v[132:133], v[168:169]
	v_pk_mul_f32 v[172:173], v[130:131], v[170:171]
	v_pk_mul_f32 v[162:163], v[136:137], v[162:163]
	v_pk_mul_f32 v[164:165], v[134:135], v[164:165]
	v_pk_mul_f32 v[168:169], v[140:141], v[166:167]
	v_pk_mul_f32 v[170:171], v[138:139], v[172:173]
	v_pk_fma_f32 v[168:169], v[144:145], v[162:163], v[168:169] neg_lo:[0,0,1] neg_hi:[0,0,1]
	v_pk_fma_f32 v[170:171], v[142:143], v[164:165], v[170:171] neg_lo:[0,0,1] neg_hi:[0,0,1]
	v_pk_mul_f32 v[142:143], v[142:143], v[172:173]
	s_cbranch_vccz .LBB0_1658
	s_nop 0
	v_cvt_pk_fp8_f32 v161, v170, v171
	v_pk_fma_f32 v[176:177], v[138:139], v[164:165], v[142:143]
	v_pk_mul_f32 v[172:173], v[144:145], v[166:167]
	s_mov_b64 s[58:59], 0
	v_cvt_pk_fp8_f32 v161, v168, v169 op_sel:[0,0,1]
	v_pk_fma_f32 v[172:173], v[140:141], v[162:163], v[172:173]
	global_store_dword v[150:151], v161, off offset:32
	s_nop 0
	v_cvt_pk_fp8_f32 v161, v176, v177
	v_cvt_pk_fp8_f32 v161, v172, v173 op_sel:[0,0,1]
	global_store_dword v[150:151], v161, off offset:40

; #define LAS __attribute__((address_space(3)))
; DI unsigned pk4_fp8(float a, float b, float c, float d) { int r = 0; r = __builtin_amdgcn_cvt_pk_fp8_f32(a, b, r, false); r = __builtin_amdgcn_cvt_pk_fp8_f32(c, d, r, true); return (unsigned)r; }
; DI void store8(bf16_t* p, f32x4 a) { u32x2 w; w.x = pk2(a[0], a[1]); w.y = pk2(a[2], a[3]); *(u32x2*)p = w; }
;     DI void head32x2(const AccT& acc, int rbase, int wc, int fq, bf16_t* dst, const float* gain, float scale, const bool F8) const {
;         LAS const float* cs8 = rope + 2 * 65 * 16; LAS const float* sn8 = cs8 + 65 * 8;
;         const int dbase = 16 * (fq >> 1) + 4 * (fq & 1);
;         const f32x4 g0 = *(const f32x4*)(gain + dbase), g1 = *(const f32x4*)(gain + dbase + 8);
; #pragma unroll
;         for (int ai = 0; ai < 2; ++ai)
; #pragma unroll
;             for (int m = 0; m < 4; ++m) {
;                 const int row = rbase + 128 * ai + 16 * m;
;                 const bool lat = row < NLAT; const int t = row & (SEQ - 1);
;                 const int pos = lat ? ((fq >> 1) ? (t & 63) : (t >> 6)) : 64;
;                 const f32x4 c = *(LAS const f32x4*)(cs8 + pos * 8 + 4 * (fq & 1)), sn = *(LAS const f32x4*)(sn8 + pos * 8 + 4 * (fq & 1));
; #pragma unroll
;                 for (int bj = 0; bj < 2; ++bj) {
;                     float ss = 0.f;
; #pragma unroll
;                     for (int n = 0; n < 2; ++n)
; #pragma unroll
;                         for (int i = 0; i < 4; ++i) ss += acc[ai][bj][m][n][i] * acc[ai][bj][m][n][i];
;                     ss = sum_x16_x32(ss);
;                     const float rinv = __builtin_amdgcn_rsqf(ss * (W8_INV * W8_INV / 32.0f) + EPS) * (scale * W8_INV);
;                     const f32x4 x1 = acc[ai][bj][m][0] * rinv * g0, x2 = acc[ai][bj][m][1] * rinv * g1;
;                     if (F8) { unsigned char* p8 = (unsigned char*)dst + (size_t)row * 256 + wc * 64 + 32 * bj + dbase; const f32x4 y1 = x1 * c - x2 * sn, y2 = x1 * sn + x2 * c;
;                         *(unsigned*)p8 = pk4_fp8(y1[0], y1[1], y1[2], y1[3]); *(unsigned*)(p8 + 8) = pk4_fp8(y2[0], y2[1], y2[2], y2[3]); }
;                     else { bf16_t* p = dst + (size_t)row * 256 + wc * 64 + 32 * bj + dbase;
;                         store8(p, x1 * c - x2 * sn); store8(p + 8, x1 * sn + x2 * c); }
;                 }
.LBB0_1660:
	v_mul_f32_e32 v150, v79, v79
	v_fmac_f32_e32 v150, v78, v78
	v_fmac_f32_e32 v150, v80, v80
	v_fmac_f32_e32 v150, v81, v81
	v_fmac_f32_e32 v150, v74, v74
	v_fmac_f32_e32 v150, v75, v75
	v_fmac_f32_e32 v150, v76, v76
	v_fmac_f32_e32 v150, v77, v77
	v_mov_b32_e32 v151, v150
	v_add_u32_e32 v152, 48, v160
	s_nop 0
	v_permlane16_swap_b32_e32 v150, v151
	v_lshrrev_b32_e32 v138, 6, v152
	v_add_f32_e32 v150, v150, v151
	v_cndmask_b32_e64 v138, v152, v138, s[6:7]
	v_mov_b32_e32 v151, v150
	v_lshlrev_b32_e32 v138, 3, v138
	s_nop 0
	v_permlane32_swap_b32_e32 v150, v151
	v_and_b32_e32 v138, 0x1f8, v138
	v_cmp_gt_i32_e32 vcc, s64, v160
	v_add_f32_e32 v150, v150, v151
	v_fmamk_f32 v150, v150, 0x37000000, v187
	v_cndmask_b32_e32 v138, v188, v138, vcc
	v_lshlrev_b32_e32 v138, 2, v138
	v_rsq_f32_e32 v161, v150
	v_add_u32_e32 v139, v174, v138
	v_add_u32_e32 v138, v175, v138
	ds_read_b128 v[142:145], v139
	ds_read_b128 v[138:141], v138
	v_mul_f32_e32 v166, s52, v161
	v_pk_mul_f32 v[168:169], v[76:77], v[166:167] op_sel_hi:[1,0]
	v_pk_mul_f32 v[170:171], v[74:75], v[166:167] op_sel_hi:[1,0]
	v_ashrrev_i32_e32 v153, 31, v152
	v_pk_mul_f32 v[162:163], v[80:81], v[166:167] op_sel_hi:[1,0]
	v_pk_mul_f32 v[164:165], v[78:79], v[166:167] op_sel_hi:[1,0]
	v_pk_mul_f32 v[166:167], v[132:133], v[168:169]
	v_pk_mul_f32 v[168:169], v[130:131], v[170:171]
	v_lshlrev_b64 v[150:151], 8, v[152:153]
	v_pk_mul_f32 v[162:163], v[136:137], v[162:163]
	v_pk_mul_f32 v[164:165], v[134:135], v[164:165]
	s_waitcnt lgkmcnt(0)
	v_pk_mul_f32 v[170:171], v[140:141], v[166:167]
	v_pk_mul_f32 v[172:173], v[138:139], v[168:169]
	v_lshl_add_u64 v[150:151], v[146:147], 0, v[150:151]
	v_pk_fma_f32 v[170:171], v[144:145], v[162:163], v[170:171] neg_lo:[0,0,1] neg_hi:[0,0,1]
	v_pk_fma_f32 v[172:173], v[142:143], v[164:165], v[172:173] neg_lo:[0,0,1] neg_hi:[0,0,1]
	s_mov_b64 s[58:59], -1
	s_and_b64 vcc, exec, s[8:9]
	v_pk_mul_f32 v[168:169], v[142:143], v[168:169]
	s_cbranch_vccz .LBB0_1662
	s_nop 0
	v_cvt_pk_fp8_f32 v161, v172, v173
	v_pk_fma_f32 v[178:179], v[138:139], v[164:165], v[168:169]
	v_pk_mul_f32 v[176:177], v[144:145], v[166:167]
	s_mov_b64 s[58:59], 0
	v_cvt_pk_fp8_f32 v161, v170, v171 op_sel:[0,0,1]
	v_pk_fma_f32 v[176:177], v[140:141], v[162:163], v[176:177]
	global_store_dword v[150:151], v161, off
	s_nop 0
	v_cvt_pk_fp8_f32 v161, v178, v179
	v_cvt_pk_fp8_f32 v161, v176, v177 op_sel:[0,0,1]
	global_store_dword v[150:151], v161, off offset:8

; #define LAS __attribute__((address_space(3)))
; DI unsigned pk4_fp8(float a, float b, float c, float d) { int r = 0; r = __builtin_amdgcn_cvt_pk_fp8_f32(a, b, r, false); r = __builtin_amdgcn_cvt_pk_fp8_f32(c, d, r, true); return (unsigned)r; }
; DI void store8(bf16_t* p, f32x4 a) { u32x2 w; w.x = pk2(a[0], a[1]); w.y = pk2(a[2], a[3]); *(u32x2*)p = w; }
;     DI void head32x2(const AccT& acc, int rbase, int wc, int fq, bf16_t* dst, const float* gain, float scale, const bool F8) const {
;         LAS const float* cs8 = rope + 2 * 65 * 16; LAS const float* sn8 = cs8 + 65 * 8;
;         const int dbase = 16 * (fq >> 1) + 4 * (fq & 1);
;         const f32x4 g0 = *(const f32x4*)(gain + dbase), g1 = *(const f32x4*)(gain + dbase + 8);
; #pragma unroll
;         for (int ai = 0; ai < 2; ++ai)
; #pragma unroll
;             for (int m = 0; m < 4; ++m) {
;                 const int row = rbase + 128 * ai + 16 * m;
;                 const bool lat = row < NLAT; const int t = row & (SEQ - 1);
;                 const int pos = lat ? ((fq >> 1) ? (t & 63) : (t >> 6)) : 64;
;                 const f32x4 c = *(LAS const f32x4*)(cs8 + pos * 8 + 4 * (fq & 1)), sn = *(LAS const f32x4*)(sn8 + pos * 8 + 4 * (fq & 1));
; #pragma unroll
;                 for (int bj = 0; bj < 2; ++bj) {
;                     float ss = 0.f;
; #pragma unroll
;                     for (int n = 0; n < 2; ++n)
; #pragma unroll
;                         for (int i = 0; i < 4; ++i) ss += acc[ai][bj][m][n][i] * acc[ai][bj][m][n][i];
;                     ss = sum_x16_x32(ss);
;                     const float rinv = __builtin_amdgcn_rsqf(ss * (W8_INV * W8_INV / 32.0f) + EPS) * (scale * W8_INV);
;                     const f32x4 x1 = acc[ai][bj][m][0] * rinv * g0, x2 = acc[ai][bj][m][1] * rinv * g1;
;                     if (F8) { unsigned char* p8 = (unsigned char*)dst + (size_t)row * 256 + wc * 64 + 32 * bj + dbase; const f32x4 y1 = x1 * c - x2 * sn, y2 = x1 * sn + x2 * c;
;                         *(unsigned*)p8 = pk4_fp8(y1[0], y1[1], y1[2], y1[3]); *(unsigned*)(p8 + 8) = pk4_fp8(y2[0], y2[1], y2[2], y2[3]); }
;                     else { bf16_t* p = dst + (size_t)row * 256 + wc * 64 + 32 * bj + dbase;
;                         store8(p, x1 * c - x2 * sn); store8(p + 8, x1 * sn + x2 * c); }
;                 }
.LBB0_1664:
	v_mul_f32_e32 v161, v71, v71
	v_fmac_f32_e32 v161, v70, v70
	v_fmac_f32_e32 v161, v72, v72
	v_fmac_f32_e32 v161, v73, v73
	v_fmac_f32_e32 v161, v66, v66
	v_fmac_f32_e32 v161, v67, v67
	v_fmac_f32_e32 v161, v68, v68
	v_fmac_f32_e32 v161, v69, v69
	v_mov_b32_e32 v162, v161
	s_nop 1
	v_permlane16_swap_b32_e32 v161, v162
	v_add_f32_e32 v161, v161, v162
	v_mov_b32_e32 v162, v161
	s_nop 1
	v_permlane32_swap_b32_e32 v161, v162
	v_add_f32_e32 v161, v161, v162
	v_fmamk_f32 v161, v161, 0x37000000, v187
	v_rsq_f32_e32 v161, v161
	s_mov_b64 s[58:59], -1
	s_and_b64 vcc, exec, s[8:9]
	v_mul_f32_e32 v166, s52, v161
	v_pk_mul_f32 v[168:169], v[68:69], v[166:167] op_sel_hi:[1,0]
	v_pk_mul_f32 v[170:171], v[66:67], v[166:167] op_sel_hi:[1,0]
	v_pk_mul_f32 v[162:163], v[72:73], v[166:167] op_sel_hi:[1,0]
	v_pk_mul_f32 v[164:165], v[70:71], v[166:167] op_sel_hi:[1,0]
	v_pk_mul_f32 v[166:167], v[132:133], v[168:169]
	v_pk_mul_f32 v[172:173], v[130:131], v[170:171]
	v_pk_mul_f32 v[162:163], v[136:137], v[162:163]
	v_pk_mul_f32 v[164:165], v[134:135], v[164:165]
	v_pk_mul_f32 v[168:169], v[140:141], v[166:167]
	v_pk_mul_f32 v[170:171], v[138:139], v[172:173]
	v_pk_fma_f32 v[168:169], v[144:145], v[162:163], v[168:169] neg_lo:[0,0,1] neg_hi:[0,0,1]
	v_pk_fma_f32 v[170:171], v[142:143], v[164:165], v[170:171] neg_lo:[0,0,1] neg_hi:[0,0,1]
	v_pk_mul_f32 v[142:143], v[142:143], v[172:173]
	s_cbranch_vccz .LBB0_1666
	s_nop 0
	v_cvt_pk_fp8_f32 v161, v170, v171
	v_pk_fma_f32 v[176:177], v[138:139], v[164:165], v[142:143]
	v_pk_mul_f32 v[172:173], v[144:145], v[166:167]
	s_mov_b64 s[58:59], 0
	v_cvt_pk_fp8_f32 v161, v168, v169 op_sel:[0,0,1]
	v_pk_fma_f32 v[172:173], v[140:141], v[162:163], v[172:173]
	global_store_dword v[150:151], v161, off offset:32
	s_nop 0
	v_cvt_pk_fp8_f32 v161, v176, v177
	v_cvt_pk_fp8_f32 v161, v172, v173 op_sel:[0,0,1]
	global_store_dword v[150:151], v161, off offset:40

; #define LAS __attribute__((address_space(3)))
; DI unsigned pk4_fp8(float a, float b, float c, float d) { int r = 0; r = __builtin_amdgcn_cvt_pk_fp8_f32(a, b, r, false); r = __builtin_amdgcn_cvt_pk_fp8_f32(c, d, r, true); return (unsigned)r; }
; DI void store8(bf16_t* p, f32x4 a) { u32x2 w; w.x = pk2(a[0], a[1]); w.y = pk2(a[2], a[3]); *(u32x2*)p = w; }
;     DI void head32x2(const AccT& acc, int rbase, int wc, int fq, bf16_t* dst, const float* gain, float scale, const bool F8) const {
;         LAS const float* cs8 = rope + 2 * 65 * 16; LAS const float* sn8 = cs8 + 65 * 8;
;         const int dbase = 16 * (fq >> 1) + 4 * (fq & 1);
;         const f32x4 g0 = *(const f32x4*)(gain + dbase), g1 = *(const f32x4*)(gain + dbase + 8);
; #pragma unroll
;         for (int ai = 0; ai < 2; ++ai)
; #pragma unroll
;             for (int m = 0; m < 4; ++m) {
;                 const int row = rbase + 128 * ai + 16 * m;
;                 const bool lat = row < NLAT; const int t = row & (SEQ - 1);
;                 const int pos = lat ? ((fq >> 1) ? (t & 63) : (t >> 6)) : 64;
;                 const f32x4 c = *(LAS const f32x4*)(cs8 + pos * 8 + 4 * (fq & 1)), sn = *(LAS const f32x4*)(sn8 + pos * 8 + 4 * (fq & 1));
; #pragma unroll
;                 for (int bj = 0; bj < 2; ++bj) {
;                     float ss = 0.f;
; #pragma unroll
;                     for (int n = 0; n < 2; ++n)
; #pragma unroll
;                         for (int i = 0; i < 4; ++i) ss += acc[ai][bj][m][n][i] * acc[ai][bj][m][n][i];
;                     ss = sum_x16_x32(ss);
;                     const float rinv = __builtin_amdgcn_rsqf(ss * (W8_INV * W8_INV / 32.0f) + EPS) * (scale * W8_INV);
;                     const f32x4 x1 = acc[ai][bj][m][0] * rinv * g0, x2 = acc[ai][bj][m][1] * rinv * g1;
;                     if (F8) { unsigned char* p8 = (unsigned char*)dst + (size_t)row * 256 + wc * 64 + 32 * bj + dbase; const f32x4 y1 = x1 * c - x2 * sn, y2 = x1 * sn + x2 * c;
;                         *(unsigned*)p8 = pk4_fp8(y1[0], y1[1], y1[2], y1[3]); *(unsigned*)(p8 + 8) = pk4_fp8(y2[0], y2[1], y2[2], y2[3]); }
;                     else { bf16_t* p = dst + (size_t)row * 256 + wc * 64 + 32 * bj + dbase;
;                         store8(p, x1 * c - x2 * sn); store8(p + 8, x1 * sn + x2 * c); }
;                 }
.LBB0_1668:
	v_mul_f32_e32 v150, v63, v63
	v_fmac_f32_e32 v150, v62, v62
	v_fmac_f32_e32 v150, v64, v64
	v_fmac_f32_e32 v150, v65, v65
	v_fmac_f32_e32 v150, v58, v58
	v_fmac_f32_e32 v150, v59, v59
	v_fmac_f32_e32 v150, v60, v60
	v_fmac_f32_e32 v150, v61, v61
	v_mov_b32_e32 v151, v150
	v_add_u32_e32 v152, 0x80, v160
	s_nop 0
	v_permlane16_swap_b32_e32 v150, v151
	v_lshrrev_b32_e32 v138, 6, v152
	v_add_f32_e32 v150, v150, v151
	v_cndmask_b32_e64 v138, v190, v138, s[6:7]
	v_mov_b32_e32 v151, v150
	v_lshlrev_b32_e32 v138, 3, v138
	s_nop 0
	v_permlane32_swap_b32_e32 v150, v151
	v_and_b32_e32 v138, 0x1f8, v138
	v_cmp_gt_i32_e32 vcc, s65, v160
	v_add_f32_e32 v150, v150, v151
	v_fmamk_f32 v150, v150, 0x37000000, v187
	v_cndmask_b32_e32 v138, v188, v138, vcc
	v_lshlrev_b32_e32 v138, 2, v138
	v_rsq_f32_e32 v161, v150
	v_add_u32_e32 v139, v174, v138
	v_add_u32_e32 v138, v175, v138
	ds_read_b128 v[142:145], v139
	ds_read_b128 v[138:141], v138
	v_mul_f32_e32 v166, s52, v161
	v_pk_mul_f32 v[168:169], v[60:61], v[166:167] op_sel_hi:[1,0]
	v_pk_mul_f32 v[170:171], v[58:59], v[166:167] op_sel_hi:[1,0]
	v_ashrrev_i32_e32 v153, 31, v152
	v_pk_mul_f32 v[162:163], v[64:65], v[166:167] op_sel_hi:[1,0]
	v_pk_mul_f32 v[164:165], v[62:63], v[166:167] op_sel_hi:[1,0]
	v_pk_mul_f32 v[166:167], v[132:133], v[168:169]
	v_pk_mul_f32 v[168:169], v[130:131], v[170:171]
	v_lshlrev_b64 v[150:151], 8, v[152:153]
	v_pk_mul_f32 v[162:163], v[136:137], v[162:163]
	v_pk_mul_f32 v[164:165], v[134:135], v[164:165]
	s_waitcnt lgkmcnt(0)
	v_pk_mul_f32 v[170:171], v[140:141], v[166:167]
	v_pk_mul_f32 v[172:173], v[138:139], v[168:169]
	v_lshl_add_u64 v[150:151], v[146:147], 0, v[150:151]
	v_pk_fma_f32 v[170:171], v[144:145], v[162:163], v[170:171] neg_lo:[0,0,1] neg_hi:[0,0,1]
	v_pk_fma_f32 v[172:173], v[142:143], v[164:165], v[172:173] neg_lo:[0,0,1] neg_hi:[0,0,1]
	s_mov_b64 s[58:59], -1
	s_and_b64 vcc, exec, s[8:9]
	v_pk_mul_f32 v[168:169], v[142:143], v[168:169]
	s_cbranch_vccz .LBB0_1670
	s_nop 0
	v_cvt_pk_fp8_f32 v161, v172, v173
	v_pk_fma_f32 v[178:179], v[138:139], v[164:165], v[168:169]
	v_pk_mul_f32 v[176:177], v[144:145], v[166:167]
	s_mov_b64 s[58:59], 0
	v_cvt_pk_fp8_f32 v161, v170, v171 op_sel:[0,0,1]
	v_pk_fma_f32 v[176:177], v[140:141], v[162:163], v[176:177]
	global_store_dword v[150:151], v161, off
	s_nop 0
	v_cvt_pk_fp8_f32 v161, v178, v179
	v_cvt_pk_fp8_f32 v161, v176, v177 op_sel:[0,0,1]
	global_store_dword v[150:151], v161, off offset:8

; #define LAS __attribute__((address_space(3)))
; DI unsigned pk4_fp8(float a, float b, float c, float d) { int r = 0; r = __builtin_amdgcn_cvt_pk_fp8_f32(a, b, r, false); r = __builtin_amdgcn_cvt_pk_fp8_f32(c, d, r, true); return (unsigned)r; }
; DI void store8(bf16_t* p, f32x4 a) { u32x2 w; w.x = pk2(a[0], a[1]); w.y = pk2(a[2], a[3]); *(u32x2*)p = w; }
;     DI void head32x2(const AccT& acc, int rbase, int wc, int fq, bf16_t* dst, const float* gain, float scale, const bool F8) const {
;         LAS const float* cs8 = rope + 2 * 65 * 16; LAS const float* sn8 = cs8 + 65 * 8;
;         const int dbase = 16 * (fq >> 1) + 4 * (fq & 1);
;         const f32x4 g0 = *(const f32x4*)(gain + dbase), g1 = *(const f32x4*)(gain + dbase + 8);
; #pragma unroll
;         for (int ai = 0; ai < 2; ++ai)
; #pragma unroll
;             for (int m = 0; m < 4; ++m) {
;                 const int row = rbase + 128 * ai + 16 * m;
;                 const bool lat = row < NLAT; const int t = row & (SEQ - 1);
;                 const int pos = lat ? ((fq >> 1) ? (t & 63) : (t >> 6)) : 64;
;                 const f32x4 c = *(LAS const f32x4*)(cs8 + pos * 8 + 4 * (fq & 1)), sn = *(LAS const f32x4*)(sn8 + pos * 8 + 4 * (fq & 1));
; #pragma unroll
;                 for (int bj = 0; bj < 2; ++bj) {
;                     float ss = 0.f;
; #pragma unroll
;                     for (int n = 0; n < 2; ++n)
; #pragma unroll
;                         for (int i = 0; i < 4; ++i) ss += acc[ai][bj][m][n][i] * acc[ai][bj][m][n][i];
;                     ss = sum_x16_x32(ss);
;                     const float rinv = __builtin_amdgcn_rsqf(ss * (W8_INV * W8_INV / 32.0f) + EPS) * (scale * W8_INV);
;                     const f32x4 x1 = acc[ai][bj][m][0] * rinv * g0, x2 = acc[ai][bj][m][1] * rinv * g1;
;                     if (F8) { unsigned char* p8 = (unsigned char*)dst + (size_t)row * 256 + wc * 64 + 32 * bj + dbase; const f32x4 y1 = x1 * c - x2 * sn, y2 = x1 * sn + x2 * c;
;                         *(unsigned*)p8 = pk4_fp8(y1[0], y1[1], y1[2], y1[3]); *(unsigned*)(p8 + 8) = pk4_fp8(y2[0], y2[1], y2[2], y2[3]); }
;                     else { bf16_t* p = dst + (size_t)row * 256 + wc * 64 + 32 * bj + dbase;
;                         store8(p, x1 * c - x2 * sn); store8(p + 8, x1 * sn + x2 * c); }
;                 }
.LBB0_1672:
	v_mul_f32_e32 v161, v55, v55
	v_fmac_f32_e32 v161, v54, v54
	v_fmac_f32_e32 v161, v56, v56
	v_fmac_f32_e32 v161, v57, v57
	v_fmac_f32_e32 v161, v50, v50
	v_fmac_f32_e32 v161, v51, v51
	v_fmac_f32_e32 v161, v52, v52
	v_fmac_f32_e32 v161, v53, v53
	v_mov_b32_e32 v162, v161
	s_nop 1
	v_permlane16_swap_b32_e32 v161, v162
	v_add_f32_e32 v161, v161, v162
	v_mov_b32_e32 v162, v161
	s_nop 1
	v_permlane32_swap_b32_e32 v161, v162
	v_add_f32_e32 v161, v161, v162
	v_fmamk_f32 v161, v161, 0x37000000, v187
	v_rsq_f32_e32 v161, v161
	s_mov_b64 s[58:59], -1
	s_and_b64 vcc, exec, s[8:9]
	v_mul_f32_e32 v166, s52, v161
	v_pk_mul_f32 v[168:169], v[52:53], v[166:167] op_sel_hi:[1,0]
	v_pk_mul_f32 v[170:171], v[50:51], v[166:167] op_sel_hi:[1,0]
	v_pk_mul_f32 v[162:163], v[56:57], v[166:167] op_sel_hi:[1,0]
	v_pk_mul_f32 v[164:165], v[54:55], v[166:167] op_sel_hi:[1,0]
	v_pk_mul_f32 v[166:167], v[132:133], v[168:169]
	v_pk_mul_f32 v[172:173], v[130:131], v[170:171]
	v_pk_mul_f32 v[162:163], v[136:137], v[162:163]
	v_pk_mul_f32 v[164:165], v[134:135], v[164:165]
	v_pk_mul_f32 v[168:169], v[140:141], v[166:167]
	v_pk_mul_f32 v[170:171], v[138:139], v[172:173]
	v_pk_fma_f32 v[168:169], v[144:145], v[162:163], v[168:169] neg_lo:[0,0,1] neg_hi:[0,0,1]
	v_pk_fma_f32 v[170:171], v[142:143], v[164:165], v[170:171] neg_lo:[0,0,1] neg_hi:[0,0,1]
	v_pk_mul_f32 v[142:143], v[142:143], v[172:173]
	s_cbranch_vccz .LBB0_1674
	s_nop 0
	v_cvt_pk_fp8_f32 v161, v170, v171
	v_pk_fma_f32 v[176:177], v[138:139], v[164:165], v[142:143]
	v_pk_mul_f32 v[172:173], v[144:145], v[166:167]
	s_mov_b64 s[58:59], 0
	v_cvt_pk_fp8_f32 v161, v168, v169 op_sel:[0,0,1]
	v_pk_fma_f32 v[172:173], v[140:141], v[162:163], v[172:173]
	global_store_dword v[150:151], v161, off offset:32
	s_nop 0
	v_cvt_pk_fp8_f32 v161, v176, v177
	v_cvt_pk_fp8_f32 v161, v172, v173 op_sel:[0,0,1]
	global_store_dword v[150:151], v161, off offset:40

; #define LAS __attribute__((address_space(3)))
; DI unsigned pk4_fp8(float a, float b, float c, float d) { int r = 0; r = __builtin_amdgcn_cvt_pk_fp8_f32(a, b, r, false); r = __builtin_amdgcn_cvt_pk_fp8_f32(c, d, r, true); return (unsigned)r; }
; DI void store8(bf16_t* p, f32x4 a) { u32x2 w; w.x = pk2(a[0], a[1]); w.y = pk2(a[2], a[3]); *(u32x2*)p = w; }
;     DI void head32x2(const AccT& acc, int rbase, int wc, int fq, bf16_t* dst, const float* gain, float scale, const bool F8) const {
;         LAS const float* cs8 = rope + 2 * 65 * 16; LAS const float* sn8 = cs8 + 65 * 8;
;         const int dbase = 16 * (fq >> 1) + 4 * (fq & 1);
;         const f32x4 g0 = *(const f32x4*)(gain + dbase), g1 = *(const f32x4*)(gain + dbase + 8);
; #pragma unroll
;         for (int ai = 0; ai < 2; ++ai)
; #pragma unroll
;             for (int m = 0; m < 4; ++m) {
;                 const int row = rbase + 128 * ai + 16 * m;
;                 const bool lat = row < NLAT; const int t = row & (SEQ - 1);
;                 const int pos = lat ? ((fq >> 1) ? (t & 63) : (t >> 6)) : 64;
;                 const f32x4 c = *(LAS const f32x4*)(cs8 + pos * 8 + 4 * (fq & 1)), sn = *(LAS const f32x4*)(sn8 + pos * 8 + 4 * (fq & 1));
; #pragma unroll
;                 for (int bj = 0; bj < 2; ++bj) {
;                     float ss = 0.f;
; #pragma unroll
;                     for (int n = 0; n < 2; ++n)
; #pragma unroll
;                         for (int i = 0; i < 4; ++i) ss += acc[ai][bj][m][n][i] * acc[ai][bj][m][n][i];
;                     ss = sum_x16_x32(ss);
;                     const float rinv = __builtin_amdgcn_rsqf(ss * (W8_INV * W8_INV / 32.0f) + EPS) * (scale * W8_INV);
;                     const f32x4 x1 = acc[ai][bj][m][0] * rinv * g0, x2 = acc[ai][bj][m][1] * rinv * g1;
;                     if (F8) { unsigned char* p8 = (unsigned char*)dst + (size_t)row * 256 + wc * 64 + 32 * bj + dbase; const f32x4 y1 = x1 * c - x2 * sn, y2 = x1 * sn + x2 * c;
;                         *(unsigned*)p8 = pk4_fp8(y1[0], y1[1], y1[2], y1[3]); *(unsigned*)(p8 + 8) = pk4_fp8(y2[0], y2[1], y2[2], y2[3]); }
;                     else { bf16_t* p = dst + (size_t)row * 256 + wc * 64 + 32 * bj + dbase;
;                         store8(p, x1 * c - x2 * sn); store8(p + 8, x1 * sn + x2 * c); }
;                 }
.LBB0_1676:
	v_mul_f32_e32 v150, v47, v47
	v_fmac_f32_e32 v150, v46, v46
	v_fmac_f32_e32 v150, v48, v48
	v_fmac_f32_e32 v150, v49, v49
	v_fmac_f32_e32 v150, v42, v42
	v_fmac_f32_e32 v150, v43, v43
	v_fmac_f32_e32 v150, v44, v44
	v_fmac_f32_e32 v150, v45, v45
	v_mov_b32_e32 v151, v150
	v_add_u32_e32 v152, 0x90, v160
	s_nop 0
	v_permlane16_swap_b32_e32 v150, v151
	v_lshrrev_b32_e32 v138, 6, v152
	v_add_f32_e32 v150, v150, v151
	v_cndmask_b32_e64 v138, v152, v138, s[6:7]
	v_mov_b32_e32 v151, v150
	v_lshlrev_b32_e32 v138, 3, v138
	s_nop 0
	v_permlane32_swap_b32_e32 v150, v151
	v_and_b32_e32 v138, 0x1f8, v138
	v_cmp_gt_i32_e32 vcc, s66, v160
	v_add_f32_e32 v150, v150, v151
	v_fmamk_f32 v150, v150, 0x37000000, v187
	v_cndmask_b32_e32 v138, v188, v138, vcc
	v_lshlrev_b32_e32 v138, 2, v138
	v_rsq_f32_e32 v161, v150
	v_add_u32_e32 v139, v174, v138
	v_add_u32_e32 v138, v175, v138
	ds_read_b128 v[142:145], v139
	ds_read_b128 v[138:141], v138
	v_mul_f32_e32 v166, s52, v161
	v_pk_mul_f32 v[168:169], v[44:45], v[166:167] op_sel_hi:[1,0]
	v_pk_mul_f32 v[170:171], v[42:43], v[166:167] op_sel_hi:[1,0]
	v_ashrrev_i32_e32 v153, 31, v152
	v_pk_mul_f32 v[162:163], v[48:49], v[166:167] op_sel_hi:[1,0]
	v_pk_mul_f32 v[164:165], v[46:47], v[166:167] op_sel_hi:[1,0]
	v_pk_mul_f32 v[166:167], v[132:133], v[168:169]
	v_pk_mul_f32 v[168:169], v[130:131], v[170:171]
	v_lshlrev_b64 v[150:151], 8, v[152:153]
	v_pk_mul_f32 v[162:163], v[136:137], v[162:163]
	v_pk_mul_f32 v[164:165], v[134:135], v[164:165]
	s_waitcnt lgkmcnt(0)
	v_pk_mul_f32 v[170:171], v[140:141], v[166:167]
	v_pk_mul_f32 v[172:173], v[138:139], v[168:169]
	v_lshl_add_u64 v[150:151], v[146:147], 0, v[150:151]
	v_pk_fma_f32 v[170:171], v[144:145], v[162:163], v[170:171] neg_lo:[0,0,1] neg_hi:[0,0,1]
	v_pk_fma_f32 v[172:173], v[142:143], v[164:165], v[172:173] neg_lo:[0,0,1] neg_hi:[0,0,1]
	s_mov_b64 s[58:59], -1
	s_and_b64 vcc, exec, s[8:9]
	v_pk_mul_f32 v[168:169], v[142:143], v[168:169]
	s_cbranch_vccz .LBB0_1678
	s_nop 0
	v_cvt_pk_fp8_f32 v161, v172, v173
	v_pk_fma_f32 v[178:179], v[138:139], v[164:165], v[168:169]
	v_pk_mul_f32 v[176:177], v[144:145], v[166:167]
	s_mov_b64 s[58:59], 0
	v_cvt_pk_fp8_f32 v161, v170, v171 op_sel:[0,0,1]
	v_pk_fma_f32 v[176:177], v[140:141], v[162:163], v[176:177]
	global_store_dword v[150:151], v161, off
	s_nop 0
	v_cvt_pk_fp8_f32 v161, v178, v179
	v_cvt_pk_fp8_f32 v161, v176, v177 op_sel:[0,0,1]
	global_store_dword v[150:151], v161, off offset:8

; #define LAS __attribute__((address_space(3)))
; DI unsigned pk4_fp8(float a, float b, float c, float d) { int r = 0; r = __builtin_amdgcn_cvt_pk_fp8_f32(a, b, r, false); r = __builtin_amdgcn_cvt_pk_fp8_f32(c, d, r, true); return (unsigned)r; }
; DI void store8(bf16_t* p, f32x4 a) { u32x2 w; w.x = pk2(a[0], a[1]); w.y = pk2(a[2], a[3]); *(u32x2*)p = w; }
;     DI void head32x2(const AccT& acc, int rbase, int wc, int fq, bf16_t* dst, const float* gain, float scale, const bool F8) const {
;         LAS const float* cs8 = rope + 2 * 65 * 16; LAS const float* sn8 = cs8 + 65 * 8;
;         const int dbase = 16 * (fq >> 1) + 4 * (fq & 1);
;         const f32x4 g0 = *(const f32x4*)(gain + dbase), g1 = *(const f32x4*)(gain + dbase + 8);
; #pragma unroll
;         for (int ai = 0; ai < 2; ++ai)
; #pragma unroll
;             for (int m = 0; m < 4; ++m) {
;                 const int row = rbase + 128 * ai + 16 * m;
;                 const bool lat = row < NLAT; const int t = row & (SEQ - 1);
;                 const int pos = lat ? ((fq >> 1) ? (t & 63) : (t >> 6)) : 64;
;                 const f32x4 c = *(LAS const f32x4*)(cs8 + pos * 8 + 4 * (fq & 1)), sn = *(LAS const f32x4*)(sn8 + pos * 8 + 4 * (fq & 1));
; #pragma unroll
;                 for (int bj = 0; bj < 2; ++bj) {
;                     float ss = 0.f;
; #pragma unroll
;                     for (int n = 0; n < 2; ++n)
; #pragma unroll
;                         for (int i = 0; i < 4; ++i) ss += acc[ai][bj][m][n][i] * acc[ai][bj][m][n][i];
;                     ss = sum_x16_x32(ss);
;                     const float rinv = __builtin_amdgcn_rsqf(ss * (W8_INV * W8_INV / 32.0f) + EPS) * (scale * W8_INV);
;                     const f32x4 x1 = acc[ai][bj][m][0] * rinv * g0, x2 = acc[ai][bj][m][1] * rinv * g1;
;                     if (F8) { unsigned char* p8 = (unsigned char*)dst + (size_t)row * 256 + wc * 64 + 32 * bj + dbase; const f32x4 y1 = x1 * c - x2 * sn, y2 = x1 * sn + x2 * c;
;                         *(unsigned*)p8 = pk4_fp8(y1[0], y1[1], y1[2], y1[3]); *(unsigned*)(p8 + 8) = pk4_fp8(y2[0], y2[1], y2[2], y2[3]); }
;                     else { bf16_t* p = dst + (size_t)row * 256 + wc * 64 + 32 * bj + dbase;
;                         store8(p, x1 * c - x2 * sn); store8(p + 8, x1 * sn + x2 * c); }
;                 }
.LBB0_1680:
	v_mul_f32_e32 v161, v39, v39
	v_fmac_f32_e32 v161, v38, v38
	v_fmac_f32_e32 v161, v40, v40
	v_fmac_f32_e32 v161, v41, v41
	v_fmac_f32_e32 v161, v34, v34
	v_fmac_f32_e32 v161, v35, v35
	v_fmac_f32_e32 v161, v36, v36
	v_fmac_f32_e32 v161, v37, v37
	v_mov_b32_e32 v162, v161
	s_nop 1
	v_permlane16_swap_b32_e32 v161, v162
	v_add_f32_e32 v161, v161, v162
	v_mov_b32_e32 v162, v161
	s_nop 1
	v_permlane32_swap_b32_e32 v161, v162
	v_add_f32_e32 v161, v161, v162
	v_fmamk_f32 v161, v161, 0x37000000, v187
	v_rsq_f32_e32 v161, v161
	s_mov_b64 s[58:59], -1
	s_and_b64 vcc, exec, s[8:9]
	v_mul_f32_e32 v166, s52, v161
	v_pk_mul_f32 v[168:169], v[36:37], v[166:167] op_sel_hi:[1,0]
	v_pk_mul_f32 v[170:171], v[34:35], v[166:167] op_sel_hi:[1,0]
	v_pk_mul_f32 v[162:163], v[40:41], v[166:167] op_sel_hi:[1,0]
	v_pk_mul_f32 v[164:165], v[38:39], v[166:167] op_sel_hi:[1,0]
	v_pk_mul_f32 v[166:167], v[132:133], v[168:169]
	v_pk_mul_f32 v[172:173], v[130:131], v[170:171]
	v_pk_mul_f32 v[162:163], v[136:137], v[162:163]
	v_pk_mul_f32 v[164:165], v[134:135], v[164:165]
	v_pk_mul_f32 v[168:169], v[140:141], v[166:167]
	v_pk_mul_f32 v[170:171], v[138:139], v[172:173]
	v_pk_fma_f32 v[168:169], v[144:145], v[162:163], v[168:169] neg_lo:[0,0,1] neg_hi:[0,0,1]
	v_pk_fma_f32 v[170:171], v[142:143], v[164:165], v[170:171] neg_lo:[0,0,1] neg_hi:[0,0,1]
	v_pk_mul_f32 v[142:143], v[142:143], v[172:173]
	s_cbranch_vccz .LBB0_1682
	s_nop 0
	v_cvt_pk_fp8_f32 v161, v170, v171
	v_pk_fma_f32 v[176:177], v[138:139], v[164:165], v[142:143]
	v_pk_mul_f32 v[172:173], v[144:145], v[166:167]
	s_mov_b64 s[58:59], 0
	v_cvt_pk_fp8_f32 v161, v168, v169 op_sel:[0,0,1]
	v_pk_fma_f32 v[172:173], v[140:141], v[162:163], v[172:173]
	global_store_dword v[150:151], v161, off offset:32
	s_nop 0
	v_cvt_pk_fp8_f32 v161, v176, v177
	v_cvt_pk_fp8_f32 v161, v172, v173 op_sel:[0,0,1]
	global_store_dword v[150:151], v161, off offset:40

; #define LAS __attribute__((address_space(3)))
; DI unsigned pk4_fp8(float a, float b, float c, float d) { int r = 0; r = __builtin_amdgcn_cvt_pk_fp8_f32(a, b, r, false); r = __builtin_amdgcn_cvt_pk_fp8_f32(c, d, r, true); return (unsigned)r; }
; DI void store8(bf16_t* p, f32x4 a) { u32x2 w; w.x = pk2(a[0], a[1]); w.y = pk2(a[2], a[3]); *(u32x2*)p = w; }
;     DI void head32x2(const AccT& acc, int rbase, int wc, int fq, bf16_t* dst, const float* gain, float scale, const bool F8) const {
;         LAS const float* cs8 = rope + 2 * 65 * 16; LAS const float* sn8 = cs8 + 65 * 8;
;         const int dbase = 16 * (fq >> 1) + 4 * (fq & 1);
;         const f32x4 g0 = *(const f32x4*)(gain + dbase), g1 = *(const f32x4*)(gain + dbase + 8);
; #pragma unroll
;         for (int ai = 0; ai < 2; ++ai)
; #pragma unroll
;             for (int m = 0; m < 4; ++m) {
;                 const int row = rbase + 128 * ai + 16 * m;
;                 const bool lat = row < NLAT; const int t = row & (SEQ - 1);
;                 const int pos = lat ? ((fq >> 1) ? (t & 63) : (t >> 6)) : 64;
;                 const f32x4 c = *(LAS const f32x4*)(cs8 + pos * 8 + 4 * (fq & 1)), sn = *(LAS const f32x4*)(sn8 + pos * 8 + 4 * (fq & 1));
; #pragma unroll
;                 for (int bj = 0; bj < 2; ++bj) {
;                     float ss = 0.f;
; #pragma unroll
;                     for (int n = 0; n < 2; ++n)
; #pragma unroll
;                         for (int i = 0; i < 4; ++i) ss += acc[ai][bj][m][n][i] * acc[ai][bj][m][n][i];
;                     ss = sum_x16_x32(ss);
;                     const float rinv = __builtin_amdgcn_rsqf(ss * (W8_INV * W8_INV / 32.0f) + EPS) * (scale * W8_INV);
;                     const f32x4 x1 = acc[ai][bj][m][0] * rinv * g0, x2 = acc[ai][bj][m][1] * rinv * g1;
;                     if (F8) { unsigned char* p8 = (unsigned char*)dst + (size_t)row * 256 + wc * 64 + 32 * bj + dbase; const f32x4 y1 = x1 * c - x2 * sn, y2 = x1 * sn + x2 * c;
;                         *(unsigned*)p8 = pk4_fp8(y1[0], y1[1], y1[2], y1[3]); *(unsigned*)(p8 + 8) = pk4_fp8(y2[0], y2[1], y2[2], y2[3]); }
;                     else { bf16_t* p = dst + (size_t)row * 256 + wc * 64 + 32 * bj + dbase;
;                         store8(p, x1 * c - x2 * sn); store8(p + 8, x1 * sn + x2 * c); }
;                 }
.LBB0_1684:
	v_mul_f32_e32 v150, v31, v31
	v_fmac_f32_e32 v150, v30, v30
	v_fmac_f32_e32 v150, v32, v32
	v_fmac_f32_e32 v150, v33, v33
	v_fmac_f32_e32 v150, v26, v26
	v_fmac_f32_e32 v150, v27, v27
	v_fmac_f32_e32 v150, v28, v28
	v_fmac_f32_e32 v150, v29, v29
	v_mov_b32_e32 v151, v150
	v_add_u32_e32 v152, 0xa0, v160
	s_nop 0
	v_permlane16_swap_b32_e32 v150, v151
	v_lshrrev_b32_e32 v138, 6, v152
	v_add_f32_e32 v150, v150, v151
	v_cndmask_b32_e64 v138, v152, v138, s[6:7]
	v_mov_b32_e32 v151, v150
	v_lshlrev_b32_e32 v138, 3, v138
	s_nop 0
	v_permlane32_swap_b32_e32 v150, v151
	v_and_b32_e32 v138, 0x1f8, v138
	v_cmp_gt_i32_e32 vcc, s4, v160
	v_add_f32_e32 v150, v150, v151
	v_fmamk_f32 v150, v150, 0x37000000, v187
	v_cndmask_b32_e32 v138, v188, v138, vcc
	v_lshlrev_b32_e32 v138, 2, v138
	v_rsq_f32_e32 v161, v150
	v_add_u32_e32 v139, v174, v138
	v_add_u32_e32 v138, v175, v138
	ds_read_b128 v[142:145], v139
	ds_read_b128 v[138:141], v138
	v_mul_f32_e32 v166, s52, v161
	v_pk_mul_f32 v[168:169], v[28:29], v[166:167] op_sel_hi:[1,0]
	v_pk_mul_f32 v[170:171], v[26:27], v[166:167] op_sel_hi:[1,0]
	v_ashrrev_i32_e32 v153, 31, v152
	v_pk_mul_f32 v[162:163], v[32:33], v[166:167] op_sel_hi:[1,0]
	v_pk_mul_f32 v[164:165], v[30:31], v[166:167] op_sel_hi:[1,0]
	v_pk_mul_f32 v[166:167], v[132:133], v[168:169]
	v_pk_mul_f32 v[168:169], v[130:131], v[170:171]
	v_lshlrev_b64 v[150:151], 8, v[152:153]
	v_pk_mul_f32 v[162:163], v[136:137], v[162:163]
	v_pk_mul_f32 v[164:165], v[134:135], v[164:165]
	s_waitcnt lgkmcnt(0)
	v_pk_mul_f32 v[170:171], v[140:141], v[166:167]
	v_pk_mul_f32 v[172:173], v[138:139], v[168:169]
	v_lshl_add_u64 v[150:151], v[146:147], 0, v[150:151]
	v_pk_fma_f32 v[170:171], v[144:145], v[162:163], v[170:171] neg_lo:[0,0,1] neg_hi:[0,0,1]
	v_pk_fma_f32 v[172:173], v[142:143], v[164:165], v[172:173] neg_lo:[0,0,1] neg_hi:[0,0,1]
	s_mov_b64 s[58:59], -1
	s_and_b64 vcc, exec, s[8:9]
	v_pk_mul_f32 v[168:169], v[142:143], v[168:169]
	s_cbranch_vccz .LBB0_1686
	s_nop 0
	v_cvt_pk_fp8_f32 v161, v172, v173
	v_pk_fma_f32 v[178:179], v[138:139], v[164:165], v[168:169]
	v_pk_mul_f32 v[176:177], v[144:145], v[166:167]
	s_mov_b64 s[58:59], 0
	v_cvt_pk_fp8_f32 v161, v170, v171 op_sel:[0,0,1]
	v_pk_fma_f32 v[176:177], v[140:141], v[162:163], v[176:177]
	global_store_dword v[150:151], v161, off
	s_nop 0
	v_cvt_pk_fp8_f32 v161, v178, v179
	v_cvt_pk_fp8_f32 v161, v176, v177 op_sel:[0,0,1]
	global_store_dword v[150:151], v161, off offset:8

; #define LAS __attribute__((address_space(3)))
; DI unsigned pk4_fp8(float a, float b, float c, float d) { int r = 0; r = __builtin_amdgcn_cvt_pk_fp8_f32(a, b, r, false); r = __builtin_amdgcn_cvt_pk_fp8_f32(c, d, r, true); return (unsigned)r; }
; DI void store8(bf16_t* p, f32x4 a) { u32x2 w; w.x = pk2(a[0], a[1]); w.y = pk2(a[2], a[3]); *(u32x2*)p = w; }
;     DI void head32x2(const AccT& acc, int rbase, int wc, int fq, bf16_t* dst, const float* gain, float scale, const bool F8) const {
;         LAS const float* cs8 = rope + 2 * 65 * 16; LAS const float* sn8 = cs8 + 65 * 8;
;         const int dbase = 16 * (fq >> 1) + 4 * (fq & 1);
;         const f32x4 g0 = *(const f32x4*)(gain + dbase), g1 = *(const f32x4*)(gain + dbase + 8);
; #pragma unroll
;         for (int ai = 0; ai < 2; ++ai)
; #pragma unroll
;             for (int m = 0; m < 4; ++m) {
;                 const int row = rbase + 128 * ai + 16 * m;
;                 const bool lat = row < NLAT; const int t = row & (SEQ - 1);
;                 const int pos = lat ? ((fq >> 1) ? (t & 63) : (t >> 6)) : 64;
;                 const f32x4 c = *(LAS const f32x4*)(cs8 + pos * 8 + 4 * (fq & 1)), sn = *(LAS const f32x4*)(sn8 + pos * 8 + 4 * (fq & 1));
; #pragma unroll
;                 for (int bj = 0; bj < 2; ++bj) {
;                     float ss = 0.f;
; #pragma unroll
;                     for (int n = 0; n < 2; ++n)
; #pragma unroll
;                         for (int i = 0; i < 4; ++i) ss += acc[ai][bj][m][n][i] * acc[ai][bj][m][n][i];
;                     ss = sum_x16_x32(ss);
;                     const float rinv = __builtin_amdgcn_rsqf(ss * (W8_INV * W8_INV / 32.0f) + EPS) * (scale * W8_INV);
;                     const f32x4 x1 = acc[ai][bj][m][0] * rinv * g0, x2 = acc[ai][bj][m][1] * rinv * g1;
;                     if (F8) { unsigned char* p8 = (unsigned char*)dst + (size_t)row * 256 + wc * 64 + 32 * bj + dbase; const f32x4 y1 = x1 * c - x2 * sn, y2 = x1 * sn + x2 * c;
;                         *(unsigned*)p8 = pk4_fp8(y1[0], y1[1], y1[2], y1[3]); *(unsigned*)(p8 + 8) = pk4_fp8(y2[0], y2[1], y2[2], y2[3]); }
;                     else { bf16_t* p = dst + (size_t)row * 256 + wc * 64 + 32 * bj + dbase;
;                         store8(p, x1 * c - x2 * sn); store8(p + 8, x1 * sn + x2 * c); }
;                 }
.LBB0_1688:
	v_mul_f32_e32 v161, v23, v23
	v_fmac_f32_e32 v161, v22, v22
	v_fmac_f32_e32 v161, v24, v24
	v_fmac_f32_e32 v161, v25, v25
	v_fmac_f32_e32 v161, v18, v18
	v_fmac_f32_e32 v161, v19, v19
	v_fmac_f32_e32 v161, v20, v20
	v_fmac_f32_e32 v161, v21, v21
	v_mov_b32_e32 v162, v161
	s_nop 1
	v_permlane16_swap_b32_e32 v161, v162
	v_add_f32_e32 v161, v161, v162
	v_mov_b32_e32 v162, v161
	s_nop 1
	v_permlane32_swap_b32_e32 v161, v162
	v_add_f32_e32 v161, v161, v162
	v_fmamk_f32 v161, v161, 0x37000000, v187
	v_rsq_f32_e32 v161, v161
	s_mov_b64 s[58:59], -1
	s_and_b64 vcc, exec, s[8:9]
	v_mul_f32_e32 v166, s52, v161
	v_pk_mul_f32 v[168:169], v[20:21], v[166:167] op_sel_hi:[1,0]
	v_pk_mul_f32 v[170:171], v[18:19], v[166:167] op_sel_hi:[1,0]
	v_pk_mul_f32 v[162:163], v[24:25], v[166:167] op_sel_hi:[1,0]
	v_pk_mul_f32 v[164:165], v[22:23], v[166:167] op_sel_hi:[1,0]
	v_pk_mul_f32 v[166:167], v[132:133], v[168:169]
	v_pk_mul_f32 v[172:173], v[130:131], v[170:171]
	v_pk_mul_f32 v[162:163], v[136:137], v[162:163]
	v_pk_mul_f32 v[164:165], v[134:135], v[164:165]
	v_pk_mul_f32 v[168:169], v[140:141], v[166:167]
	v_pk_mul_f32 v[170:171], v[138:139], v[172:173]
	v_pk_fma_f32 v[168:169], v[144:145], v[162:163], v[168:169] neg_lo:[0,0,1] neg_hi:[0,0,1]
	v_pk_fma_f32 v[170:171], v[142:143], v[164:165], v[170:171] neg_lo:[0,0,1] neg_hi:[0,0,1]
	v_pk_mul_f32 v[142:143], v[142:143], v[172:173]
	s_cbranch_vccz .LBB0_1690
	s_nop 0
	v_cvt_pk_fp8_f32 v161, v170, v171
	v_pk_fma_f32 v[176:177], v[138:139], v[164:165], v[142:143]
	v_pk_mul_f32 v[172:173], v[144:145], v[166:167]
	s_mov_b64 s[58:59], 0
	v_cvt_pk_fp8_f32 v161, v168, v169 op_sel:[0,0,1]
	v_pk_fma_f32 v[172:173], v[140:141], v[162:163], v[172:173]
	global_store_dword v[150:151], v161, off offset:32
	s_nop 0
	v_cvt_pk_fp8_f32 v161, v176, v177
	v_cvt_pk_fp8_f32 v161, v172, v173 op_sel:[0,0,1]
	global_store_dword v[150:151], v161, off offset:40

; #define LAS __attribute__((address_space(3)))
; DI unsigned pk4_fp8(float a, float b, float c, float d) { int r = 0; r = __builtin_amdgcn_cvt_pk_fp8_f32(a, b, r, false); r = __builtin_amdgcn_cvt_pk_fp8_f32(c, d, r, true); return (unsigned)r; }
; DI void store8(bf16_t* p, f32x4 a) { u32x2 w; w.x = pk2(a[0], a[1]); w.y = pk2(a[2], a[3]); *(u32x2*)p = w; }
;     DI void head32x2(const AccT& acc, int rbase, int wc, int fq, bf16_t* dst, const float* gain, float scale, const bool F8) const {
;         LAS const float* cs8 = rope + 2 * 65 * 16; LAS const float* sn8 = cs8 + 65 * 8;
;         const int dbase = 16 * (fq >> 1) + 4 * (fq & 1);
;         const f32x4 g0 = *(const f32x4*)(gain + dbase), g1 = *(const f32x4*)(gain + dbase + 8);
; #pragma unroll
;         for (int ai = 0; ai < 2; ++ai)
; #pragma unroll
;             for (int m = 0; m < 4; ++m) {
;                 const int row = rbase + 128 * ai + 16 * m;
;                 const bool lat = row < NLAT; const int t = row & (SEQ - 1);
;                 const int pos = lat ? ((fq >> 1) ? (t & 63) : (t >> 6)) : 64;
;                 const f32x4 c = *(LAS const f32x4*)(cs8 + pos * 8 + 4 * (fq & 1)), sn = *(LAS const f32x4*)(sn8 + pos * 8 + 4 * (fq & 1));
; #pragma unroll
;                 for (int bj = 0; bj < 2; ++bj) {
;                     float ss = 0.f;
; #pragma unroll
;                     for (int n = 0; n < 2; ++n)
; #pragma unroll
;                         for (int i = 0; i < 4; ++i) ss += acc[ai][bj][m][n][i] * acc[ai][bj][m][n][i];
;                     ss = sum_x16_x32(ss);
;                     const float rinv = __builtin_amdgcn_rsqf(ss * (W8_INV * W8_INV / 32.0f) + EPS) * (scale * W8_INV);
;                     const f32x4 x1 = acc[ai][bj][m][0] * rinv * g0, x2 = acc[ai][bj][m][1] * rinv * g1;
;                     if (F8) { unsigned char* p8 = (unsigned char*)dst + (size_t)row * 256 + wc * 64 + 32 * bj + dbase; const f32x4 y1 = x1 * c - x2 * sn, y2 = x1 * sn + x2 * c;
;                         *(unsigned*)p8 = pk4_fp8(y1[0], y1[1], y1[2], y1[3]); *(unsigned*)(p8 + 8) = pk4_fp8(y2[0], y2[1], y2[2], y2[3]); }
;                     else { bf16_t* p = dst + (size_t)row * 256 + wc * 64 + 32 * bj + dbase;
;                         store8(p, x1 * c - x2 * sn); store8(p + 8, x1 * sn + x2 * c); }
;                 }
.LBB0_1692:
	v_mul_f32_e32 v151, v15, v15
	v_fmac_f32_e32 v151, v14, v14
	v_fmac_f32_e32 v151, v16, v16
	v_fmac_f32_e32 v151, v17, v17
	v_fmac_f32_e32 v151, v10, v10
	v_fmac_f32_e32 v151, v11, v11
	v_fmac_f32_e32 v151, v12, v12
	v_fmac_f32_e32 v151, v13, v13
	v_mov_b32_e32 v152, v151
	v_add_u32_e32 v150, 0xb0, v160
	s_nop 0
	v_permlane16_swap_b32_e32 v151, v152
	v_lshrrev_b32_e32 v138, 6, v150
	v_add_f32_e32 v151, v151, v152
	v_cndmask_b32_e64 v138, v150, v138, s[6:7]
	v_mov_b32_e32 v152, v151
	v_lshlrev_b32_e32 v138, 3, v138
	s_nop 0
	v_permlane32_swap_b32_e32 v151, v152
	v_and_b32_e32 v138, 0x1f8, v138
	v_cmp_gt_i32_e32 vcc, s5, v160
	v_add_f32_e32 v151, v151, v152
	v_fmamk_f32 v151, v151, 0x37000000, v187
	v_cndmask_b32_e32 v138, v188, v138, vcc
	v_lshlrev_b32_e32 v138, 2, v138
	v_rsq_f32_e32 v161, v151
	v_add_u32_e32 v139, v174, v138
	v_add_u32_e32 v138, v175, v138
	ds_read_b128 v[142:145], v139
	ds_read_b128 v[138:141], v138
	v_ashrrev_i32_e32 v151, 31, v150
	v_mul_f32_e32 v164, s52, v161
	v_lshlrev_b64 v[152:153], 8, v[150:151]
	v_pk_mul_f32 v[166:167], v[12:13], v[164:165] op_sel_hi:[1,0]
	v_pk_mul_f32 v[168:169], v[10:11], v[164:165] op_sel_hi:[1,0]
	v_lshl_add_u64 v[146:147], v[146:147], 0, v[152:153]
	v_pk_mul_f32 v[152:153], v[16:17], v[164:165] op_sel_hi:[1,0]
	v_pk_mul_f32 v[162:163], v[14:15], v[164:165] op_sel_hi:[1,0]
	v_pk_mul_f32 v[164:165], v[132:133], v[166:167]
	v_pk_mul_f32 v[166:167], v[130:131], v[168:169]
	v_pk_mul_f32 v[152:153], v[136:137], v[152:153]
	v_pk_mul_f32 v[162:163], v[134:135], v[162:163]
	s_waitcnt lgkmcnt(0)
	v_pk_mul_f32 v[168:169], v[140:141], v[164:165]
	v_pk_mul_f32 v[170:171], v[138:139], v[166:167]
	v_pk_fma_f32 v[168:169], v[144:145], v[152:153], v[168:169] neg_lo:[0,0,1] neg_hi:[0,0,1]
	v_pk_fma_f32 v[170:171], v[142:143], v[162:163], v[170:171] neg_lo:[0,0,1] neg_hi:[0,0,1]
	s_mov_b64 s[6:7], -1
	s_and_b64 vcc, exec, s[8:9]
	v_pk_mul_f32 v[166:167], v[142:143], v[166:167]
	s_cbranch_vccz .LBB0_1694
	s_nop 0
	v_cvt_pk_fp8_f32 v161, v170, v171
	v_pk_fma_f32 v[174:175], v[138:139], v[162:163], v[166:167]
	v_pk_mul_f32 v[172:173], v[144:145], v[164:165]
	s_mov_b64 s[6:7], 0
	v_cvt_pk_fp8_f32 v161, v168, v169 op_sel:[0,0,1]
	v_pk_fma_f32 v[172:173], v[140:141], v[152:153], v[172:173]
	global_store_dword v[146:147], v161, off
	s_nop 0
	v_cvt_pk_fp8_f32 v161, v174, v175
	v_cvt_pk_fp8_f32 v161, v172, v173 op_sel:[0,0,1]
	global_store_dword v[146:147], v161, off offset:8

; #define LAS __attribute__((address_space(3)))
; DI unsigned pk4_fp8(float a, float b, float c, float d) { int r = 0; r = __builtin_amdgcn_cvt_pk_fp8_f32(a, b, r, false); r = __builtin_amdgcn_cvt_pk_fp8_f32(c, d, r, true); return (unsigned)r; }
; DI void store8(bf16_t* p, f32x4 a) { u32x2 w; w.x = pk2(a[0], a[1]); w.y = pk2(a[2], a[3]); *(u32x2*)p = w; }
;     DI void head32x2(const AccT& acc, int rbase, int wc, int fq, bf16_t* dst, const float* gain, float scale, const bool F8) const {
;         LAS const float* cs8 = rope + 2 * 65 * 16; LAS const float* sn8 = cs8 + 65 * 8;
;         const int dbase = 16 * (fq >> 1) + 4 * (fq & 1);
;         const f32x4 g0 = *(const f32x4*)(gain + dbase), g1 = *(const f32x4*)(gain + dbase + 8);
; #pragma unroll
;         for (int ai = 0; ai < 2; ++ai)
; #pragma unroll
;             for (int m = 0; m < 4; ++m) {
;                 const int row = rbase + 128 * ai + 16 * m;
;                 const bool lat = row < NLAT; const int t = row & (SEQ - 1);
;                 const int pos = lat ? ((fq >> 1) ? (t & 63) : (t >> 6)) : 64;
;                 const f32x4 c = *(LAS const f32x4*)(cs8 + pos * 8 + 4 * (fq & 1)), sn = *(LAS const f32x4*)(sn8 + pos * 8 + 4 * (fq & 1));
; #pragma unroll
;                 for (int bj = 0; bj < 2; ++bj) {
;                     float ss = 0.f;
; #pragma unroll
;                     for (int n = 0; n < 2; ++n)
; #pragma unroll
;                         for (int i = 0; i < 4; ++i) ss += acc[ai][bj][m][n][i] * acc[ai][bj][m][n][i];
;                     ss = sum_x16_x32(ss);
;                     const float rinv = __builtin_amdgcn_rsqf(ss * (W8_INV * W8_INV / 32.0f) + EPS) * (scale * W8_INV);
;                     const f32x4 x1 = acc[ai][bj][m][0] * rinv * g0, x2 = acc[ai][bj][m][1] * rinv * g1;
;                     if (F8) { unsigned char* p8 = (unsigned char*)dst + (size_t)row * 256 + wc * 64 + 32 * bj + dbase; const f32x4 y1 = x1 * c - x2 * sn, y2 = x1 * sn + x2 * c;
;                         *(unsigned*)p8 = pk4_fp8(y1[0], y1[1], y1[2], y1[3]); *(unsigned*)(p8 + 8) = pk4_fp8(y2[0], y2[1], y2[2], y2[3]); }
;                     else { bf16_t* p = dst + (size_t)row * 256 + wc * 64 + 32 * bj + dbase;
;                         store8(p, x1 * c - x2 * sn); store8(p + 8, x1 * sn + x2 * c); }
;                 }
.LBB0_1696:
	v_mul_f32_e32 v150, v7, v7
	v_fmac_f32_e32 v150, v6, v6
	v_fmac_f32_e32 v150, v8, v8
	v_fmac_f32_e32 v150, v9, v9
	v_fmac_f32_e32 v150, v2, v2
	v_fmac_f32_e32 v150, v3, v3
	v_fmac_f32_e32 v150, v4, v4
	v_fmac_f32_e32 v150, v5, v5
	v_mov_b32_e32 v151, v150
	s_nop 1
	v_permlane16_swap_b32_e32 v150, v151
	v_add_f32_e32 v150, v150, v151
	v_mov_b32_e32 v151, v150
	s_nop 1
	v_permlane32_swap_b32_e32 v150, v151
	v_add_f32_e32 v150, v150, v151
	v_fmamk_f32 v150, v150, 0x37000000, v187
	v_rsq_f32_e32 v150, v150
	s_mov_b64 s[6:7], -1
	s_and_b64 vcc, exec, s[8:9]
	v_mul_f32_e32 v150, s52, v150
	v_pk_mul_f32 v[152:153], v[8:9], v[150:151] op_sel_hi:[1,0]
	v_pk_mul_f32 v[162:163], v[6:7], v[150:151] op_sel_hi:[1,0]
	v_pk_mul_f32 v[136:137], v[136:137], v[152:153]
	v_pk_mul_f32 v[152:153], v[4:5], v[150:151] op_sel_hi:[1,0]
	v_pk_mul_f32 v[150:151], v[2:3], v[150:151] op_sel_hi:[1,0]
	v_pk_mul_f32 v[132:133], v[132:133], v[152:153]
	v_pk_mul_f32 v[130:131], v[130:131], v[150:151]
	v_pk_mul_f32 v[134:135], v[134:135], v[162:163]
	v_pk_mul_f32 v[150:151], v[140:141], v[132:133]
	v_pk_mul_f32 v[152:153], v[138:139], v[130:131]
	v_pk_fma_f32 v[150:151], v[144:145], v[136:137], v[150:151] neg_lo:[0,0,1] neg_hi:[0,0,1]
	v_pk_fma_f32 v[152:153], v[142:143], v[134:135], v[152:153] neg_lo:[0,0,1] neg_hi:[0,0,1]
	v_pk_mul_f32 v[130:131], v[142:143], v[130:131]
	s_cbranch_vccz .LBB0_1698
	s_nop 0
	v_cvt_pk_fp8_f32 v161, v152, v153
	v_pk_fma_f32 v[162:163], v[138:139], v[134:135], v[130:131]
	v_pk_mul_f32 v[142:143], v[144:145], v[132:133]
	s_mov_b64 s[6:7], 0
	v_cvt_pk_fp8_f32 v161, v150, v151 op_sel:[0,0,1]
	v_pk_fma_f32 v[142:143], v[140:141], v[136:137], v[142:143]
	global_store_dword v[146:147], v161, off offset:32
	s_nop 0
	v_cvt_pk_fp8_f32 v161, v162, v163
	v_cvt_pk_fp8_f32 v161, v142, v143 op_sel:[0,0,1]
	global_store_dword v[146:147], v161, off offset:40

; #define LAS __attribute__((address_space(3)))
; DI unsigned pk4_fp8(float a, float b, float c, float d) { int r = 0; r = __builtin_amdgcn_cvt_pk_fp8_f32(a, b, r, false); r = __builtin_amdgcn_cvt_pk_fp8_f32(c, d, r, true); return (unsigned)r; }
;     DI void head64(const AccT& acc, int rbase, int wc, int fq, bf16_t* dst, int pitch, const float* gain, float scale, const bool F8) const {
;     ...
;                 for (int bj = 0; bj < 2; ++bj) {
;                     const f32x4 x1 = acc[ai][bj][m][0] * rinv * g[bj][0], x2 = acc[ai][bj][m][1] * rinv * g[bj][1];
;                     const int pos = lat ? (bj ? (t & 63) : (t >> 6)) : 64;
;                     const f32x4 c = *(LAS const f32x4*)(cs16 + pos * 16 + 4 * fq), sn = *(LAS const f32x4*)(sn16 + pos * 16 + 4 * fq);
;                     if (F8) { unsigned char* p8 = (unsigned char*)dst + (size_t)row * pitch + wc * 64 + 32 * bj + 4 * fq; const f32x4 y1 = x1 * c - x2 * sn, y2 = x1 * sn + x2 * c;
;                         *(unsigned*)p8 = pk4_fp8(y1[0], y1[1], y1[2], y1[3]); *(unsigned*)(p8 + 16) = pk4_fp8(y2[0], y2[1], y2[2], y2[3]); }
.LBB0_1716:
	v_lshl_add_u64 v[164:165], s[58:59], 0, v[164:165]
	s_andn2_b64 vcc, exec, s[60:61]
	v_lshl_add_u64 v[176:177], v[164:165], 0, v[176:177]
	s_cbranch_vccnz .LBB0_1718
	v_pk_fma_f32 v[146:147], v[146:147], v[174:175], v[150:151]
	s_nop 0
	v_cvt_pk_fp8_f32 v150, v182, v183
	s_nop 0
	v_cvt_pk_fp8_f32 v151, v146, v147
	v_pk_mul_f32 v[146:147], v[152:153], v[170:171]
	v_cvt_pk_fp8_f32 v150, v178, v179 op_sel:[0,0,1]
	v_pk_fma_f32 v[146:147], v[148:149], v[172:173], v[146:147]
	s_nop 0
	v_cvt_pk_fp8_f32 v151, v146, v147 op_sel:[0,0,1]
	global_store_dword v[176:177], v150, off
	global_store_dword v[176:177], v151, off offset:16

; #define LAS __attribute__((address_space(3)))
; DI unsigned pk4_fp8(float a, float b, float c, float d) { int r = 0; r = __builtin_amdgcn_cvt_pk_fp8_f32(a, b, r, false); r = __builtin_amdgcn_cvt_pk_fp8_f32(c, d, r, true); return (unsigned)r; }
;     DI void head64(const AccT& acc, int rbase, int wc, int fq, bf16_t* dst, int pitch, const float* gain, float scale, const bool F8) const {
;     ...
;                 for (int bj = 0; bj < 2; ++bj) {
;                     const f32x4 x1 = acc[ai][bj][m][0] * rinv * g[bj][0], x2 = acc[ai][bj][m][1] * rinv * g[bj][1];
;                     const int pos = lat ? (bj ? (t & 63) : (t >> 6)) : 64;
;                     const f32x4 c = *(LAS const f32x4*)(cs16 + pos * 16 + 4 * fq), sn = *(LAS const f32x4*)(sn16 + pos * 16 + 4 * fq);
;                     if (F8) { unsigned char* p8 = (unsigned char*)dst + (size_t)row * pitch + wc * 64 + 32 * bj + 4 * fq; const f32x4 y1 = x1 * c - x2 * sn, y2 = x1 * sn + x2 * c;
;                         *(unsigned*)p8 = pk4_fp8(y1[0], y1[1], y1[2], y1[3]); *(unsigned*)(p8 + 16) = pk4_fp8(y2[0], y2[1], y2[2], y2[3]); }
.LBB0_1720:
	s_andn2_b64 vcc, exec, s[58:59]
	s_mov_b64 s[8:9], 8
	s_cbranch_vccnz .LBB0_1722
	v_pk_fma_f32 v[146:147], v[174:175], v[146:147], v[150:151]
	s_nop 0
	v_cvt_pk_fp8_f32 v150, v178, v179
	s_nop 0
	v_cvt_pk_fp8_f32 v151, v146, v147
	v_pk_mul_f32 v[146:147], v[170:171], v[152:153]
	v_cvt_pk_fp8_f32 v150, v172, v173 op_sel:[0,0,1]
	v_pk_fma_f32 v[146:147], v[166:167], v[148:149], v[146:147]
	s_mov_b64 s[8:9], 7
	v_cvt_pk_fp8_f32 v151, v146, v147 op_sel:[0,0,1]
	global_store_dword v[176:177], v150, off offset:32
	global_store_dword v[176:177], v151, off offset:48

; #define LAS __attribute__((address_space(3)))
; DI unsigned pk4_fp8(float a, float b, float c, float d) { int r = 0; r = __builtin_amdgcn_cvt_pk_fp8_f32(a, b, r, false); r = __builtin_amdgcn_cvt_pk_fp8_f32(c, d, r, true); return (unsigned)r; }
;     DI void head64(const AccT& acc, int rbase, int wc, int fq, bf16_t* dst, int pitch, const float* gain, float scale, const bool F8) const {
;     ...
;                 for (int bj = 0; bj < 2; ++bj) {
;                     const f32x4 x1 = acc[ai][bj][m][0] * rinv * g[bj][0], x2 = acc[ai][bj][m][1] * rinv * g[bj][1];
;                     const int pos = lat ? (bj ? (t & 63) : (t >> 6)) : 64;
;                     const f32x4 c = *(LAS const f32x4*)(cs16 + pos * 16 + 4 * fq), sn = *(LAS const f32x4*)(sn16 + pos * 16 + 4 * fq);
;                     if (F8) { unsigned char* p8 = (unsigned char*)dst + (size_t)row * pitch + wc * 64 + 32 * bj + 4 * fq; const f32x4 y1 = x1 * c - x2 * sn, y2 = x1 * sn + x2 * c;
;                         *(unsigned*)p8 = pk4_fp8(y1[0], y1[1], y1[2], y1[3]); *(unsigned*)(p8 + 16) = pk4_fp8(y2[0], y2[1], y2[2], y2[3]); }
.LBB0_1724:
	s_andn2_b64 vcc, exec, s[58:59]
	v_lshl_add_u64 v[172:173], v[164:165], 0, v[172:173]
	s_cbranch_vccnz .LBB0_1726
	v_pk_fma_f32 v[146:147], v[146:147], v[180:181], v[150:151]
	s_nop 0
	v_cvt_pk_fp8_f32 v150, v182, v183
	s_nop 0
	v_cvt_pk_fp8_f32 v151, v146, v147
	v_pk_mul_f32 v[146:147], v[152:153], v[174:175]
	v_cvt_pk_fp8_f32 v150, v178, v179 op_sel:[0,0,1]
	v_pk_fma_f32 v[146:147], v[148:149], v[176:177], v[146:147]
	s_nop 0
	v_cvt_pk_fp8_f32 v151, v146, v147 op_sel:[0,0,1]
	global_store_dword v[172:173], v150, off
	global_store_dword v[172:173], v151, off offset:16

; #define LAS __attribute__((address_space(3)))
; DI unsigned pk4_fp8(float a, float b, float c, float d) { int r = 0; r = __builtin_amdgcn_cvt_pk_fp8_f32(a, b, r, false); r = __builtin_amdgcn_cvt_pk_fp8_f32(c, d, r, true); return (unsigned)r; }
;     DI void head64(const AccT& acc, int rbase, int wc, int fq, bf16_t* dst, int pitch, const float* gain, float scale, const bool F8) const {
;     ...
;                 for (int bj = 0; bj < 2; ++bj) {
;                     const f32x4 x1 = acc[ai][bj][m][0] * rinv * g[bj][0], x2 = acc[ai][bj][m][1] * rinv * g[bj][1];
;                     const int pos = lat ? (bj ? (t & 63) : (t >> 6)) : 64;
;                     const f32x4 c = *(LAS const f32x4*)(cs16 + pos * 16 + 4 * fq), sn = *(LAS const f32x4*)(sn16 + pos * 16 + 4 * fq);
;                     if (F8) { unsigned char* p8 = (unsigned char*)dst + (size_t)row * pitch + wc * 64 + 32 * bj + 4 * fq; const f32x4 y1 = x1 * c - x2 * sn, y2 = x1 * sn + x2 * c;
;                         *(unsigned*)p8 = pk4_fp8(y1[0], y1[1], y1[2], y1[3]); *(unsigned*)(p8 + 16) = pk4_fp8(y2[0], y2[1], y2[2], y2[3]); }
.LBB0_1728:
	s_andn2_b64 vcc, exec, s[8:9]
	s_mov_b64 s[8:9], 8
	s_cbranch_vccnz .LBB0_1730
	v_pk_fma_f32 v[146:147], v[176:177], v[146:147], v[150:151]
	s_nop 0
	v_cvt_pk_fp8_f32 v150, v178, v179
	s_nop 0
	v_cvt_pk_fp8_f32 v151, v146, v147
	v_pk_mul_f32 v[146:147], v[174:175], v[152:153]
	v_cvt_pk_fp8_f32 v150, v170, v171 op_sel:[0,0,1]
	v_pk_fma_f32 v[146:147], v[168:169], v[148:149], v[146:147]
	s_mov_b64 s[8:9], 7
	v_cvt_pk_fp8_f32 v151, v146, v147 op_sel:[0,0,1]
	global_store_dword v[172:173], v150, off offset:32
	global_store_dword v[172:173], v151, off offset:48

; #define LAS __attribute__((address_space(3)))
; DI unsigned pk4_fp8(float a, float b, float c, float d) { int r = 0; r = __builtin_amdgcn_cvt_pk_fp8_f32(a, b, r, false); r = __builtin_amdgcn_cvt_pk_fp8_f32(c, d, r, true); return (unsigned)r; }
;     DI void head64(const AccT& acc, int rbase, int wc, int fq, bf16_t* dst, int pitch, const float* gain, float scale, const bool F8) const {
;     ...
;                 for (int bj = 0; bj < 2; ++bj) {
;                     const f32x4 x1 = acc[ai][bj][m][0] * rinv * g[bj][0], x2 = acc[ai][bj][m][1] * rinv * g[bj][1];
;                     const int pos = lat ? (bj ? (t & 63) : (t >> 6)) : 64;
;                     const f32x4 c = *(LAS const f32x4*)(cs16 + pos * 16 + 4 * fq), sn = *(LAS const f32x4*)(sn16 + pos * 16 + 4 * fq);
;                     if (F8) { unsigned char* p8 = (unsigned char*)dst + (size_t)row * pitch + wc * 64 + 32 * bj + 4 * fq; const f32x4 y1 = x1 * c - x2 * sn, y2 = x1 * sn + x2 * c;
;                         *(unsigned*)p8 = pk4_fp8(y1[0], y1[1], y1[2], y1[3]); *(unsigned*)(p8 + 16) = pk4_fp8(y2[0], y2[1], y2[2], y2[3]); }
.LBB0_1748:
	s_andn2_b64 vcc, exec, s[58:59]
	v_lshl_add_u64 v[170:171], v[164:165], 0, v[170:171]
	s_cbranch_vccnz .LBB0_1750
	v_pk_fma_f32 v[146:147], v[146:147], v[178:179], v[150:151]
	s_nop 0
	v_cvt_pk_fp8_f32 v150, v180, v181
	s_nop 0
	v_cvt_pk_fp8_f32 v151, v146, v147
	v_pk_mul_f32 v[146:147], v[152:153], v[172:173]
	v_cvt_pk_fp8_f32 v150, v176, v177 op_sel:[0,0,1]
	v_pk_fma_f32 v[146:147], v[148:149], v[174:175], v[146:147]
	s_nop 0
	v_cvt_pk_fp8_f32 v151, v146, v147 op_sel:[0,0,1]
	global_store_dword v[170:171], v150, off
	global_store_dword v[170:171], v151, off offset:16

; #define LAS __attribute__((address_space(3)))
; DI unsigned pk4_fp8(float a, float b, float c, float d) { int r = 0; r = __builtin_amdgcn_cvt_pk_fp8_f32(a, b, r, false); r = __builtin_amdgcn_cvt_pk_fp8_f32(c, d, r, true); return (unsigned)r; }
;     DI void head64(const AccT& acc, int rbase, int wc, int fq, bf16_t* dst, int pitch, const float* gain, float scale, const bool F8) const {
;     ...
;                 for (int bj = 0; bj < 2; ++bj) {
;                     const f32x4 x1 = acc[ai][bj][m][0] * rinv * g[bj][0], x2 = acc[ai][bj][m][1] * rinv * g[bj][1];
;                     const int pos = lat ? (bj ? (t & 63) : (t >> 6)) : 64;
;                     const f32x4 c = *(LAS const f32x4*)(cs16 + pos * 16 + 4 * fq), sn = *(LAS const f32x4*)(sn16 + pos * 16 + 4 * fq);
;                     if (F8) { unsigned char* p8 = (unsigned char*)dst + (size_t)row * pitch + wc * 64 + 32 * bj + 4 * fq; const f32x4 y1 = x1 * c - x2 * sn, y2 = x1 * sn + x2 * c;
;                         *(unsigned*)p8 = pk4_fp8(y1[0], y1[1], y1[2], y1[3]); *(unsigned*)(p8 + 16) = pk4_fp8(y2[0], y2[1], y2[2], y2[3]); }
.LBB0_1752:
	s_andn2_b64 vcc, exec, s[8:9]
	s_mov_b64 s[8:9], 8
	s_cbranch_vccnz .LBB0_1754
	v_pk_fma_f32 v[146:147], v[176:177], v[146:147], v[150:151]
	s_nop 0
	v_cvt_pk_fp8_f32 v150, v178, v179
	s_nop 0
	v_cvt_pk_fp8_f32 v151, v146, v147
	v_pk_mul_f32 v[146:147], v[172:173], v[152:153]
	v_cvt_pk_fp8_f32 v150, v174, v175 op_sel:[0,0,1]
	v_pk_fma_f32 v[146:147], v[168:169], v[148:149], v[146:147]
	s_mov_b64 s[8:9], 7
	v_cvt_pk_fp8_f32 v151, v146, v147 op_sel:[0,0,1]
	global_store_dword v[170:171], v150, off offset:32
	global_store_dword v[170:171], v151, off offset:48

; #define LAS __attribute__((address_space(3)))
; DI unsigned pk4_fp8(float a, float b, float c, float d) { int r = 0; r = __builtin_amdgcn_cvt_pk_fp8_f32(a, b, r, false); r = __builtin_amdgcn_cvt_pk_fp8_f32(c, d, r, true); return (unsigned)r; }
;     DI void head64(const AccT& acc, int rbase, int wc, int fq, bf16_t* dst, int pitch, const float* gain, float scale, const bool F8) const {
;     ...
;                 for (int bj = 0; bj < 2; ++bj) {
;                     const f32x4 x1 = acc[ai][bj][m][0] * rinv * g[bj][0], x2 = acc[ai][bj][m][1] * rinv * g[bj][1];
;                     const int pos = lat ? (bj ? (t & 63) : (t >> 6)) : 64;
;                     const f32x4 c = *(LAS const f32x4*)(cs16 + pos * 16 + 4 * fq), sn = *(LAS const f32x4*)(sn16 + pos * 16 + 4 * fq);
;                     if (F8) { unsigned char* p8 = (unsigned char*)dst + (size_t)row * pitch + wc * 64 + 32 * bj + 4 * fq; const f32x4 y1 = x1 * c - x2 * sn, y2 = x1 * sn + x2 * c;
;                         *(unsigned*)p8 = pk4_fp8(y1[0], y1[1], y1[2], y1[3]); *(unsigned*)(p8 + 16) = pk4_fp8(y2[0], y2[1], y2[2], y2[3]); }
.LBB0_1772:
	s_andn2_b64 vcc, exec, s[58:59]
	v_lshl_add_u64 v[146:147], v[164:165], 0, v[168:169]
	s_cbranch_vccnz .LBB0_1774
	s_nop 0
	v_pk_fma_f32 v[142:143], v[142:143], v[170:171], v[174:175]
	v_cvt_pk_fp8_f32 v153, v172, v173
	s_nop 0
	v_cvt_pk_fp8_f32 v161, v142, v143
	v_pk_mul_f32 v[142:143], v[148:149], v[162:163]
	v_cvt_pk_fp8_f32 v153, v138, v139 op_sel:[0,0,1]
	v_pk_fma_f32 v[140:141], v[144:145], v[140:141], v[142:143]
	s_nop 0
	v_cvt_pk_fp8_f32 v161, v140, v141 op_sel:[0,0,1]
	global_store_dword v[146:147], v153, off
	global_store_dword v[146:147], v161, off offset:16

; #define LAS __attribute__((address_space(3)))
; DI unsigned pk4_fp8(float a, float b, float c, float d) { int r = 0; r = __builtin_amdgcn_cvt_pk_fp8_f32(a, b, r, false); r = __builtin_amdgcn_cvt_pk_fp8_f32(c, d, r, true); return (unsigned)r; }
;     DI void head64(const AccT& acc, int rbase, int wc, int fq, bf16_t* dst, int pitch, const float* gain, float scale, const bool F8) const {
;     ...
;                 for (int bj = 0; bj < 2; ++bj) {
;                     const f32x4 x1 = acc[ai][bj][m][0] * rinv * g[bj][0], x2 = acc[ai][bj][m][1] * rinv * g[bj][1];
;                     const int pos = lat ? (bj ? (t & 63) : (t >> 6)) : 64;
;                     const f32x4 c = *(LAS const f32x4*)(cs16 + pos * 16 + 4 * fq), sn = *(LAS const f32x4*)(sn16 + pos * 16 + 4 * fq);
;                     if (F8) { unsigned char* p8 = (unsigned char*)dst + (size_t)row * pitch + wc * 64 + 32 * bj + 4 * fq; const f32x4 y1 = x1 * c - x2 * sn, y2 = x1 * sn + x2 * c;
;                         *(unsigned*)p8 = pk4_fp8(y1[0], y1[1], y1[2], y1[3]); *(unsigned*)(p8 + 16) = pk4_fp8(y2[0], y2[1], y2[2], y2[3]); }
.LBB0_1776:
	s_andn2_b64 vcc, exec, s[8:9]
	s_cbranch_vccnz .LBB0_1778
	v_pk_fma_f32 v[134:135], v[144:145], v[134:135], v[138:139]
	s_nop 0
	v_cvt_pk_fp8_f32 v138, v148, v149
	s_nop 0
	v_cvt_pk_fp8_f32 v139, v134, v135
	v_pk_mul_f32 v[134:135], v[142:143], v[140:141]
	v_cvt_pk_fp8_f32 v138, v130, v131 op_sel:[0,0,1]
	v_pk_fma_f32 v[132:133], v[132:133], v[136:137], v[134:135]
	s_nop 0
	v_cvt_pk_fp8_f32 v139, v132, v133 op_sel:[0,0,1]
	global_store_dword v[146:147], v138, off offset:32
	global_store_dword v[146:147], v139, off offset:48

; DI unsigned pk4_fp8(float a, float b, float c, float d) { int r = 0; r = __builtin_amdgcn_cvt_pk_fp8_f32(a, b, r, false); r = __builtin_amdgcn_cvt_pk_fp8_f32(c, d, r, true); return (unsigned)r; }
;     DI void operator()(EPI_ARGS) const {
;     ...
;         const bool ctx = u.pn >= 128; const int b = ctx ? (u.pn - 128) : (u.pn >> 4); const int t0 = ctx ? 0 : (u.pn & 15) * 256;
;         bf16_t* base; size_t pitch; int tokoff;
;         if (u.pm == 0) {
;             unsigned char* vb = WSB(unsigned char, WS_VTD) + (size_t)b * 4 * 64 * KEYS; const int tko = ctx ? SEQ : t0;
; #pragma unroll
;             for (int ai = 0; ai < 2; ++ai)
; #pragma unroll
;                 for (int m = 0; m < 4; ++m) { const int lrow = 128 * ai + 64 * wr + 16 * m + fr;
; #pragma unroll
;                     for (int bj = 0; bj < 2; ++bj) { const f32x4 x0 = acc[ai][bj][m][0] * W8_INV, x1 = acc[ai][bj][m][1] * W8_INV;
;                         *(u32x2*)(vb + (size_t)lrow * KEYS + tko + 128 * bj + 32 * wc + 8 * fq) = (u32x2){pk4_fp8(x0[0], x0[1], x0[2], x0[3]), pk4_fp8(x1[0], x1[1], x1[2], x1[3])}; } }
;             return; }
.LBB0_1811:
	v_pk_mul_f32 v[126:127], v[126:127], s[16:17] op_sel_hi:[1,0]
	s_nop 0
	v_cvt_pk_fp8_f32 v132, v126, v127
	s_and_b64 s[20:21], s[20:21], exec
	s_cselect_b32 s20, s22, s24
	v_pk_mul_f32 v[122:123], v[122:123], s[16:17] op_sel_hi:[1,0]
	s_nop 0
	s_mul_hi_i32 s21, s20, 0x110000
	s_mul_i32 s20, s20, 0x110000
	v_cvt_pk_fp8_f32 v133, v122, v123
	v_pk_mul_f32 v[122:123], v[128:129], s[16:17] op_sel_hi:[1,0]
	s_cselect_b32 s8, 0x1000, s73
	s_add_u32 s20, s60, s20
	v_cvt_pk_fp8_f32 v132, v122, v123 op_sel:[0,0,1]
	v_pk_mul_f32 v[118:119], v[118:119], s[16:17] op_sel_hi:[1,0]
	v_pk_mul_f32 v[110:111], v[110:111], s[16:17] op_sel_hi:[1,0]
	s_nop 0
	s_nop 0
	s_addc_u32 s21, s61, s21
	v_cvt_pk_fp8_f32 v122, v118, v119
	v_cvt_pk_fp8_f32 v123, v110, v111
	s_add_u32 s8, s20, s8
	s_addc_u32 s21, s21, 0
	v_pk_mul_f32 v[124:125], v[124:125], s[16:17] op_sel_hi:[1,0]
	s_add_u32 s20, s8, s5
	v_lshlrev_b32_e32 v130, 3, v143
	v_cvt_pk_fp8_f32 v133, v124, v125 op_sel:[0,0,1]
	v_pk_mul_f32 v[110:111], v[120:121], s[16:17] op_sel_hi:[1,0]
	v_pk_mul_f32 v[112:113], v[112:113], s[16:17] op_sel_hi:[1,0]
	s_addc_u32 s21, s21, 0
	v_ashrrev_i32_e32 v131, 31, v130
	v_cvt_pk_fp8_f32 v122, v110, v111 op_sel:[0,0,1]
	v_cvt_pk_fp8_f32 v123, v112, v113 op_sel:[0,0,1]
	v_add_u32_e32 v144, s49, v144
	v_lshl_add_u64 v[130:131], s[20:21], 0, v[130:131]
	v_mad_i64_i32 v[110:111], s[20:21], v144, s64, v[130:131]
	global_store_dwordx2 v[110:111], v[132:133], off
	global_store_dwordx2 v[110:111], v[122:123], off offset:128
	v_pk_mul_f32 v[110:111], v[114:115], s[16:17] op_sel_hi:[1,0]
	s_nop 0
	v_cvt_pk_fp8_f32 v112, v110, v111
	v_pk_mul_f32 v[106:107], v[106:107], s[16:17] op_sel_hi:[1,0]
	s_nop 0
	v_cvt_pk_fp8_f32 v113, v106, v107
	v_pk_mul_f32 v[106:107], v[116:117], s[16:17] op_sel_hi:[1,0]
	v_pk_mul_f32 v[102:103], v[102:103], s[16:17] op_sel_hi:[1,0]
	v_cvt_pk_fp8_f32 v112, v106, v107 op_sel:[0,0,1]
	v_pk_mul_f32 v[94:95], v[94:95], s[16:17] op_sel_hi:[1,0]
	s_nop 0
	s_nop 0
	v_cvt_pk_fp8_f32 v106, v102, v103
	v_cvt_pk_fp8_f32 v107, v94, v95
	v_pk_mul_f32 v[108:109], v[108:109], s[16:17] op_sel_hi:[1,0]
	v_pk_mul_f32 v[94:95], v[104:105], s[16:17] op_sel_hi:[1,0]
	v_cvt_pk_fp8_f32 v113, v108, v109 op_sel:[0,0,1]
	v_pk_mul_f32 v[96:97], v[96:97], s[16:17] op_sel_hi:[1,0]
	v_cvt_pk_fp8_f32 v106, v94, v95 op_sel:[0,0,1]
	v_cvt_pk_fp8_f32 v107, v96, v97 op_sel:[0,0,1]
	v_add_u32_e32 v118, 16, v144
	v_mad_i64_i32 v[94:95], s[20:21], v118, s64, v[130:131]
	global_store_dwordx2 v[94:95], v[112:113], off
	global_store_dwordx2 v[94:95], v[106:107], off offset:128
	v_pk_mul_f32 v[94:95], v[98:99], s[16:17] op_sel_hi:[1,0]
	s_nop 0
	v_cvt_pk_fp8_f32 v96, v94, v95
	v_pk_mul_f32 v[90:91], v[90:91], s[16:17] op_sel_hi:[1,0]
	s_nop 0
	v_cvt_pk_fp8_f32 v97, v90, v91
	v_pk_mul_f32 v[90:91], v[100:101], s[16:17] op_sel_hi:[1,0]
	v_pk_mul_f32 v[86:87], v[86:87], s[16:17] op_sel_hi:[1,0]
	v_cvt_pk_fp8_f32 v96, v90, v91 op_sel:[0,0,1]
	v_pk_mul_f32 v[78:79], v[78:79], s[16:17] op_sel_hi:[1,0]
	s_nop 0
	s_nop 0
	v_cvt_pk_fp8_f32 v90, v86, v87
	v_cvt_pk_fp8_f32 v91, v78, v79
	v_pk_mul_f32 v[92:93], v[92:93], s[16:17] op_sel_hi:[1,0]
	v_pk_mul_f32 v[78:79], v[88:89], s[16:17] op_sel_hi:[1,0]
	v_cvt_pk_fp8_f32 v97, v92, v93 op_sel:[0,0,1]
	v_pk_mul_f32 v[80:81], v[80:81], s[16:17] op_sel_hi:[1,0]
	v_cvt_pk_fp8_f32 v90, v78, v79 op_sel:[0,0,1]
	v_cvt_pk_fp8_f32 v91, v80, v81 op_sel:[0,0,1]
	v_add_u32_e32 v102, 32, v144
	v_mad_i64_i32 v[78:79], s[20:21], v102, s64, v[130:131]
	global_store_dwordx2 v[78:79], v[96:97], off
	global_store_dwordx2 v[78:79], v[90:91], off offset:128
	v_pk_mul_f32 v[78:79], v[82:83], s[16:17] op_sel_hi:[1,0]
	s_nop 0
	v_cvt_pk_fp8_f32 v80, v78, v79
	v_pk_mul_f32 v[74:75], v[74:75], s[16:17] op_sel_hi:[1,0]
	s_nop 0
	v_cvt_pk_fp8_f32 v81, v74, v75
	v_pk_mul_f32 v[74:75], v[84:85], s[16:17] op_sel_hi:[1,0]
	v_pk_mul_f32 v[70:71], v[70:71], s[16:17] op_sel_hi:[1,0]
	v_cvt_pk_fp8_f32 v80, v74, v75 op_sel:[0,0,1]
	v_pk_mul_f32 v[66:67], v[66:67], s[16:17] op_sel_hi:[1,0]
	s_nop 0
	s_nop 0
	v_cvt_pk_fp8_f32 v74, v70, v71
	v_cvt_pk_fp8_f32 v75, v66, v67
	v_pk_mul_f32 v[76:77], v[76:77], s[16:17] op_sel_hi:[1,0]
	v_pk_mul_f32 v[66:67], v[72:73], s[16:17] op_sel_hi:[1,0]
	v_cvt_pk_fp8_f32 v81, v76, v77 op_sel:[0,0,1]
	v_pk_mul_f32 v[68:69], v[68:69], s[16:17] op_sel_hi:[1,0]
; DI unsigned pk4_fp8(float a, float b, float c, float d) { int r = 0; r = __builtin_amdgcn_cvt_pk_fp8_f32(a, b, r, false); r = __builtin_amdgcn_cvt_pk_fp8_f32(c, d, r, true); return (unsigned)r; }
;     DI void operator()(EPI_ARGS) const {
;     ...
;         const bool ctx = u.pn >= 128; const int b = ctx ? (u.pn - 128) : (u.pn >> 4); const int t0 = ctx ? 0 : (u.pn & 15) * 256;
;         bf16_t* base; size_t pitch; int tokoff;
;         if (u.pm == 0) {
;             unsigned char* vb = WSB(unsigned char, WS_VTD) + (size_t)b * 4 * 64 * KEYS; const int tko = ctx ? SEQ : t0;
; #pragma unroll
;             for (int ai = 0; ai < 2; ++ai)
; #pragma unroll
;                 for (int m = 0; m < 4; ++m) { const int lrow = 128 * ai + 64 * wr + 16 * m + fr;
; #pragma unroll
;                     for (int bj = 0; bj < 2; ++bj) { const f32x4 x0 = acc[ai][bj][m][0] * W8_INV, x1 = acc[ai][bj][m][1] * W8_INV;
;                         *(u32x2*)(vb + (size_t)lrow * KEYS + tko + 128 * bj + 32 * wc + 8 * fq) = (u32x2){pk4_fp8(x0[0], x0[1], x0[2], x0[3]), pk4_fp8(x1[0], x1[1], x1[2], x1[3])}; } }
;             return; }
	v_cvt_pk_fp8_f32 v74, v66, v67 op_sel:[0,0,1]
	v_cvt_pk_fp8_f32 v75, v68, v69 op_sel:[0,0,1]
	v_add_u32_e32 v86, 48, v144
	v_mad_i64_i32 v[66:67], s[20:21], v86, s64, v[130:131]
	global_store_dwordx2 v[66:67], v[80:81], off
	global_store_dwordx2 v[66:67], v[74:75], off offset:128
	v_pk_mul_f32 v[62:63], v[62:63], s[16:17] op_sel_hi:[1,0]
	s_nop 0
	v_cvt_pk_fp8_f32 v66, v62, v63
	v_pk_mul_f32 v[58:59], v[58:59], s[16:17] op_sel_hi:[1,0]
	s_nop 0
	v_cvt_pk_fp8_f32 v67, v58, v59
	v_pk_mul_f32 v[58:59], v[64:65], s[16:17] op_sel_hi:[1,0]
	v_pk_mul_f32 v[54:55], v[54:55], s[16:17] op_sel_hi:[1,0]
	v_cvt_pk_fp8_f32 v66, v58, v59 op_sel:[0,0,1]
	v_pk_mul_f32 v[46:47], v[46:47], s[16:17] op_sel_hi:[1,0]
	s_nop 0
	s_nop 0
	v_cvt_pk_fp8_f32 v58, v54, v55
	v_cvt_pk_fp8_f32 v59, v46, v47
	v_pk_mul_f32 v[60:61], v[60:61], s[16:17] op_sel_hi:[1,0]
	v_pk_mul_f32 v[46:47], v[56:57], s[16:17] op_sel_hi:[1,0]
	v_cvt_pk_fp8_f32 v67, v60, v61 op_sel:[0,0,1]
	v_pk_mul_f32 v[48:49], v[48:49], s[16:17] op_sel_hi:[1,0]
	v_cvt_pk_fp8_f32 v58, v46, v47 op_sel:[0,0,1]
	v_cvt_pk_fp8_f32 v59, v48, v49 op_sel:[0,0,1]
	v_add_u32_e32 v68, 0x80, v144
	v_mad_i64_i32 v[46:47], s[20:21], v68, s64, v[130:131]
	global_store_dwordx2 v[46:47], v[66:67], off
	global_store_dwordx2 v[46:47], v[58:59], off offset:128
	v_pk_mul_f32 v[46:47], v[50:51], s[16:17] op_sel_hi:[1,0]
	s_nop 0
	v_cvt_pk_fp8_f32 v48, v46, v47
	v_pk_mul_f32 v[42:43], v[42:43], s[16:17] op_sel_hi:[1,0]
	s_nop 0
	v_cvt_pk_fp8_f32 v49, v42, v43
	v_pk_mul_f32 v[42:43], v[52:53], s[16:17] op_sel_hi:[1,0]
	v_pk_mul_f32 v[38:39], v[38:39], s[16:17] op_sel_hi:[1,0]
	v_cvt_pk_fp8_f32 v48, v42, v43 op_sel:[0,0,1]
	v_pk_mul_f32 v[30:31], v[30:31], s[16:17] op_sel_hi:[1,0]
	s_nop 0
	s_nop 0
	v_cvt_pk_fp8_f32 v42, v38, v39
	v_cvt_pk_fp8_f32 v43, v30, v31
	v_pk_mul_f32 v[44:45], v[44:45], s[16:17] op_sel_hi:[1,0]
	v_pk_mul_f32 v[30:31], v[40:41], s[16:17] op_sel_hi:[1,0]
	v_cvt_pk_fp8_f32 v49, v44, v45 op_sel:[0,0,1]
	v_pk_mul_f32 v[32:33], v[32:33], s[16:17] op_sel_hi:[1,0]
	v_cvt_pk_fp8_f32 v42, v30, v31 op_sel:[0,0,1]
	v_cvt_pk_fp8_f32 v43, v32, v33 op_sel:[0,0,1]
	v_add_u32_e32 v54, 0x90, v144
	v_mad_i64_i32 v[30:31], s[20:21], v54, s64, v[130:131]
	global_store_dwordx2 v[30:31], v[48:49], off
	global_store_dwordx2 v[30:31], v[42:43], off offset:128
	v_pk_mul_f32 v[30:31], v[34:35], s[16:17] op_sel_hi:[1,0]
	s_nop 0
	v_cvt_pk_fp8_f32 v32, v30, v31
	v_pk_mul_f32 v[26:27], v[26:27], s[16:17] op_sel_hi:[1,0]
	s_nop 0
	v_cvt_pk_fp8_f32 v33, v26, v27
	v_pk_mul_f32 v[26:27], v[36:37], s[16:17] op_sel_hi:[1,0]
	v_pk_mul_f32 v[22:23], v[22:23], s[16:17] op_sel_hi:[1,0]
	v_cvt_pk_fp8_f32 v32, v26, v27 op_sel:[0,0,1]
	v_pk_mul_f32 v[14:15], v[14:15], s[16:17] op_sel_hi:[1,0]
	s_nop 0
	s_nop 0
	v_cvt_pk_fp8_f32 v26, v22, v23
	v_cvt_pk_fp8_f32 v27, v14, v15
	v_pk_mul_f32 v[28:29], v[28:29], s[16:17] op_sel_hi:[1,0]
	v_pk_mul_f32 v[14:15], v[24:25], s[16:17] op_sel_hi:[1,0]
	v_cvt_pk_fp8_f32 v33, v28, v29 op_sel:[0,0,1]
	v_pk_mul_f32 v[16:17], v[16:17], s[16:17] op_sel_hi:[1,0]
	v_cvt_pk_fp8_f32 v26, v14, v15 op_sel:[0,0,1]
	v_cvt_pk_fp8_f32 v27, v16, v17 op_sel:[0,0,1]
	v_add_u32_e32 v38, 0xa0, v144
	v_mad_i64_i32 v[14:15], s[20:21], v38, s64, v[130:131]
	global_store_dwordx2 v[14:15], v[32:33], off
	global_store_dwordx2 v[14:15], v[26:27], off offset:128
	v_pk_mul_f32 v[14:15], v[18:19], s[16:17] op_sel_hi:[1,0]
	s_nop 0
	v_cvt_pk_fp8_f32 v16, v14, v15
	v_pk_mul_f32 v[10:11], v[10:11], s[16:17] op_sel_hi:[1,0]
	s_nop 0
	v_cvt_pk_fp8_f32 v17, v10, v11
	v_pk_mul_f32 v[10:11], v[20:21], s[16:17] op_sel_hi:[1,0]
	v_pk_mul_f32 v[6:7], v[6:7], s[16:17] op_sel_hi:[1,0]
	v_cvt_pk_fp8_f32 v16, v10, v11 op_sel:[0,0,1]
	v_pk_mul_f32 v[2:3], v[2:3], s[16:17] op_sel_hi:[1,0]
	s_nop 0
	s_nop 0
	v_cvt_pk_fp8_f32 v10, v6, v7
	v_cvt_pk_fp8_f32 v11, v2, v3
	v_pk_mul_f32 v[12:13], v[12:13], s[16:17] op_sel_hi:[1,0]
	v_pk_mul_f32 v[2:3], v[8:9], s[16:17] op_sel_hi:[1,0]
	v_cvt_pk_fp8_f32 v17, v12, v13 op_sel:[0,0,1]
	v_pk_mul_f32 v[4:5], v[4:5], s[16:17] op_sel_hi:[1,0]
	v_cvt_pk_fp8_f32 v10, v2, v3 op_sel:[0,0,1]
	v_cvt_pk_fp8_f32 v11, v4, v5 op_sel:[0,0,1]
	v_add_u32_e32 v22, 0xb0, v144
	v_mad_i64_i32 v[2:3], s[20:21], v22, s64, v[130:131]
	global_store_dwordx2 v[2:3], v[16:17], off
	global_store_dwordx2 v[2:3], v[10:11], off offset:128

; DI void attn_unit_d8(unsigned char* lds, const AttnArgs& a) {
;     ...
;     const int lane = tid & 63, r = lane & 31, h = lane >> 5; const int wid = __builtin_amdgcn_readfirstlane(tid >> 6);
;     v8i qfa, qfb;
;     { const bf16_t* qp = a.q + (size_t)(wid * 32 + r) * 256 + 32 * h;
;       const u32x4 q0 = *(const u32x4*)qp, q1 = *(const u32x4*)(qp + 8), q2 = *(const u32x4*)(qp + 16), q3 = *(const u32x4*)(qp + 24);
;       const u32x2 c0 = bf8_to_fp8(q0), c1 = bf8_to_fp8(q1), c2 = bf8_to_fp8(q2), c3 = bf8_to_fp8(q3);
;       const v8i qv = (v8i){(int)c0.x, (int)c0.y, (int)c1.x, (int)c1.y, (int)c2.x, (int)c2.y, (int)c3.x, (int)c3.y}, zz = (v8i){0, 0, 0, 0, 0, 0, 0, 0};
;       qfa = h == 0 ? qv : zz; qfb = h == 1 ? qv : zz; }
;     const int lrow = tid >> 3, lch = tid & 7;
;     const unsigned char* vsrc = a.vt8 + (size_t)lrow * KEYS + 8 * lch;
;     const int ldst = lrow * A8_PITCH + lch * 8;
;     const int ldv = A8_VOFF + lrow * A8_PITCH + (lch >> 2) * 16 + (lch & 3) * 4;
;     const int koff = r * A8_PITCH + 32 * h, voff = A8_VOFF + r * A8_PITCH + 32 * h;
;     f32x16 o0[2], o1[2];
; #pragma unroll
;     for (int d = 0; d < 2; ++d) { o0[d] = (f32x16){}; o1[d] = (f32x16){}; }
;     f32x4 l0 = {0.f, 0.f, 0.f, 0.f}, l1 = {0.f, 0.f, 0.f, 0.f};
;     constexpr int D8_SLOT = 2 * 64 * A8_PITCH;
;     u32x2 kreg0, vreg0, kreg1, vreg1;
;     auto gload = [&](int t, u32x2& kreg, u32x2& vreg) __attribute__((always_inline)) {
;         const unsigned char* kp = (t < 64) ? a.klat8 + (size_t)(t * 64 + lrow) * 256 : a.kctx8 + (size_t)((t - 64) * 64 + lrow) * 256;
;         kreg = *(const u32x2*)(kp + 8 * lch);
;         vreg = *(const u32x2*)(vsrc + (size_t)t * 64);
;     };
;     auto lstore = [&](int slot, const u32x2& kreg, const u32x2& vreg) __attribute__((always_inline)) { unsigned char* b = lds + slot * D8_SLOT;
;         *(u32x2*)(b + ldst) = kreg; *(unsigned*)(b + ldv) = vreg.x; *(unsigned*)(b + ldv + 32) = vreg.y; };
;     auto rd32 = [&](const unsigned char* p) __attribute__((always_inline)) -> v8i { const u32x4 lo = *(const u32x4*)p, hi = *(const u32x4*)(p + 16);
;         return (v8i){(int)lo.x, (int)lo.y, (int)lo.z, (int)lo.w, (int)hi.x, (int)hi.y, (int)hi.z, (int)hi.w}; };
;     auto expsum = [&](f32x16& sc, f32x4& l) __attribute__((always_inline)) {
; #pragma unroll
;         for (int i = 0; i < 16; ++i) sc[i] = __builtin_amdgcn_exp2f(sc[i]);
; #pragma unroll
.LBB0_1885:
	s_ashr_i32 s8, s46, 6
	s_lshl_b32 s16, s46, 8
	s_lshl_b32 s18, s8, 12
	s_and_b32 s16, s16, 0xf00
	s_or_b32 s16, s18, s16
	s_ashr_i32 s17, s16, 31
	s_lshl_b64 s[20:21], s[16:17], 9
	s_add_u32 s19, s4, s20
	s_addc_u32 s20, s5, s21
	s_lshl_b32 s21, s46, 2
	s_and_b32 s47, s21, 0xc0
	s_lshl_b32 s21, s47, 1
	s_add_u32 s50, s19, s21
	s_addc_u32 s51, s20, 0
	s_lshl_b32 s20, s8, 8
	s_ashr_i32 s19, s18, 31
	s_or_b32 s8, s20, s47
	s_lshl_b64 s[18:19], s[18:19], 8
	s_mul_hi_i32 s21, s8, 0x1100
	s_mulk_i32 s8, 0x1100
	s_add_u32 s22, s28, s8
	s_addc_u32 s23, s29, s21
	s_add_u32 s8, s24, s18
	s_addc_u32 s19, s25, s19
	v_mov_b32_e32 v18, v0
	s_add_u32 s18, s8, s47
	s_addc_u32 s19, s19, 0
	v_readfirstlane_b32 s8, v18
	v_and_b32_e32 v30, 31, v18
	s_ashr_i32 s8, s8, 6
	v_lshl_or_b32 v180, s8, 5, v30
	v_ashrrev_i32_e32 v181, 31, v180
	v_bfe_u32 v217, v18, 5, 1
	v_lshlrev_b64 v[2:3], 9, v[180:181]
	v_lshl_add_u64 v[2:3], s[50:51], 0, v[2:3]
	v_lshlrev_b32_e32 v178, 6, v217
	v_lshl_add_u64 v[14:15], v[2:3], 0, v[178:179]
	global_load_dwordx4 v[2:5], v[14:15], off
	global_load_dwordx4 v[6:9], v[14:15], off offset:16
	global_load_dwordx4 v[10:13], v[14:15], off offset:32
	s_nop 0
	global_load_dwordx4 v[14:17], v[14:15], off offset:48
	v_ashrrev_i32_e32 v182, 3, v18
	v_ashrrev_i32_e32 v183, 31, v182
	v_bfe_i32 v37, v18, 5, 1
	v_and_b32_e32 v38, 7, v18
	v_lshlrev_b64 v[18:19], 8, v[182:183]
	v_lshl_add_u64 v[18:19], s[18:19], 0, v[18:19]
	v_lshlrev_b32_e32 v178, 3, v38
	v_lshl_add_u64 v[18:19], v[18:19], 0, v[178:179]
	v_mov_b64_e32 v[20:21], s[22:23]
	v_add_co_u32_e32 v22, vcc, s39, v18
	v_mad_i64_i32 v[20:21], s[22:23], v182, s37, v[20:21]
	s_nop 0
	v_addc_co_u32_e32 v23, vcc, 0, v19, vcc
	v_lshl_add_u64 v[184:185], v[20:21], 0, v[178:179]
	global_load_dwordx2 v[20:21], v[18:19], off
	v_add_co_u32_e32 v18, vcc, s40, v18
	s_nop 0
	s_nop 0
	v_addc_co_u32_e32 v19, vcc, 0, v19, vcc
	global_load_dwordx2 v[24:25], v[184:185], off
	global_load_dwordx2 v[26:27], v[184:185], off offset:64
	global_load_dwordx2 v[28:29], v[184:185], off offset:128
	s_nop 0
	global_load_dwordx2 v[22:23], v[22:23], off
	s_nop 0
	global_load_dwordx2 v[18:19], v[18:19], off
	s_nop 0
	s_nop 0
	s_nop 0
	s_nop 0
	s_nop 0
	v_cmp_eq_u32_e32 vcc, 0, v217
	v_lshlrev_b32_e32 v39, 5, v217
	s_cmp_lt_i32 s8, 4
	s_waitcnt vmcnt(9)
	v_lshlrev_b32_e32 v40, 16, v2
	v_and_b32_e32 v2, 0xffff0000, v2
	v_lshlrev_b32_e32 v42, 16, v4
	v_and_b32_e32 v4, 0xffff0000, v4
	v_cvt_pk_fp8_f32 v31, v40, v2
	v_cvt_pk_fp8_f32 v32, v42, v4
	v_lshlrev_b32_e32 v41, 16, v3
	v_and_b32_e32 v3, 0xffff0000, v3
	v_lshlrev_b32_e32 v43, 16, v5
	v_and_b32_e32 v5, 0xffff0000, v5
	s_waitcnt vmcnt(8)
	v_lshlrev_b32_e32 v44, 16, v6
	v_and_b32_e32 v6, 0xffff0000, v6
	v_cvt_pk_fp8_f32 v31, v41, v3 op_sel:[0,0,1]
	s_waitcnt vmcnt(6)
	v_lshlrev_b32_e32 v2, 16, v14
	v_and_b32_e32 v3, 0xffff0000, v14
	s_nop 0
	v_cvt_pk_fp8_f32 v33, v44, v6
	v_cvt_pk_fp8_f32 v32, v43, v5 op_sel:[0,0,1]
	v_cvt_pk_fp8_f32 v4, v2, v3
	v_lshlrev_b32_e32 v3, 16, v16
	v_and_b32_e32 v5, 0xffff0000, v16
	s_nop 0
	v_lshlrev_b32_e32 v46, 16, v8
	v_and_b32_e32 v8, 0xffff0000, v8
	v_lshlrev_b32_e32 v48, 16, v10
	v_and_b32_e32 v10, 0xffff0000, v10
	v_lshlrev_b32_e32 v50, 16, v12
	v_and_b32_e32 v12, 0xffff0000, v12
	v_cvt_pk_fp8_f32 v6, v3, v5
	v_cvt_pk_fp8_f32 v34, v46, v8
	v_cvt_pk_fp8_f32 v35, v48, v10
	v_cvt_pk_fp8_f32 v36, v50, v12
	v_lshlrev_b32_e32 v45, 16, v7
	v_and_b32_e32 v7, 0xffff0000, v7
	v_lshlrev_b32_e32 v2, 16, v15
	v_and_b32_e32 v3, 0xffff0000, v15
	v_cvt_pk_fp8_f32 v33, v45, v7 op_sel:[0,0,1]
	v_lshlrev_b32_e32 v5, 16, v17
	v_and_b32_e32 v7, 0xffff0000, v17
	v_cvt_pk_fp8_f32 v4, v2, v3 op_sel:[0,0,1]
	v_lshlrev_b32_e32 v3, 2, v38
	v_lshlrev_b32_e32 v47, 16, v9
	v_and_b32_e32 v9, 0xffff0000, v9
	v_lshlrev_b32_e32 v49, 16, v11
	v_and_b32_e32 v11, 0xffff0000, v11
	v_lshlrev_b32_e32 v51, 16, v13
	v_and_b32_e32 v13, 0xffff0000, v13
	v_cvt_pk_fp8_f32 v6, v5, v7 op_sel:[0,0,1]
	v_mul_lo_u32 v2, v182, s38
	v_and_b32_e32 v5, 16, v3
	v_cvt_pk_fp8_f32 v34, v47, v9 op_sel:[0,0,1]
	v_cvt_pk_fp8_f32 v35, v49, v11 op_sel:[0,0,1]
	v_cvt_pk_fp8_f32 v36, v51, v13 op_sel:[0,0,1]
	v_add_u32_e32 v183, v2, v178
	v_add_u32_e32 v2, v2, v5
	v_and_or_b32 v218, v3, 12, v2
	v_add_u32_e32 v2, 0, v218
	v_cndmask_b32_e32 v120, 0, v4, vcc
	v_mul_u32_u24_e32 v7, 0x50, v30
	v_and_b32_e32 v128, v37, v4
	v_add_u32_e32 v4, 0, v183
	v_add_u32_e32 v3, 0x1400, v2
	v_cndmask_b32_e32 v121, 0, v6, vcc
	v_cndmask_b32_e32 v119, 0, v36, vcc
	v_cndmask_b32_e32 v118, 0, v35, vcc
	v_cndmask_b32_e32 v117, 0, v34, vcc
	v_cndmask_b32_e32 v116, 0, v33, vcc
	v_cndmask_b32_e32 v115, 0, v32, vcc
	v_cndmask_b32_e32 v114, 0, v31, vcc
	v_and_b32_e32 v129, v37, v6
	v_and_b32_e32 v127, v37, v36
	v_and_b32_e32 v126, v37, v35
	v_and_b32_e32 v125, v37, v34
	v_and_b32_e32 v124, v37, v33
	v_and_b32_e32 v123, v37, v32
	v_and_b32_e32 v122, v37, v31
	s_waitcnt vmcnt(5)
	ds_write_b64 v4, v[20:21]
	s_waitcnt vmcnt(4)
	ds_write2_b32 v3, v24, v25 offset1:8
	s_waitcnt vmcnt(1)
	ds_write_b64 v4, v[22:23] offset:10240
	v_add_u32_e32 v3, 0x3c00, v2
	v_add_u32_e32 v2, 0x6400, v2
	v_add3_u32 v219, v39, v7, 0
	ds_write2_b32 v3, v26, v27 offset1:8
	s_waitcnt vmcnt(0)
	ds_write_b64 v4, v[18:19] offset:20480
	ds_write2_b32 v2, v28, v29 offset1:8
	s_waitcnt lgkmcnt(0)
	s_barrier
	ds_read_b128 v[2:5], v219
	ds_read_b128 v[6:9], v219 offset:16
	s_waitcnt lgkmcnt(0)
	v_mfma_f32_32x32x64_f8f6f4 v[82:97], v[2:9], v[114:121], 0
	v_mfma_f32_32x32x64_f8f6f4 v[66:81], v[2:9], v[122:129], 0
	s_cbranch_scc1 .LBB0_1887
	s_setprio 1

; DI f32x16 mfma8(v8i a, v8i b, f32x16 c) { return __builtin_amdgcn_mfma_scale_f32_32x32x64_f8f6f4(a, b, c, 0, 0, 0, 0, 0, 0); }
; DI void attn_unit_d8(unsigned char* lds, const AttnArgs& a) {
;     ...
;     auto tile = [&](const unsigned char* Kb, const unsigned char* Kn, v8i& Pa, v8i& Pb, v8i& v0, v8i& v1, const v8i& Qa, const v8i& Qb, const v8i& w0, const v8i& w1) __attribute__((always_inline)) {
;         qk(Kb, 1, s1a, s1b);
;         v0 = rd32(Kb + voff); v1 = rd32(Kb + voff + 32 * A8_PITCH);
;         o0[0] = mfma8(w0, Qa, o0[0]); o1[0] = mfma8(w0, Qb, o1[0]); o0[1] = mfma8(w1, Qa, o0[1]); o1[1] = mfma8(w1, Qb, o1[1]);
;         expsum(s0a, l0); expsum(s0b, l1); pack4(s0a, Pa, 0); pack4(s0b, Pb, 0);
;         qk(Kn, 0, s0a, s0b);
;         expsum(s1a, l0); expsum(s1b, l1); pack4(s1a, Pa, 4); pack4(s1b, Pb, 4);
; #pragma unroll
;         for (int i = 0; i < 8; ++i) { __builtin_amdgcn_sched_group_barrier(0x008, 1, 0); __builtin_amdgcn_sched_group_barrier(0x402, 22, 0); }
;     };
;     for (int t = a.t0; t < a.t1; t += 2) {
;         const int s1 = sb + 1 >= 5 ? sb - 4 : sb + 1, s2 = sb + 2 >= 5 ? sb - 3 : sb + 2, s3 = sb + 3 >= 5 ? sb - 2 : sb + 3, s4 = sb + 4 >= 5 ? sb - 1 : sb + 4;
;         { const int ta = t + 3, tb = t + 4; gload(ta < a.t1 ? ta : a.t1 - 1, kreg0, vreg0); gload(tb < a.t1 ? tb : a.t1 - 1, kreg1, vreg1); }
;         tile(lds + sb * D8_SLOT, lds + s1 * D8_SLOT, PaX, PbX, vX0, vX1, PaY, PbY, vY0, vY1);
;         tile(lds + s1 * D8_SLOT, lds + s2 * D8_SLOT, PaY, PbY, vY0, vY1, PaX, PbX, vX0, vX1);
;         lstore(s3, kreg0, vreg0); lstore(s4, kreg1, vreg1);
;         __syncthreads();
;         sb = s2;
;     }
.LBB0_1888:
	s_add_i32 s22, s22, 2
	s_mul_i32 s8, s23, 0x2800
	s_cmp_gt_i32 s23, 3
	v_mfma_f32_32x32x64_f8f6f4 v[50:65], v[154:161], v[138:145], v[50:65]
	v_exp_f32_e32 v194, v90
	v_add_u32_e32 v90, s8, v219
	s_cselect_b32 s8, -4, 1
	s_add_i32 s51, s8, s23
	s_cmp_gt_i32 s23, 2
	s_cselect_b32 s8, -3, 2
	s_add_i32 s8, s8, s23
	s_cmp_gt_i32 s23, 1
	s_cselect_b32 s52, -2, 3
	s_add_i32 s52, s52, s23
	s_cmp_gt_i32 s23, 0
	s_cselect_b32 s53, -1, 4
	s_min_u32 s56, s22, 64
	s_add_i32 s53, s53, s23
	s_cmp_lt_u32 s22, 61
	s_mul_i32 s50, s8, 0x2800
	s_mov_b32 s23, s8
	s_cselect_b64 s[54:55], -1, 0
	s_lshl_b32 s8, s56, 6
	s_add_i32 s56, s8, 0xc0
	s_add_i32 s57, s8, 0xfffff0c0
	s_and_b64 s[54:55], s[54:55], exec
	v_lshl_add_u64 v[98:99], v[184:185], 0, s[8:9]
	s_cselect_b32 s8, s56, s57
	s_cselect_b32 s55, s19, s21
	s_cselect_b32 s54, s18, s20
	s_min_u32 s58, s22, 63
	v_exp_f32_e32 v200, v82
	v_exp_f32_e32 v201, v83
	v_exp_f32_e32 v198, v84
	v_exp_f32_e32 v199, v85
	v_exp_f32_e32 v202, v86
	v_exp_f32_e32 v203, v87
	v_exp_f32_e32 v196, v88
	v_exp_f32_e32 v197, v89
	ds_read_b128 v[82:85], v90 offset:2560
	ds_read_b128 v[86:89], v90 offset:2576
	global_load_dwordx2 v[204:205], v[98:99], off offset:192
	v_add_u32_e32 v98, s8, v182
	s_cmp_lt_u32 s22, 60
	v_ashrrev_i32_e32 v99, 31, v98
	s_cselect_b64 s[56:57], -1, 0
	s_lshl_b32 s8, s58, 6
	v_lshlrev_b64 v[98:99], 8, v[98:99]
	s_add_i32 s58, s8, 0x100
	s_add_i32 s59, s8, 0xfffff100
	v_lshl_add_u64 v[98:99], s[54:55], 0, v[98:99]
	s_and_b64 s[54:55], s[56:57], exec
	v_lshl_add_u64 v[100:101], v[184:185], 0, s[8:9]
	s_cselect_b32 s8, s58, s59
	v_lshl_add_u64 v[220:221], v[98:99], 0, v[178:179]
	v_add_u32_e32 v98, s8, v182
	v_ashrrev_i32_e32 v99, 31, v98
	s_cselect_b32 s55, s19, s21
	s_cselect_b32 s54, s18, s20
	v_lshlrev_b64 v[98:99], 8, v[98:99]
	v_lshl_add_u64 v[98:99], s[54:55], 0, v[98:99]
	global_load_dwordx2 v[206:207], v[100:101], off offset:256
	v_lshl_add_u64 v[222:223], v[98:99], 0, v[178:179]
	s_waitcnt lgkmcnt(0)
	v_mfma_f32_32x32x64_f8f6f4 v[98:113], v[82:89], v[114:121], 0
	v_exp_f32_e32 v195, v91
	v_exp_f32_e32 v224, v92
	v_exp_f32_e32 v225, v93
	v_exp_f32_e32 v226, v94
	v_exp_f32_e32 v227, v95
	v_exp_f32_e32 v228, v96
	v_exp_f32_e32 v229, v97
	ds_read_b128 v[170:173], v90 offset:5120
	ds_read_b128 v[174:177], v90 offset:5136
	ds_read_b128 v[162:165], v90 offset:7680
	ds_read_b128 v[166:169], v90 offset:7696
	v_pk_add_f32 v[90:91], v[188:189], v[200:201]
	v_pk_add_f32 v[92:93], v[186:187], v[198:199]
	v_pk_add_f32 v[90:91], v[202:203], v[90:91]
	v_pk_add_f32 v[92:93], v[196:197], v[92:93]
	v_pk_add_f32 v[90:91], v[194:195], v[90:91]
	v_pk_add_f32 v[92:93], v[224:225], v[92:93]
	v_exp_f32_e32 v66, v66
	v_exp_f32_e32 v67, v67
	v_exp_f32_e32 v68, v68
	v_exp_f32_e32 v69, v69
	v_exp_f32_e32 v70, v70
	v_exp_f32_e32 v71, v71
	v_exp_f32_e32 v72, v72
	v_pk_add_f32 v[230:231], v[228:229], v[92:93]
	v_pk_add_f32 v[232:233], v[226:227], v[90:91]
	v_mfma_f32_32x32x64_f8f6f4 v[82:97], v[82:89], v[122:129], 0
	v_exp_f32_e32 v73, v73
	v_exp_f32_e32 v74, v74
	v_exp_f32_e32 v75, v75
	v_exp_f32_e32 v76, v76
	v_exp_f32_e32 v77, v77
	v_exp_f32_e32 v78, v78
	v_exp_f32_e32 v79, v79
	v_exp_f32_e32 v80, v80
	v_exp_f32_e32 v81, v81
	v_pk_add_f32 v[188:189], v[192:193], v[66:67]
	v_pk_add_f32 v[190:191], v[190:191], v[68:69]
	s_nop 0
	v_pk_add_f32 v[188:189], v[70:71], v[188:189]
	v_pk_add_f32 v[190:191], v[72:73], v[190:191]
	s_nop 0
	v_cvt_scalef32_pk_fp8_f32 v186, v200, v201, s36
	v_pk_add_f32 v[188:189], v[74:75], v[188:189]
	v_pk_add_f32 v[190:191], v[76:77], v[190:191]
	v_cvt_scalef32_pk_fp8_f32 v187, v202, v203, s36
	v_cvt_scalef32_pk_fp8_f32 v186, v198, v199, s36 op_sel:[0,0,0,1]
	v_pk_add_f32 v[192:193], v[78:79], v[188:189]
	v_pk_add_f32 v[190:191], v[80:81], v[190:191]
	v_mfma_f32_32x32x64_f8f6f4 v[2:17], v[154:161], v[130:137], v[2:17]
	s_nop 0
	s_nop 0
	s_nop 0
	s_nop 0
	s_nop 0
	s_nop 0
	s_mulk_i32 s51, 0x2800
	v_cvt_scalef32_pk_fp8_f32 v188, v194, v195, s36
	v_cvt_scalef32_pk_fp8_f32 v189, v226, v227, s36
	v_cvt_scalef32_pk_fp8_f32 v154, v66, v67, s36
	v_cvt_scalef32_pk_fp8_f32 v155, v70, v71, s36
	v_cvt_scalef32_pk_fp8_f32 v156, v74, v75, s36
	v_cvt_scalef32_pk_fp8_f32 v157, v78, v79, s36
	v_cvt_scalef32_pk_fp8_f32 v187, v196, v197, s36 op_sel:[0,0,0,1]
	v_add_u32_e32 v234, s51, v219
	v_cvt_scalef32_pk_fp8_f32 v188, v224, v225, s36 op_sel:[0,0,0,1]
	v_cvt_scalef32_pk_fp8_f32 v189, v228, v229, s36 op_sel:[0,0,0,1]
	v_cvt_scalef32_pk_fp8_f32 v154, v68, v69, s36 op_sel:[0,0,0,1]
	v_cvt_scalef32_pk_fp8_f32 v155, v72, v73, s36 op_sel:[0,0,0,1]
	v_cvt_scalef32_pk_fp8_f32 v156, v76, v77, s36 op_sel:[0,0,0,1]
	v_cvt_scalef32_pk_fp8_f32 v157, v80, v81, s36 op_sel:[0,0,0,1]
	v_exp_f32_e32 v98, v98
	v_exp_f32_e32 v99, v99
	v_mfma_f32_32x32x64_f8f6f4 v[34:49], v[146:153], v[138:145], v[34:49]
	v_exp_f32_e32 v100, v100
	v_exp_f32_e32 v101, v101
	v_exp_f32_e32 v102, v102
	v_exp_f32_e32 v103, v103
	v_exp_f32_e32 v104, v104
	v_exp_f32_e32 v105, v105
	v_exp_f32_e32 v106, v106
	v_exp_f32_e32 v107, v107
	v_exp_f32_e32 v108, v108
	v_exp_f32_e32 v109, v109
	v_exp_f32_e32 v110, v110
	v_exp_f32_e32 v111, v111
	v_exp_f32_e32 v112, v112
	v_exp_f32_e32 v113, v113
	ds_read_b128 v[194:197], v234
	ds_read_b128 v[198:201], v234 offset:16
	v_pk_add_f32 v[66:67], v[232:233], v[98:99]
	v_pk_add_f32 v[68:69], v[230:231], v[100:101]
	v_pk_add_f32 v[66:67], v[102:103], v[66:67]
	v_pk_add_f32 v[68:69], v[104:105], v[68:69]
	v_pk_add_f32 v[66:67], v[106:107], v[66:67]
	v_pk_add_f32 v[68:69], v[108:109], v[68:69]
	v_pk_add_f32 v[140:141], v[110:111], v[66:67]
	v_pk_add_f32 v[138:139], v[112:113], v[68:69]
	v_mfma_f32_32x32x64_f8f6f4 v[18:33], v[146:153], v[130:137], v[18:33]
	v_exp_f32_e32 v82, v82
	v_exp_f32_e32 v83, v83
	v_exp_f32_e32 v84, v84
	v_exp_f32_e32 v85, v85
	v_exp_f32_e32 v86, v86
	v_exp_f32_e32 v87, v87
	v_exp_f32_e32 v88, v88
	v_exp_f32_e32 v89, v89
	v_exp_f32_e32 v90, v90
	v_exp_f32_e32 v91, v91
	v_exp_f32_e32 v92, v92
	v_exp_f32_e32 v93, v93
	v_exp_f32_e32 v94, v94
	v_exp_f32_e32 v95, v95
	v_exp_f32_e32 v96, v96
	v_exp_f32_e32 v97, v97
	v_pk_add_f32 v[66:67], v[192:193], v[82:83]
	v_pk_add_f32 v[68:69], v[190:191], v[84:85]
	v_pk_add_f32 v[66:67], v[86:87], v[66:67]
	v_pk_add_f32 v[68:69], v[88:89], v[68:69]
	v_pk_add_f32 v[130:131], v[90:91], v[66:67]
	v_pk_add_f32 v[132:133], v[92:93], v[68:69]
	s_waitcnt lgkmcnt(0)
; DI f32x16 mfma8(v8i a, v8i b, f32x16 c) { return __builtin_amdgcn_mfma_scale_f32_32x32x64_f8f6f4(a, b, c, 0, 0, 0, 0, 0, 0); }
; DI void attn_unit_d8(unsigned char* lds, const AttnArgs& a) {
;     ...
;     auto tile = [&](const unsigned char* Kb, const unsigned char* Kn, v8i& Pa, v8i& Pb, v8i& v0, v8i& v1, const v8i& Qa, const v8i& Qb, const v8i& w0, const v8i& w1) __attribute__((always_inline)) {
;         qk(Kb, 1, s1a, s1b);
;         v0 = rd32(Kb + voff); v1 = rd32(Kb + voff + 32 * A8_PITCH);
;         o0[0] = mfma8(w0, Qa, o0[0]); o1[0] = mfma8(w0, Qb, o1[0]); o0[1] = mfma8(w1, Qa, o0[1]); o1[1] = mfma8(w1, Qb, o1[1]);
;         expsum(s0a, l0); expsum(s0b, l1); pack4(s0a, Pa, 0); pack4(s0b, Pb, 0);
;         qk(Kn, 0, s0a, s0b);
;         expsum(s1a, l0); expsum(s1b, l1); pack4(s1a, Pa, 4); pack4(s1b, Pb, 4);
; #pragma unroll
;         for (int i = 0; i < 8; ++i) { __builtin_amdgcn_sched_group_barrier(0x008, 1, 0); __builtin_amdgcn_sched_group_barrier(0x402, 22, 0); }
;     };
;     for (int t = a.t0; t < a.t1; t += 2) {
;         const int s1 = sb + 1 >= 5 ? sb - 4 : sb + 1, s2 = sb + 2 >= 5 ? sb - 3 : sb + 2, s3 = sb + 3 >= 5 ? sb - 2 : sb + 3, s4 = sb + 4 >= 5 ? sb - 1 : sb + 4;
;         { const int ta = t + 3, tb = t + 4; gload(ta < a.t1 ? ta : a.t1 - 1, kreg0, vreg0); gload(tb < a.t1 ? tb : a.t1 - 1, kreg1, vreg1); }
;         tile(lds + sb * D8_SLOT, lds + s1 * D8_SLOT, PaX, PbX, vX0, vX1, PaY, PbY, vY0, vY1);
;         tile(lds + s1 * D8_SLOT, lds + s2 * D8_SLOT, PaY, PbY, vY0, vY1, PaX, PbX, vX0, vX1);
;         lstore(s3, kreg0, vreg0); lstore(s4, kreg1, vreg1);
;         __syncthreads();
;         sb = s2;
;     }
	v_mfma_f32_32x32x64_f8f6f4 v[66:81], v[194:201], v[114:121], 0
	s_nop 0
	s_nop 0
	s_nop 0
	s_nop 0
	s_nop 0
	s_nop 0
	s_nop 0
	v_cvt_scalef32_pk_fp8_f32 v190, v98, v99, s36
	v_cvt_scalef32_pk_fp8_f32 v191, v102, v103, s36
	v_cvt_scalef32_pk_fp8_f32 v192, v106, v107, s36
	v_cvt_scalef32_pk_fp8_f32 v193, v110, v111, s36
	v_cvt_scalef32_pk_fp8_f32 v158, v82, v83, s36
	v_cvt_scalef32_pk_fp8_f32 v159, v86, v87, s36
	v_pk_add_f32 v[142:143], v[96:97], v[132:133]
	v_pk_add_f32 v[144:145], v[94:95], v[130:131]
	v_cvt_scalef32_pk_fp8_f32 v160, v90, v91, s36
	v_cvt_scalef32_pk_fp8_f32 v190, v100, v101, s36 op_sel:[0,0,0,1]
	v_cvt_scalef32_pk_fp8_f32 v191, v104, v105, s36 op_sel:[0,0,0,1]
	v_cvt_scalef32_pk_fp8_f32 v192, v108, v109, s36 op_sel:[0,0,0,1]
	v_cvt_scalef32_pk_fp8_f32 v193, v112, v113, s36 op_sel:[0,0,0,1]
	v_cvt_scalef32_pk_fp8_f32 v158, v84, v85, s36 op_sel:[0,0,0,1]
	v_cvt_scalef32_pk_fp8_f32 v159, v88, v89, s36 op_sel:[0,0,0,1]
	v_mfma_f32_32x32x64_f8f6f4 v[98:113], v[194:201], v[122:129], 0
	global_load_dwordx2 v[194:195], v[220:221], off
	global_load_dwordx2 v[196:197], v[222:223], off
	ds_read_b128 v[130:133], v234 offset:2560
	ds_read_b128 v[134:137], v234 offset:2576
	v_exp_f32_e32 v146, v66
	v_exp_f32_e32 v147, v67
	s_mulk_i32 s52, 0x2800
	s_nop 0
	s_add_i32 s8, s52, 0
	v_cvt_scalef32_pk_fp8_f32 v161, v94, v95, s36
	v_add_u32_e32 v224, s8, v183
	v_cvt_scalef32_pk_fp8_f32 v160, v92, v93, s36 op_sel:[0,0,0,1]
	v_cvt_scalef32_pk_fp8_f32 v161, v96, v97, s36 op_sel:[0,0,0,1]
	v_exp_f32_e32 v148, v68
	v_exp_f32_e32 v149, v69
	v_exp_f32_e32 v150, v70
	v_exp_f32_e32 v151, v71
	v_exp_f32_e32 v152, v72
	v_exp_f32_e32 v153, v73
	v_exp_f32_e32 v198, v74
	v_exp_f32_e32 v199, v75
	v_exp_f32_e32 v200, v76
	v_exp_f32_e32 v201, v77
	v_exp_f32_e32 v202, v78
	v_exp_f32_e32 v203, v79
	v_exp_f32_e32 v220, v80
	v_exp_f32_e32 v221, v81
	v_pk_add_f32 v[66:67], v[140:141], v[146:147]
	s_waitcnt lgkmcnt(0)
	v_mfma_f32_32x32x64_f8f6f4 v[82:97], v[130:137], v[114:121], 0
	v_add_f32_e64 v68, v138, v148
	v_add_f32_e64 v69, v139, v149
	v_add_f32_e64 v66, v150, v66
	v_add_f32_e64 v67, v151, v67
	v_add_f32_e64 v68, v152, v68
	v_add_f32_e64 v69, v153, v69
	v_add_f32_e64 v138, v198, v66
	v_add_f32_e64 v139, v199, v67
	v_add_f32_e64 v140, v200, v68
	v_add_f32_e64 v141, v201, v69
	v_exp_f32_e32 v98, v98
	v_exp_f32_e32 v99, v99
	v_exp_f32_e32 v100, v100
	v_exp_f32_e32 v101, v101
	v_exp_f32_e32 v102, v102
	v_exp_f32_e32 v103, v103
	v_exp_f32_e32 v104, v104
	v_exp_f32_e32 v105, v105
	v_exp_f32_e32 v106, v106
	v_exp_f32_e32 v107, v107
	v_exp_f32_e32 v108, v108
	v_exp_f32_e32 v109, v109
	v_exp_f32_e32 v110, v110
	v_exp_f32_e32 v111, v111
	v_exp_f32_e32 v112, v112
	v_exp_f32_e32 v113, v113
	v_exp_f32_e32 v82, v82
	v_mfma_f32_32x32x64_f8f6f4 v[66:81], v[130:137], v[122:129], 0
	v_add_f32_e64 v130, v144, v98
	v_add_f32_e64 v131, v145, v99
	v_add_f32_e64 v132, v142, v100
	v_add_f32_e64 v133, v143, v101
	v_add_f32_e64 v142, v102, v130
	v_add_f32_e64 v143, v103, v131
	v_add_f32_e64 v132, v104, v132
	v_add_f32_e64 v133, v105, v133
	v_add_f32_e64 v134, v220, v140
	v_add_f32_e64 v135, v221, v141
	v_add_f32_e64 v136, v202, v138
	v_add_f32_e64 v137, v203, v139
	s_nop 0
	s_nop 0
	s_nop 0
	s_nop 0
	s_nop 0
	s_nop 0
	v_pk_add_f32 v[142:143], v[106:107], v[142:143]
	v_pk_add_f32 v[132:133], v[108:109], v[132:133]
	v_cvt_scalef32_pk_fp8_f32 v138, v146, v147, s36
	v_cvt_scalef32_pk_fp8_f32 v139, v150, v151, s36
	v_cvt_scalef32_pk_fp8_f32 v140, v198, v199, s36
	v_cvt_scalef32_pk_fp8_f32 v141, v202, v203, s36
	v_cvt_scalef32_pk_fp8_f32 v130, v98, v99, s36
	v_cvt_scalef32_pk_fp8_f32 v131, v102, v103, s36
	v_pk_add_f32 v[146:147], v[112:113], v[132:133]
	v_pk_add_f32 v[150:151], v[110:111], v[142:143]
	v_mfma_f32_32x32x64_f8f6f4 v[50:65], v[170:177], v[186:193], v[50:65]
	v_exp_f32_e32 v83, v83
	v_exp_f32_e32 v84, v84
	v_exp_f32_e32 v85, v85
	v_add_u32_e32 v102, s50, v219
	v_exp_f32_e32 v86, v86
	v_exp_f32_e32 v87, v87
	v_exp_f32_e32 v88, v88
	v_exp_f32_e32 v89, v89
	v_cvt_scalef32_pk_fp8_f32 v130, v100, v101, s36 op_sel:[0,0,0,1]
	v_cvt_scalef32_pk_fp8_f32 v131, v104, v105, s36 op_sel:[0,0,0,1]
	v_exp_f32_e32 v90, v90
	v_exp_f32_e32 v91, v91
	v_exp_f32_e32 v92, v92
	v_exp_f32_e32 v93, v93
	ds_read_b128 v[98:101], v102
	ds_read_b128 v[102:105], v102 offset:16
	s_nop 0
	v_cvt_scalef32_pk_fp8_f32 v138, v148, v149, s36 op_sel:[0,0,0,1]
	v_cvt_scalef32_pk_fp8_f32 v139, v152, v153, s36 op_sel:[0,0,0,1]
	v_cvt_scalef32_pk_fp8_f32 v140, v200, v201, s36 op_sel:[0,0,0,1]
	v_cvt_scalef32_pk_fp8_f32 v141, v220, v221, s36 op_sel:[0,0,0,1]
	s_nop 0
	v_exp_f32_e32 v94, v94
	v_exp_f32_e32 v95, v95
	v_mfma_f32_32x32x64_f8f6f4 v[2:17], v[170:177], v[154:161], v[2:17]
	v_exp_f32_e32 v148, v96
	v_cvt_scalef32_pk_fp8_f32 v132, v106, v107, s36
	v_exp_f32_e32 v149, v97
	v_pk_add_f32 v[96:97], v[136:137], v[82:83]
	v_pk_add_f32 v[106:107], v[134:135], v[84:85]
	v_exp_f32_e32 v66, v66
	v_exp_f32_e32 v67, v67
	v_exp_f32_e32 v68, v68
	v_exp_f32_e32 v69, v69
	v_cvt_scalef32_pk_fp8_f32 v133, v110, v111, s36
	v_pk_add_f32 v[106:107], v[88:89], v[106:107]
	v_pk_add_f32 v[96:97], v[86:87], v[96:97]
	v_exp_f32_e32 v70, v70
	v_exp_f32_e32 v71, v71
	v_exp_f32_e32 v72, v72
	v_exp_f32_e32 v73, v73
	v_cvt_scalef32_pk_fp8_f32 v132, v108, v109, s36 op_sel:[0,0,0,1]
	v_cvt_scalef32_pk_fp8_f32 v133, v112, v113, s36 op_sel:[0,0,0,1]
	v_pk_add_f32 v[96:97], v[90:91], v[96:97]
	v_pk_add_f32 v[106:107], v[92:93], v[106:107]
	v_exp_f32_e32 v74, v74
	v_exp_f32_e32 v75, v75
	v_mfma_f32_32x32x64_f8f6f4 v[34:49], v[162:169], v[186:193], v[34:49]
	v_exp_f32_e32 v76, v76
	v_exp_f32_e32 v77, v77
	v_exp_f32_e32 v78, v78
	v_exp_f32_e32 v79, v79
; DI f32x16 mfma8(v8i a, v8i b, f32x16 c) { return __builtin_amdgcn_mfma_scale_f32_32x32x64_f8f6f4(a, b, c, 0, 0, 0, 0, 0, 0); }
; DI void attn_unit_d8(unsigned char* lds, const AttnArgs& a) {
;     ...
;     for (int t = a.t0; t < a.t1; t += 2) {
;         const int s1 = sb + 1 >= 5 ? sb - 4 : sb + 1, s2 = sb + 2 >= 5 ? sb - 3 : sb + 2, s3 = sb + 3 >= 5 ? sb - 2 : sb + 3, s4 = sb + 4 >= 5 ? sb - 1 : sb + 4;
;         { const int ta = t + 3, tb = t + 4; gload(ta < a.t1 ? ta : a.t1 - 1, kreg0, vreg0); gload(tb < a.t1 ? tb : a.t1 - 1, kreg1, vreg1); }
;         tile(lds + sb * D8_SLOT, lds + s1 * D8_SLOT, PaX, PbX, vX0, vX1, PaY, PbY, vY0, vY1);
;         tile(lds + s1 * D8_SLOT, lds + s2 * D8_SLOT, PaY, PbY, vY0, vY1, PaX, PbX, vX0, vX1);
;         lstore(s3, kreg0, vreg0); lstore(s4, kreg1, vreg1);
;         __syncthreads();
;         sb = s2;
;     }
;     o0[0] = mfma8(vY0, PaY, o0[0]); o1[0] = mfma8(vY0, PbY, o1[0]); o0[1] = mfma8(vY1, PaY, o0[1]); o1[1] = mfma8(vY1, PbY, o1[1]);
;     __builtin_amdgcn_s_setprio(0);
;     float lt0 = l0[0] + l0[1] + l0[2] + l0[3]; lt0 += __shfl_xor(lt0, 32);
;     float lt1 = l1[0] + l1[1] + l1[2] + l1[3]; lt1 += __shfl_xor(lt1, 32);
;     unsigned char* op = a.out8 + (size_t)(wid * 32 + r) * 1024 + 4 * h;
;     const float r0 = 16.0f / lt0, r1 = 16.0f * a.lam / lt1;
;     float ss = 0.f;
; #pragma unroll
;     for (int d = 0; d < 2; ++d)
; #pragma unroll
;         for (int i = 0; i < 16; ++i) { const float v = o0[d][i] * r0 - o1[d][i] * r1; o0[d][i] = v; ss += v * v; }
;     ss += __shfl_xor(ss, 32);
	s_nop 0
	v_exp_f32_e32 v80, v80
	v_exp_f32_e32 v81, v81
	s_nop 0
	s_nop 0
	v_cvt_scalef32_pk_fp8_f32 v142, v82, v83, s36
	s_nop 0
	v_cvt_scalef32_pk_fp8_f32 v143, v86, v87, s36
	v_cvt_scalef32_pk_fp8_f32 v144, v90, v91, s36
	v_cvt_scalef32_pk_fp8_f32 v142, v84, v85, s36 op_sel:[0,0,0,1]
	v_pk_add_f32 v[82:83], v[150:151], v[66:67]
	v_pk_add_f32 v[84:85], v[146:147], v[68:69]
	s_mulk_i32 s53, 0x2800
	v_pk_add_f32 v[186:187], v[148:149], v[106:107]
	v_pk_add_f32 v[188:189], v[94:95], v[96:97]
	v_cvt_scalef32_pk_fp8_f32 v145, v94, v95, s36
	v_cvt_scalef32_pk_fp8_f32 v143, v88, v89, s36 op_sel:[0,0,0,1]
	v_cvt_scalef32_pk_fp8_f32 v144, v92, v93, s36 op_sel:[0,0,0,1]
	v_pk_add_f32 v[84:85], v[72:73], v[84:85]
	v_mfma_f32_32x32x64_f8f6f4 v[18:33], v[162:169], v[154:161], v[18:33]
	v_add_f32_e64 v82, v70, v82
	v_add_f32_e64 v83, v71, v83
	s_nop 0
	s_nop 0
	s_nop 0
	s_nop 0
	s_add_i32 s51, s53, 0
	v_add_f32_e64 v82, v74, v82
	v_add_f32_e64 v83, v75, v83
	v_add_f32_e64 v84, v76, v84
	v_add_f32_e64 v85, v77, v85
	v_cvt_scalef32_pk_fp8_f32 v134, v66, v67, s36
	v_cvt_scalef32_pk_fp8_f32 v135, v70, v71, s36
	v_cvt_scalef32_pk_fp8_f32 v136, v74, v75, s36
	v_cvt_scalef32_pk_fp8_f32 v137, v78, v79, s36
	v_pk_add_f32 v[190:191], v[80:81], v[84:85]
	v_pk_add_f32 v[192:193], v[78:79], v[82:83]
	v_add_u32_e32 v106, s8, v218
	v_add_u32_e32 v107, s51, v183
	v_cvt_scalef32_pk_fp8_f32 v145, v148, v149, s36 op_sel:[0,0,0,1]
	v_cvt_scalef32_pk_fp8_f32 v134, v68, v69, s36 op_sel:[0,0,0,1]
	v_cvt_scalef32_pk_fp8_f32 v135, v72, v73, s36 op_sel:[0,0,0,1]
	v_cvt_scalef32_pk_fp8_f32 v136, v76, v77, s36 op_sel:[0,0,0,1]
	v_cvt_scalef32_pk_fp8_f32 v137, v80, v81, s36 op_sel:[0,0,0,1]
	s_waitcnt lgkmcnt(0)
	v_mfma_f32_32x32x64_f8f6f4 v[82:97], v[98:105], v[114:121], 0
	ds_read_b128 v[154:157], v234 offset:5120
	ds_read_b128 v[158:161], v234 offset:5136
	ds_read_b128 v[146:149], v234 offset:7680
	ds_read_b128 v[150:153], v234 offset:7696
	s_cmpk_lt_u32 s22, 0x42
	s_waitcnt vmcnt(1)
	ds_write_b64 v224, v[194:195]
	v_mfma_f32_32x32x64_f8f6f4 v[66:81], v[98:105], v[122:129], 0
	v_add_u32_e32 v98, s51, v218
	v_add_u32_e32 v99, 0x1400, v106
	v_add_u32_e32 v98, 0x1400, v98
	ds_write2_b32 v99, v204, v205 offset1:8
	s_waitcnt vmcnt(0)
	ds_write_b64 v107, v[196:197]
	ds_write2_b32 v98, v206, v207 offset1:8
	s_waitcnt lgkmcnt(0)
	s_barrier
	s_cbranch_scc1 .LBB0_1888
	s_lshl_b64 s[16:17], s[16:17], 10
	s_add_u32 s8, s10, s16
	s_addc_u32 s17, s11, s17
	s_add_u32 s16, s8, s47
	v_mfma_f32_32x32x64_f8f6f4 v[50:65], v[154:161], v[138:145], v[50:65]
	s_addc_u32 s17, s17, 0
	v_mfma_f32_32x32x64_f8f6f4 v[2:17], v[154:161], v[130:137], v[2:17]
	v_mfma_f32_32x32x64_f8f6f4 v[34:49], v[146:153], v[138:145], v[34:49]
	v_mfma_f32_32x32x64_f8f6f4 v[18:33], v[146:153], v[130:137], v[18:33]
	s_setprio 0
	v_add_f32_e32 v66, v188, v189
	v_add_f32_e32 v66, v186, v66
	v_add_f32_e32 v66, v187, v66
	ds_bpermute_b32 v67, v1, v66
	v_add_f32_e32 v68, v192, v193
	v_add_f32_e32 v68, v190, v68
	v_add_f32_e32 v68, v191, v68
	ds_bpermute_b32 v69, v1, v68
	s_waitcnt lgkmcnt(1)
	v_add_f32_e32 v66, v66, v67
	v_div_scale_f32 v67, s[18:19], v66, v66, s36
	v_rcp_f32_e32 v70, v67
	s_waitcnt lgkmcnt(0)
	v_add_f32_e32 v68, v68, v69
	v_lshlrev_b32_e32 v178, 2, v217
	s_add_i32 s46, s46, s60
	v_fma_f32 v69, -v67, v70, 1.0
	v_fmac_f32_e32 v70, v69, v70
	v_div_scale_f32 v69, vcc, s36, v66, s36
	v_mul_f32_e32 v71, v69, v70
	v_fma_f32 v72, -v67, v71, v69
	v_fmac_f32_e32 v71, v72, v70
	v_fma_f32 v67, -v67, v71, v69
	v_div_scale_f32 v69, s[18:19], v68, v68, v214
	v_rcp_f32_e32 v72, v69
	v_div_fmas_f32 v67, v67, v70, v71
	v_div_fixup_f32 v66, v67, v66, s36
	s_cmpk_gt_i32 s46, 0x1ff
	v_fma_f32 v67, -v69, v72, 1.0
	v_fmac_f32_e32 v72, v67, v72
	v_div_scale_f32 v67, vcc, v214, v68, v214
	v_mul_f32_e32 v70, v67, v72
	v_fma_f32 v71, -v69, v70, v67
	v_fmac_f32_e32 v70, v71, v72
	v_fma_f32 v67, -v69, v70, v67
	v_div_fmas_f32 v67, v67, v72, v70
	v_div_fixup_f32 v68, v67, v68, v214
	v_mul_f32_e32 v2, v2, v68
	v_fma_f32 v50, v50, v66, -v2
	v_mul_f32_e32 v2, v3, v68
	v_fma_f32 v51, v51, v66, -v2
	v_mul_f32_e32 v67, v51, v51
	v_mul_f32_e32 v2, v4, v68
	v_fmac_f32_e32 v67, v50, v50
	v_fma_f32 v52, v52, v66, -v2
	v_mul_f32_e32 v2, v5, v68
	v_fmac_f32_e32 v67, v52, v52
	v_fma_f32 v53, v53, v66, -v2
	v_mul_f32_e32 v2, v6, v68
	v_fmac_f32_e32 v67, v53, v53
	v_fma_f32 v54, v54, v66, -v2
	v_mul_f32_e32 v2, v7, v68
	v_fmac_f32_e32 v67, v54, v54
	v_fma_f32 v55, v55, v66, -v2
	v_mul_f32_e32 v2, v8, v68
	v_fmac_f32_e32 v67, v55, v55
	v_fma_f32 v56, v56, v66, -v2
	v_mul_f32_e32 v2, v9, v68
	v_fmac_f32_e32 v67, v56, v56
	v_fma_f32 v57, v57, v66, -v2
	v_mul_f32_e32 v2, v10, v68
	v_fmac_f32_e32 v67, v57, v57
	v_fma_f32 v58, v58, v66, -v2
	v_mul_f32_e32 v2, v11, v68
	v_fmac_f32_e32 v67, v58, v58
	v_fma_f32 v59, v59, v66, -v2
	v_mul_f32_e32 v2, v12, v68
	v_fmac_f32_e32 v67, v59, v59
	v_fma_f32 v60, v60, v66, -v2
	v_mul_f32_e32 v2, v13, v68
	v_fmac_f32_e32 v67, v60, v60
	v_fma_f32 v61, v61, v66, -v2
	v_mul_f32_e32 v14, v14, v68
	v_fmac_f32_e32 v67, v61, v61
	v_fma_f32 v62, v62, v66, -v14
	v_mul_f32_e32 v14, v15, v68
	v_fmac_f32_e32 v67, v62, v62
	v_fma_f32 v63, v63, v66, -v14
	v_mul_f32_e32 v14, v16, v68
	v_lshlrev_b32_e32 v69, 4, v217
	v_fmac_f32_e32 v67, v63, v63
	v_fma_f32 v64, v64, v66, -v14
	v_mul_f32_e32 v14, v17, v68
	global_load_dwordx4 v[2:5], v69, s[12:13] offset:480
	global_load_dwordx4 v[6:9], v69, s[12:13] offset:288
	global_load_dwordx4 v[10:13], v69, s[12:13] offset:256
	v_fmac_f32_e32 v67, v64, v64
	v_fma_f32 v65, v65, v66, -v14
	v_mul_f32_e32 v14, v18, v68
	v_fmac_f32_e32 v67, v65, v65
	v_fma_f32 v70, v34, v66, -v14
	v_mul_f32_e32 v14, v19, v68
; DI unsigned pk4_fp8(float a, float b, float c, float d) { int r = 0; r = __builtin_amdgcn_cvt_pk_fp8_f32(a, b, r, false); r = __builtin_amdgcn_cvt_pk_fp8_f32(c, d, r, true); return (unsigned)r; }
; DI float clamp448(float x) { return __builtin_amdgcn_fmed3f(x, -448.0f, 448.0f); }
; DI void attn_unit_d8(unsigned char* lds, const AttnArgs& a) {
;     ...
;     float lt0 = l0[0] + l0[1] + l0[2] + l0[3]; lt0 += __shfl_xor(lt0, 32);
;     float lt1 = l1[0] + l1[1] + l1[2] + l1[3]; lt1 += __shfl_xor(lt1, 32);
;     unsigned char* op = a.out8 + (size_t)(wid * 32 + r) * 1024 + 4 * h;
;     const float r0 = 16.0f / lt0, r1 = 16.0f * a.lam / lt1;
;     float ss = 0.f;
; #pragma unroll
;     for (int d = 0; d < 2; ++d)
; #pragma unroll
;         for (int i = 0; i < 16; ++i) { const float v = o0[d][i] * r0 - o1[d][i] * r1; o0[d][i] = v; ss += v * v; }
;     ss += __shfl_xor(ss, 32);
;     const float rinv = rsqrtf(ss * (1.0f / 64.0f) + EPS) * a.oscale * CAT_SCALE;
;     f32x4 ggv[2][4];
; #pragma unroll
;     for (int d = 0; d < 2; ++d)
; #pragma unroll
;         for (int g = 0; g < 4; ++g) ggv[d][g] = *(const f32x4*)(a.subg + 32 * d + 8 * g + 4 * h);
;     asm volatile("" : "+v"(ggv[0][0]), "+v"(ggv[1][3]));
; #pragma unroll
;     for (int d = 0; d < 2; ++d)
; #pragma unroll
;         for (int g = 0; g < 4; ++g) { const f32x4 gg = ggv[d][g];
;             *(unsigned*)(op + 32 * d + 8 * g) = pk4_fp8(clamp448(o0[d][4 * g] * rinv * gg[0]), clamp448(o0[d][4 * g + 1] * rinv * gg[1]), clamp448(o0[d][4 * g + 2] * rinv * gg[2]), clamp448(o0[d][4 * g + 3] * rinv * gg[3])); }
; }
	v_fmac_f32_e32 v67, v70, v70
	v_fma_f32 v71, v35, v66, -v14
	v_mul_f32_e32 v14, v20, v68
	v_fmac_f32_e32 v67, v71, v71
	v_fma_f32 v72, v36, v66, -v14
	v_mul_f32_e32 v14, v21, v68
	v_fmac_f32_e32 v67, v72, v72
	v_fma_f32 v73, v37, v66, -v14
	v_mul_f32_e32 v14, v22, v68
	v_fmac_f32_e32 v67, v73, v73
	v_fma_f32 v74, v38, v66, -v14
	v_mul_f32_e32 v14, v23, v68
	v_fmac_f32_e32 v67, v74, v74
	v_fma_f32 v75, v39, v66, -v14
	v_fmac_f32_e32 v67, v75, v75
	v_pk_mul_f32 v[14:15], v[24:25], v[68:69] op_sel_hi:[1,0]
	v_pk_mul_f32 v[22:23], v[32:33], v[68:69] op_sel_hi:[1,0]
	v_pk_fma_f32 v[34:35], v[40:41], v[66:67], v[14:15] op_sel_hi:[1,0,1] neg_lo:[0,0,1] neg_hi:[0,0,1]
	s_nop 0
	v_pk_mul_f32 v[14:15], v[34:35], v[34:35]
	s_nop 0
	v_add_f32_e32 v14, v14, v67
	v_add_f32_e32 v20, v15, v14
	v_pk_mul_f32 v[14:15], v[26:27], v[68:69] op_sel_hi:[1,0]
	s_nop 0
	v_pk_fma_f32 v[36:37], v[42:43], v[66:67], v[14:15] op_sel_hi:[1,0,1] neg_lo:[0,0,1] neg_hi:[0,0,1]
	global_load_dwordx4 v[14:17], v69, s[12:13] offset:320
	v_pk_mul_f32 v[18:19], v[36:37], v[36:37]
	v_pk_fma_f32 v[42:43], v[48:49], v[66:67], v[22:23] op_sel_hi:[1,0,1] neg_lo:[0,0,1] neg_hi:[0,0,1]
	v_add_f32_e32 v18, v18, v20
	v_add_f32_e32 v20, v19, v18
	v_pk_mul_f32 v[18:19], v[28:29], v[68:69] op_sel_hi:[1,0]
	v_pk_mul_f32 v[22:23], v[42:43], v[42:43]
	v_pk_fma_f32 v[38:39], v[44:45], v[66:67], v[18:19] op_sel_hi:[1,0,1] neg_lo:[0,0,1] neg_hi:[0,0,1]
	s_nop 0
	v_pk_mul_f32 v[18:19], v[38:39], v[38:39]
	s_nop 0
	v_add_f32_e32 v18, v18, v20
	v_add_f32_e32 v20, v19, v18
	v_pk_mul_f32 v[18:19], v[30:31], v[68:69] op_sel_hi:[1,0]
	s_nop 0
	v_pk_fma_f32 v[40:41], v[46:47], v[66:67], v[18:19] op_sel_hi:[1,0,1] neg_lo:[0,0,1] neg_hi:[0,0,1]
	s_nop 0
	v_pk_mul_f32 v[18:19], v[40:41], v[40:41]
	s_nop 0
	v_add_f32_e32 v18, v18, v20
	v_add_f32_e32 v24, v19, v18
	v_add_f32_e32 v22, v22, v24
	v_add_f32_e32 v26, v23, v22
	ds_bpermute_b32 v27, v1, v26
	global_load_dwordx4 v[18:21], v69, s[12:13] offset:352
	global_load_dwordx4 v[22:25], v69, s[12:13] offset:448
	s_waitcnt lgkmcnt(0)
	v_add_f32_e32 v26, v26, v27
	v_fmamk_f32 v26, v26, 0x3c800000, v215
	v_mul_f32_e32 v27, 0x4b800000, v26
	v_cmp_gt_f32_e32 vcc, s41, v26
	s_nop 1
	v_cndmask_b32_e32 v30, v26, v27, vcc
	global_load_dwordx4 v[26:29], v69, s[12:13] offset:384
	v_rsq_f32_e32 v32, v30
	v_lshlrev_b64 v[30:31], 10, v[180:181]
	v_lshl_add_u64 v[44:45], s[16:17], 0, v[30:31]
	v_lshl_add_u64 v[44:45], v[44:45], 0, v[178:179]
	v_mul_f32_e32 v30, 0x45800000, v32
	v_cndmask_b32_e32 v30, v32, v30, vcc
	v_mul_f32_e32 v48, v213, v30
	global_load_dwordx4 v[30:33], v69, s[12:13] offset:416
	v_mul_f32_e32 v48, 0x41800000, v48
	s_waitcnt vmcnt(5)
	v_mul_f32_e32 v49, v50, v48
	v_mul_f32_e32 v10, v10, v49
	v_mul_f32_e32 v49, v51, v48
	v_mul_f32_e32 v11, v11, v49
	v_mul_f32_e32 v49, v52, v48
	v_med3_f32 v10, v10, s42, v216
	v_med3_f32 v11, v11, s42, v216
	v_mul_f32_e32 v12, v12, v49
	s_nop 0
	v_cvt_pk_fp8_f32 v49, v10, v11
	v_mul_f32_e32 v10, v53, v48
	v_mul_f32_e32 v10, v13, v10
	v_med3_f32 v12, v12, s42, v216
	v_med3_f32 v10, v10, s42, v216
	v_cvt_pk_fp8_f32 v49, v12, v10 op_sel:[0,0,1]
	v_mul_f32_e32 v10, v54, v48
	v_mul_f32_e32 v6, v6, v10
	v_mul_f32_e32 v10, v55, v48
	v_mul_f32_e32 v7, v7, v10
	v_mul_f32_e32 v10, v56, v48
	v_med3_f32 v6, v6, s42, v216
	v_med3_f32 v7, v7, s42, v216
	v_mul_f32_e32 v8, v8, v10
	s_nop 0
	v_cvt_pk_fp8_f32 v10, v6, v7
	v_mul_f32_e32 v6, v57, v48
	v_mul_f32_e32 v6, v9, v6
	v_med3_f32 v8, v8, s42, v216
	v_med3_f32 v6, v6, s42, v216
	v_cvt_pk_fp8_f32 v10, v8, v6 op_sel:[0,0,1]
	v_add_co_u32_e32 v6, vcc, s43, v44
	v_lshl_add_u64 v[46:47], v[44:45], 0, s[14:15]
	s_nop 0
	v_addc_co_u32_e32 v7, vcc, 0, v45, vcc
	global_store_dword v[6:7], v49, off offset:768
	global_store_dword v[46:47], v10, off offset:8
	v_mul_f32_e32 v6, v58, v48
	v_mul_f32_e32 v7, v59, v48
	s_waitcnt vmcnt(6)
	v_mul_f32_e32 v6, v14, v6
	v_mul_f32_e32 v7, v15, v7
	v_med3_f32 v6, v6, s42, v216
	v_med3_f32 v7, v7, s42, v216
	s_nop 0
	v_cvt_pk_fp8_f32 v9, v6, v7
	v_mul_f32_e32 v8, v60, v48
	v_mul_f32_e32 v6, v61, v48
	v_mul_f32_e32 v8, v16, v8
	v_mul_f32_e32 v6, v17, v6
	v_med3_f32 v8, v8, s42, v216
	v_med3_f32 v6, v6, s42, v216
	v_cvt_pk_fp8_f32 v9, v8, v6 op_sel:[0,0,1]
	v_mul_f32_e32 v6, v62, v48
	v_mul_f32_e32 v7, v63, v48
	s_nop 0
	v_mul_f32_e32 v8, v64, v48
	s_nop 0
	s_waitcnt vmcnt(5)
	v_mul_f32_e32 v6, v18, v6
	v_mul_f32_e32 v7, v19, v7
	v_med3_f32 v6, v6, s42, v216
	v_med3_f32 v7, v7, s42, v216
	v_cvt_pk_fp8_f32 v10, v6, v7
	v_mul_f32_e32 v6, v65, v48
	v_mul_f32_e32 v8, v20, v8
	v_mul_f32_e32 v6, v21, v6
	v_med3_f32 v8, v8, s42, v216
	v_med3_f32 v6, v6, s42, v216
	v_cvt_pk_fp8_f32 v10, v8, v6 op_sel:[0,0,1]
	v_mul_f32_e32 v6, v70, v48
	v_mul_f32_e32 v7, v71, v48
	s_waitcnt vmcnt(3)
	v_mul_f32_e32 v6, v26, v6
	v_mul_f32_e32 v7, v27, v7
	v_med3_f32 v6, v6, s42, v216
	v_med3_f32 v7, v7, s42, v216
	v_cvt_pk_fp8_f32 v11, v6, v7
	v_mul_f32_e32 v8, v72, v48
	v_mul_f32_e32 v6, v73, v48
	v_mul_f32_e32 v8, v28, v8
	v_mul_f32_e32 v6, v29, v6
	v_med3_f32 v8, v8, s42, v216
	v_med3_f32 v6, v6, s42, v216
	v_cvt_pk_fp8_f32 v11, v8, v6 op_sel:[0,0,1]
	v_mul_f32_e32 v6, v74, v48
	v_mul_f32_e32 v7, v75, v48
	s_waitcnt vmcnt(2)
	v_mul_f32_e32 v6, v30, v6
	v_mul_f32_e32 v7, v31, v7
	v_med3_f32 v6, v6, s42, v216
	v_med3_f32 v7, v7, s42, v216
	s_nop 0
	v_cvt_pk_fp8_f32 v12, v6, v7
	v_mul_f32_e32 v8, v34, v48
	v_mul_f32_e32 v6, v35, v48
	v_mul_f32_e32 v8, v32, v8
	v_mul_f32_e32 v6, v33, v6
	v_med3_f32 v8, v8, s42, v216
	v_med3_f32 v6, v6, s42, v216
	v_cvt_pk_fp8_f32 v12, v8, v6 op_sel:[0,0,1]
	v_mul_f32_e32 v6, v36, v48
	v_mul_f32_e32 v7, v37, v48
	v_mul_f32_e32 v6, v22, v6
	v_mul_f32_e32 v7, v23, v7
	global_store_dword v[46:47], v9, off offset:16
	global_store_dword v[46:47], v10, off offset:24
	global_store_dword v[46:47], v11, off offset:32
	global_store_dword v[46:47], v12, off offset:40
	v_med3_f32 v6, v6, s42, v216
	v_med3_f32 v7, v7, s42, v216
	s_nop 0
	v_cvt_pk_fp8_f32 v9, v6, v7
	v_mul_f32_e32 v8, v38, v48
	v_mul_f32_e32 v6, v39, v48
	v_mul_f32_e32 v8, v24, v8
	v_mul_f32_e32 v6, v25, v6
	v_med3_f32 v8, v8, s42, v216
	v_med3_f32 v6, v6, s42, v216
	v_cvt_pk_fp8_f32 v9, v8, v6 op_sel:[0,0,1]
	v_mul_f32_e32 v6, v40, v48
	v_mul_f32_e32 v2, v2, v6
	v_mul_f32_e32 v6, v41, v48
	v_mul_f32_e32 v3, v3, v6
	v_mul_f32_e32 v6, v42, v48
	v_med3_f32 v2, v2, s42, v216
	v_med3_f32 v3, v3, s42, v216
	v_mul_f32_e32 v4, v4, v6
	s_nop 0
	v_cvt_pk_fp8_f32 v6, v2, v3
	v_mul_f32_e32 v2, v43, v48
	v_mul_f32_e32 v2, v5, v2
	v_med3_f32 v4, v4, s42, v216
	v_med3_f32 v2, v2, s42, v216
	v_cvt_pk_fp8_f32 v6, v4, v2 op_sel:[0,0,1]
	global_store_dword v[46:47], v9, off offset:48
	global_store_dword v[46:47], v6, off offset:56
	s_cbranch_scc0 .LBB0_1885

; DI unsigned pk4_fp8(float a, float b, float c, float d) { int r = 0; r = __builtin_amdgcn_cvt_pk_fp8_f32(a, b, r, false); r = __builtin_amdgcn_cvt_pk_fp8_f32(c, d, r, true); return (unsigned)r; }
; DI float clamp448(float x) { return __builtin_amdgcn_fmed3f(x, -448.0f, 448.0f); }
; DI void attn_unit_a8(unsigned char* lds, const AttnArgs& a) {
;     ...
;     float lt0 = l0[0] + l0[1] + l0[2] + l0[3];
;     lt0 += __shfl_xor(lt0, 32);
;     unsigned char* op = a.out8 + (size_t)(wid * 32 + r) * 1024 + 4 * h;
;     const float rl = 16.0f * CAT_SCALE / lt0;
; #pragma unroll
;     for (int d = 0; d < 2; ++d)
; #pragma unroll
;         for (int g = 0; g < 4; ++g) *(unsigned*)(op + 32 * d + 8 * g) = pk4_fp8(clamp448(o0[d][4 * g] * rl), clamp448(o0[d][4 * g + 1] * rl), clamp448(o0[d][4 * g + 2] * rl), clamp448(o0[d][4 * g + 3] * rl));
; template <int li>
; DI void layer_phases(unsigned char* smem, LAS unsigned char* ldsL, const int lo, const int hi) {
;     ...
;               for (int it = 0; ; ++it) {
;                 int L = (int)blockIdx.x + it * G;
;                 if (G == 256 && it == 2) { const int j = (int)blockIdx.x - 32; if (j < 0 || j >= 32) break; L = 512 + j; }
;                 if (L >= (li == DEPTH - 1 ? 512 : 512 + 32)) break;
.LBB0_1913:
	v_add_f32_e32 v34, v108, v109
	v_add_f32_e32 v34, v110, v34
	v_add_f32_e32 v34, v111, v34
	ds_bpermute_b32 v35, v1, v34
	s_lshl_b64 s[10:11], s[40:41], 10
	s_add_u32 s8, s58, s10
	s_addc_u32 s11, s59, s11
	s_add_u32 s10, s8, s74
	s_addc_u32 s11, s11, 0
	s_waitcnt lgkmcnt(0)
	v_add_f32_e32 v36, v34, v35
	v_lshlrev_b64 v[34:35], 10, v[128:129]
	v_lshl_add_u64 v[34:35], s[10:11], 0, v[34:35]
	v_div_scale_f32 v37, s[10:11], v36, v36, s71
	v_rcp_f32_e32 v38, v37
	v_lshrrev_b32_e32 v39, 3, v167
	v_and_b32_e32 v106, 4, v39
	s_add_i32 s73, s73, 1
	v_fma_f32 v39, -v37, v38, 1.0
	v_fmac_f32_e32 v38, v39, v38
	v_div_scale_f32 v39, vcc, s71, v36, s71
	v_mul_f32_e32 v40, v39, v38
	v_fma_f32 v41, -v37, v40, v39
	v_fmac_f32_e32 v40, v41, v38
	v_fma_f32 v37, -v37, v40, v39
	v_div_fmas_f32 v37, v37, v38, v40
	v_div_fixup_f32 v36, v37, v36, s71
	v_mul_f32_e32 v18, v18, v36
	v_mul_f32_e32 v19, v19, v36
	v_med3_f32 v18, v18, s72, v166
	v_med3_f32 v19, v19, s72, v166
	s_nop 0
	v_cvt_pk_fp8_f32 v37, v18, v19
	v_mul_f32_e32 v20, v20, v36
	v_mul_f32_e32 v19, v21, v36
	v_med3_f32 v18, v20, s72, v166
	v_med3_f32 v19, v19, s72, v166
	v_cvt_pk_fp8_f32 v37, v18, v19 op_sel:[0,0,1]
	v_mul_f32_e32 v18, v22, v36
	v_mul_f32_e32 v19, v23, v36
	v_med3_f32 v18, v18, s72, v166
	v_med3_f32 v19, v19, s72, v166
	s_nop 0
	v_cvt_pk_fp8_f32 v21, v18, v19
	v_mul_f32_e32 v20, v24, v36
	v_mul_f32_e32 v19, v25, v36
	v_med3_f32 v18, v20, s72, v166
	v_med3_f32 v19, v19, s72, v166
	v_cvt_pk_fp8_f32 v21, v18, v19 op_sel:[0,0,1]
	v_mul_f32_e32 v18, v26, v36
	v_mul_f32_e32 v19, v27, v36
	v_med3_f32 v18, v18, s72, v166
	v_med3_f32 v19, v19, s72, v166
	s_nop 0
	v_cvt_pk_fp8_f32 v22, v18, v19
	v_mul_f32_e32 v20, v28, v36
	v_mul_f32_e32 v19, v29, v36
	v_med3_f32 v18, v20, s72, v166
	v_med3_f32 v19, v19, s72, v166
	v_cvt_pk_fp8_f32 v22, v18, v19 op_sel:[0,0,1]
	v_mul_f32_e32 v18, v30, v36
	v_mul_f32_e32 v19, v31, v36
	v_med3_f32 v18, v18, s72, v166
	v_med3_f32 v19, v19, s72, v166
	s_nop 0
	v_cvt_pk_fp8_f32 v23, v18, v19
	v_mul_f32_e32 v20, v32, v36
	v_mul_f32_e32 v19, v33, v36
	v_med3_f32 v18, v20, s72, v166
	v_med3_f32 v19, v19, s72, v166
	v_mul_f32_e32 v2, v2, v36
	v_mul_f32_e32 v3, v3, v36
	v_cvt_pk_fp8_f32 v23, v18, v19 op_sel:[0,0,1]
	v_med3_f32 v2, v2, s72, v166
	v_med3_f32 v3, v3, s72, v166
	s_nop 0
	v_cvt_pk_fp8_f32 v18, v2, v3
	v_mul_f32_e32 v4, v4, v36
	v_mul_f32_e32 v3, v5, v36
	v_med3_f32 v2, v4, s72, v166
	v_med3_f32 v3, v3, s72, v166
	v_cvt_pk_fp8_f32 v18, v2, v3 op_sel:[0,0,1]
	v_mul_f32_e32 v2, v6, v36
	v_mul_f32_e32 v3, v7, v36
	v_med3_f32 v2, v2, s72, v166
	v_med3_f32 v3, v3, s72, v166
	s_nop 0
	v_cvt_pk_fp8_f32 v5, v2, v3
	v_mul_f32_e32 v4, v8, v36
	v_mul_f32_e32 v3, v9, v36
	v_med3_f32 v2, v4, s72, v166
	v_med3_f32 v3, v3, s72, v166
	v_cvt_pk_fp8_f32 v5, v2, v3 op_sel:[0,0,1]
	v_mul_f32_e32 v2, v10, v36
	v_mul_f32_e32 v3, v11, v36
	v_med3_f32 v2, v2, s72, v166
	v_med3_f32 v3, v3, s72, v166
	s_nop 0
	v_cvt_pk_fp8_f32 v6, v2, v3
	s_cmp_eq_u32 s73, 2
	s_cselect_b64 s[10:11], -1, 0
	v_mul_f32_e32 v4, v12, v36
	v_mul_f32_e32 v3, v13, v36
	s_and_b64 s[10:11], s[46:47], s[10:11]
	v_med3_f32 v2, v4, s72, v166
	v_med3_f32 v3, v3, s72, v166
	s_and_b64 s[12:13], s[26:27], s[10:11]
	v_cvt_pk_fp8_f32 v6, v2, v3 op_sel:[0,0,1]
	v_mul_f32_e32 v2, v14, v36
	v_mul_f32_e32 v3, v15, v36
	s_mul_i32 s8, s73, s60
	s_and_b64 s[10:11], s[10:11], exec
	v_med3_f32 v2, v2, s72, v166
	v_med3_f32 v3, v3, s72, v166
	s_nop 0
	s_cselect_b32 s8, 0x1e0, s8
	v_cvt_pk_fp8_f32 v7, v2, v3
	s_add_i32 s76, s8, s2
	s_cmpk_gt_i32 s76, 0x1ff
	v_mul_f32_e32 v4, v16, v36
	v_mul_f32_e32 v3, v17, v36
	s_cselect_b64 s[10:11], -1, 0
	v_med3_f32 v2, v4, s72, v166
	v_med3_f32 v3, v3, s72, v166
	s_or_b64 s[10:11], s[12:13], s[10:11]
	v_lshl_add_u64 v[34:35], v[34:35], 0, v[106:107]
	v_cvt_pk_fp8_f32 v7, v2, v3 op_sel:[0,0,1]
	s_and_b64 vcc, exec, s[10:11]
	global_store_dword v[34:35], v37, off
	global_store_dword v[34:35], v21, off offset:8
	global_store_dword v[34:35], v22, off offset:16
	global_store_dword v[34:35], v23, off offset:24
	global_store_dword v[34:35], v18, off offset:32
	global_store_dword v[34:35], v5, off offset:40
	global_store_dword v[34:35], v6, off offset:48
	global_store_dword v[34:35], v7, off offset:56
	s_cbranch_vccnz .LBB0_1938

; DI void attn_unit_a8(unsigned char* lds, const AttnArgs& a) {
;     ...
;     { const bf16_t* qp = a.q + (size_t)(wid * 32 + r) * 256 + 32 * h;
;       const u32x4 q0 = *(const u32x4*)qp, q1 = *(const u32x4*)(qp + 8), q2 = *(const u32x4*)(qp + 16), q3 = *(const u32x4*)(qp + 24);
;       const u32x2 c0 = bf8_to_fp8(q0), c1 = bf8_to_fp8(q1), c2 = bf8_to_fp8(q2), c3 = bf8_to_fp8(q3);
;       qf8 = (v8i){(int)c0.x, (int)c0.y, (int)c1.x, (int)c1.y, (int)c2.x, (int)c2.y, (int)c3.x, (int)c3.y}; }
;     const int lrow = tid >> 3, lch = tid & 7;
;     const unsigned char* vsrc = a.vt8 + (size_t)lrow * KEYS + 8 * lch;
;     const int ldk = lrow * A8_PITCH + 8 * lch;
;     const int ldv = A8_VOFF + lrow * A8_PITCH + (lch >> 2) * 16 + (lch & 3) * 4;
;     const int koff = r * A8_PITCH + 32 * h, voff = A8_VOFF + r * A8_PITCH + 32 * h;
;     f32x16 o0[2]; o0[0] = (f32x16){}; o0[1] = (f32x16){};
;     f32x4 l0 = {0.f, 0.f, 0.f, 0.f};
;     u32x2 kregA, vregA, kregB, vregB;
;     auto gload = [&](int t, u32x2& kreg, u32x2& vreg) __attribute__((always_inline)) {
;         const unsigned char* kp = (t < 64) ? a.klat8 + (size_t)(t * 64 + lrow) * 128 : a.kctx8 + (size_t)((t - 64) * 64 + lrow) * 128;
;         kreg = *(const u32x2*)(kp + 8 * lch);
;         vreg = *(const u32x2*)(vsrc + (size_t)t * 64);
;     };
;     auto lstore = [&](int slot, const u32x2& kreg, const u32x2& vreg) __attribute__((always_inline)) { unsigned char* b = lds + slot * AT_BUFB;
;         *(u32x2*)(b + ldk) = kreg; *(unsigned*)(b + ldv) = vreg.x; *(unsigned*)(b + ldv + 32) = vreg.y; };
;     auto rd32 = [&](const unsigned char* p) __attribute__((always_inline)) -> v8i { const u32x4 lo = *(const u32x4*)p, hi = *(const u32x4*)(p + 16);
;         return (v8i){(int)lo.x, (int)lo.y, (int)lo.z, (int)lo.w, (int)hi.x, (int)hi.y, (int)hi.z, (int)hi.w}; };
;     auto kread = [&](const unsigned char* Kb, int hh) __attribute__((always_inline)) -> v8i { return rd32(Kb + koff + hh * 32 * A8_PITCH); };
;     auto vread = [&](const unsigned char* Vb, int dblk) __attribute__((always_inline)) -> v8i { return rd32(Vb + voff + dblk * 32 * A8_PITCH); };
;     const f32x16 cinit = (f32x16){};
;     ...
;     const int wcol = tid >> 1, whalf = tid & 1;
;     const unsigned wper_gu = (unsigned)((wcol >> 7) * 256 + (wcol & 96) + invperm32(wcol & 31)) * 1024u + 16u * whalf;
.LBB0_1920:
	s_lshl_b32 s8, s20, 5
	s_and_b32 s77, s8, 64
	s_lshl_b32 s80, s75, 7
	s_ashr_i32 s11, s10, 31
	s_or_b32 s8, s77, s80
	s_lshl_b32 s74, s20, 6
	s_lshl_b64 s[52:53], s[10:11], 7
	s_mul_hi_i32 s11, s8, 0x1100
	s_mulk_i32 s8, 0x1100
	s_add_u32 s10, s56, s8
	s_addc_u32 s11, s57, s11
	s_add_u32 s8, s54, s52
	s_addc_u32 s12, s55, s53
	v_ashrrev_i32_e32 v130, 3, v167
	v_and_b32_e32 v23, 7, v167
	v_mov_b64_e32 v[18:19], s[10:11]
	s_add_u32 s42, s8, s77
	v_ashrrev_i32_e32 v131, 31, v130
	v_mad_i64_i32 v[18:19], s[10:11], v130, s4, v[18:19]
	v_lshlrev_b32_e32 v132, 3, v23
	v_mov_b32_e32 v133, v107
	s_addc_u32 s43, s12, 0
	v_lshl_add_u64 v[134:135], v[18:19], 0, v[132:133]
	v_lshlrev_b64 v[18:19], 7, v[130:131]
	v_lshl_add_u64 v[24:25], s[42:43], 0, v[18:19]
	v_lshl_add_u64 v[24:25], v[24:25], 0, v[132:133]
	v_add_co_u32_e32 v28, vcc, s61, v24
	global_load_dwordx2 v[26:27], v[24:25], off
	s_nop 0
	v_addc_co_u32_e32 v29, vcc, 0, v25, vcc
	global_load_dwordx2 v[30:31], v[134:135], off
	s_nop 0
	global_load_dwordx2 v[28:29], v[28:29], off
	s_nop 0
	global_load_dwordx2 v[32:33], v[134:135], off offset:64
	s_waitcnt vmcnt(4)
	v_lshlrev_b32_e32 v34, 16, v14
	v_and_b32_e32 v14, 0xffff0000, v14
	s_nop 0
	v_cvt_pk_fp8_f32 v98, v34, v14
	v_lshlrev_b32_e32 v34, 16, v16
	v_and_b32_e32 v16, 0xffff0000, v16
	s_nop 0
	v_cvt_pk_fp8_f32 v99, v34, v16
	v_lshlrev_b32_e32 v14, 16, v15
	v_and_b32_e32 v15, 0xffff0000, v15
	v_cvt_pk_fp8_f32 v98, v14, v15 op_sel:[0,0,1]
	v_lshlrev_b32_e32 v14, 16, v17
	v_and_b32_e32 v15, 0xffff0000, v17
	v_cvt_pk_fp8_f32 v99, v14, v15 op_sel:[0,0,1]
	v_lshlrev_b32_e32 v14, 16, v10
	v_and_b32_e32 v10, 0xffff0000, v10
	s_nop 0
	v_cvt_pk_fp8_f32 v100, v14, v10
	v_lshlrev_b32_e32 v14, 16, v12
	v_and_b32_e32 v12, 0xffff0000, v12
	s_nop 0
	v_cvt_pk_fp8_f32 v101, v14, v12
	v_lshlrev_b32_e32 v10, 16, v11
	v_and_b32_e32 v11, 0xffff0000, v11
	v_cvt_pk_fp8_f32 v100, v10, v11 op_sel:[0,0,1]
	v_lshlrev_b32_e32 v10, 16, v13
	v_and_b32_e32 v11, 0xffff0000, v13
	v_cvt_pk_fp8_f32 v101, v10, v11 op_sel:[0,0,1]
	v_lshlrev_b32_e32 v10, 16, v6
	v_and_b32_e32 v6, 0xffff0000, v6
	s_nop 0
	v_cvt_pk_fp8_f32 v102, v10, v6
	v_lshlrev_b32_e32 v10, 16, v8
	v_and_b32_e32 v8, 0xffff0000, v8
	s_nop 0
	v_cvt_pk_fp8_f32 v103, v10, v8
	v_lshlrev_b32_e32 v6, 16, v7
	v_and_b32_e32 v7, 0xffff0000, v7
	v_cvt_pk_fp8_f32 v102, v6, v7 op_sel:[0,0,1]
	v_lshlrev_b32_e32 v6, 16, v9
	v_and_b32_e32 v7, 0xffff0000, v9
	v_cvt_pk_fp8_f32 v103, v6, v7 op_sel:[0,0,1]
	v_lshlrev_b32_e32 v6, 16, v2
	v_and_b32_e32 v2, 0xffff0000, v2
	s_nop 0
	v_cvt_pk_fp8_f32 v104, v6, v2
	v_lshlrev_b32_e32 v6, 16, v4
	v_and_b32_e32 v4, 0xffff0000, v4
	s_nop 0
	v_cvt_pk_fp8_f32 v105, v6, v4
	v_lshlrev_b32_e32 v2, 16, v3
	v_and_b32_e32 v3, 0xffff0000, v3
	v_cvt_pk_fp8_f32 v104, v2, v3 op_sel:[0,0,1]
	v_lshlrev_b32_e32 v2, 16, v5
	v_and_b32_e32 v3, 0xffff0000, v5
	v_cvt_pk_fp8_f32 v105, v2, v3 op_sel:[0,0,1]
	v_lshlrev_b32_e32 v3, 2, v23
	v_mul_lo_u32 v2, v130, s5
	v_and_b32_e32 v4, 16, v3
	v_add_u32_e32 v131, v2, v132
	v_add_u32_e32 v2, v2, v4
	v_and_or_b32 v168, v3, 12, v2
	v_add_u32_e32 v2, 0, v168
	v_add_u32_e32 v5, 0, v131
	v_add_u32_e32 v3, 0x1400, v2
	v_add_u32_e32 v2, 0x5800, v2
	s_waitcnt vmcnt(3)
	ds_write_b64 v5, v[26:27]
	s_waitcnt vmcnt(2)
	ds_write2_b32 v3, v30, v31 offset1:8
	s_waitcnt vmcnt(1)
	ds_write_b64 v5, v[28:29] offset:18048
	s_waitcnt vmcnt(0)
	ds_write2_b32 v2, v32, v33 offset0:160 offset1:168
	v_add_co_u32_e32 v2, vcc, s64, v24
	s_waitcnt lgkmcnt(0)
	s_nop 0
	v_addc_co_u32_e32 v3, vcc, 0, v25, vcc
	s_barrier
	global_load_dwordx2 v[136:137], v[2:3], off
	global_load_dwordx2 v[138:139], v[134:135], off offset:128
	v_mul_u32_u24_e32 v2, 0x50, v21
	v_add3_u32 v169, v2, v22, 0
	ds_read_b128 v[2:5], v169
	ds_read_b128 v[6:9], v169 offset:16
	s_waitcnt lgkmcnt(0)
	v_mfma_f32_32x32x64_f8f6f4 v[34:49], v[2:9], v[98:105], 0
	ds_read_b128 v[2:5], v169 offset:2560
	ds_read_b128 v[6:9], v169 offset:2576
	s_andn2_b64 vcc, exec, s[50:51]
	s_waitcnt lgkmcnt(0)
	v_mfma_f32_32x32x64_f8f6f4 v[50:65], v[2:9], v[98:105], 0
	s_cbranch_vccnz .LBB0_1932
	v_ashrrev_i32_e32 v5, 1, v167
	v_lshlrev_b32_e32 v6, 2, v5
	v_and_b32_e32 v170, 16, v6
	v_lshrrev_b32_e32 v6, 1, v5
	v_and_b32_e32 v4, 0x3fff00, v167
	v_and_b32_e32 v7, 12, v6
	v_and_b32_e32 v8, 0x63, v5
	v_or3_b32 v171, v8, v4, v7
	v_lshlrev_b32_e32 v4, 4, v167
	v_and_b32_e32 v172, 16, v4
	v_lshlrev_b32_e32 v4, 4, v5
	v_lshrrev_b32_e32 v7, 2, v5
	v_and_b32_e32 v8, 0x3fff03, v5
	v_and_b32_e32 v6, 0x60, v6
	v_and_b32_e32 v7, 12, v7
	v_and_or_b32 v4, v4, s65, v8
	v_or3_b32 v173, v4, v6, v7
	s_lshl_b32 s20, s79, 2
	s_and_b32 s21, s78, 0x300
	s_and_b32 s22, s78, 0x700
	v_mov_b32_e32 v4, v107
	v_mad_i64_i32 v[2:3], s[10:11], v130, s4, 0
	v_mad_u64_u32 v[4:5], s[10:11], v5, 36, v[4:5]
	s_add_u32 s8, s24, s77
	s_addc_u32 s11, s25, 0
	s_add_u32 s10, s8, s52
	s_addc_u32 s11, s11, s53
	s_add_i32 s8, s80, s77
	v_lshl_add_u64 v[140:141], s[10:11], 0, v[18:19]
	s_mul_hi_i32 s11, s8, 0x1100
	s_mulk_i32 s8, 0x1100
	s_add_u32 s10, s24, s8
	v_mad_u32_u24 v6, v20, 36, 0
	s_addc_u32 s11, s25, s11
	v_mov_b32_e32 v18, 0
	v_lshl_add_u64 v[142:143], s[10:11], 0, v[2:3]
	s_mov_b32 s23, 0
	v_add_u32_e32 v174, s20, v6
	v_lshlrev_b32_e32 v106, 2, v20
	v_add_u32_e32 v175, v4, v172
	s_mov_b32 s50, 0
	s_mov_b32 s18, 0
	v_mov_b32_e32 v19, v18
	v_mov_b32_e32 v20, v18
	v_mov_b32_e32 v21, v18
	v_mov_b32_e32 v22, v18
	v_mov_b32_e32 v23, v18
	v_mov_b32_e32 v24, v18
	v_mov_b32_e32 v25, v18
	v_mov_b32_e32 v26, v18
	v_mov_b32_e32 v27, v18
	v_mov_b32_e32 v28, v18
	v_mov_b32_e32 v29, v18
	v_mov_b32_e32 v30, v18
	v_mov_b32_e32 v31, v18
	v_mov_b32_e32 v32, v18
	v_mov_b32_e32 v33, v18
	v_mov_b32_e32 v2, v18
	v_mov_b32_e32 v3, v18
	v_mov_b32_e32 v4, v18
	v_mov_b32_e32 v5, v18
	v_mov_b32_e32 v6, v18
	v_mov_b32_e32 v7, v18
	v_mov_b32_e32 v8, v18
	v_mov_b32_e32 v9, v18
	v_mov_b32_e32 v10, v18
	v_mov_b32_e32 v11, v18
	v_mov_b32_e32 v12, v18
	v_mov_b32_e32 v13, v18
	v_mov_b32_e32 v14, v18
	v_mov_b32_e32 v15, v18
	v_mov_b32_e32 v16, v18
	v_mov_b32_e32 v17, v18
	v_mov_b32_e32 v108, v18
	v_mov_b32_e32 v109, v18
	v_mov_b32_e32 v110, v18
	v_mov_b32_e32 v111, v18
	s_branch .LBB0_1923
; DI void attn_unit_a8(unsigned char* lds, const AttnArgs& a) {
;     ...
;     auto w_decode = [&](int j, const float*& src, unsigned char*& dst, int& ld, int& n0, int& k0, bool& gu) __attribute__((always_inline)) {
;         const int g = (j >> 2) * 512 + a.wl, e = g / 96, rr = g - e * 96; KParamsPtr kp = kparams();
;         if (rr < 64) { src = kp->w_gu + ((size_t)a.wli * NE + e) * (1024 * 2048); dst = kp->ws + WS_WGU + (size_t)a.wli * SZ_WGU + (size_t)e * 2048 * 1024; ld = 2048; n0 = (rr & 7) * 256; k0 = ((rr >> 3) * 4 + (j & 3)) * 32; gu = true; }
;         else { const int q = rr - 64; src = kp->w_dn + ((size_t)a.wli * NE + e) * (1024 * 1024); dst = kp->ws + WS_WDN + (size_t)a.wli * SZ_WDN + (size_t)e * 1024 * 1024; ld = 1024; n0 = (q & 3) * 256; k0 = ((q >> 2) * 4 + (j & 3)) * 32; gu = false; } };
;     auto w_issue = [&](int j) __attribute__((always_inline)) { const float* src; unsigned char* dst; int ld, n0, k0; bool gu; w_decode(j, src, dst, ld, n0, k0, gu);
;         const float* p = src + (size_t)(k0 + 4 * wid) * ld + n0 + wn4;
;         wq[0] = __builtin_nontemporal_load((const f32x4*)p); wq[1] = __builtin_nontemporal_load((const f32x4*)(p + ld));
;         wq[2] = __builtin_nontemporal_load((const f32x4*)(p + (size_t)2 * ld)); wq[3] = __builtin_nontemporal_load((const f32x4*)(p + (size_t)3 * ld)); };
;     ...
;     auto step = [&](int t, u32x2& kl, u32x2& vl, const u32x2& ks, const u32x2& vs, f32x16& c0, f32x16& c1, f32x16& n0, f32x16& n1, const int hk, const int wj) __attribute__((always_inline)) {
;         const int slot1 = slot == 2 ? 0 : slot + 1, slot2 = slot1 == 2 ? 0 : slot1 + 1;
;         if (hk == 1) { w_cvt(); w_issue(wj + 1 < AT_NWT ? wj + 1 : AT_NWT - 1); }
;         if (hk == 2) w_store(wj);
;         { const int tn = t + 3; gload(tn < a.t1 ? tn : a.t1 - 1, kl, vl); }
;         const unsigned char* Kb = lds + slot * AT_BUFB; const unsigned char* Kn = lds + slot1 * AT_BUFB;
;         const v8i k0 = kread(Kn, 0), k1 = kread(Kn, 1), v0 = vread(Kb, 0), v1 = vread(Kb, 1);
;         n0 = mfma8(k0, qf8, cinit); n1 = mfma8(k1, qf8, cinit);
;         expsum(c0); expsum(c1);
;         const v8i P = pack8(c0, c1);
;         o0[0] = mfma8(v0, P, o0[0]); o0[1] = mfma8(v1, P, o0[1]);
;         lstore(slot2, ks, vs);
;         __syncthreads();
;         slot = slot1;
;     };
.LBB0_1922:
	s_lshl_b32 s8, s18, 1
	s_waitcnt lgkmcnt(0)
	s_lshr_b32 s16, s18, 3
	s_and_b32 s8, s8, 0x600
	s_and_b32 s16, s16, 0x80
	s_or_b32 s8, s8, s16
	s_and_b64 s[14:15], s[14:15], exec
	v_pk_add_f32 v[54:55], v[164:165], v[108:109]
	s_cselect_b32 s8, s8, s18
	s_and_b32 s14, s50, 3
	v_pk_add_f32 v[54:55], v[154:155], v[54:55]
	s_add_i32 s14, s52, s14
	v_pk_add_f32 v[54:55], v[158:159], v[54:55]
	s_lshl_b32 s14, s14, 5
	s_lshl_b32 s8, s8, 10
	v_pk_add_f32 v[56:57], v[160:161], v[110:111]
	v_pk_add_f32 v[46:47], v[46:47], v[54:55]
	s_add_i32 s14, s8, s14
	s_add_i32 s51, s51, 1
	v_pk_add_f32 v[56:57], v[162:163], v[56:57]
	v_pk_add_f32 v[46:47], v[50:51], v[46:47]
	s_and_b64 s[12:13], s[12:13], exec
	v_pk_add_f32 v[56:57], v[152:153], v[56:57]
	v_pk_add_f32 v[40:41], v[40:41], v[46:47]
	s_cselect_b32 s18, 0, s51
	v_pk_add_f32 v[56:57], v[156:157], v[56:57]
	v_pk_add_f32 v[50:51], v[42:43], v[40:41]
	s_mul_i32 s8, s18, 0x4680
	v_pk_add_f32 v[44:45], v[44:45], v[56:57]
	v_add_u32_e32 v58, s8, v169
	v_pk_add_f32 v[110:111], v[34:35], v[50:51]
	v_add_u32_e32 v34, 0xd800, v175
	v_pk_add_f32 v[48:49], v[48:49], v[44:45]
	ds_read_b128 v[40:43], v58
	ds_read_b128 v[44:47], v58 offset:16
	v_add_u32_e32 v35, 0xd808, v175
	ds_read2_b32 v[54:55], v34 offset1:1
	ds_read2_b32 v[56:57], v35 offset1:1
	v_add_u32_e32 v50, v52, v170
	v_lshl_or_b32 v50, v50, 10, v172
	v_add_u32_e32 v50, s14, v50
	v_exp_f32_e32 v82, v82
	s_waitcnt lgkmcnt(0)
	global_store_dwordx4 v50, v[54:57], s[10:11]
	ds_read_b128 v[50:53], v58 offset:2560
	ds_read_b128 v[54:57], v58 offset:2576
	v_add_co_u32_e32 v58, vcc, s70, v148
	v_exp_f32_e32 v83, v83
	s_nop 0
	v_addc_co_u32_e32 v59, vcc, 0, v149, vcc
	global_load_dwordx2 v[136:137], v[58:59], off
	global_load_dwordx2 v[138:139], v[150:151], off offset:256
	v_exp_f32_e32 v86, v86
	v_exp_f32_e32 v87, v87
	v_exp_f32_e32 v90, v90
	v_exp_f32_e32 v91, v91
	v_exp_f32_e32 v94, v94
	v_exp_f32_e32 v95, v95
	v_exp_f32_e32 v164, v66
	v_exp_f32_e32 v165, v67
	v_exp_f32_e32 v178, v70
	v_exp_f32_e32 v179, v71
	v_exp_f32_e32 v74, v74
	v_exp_f32_e32 v75, v75
	v_exp_f32_e32 v78, v78
	v_exp_f32_e32 v79, v79
	ds_read_b128 v[148:151], v176 offset:5120
	ds_read_b128 v[152:155], v176 offset:5136
	ds_read_b128 v[156:159], v176 offset:7680
	ds_read_b128 v[160:163], v176 offset:7696
	v_exp_f32_e32 v84, v84
	v_exp_f32_e32 v85, v85
	v_exp_f32_e32 v88, v88
	v_exp_f32_e32 v89, v89
	v_exp_f32_e32 v92, v92
	v_exp_f32_e32 v93, v93
	v_exp_f32_e32 v96, v96
	v_exp_f32_e32 v97, v97
	v_exp_f32_e32 v176, v68
	v_exp_f32_e32 v177, v69
	v_exp_f32_e32 v180, v72
	v_exp_f32_e32 v181, v73
	v_exp_f32_e32 v76, v76
	v_exp_f32_e32 v77, v77
	v_exp_f32_e32 v80, v80
	v_exp_f32_e32 v81, v81
	s_nop 0
	s_nop 0
	s_nop 0
	s_nop 0
	s_nop 0
	s_nop 0
	s_nop 0
	s_nop 0
	v_cvt_scalef32_pk_fp8_f32 v66, v82, v83, s69
	v_cvt_scalef32_pk_fp8_f32 v70, v164, v165, s69
	v_cvt_scalef32_pk_fp8_f32 v67, v86, v87, s69
	v_cvt_scalef32_pk_fp8_f32 v71, v178, v179, s69
	v_cvt_scalef32_pk_fp8_f32 v68, v90, v91, s69
	v_cvt_scalef32_pk_fp8_f32 v72, v74, v75, s69
	v_cvt_scalef32_pk_fp8_f32 v69, v94, v95, s69
	v_cvt_scalef32_pk_fp8_f32 v73, v78, v79, s69
	v_pk_add_f32 v[36:37], v[36:37], v[48:49]
	v_cvt_scalef32_pk_fp8_f32 v66, v84, v85, s69 op_sel:[0,0,0,1]
	v_cvt_scalef32_pk_fp8_f32 v70, v176, v177, s69 op_sel:[0,0,0,1]
	v_cvt_scalef32_pk_fp8_f32 v67, v88, v89, s69 op_sel:[0,0,0,1]
	v_cvt_scalef32_pk_fp8_f32 v71, v180, v181, s69 op_sel:[0,0,0,1]
	v_cvt_scalef32_pk_fp8_f32 v68, v92, v93, s69 op_sel:[0,0,0,1]
	v_cvt_scalef32_pk_fp8_f32 v72, v76, v77, s69 op_sel:[0,0,0,1]
	v_cvt_scalef32_pk_fp8_f32 v69, v96, v97, s69 op_sel:[0,0,0,1]
	v_cvt_scalef32_pk_fp8_f32 v73, v80, v81, s69 op_sel:[0,0,0,1]
	v_pk_add_f32 v[108:109], v[38:39], v[36:37]
	v_mfma_f32_32x32x64_f8f6f4 v[34:49], v[40:47], v[98:105], 0
	v_add_f32_e64 v110, v110, v82
	v_add_f32_e64 v111, v111, v83
	v_add_f32_e64 v82, v108, v84
	v_add_f32_e64 v83, v109, v85
	v_add_f32_e64 v84, v86, v110
	v_add_f32_e64 v85, v87, v111
	v_add_f32_e64 v82, v88, v82
	v_add_f32_e64 v83, v89, v83
	s_addk_i32 s8, 0x4680
	v_add_f32_e64 v84, v90, v84
	v_add_f32_e64 v85, v91, v85
	v_add_f32_e64 v82, v92, v82
	v_add_f32_e64 v83, v93, v83
	s_cmp_lg_u32 s18, 2
	v_pk_add_f32 v[82:83], v[96:97], v[82:83]
	v_pk_add_f32 v[84:85], v[94:95], v[84:85]
	s_cselect_b32 s8, s8, 0
	v_pk_add_f32 v[84:85], v[164:165], v[84:85]
	v_pk_add_f32 v[82:83], v[176:177], v[82:83]
	s_add_i32 s8, s8, 0
	v_pk_add_f32 v[82:83], v[180:181], v[82:83]
	s_waitcnt lgkmcnt(4)
	v_mfma_f32_32x32x64_f8f6f4 v[50:65], v[50:57], v[98:105], 0
	v_add_f32_e64 v84, v178, v84
	v_add_f32_e64 v85, v179, v85
	v_add_f32_e64 v76, v76, v82
	v_add_f32_e64 v77, v77, v83
	v_add_f32_e64 v74, v74, v84
	v_add_f32_e64 v75, v75, v85
	s_add_i32 s50, s50, 1
	s_addk_i32 s23, 0x80
	v_add_f32_e64 v110, v80, v76
	v_add_f32_e64 v111, v81, v77
	v_add_f32_e64 v108, v78, v74
	v_add_f32_e64 v109, v79, v75
	v_lshl_add_u64 v[140:141], v[140:141], 0, s[36:37]
	s_cmp_lg_u32 s50, 24
	v_lshl_add_u64 v[142:143], v[142:143], 0, s[38:39]
	s_waitcnt lgkmcnt(2)
	v_mfma_f32_32x32x64_f8f6f4 v[18:33], v[148:155], v[66:73], v[18:33]
	s_waitcnt lgkmcnt(0)
	v_mfma_f32_32x32x64_f8f6f4 v[2:17], v[156:163], v[66:73], v[2:17]
	v_add_u32_e32 v66, s8, v131
	s_waitcnt vmcnt(4)
	ds_write_b64 v66, v[144:145]
	v_add_u32_e32 v66, s8, v168
	v_add_u32_e32 v66, 0x1400, v66
	s_waitcnt vmcnt(3)
	ds_write2_b32 v66, v146, v147 offset1:8
	s_waitcnt lgkmcnt(0)
	s_barrier
	s_cbranch_scc0 .LBB0_1931
.LBB0_1923:
	s_min_u32 s19, s50, 22
	s_add_i32 s19, s19, 1
	s_lshl_b32 s8, s19, 7
	s_and_b32 s8, s8, 0x1e00
	s_nop 0
	s_nop 0
	s_add_i32 s10, s8, s76
	v_cvt_scalef32_pk_fp8_f32 v66, v116, v112, s66
	v_cvt_scalef32_pk_fp8_f32 v67, v117, v113, s66
	s_mul_hi_u32 s8, s10, 0xaaaaaaab
	v_cvt_scalef32_pk_fp8_f32 v66, v120, v124, s66 op_sel:[0,0,0,1]
	v_cvt_scalef32_pk_fp8_f32 v67, v121, v125, s66 op_sel:[0,0,0,1]
	v_add_u32_e32 v68, 0xd800, v174
	s_lshr_b32 s8, s8, 6
	ds_write2_b32 v68, v66, v67 offset1:9
	s_nop 0
	s_nop 0
	s_mul_i32 s52, s8, 0xffffffa0
	v_cvt_scalef32_pk_fp8_f32 v66, v118, v114, s66
	v_cvt_scalef32_pk_fp8_f32 v67, v119, v115, s66
	s_add_i32 s52, s52, s10
	v_cvt_scalef32_pk_fp8_f32 v66, v122, v126, s66 op_sel:[0,0,0,1]
	v_cvt_scalef32_pk_fp8_f32 v67, v123, v127, s66 op_sel:[0,0,0,1]
	s_mov_b64 s[14:15], s[0:1]
	s_cmp_gt_i32 s52, 63
	s_mov_b64 s[16:17], -1
	ds_write2_b32 v68, v66, v67 offset0:18 offset1:27
	s_cbranch_scc0 .LBB0_1925
	s_load_dwordx2 s[10:11], s[14:15], 0xc0
	s_lshl_b64 s[12:13], s[8:9], 22
	s_mov_b64 s[16:17], 0
	s_waitcnt lgkmcnt(0)
	s_add_u32 s10, s10, s12
	s_addc_u32 s11, s11, s13
	s_add_u32 s10, s10, 0x8000000
	s_addc_u32 s11, s11, 0
	s_and_b32 s12, s52, 0x7ffffffc
	s_sub_i32 s51, s12, 64

; DI void attn_unit_a8(unsigned char* lds, const AttnArgs& a) {
;     ...
;     auto w_decode = [&](int j, const float*& src, unsigned char*& dst, int& ld, int& n0, int& k0, bool& gu) __attribute__((always_inline)) {
;         const int g = (j >> 2) * 512 + a.wl, e = g / 96, rr = g - e * 96; KParamsPtr kp = kparams();
;         if (rr < 64) { src = kp->w_gu + ((size_t)a.wli * NE + e) * (1024 * 2048); dst = kp->ws + WS_WGU + (size_t)a.wli * SZ_WGU + (size_t)e * 2048 * 1024; ld = 2048; n0 = (rr & 7) * 256; k0 = ((rr >> 3) * 4 + (j & 3)) * 32; gu = true; }
;         else { const int q = rr - 64; src = kp->w_dn + ((size_t)a.wli * NE + e) * (1024 * 1024); dst = kp->ws + WS_WDN + (size_t)a.wli * SZ_WDN + (size_t)e * 1024 * 1024; ld = 1024; n0 = (q & 3) * 256; k0 = ((q >> 2) * 4 + (j & 3)) * 32; gu = false; } };
;     auto w_issue = [&](int j) __attribute__((always_inline)) { const float* src; unsigned char* dst; int ld, n0, k0; bool gu; w_decode(j, src, dst, ld, n0, k0, gu);
;         const float* p = src + (size_t)(k0 + 4 * wid) * ld + n0 + wn4;
;         wq[0] = __builtin_nontemporal_load((const f32x4*)p); wq[1] = __builtin_nontemporal_load((const f32x4*)(p + ld));
;         wq[2] = __builtin_nontemporal_load((const f32x4*)(p + (size_t)2 * ld)); wq[3] = __builtin_nontemporal_load((const f32x4*)(p + (size_t)3 * ld)); };
;     ...
;     auto step = [&](int t, u32x2& kl, u32x2& vl, const u32x2& ks, const u32x2& vs, f32x16& c0, f32x16& c1, f32x16& n0, f32x16& n1, const int hk, const int wj) __attribute__((always_inline)) {
;         const int slot1 = slot == 2 ? 0 : slot + 1, slot2 = slot1 == 2 ? 0 : slot1 + 1;
;         if (hk == 1) { w_cvt(); w_issue(wj + 1 < AT_NWT ? wj + 1 : AT_NWT - 1); }
;         if (hk == 2) w_store(wj);
;         { const int tn = t + 3; gload(tn < a.t1 ? tn : a.t1 - 1, kl, vl); }
;         const unsigned char* Kb = lds + slot * AT_BUFB; const unsigned char* Kn = lds + slot1 * AT_BUFB;
;         const v8i k0 = kread(Kn, 0), k1 = kread(Kn, 1), v0 = vread(Kb, 0), v1 = vread(Kb, 1);
;         n0 = mfma8(k0, qf8, cinit); n1 = mfma8(k1, qf8, cinit);
;         expsum(c0); expsum(c1);
;         const v8i P = pack8(c0, c1);
;         o0[0] = mfma8(v0, P, o0[0]); o0[1] = mfma8(v1, P, o0[1]);
;         lstore(slot2, ks, vs);
;         __syncthreads();
;         slot = slot1;
;     };
.LBB0_1927:
	s_and_b32 s8, s19, 3
	s_add_i32 s8, s51, s8
	s_lshl_b32 s8, s8, 5
	s_add_i32 s8, s8, s20
	s_mul_hi_i32 s15, s12, s8
	s_mul_i32 s14, s12, s8
	s_lshl_b64 s[14:15], s[14:15], 2
	s_add_u32 s8, s10, s14
	s_addc_u32 s11, s11, s15
	s_lshl_b32 s10, s13, 2
	s_add_u32 s10, s8, s10
	s_addc_u32 s11, s11, 0
	s_lshl_b32 s8, s12, 2
	s_add_i32 s12, s18, 1
	s_cmp_lg_u32 s18, 2
	s_cselect_b32 s51, s12, 0
	s_mul_i32 s12, s51, 0x4680
	v_add_u32_e32 v176, s12, v169
	ds_read_b128 v[66:69], v176
	ds_read_b128 v[70:73], v176 offset:16
	v_lshl_add_u64 v[74:75], s[10:11], 0, v[106:107]
	v_lshl_add_u64 v[74:75], v[74:75], 0, s[8:9]
	v_lshl_add_u64 v[148:149], v[140:141], 0, v[132:133]
	global_load_dwordx4 v[116:119], v106, s[10:11] nt
	global_load_dwordx4 v[112:115], v[74:75], off nt
	v_lshl_add_u64 v[74:75], v[74:75], 0, s[8:9]
	s_waitcnt lgkmcnt(0)
	v_mfma_f32_32x32x64_f8f6f4 v[82:97], v[66:73], v[98:105], 0
	v_add_co_u32_e32 v66, vcc, s67, v148
	v_lshl_add_u64 v[76:77], v[74:75], 0, s[8:9]
	global_load_dwordx4 v[120:123], v[74:75], off nt
	global_load_dwordx4 v[124:127], v[76:77], off nt
	v_addc_co_u32_e32 v67, vcc, 0, v149, vcc
	v_lshl_add_u64 v[74:75], v[142:143], 0, v[132:133]
	v_add_co_u32_e32 v150, vcc, s68, v74
	s_mul_i32 s8, s18, 0x4680
	s_nop 0
	v_addc_co_u32_e32 v151, vcc, 0, v75, vcc
	v_add_u32_e32 v177, s8, v169
	global_load_dwordx2 v[144:145], v[66:67], off
	ds_read_b128 v[66:69], v176 offset:2560
	ds_read_b128 v[70:73], v176 offset:2576
	ds_read_b128 v[178:181], v177 offset:5120
	ds_read_b128 v[182:185], v177 offset:5136
	global_load_dwordx2 v[146:147], v[150:151], off offset:192
	v_exp_f32_e32 v164, v34
	v_exp_f32_e32 v165, v35
	v_exp_f32_e32 v154, v38
	v_exp_f32_e32 v155, v39
	v_exp_f32_e32 v162, v40
	v_exp_f32_e32 v163, v41
	v_exp_f32_e32 v158, v42
	v_exp_f32_e32 v159, v43
	v_exp_f32_e32 v46, v46
	v_exp_f32_e32 v47, v47
	v_exp_f32_e32 v50, v50
	v_exp_f32_e32 v51, v51
	v_exp_f32_e32 v40, v54
	v_exp_f32_e32 v41, v55
	v_exp_f32_e32 v42, v58
	v_exp_f32_e32 v43, v59
	v_exp_f32_e32 v34, v62
	v_exp_f32_e32 v35, v63
	v_exp_f32_e32 v160, v36
	v_exp_f32_e32 v161, v37
	v_exp_f32_e32 v152, v44
	v_exp_f32_e32 v153, v45
	v_exp_f32_e32 v156, v48
	v_exp_f32_e32 v157, v49
	v_exp_f32_e32 v44, v52
	v_exp_f32_e32 v45, v53
	v_exp_f32_e32 v48, v56
	v_exp_f32_e32 v49, v57
	v_exp_f32_e32 v36, v60
	v_exp_f32_e32 v37, v61
	v_exp_f32_e32 v38, v64
	v_exp_f32_e32 v39, v65
	s_nop 0
	s_nop 0
	s_nop 0
	s_nop 0
	s_nop 0
	s_nop 0
	s_nop 0
	s_nop 0
	v_cvt_scalef32_pk_fp8_f32 v52, v164, v165, s69
	v_cvt_scalef32_pk_fp8_f32 v56, v50, v51, s69
	v_cvt_scalef32_pk_fp8_f32 v53, v154, v155, s69
	v_cvt_scalef32_pk_fp8_f32 v57, v40, v41, s69
	v_cvt_scalef32_pk_fp8_f32 v54, v158, v159, s69
	v_cvt_scalef32_pk_fp8_f32 v58, v42, v43, s69
	v_cvt_scalef32_pk_fp8_f32 v55, v46, v47, s69
	v_cvt_scalef32_pk_fp8_f32 v59, v34, v35, s69
	v_cvt_scalef32_pk_fp8_f32 v52, v160, v161, s69 op_sel:[0,0,0,1]
	v_cvt_scalef32_pk_fp8_f32 v56, v44, v45, s69 op_sel:[0,0,0,1]
	v_cvt_scalef32_pk_fp8_f32 v53, v162, v163, s69 op_sel:[0,0,0,1]
	v_cvt_scalef32_pk_fp8_f32 v57, v48, v49, s69 op_sel:[0,0,0,1]
	v_cvt_scalef32_pk_fp8_f32 v54, v152, v153, s69 op_sel:[0,0,0,1]
	v_cvt_scalef32_pk_fp8_f32 v58, v36, v37, s69 op_sel:[0,0,0,1]
	v_cvt_scalef32_pk_fp8_f32 v55, v156, v157, s69 op_sel:[0,0,0,1]
	v_cvt_scalef32_pk_fp8_f32 v59, v38, v39, s69 op_sel:[0,0,0,1]
	s_add_i32 s8, s12, 0x4680
	s_cmp_eq_u32 s51, 2
	s_waitcnt lgkmcnt(0)
	v_mfma_f32_32x32x64_f8f6f4 v[18:33], v[178:185], v[52:59], v[18:33]
	ds_read_b128 v[178:181], v177 offset:7680
	ds_read_b128 v[182:185], v177 offset:7696
	s_cselect_b64 s[12:13], -1, 0
	s_and_b64 s[10:11], s[12:13], exec
	s_cselect_b32 s8, 0, s8
	s_add_i32 s8, s8, 0
	s_mov_b64 s[18:19], -1
	v_mfma_f32_32x32x64_f8f6f4 v[66:81], v[66:73], v[98:105], 0
	s_waitcnt lgkmcnt(0)
	v_mfma_f32_32x32x64_f8f6f4 v[2:17], v[178:185], v[52:59], v[2:17]
	v_add_u32_e32 v52, s8, v131
	s_waitcnt vmcnt(7)
	ds_write_b64 v52, v[136:137]
	v_add_u32_e32 v52, s8, v168
	s_and_b32 s8, s23, 0xe00
	s_add_i32 s10, s8, s76
	s_mul_hi_u32 s8, s10, 0xaaaaaaab
	s_lshr_b32 s8, s8, 6
	s_mul_i32 s53, s8, 0xffffffa0
	v_add_u32_e32 v52, 0x1400, v52
	s_add_i32 s53, s53, s10
	s_mov_b64 s[10:11], s[0:1]
	s_waitcnt vmcnt(6)
	ds_write2_b32 v52, v138, v139 offset1:8
	s_waitcnt lgkmcnt(0)
	s_barrier
	s_load_dwordx2 s[16:17], s[10:11], 0xd8
	s_cmp_lt_i32 s53, 64
	s_cselect_b64 s[14:15], -1, 0
	s_cmp_gt_i32 s53, 63
	s_cbranch_scc0 .LBB0_1929
	s_lshl_b64 s[10:11], s[8:9], 20
	s_waitcnt lgkmcnt(0)
	s_add_u32 s10, s16, s10
	s_addc_u32 s11, s17, s11
	s_add_u32 s10, s10, 0x15094000
	s_addc_u32 s11, s11, 0
	s_and_b32 s18, s53, 0x7ffffffc
	s_sub_i32 s52, s18, 64
	s_mov_b64 s[18:19], 0

; DI f32x16 mfma8(v8i a, v8i b, f32x16 c) { return __builtin_amdgcn_mfma_scale_f32_32x32x64_f8f6f4(a, b, c, 0, 0, 0, 0, 0, 0); }
; DI void attn_unit_a8(unsigned char* lds, const AttnArgs& a) {
;     ...
;     auto step = [&](int t, u32x2& kl, u32x2& vl, const u32x2& ks, const u32x2& vs, f32x16& c0, f32x16& c1, f32x16& n0, f32x16& n1, const int hk, const int wj) __attribute__((always_inline)) {
;         const int slot1 = slot == 2 ? 0 : slot + 1, slot2 = slot1 == 2 ? 0 : slot1 + 1;
;         if (hk == 1) { w_cvt(); w_issue(wj + 1 < AT_NWT ? wj + 1 : AT_NWT - 1); }
;         if (hk == 2) w_store(wj);
;         { const int tn = t + 3; gload(tn < a.t1 ? tn : a.t1 - 1, kl, vl); }
;         const unsigned char* Kb = lds + slot * AT_BUFB; const unsigned char* Kn = lds + slot1 * AT_BUFB;
;         const v8i k0 = kread(Kn, 0), k1 = kread(Kn, 1), v0 = vread(Kb, 0), v1 = vread(Kb, 1);
;         n0 = mfma8(k0, qf8, cinit); n1 = mfma8(k1, qf8, cinit);
;         expsum(c0); expsum(c1);
;         const v8i P = pack8(c0, c1);
;         o0[0] = mfma8(v0, P, o0[0]); o0[1] = mfma8(v1, P, o0[1]);
;         lstore(slot2, ks, vs);
;         __syncthreads();
;         slot = slot1;
;     };
;     {
;         int t = a.t0;
;         if (wrider)
;             for (int j = 0; j < AT_NWT; ++j, t += 2) { step(t, kregB, vregB, kregA, vregA, sx0, sx1, sy0, sy1, 1, j); step(t + 1, kregA, vregA, kregB, vregB, sy0, sy1, sx0, sx1, 2, j); }
;         for (; t < a.t1; t += 2) {
;             step(t, kregB, vregB, kregA, vregA, sx0, sx1, sy0, sy1, 0, 0);
;             if (t + 1 < a.t1) step(t + 1, kregA, vregA, kregB, vregB, sy0, sy1, sx0, sx1, 0, 0);
;             else { sx0 = sy0; sx1 = sy1; }
;         }
.LBB0_1934:
	s_min_u32 s8, s50, 64
	s_cmp_lt_u32 s50, 61
	s_cselect_b64 s[10:11], -1, 0
	s_lshl_b32 s8, s8, 6
	s_add_i32 s15, s8, 0xc0
	s_add_i32 s18, s8, 0xfffff0c0
	s_and_b64 s[16:17], s[10:11], exec
	s_cselect_b32 s15, s15, s18
	s_mov_b32 s18, s14
	s_add_i32 s14, s14, 1
	s_cmp_lg_u32 s18, 2
	s_cselect_b32 s14, s14, 0
	s_mul_i32 s19, s14, 0x4680
	v_mov_b64_e32 v[80:81], v[64:65]
	v_add_u32_e32 v106, s19, v169
	v_mov_b64_e32 v[78:79], v[62:63]
	v_mov_b64_e32 v[76:77], v[60:61]
	v_mov_b64_e32 v[74:75], v[58:59]
	v_mov_b64_e32 v[72:73], v[56:57]
	v_mov_b64_e32 v[70:71], v[54:55]
	v_mov_b64_e32 v[68:69], v[52:53]
	v_mov_b64_e32 v[66:67], v[50:51]
	ds_read_b128 v[50:53], v106
	ds_read_b128 v[54:57], v106 offset:16
	v_add_u32_e32 v58, s15, v130
	v_mov_b64_e32 v[96:97], v[48:49]
	s_and_b64 s[10:11], s[10:11], exec
	v_ashrrev_i32_e32 v59, 31, v58
	v_mov_b64_e32 v[94:95], v[46:47]
	v_mov_b64_e32 v[92:93], v[44:45]
	v_mov_b64_e32 v[90:91], v[42:43]
	v_mov_b64_e32 v[88:89], v[40:41]
	v_mov_b64_e32 v[86:87], v[38:39]
	v_mov_b64_e32 v[84:85], v[36:37]
	v_mov_b64_e32 v[82:83], v[34:35]
	s_cselect_b32 s16, s42, s12
	s_cselect_b32 s17, s43, s13
	s_waitcnt lgkmcnt(0)
	v_mfma_f32_32x32x64_f8f6f4 v[34:49], v[50:57], v[98:105], 0
	v_lshlrev_b64 v[50:51], 7, v[58:59]
	v_lshl_add_u64 v[50:51], s[16:17], 0, v[50:51]
	v_lshl_add_u64 v[50:51], v[50:51], 0, v[132:133]
	v_lshl_add_u64 v[58:59], v[134:135], 0, s[8:9]
	global_load_dwordx2 v[112:113], v[50:51], off
	ds_read_b128 v[50:53], v106 offset:2560
	ds_read_b128 v[54:57], v106 offset:2576
	global_load_dwordx2 v[114:115], v[58:59], off offset:192
	s_mulk_i32 s18, 0x4680
	v_add_u32_e32 v58, s18, v169
	v_exp_f32_e32 v82, v82
	v_exp_f32_e32 v83, v83
	v_exp_f32_e32 v86, v86
	v_exp_f32_e32 v87, v87
	v_exp_f32_e32 v90, v90
	v_exp_f32_e32 v91, v91
	v_exp_f32_e32 v94, v94
	v_exp_f32_e32 v95, v95
	v_exp_f32_e32 v124, v66
	v_exp_f32_e32 v125, v67
	v_exp_f32_e32 v148, v70
	v_exp_f32_e32 v149, v71
	v_exp_f32_e32 v74, v74
	v_exp_f32_e32 v75, v75
	v_exp_f32_e32 v78, v78
	v_exp_f32_e32 v79, v79
	ds_read_b128 v[116:119], v58 offset:5120
	ds_read_b128 v[120:123], v58 offset:5136
	ds_read_b128 v[140:143], v58 offset:7680
	ds_read_b128 v[144:147], v58 offset:7696
	v_exp_f32_e32 v84, v84
	v_exp_f32_e32 v85, v85
	v_exp_f32_e32 v88, v88
	v_exp_f32_e32 v89, v89
	v_exp_f32_e32 v92, v92
	v_exp_f32_e32 v93, v93
	v_exp_f32_e32 v96, v96
	v_exp_f32_e32 v97, v97
	v_exp_f32_e32 v126, v68
	v_exp_f32_e32 v127, v69
	v_exp_f32_e32 v150, v72
	v_exp_f32_e32 v151, v73
	v_exp_f32_e32 v76, v76
	v_exp_f32_e32 v77, v77
	v_exp_f32_e32 v80, v80
	v_exp_f32_e32 v81, v81
	s_nop 0
	s_nop 0
	s_nop 0
	s_nop 0
	s_nop 0
	s_nop 0
	s_nop 0
	s_nop 0
	v_cvt_scalef32_pk_fp8_f32 v66, v82, v83, s69
	v_cvt_scalef32_pk_fp8_f32 v70, v124, v125, s69
	v_cvt_scalef32_pk_fp8_f32 v67, v86, v87, s69
	v_cvt_scalef32_pk_fp8_f32 v71, v148, v149, s69
	v_cvt_scalef32_pk_fp8_f32 v68, v90, v91, s69
	v_cvt_scalef32_pk_fp8_f32 v72, v74, v75, s69
	v_cvt_scalef32_pk_fp8_f32 v69, v94, v95, s69
	v_cvt_scalef32_pk_fp8_f32 v73, v78, v79, s69
	v_cvt_scalef32_pk_fp8_f32 v66, v84, v85, s69 op_sel:[0,0,0,1]
	v_cvt_scalef32_pk_fp8_f32 v70, v126, v127, s69 op_sel:[0,0,0,1]
	v_cvt_scalef32_pk_fp8_f32 v67, v88, v89, s69 op_sel:[0,0,0,1]
	v_cvt_scalef32_pk_fp8_f32 v71, v150, v151, s69 op_sel:[0,0,0,1]
	v_cvt_scalef32_pk_fp8_f32 v68, v92, v93, s69 op_sel:[0,0,0,1]
	v_cvt_scalef32_pk_fp8_f32 v72, v76, v77, s69 op_sel:[0,0,0,1]
	v_cvt_scalef32_pk_fp8_f32 v69, v96, v97, s69 op_sel:[0,0,0,1]
	v_cvt_scalef32_pk_fp8_f32 v73, v80, v81, s69 op_sel:[0,0,0,1]
	s_waitcnt lgkmcnt(4)
	v_mfma_f32_32x32x64_f8f6f4 v[50:65], v[50:57], v[98:105], 0
	s_add_i32 s15, s19, 0x4680
	s_cmp_eq_u32 s14, 2
	v_add_f32_e64 v110, v110, v84
	v_add_f32_e64 v111, v111, v85
	v_add_f32_e64 v82, v108, v82
	v_add_f32_e64 v83, v109, v83
	s_cselect_b64 s[10:11], -1, 0
	v_add_f32_e64 v84, v88, v110
	v_add_f32_e64 v85, v89, v111
	v_add_f32_e64 v82, v86, v82
	v_add_f32_e64 v83, v87, v83
	v_add_f32_e64 v84, v92, v84
	v_add_f32_e64 v85, v93, v85
	v_pk_add_f32 v[82:83], v[90:91], v[82:83]
	s_and_b64 s[16:17], s[10:11], exec
	v_pk_add_f32 v[84:85], v[96:97], v[84:85]
	v_pk_add_f32 v[82:83], v[94:95], v[82:83]
	s_cselect_b32 s8, 0, s15
	v_pk_add_f32 v[82:83], v[124:125], v[82:83]
	v_pk_add_f32 v[84:85], v[126:127], v[84:85]
	s_waitcnt lgkmcnt(2)
	v_mfma_f32_32x32x64_f8f6f4 v[18:33], v[116:123], v[66:73], v[18:33]
	s_add_i32 s8, s8, 0
	v_add_f32_e64 v84, v150, v84
	v_add_f32_e64 v85, v151, v85
	v_add_f32_e64 v82, v148, v82
	v_add_f32_e64 v83, v149, v83
	v_add_f32_e64 v76, v76, v84
	v_add_f32_e64 v77, v77, v85
	v_add_f32_e64 v74, v74, v82
	v_add_f32_e64 v75, v75, v83
	v_add_f32_e64 v110, v80, v76
	v_add_f32_e64 v111, v81, v77
	v_add_f32_e64 v108, v78, v74
	v_add_f32_e64 v109, v79, v75
	s_cmpk_gt_u32 s50, 0x42
	s_waitcnt lgkmcnt(0)
	v_mfma_f32_32x32x64_f8f6f4 v[2:17], v[140:147], v[66:73], v[2:17]
	v_add_u32_e32 v66, s8, v131
	s_waitcnt vmcnt(3)
	ds_write_b64 v66, v[136:137]
	v_add_u32_e32 v66, s8, v168
	v_add_u32_e32 v66, 0x1400, v66
	s_waitcnt vmcnt(2)
	ds_write2_b32 v66, v138, v139 offset1:8
	s_waitcnt lgkmcnt(0)
	s_barrier
; DI f32x16 mfma8(v8i a, v8i b, f32x16 c) { return __builtin_amdgcn_mfma_scale_f32_32x32x64_f8f6f4(a, b, c, 0, 0, 0, 0, 0, 0); }
; DI void attn_unit_a8(unsigned char* lds, const AttnArgs& a) {
;     ...
;     auto step = [&](int t, u32x2& kl, u32x2& vl, const u32x2& ks, const u32x2& vs, f32x16& c0, f32x16& c1, f32x16& n0, f32x16& n1, const int hk, const int wj) __attribute__((always_inline)) {
;         const int slot1 = slot == 2 ? 0 : slot + 1, slot2 = slot1 == 2 ? 0 : slot1 + 1;
;         if (hk == 1) { w_cvt(); w_issue(wj + 1 < AT_NWT ? wj + 1 : AT_NWT - 1); }
;         if (hk == 2) w_store(wj);
;         { const int tn = t + 3; gload(tn < a.t1 ? tn : a.t1 - 1, kl, vl); }
;         const unsigned char* Kb = lds + slot * AT_BUFB; const unsigned char* Kn = lds + slot1 * AT_BUFB;
;         const v8i k0 = kread(Kn, 0), k1 = kread(Kn, 1), v0 = vread(Kb, 0), v1 = vread(Kb, 1);
;         n0 = mfma8(k0, qf8, cinit); n1 = mfma8(k1, qf8, cinit);
;         expsum(c0); expsum(c1);
;         const v8i P = pack8(c0, c1);
;         o0[0] = mfma8(v0, P, o0[0]); o0[1] = mfma8(v1, P, o0[1]);
;         lstore(slot2, ks, vs);
;         __syncthreads();
;         slot = slot1;
;     };
;     {
;         int t = a.t0;
;         if (wrider)
;             for (int j = 0; j < AT_NWT; ++j, t += 2) { step(t, kregB, vregB, kregA, vregA, sx0, sx1, sy0, sy1, 1, j); step(t + 1, kregA, vregA, kregB, vregB, sy0, sy1, sx0, sx1, 2, j); }
;         for (; t < a.t1; t += 2) {
;             step(t, kregB, vregB, kregA, vregA, sx0, sx1, sy0, sy1, 0, 0);
;             if (t + 1 < a.t1) step(t + 1, kregA, vregA, kregB, vregB, sy0, sy1, sx0, sx1, 0, 0);
;             else { sx0 = sy0; sx1 = sy1; }
;         }
	s_cbranch_scc1 .LBB0_1936
	s_min_u32 s8, s50, 63
	s_cmp_lt_u32 s50, 60
	s_cselect_b64 s[16:17], -1, 0
	s_lshl_b32 s8, s8, 6
	s_add_i32 s15, s8, 0x100
	s_add_i32 s20, s8, 0xfffff100
	s_and_b64 s[18:19], s[16:17], exec
	s_cselect_b32 s15, s15, s20
	s_add_i32 s14, s14, 1
	s_and_b64 s[10:11], s[10:11], exec
	v_add_u32_e32 v82, s15, v130
	s_cselect_b32 s14, 0, s14
	s_and_b64 s[16:17], s[16:17], exec
	v_ashrrev_i32_e32 v83, 31, v82
	s_cselect_b32 s17, s43, s13
	s_cselect_b32 s16, s42, s12
	v_lshlrev_b64 v[82:83], 7, v[82:83]
	s_mul_i32 s10, s14, 0x4680
	v_lshl_add_u64 v[90:91], s[16:17], 0, v[82:83]
	v_add_u32_e32 v86, s10, v169
	v_lshl_add_u64 v[90:91], v[90:91], 0, v[132:133]
	ds_read_b128 v[66:69], v86
	ds_read_b128 v[70:73], v86 offset:16
	ds_read_b128 v[82:85], v86 offset:2560
	ds_read_b128 v[86:89], v86 offset:2576
	global_load_dwordx2 v[136:137], v[90:91], off
	v_lshl_add_u64 v[90:91], v[134:135], 0, s[8:9]
	global_load_dwordx2 v[138:139], v[90:91], off offset:256
	v_exp_f32_e32 v124, v34
	v_exp_f32_e32 v125, v35
	v_exp_f32_e32 v36, v36
	v_exp_f32_e32 v37, v37
	v_exp_f32_e32 v126, v38
	v_exp_f32_e32 v127, v39
	v_exp_f32_e32 v42, v42
	v_exp_f32_e32 v43, v43
	v_exp_f32_e32 v46, v46
	v_exp_f32_e32 v47, v47
	v_exp_f32_e32 v50, v50
	v_exp_f32_e32 v51, v51
	v_exp_f32_e32 v54, v54
	v_exp_f32_e32 v55, v55
	v_exp_f32_e32 v58, v58
	v_exp_f32_e32 v59, v59
	v_exp_f32_e32 v62, v62
	v_exp_f32_e32 v63, v63
	ds_read_b128 v[116:119], v106 offset:5120
	ds_read_b128 v[120:123], v106 offset:5136
	ds_read_b128 v[140:143], v106 offset:7680
	ds_read_b128 v[144:147], v106 offset:7696
	v_exp_f32_e32 v148, v40
	v_exp_f32_e32 v149, v41
	v_exp_f32_e32 v44, v44
	v_exp_f32_e32 v45, v45
	v_exp_f32_e32 v48, v48
	v_exp_f32_e32 v49, v49
	v_exp_f32_e32 v52, v52
	v_exp_f32_e32 v53, v53
	v_exp_f32_e32 v56, v56
	v_exp_f32_e32 v57, v57
	v_exp_f32_e32 v60, v60
	v_exp_f32_e32 v61, v61
	v_exp_f32_e32 v64, v64
	v_exp_f32_e32 v65, v65
	s_nop 0
	v_cvt_scalef32_pk_fp8_f32 v34, v124, v125, s69
	v_pk_add_f32 v[110:111], v[110:111], v[36:37]
	v_cvt_scalef32_pk_fp8_f32 v34, v36, v37, s69 op_sel:[0,0,0,1]
	s_nop 0
	s_nop 0
	s_nop 0
	s_nop 0
	s_nop 0
	s_nop 0
	s_nop 0
	s_waitcnt lgkmcnt(6)
	v_mfma_f32_32x32x64_f8f6f4 v[66:81], v[66:73], v[98:105], 0
	v_cvt_scalef32_pk_fp8_f32 v38, v50, v51, s69
	v_cvt_scalef32_pk_fp8_f32 v35, v126, v127, s69
	v_cvt_scalef32_pk_fp8_f32 v39, v54, v55, s69
	v_cvt_scalef32_pk_fp8_f32 v36, v42, v43, s69
	v_cvt_scalef32_pk_fp8_f32 v40, v58, v59, s69
	v_cvt_scalef32_pk_fp8_f32 v37, v46, v47, s69
	v_cvt_scalef32_pk_fp8_f32 v41, v62, v63, s69
	v_cvt_scalef32_pk_fp8_f32 v38, v52, v53, s69 op_sel:[0,0,0,1]
	v_cvt_scalef32_pk_fp8_f32 v35, v148, v149, s69 op_sel:[0,0,0,1]
	v_cvt_scalef32_pk_fp8_f32 v39, v56, v57, s69 op_sel:[0,0,0,1]
	v_cvt_scalef32_pk_fp8_f32 v36, v44, v45, s69 op_sel:[0,0,0,1]
	v_cvt_scalef32_pk_fp8_f32 v40, v60, v61, s69 op_sel:[0,0,0,1]
	v_cvt_scalef32_pk_fp8_f32 v37, v48, v49, s69 op_sel:[0,0,0,1]
	v_cvt_scalef32_pk_fp8_f32 v41, v64, v65, s69 op_sel:[0,0,0,1]
	v_pk_add_f32 v[108:109], v[108:109], v[124:125]
	s_waitcnt lgkmcnt(4)
	v_mfma_f32_32x32x64_f8f6f4 v[82:97], v[82:89], v[98:105], 0
	s_addk_i32 s10, 0x4680
	v_add_f32_e64 v110, v148, v110
	v_add_f32_e64 v111, v149, v111
	v_add_f32_e64 v108, v126, v108
	v_add_f32_e64 v109, v127, v109
	s_cmp_lg_u32 s14, 2
	v_add_f32_e64 v42, v42, v108
	v_add_f32_e64 v43, v43, v109
	v_add_f32_e64 v44, v44, v110
	v_add_f32_e64 v45, v45, v111
	s_cselect_b32 s8, s10, 0
	v_add_f32_e64 v44, v48, v44
	v_add_f32_e64 v45, v49, v45
	v_pk_add_f32 v[42:43], v[46:47], v[42:43]
	s_add_i32 s8, s8, 0
	v_pk_add_f32 v[42:43], v[50:51], v[42:43]
	v_pk_add_f32 v[44:45], v[52:53], v[44:45]
	v_pk_add_f32 v[42:43], v[54:55], v[42:43]
	v_pk_add_f32 v[44:45], v[56:57], v[44:45]
	v_pk_add_f32 v[42:43], v[58:59], v[42:43]
	s_waitcnt lgkmcnt(2)
	v_mfma_f32_32x32x64_f8f6f4 v[18:33], v[116:123], v[34:41], v[18:33]
	v_add_f32_e64 v44, v60, v44
	v_add_f32_e64 v45, v61, v45
	v_add_f32_e64 v108, v62, v42
	v_add_f32_e64 v109, v63, v43
	v_add_f32_e64 v110, v64, v44
	v_add_f32_e64 v111, v65, v45
	v_mov_b64_e32 v[50:51], v[82:83]
	v_mov_b64_e32 v[52:53], v[84:85]
	v_mov_b64_e32 v[54:55], v[86:87]
	v_mov_b64_e32 v[56:57], v[88:89]
	v_mov_b64_e32 v[58:59], v[90:91]
	v_mov_b64_e32 v[60:61], v[92:93]
	v_mov_b64_e32 v[62:63], v[94:95]
	v_mov_b64_e32 v[64:65], v[96:97]
	s_waitcnt lgkmcnt(0)
	v_mfma_f32_32x32x64_f8f6f4 v[2:17], v[140:147], v[34:41], v[2:17]
	v_add_u32_e32 v34, s8, v131
	s_waitcnt vmcnt(3)
	ds_write_b64 v34, v[112:113]
	v_add_u32_e32 v34, s8, v168
	v_add_u32_e32 v34, 0x1400, v34
	s_waitcnt vmcnt(2)
	ds_write2_b32 v34, v114, v115 offset1:8
	v_mov_b64_e32 v[34:35], v[66:67]
	v_mov_b64_e32 v[36:37], v[68:69]
	v_mov_b64_e32 v[38:39], v[70:71]
	v_mov_b64_e32 v[40:41], v[72:73]
	v_mov_b64_e32 v[42:43], v[74:75]
	v_mov_b64_e32 v[44:45], v[76:77]
	v_mov_b64_e32 v[46:47], v[78:79]
	v_mov_b64_e32 v[48:49], v[80:81]
	s_waitcnt lgkmcnt(0)
	s_barrier

; DI unsigned pk4_fp8(float a, float b, float c, float d) { int r = 0; r = __builtin_amdgcn_cvt_pk_fp8_f32(a, b, r, false); r = __builtin_amdgcn_cvt_pk_fp8_f32(c, d, r, true); return (unsigned)r; }
; DI float clamp448(float x) { return __builtin_amdgcn_fmed3f(x, -448.0f, 448.0f); }
; DI float sigmoidf_(float x) { return 1.0f / (1.0f + __expf(-x)); }
; DI void conv_unit(unsigned char* lds, int seqrow, int L, int t0, const bf16_t* BU, const bf16_t* BG, const float* cw, const float* cb, const float* lg, const float* lb, unsigned char* CAT) {
;     ...
;     for (int tt = wv; tt < 64; tt += 8) {
;         const f32x4 v = *(const f32x4*)(z + tt * 256 + 4 * lane);
;         const float mean = wave_sum(v[0] + v[1] + v[2] + v[3]) * (1.0f / 256.0f);
;         const f32x4 d = v - mean;
;         const float var = wave_sum(d[0] * d[0] + d[1] * d[1] + d[2] * d[2] + d[3] * d[3]) * (1.0f / 256.0f);
;         const f32x4 y = d * rsqrtf(var + EPS) * g4 + b4;
;         f32x4 o;
; #pragma unroll
;         for (int e = 0; e < 4; ++e) o[e] = y[e] * sigmoidf_(y[e]);
;         *(unsigned*)(CAT + (size_t)(seqrow + t0 + tt) * 1024 + 256 + 4 * lane) = pk4_fp8(clamp448(o[0] * CAT_SCALE), clamp448(o[1] * CAT_SCALE), clamp448(o[2] * CAT_SCALE), clamp448(o[3] * CAT_SCALE));
;     }
.LBB0_2051:
	ds_read_b128 v[12:15], v11
	v_add_u32_e32 v18, 8, v10
	v_add_u32_e32 v16, s69, v10
	v_cmp_lt_i32_e32 vcc, 55, v10
	v_mov_b32_e32 v10, v18
	s_waitcnt lgkmcnt(0)
	v_add_f32_e32 v18, v12, v13
	v_add_f32_e32 v18, v14, v18
	v_add_f32_e32 v18, v15, v18
	ds_bpermute_b32 v19, v1, v18
	s_or_b64 s[14:15], vcc, s[14:15]
	v_ashrrev_i32_e32 v17, 31, v16
	v_lshlrev_b64 v[16:17], 10, v[16:17]
	v_lshl_add_u64 v[16:17], s[50:51], 0, v[16:17]
	s_waitcnt lgkmcnt(0)
	v_add_f32_e32 v18, v18, v19
	ds_bpermute_b32 v19, v208, v18
	s_nop 0
	v_lshl_add_u64 v[16:17], v[16:17], 0, v[58:59]
	v_add_u32_e32 v11, 0x2000, v11
	s_waitcnt lgkmcnt(0)
	v_add_f32_e32 v18, v18, v19
	ds_bpermute_b32 v19, v209, v18
	s_waitcnt lgkmcnt(0)
	v_add_f32_e32 v18, v18, v19
	ds_bpermute_b32 v19, v210, v18
	s_waitcnt lgkmcnt(0)
	v_add_f32_e32 v18, v18, v19
	ds_bpermute_b32 v19, v211, v18
	s_waitcnt lgkmcnt(0)
	v_add_f32_e32 v18, v18, v19
	ds_bpermute_b32 v19, v212, v18
	s_waitcnt lgkmcnt(0)
	v_add_f32_e32 v18, v18, v19
	v_fmamk_f32 v13, v18, 0xbb800000, v13
	v_fmamk_f32 v12, v18, 0xbb800000, v12
	v_fmamk_f32 v15, v18, 0xbb800000, v15
	v_fmac_f32_e32 v14, 0xbb800000, v18
	v_pk_mul_f32 v[20:21], v[12:13], v[12:13]
	v_pk_mul_f32 v[18:19], v[14:15], v[14:15]
	v_add_f32_e32 v20, v20, v21
	v_add_f32_e32 v18, v18, v20
	v_add_f32_e32 v18, v19, v18
	ds_bpermute_b32 v19, v1, v18
	s_waitcnt lgkmcnt(0)
	v_add_f32_e32 v18, v18, v19
	ds_bpermute_b32 v19, v208, v18
	s_waitcnt lgkmcnt(0)
	v_add_f32_e32 v18, v18, v19
	ds_bpermute_b32 v19, v209, v18
	s_waitcnt lgkmcnt(0)
	v_add_f32_e32 v18, v18, v19
	ds_bpermute_b32 v19, v210, v18
	s_waitcnt lgkmcnt(0)
	v_add_f32_e32 v18, v18, v19
	ds_bpermute_b32 v19, v211, v18
	s_waitcnt lgkmcnt(0)
	v_add_f32_e32 v18, v18, v19
	ds_bpermute_b32 v19, v212, v18
	s_waitcnt lgkmcnt(0)
	v_add_f32_e32 v18, v18, v19
	v_fmamk_f32 v18, v18, 0x3b800000, v62
	v_mul_f32_e32 v19, 0x4b800000, v18
	v_cmp_gt_f32_e32 vcc, s67, v18
	s_nop 1
	v_cndmask_b32_e32 v18, v18, v19, vcc
	v_rsq_f32_e32 v18, v18
	s_nop 0
	v_mul_f32_e32 v19, 0x45800000, v18
	v_cndmask_b32_e32 v18, v18, v19, vcc
	v_pk_mul_f32 v[12:13], v[12:13], v[18:19] op_sel_hi:[1,0]
	v_pk_mul_f32 v[14:15], v[14:15], v[18:19] op_sel_hi:[1,0]
	v_fma_f32 v12, v6, v12, v2
	v_fma_f32 v13, v7, v13, v3
	v_mul_f32_e32 v18, 0xbfb8aa3b, v12
	v_mul_f32_e32 v19, 0xbfb8aa3b, v13
	v_exp_f32_e32 v18, v18
	v_fma_f32 v14, v8, v14, v4
	v_exp_f32_e32 v19, v19
	v_mul_f32_e32 v20, 0xbfb8aa3b, v14
	v_fma_f32 v15, v9, v15, v5
	v_exp_f32_e32 v20, v20
	v_mul_f32_e32 v21, 0xbfb8aa3b, v15
	v_add_f32_e32 v18, 1.0, v18
	v_exp_f32_e32 v21, v21
	v_add_f32_e32 v19, 1.0, v19
	v_div_scale_f32 v23, s[6:7], v18, v18, 1.0
	v_div_scale_f32 v25, s[6:7], v19, v19, 1.0
	v_rcp_f32_e32 v31, v23
	v_add_f32_e32 v20, 1.0, v20
	v_rcp_f32_e32 v32, v25
	v_div_scale_f32 v27, s[8:9], v20, v20, 1.0
	v_add_f32_e32 v21, 1.0, v21
	v_rcp_f32_e32 v33, v27
	v_div_scale_f32 v29, s[10:11], v21, v21, 1.0
	v_fma_f32 v35, -v23, v31, 1.0
	v_div_scale_f32 v24, vcc, 1.0, v18, 1.0
	v_rcp_f32_e32 v34, v29
	v_fma_f32 v36, -v25, v32, 1.0
	v_fmac_f32_e32 v31, v35, v31
	v_div_scale_f32 v26, s[6:7], 1.0, v19, 1.0
	v_fmac_f32_e32 v32, v36, v32
	v_mul_f32_e32 v35, v24, v31
	v_fma_f32 v37, -v27, v33, 1.0
	v_mul_f32_e32 v36, v26, v32
	v_fma_f32 v39, -v23, v35, v24
	v_div_scale_f32 v28, s[8:9], 1.0, v20, 1.0
	v_fmac_f32_e32 v33, v37, v33
	v_fma_f32 v40, -v25, v36, v26
	v_fmac_f32_e32 v35, v39, v31
	v_fma_f32 v38, -v29, v34, 1.0
	v_mul_f32_e32 v37, v28, v33
	v_fmac_f32_e32 v36, v40, v32
	v_fma_f32 v23, -v23, v35, v24
	v_div_scale_f32 v30, s[10:11], 1.0, v21, 1.0
	v_fmac_f32_e32 v34, v38, v34
	v_fma_f32 v41, -v27, v37, v28
	v_fma_f32 v24, -v25, v36, v26
	v_div_fmas_f32 v23, v23, v31, v35
	s_mov_b64 vcc, s[6:7]
	v_mul_f32_e32 v38, v30, v34
	v_fmac_f32_e32 v37, v41, v33
	v_div_fixup_f32 v18, v23, v18, 1.0
	v_div_fmas_f32 v23, v24, v32, v36
	v_fma_f32 v42, -v29, v38, v30
	v_fma_f32 v25, -v27, v37, v28
	v_mul_f32_e32 v12, v12, v18
	v_div_fixup_f32 v18, v23, v19, 1.0
	s_mov_b64 vcc, s[8:9]
	v_fmac_f32_e32 v38, v42, v34
	v_div_fmas_f32 v19, v25, v33, v37
	v_mul_f32_e32 v13, v13, v18
	v_fma_f32 v26, -v29, v38, v30
	v_div_fixup_f32 v18, v19, v20, 1.0
	s_mov_b64 vcc, s[10:11]
	v_mul_f32_e32 v20, 0x41800000, v12
	v_mul_f32_e32 v13, 0x41800000, v13
	v_div_fmas_f32 v19, v26, v34, v38
	v_mul_f32_e32 v14, v14, v18
	v_med3_f32 v18, v20, s68, v63
	v_med3_f32 v13, v13, s68, v63
	v_add_co_u32_e32 v12, vcc, 0x2add4000, v16
	v_div_fixup_f32 v16, v19, v21, 1.0
	v_cvt_pk_fp8_f32 v22, v18, v13
	v_mul_f32_e32 v15, v15, v16
	v_mul_f32_e32 v14, 0x41800000, v14
	v_med3_f32 v13, v14, s68, v63
	v_mul_f32_e32 v14, 0x41800000, v15
	v_med3_f32 v14, v14, s68, v63
	v_cvt_pk_fp8_f32 v22, v13, v14 op_sel:[0,0,1]
	v_addc_co_u32_e32 v13, vcc, 0, v17, vcc
	global_store_dword v[12:13], v22, off offset:256
	s_andn2_b64 exec, exec, s[14:15]
	s_cbranch_execnz .LBB0_2051
	s_branch .LBB0_1940

; DI unsigned pk4_fp8(float a, float b, float c, float d) { int r = 0; r = __builtin_amdgcn_cvt_pk_fp8_f32(a, b, r, false); r = __builtin_amdgcn_cvt_pk_fp8_f32(c, d, r, true); return (unsigned)r; }
; DI float clamp448(float x) { return __builtin_amdgcn_fmed3f(x, -448.0f, 448.0f); }
; DI float bflo(unsigned u) { return __uint_as_float(u << 16); }
; DI float bfhi(unsigned u) { return __uint_as_float(u & 0xffff0000u); }
; DI void phase_router(unsigned char* lds, const Params& P, int li, const bf16_t* X1, unsigned char* H8, const float* modl, unsigned* cnt, int* tok_e, int* tok_pos, float* tok_gate, int* tok_list, int G, int ntok, int chsz) {
;     ...
;                 if (tl < chsz) {
;                     const u32x4 a = ra[rr], b = rbv[rr];
;                     v[0] = (f32x4){bflo(a[0]), bfhi(a[0]), bflo(a[1]), bfhi(a[1])}; v[1] = (f32x4){bflo(a[2]), bfhi(a[2]), bflo(a[3]), bfhi(a[3])};
;                     v[2] = (f32x4){bflo(b[0]), bfhi(b[0]), bflo(b[1]), bfhi(b[1])}; v[3] = (f32x4){bflo(b[2]), bfhi(b[2]), bflo(b[3]), bfhi(b[3])};
;                     const int b9 = tok < NLAT ? (tok >> 12) : 8; if (b9 != cur_b9) load_mod(b9);
;                     float ss = 0.f;
; #pragma unroll
;                     for (int j = 0; j < 4; ++j)
; #pragma unroll
;                         for (int i = 0; i < 4; ++i) ss += v[j][i] * v[j][i];
;                     ss = wave_sum(ss);
;                     const float rinv = __builtin_amdgcn_rsqf(ss * (1.0f / 1024.0f) + EPS);
; #pragma unroll
;                     for (int j = 0; j < 4; ++j) v[j] = v[j] * rinv * ma[j] + mb[j];
;                     { unsigned char* hr = H8 + (size_t)tok * 1024; u32x2 w0, w1;
;                       w0.x = pk4_fp8(clamp448(v[0][0]), clamp448(v[0][1]), clamp448(v[0][2]), clamp448(v[0][3])); w0.y = pk4_fp8(clamp448(v[1][0]), clamp448(v[1][1]), clamp448(v[1][2]), clamp448(v[1][3]));
;                       w1.x = pk4_fp8(clamp448(v[2][0]), clamp448(v[2][1]), clamp448(v[2][2]), clamp448(v[2][3])); w1.y = pk4_fp8(clamp448(v[3][0]), clamp448(v[3][1]), clamp448(v[3][2]), clamp448(v[3][3]));
;                       *(u32x2*)(hr + 8 * lane) = w0; *(u32x2*)(hr + 512 + 8 * lane) = w1; } }
.LBB0_2184:
	s_or_b64 exec, exec, s[26:27]
	s_waitcnt vmcnt(1)
	v_and_b32_e32 v107, 0xffff0000, v102
	v_lshlrev_b32_e32 v106, 16, v102
	v_mul_f32_e32 v112, v107, v107
	v_lshlrev_b32_e32 v102, 16, v103
	v_fmac_f32_e32 v112, v106, v106
	v_and_b32_e32 v103, 0xffff0000, v103
	v_fmac_f32_e32 v112, v102, v102
	v_lshlrev_b32_e32 v110, 16, v104
	v_fmac_f32_e32 v112, v103, v103
	v_and_b32_e32 v111, 0xffff0000, v104
	v_fmac_f32_e32 v112, v110, v110
	v_lshlrev_b32_e32 v104, 16, v105
	v_fmac_f32_e32 v112, v111, v111
	v_and_b32_e32 v105, 0xffff0000, v105
	v_fmac_f32_e32 v112, v104, v104
	s_waitcnt vmcnt(0)
	v_lshlrev_b32_e32 v114, 16, v98
	v_fmac_f32_e32 v112, v105, v105
	v_and_b32_e32 v115, 0xffff0000, v98
	v_fmac_f32_e32 v112, v114, v114
	v_lshlrev_b32_e32 v98, 16, v99
	v_fmac_f32_e32 v112, v115, v115
	v_and_b32_e32 v99, 0xffff0000, v99
	v_fmac_f32_e32 v112, v98, v98
	v_lshlrev_b32_e32 v118, 16, v100
	v_fmac_f32_e32 v112, v99, v99
	v_and_b32_e32 v119, 0xffff0000, v100
	v_and_b32_e32 v100, 0xffff0000, v101
	v_lshlrev_b32_e32 v101, 16, v101
	v_fmac_f32_e32 v112, v118, v118
	v_fmac_f32_e32 v112, v119, v119
	v_pk_mul_f32 v[108:109], v[100:101], v[100:101]
	v_ashrrev_i32_e32 v123, 31, v122
	v_add_f32_e32 v109, v109, v112
	v_add_f32_e32 v108, v108, v109
	v_and_b32_e32 v109, 64, v171
	v_add_u32_e32 v109, 64, v109
	v_xor_b32_e32 v112, 32, v171
	v_cmp_lt_i32_e32 vcc, v112, v109
	s_nop 1
	v_cndmask_b32_e32 v112, v171, v112, vcc
	v_lshlrev_b32_e32 v112, 2, v112
	ds_bpermute_b32 v112, v112, v108
	s_waitcnt lgkmcnt(0)
	v_add_f32_e32 v108, v108, v112
	v_xor_b32_e32 v112, 16, v171
	v_cmp_lt_i32_e32 vcc, v112, v109
	s_nop 1
	v_cndmask_b32_e32 v112, v171, v112, vcc
	v_lshlrev_b32_e32 v112, 2, v112
	ds_bpermute_b32 v112, v112, v108
	s_waitcnt lgkmcnt(0)
	v_add_f32_e32 v108, v108, v112
	v_xor_b32_e32 v112, 8, v171
	v_cmp_lt_i32_e32 vcc, v112, v109
	s_nop 1
	v_cndmask_b32_e32 v112, v171, v112, vcc
	v_lshlrev_b32_e32 v112, 2, v112
	ds_bpermute_b32 v112, v112, v108
	s_waitcnt lgkmcnt(0)
	v_add_f32_e32 v108, v108, v112
	v_xor_b32_e32 v112, 4, v171
	v_cmp_lt_i32_e32 vcc, v112, v109
	s_nop 1
	v_cndmask_b32_e32 v112, v171, v112, vcc
	v_lshlrev_b32_e32 v112, 2, v112
	ds_bpermute_b32 v112, v112, v108
	s_waitcnt lgkmcnt(0)
	v_add_f32_e32 v108, v108, v112
	v_xor_b32_e32 v112, 2, v171
	v_cmp_lt_i32_e32 vcc, v112, v109
	s_nop 1
	v_cndmask_b32_e32 v112, v171, v112, vcc
	v_lshlrev_b32_e32 v112, 2, v112
	ds_bpermute_b32 v112, v112, v108
	s_waitcnt lgkmcnt(0)
	v_add_f32_e32 v108, v108, v112
	v_xor_b32_e32 v112, 1, v171
	v_cmp_lt_i32_e32 vcc, v112, v109
	s_nop 1
	v_cndmask_b32_e32 v109, v171, v112, vcc
	v_lshlrev_b32_e32 v109, 2, v109
	ds_bpermute_b32 v109, v109, v108
	s_waitcnt lgkmcnt(0)
	v_add_f32_e32 v108, v108, v109
	v_fmamk_f32 v108, v108, 0x3a800000, v168
	v_rsq_f32_e32 v120, v108
	s_nop 0
	v_pk_mul_f32 v[106:107], v[106:107], v[120:121] op_sel_hi:[1,0]
	v_pk_mul_f32 v[102:103], v[102:103], v[120:121] op_sel_hi:[1,0]
	v_pk_mul_f32 v[98:99], v[98:99], v[120:121] op_sel_hi:[1,0]
	v_pk_fma_f32 v[108:109], v[84:85], v[102:103], v[72:73]
	v_pk_fma_f32 v[106:107], v[82:83], v[106:107], v[70:71]
	v_pk_mul_f32 v[102:103], v[110:111], v[120:121] op_sel_hi:[1,0]
	v_pk_fma_f32 v[116:117], v[92:93], v[98:99], v[80:81]
	v_pk_mul_f32 v[98:99], v[118:119], v[120:121] op_sel_hi:[1,0]
	v_pk_mul_f32 v[100:101], v[100:101], v[120:121] op_sel:[1,0] op_sel_hi:[0,0]
	v_pk_mul_f32 v[104:105], v[104:105], v[120:121] op_sel_hi:[1,0]
	v_pk_fma_f32 v[110:111], v[86:87], v[102:103], v[66:67]
	v_pk_mul_f32 v[102:103], v[114:115], v[120:121] op_sel_hi:[1,0]
	v_pk_fma_f32 v[120:121], v[96:97], v[100:101], v[76:77]
	v_pk_fma_f32 v[118:119], v[94:95], v[98:99], v[74:75]
	v_med3_f32 v99, v106, s46, v172
	v_med3_f32 v100, v107, s46, v172
	s_nop 0
	v_pk_fma_f32 v[114:115], v[90:91], v[102:103], v[78:79]
	v_cvt_pk_fp8_f32 v98, v99, v100
	v_med3_f32 v100, v110, s46, v172
	v_med3_f32 v103, v111, s46, v172
	s_nop 0
	v_cvt_pk_fp8_f32 v99, v100, v103
	v_pk_fma_f32 v[112:113], v[88:89], v[104:105], v[68:69]
	v_med3_f32 v101, v108, s46, v172
	v_med3_f32 v102, v109, s46, v172
	v_cvt_pk_fp8_f32 v98, v101, v102 op_sel:[0,0,1]
	v_med3_f32 v100, v112, s46, v172
	v_med3_f32 v101, v113, s46, v172
	v_cvt_pk_fp8_f32 v99, v100, v101 op_sel:[0,0,1]
	v_med3_f32 v101, v114, s46, v172
	v_med3_f32 v102, v115, s46, v172
	s_nop 0
	v_cvt_pk_fp8_f32 v100, v101, v102
	v_med3_f32 v102, v118, s46, v172
	v_med3_f32 v105, v119, s46, v172
	s_nop 0
	v_cvt_pk_fp8_f32 v101, v102, v105
	v_med3_f32 v103, v116, s46, v172
	v_med3_f32 v104, v117, s46, v172
	v_cvt_pk_fp8_f32 v100, v103, v104 op_sel:[0,0,1]
	v_med3_f32 v102, v120, s46, v172
	v_med3_f32 v103, v121, s46, v172
	v_cvt_pk_fp8_f32 v101, v102, v103 op_sel:[0,0,1]
	v_lshlrev_b64 v[102:103], 10, v[122:123]
	v_lshl_add_u64 v[102:103], v[148:149], 0, v[102:103]
	global_store_dwordx2 v[102:103], v[98:99], off
	global_store_dwordx2 v[102:103], v[100:101], off offset:512

; DI unsigned pk4_fp8(float a, float b, float c, float d) { int r = 0; r = __builtin_amdgcn_cvt_pk_fp8_f32(a, b, r, false); r = __builtin_amdgcn_cvt_pk_fp8_f32(c, d, r, true); return (unsigned)r; }
; DI float clamp448(float x) { return __builtin_amdgcn_fmed3f(x, -448.0f, 448.0f); }
; DI float bflo(unsigned u) { return __uint_as_float(u << 16); }
; DI float bfhi(unsigned u) { return __uint_as_float(u & 0xffff0000u); }
; DI void phase_router(unsigned char* lds, const Params& P, int li, const bf16_t* X1, unsigned char* H8, const float* modl, unsigned* cnt, int* tok_e, int* tok_pos, float* tok_gate, int* tok_list, int G, int ntok, int chsz) {
;     ...
;                 if (tl < chsz) {
;                     const u32x4 a = ra[rr], b = rbv[rr];
;                     v[0] = (f32x4){bflo(a[0]), bfhi(a[0]), bflo(a[1]), bfhi(a[1])}; v[1] = (f32x4){bflo(a[2]), bfhi(a[2]), bflo(a[3]), bfhi(a[3])};
;                     v[2] = (f32x4){bflo(b[0]), bfhi(b[0]), bflo(b[1]), bfhi(b[1])}; v[3] = (f32x4){bflo(b[2]), bfhi(b[2]), bflo(b[3]), bfhi(b[3])};
;                     const int b9 = tok < NLAT ? (tok >> 12) : 8; if (b9 != cur_b9) load_mod(b9);
;                     float ss = 0.f;
; #pragma unroll
;                     for (int j = 0; j < 4; ++j)
; #pragma unroll
;                         for (int i = 0; i < 4; ++i) ss += v[j][i] * v[j][i];
;                     ss = wave_sum(ss);
;                     const float rinv = __builtin_amdgcn_rsqf(ss * (1.0f / 1024.0f) + EPS);
; #pragma unroll
;                     for (int j = 0; j < 4; ++j) v[j] = v[j] * rinv * ma[j] + mb[j];
;                     { unsigned char* hr = H8 + (size_t)tok * 1024; u32x2 w0, w1;
;                       w0.x = pk4_fp8(clamp448(v[0][0]), clamp448(v[0][1]), clamp448(v[0][2]), clamp448(v[0][3])); w0.y = pk4_fp8(clamp448(v[1][0]), clamp448(v[1][1]), clamp448(v[1][2]), clamp448(v[1][3]));
;                       w1.x = pk4_fp8(clamp448(v[2][0]), clamp448(v[2][1]), clamp448(v[2][2]), clamp448(v[2][3])); w1.y = pk4_fp8(clamp448(v[3][0]), clamp448(v[3][1]), clamp448(v[3][2]), clamp448(v[3][3]));
;                       *(u32x2*)(hr + 8 * lane) = w0; *(u32x2*)(hr + 512 + 8 * lane) = w1; } }
.LBB0_2189:
	s_or_b64 exec, exec, s[26:27]
	s_waitcnt vmcnt(3)
	v_and_b32_e32 v115, 0xffff0000, v110
	v_lshlrev_b32_e32 v114, 16, v110
	v_mul_f32_e32 v120, v115, v115
	v_lshlrev_b32_e32 v110, 16, v111
	v_fmac_f32_e32 v120, v114, v114
	v_and_b32_e32 v111, 0xffff0000, v111
	v_fmac_f32_e32 v120, v110, v110
	v_lshlrev_b32_e32 v118, 16, v112
	v_fmac_f32_e32 v120, v111, v111
	v_and_b32_e32 v119, 0xffff0000, v112
	v_fmac_f32_e32 v120, v118, v118
	v_lshlrev_b32_e32 v112, 16, v113
	v_fmac_f32_e32 v120, v119, v119
	v_and_b32_e32 v113, 0xffff0000, v113
	v_fmac_f32_e32 v120, v112, v112
	s_waitcnt vmcnt(2)
	v_lshlrev_b32_e32 v122, 16, v106
	v_fmac_f32_e32 v120, v113, v113
	v_and_b32_e32 v123, 0xffff0000, v106
	v_fmac_f32_e32 v120, v122, v122
	v_lshlrev_b32_e32 v106, 16, v107
	v_fmac_f32_e32 v120, v123, v123
	v_and_b32_e32 v107, 0xffff0000, v107
	v_fmac_f32_e32 v120, v106, v106
	v_lshlrev_b32_e32 v126, 16, v108
	v_fmac_f32_e32 v120, v107, v107
	v_and_b32_e32 v127, 0xffff0000, v108
	v_and_b32_e32 v108, 0xffff0000, v109
	v_lshlrev_b32_e32 v109, 16, v109
	v_fmac_f32_e32 v120, v126, v126
	v_fmac_f32_e32 v120, v127, v127
	v_pk_mul_f32 v[116:117], v[108:109], v[108:109]
	v_ashrrev_i32_e32 v153, 31, v152
	v_add_f32_e32 v117, v117, v120
	v_add_f32_e32 v116, v116, v117
	v_and_b32_e32 v117, 64, v171
	v_add_u32_e32 v117, 64, v117
	v_xor_b32_e32 v120, 32, v171
	v_cmp_lt_i32_e32 vcc, v120, v117
	s_nop 1
	v_cndmask_b32_e32 v120, v171, v120, vcc
	v_lshlrev_b32_e32 v120, 2, v120
	ds_bpermute_b32 v120, v120, v116
	s_waitcnt lgkmcnt(0)
	v_add_f32_e32 v116, v116, v120
	v_xor_b32_e32 v120, 16, v171
	v_cmp_lt_i32_e32 vcc, v120, v117
	s_nop 1
	v_cndmask_b32_e32 v120, v171, v120, vcc
	v_lshlrev_b32_e32 v120, 2, v120
	ds_bpermute_b32 v120, v120, v116
	s_waitcnt lgkmcnt(0)
	v_add_f32_e32 v116, v116, v120
	v_xor_b32_e32 v120, 8, v171
	v_cmp_lt_i32_e32 vcc, v120, v117
	s_nop 1
	v_cndmask_b32_e32 v120, v171, v120, vcc
	v_lshlrev_b32_e32 v120, 2, v120
	ds_bpermute_b32 v120, v120, v116
	s_waitcnt lgkmcnt(0)
	v_add_f32_e32 v116, v116, v120
	v_xor_b32_e32 v120, 4, v171
	v_cmp_lt_i32_e32 vcc, v120, v117
	s_nop 1
	v_cndmask_b32_e32 v120, v171, v120, vcc
	v_lshlrev_b32_e32 v120, 2, v120
	ds_bpermute_b32 v120, v120, v116
	s_waitcnt lgkmcnt(0)
	v_add_f32_e32 v116, v116, v120
	v_xor_b32_e32 v120, 2, v171
	v_cmp_lt_i32_e32 vcc, v120, v117
	s_nop 1
	v_cndmask_b32_e32 v120, v171, v120, vcc
	v_lshlrev_b32_e32 v120, 2, v120
	ds_bpermute_b32 v120, v120, v116
	s_waitcnt lgkmcnt(0)
	v_add_f32_e32 v116, v116, v120
	v_xor_b32_e32 v120, 1, v171
	v_cmp_lt_i32_e32 vcc, v120, v117
	s_nop 1
	v_cndmask_b32_e32 v117, v171, v120, vcc
	v_lshlrev_b32_e32 v117, 2, v117
	ds_bpermute_b32 v117, v117, v116
	s_waitcnt lgkmcnt(0)
	v_add_f32_e32 v116, v116, v117
	v_fmamk_f32 v116, v116, 0x3a800000, v168
	v_rsq_f32_e32 v128, v116
	s_nop 0
	v_pk_mul_f32 v[114:115], v[114:115], v[128:129] op_sel_hi:[1,0]
	v_pk_mul_f32 v[110:111], v[110:111], v[128:129] op_sel_hi:[1,0]
	v_pk_mul_f32 v[106:107], v[106:107], v[128:129] op_sel_hi:[1,0]
	v_pk_fma_f32 v[116:117], v[84:85], v[110:111], v[72:73]
	v_pk_fma_f32 v[114:115], v[82:83], v[114:115], v[70:71]
	v_pk_mul_f32 v[110:111], v[118:119], v[128:129] op_sel_hi:[1,0]
	s_waitcnt vmcnt(0)
	v_pk_fma_f32 v[124:125], v[92:93], v[106:107], v[80:81]
	v_pk_mul_f32 v[106:107], v[126:127], v[128:129] op_sel_hi:[1,0]
	v_pk_mul_f32 v[108:109], v[108:109], v[128:129] op_sel:[1,0] op_sel_hi:[0,0]
	v_pk_mul_f32 v[112:113], v[112:113], v[128:129] op_sel_hi:[1,0]
	v_pk_fma_f32 v[118:119], v[86:87], v[110:111], v[66:67]
	v_pk_mul_f32 v[110:111], v[122:123], v[128:129] op_sel_hi:[1,0]
	v_pk_fma_f32 v[128:129], v[96:97], v[108:109], v[76:77]
	v_pk_fma_f32 v[126:127], v[94:95], v[106:107], v[74:75]
	v_med3_f32 v107, v114, s46, v172
	v_med3_f32 v108, v115, s46, v172
	s_nop 0
	v_pk_fma_f32 v[122:123], v[90:91], v[110:111], v[78:79]
	v_cvt_pk_fp8_f32 v106, v107, v108
	v_med3_f32 v108, v118, s46, v172
	v_med3_f32 v111, v119, s46, v172
	s_nop 0
	v_cvt_pk_fp8_f32 v107, v108, v111
	v_pk_fma_f32 v[120:121], v[88:89], v[112:113], v[68:69]
	v_med3_f32 v109, v116, s46, v172
	v_med3_f32 v110, v117, s46, v172
	v_cvt_pk_fp8_f32 v106, v109, v110 op_sel:[0,0,1]
	v_med3_f32 v108, v120, s46, v172
	v_med3_f32 v109, v121, s46, v172
	v_cvt_pk_fp8_f32 v107, v108, v109 op_sel:[0,0,1]
	v_med3_f32 v109, v122, s46, v172
	v_med3_f32 v110, v123, s46, v172
	s_nop 0
	v_cvt_pk_fp8_f32 v108, v109, v110
	v_med3_f32 v110, v126, s46, v172
	v_med3_f32 v113, v127, s46, v172
	s_nop 0
	v_cvt_pk_fp8_f32 v109, v110, v113
	v_med3_f32 v111, v124, s46, v172
	v_med3_f32 v112, v125, s46, v172
	v_cvt_pk_fp8_f32 v108, v111, v112 op_sel:[0,0,1]
	v_med3_f32 v110, v128, s46, v172
	v_med3_f32 v111, v129, s46, v172
	v_cvt_pk_fp8_f32 v109, v110, v111 op_sel:[0,0,1]
	v_lshlrev_b64 v[110:111], 10, v[152:153]
	v_lshl_add_u64 v[110:111], v[148:149], 0, v[110:111]
	global_store_dwordx2 v[110:111], v[106:107], off
	global_store_dwordx2 v[110:111], v[108:109], off offset:512

; DI unsigned pk4_fp8(float a, float b, float c, float d) { int r = 0; r = __builtin_amdgcn_cvt_pk_fp8_f32(a, b, r, false); r = __builtin_amdgcn_cvt_pk_fp8_f32(c, d, r, true); return (unsigned)r; }
; DI float clamp448(float x) { return __builtin_amdgcn_fmed3f(x, -448.0f, 448.0f); }
; DI float bflo(unsigned u) { return __uint_as_float(u << 16); }
; DI float bfhi(unsigned u) { return __uint_as_float(u & 0xffff0000u); }
; DI void phase_router(unsigned char* lds, const Params& P, int li, const bf16_t* X1, unsigned char* H8, const float* modl, unsigned* cnt, int* tok_e, int* tok_pos, float* tok_gate, int* tok_list, int G, int ntok, int chsz) {
;     ...
;                 if (tl < chsz) {
;                     const u32x4 a = ra[rr], b = rbv[rr];
;                     v[0] = (f32x4){bflo(a[0]), bfhi(a[0]), bflo(a[1]), bfhi(a[1])}; v[1] = (f32x4){bflo(a[2]), bfhi(a[2]), bflo(a[3]), bfhi(a[3])};
;                     v[2] = (f32x4){bflo(b[0]), bfhi(b[0]), bflo(b[1]), bfhi(b[1])}; v[3] = (f32x4){bflo(b[2]), bfhi(b[2]), bflo(b[3]), bfhi(b[3])};
;                     const int b9 = tok < NLAT ? (tok >> 12) : 8; if (b9 != cur_b9) load_mod(b9);
;                     float ss = 0.f;
; #pragma unroll
;                     for (int j = 0; j < 4; ++j)
; #pragma unroll
;                         for (int i = 0; i < 4; ++i) ss += v[j][i] * v[j][i];
;                     ss = wave_sum(ss);
;                     const float rinv = __builtin_amdgcn_rsqf(ss * (1.0f / 1024.0f) + EPS);
; #pragma unroll
;                     for (int j = 0; j < 4; ++j) v[j] = v[j] * rinv * ma[j] + mb[j];
;                     { unsigned char* hr = H8 + (size_t)tok * 1024; u32x2 w0, w1;
;                       w0.x = pk4_fp8(clamp448(v[0][0]), clamp448(v[0][1]), clamp448(v[0][2]), clamp448(v[0][3])); w0.y = pk4_fp8(clamp448(v[1][0]), clamp448(v[1][1]), clamp448(v[1][2]), clamp448(v[1][3]));
;                       w1.x = pk4_fp8(clamp448(v[2][0]), clamp448(v[2][1]), clamp448(v[2][2]), clamp448(v[2][3])); w1.y = pk4_fp8(clamp448(v[3][0]), clamp448(v[3][1]), clamp448(v[3][2]), clamp448(v[3][3]));
;                       *(u32x2*)(hr + 8 * lane) = w0; *(u32x2*)(hr + 512 + 8 * lane) = w1; } }
.LBB0_2196:
	s_or_b64 exec, exec, s[36:37]
	v_and_b32_e32 v115, 0xffff0000, v110
	v_lshlrev_b32_e32 v114, 16, v110
	v_mul_f32_e32 v120, v115, v115
	v_lshlrev_b32_e32 v110, 16, v111
	v_fmac_f32_e32 v120, v114, v114
	v_and_b32_e32 v111, 0xffff0000, v111
	v_fmac_f32_e32 v120, v110, v110
	v_lshlrev_b32_e32 v118, 16, v112
	v_fmac_f32_e32 v120, v111, v111
	v_and_b32_e32 v119, 0xffff0000, v112
	v_fmac_f32_e32 v120, v118, v118
	v_lshlrev_b32_e32 v112, 16, v113
	v_fmac_f32_e32 v120, v119, v119
	v_and_b32_e32 v113, 0xffff0000, v113
	v_fmac_f32_e32 v120, v112, v112
	v_lshlrev_b32_e32 v122, 16, v106
	v_fmac_f32_e32 v120, v113, v113
	v_and_b32_e32 v123, 0xffff0000, v106
	v_fmac_f32_e32 v120, v122, v122
	v_lshlrev_b32_e32 v106, 16, v107
	v_fmac_f32_e32 v120, v123, v123
	v_and_b32_e32 v107, 0xffff0000, v107
	v_fmac_f32_e32 v120, v106, v106
	v_lshlrev_b32_e32 v126, 16, v108
	v_fmac_f32_e32 v120, v107, v107
	v_and_b32_e32 v127, 0xffff0000, v108
	v_and_b32_e32 v108, 0xffff0000, v109
	v_lshlrev_b32_e32 v109, 16, v109
	v_fmac_f32_e32 v120, v126, v126
	v_fmac_f32_e32 v120, v127, v127
	v_pk_mul_f32 v[116:117], v[108:109], v[108:109]
	v_ashrrev_i32_e32 v153, 31, v152
	v_add_f32_e32 v117, v117, v120
	v_add_f32_e32 v116, v116, v117
	v_and_b32_e32 v117, 64, v171
	v_add_u32_e32 v117, 64, v117
	v_xor_b32_e32 v120, 32, v171
	v_cmp_lt_i32_e64 s[10:11], v120, v117
	s_nop 1
	v_cndmask_b32_e64 v120, v171, v120, s[10:11]
	v_lshlrev_b32_e32 v120, 2, v120
	ds_bpermute_b32 v120, v120, v116
	s_waitcnt lgkmcnt(0)
	v_add_f32_e32 v116, v116, v120
	v_xor_b32_e32 v120, 16, v171
	v_cmp_lt_i32_e64 s[10:11], v120, v117
	s_nop 1
	v_cndmask_b32_e64 v120, v171, v120, s[10:11]
	v_lshlrev_b32_e32 v120, 2, v120
	ds_bpermute_b32 v120, v120, v116
	s_waitcnt lgkmcnt(0)
	v_add_f32_e32 v116, v116, v120
	v_xor_b32_e32 v120, 8, v171
	v_cmp_lt_i32_e64 s[10:11], v120, v117
	s_nop 1
	v_cndmask_b32_e64 v120, v171, v120, s[10:11]
	v_lshlrev_b32_e32 v120, 2, v120
	ds_bpermute_b32 v120, v120, v116
	s_waitcnt lgkmcnt(0)
	v_add_f32_e32 v116, v116, v120
	v_xor_b32_e32 v120, 4, v171
	v_cmp_lt_i32_e64 s[10:11], v120, v117
	s_nop 1
	v_cndmask_b32_e64 v120, v171, v120, s[10:11]
	v_lshlrev_b32_e32 v120, 2, v120
	ds_bpermute_b32 v120, v120, v116
	s_waitcnt lgkmcnt(0)
	v_add_f32_e32 v116, v116, v120
	v_xor_b32_e32 v120, 2, v171
	v_cmp_lt_i32_e64 s[10:11], v120, v117
	s_nop 1
	v_cndmask_b32_e64 v120, v171, v120, s[10:11]
	v_lshlrev_b32_e32 v120, 2, v120
	ds_bpermute_b32 v120, v120, v116
	s_waitcnt lgkmcnt(0)
	v_add_f32_e32 v116, v116, v120
	v_xor_b32_e32 v120, 1, v171
	v_cmp_lt_i32_e64 s[10:11], v120, v117
	s_nop 1
	v_cndmask_b32_e64 v117, v171, v120, s[10:11]
	v_lshlrev_b32_e32 v117, 2, v117
	ds_bpermute_b32 v117, v117, v116
	s_waitcnt lgkmcnt(0)
	v_add_f32_e32 v116, v116, v117
	v_fmamk_f32 v116, v116, 0x3a800000, v168
	v_rsq_f32_e32 v128, v116
	s_nop 0
	v_pk_mul_f32 v[114:115], v[114:115], v[128:129] op_sel_hi:[1,0]
	v_pk_mul_f32 v[110:111], v[110:111], v[128:129] op_sel_hi:[1,0]
	v_pk_mul_f32 v[106:107], v[106:107], v[128:129] op_sel_hi:[1,0]
	s_waitcnt vmcnt(2)
	v_pk_fma_f32 v[116:117], v[84:85], v[110:111], v[72:73]
	v_pk_fma_f32 v[114:115], v[82:83], v[114:115], v[70:71]
	v_pk_mul_f32 v[110:111], v[118:119], v[128:129] op_sel_hi:[1,0]
	s_waitcnt vmcnt(0)
	v_pk_fma_f32 v[124:125], v[92:93], v[106:107], v[80:81]
	v_pk_mul_f32 v[106:107], v[126:127], v[128:129] op_sel_hi:[1,0]
	v_pk_mul_f32 v[108:109], v[108:109], v[128:129] op_sel:[1,0] op_sel_hi:[0,0]
	v_pk_mul_f32 v[112:113], v[112:113], v[128:129] op_sel_hi:[1,0]
	v_pk_fma_f32 v[118:119], v[86:87], v[110:111], v[66:67]
	v_pk_mul_f32 v[110:111], v[122:123], v[128:129] op_sel_hi:[1,0]
	v_pk_fma_f32 v[128:129], v[96:97], v[108:109], v[76:77]
	v_pk_fma_f32 v[126:127], v[94:95], v[106:107], v[74:75]
	v_med3_f32 v107, v114, s46, v172
	v_med3_f32 v108, v115, s46, v172
	s_nop 0
	v_pk_fma_f32 v[122:123], v[90:91], v[110:111], v[78:79]
	v_cvt_pk_fp8_f32 v106, v107, v108
	v_med3_f32 v108, v118, s46, v172
	v_med3_f32 v111, v119, s46, v172
	s_nop 0
	v_cvt_pk_fp8_f32 v107, v108, v111
	v_pk_fma_f32 v[120:121], v[88:89], v[112:113], v[68:69]
	v_med3_f32 v109, v116, s46, v172
	v_med3_f32 v110, v117, s46, v172
	v_cvt_pk_fp8_f32 v106, v109, v110 op_sel:[0,0,1]
	v_med3_f32 v108, v120, s46, v172
	v_med3_f32 v109, v121, s46, v172
	v_cvt_pk_fp8_f32 v107, v108, v109 op_sel:[0,0,1]
	v_med3_f32 v109, v122, s46, v172
	v_med3_f32 v110, v123, s46, v172
	s_nop 0
	v_cvt_pk_fp8_f32 v108, v109, v110
	v_med3_f32 v110, v126, s46, v172
	v_med3_f32 v113, v127, s46, v172
	s_nop 0
	v_cvt_pk_fp8_f32 v109, v110, v113
	v_med3_f32 v111, v124, s46, v172
	v_med3_f32 v112, v125, s46, v172
	v_cvt_pk_fp8_f32 v108, v111, v112 op_sel:[0,0,1]
	v_med3_f32 v110, v128, s46, v172
	v_med3_f32 v111, v129, s46, v172
	v_cvt_pk_fp8_f32 v109, v110, v111 op_sel:[0,0,1]
	v_lshlrev_b64 v[110:111], 10, v[152:153]
	v_lshl_add_u64 v[110:111], v[148:149], 0, v[110:111]
	global_store_dwordx2 v[110:111], v[106:107], off
	global_store_dwordx2 v[110:111], v[108:109], off offset:512

; DI unsigned pk4_fp8(float a, float b, float c, float d) { int r = 0; r = __builtin_amdgcn_cvt_pk_fp8_f32(a, b, r, false); r = __builtin_amdgcn_cvt_pk_fp8_f32(c, d, r, true); return (unsigned)r; }
; DI float clamp448(float x) { return __builtin_amdgcn_fmed3f(x, -448.0f, 448.0f); }
; DI float bflo(unsigned u) { return __uint_as_float(u << 16); }
; DI float bfhi(unsigned u) { return __uint_as_float(u & 0xffff0000u); }
; DI void phase_router(unsigned char* lds, const Params& P, int li, const bf16_t* X1, unsigned char* H8, const float* modl, unsigned* cnt, int* tok_e, int* tok_pos, float* tok_gate, int* tok_list, int G, int ntok, int chsz) {
;     ...
;                     const u32x4 a = ra[rr], b = rbv[rr];
;                     v[0] = (f32x4){bflo(a[0]), bfhi(a[0]), bflo(a[1]), bfhi(a[1])}; v[1] = (f32x4){bflo(a[2]), bfhi(a[2]), bflo(a[3]), bfhi(a[3])};
;                     v[2] = (f32x4){bflo(b[0]), bfhi(b[0]), bflo(b[1]), bfhi(b[1])}; v[3] = (f32x4){bflo(b[2]), bfhi(b[2]), bflo(b[3]), bfhi(b[3])};
;                     const int b9 = tok < NLAT ? (tok >> 12) : 8; if (b9 != cur_b9) load_mod(b9);
;                     float ss = 0.f;
; #pragma unroll
;                     for (int j = 0; j < 4; ++j)
; #pragma unroll
;                         for (int i = 0; i < 4; ++i) ss += v[j][i] * v[j][i];
;                     ss = wave_sum(ss);
;                     const float rinv = __builtin_amdgcn_rsqf(ss * (1.0f / 1024.0f) + EPS);
; #pragma unroll
;                     for (int j = 0; j < 4; ++j) v[j] = v[j] * rinv * ma[j] + mb[j];
;                     { unsigned char* hr = H8 + (size_t)tok * 1024; u32x2 w0, w1;
;                       w0.x = pk4_fp8(clamp448(v[0][0]), clamp448(v[0][1]), clamp448(v[0][2]), clamp448(v[0][3])); w0.y = pk4_fp8(clamp448(v[1][0]), clamp448(v[1][1]), clamp448(v[1][2]), clamp448(v[1][3]));
;                       w1.x = pk4_fp8(clamp448(v[2][0]), clamp448(v[2][1]), clamp448(v[2][2]), clamp448(v[2][3])); w1.y = pk4_fp8(clamp448(v[3][0]), clamp448(v[3][1]), clamp448(v[3][2]), clamp448(v[3][3]));
;                       *(u32x2*)(hr + 8 * lane) = w0; *(u32x2*)(hr + 512 + 8 * lane) = w1; } }
.LBB0_2200:
	s_or_b64 exec, exec, s[26:27]
	v_and_b32_e32 v107, 0xffff0000, v102
	v_lshlrev_b32_e32 v106, 16, v102
	v_mul_f32_e32 v112, v107, v107
	v_lshlrev_b32_e32 v102, 16, v103
	v_fmac_f32_e32 v112, v106, v106
	v_and_b32_e32 v103, 0xffff0000, v103
	v_fmac_f32_e32 v112, v102, v102
	v_lshlrev_b32_e32 v110, 16, v104
	v_fmac_f32_e32 v112, v103, v103
	v_and_b32_e32 v111, 0xffff0000, v104
	v_fmac_f32_e32 v112, v110, v110
	v_lshlrev_b32_e32 v104, 16, v105
	v_fmac_f32_e32 v112, v111, v111
	v_and_b32_e32 v105, 0xffff0000, v105
	v_fmac_f32_e32 v112, v104, v104
	v_lshlrev_b32_e32 v114, 16, v98
	v_fmac_f32_e32 v112, v105, v105
	v_and_b32_e32 v115, 0xffff0000, v98
	v_fmac_f32_e32 v112, v114, v114
	v_lshlrev_b32_e32 v98, 16, v99
	v_fmac_f32_e32 v112, v115, v115
	v_and_b32_e32 v99, 0xffff0000, v99
	v_fmac_f32_e32 v112, v98, v98
	v_lshlrev_b32_e32 v118, 16, v100
	v_fmac_f32_e32 v112, v99, v99
	v_and_b32_e32 v119, 0xffff0000, v100
	v_and_b32_e32 v100, 0xffff0000, v101
	v_lshlrev_b32_e32 v101, 16, v101
	v_fmac_f32_e32 v112, v118, v118
	v_fmac_f32_e32 v112, v119, v119
	v_pk_mul_f32 v[108:109], v[100:101], v[100:101]
	v_ashrrev_i32_e32 v123, 31, v122
	v_add_f32_e32 v109, v109, v112
	v_add_f32_e32 v108, v108, v109
	v_and_b32_e32 v109, 64, v171
	v_add_u32_e32 v109, 64, v109
	v_xor_b32_e32 v112, 32, v171
	v_cmp_lt_i32_e32 vcc, v112, v109
	s_nop 1
	v_cndmask_b32_e32 v112, v171, v112, vcc
	v_lshlrev_b32_e32 v112, 2, v112
	ds_bpermute_b32 v112, v112, v108
	s_waitcnt lgkmcnt(0)
	v_add_f32_e32 v108, v108, v112
	v_xor_b32_e32 v112, 16, v171
	v_cmp_lt_i32_e32 vcc, v112, v109
	s_nop 1
	v_cndmask_b32_e32 v112, v171, v112, vcc
	v_lshlrev_b32_e32 v112, 2, v112
	ds_bpermute_b32 v112, v112, v108
	s_waitcnt lgkmcnt(0)
	v_add_f32_e32 v108, v108, v112
	v_xor_b32_e32 v112, 8, v171
	v_cmp_lt_i32_e32 vcc, v112, v109
	s_nop 1
	v_cndmask_b32_e32 v112, v171, v112, vcc
	v_lshlrev_b32_e32 v112, 2, v112
	ds_bpermute_b32 v112, v112, v108
	s_waitcnt lgkmcnt(0)
	v_add_f32_e32 v108, v108, v112
	v_xor_b32_e32 v112, 4, v171
	v_cmp_lt_i32_e32 vcc, v112, v109
	s_nop 1
	v_cndmask_b32_e32 v112, v171, v112, vcc
	v_lshlrev_b32_e32 v112, 2, v112
	ds_bpermute_b32 v112, v112, v108
	s_waitcnt lgkmcnt(0)
	v_add_f32_e32 v108, v108, v112
	v_xor_b32_e32 v112, 2, v171
	v_cmp_lt_i32_e32 vcc, v112, v109
	s_nop 1
	v_cndmask_b32_e32 v112, v171, v112, vcc
	v_lshlrev_b32_e32 v112, 2, v112
	ds_bpermute_b32 v112, v112, v108
	s_waitcnt lgkmcnt(0)
	v_add_f32_e32 v108, v108, v112
	v_xor_b32_e32 v112, 1, v171
	v_cmp_lt_i32_e32 vcc, v112, v109
	s_nop 1
	v_cndmask_b32_e32 v109, v171, v112, vcc
	v_lshlrev_b32_e32 v109, 2, v109
	ds_bpermute_b32 v109, v109, v108
	s_waitcnt lgkmcnt(0)
	v_add_f32_e32 v108, v108, v109
	v_fmamk_f32 v108, v108, 0x3a800000, v168
	v_rsq_f32_e32 v120, v108
	s_nop 0
	v_pk_mul_f32 v[106:107], v[106:107], v[120:121] op_sel_hi:[1,0]
	v_pk_mul_f32 v[102:103], v[102:103], v[120:121] op_sel_hi:[1,0]
	v_pk_mul_f32 v[98:99], v[98:99], v[120:121] op_sel_hi:[1,0]
	s_waitcnt vmcnt(2)
	v_pk_fma_f32 v[108:109], v[84:85], v[102:103], v[72:73]
	v_pk_fma_f32 v[106:107], v[82:83], v[106:107], v[70:71]
	v_pk_mul_f32 v[102:103], v[110:111], v[120:121] op_sel_hi:[1,0]
	s_waitcnt vmcnt(0)
	v_pk_fma_f32 v[116:117], v[92:93], v[98:99], v[80:81]
	v_pk_mul_f32 v[98:99], v[118:119], v[120:121] op_sel_hi:[1,0]
	v_pk_mul_f32 v[100:101], v[100:101], v[120:121] op_sel:[1,0] op_sel_hi:[0,0]
	v_pk_mul_f32 v[104:105], v[104:105], v[120:121] op_sel_hi:[1,0]
	v_pk_fma_f32 v[110:111], v[86:87], v[102:103], v[66:67]
	v_pk_mul_f32 v[102:103], v[114:115], v[120:121] op_sel_hi:[1,0]
	v_pk_fma_f32 v[120:121], v[96:97], v[100:101], v[76:77]
	v_pk_fma_f32 v[118:119], v[94:95], v[98:99], v[74:75]
	v_med3_f32 v99, v106, s46, v172
	v_med3_f32 v100, v107, s46, v172
	s_nop 0
	v_pk_fma_f32 v[114:115], v[90:91], v[102:103], v[78:79]
	v_cvt_pk_fp8_f32 v98, v99, v100
	v_med3_f32 v100, v110, s46, v172
	v_med3_f32 v103, v111, s46, v172
	s_nop 0
	v_cvt_pk_fp8_f32 v99, v100, v103
	v_pk_fma_f32 v[112:113], v[88:89], v[104:105], v[68:69]
	v_med3_f32 v101, v108, s46, v172
	v_med3_f32 v102, v109, s46, v172
	v_cvt_pk_fp8_f32 v98, v101, v102 op_sel:[0,0,1]
	v_med3_f32 v100, v112, s46, v172
	v_med3_f32 v101, v113, s46, v172
	v_cvt_pk_fp8_f32 v99, v100, v101 op_sel:[0,0,1]
	v_med3_f32 v101, v114, s46, v172
	v_med3_f32 v102, v115, s46, v172
	s_nop 0
	v_cvt_pk_fp8_f32 v100, v101, v102
	v_med3_f32 v102, v118, s46, v172
	v_med3_f32 v105, v119, s46, v172
	s_nop 0
	v_cvt_pk_fp8_f32 v101, v102, v105
	v_med3_f32 v103, v116, s46, v172
	v_med3_f32 v104, v117, s46, v172
	v_cvt_pk_fp8_f32 v100, v103, v104 op_sel:[0,0,1]
	v_med3_f32 v102, v120, s46, v172
	v_med3_f32 v103, v121, s46, v172
	v_cvt_pk_fp8_f32 v101, v102, v103 op_sel:[0,0,1]
	v_lshlrev_b64 v[102:103], 10, v[122:123]
	v_lshl_add_u64 v[102:103], v[148:149], 0, v[102:103]
	global_store_dwordx2 v[102:103], v[98:99], off
	global_store_dwordx2 v[102:103], v[100:101], off offset:512

; DI KParamsPtr kparams() { KParamsPtr p = (KParamsPtr)__builtin_amdgcn_kernarg_segment_ptr(); asm volatile("" : "+s"(p)); return p; }
; DI unsigned pk4_fp8(float a, float b, float c, float d) { int r = 0; r = __builtin_amdgcn_cvt_pk_fp8_f32(a, b, r, false); r = __builtin_amdgcn_cvt_pk_fp8_f32(c, d, r, true); return (unsigned)r; }
;     DI void operator()(EPI_ARGS) const {
;     ...
;         unsigned char* ACT = WSB(unsigned char, WS_ACT);
;         const int rbase = u.pm * 256 + wr * 64 + fr, cbase = u.pn * 128 + 32 * wc + 8 * fq;
;         const float* bb = kparams()->b_gu + ((size_t)li * NE + u.e) * 2048 + cbase;
;         constexpr float CG = -1.702f * LOG2E;
;         f32x4 bg[2], bu1[2];
; #pragma unroll
;         for (int n = 0; n < 2; ++n) { bg[n] = *(const f32x4*)(bb + 4 * n) * CG; bu1[n] = (*(const f32x4*)(bb + 1024 + 4 * n) + 1.0f) * (1.0f / CG); }
; #pragma unroll
;         for (int ai = 0; ai < 2; ++ai)
; #pragma unroll
;             for (int m = 0; m < 4; ++m) {
;                 const int row = rbase + 128 * ai + 16 * m;
;                 f32x4 o[2];
; #pragma unroll
;                 for (int n = 0; n < 2; ++n) {
;                     const f32x4 gg = acc[ai][0][m][n] * (W8_INV * CG) + bg[n], uu = acc[ai][1][m][n] * (W8_INV / CG) + bu1[n];
;                     f32x4 gv, u1, e;
; #pragma unroll
;                     for (int i = 0; i < 4; ++i) { gv[i] = fmaxf(gg[i], 7.0f * CG); u1[i] = __builtin_amdgcn_fmed3f(uu[i], 8.0f / CG, -6.0f / CG); }
; #pragma unroll
;                     for (int i = 0; i < 4; ++i) e[i] = __builtin_amdgcn_exp2f(gv[i]);
;                     const f32x4 d = e + 1.0f;
;                     f32x4 r;
; #pragma unroll
;                     for (int i = 0; i < 4; ++i) r[i] = __builtin_amdgcn_rcpf(d[i]);
;                     o[n] = gv * u1 * r;
;                 }
;                 u32x2 w; w.x = pk4_fp8(o[0][0], o[0][1], o[0][2], o[0][3]); w.y = pk4_fp8(o[1][0], o[1][1], o[1][2], o[1][3]);
;                 *(u32x2*)(ACT + (size_t)row * 1024 + cbase) = w;
;             }
.LBB0_2549:
	v_mov_b32_e32 v2, v208
	v_mov_b32_e32 v16, v1
	s_mov_b64 s[44:45], s[0:1]
	s_load_dwordx2 s[44:45], s[44:45], 0xb8
	s_lshl_b32 s43, s43, 7
	s_or_b32 s43, s43, s29
	v_lshl_add_u32 v10, v2, 3, s43
	s_ashr_i32 s43, s42, 31
	s_lshl_b32 s12, s62, 8
	s_lshl_b64 s[42:43], s[42:43], 13
	s_waitcnt lgkmcnt(0)
	s_add_u32 s42, s44, s42
	s_addc_u32 s43, s45, s43
	v_ashrrev_i32_e32 v11, 31, v10
	v_lshl_add_u64 v[12:13], v[10:11], 2, s[42:43]
	v_add_co_u32_e32 v6, vcc, s70, v12
	v_lshl_add_u64 v[14:15], v[12:13], 0, s[24:25]
	s_nop 0
	v_addc_co_u32_e32 v7, vcc, 0, v13, vcc
	v_lshl_add_u64 v[12:13], v[12:13], 0, s[26:27]
	global_load_dwordx4 v[2:5], v[6:7], off offset:-4096
	s_nop 0
	global_load_dwordx4 v[6:9], v[6:7], off
	s_add_i32 s12, s12, s57
	global_load_dwordx4 v[18:21], v[14:15], off offset:16
	global_load_dwordx4 v[22:25], v[12:13], off offset:16
	v_add_u32_e32 v28, s12, v16
	s_nop 0
	v_lshl_add_u64 v[10:11], s[22:23], 0, v[10:11]
	s_waitcnt vmcnt(0)
	v_pk_mul_f32 v[12:13], v[4:5], s[36:37] op_sel_hi:[1,0]
	v_pk_mul_f32 v[16:17], v[2:3], s[36:37] op_sel_hi:[1,0]
	v_pk_add_f32 v[4:5], v[8:9], 1.0 op_sel_hi:[1,0]
	v_pk_add_f32 v[8:9], v[6:7], 1.0 op_sel_hi:[1,0]
	v_pk_mul_f32 v[2:3], v[20:21], s[36:37] op_sel_hi:[1,0]
	v_pk_mul_f32 v[6:7], v[18:19], s[36:37] op_sel_hi:[1,0]
	v_pk_add_f32 v[20:21], v[24:25], 1.0 op_sel_hi:[1,0]
	v_pk_mul_f32 v[14:15], v[4:5], s[38:39] op_sel_hi:[1,0]
	v_pk_mul_f32 v[4:5], v[20:21], s[38:39] op_sel_hi:[1,0]
	v_fmamk_f32 v20, v190, 0xbd1d265f, v16
	v_fmamk_f32 v21, v191, 0xbd1d265f, v17
	v_fmamk_f32 v24, v186, 0xbd1d265f, v6
	v_fmamk_f32 v25, v187, 0xbd1d265f, v7
	v_fmamk_f32 v27, v188, 0xbd1d265f, v2
	v_fmamk_f32 v29, v189, 0xbd1d265f, v3
	v_max_f32_e32 v20, 0xc1898193, v20
	v_max_f32_e32 v21, 0xc1898193, v21
	v_max_f32_e32 v24, 0xc1898193, v24
	v_max_f32_e32 v25, 0xc1898193, v25
	v_max_f32_e32 v30, 0xc1898193, v27
	v_fmamk_f32 v27, v180, 0xbbd083aa, v4
	v_max_f32_e32 v31, 0xc1898193, v29
	v_fmamk_f32 v29, v181, 0xbbd083aa, v5
	v_exp_f32_e32 v40, v20
	v_exp_f32_e32 v41, v21
	v_med3_f32 v38, v27, s71, v203
	v_med3_f32 v39, v29, s71, v203
	v_exp_f32_e32 v27, v24
	v_exp_f32_e32 v29, v25
	v_pk_add_f32 v[22:23], v[22:23], 1.0 op_sel_hi:[1,0]
	v_pk_mul_f32 v[18:19], v[8:9], s[38:39] op_sel_hi:[1,0]
	v_pk_mul_f32 v[8:9], v[22:23], s[38:39] op_sel_hi:[1,0]
	v_fmamk_f32 v22, v192, 0xbd1d265f, v12
	v_fmamk_f32 v23, v193, 0xbd1d265f, v13
	v_fmamk_f32 v32, v182, 0xbbd083aa, v18
	v_fmamk_f32 v33, v183, 0xbbd083aa, v19
	v_max_f32_e32 v22, 0xc1898193, v22
	v_max_f32_e32 v23, 0xc1898193, v23
	v_fmamk_f32 v36, v178, 0xbbd083aa, v8
	v_fmamk_f32 v37, v179, 0xbbd083aa, v9
	v_med3_f32 v32, v32, s71, v203
	v_med3_f32 v33, v33, s71, v203
	v_exp_f32_e32 v42, v22
	v_exp_f32_e32 v43, v23
	v_med3_f32 v36, v36, s71, v203
	v_med3_f32 v37, v37, s71, v203
	v_exp_f32_e32 v44, v30
	v_exp_f32_e32 v45, v31
	v_pk_mul_f32 v[20:21], v[20:21], v[32:33]
	v_add_f32_e32 v32, 1.0, v40
	v_add_f32_e32 v33, 1.0, v41
	v_add_f32_e32 v27, 1.0, v27
	v_add_f32_e32 v29, 1.0, v29
	v_pk_mul_f32 v[24:25], v[24:25], v[36:37]
	v_rcp_f32_e32 v32, v32
	v_rcp_f32_e32 v33, v33
	v_rcp_f32_e32 v36, v27
	v_rcp_f32_e32 v37, v29
	v_fmamk_f32 v34, v184, 0xbbd083aa, v14
	v_fmamk_f32 v35, v185, 0xbbd083aa, v15
	v_med3_f32 v34, v34, s71, v203
	v_med3_f32 v35, v35, s71, v203
	v_pk_mul_f32 v[22:23], v[22:23], v[34:35]
	v_add_f32_e32 v34, 1.0, v42
	v_add_f32_e32 v35, 1.0, v43
	v_add_f32_e32 v40, 1.0, v44
	v_add_f32_e32 v41, 1.0, v45
	v_rcp_f32_e32 v34, v34
	v_rcp_f32_e32 v35, v35
	v_rcp_f32_e32 v40, v40
	v_rcp_f32_e32 v41, v41
	v_pk_mul_f32 v[20:21], v[20:21], v[32:33]
	v_pk_mul_f32 v[24:25], v[24:25], v[36:37]
	s_nop 0
	v_cvt_pk_fp8_f32 v26, v20, v21
	v_cvt_pk_fp8_f32 v27, v24, v25
	v_pk_mul_f32 v[20:21], v[30:31], v[38:39]
	v_pk_mul_f32 v[22:23], v[22:23], v[34:35]
	v_pk_mul_f32 v[20:21], v[20:21], v[40:41]
	v_cvt_pk_fp8_f32 v26, v22, v23 op_sel:[0,0,1]
	v_cvt_pk_fp8_f32 v27, v20, v21 op_sel:[0,0,1]
	v_ashrrev_i32_e32 v29, 31, v28
	v_lshlrev_b64 v[20:21], 10, v[28:29]
	v_lshl_add_u64 v[10:11], v[10:11], 0, v[20:21]
	v_fmamk_f32 v25, v172, 0xbbd083aa, v14
	global_store_dwordx2 v[10:11], v[26:27], off
	v_fmamk_f32 v24, v176, 0xbd1d265f, v12
	v_med3_f32 v26, v25, s71, v203
	v_fmamk_f32 v25, v177, 0xbd1d265f, v13
	v_max_f32_e32 v24, 0xc1898193, v24
	v_max_f32_e32 v25, 0xc1898193, v25
	v_exp_f32_e32 v30, v24
	v_exp_f32_e32 v31, v25
	v_fmamk_f32 v21, v170, 0xbbd083aa, v18
	v_fmamk_f32 v20, v174, 0xbd1d265f, v16
	v_med3_f32 v22, v21, s71, v203
	v_fmamk_f32 v21, v175, 0xbd1d265f, v17
	v_max_f32_e32 v20, 0xc1898193, v20
	v_max_f32_e32 v21, 0xc1898193, v21
	v_exp_f32_e32 v28, v20
	v_exp_f32_e32 v29, v21
	v_add_f32_e32 v30, 1.0, v30
	v_add_f32_e32 v31, 1.0, v31
	v_rcp_f32_e32 v30, v30
	v_rcp_f32_e32 v31, v31
	v_fmamk_f32 v27, v173, 0xbbd083aa, v15
	v_fmamk_f32 v23, v171, 0xbbd083aa, v19
	v_med3_f32 v27, v27, s71, v203
	v_med3_f32 v23, v23, s71, v203
	v_add_f32_e32 v28, 1.0, v28
	v_add_f32_e32 v29, 1.0, v29
	v_pk_mul_f32 v[24:25], v[24:25], v[26:27]
	v_rcp_f32_e32 v28, v28
	v_rcp_f32_e32 v29, v29
	v_pk_mul_f32 v[20:21], v[20:21], v[22:23]
	v_pk_mul_f32 v[22:23], v[24:25], v[30:31]
	v_fmamk_f32 v25, v162, 0xbbd083aa, v8
	v_fmamk_f32 v24, v166, 0xbd1d265f, v6
	v_med3_f32 v26, v25, s71, v203
	v_fmamk_f32 v25, v167, 0xbd1d265f, v7
	v_max_f32_e32 v24, 0xc1898193, v24
	v_max_f32_e32 v25, 0xc1898193, v25
	v_exp_f32_e32 v32, v24
	v_exp_f32_e32 v33, v25
	v_pk_mul_f32 v[20:21], v[20:21], v[28:29]
	v_fmamk_f32 v29, v164, 0xbbd083aa, v4
	v_fmamk_f32 v28, v168, 0xbd1d265f, v2
	v_med3_f32 v30, v29, s71, v203
	v_fmamk_f32 v29, v169, 0xbd1d265f, v3
	v_max_f32_e32 v28, 0xc1898193, v28
; DI unsigned pk4_fp8(float a, float b, float c, float d) { int r = 0; r = __builtin_amdgcn_cvt_pk_fp8_f32(a, b, r, false); r = __builtin_amdgcn_cvt_pk_fp8_f32(c, d, r, true); return (unsigned)r; }
;     DI void operator()(EPI_ARGS) const {
;     ...
; #pragma unroll
;         for (int ai = 0; ai < 2; ++ai)
; #pragma unroll
;             for (int m = 0; m < 4; ++m) {
;                 const int row = rbase + 128 * ai + 16 * m;
;                 f32x4 o[2];
; #pragma unroll
;                 for (int n = 0; n < 2; ++n) {
;                     const f32x4 gg = acc[ai][0][m][n] * (W8_INV * CG) + bg[n], uu = acc[ai][1][m][n] * (W8_INV / CG) + bu1[n];
;                     f32x4 gv, u1, e;
; #pragma unroll
;                     for (int i = 0; i < 4; ++i) { gv[i] = fmaxf(gg[i], 7.0f * CG); u1[i] = __builtin_amdgcn_fmed3f(uu[i], 8.0f / CG, -6.0f / CG); }
; #pragma unroll
;                     for (int i = 0; i < 4; ++i) e[i] = __builtin_amdgcn_exp2f(gv[i]);
;                     const f32x4 d = e + 1.0f;
;                     f32x4 r;
; #pragma unroll
;                     for (int i = 0; i < 4; ++i) r[i] = __builtin_amdgcn_rcpf(d[i]);
;                     o[n] = gv * u1 * r;
;                 }
;                 u32x2 w; w.x = pk4_fp8(o[0][0], o[0][1], o[0][2], o[0][3]); w.y = pk4_fp8(o[1][0], o[1][1], o[1][2], o[1][3]);
;                 *(u32x2*)(ACT + (size_t)row * 1024 + cbase) = w;
;             }
	v_max_f32_e32 v29, 0xc1898193, v29
	v_exp_f32_e32 v34, v28
	v_exp_f32_e32 v35, v29
	v_add_f32_e32 v32, 1.0, v32
	v_add_f32_e32 v33, 1.0, v33
	v_rcp_f32_e32 v32, v32
	v_rcp_f32_e32 v33, v33
	v_fmamk_f32 v27, v163, 0xbbd083aa, v9
	v_med3_f32 v27, v27, s71, v203
	v_add_f32_e32 v34, 1.0, v34
	v_add_f32_e32 v35, 1.0, v35
	v_pk_mul_f32 v[24:25], v[24:25], v[26:27]
	v_rcp_f32_e32 v34, v34
	v_rcp_f32_e32 v35, v35
	v_pk_mul_f32 v[24:25], v[24:25], v[32:33]
	s_nop 0
	s_nop 0
	v_fmamk_f32 v31, v165, 0xbbd083aa, v5
	v_cvt_pk_fp8_f32 v26, v20, v21
	v_cvt_pk_fp8_f32 v27, v24, v25
	v_med3_f32 v31, v31, s71, v203
	v_pk_mul_f32 v[20:21], v[28:29], v[30:31]
	v_cvt_pk_fp8_f32 v26, v22, v23 op_sel:[0,0,1]
	v_pk_mul_f32 v[20:21], v[20:21], v[34:35]
	v_fmamk_f32 v25, v156, 0xbbd083aa, v14
	v_cvt_pk_fp8_f32 v27, v20, v21 op_sel:[0,0,1]
	v_add_co_u32_e32 v20, vcc, s56, v10
	v_fmamk_f32 v24, v160, 0xbd1d265f, v12
	s_nop 0
	v_addc_co_u32_e32 v21, vcc, 0, v11, vcc
	global_store_dwordx2 v[20:21], v[26:27], off
	v_med3_f32 v26, v25, s71, v203
	v_fmamk_f32 v25, v161, 0xbd1d265f, v13
	v_max_f32_e32 v24, 0xc1898193, v24
	v_max_f32_e32 v25, 0xc1898193, v25
	v_exp_f32_e32 v30, v24
	v_exp_f32_e32 v31, v25
	v_fmamk_f32 v21, v154, 0xbbd083aa, v18
	v_fmamk_f32 v20, v158, 0xbd1d265f, v16
	v_med3_f32 v22, v21, s71, v203
	v_fmamk_f32 v21, v159, 0xbd1d265f, v17
	v_max_f32_e32 v20, 0xc1898193, v20
	v_max_f32_e32 v21, 0xc1898193, v21
	v_exp_f32_e32 v28, v20
	v_exp_f32_e32 v29, v21
	v_add_f32_e32 v30, 1.0, v30
	v_add_f32_e32 v31, 1.0, v31
	v_rcp_f32_e32 v30, v30
	v_rcp_f32_e32 v31, v31
	v_fmamk_f32 v27, v157, 0xbbd083aa, v15
	v_fmamk_f32 v23, v155, 0xbbd083aa, v19
	v_med3_f32 v27, v27, s71, v203
	v_med3_f32 v23, v23, s71, v203
	v_add_f32_e32 v28, 1.0, v28
	v_add_f32_e32 v29, 1.0, v29
	v_pk_mul_f32 v[24:25], v[24:25], v[26:27]
	v_rcp_f32_e32 v28, v28
	v_rcp_f32_e32 v29, v29
	v_pk_mul_f32 v[20:21], v[20:21], v[22:23]
	v_pk_mul_f32 v[22:23], v[24:25], v[30:31]
	v_fmamk_f32 v25, v146, 0xbbd083aa, v8
	v_fmamk_f32 v24, v150, 0xbd1d265f, v6
	v_med3_f32 v26, v25, s71, v203
	v_fmamk_f32 v25, v151, 0xbd1d265f, v7
	v_max_f32_e32 v24, 0xc1898193, v24
	v_max_f32_e32 v25, 0xc1898193, v25
	v_exp_f32_e32 v32, v24
	v_exp_f32_e32 v33, v25
	v_pk_mul_f32 v[20:21], v[20:21], v[28:29]
	v_fmamk_f32 v29, v148, 0xbbd083aa, v4
	v_fmamk_f32 v28, v152, 0xbd1d265f, v2
	v_med3_f32 v30, v29, s71, v203
	v_fmamk_f32 v29, v153, 0xbd1d265f, v3
	v_max_f32_e32 v28, 0xc1898193, v28
	v_max_f32_e32 v29, 0xc1898193, v29
	v_exp_f32_e32 v34, v28
	v_exp_f32_e32 v35, v29
	v_add_f32_e32 v32, 1.0, v32
	v_add_f32_e32 v33, 1.0, v33
	v_rcp_f32_e32 v32, v32
	v_rcp_f32_e32 v33, v33
	v_fmamk_f32 v27, v147, 0xbbd083aa, v9
	v_med3_f32 v27, v27, s71, v203
	v_add_f32_e32 v34, 1.0, v34
	v_add_f32_e32 v35, 1.0, v35
	v_pk_mul_f32 v[24:25], v[24:25], v[26:27]
	v_rcp_f32_e32 v34, v34
	v_rcp_f32_e32 v35, v35
	v_pk_mul_f32 v[24:25], v[24:25], v[32:33]
	s_nop 0
	s_nop 0
	v_fmamk_f32 v31, v149, 0xbbd083aa, v5
	v_cvt_pk_fp8_f32 v26, v20, v21
	v_cvt_pk_fp8_f32 v27, v24, v25
	v_med3_f32 v31, v31, s71, v203
	v_pk_mul_f32 v[20:21], v[28:29], v[30:31]
	v_cvt_pk_fp8_f32 v26, v22, v23 op_sel:[0,0,1]
	v_pk_mul_f32 v[20:21], v[20:21], v[34:35]
	v_fmamk_f32 v25, v140, 0xbbd083aa, v14
	v_cvt_pk_fp8_f32 v27, v20, v21 op_sel:[0,0,1]
	v_add_co_u32_e32 v20, vcc, s66, v10
	v_fmamk_f32 v24, v144, 0xbd1d265f, v12
	s_nop 0
	v_addc_co_u32_e32 v21, vcc, 0, v11, vcc
	global_store_dwordx2 v[20:21], v[26:27], off
	v_med3_f32 v26, v25, s71, v203
	v_fmamk_f32 v25, v145, 0xbd1d265f, v13
	v_max_f32_e32 v24, 0xc1898193, v24
	v_max_f32_e32 v25, 0xc1898193, v25
	v_exp_f32_e32 v30, v24
	v_exp_f32_e32 v31, v25
	v_fmamk_f32 v21, v138, 0xbbd083aa, v18
	v_fmamk_f32 v20, v142, 0xbd1d265f, v16
	v_med3_f32 v22, v21, s71, v203
	v_fmamk_f32 v21, v143, 0xbd1d265f, v17
	v_max_f32_e32 v20, 0xc1898193, v20
	v_max_f32_e32 v21, 0xc1898193, v21
	v_exp_f32_e32 v28, v20
	v_exp_f32_e32 v29, v21
	v_add_f32_e32 v30, 1.0, v30
	v_add_f32_e32 v31, 1.0, v31
	v_rcp_f32_e32 v30, v30
	v_rcp_f32_e32 v31, v31
	v_fmamk_f32 v27, v141, 0xbbd083aa, v15
	v_fmamk_f32 v23, v139, 0xbbd083aa, v19
	v_med3_f32 v27, v27, s71, v203
	v_med3_f32 v23, v23, s71, v203
	v_add_f32_e32 v28, 1.0, v28
	v_add_f32_e32 v29, 1.0, v29
	v_pk_mul_f32 v[24:25], v[24:25], v[26:27]
	v_rcp_f32_e32 v28, v28
	v_rcp_f32_e32 v29, v29
	v_pk_mul_f32 v[20:21], v[20:21], v[22:23]
	v_pk_mul_f32 v[22:23], v[24:25], v[30:31]
	v_fmamk_f32 v25, v130, 0xbbd083aa, v8
	v_fmamk_f32 v24, v134, 0xbd1d265f, v6
	v_med3_f32 v26, v25, s71, v203
	v_fmamk_f32 v25, v135, 0xbd1d265f, v7
	v_max_f32_e32 v24, 0xc1898193, v24
	v_max_f32_e32 v25, 0xc1898193, v25
	v_exp_f32_e32 v32, v24
	v_exp_f32_e32 v33, v25
	v_pk_mul_f32 v[20:21], v[20:21], v[28:29]
	v_fmamk_f32 v29, v132, 0xbbd083aa, v4
	v_fmamk_f32 v28, v136, 0xbd1d265f, v2
	v_med3_f32 v30, v29, s71, v203
	v_fmamk_f32 v29, v137, 0xbd1d265f, v3
	v_max_f32_e32 v28, 0xc1898193, v28
	v_max_f32_e32 v29, 0xc1898193, v29
	v_exp_f32_e32 v34, v28
	v_exp_f32_e32 v35, v29
	v_add_f32_e32 v32, 1.0, v32
	v_add_f32_e32 v33, 1.0, v33
	v_rcp_f32_e32 v32, v32
	v_rcp_f32_e32 v33, v33
	v_fmamk_f32 v27, v131, 0xbbd083aa, v9
	v_med3_f32 v27, v27, s71, v203
	v_add_f32_e32 v34, 1.0, v34
	v_add_f32_e32 v35, 1.0, v35
	v_pk_mul_f32 v[24:25], v[24:25], v[26:27]
	v_rcp_f32_e32 v34, v34
	v_rcp_f32_e32 v35, v35
	v_pk_mul_f32 v[24:25], v[24:25], v[32:33]
	s_nop 0
	s_nop 0
	v_fmamk_f32 v31, v133, 0xbbd083aa, v5
	v_cvt_pk_fp8_f32 v26, v20, v21
	v_cvt_pk_fp8_f32 v27, v24, v25
	v_med3_f32 v31, v31, s71, v203
	v_pk_mul_f32 v[20:21], v[28:29], v[30:31]
	v_cvt_pk_fp8_f32 v26, v22, v23 op_sel:[0,0,1]
	v_pk_mul_f32 v[20:21], v[20:21], v[34:35]
; DI unsigned pk4_fp8(float a, float b, float c, float d) { int r = 0; r = __builtin_amdgcn_cvt_pk_fp8_f32(a, b, r, false); r = __builtin_amdgcn_cvt_pk_fp8_f32(c, d, r, true); return (unsigned)r; }
;     DI void operator()(EPI_ARGS) const {
;     ...
; #pragma unroll
;         for (int ai = 0; ai < 2; ++ai)
; #pragma unroll
;             for (int m = 0; m < 4; ++m) {
;                 const int row = rbase + 128 * ai + 16 * m;
;                 f32x4 o[2];
; #pragma unroll
;                 for (int n = 0; n < 2; ++n) {
;                     const f32x4 gg = acc[ai][0][m][n] * (W8_INV * CG) + bg[n], uu = acc[ai][1][m][n] * (W8_INV / CG) + bu1[n];
;                     f32x4 gv, u1, e;
; #pragma unroll
;                     for (int i = 0; i < 4; ++i) { gv[i] = fmaxf(gg[i], 7.0f * CG); u1[i] = __builtin_amdgcn_fmed3f(uu[i], 8.0f / CG, -6.0f / CG); }
; #pragma unroll
;                     for (int i = 0; i < 4; ++i) e[i] = __builtin_amdgcn_exp2f(gv[i]);
;                     const f32x4 d = e + 1.0f;
;                     f32x4 r;
; #pragma unroll
;                     for (int i = 0; i < 4; ++i) r[i] = __builtin_amdgcn_rcpf(d[i]);
;                     o[n] = gv * u1 * r;
;                 }
;                 u32x2 w; w.x = pk4_fp8(o[0][0], o[0][1], o[0][2], o[0][3]); w.y = pk4_fp8(o[1][0], o[1][1], o[1][2], o[1][3]);
;                 *(u32x2*)(ACT + (size_t)row * 1024 + cbase) = w;
;             }
	v_fmamk_f32 v25, v124, 0xbbd083aa, v14
	v_cvt_pk_fp8_f32 v27, v20, v21 op_sel:[0,0,1]
	v_add_co_u32_e32 v20, vcc, s69, v10
	v_fmamk_f32 v24, v128, 0xbd1d265f, v12
	s_nop 0
	v_addc_co_u32_e32 v21, vcc, 0, v11, vcc
	global_store_dwordx2 v[20:21], v[26:27], off
	v_med3_f32 v26, v25, s71, v203
	v_fmamk_f32 v25, v129, 0xbd1d265f, v13
	v_max_f32_e32 v24, 0xc1898193, v24
	v_max_f32_e32 v25, 0xc1898193, v25
	v_exp_f32_e32 v30, v24
	v_exp_f32_e32 v31, v25
	v_fmamk_f32 v21, v122, 0xbbd083aa, v18
	v_fmamk_f32 v20, v126, 0xbd1d265f, v16
	v_med3_f32 v22, v21, s71, v203
	v_fmamk_f32 v21, v127, 0xbd1d265f, v17
	v_max_f32_e32 v20, 0xc1898193, v20
	v_max_f32_e32 v21, 0xc1898193, v21
	v_exp_f32_e32 v28, v20
	v_exp_f32_e32 v29, v21
	v_add_f32_e32 v30, 1.0, v30
	v_add_f32_e32 v31, 1.0, v31
	v_rcp_f32_e32 v30, v30
	v_rcp_f32_e32 v31, v31
	v_fmamk_f32 v27, v125, 0xbbd083aa, v15
	v_fmamk_f32 v23, v123, 0xbbd083aa, v19
	v_med3_f32 v27, v27, s71, v203
	v_med3_f32 v23, v23, s71, v203
	v_add_f32_e32 v28, 1.0, v28
	v_add_f32_e32 v29, 1.0, v29
	v_pk_mul_f32 v[24:25], v[24:25], v[26:27]
	v_rcp_f32_e32 v28, v28
	v_rcp_f32_e32 v29, v29
	v_pk_mul_f32 v[20:21], v[20:21], v[22:23]
	v_pk_mul_f32 v[22:23], v[24:25], v[30:31]
	v_fmamk_f32 v25, v114, 0xbbd083aa, v8
	v_fmamk_f32 v24, v118, 0xbd1d265f, v6
	v_med3_f32 v26, v25, s71, v203
	v_fmamk_f32 v25, v119, 0xbd1d265f, v7
	v_max_f32_e32 v24, 0xc1898193, v24
	v_max_f32_e32 v25, 0xc1898193, v25
	v_exp_f32_e32 v32, v24
	v_exp_f32_e32 v33, v25
	v_pk_mul_f32 v[20:21], v[20:21], v[28:29]
	v_fmamk_f32 v29, v116, 0xbbd083aa, v4
	v_fmamk_f32 v28, v120, 0xbd1d265f, v2
	v_med3_f32 v30, v29, s71, v203
	v_fmamk_f32 v29, v121, 0xbd1d265f, v3
	v_max_f32_e32 v28, 0xc1898193, v28
	v_max_f32_e32 v29, 0xc1898193, v29
	v_exp_f32_e32 v34, v28
	v_exp_f32_e32 v35, v29
	v_add_f32_e32 v32, 1.0, v32
	v_add_f32_e32 v33, 1.0, v33
	v_rcp_f32_e32 v32, v32
	v_rcp_f32_e32 v33, v33
	v_fmamk_f32 v27, v115, 0xbbd083aa, v9
	v_med3_f32 v27, v27, s71, v203
	v_add_f32_e32 v34, 1.0, v34
	v_add_f32_e32 v35, 1.0, v35
	v_pk_mul_f32 v[24:25], v[24:25], v[26:27]
	v_rcp_f32_e32 v34, v34
	v_rcp_f32_e32 v35, v35
	v_pk_mul_f32 v[24:25], v[24:25], v[32:33]
	s_nop 0
	s_nop 0
	v_fmamk_f32 v31, v117, 0xbbd083aa, v5
	v_cvt_pk_fp8_f32 v26, v20, v21
	v_cvt_pk_fp8_f32 v27, v24, v25
	v_med3_f32 v31, v31, s71, v203
	v_pk_mul_f32 v[20:21], v[28:29], v[30:31]
	v_cvt_pk_fp8_f32 v26, v22, v23 op_sel:[0,0,1]
	v_pk_mul_f32 v[20:21], v[20:21], v[34:35]
	v_fmamk_f32 v25, v108, 0xbbd083aa, v14
	v_cvt_pk_fp8_f32 v27, v20, v21 op_sel:[0,0,1]
	v_add_co_u32_e32 v20, vcc, s55, v10
	v_fmamk_f32 v24, v112, 0xbd1d265f, v12
	s_nop 0
	v_addc_co_u32_e32 v21, vcc, 0, v11, vcc
	global_store_dwordx2 v[20:21], v[26:27], off
	v_med3_f32 v26, v25, s71, v203
	v_fmamk_f32 v25, v113, 0xbd1d265f, v13
	v_max_f32_e32 v24, 0xc1898193, v24
	v_max_f32_e32 v25, 0xc1898193, v25
	v_exp_f32_e32 v30, v24
	v_exp_f32_e32 v31, v25
	v_fmamk_f32 v21, v106, 0xbbd083aa, v18
	v_fmamk_f32 v20, v110, 0xbd1d265f, v16
	v_med3_f32 v22, v21, s71, v203
	v_fmamk_f32 v21, v111, 0xbd1d265f, v17
	v_max_f32_e32 v20, 0xc1898193, v20
	v_max_f32_e32 v21, 0xc1898193, v21
	v_exp_f32_e32 v28, v20
	v_exp_f32_e32 v29, v21
	v_add_f32_e32 v30, 1.0, v30
	v_add_f32_e32 v31, 1.0, v31
	v_rcp_f32_e32 v30, v30
	v_rcp_f32_e32 v31, v31
	v_fmamk_f32 v27, v109, 0xbbd083aa, v15
	v_fmamk_f32 v23, v107, 0xbbd083aa, v19
	v_med3_f32 v27, v27, s71, v203
	v_med3_f32 v23, v23, s71, v203
	v_add_f32_e32 v28, 1.0, v28
	v_add_f32_e32 v29, 1.0, v29
	v_pk_mul_f32 v[24:25], v[24:25], v[26:27]
	v_rcp_f32_e32 v28, v28
	v_rcp_f32_e32 v29, v29
	v_pk_mul_f32 v[20:21], v[20:21], v[22:23]
	v_pk_mul_f32 v[22:23], v[24:25], v[30:31]
	v_fmamk_f32 v25, v98, 0xbbd083aa, v8
	v_fmamk_f32 v24, v102, 0xbd1d265f, v6
	v_med3_f32 v26, v25, s71, v203
	v_fmamk_f32 v25, v103, 0xbd1d265f, v7
	v_max_f32_e32 v24, 0xc1898193, v24
	v_max_f32_e32 v25, 0xc1898193, v25
	v_exp_f32_e32 v32, v24
	v_exp_f32_e32 v33, v25
	v_pk_mul_f32 v[20:21], v[20:21], v[28:29]
	v_fmamk_f32 v29, v100, 0xbbd083aa, v4
	v_fmamk_f32 v28, v104, 0xbd1d265f, v2
	v_med3_f32 v30, v29, s71, v203
	v_fmamk_f32 v29, v105, 0xbd1d265f, v3
	v_max_f32_e32 v28, 0xc1898193, v28
	v_max_f32_e32 v29, 0xc1898193, v29
	v_exp_f32_e32 v34, v28
	v_exp_f32_e32 v35, v29
	v_add_f32_e32 v32, 1.0, v32
	v_add_f32_e32 v33, 1.0, v33
	v_rcp_f32_e32 v32, v32
	v_rcp_f32_e32 v33, v33
	v_fmamk_f32 v27, v99, 0xbbd083aa, v9
	v_med3_f32 v27, v27, s71, v203
	v_add_f32_e32 v34, 1.0, v34
	v_add_f32_e32 v35, 1.0, v35
	v_pk_mul_f32 v[24:25], v[24:25], v[26:27]
	v_rcp_f32_e32 v34, v34
	v_rcp_f32_e32 v35, v35
	v_pk_mul_f32 v[24:25], v[24:25], v[32:33]
	s_nop 0
	s_nop 0
	v_fmamk_f32 v31, v101, 0xbbd083aa, v5
	v_cvt_pk_fp8_f32 v26, v20, v21
	v_cvt_pk_fp8_f32 v27, v24, v25
	v_med3_f32 v31, v31, s71, v203
	v_pk_mul_f32 v[20:21], v[28:29], v[30:31]
	v_cvt_pk_fp8_f32 v26, v22, v23 op_sel:[0,0,1]
	v_pk_mul_f32 v[20:21], v[20:21], v[34:35]
	v_fmamk_f32 v25, v92, 0xbbd083aa, v14
	v_cvt_pk_fp8_f32 v27, v20, v21 op_sel:[0,0,1]
	v_add_co_u32_e32 v20, vcc, s72, v10
; DI unsigned pk4_fp8(float a, float b, float c, float d) { int r = 0; r = __builtin_amdgcn_cvt_pk_fp8_f32(a, b, r, false); r = __builtin_amdgcn_cvt_pk_fp8_f32(c, d, r, true); return (unsigned)r; }
; #define PG8_BAR __builtin_amdgcn_s_barrier()
; template <class Epi, class Sched, bool PERM, bool FP8 = false, bool GATHER = false>
; DI void gemm_phase(LAS unsigned char* lds, const unsigned char* wsb, const unsigned lda, const unsigned ldb, const int nt, const Sched& S, const Epi& E) {
;     ...
;         if (!has_next) break;
; #pragma unroll
;         for (int a = 0; a < 2; ++a)
; #pragma unroll
;             for (int b = 0; b < 2; ++b)
; #pragma unroll
;                 for (int m = 0; m < 4; ++m)
; #pragma unroll
;                     for (int n = 0; n < 2; ++n) acc[a][b][m][n] = (f32x4){0.f, 0.f, 0.f, 0.f};
;         cur = nxt; cA = nA; cB = nB; ++ui;
;         if (wr == 1) PG8_BAR;
;     DI void operator()(EPI_ARGS) const {
;     ...
; #pragma unroll
;         for (int ai = 0; ai < 2; ++ai)
; #pragma unroll
;             for (int m = 0; m < 4; ++m) {
;                 const int row = rbase + 128 * ai + 16 * m;
;                 f32x4 o[2];
; #pragma unroll
;                 for (int n = 0; n < 2; ++n) {
;                     const f32x4 gg = acc[ai][0][m][n] * (W8_INV * CG) + bg[n], uu = acc[ai][1][m][n] * (W8_INV / CG) + bu1[n];
;                     f32x4 gv, u1, e;
; #pragma unroll
;                     for (int i = 0; i < 4; ++i) { gv[i] = fmaxf(gg[i], 7.0f * CG); u1[i] = __builtin_amdgcn_fmed3f(uu[i], 8.0f / CG, -6.0f / CG); }
; #pragma unroll
;                     for (int i = 0; i < 4; ++i) e[i] = __builtin_amdgcn_exp2f(gv[i]);
;                     const f32x4 d = e + 1.0f;
;                     f32x4 r;
; #pragma unroll
;                     for (int i = 0; i < 4; ++i) r[i] = __builtin_amdgcn_rcpf(d[i]);
;                     o[n] = gv * u1 * r;
;                 }
;                 u32x2 w; w.x = pk4_fp8(o[0][0], o[0][1], o[0][2], o[0][3]); w.y = pk4_fp8(o[1][0], o[1][1], o[1][2], o[1][3]);
;                 *(u32x2*)(ACT + (size_t)row * 1024 + cbase) = w;
;             }
	v_fmamk_f32 v24, v96, 0xbd1d265f, v12
	s_nop 0
	v_addc_co_u32_e32 v21, vcc, 0, v11, vcc
	global_store_dwordx2 v[20:21], v[26:27], off
	v_med3_f32 v26, v25, s71, v203
	v_fmamk_f32 v25, v97, 0xbd1d265f, v13
	v_max_f32_e32 v24, 0xc1898193, v24
	v_max_f32_e32 v25, 0xc1898193, v25
	v_exp_f32_e32 v30, v24
	v_exp_f32_e32 v31, v25
	v_fmamk_f32 v21, v90, 0xbbd083aa, v18
	v_fmamk_f32 v20, v94, 0xbd1d265f, v16
	v_med3_f32 v22, v21, s71, v203
	v_fmamk_f32 v21, v95, 0xbd1d265f, v17
	v_max_f32_e32 v20, 0xc1898193, v20
	v_max_f32_e32 v21, 0xc1898193, v21
	v_exp_f32_e32 v28, v20
	v_exp_f32_e32 v29, v21
	v_add_f32_e32 v30, 1.0, v30
	v_add_f32_e32 v31, 1.0, v31
	v_rcp_f32_e32 v30, v30
	v_rcp_f32_e32 v31, v31
	v_fmamk_f32 v27, v93, 0xbbd083aa, v15
	v_fmamk_f32 v23, v91, 0xbbd083aa, v19
	v_med3_f32 v27, v27, s71, v203
	v_med3_f32 v23, v23, s71, v203
	v_add_f32_e32 v28, 1.0, v28
	v_add_f32_e32 v29, 1.0, v29
	v_pk_mul_f32 v[24:25], v[24:25], v[26:27]
	v_rcp_f32_e32 v28, v28
	v_rcp_f32_e32 v29, v29
	v_pk_mul_f32 v[20:21], v[20:21], v[22:23]
	v_pk_mul_f32 v[22:23], v[24:25], v[30:31]
	v_fmamk_f32 v25, v82, 0xbbd083aa, v8
	v_fmamk_f32 v24, v86, 0xbd1d265f, v6
	v_med3_f32 v26, v25, s71, v203
	v_fmamk_f32 v25, v87, 0xbd1d265f, v7
	v_max_f32_e32 v24, 0xc1898193, v24
	v_max_f32_e32 v25, 0xc1898193, v25
	v_exp_f32_e32 v32, v24
	v_exp_f32_e32 v33, v25
	v_pk_mul_f32 v[20:21], v[20:21], v[28:29]
	v_fmamk_f32 v29, v84, 0xbbd083aa, v4
	v_fmamk_f32 v28, v88, 0xbd1d265f, v2
	v_med3_f32 v30, v29, s71, v203
	v_fmamk_f32 v29, v89, 0xbd1d265f, v3
	v_max_f32_e32 v28, 0xc1898193, v28
	v_max_f32_e32 v29, 0xc1898193, v29
	v_exp_f32_e32 v34, v28
	v_exp_f32_e32 v35, v29
	v_add_f32_e32 v32, 1.0, v32
	v_add_f32_e32 v33, 1.0, v33
	v_rcp_f32_e32 v32, v32
	v_rcp_f32_e32 v33, v33
	v_fmamk_f32 v27, v83, 0xbbd083aa, v9
	v_med3_f32 v27, v27, s71, v203
	v_add_f32_e32 v34, 1.0, v34
	v_add_f32_e32 v35, 1.0, v35
	v_pk_mul_f32 v[24:25], v[24:25], v[26:27]
	v_rcp_f32_e32 v34, v34
	v_rcp_f32_e32 v35, v35
	v_pk_mul_f32 v[24:25], v[24:25], v[32:33]
	s_nop 0
	s_nop 0
	v_fmamk_f32 v31, v85, 0xbbd083aa, v5
	v_cvt_pk_fp8_f32 v26, v20, v21
	v_cvt_pk_fp8_f32 v27, v24, v25
	v_med3_f32 v31, v31, s71, v203
	v_pk_mul_f32 v[20:21], v[28:29], v[30:31]
	v_cvt_pk_fp8_f32 v26, v22, v23 op_sel:[0,0,1]
	v_pk_mul_f32 v[20:21], v[20:21], v[34:35]
	v_fmamk_f32 v16, v78, 0xbd1d265f, v16
	v_cvt_pk_fp8_f32 v27, v20, v21 op_sel:[0,0,1]
	v_add_co_u32_e32 v20, vcc, s73, v10
	v_fmamk_f32 v18, v74, 0xbbd083aa, v18
	v_fmac_f32_e32 v17, 0xbd1d265f, v79
	v_fmac_f32_e32 v19, 0xbbd083aa, v75
	v_fmamk_f32 v12, v80, 0xbd1d265f, v12
	v_fmamk_f32 v14, v76, 0xbbd083aa, v14
	v_fmac_f32_e32 v13, 0xbd1d265f, v81
	v_fmac_f32_e32 v15, 0xbbd083aa, v77
	v_fmamk_f32 v6, v70, 0xbd1d265f, v6
	v_fmac_f32_e32 v7, 0xbd1d265f, v71
	v_addc_co_u32_e32 v21, vcc, 0, v11, vcc
	v_max_f32_e32 v16, 0xc1898193, v16
	v_med3_f32 v18, v18, s71, v203
	v_max_f32_e32 v17, 0xc1898193, v17
	v_med3_f32 v19, v19, s71, v203
	v_max_f32_e32 v12, 0xc1898193, v12
	v_med3_f32 v14, v14, s71, v203
	v_max_f32_e32 v13, 0xc1898193, v13
	v_med3_f32 v15, v15, s71, v203
	v_max_f32_e32 v6, 0xc1898193, v6
	v_max_f32_e32 v7, 0xc1898193, v7
	global_store_dwordx2 v[20:21], v[26:27], off
	v_exp_f32_e32 v20, v16
	v_exp_f32_e32 v21, v17
	v_exp_f32_e32 v22, v12
	v_exp_f32_e32 v23, v13
	v_pk_mul_f32 v[12:13], v[12:13], v[14:15]
	v_pk_mul_f32 v[14:15], v[16:17], v[18:19]
	v_exp_f32_e32 v16, v6
	v_exp_f32_e32 v17, v7
	v_fmamk_f32 v2, v72, 0xbd1d265f, v2
	v_fmac_f32_e32 v3, 0xbd1d265f, v73
	v_max_f32_e32 v2, 0xc1898193, v2
	v_max_f32_e32 v3, 0xc1898193, v3
	v_add_f32_e32 v20, 1.0, v20
	v_add_f32_e32 v21, 1.0, v21
	v_exp_f32_e32 v18, v2
	v_exp_f32_e32 v19, v3
	v_add_f32_e32 v16, 1.0, v16
	v_add_f32_e32 v17, 1.0, v17
	v_rcp_f32_e32 v20, v20
	v_rcp_f32_e32 v21, v21
	v_rcp_f32_e32 v16, v16
	v_rcp_f32_e32 v17, v17
	v_fmamk_f32 v8, v66, 0xbbd083aa, v8
	v_fmac_f32_e32 v9, 0xbbd083aa, v67
	v_med3_f32 v8, v8, s71, v203
	v_med3_f32 v9, v9, s71, v203
	v_add_f32_e32 v22, 1.0, v22
	v_add_f32_e32 v23, 1.0, v23
	v_add_f32_e32 v18, 1.0, v18
	v_add_f32_e32 v19, 1.0, v19
	v_pk_mul_f32 v[6:7], v[6:7], v[8:9]
	v_rcp_f32_e32 v22, v22
	v_rcp_f32_e32 v23, v23
	v_pk_mul_f32 v[14:15], v[14:15], v[20:21]
	v_rcp_f32_e32 v18, v18
	v_rcp_f32_e32 v19, v19
	v_pk_mul_f32 v[6:7], v[6:7], v[16:17]
	s_nop 0
	s_nop 0
	v_fmamk_f32 v4, v68, 0xbbd083aa, v4
	v_fmac_f32_e32 v5, 0xbbd083aa, v69
	v_cvt_pk_fp8_f32 v8, v14, v15
	v_cvt_pk_fp8_f32 v9, v6, v7
	v_med3_f32 v4, v4, s71, v203
	v_med3_f32 v5, v5, s71, v203
	v_pk_mul_f32 v[2:3], v[2:3], v[4:5]
	v_pk_mul_f32 v[12:13], v[12:13], v[22:23]
	v_pk_mul_f32 v[2:3], v[2:3], v[18:19]
	v_cvt_pk_fp8_f32 v8, v12, v13 op_sel:[0,0,1]
	v_cvt_pk_fp8_f32 v9, v2, v3 op_sel:[0,0,1]
	v_add_co_u32_e32 v2, vcc, 0x2c000, v10
	s_nop 1
	v_addc_co_u32_e32 v3, vcc, 0, v11, vcc
	s_andn2_b64 vcc, exec, s[40:41]
	s_mov_b64 s[40:41], -1
	global_store_dwordx2 v[2:3], v[8:9], off
	s_cbranch_vccnz .LBB0_2535
	s_andn2_b64 vcc, exec, s[14:15]
	s_cbranch_vccnz .LBB0_2534
	s_barrier
	s_branch .LBB0_2534

; DI KParamsPtr kparams() { KParamsPtr p = (KParamsPtr)__builtin_amdgcn_kernarg_segment_ptr(); asm volatile("" : "+s"(p)); return p; }
; DI unsigned pk4_fp8(float a, float b, float c, float d) { int r = 0; r = __builtin_amdgcn_cvt_pk_fp8_f32(a, b, r, false); r = __builtin_amdgcn_cvt_pk_fp8_f32(c, d, r, true); return (unsigned)r; }
; DI float clamp448(float x) { return __builtin_amdgcn_fmed3f(x, -448.0f, 448.0f); }
;     DI void operator()(EPI_ARGS) const {
;     ...
;         unsigned char* YB = WSB(unsigned char, WS_XP) + (size_t)MAXMT * 256 * 1024;
;         const int rbase = u.pm * 256 + wr * 64 + fr, cbase = u.pn * 256 + 64 * wc + 16 * fq;
;         const float* bb = kparams()->b_dn + ((size_t)li * NE + u.e) * 1024 + cbase;
;         f32x4 bv[2][2];
; #pragma unroll
;         for (int bj = 0; bj < 2; ++bj)
; #pragma unroll
;             for (int n = 0; n < 2; ++n) bv[bj][n] = *(const f32x4*)(bb + 8 * bj + 4 * n);
; #pragma unroll
;         for (int ai = 0; ai < 2; ++ai)
; #pragma unroll
;             for (int m = 0; m < 4; ++m) {
;                 const int row = rbase + 128 * ai + 16 * m;
;                 u32x4 w;
; #pragma unroll
;                 for (int bj = 0; bj < 2; ++bj)
; #pragma unroll
;                     for (int n = 0; n < 2; ++n) { const f32x4 a = acc[ai][bj][m][n] * W8_INV + bv[bj][n]; w[2 * bj + n] = pk4_fp8(clamp448(a[0]), clamp448(a[1]), clamp448(a[2]), clamp448(a[3])); }
;                 *(u32x4*)(YB + (size_t)row * 1024 + cbase) = w;
;             }
.LBB0_2655:
	v_mov_b32_e32 v130, v152
	v_mov_b32_e32 v157, v1
	s_mov_b64 s[24:25], s[0:1]
	s_load_dwordx2 s[24:25], s[24:25], 0xc8
	s_lshl_b32 s23, s23, 8
	s_or_b32 s23, s23, s50
	v_lshl_add_u32 v150, v130, 4, s23
	s_ashr_i32 s23, s22, 31
	s_lshl_b32 s62, s63, 8
	s_lshl_b64 s[22:23], s[22:23], 12
	s_waitcnt lgkmcnt(0)
	s_add_u32 s22, s24, s22
	s_addc_u32 s23, s25, s23
	v_ashrrev_i32_e32 v151, 31, v150
	v_lshl_add_u64 v[130:131], v[150:151], 2, s[22:23]
	v_add_co_u32_e32 v132, vcc, s52, v130
	s_nop 0
	s_nop 0
	v_addc_co_u32_e32 v133, vcc, 0, v131, vcc
	v_lshl_add_u64 v[130:131], v[130:131], 0, s[16:17]
	global_load_dwordx4 v[142:145], v[132:133], off
	global_load_dwordx4 v[138:141], v[130:131], off offset:16
	global_load_dwordx4 v[134:137], v[130:131], off offset:32
	s_nop 0
	global_load_dwordx4 v[130:133], v[130:131], off offset:48
	s_nop 0
	s_nop 0
	s_nop 0
	s_add_i32 s62, s62, s42
	v_add_u32_e32 v166, s62, v157
	v_ashrrev_i32_e32 v167, 31, v166
	v_lshl_add_u64 v[150:151], s[14:15], 0, v[150:151]
	v_lshlrev_b64 v[166:167], 10, v[166:167]
	v_lshl_add_u64 v[150:151], v[150:151], 0, v[166:167]
	v_mov_b32_e32 v158, 0
	v_mov_b32_e32 v159, 0
	v_mov_b32_e32 v160, 0
	v_mov_b32_e32 v161, 0
	s_waitcnt vmcnt(0)
	v_pk_fma_f32 v[114:115], v[114:115], s[18:19], v[138:139] op_sel_hi:[1,0,1]
	v_pk_fma_f32 v[118:119], v[118:119], s[18:19], v[142:143] op_sel_hi:[1,0,1]
	v_pk_fma_f32 v[102:103], v[102:103], s[18:19], v[134:135] op_sel_hi:[1,0,1]
	v_pk_fma_f32 v[98:99], v[98:99], s[18:19], v[130:131] op_sel_hi:[1,0,1]
	v_med3_f32 v118, v118, s54, v156
	v_med3_f32 v119, v119, s54, v156
	v_med3_f32 v114, v114, s54, v156
	v_med3_f32 v115, v115, s54, v156
	v_med3_f32 v102, v102, s54, v156
	v_med3_f32 v103, v103, s54, v156
	v_med3_f32 v98, v98, s54, v156
	v_med3_f32 v99, v99, s54, v156
	v_cvt_pk_fp8_f32 v162, v118, v119
	v_cvt_pk_fp8_f32 v163, v114, v115
	v_cvt_pk_fp8_f32 v164, v102, v103
	v_cvt_pk_fp8_f32 v165, v98, v99
	v_pk_fma_f32 v[120:121], v[120:121], s[18:19], v[144:145] op_sel_hi:[1,0,1]
	v_pk_fma_f32 v[116:117], v[116:117], s[18:19], v[140:141] op_sel_hi:[1,0,1]
	v_pk_fma_f32 v[104:105], v[104:105], s[18:19], v[136:137] op_sel_hi:[1,0,1]
	v_pk_fma_f32 v[100:101], v[100:101], s[18:19], v[132:133] op_sel_hi:[1,0,1]
	v_med3_f32 v120, v120, s54, v156
	v_med3_f32 v121, v121, s54, v156
	v_med3_f32 v116, v116, s54, v156
	v_med3_f32 v117, v117, s54, v156
	v_med3_f32 v104, v104, s54, v156
	v_med3_f32 v105, v105, s54, v156
	v_med3_f32 v100, v100, s54, v156
	v_med3_f32 v98, v101, s54, v156
	v_cvt_pk_fp8_f32 v162, v120, v121 op_sel:[0,0,1]
	v_cvt_pk_fp8_f32 v163, v116, v117 op_sel:[0,0,1]
	v_cvt_pk_fp8_f32 v164, v104, v105 op_sel:[0,0,1]
	v_cvt_pk_fp8_f32 v165, v100, v98 op_sel:[0,0,1]
	v_add_co_u32_e32 v98, vcc, s41, v150
	v_pk_fma_f32 v[94:95], v[94:95], s[18:19], v[142:143] op_sel_hi:[1,0,1]
	s_nop 0
	v_addc_co_u32_e32 v99, vcc, 0, v151, vcc
	global_store_dwordx4 v[98:99], v[162:165], off
	v_med3_f32 v98, v94, s54, v156
	v_med3_f32 v95, v95, s54, v156
	s_nop 0
	v_cvt_pk_fp8_f32 v94, v98, v95
	v_pk_fma_f32 v[96:97], v[96:97], s[18:19], v[144:145] op_sel_hi:[1,0,1]
	v_pk_fma_f32 v[90:91], v[90:91], s[18:19], v[138:139] op_sel_hi:[1,0,1]
	v_med3_f32 v95, v96, s54, v156
	v_med3_f32 v96, v97, s54, v156
	v_pk_fma_f32 v[86:87], v[86:87], s[18:19], v[134:135] op_sel_hi:[1,0,1]
	v_pk_fma_f32 v[78:79], v[78:79], s[18:19], v[130:131] op_sel_hi:[1,0,1]
	v_cvt_pk_fp8_f32 v94, v95, v96 op_sel:[0,0,1]
	v_med3_f32 v90, v90, s54, v156
	v_med3_f32 v91, v91, s54, v156
	s_nop 0
	v_med3_f32 v86, v86, s54, v156
	v_med3_f32 v87, v87, s54, v156
	s_nop 0
	v_med3_f32 v78, v78, s54, v156
	v_med3_f32 v79, v79, s54, v156
	s_nop 0
	v_cvt_pk_fp8_f32 v95, v90, v91
	v_cvt_pk_fp8_f32 v96, v86, v87
	v_cvt_pk_fp8_f32 v97, v78, v79
	v_pk_fma_f32 v[90:91], v[92:93], s[18:19], v[140:141] op_sel_hi:[1,0,1]
	v_pk_fma_f32 v[86:87], v[88:89], s[18:19], v[136:137] op_sel_hi:[1,0,1]
	v_pk_fma_f32 v[78:79], v[80:81], s[18:19], v[132:133] op_sel_hi:[1,0,1]
	v_med3_f32 v90, v90, s54, v156
	v_med3_f32 v91, v91, s54, v156
	v_med3_f32 v86, v86, s54, v156
	v_med3_f32 v87, v87, s54, v156
	v_med3_f32 v78, v78, s54, v156
	v_med3_f32 v79, v79, s54, v156
	v_cvt_pk_fp8_f32 v95, v90, v91 op_sel:[0,0,1]
	v_cvt_pk_fp8_f32 v96, v86, v87 op_sel:[0,0,1]
	v_cvt_pk_fp8_f32 v97, v78, v79 op_sel:[0,0,1]
	v_add_co_u32_e32 v78, vcc, s49, v150
	v_pk_fma_f32 v[74:75], v[74:75], s[18:19], v[138:139] op_sel_hi:[1,0,1]
	s_nop 0
	v_addc_co_u32_e32 v79, vcc, 0, v151, vcc
	global_store_dwordx4 v[78:79], v[94:97], off
	v_pk_fma_f32 v[78:79], v[82:83], s[18:19], v[142:143] op_sel_hi:[1,0,1]
	v_pk_fma_f32 v[70:71], v[70:71], s[18:19], v[134:135] op_sel_hi:[1,0,1]
	v_med3_f32 v80, v78, s54, v156
	v_med3_f32 v79, v79, s54, v156
	s_nop 0
	v_cvt_pk_fp8_f32 v78, v80, v79
	v_pk_fma_f32 v[80:81], v[84:85], s[18:19], v[144:145] op_sel_hi:[1,0,1]
	v_pk_fma_f32 v[66:67], v[66:67], s[18:19], v[130:131] op_sel_hi:[1,0,1]
	v_med3_f32 v79, v80, s54, v156
	v_med3_f32 v80, v81, s54, v156
	v_cvt_pk_fp8_f32 v78, v79, v80 op_sel:[0,0,1]
	v_med3_f32 v74, v74, s54, v156
	v_med3_f32 v75, v75, s54, v156
	s_nop 0
	v_med3_f32 v70, v70, s54, v156
	v_med3_f32 v71, v71, s54, v156
	s_nop 0
	v_med3_f32 v66, v66, s54, v156
	v_med3_f32 v67, v67, s54, v156
	s_nop 0
	v_cvt_pk_fp8_f32 v79, v74, v75
	v_cvt_pk_fp8_f32 v80, v70, v71
	v_cvt_pk_fp8_f32 v81, v66, v67
	v_pk_fma_f32 v[74:75], v[76:77], s[18:19], v[140:141] op_sel_hi:[1,0,1]
	v_pk_fma_f32 v[70:71], v[72:73], s[18:19], v[136:137] op_sel_hi:[1,0,1]
	v_pk_fma_f32 v[66:67], v[68:69], s[18:19], v[132:133] op_sel_hi:[1,0,1]
	v_med3_f32 v74, v74, s54, v156
	v_med3_f32 v75, v75, s54, v156
	v_med3_f32 v70, v70, s54, v156
; DI unsigned pk4_fp8(float a, float b, float c, float d) { int r = 0; r = __builtin_amdgcn_cvt_pk_fp8_f32(a, b, r, false); r = __builtin_amdgcn_cvt_pk_fp8_f32(c, d, r, true); return (unsigned)r; }
; DI float clamp448(float x) { return __builtin_amdgcn_fmed3f(x, -448.0f, 448.0f); }
;     DI void operator()(EPI_ARGS) const {
;     ...
; #pragma unroll
;         for (int ai = 0; ai < 2; ++ai)
; #pragma unroll
;             for (int m = 0; m < 4; ++m) {
;                 const int row = rbase + 128 * ai + 16 * m;
;                 u32x4 w;
; #pragma unroll
;                 for (int bj = 0; bj < 2; ++bj)
; #pragma unroll
;                     for (int n = 0; n < 2; ++n) { const f32x4 a = acc[ai][bj][m][n] * W8_INV + bv[bj][n]; w[2 * bj + n] = pk4_fp8(clamp448(a[0]), clamp448(a[1]), clamp448(a[2]), clamp448(a[3])); }
;                 *(u32x4*)(YB + (size_t)row * 1024 + cbase) = w;
;             }
	v_med3_f32 v71, v71, s54, v156
	v_med3_f32 v66, v66, s54, v156
	v_med3_f32 v67, v67, s54, v156
	v_cvt_pk_fp8_f32 v79, v74, v75 op_sel:[0,0,1]
	v_cvt_pk_fp8_f32 v80, v70, v71 op_sel:[0,0,1]
	v_cvt_pk_fp8_f32 v81, v66, v67 op_sel:[0,0,1]
	v_add_co_u32_e32 v66, vcc, s53, v150
	v_pk_fma_f32 v[62:63], v[62:63], s[18:19], v[142:143] op_sel_hi:[1,0,1]
	s_nop 0
	v_addc_co_u32_e32 v67, vcc, 0, v151, vcc
	global_store_dwordx4 v[66:67], v[78:81], off
	v_med3_f32 v66, v62, s54, v156
	v_med3_f32 v63, v63, s54, v156
	s_nop 0
	v_cvt_pk_fp8_f32 v62, v66, v63
	v_pk_fma_f32 v[64:65], v[64:65], s[18:19], v[144:145] op_sel_hi:[1,0,1]
	v_pk_fma_f32 v[58:59], v[58:59], s[18:19], v[138:139] op_sel_hi:[1,0,1]
	v_med3_f32 v63, v64, s54, v156
	v_med3_f32 v64, v65, s54, v156
	v_pk_fma_f32 v[54:55], v[54:55], s[18:19], v[134:135] op_sel_hi:[1,0,1]
	v_pk_fma_f32 v[46:47], v[46:47], s[18:19], v[130:131] op_sel_hi:[1,0,1]
	v_cvt_pk_fp8_f32 v62, v63, v64 op_sel:[0,0,1]
	v_med3_f32 v58, v58, s54, v156
	v_med3_f32 v59, v59, s54, v156
	s_nop 0
	v_med3_f32 v54, v54, s54, v156
	v_med3_f32 v55, v55, s54, v156
	s_nop 0
	v_med3_f32 v46, v46, s54, v156
	v_med3_f32 v47, v47, s54, v156
	s_nop 0
	v_cvt_pk_fp8_f32 v63, v58, v59
	v_cvt_pk_fp8_f32 v64, v54, v55
	v_cvt_pk_fp8_f32 v65, v46, v47
	v_pk_fma_f32 v[58:59], v[60:61], s[18:19], v[140:141] op_sel_hi:[1,0,1]
	v_pk_fma_f32 v[54:55], v[56:57], s[18:19], v[136:137] op_sel_hi:[1,0,1]
	v_pk_fma_f32 v[46:47], v[48:49], s[18:19], v[132:133] op_sel_hi:[1,0,1]
	v_med3_f32 v58, v58, s54, v156
	v_med3_f32 v59, v59, s54, v156
	v_med3_f32 v54, v54, s54, v156
	v_med3_f32 v55, v55, s54, v156
	v_med3_f32 v46, v46, s54, v156
	v_med3_f32 v47, v47, s54, v156
	v_cvt_pk_fp8_f32 v63, v58, v59 op_sel:[0,0,1]
	v_cvt_pk_fp8_f32 v64, v54, v55 op_sel:[0,0,1]
	v_cvt_pk_fp8_f32 v65, v46, v47 op_sel:[0,0,1]
	v_add_co_u32_e32 v46, vcc, s52, v150
	v_pk_fma_f32 v[42:43], v[42:43], s[18:19], v[138:139] op_sel_hi:[1,0,1]
	s_nop 0
	v_addc_co_u32_e32 v47, vcc, 0, v151, vcc
	global_store_dwordx4 v[46:47], v[62:65], off
	v_pk_fma_f32 v[46:47], v[50:51], s[18:19], v[142:143] op_sel_hi:[1,0,1]
	v_pk_fma_f32 v[38:39], v[38:39], s[18:19], v[134:135] op_sel_hi:[1,0,1]
	v_med3_f32 v48, v46, s54, v156
	v_med3_f32 v47, v47, s54, v156
	s_nop 0
	v_cvt_pk_fp8_f32 v46, v48, v47
	v_pk_fma_f32 v[48:49], v[52:53], s[18:19], v[144:145] op_sel_hi:[1,0,1]
	v_pk_fma_f32 v[30:31], v[30:31], s[18:19], v[130:131] op_sel_hi:[1,0,1]
	v_med3_f32 v47, v48, s54, v156
	v_med3_f32 v48, v49, s54, v156
	v_cvt_pk_fp8_f32 v46, v47, v48 op_sel:[0,0,1]
	v_med3_f32 v42, v42, s54, v156
	v_med3_f32 v43, v43, s54, v156
	s_nop 0
	v_med3_f32 v38, v38, s54, v156
	v_med3_f32 v39, v39, s54, v156
	s_nop 0
	v_med3_f32 v30, v30, s54, v156
	v_med3_f32 v31, v31, s54, v156
	s_nop 0
	v_cvt_pk_fp8_f32 v47, v42, v43
	v_cvt_pk_fp8_f32 v48, v38, v39
	v_cvt_pk_fp8_f32 v49, v30, v31
	v_pk_fma_f32 v[42:43], v[44:45], s[18:19], v[140:141] op_sel_hi:[1,0,1]
	v_pk_fma_f32 v[38:39], v[40:41], s[18:19], v[136:137] op_sel_hi:[1,0,1]
	v_pk_fma_f32 v[30:31], v[32:33], s[18:19], v[132:133] op_sel_hi:[1,0,1]
	v_med3_f32 v42, v42, s54, v156
	v_med3_f32 v43, v43, s54, v156
	v_med3_f32 v38, v38, s54, v156
	v_med3_f32 v39, v39, s54, v156
	v_med3_f32 v30, v30, s54, v156
	v_med3_f32 v31, v31, s54, v156
	v_cvt_pk_fp8_f32 v47, v42, v43 op_sel:[0,0,1]
	v_cvt_pk_fp8_f32 v48, v38, v39 op_sel:[0,0,1]
	v_cvt_pk_fp8_f32 v49, v30, v31 op_sel:[0,0,1]
	v_add_co_u32_e32 v30, vcc, s55, v150
	v_pk_fma_f32 v[26:27], v[26:27], s[18:19], v[138:139] op_sel_hi:[1,0,1]
	s_nop 0
	v_addc_co_u32_e32 v31, vcc, 0, v151, vcc
	global_store_dwordx4 v[30:31], v[46:49], off
	v_pk_fma_f32 v[30:31], v[34:35], s[18:19], v[142:143] op_sel_hi:[1,0,1]
	v_pk_fma_f32 v[22:23], v[22:23], s[18:19], v[134:135] op_sel_hi:[1,0,1]
	v_med3_f32 v32, v30, s54, v156
	v_med3_f32 v31, v31, s54, v156
	s_nop 0
	v_cvt_pk_fp8_f32 v30, v32, v31
	v_pk_fma_f32 v[32:33], v[36:37], s[18:19], v[144:145] op_sel_hi:[1,0,1]
	v_pk_fma_f32 v[14:15], v[14:15], s[18:19], v[130:131] op_sel_hi:[1,0,1]
	v_med3_f32 v31, v32, s54, v156
	v_med3_f32 v32, v33, s54, v156
	v_cvt_pk_fp8_f32 v30, v31, v32 op_sel:[0,0,1]
	v_med3_f32 v26, v26, s54, v156
	v_med3_f32 v27, v27, s54, v156
	s_nop 0
; DI unsigned pk4_fp8(float a, float b, float c, float d) { int r = 0; r = __builtin_amdgcn_cvt_pk_fp8_f32(a, b, r, false); r = __builtin_amdgcn_cvt_pk_fp8_f32(c, d, r, true); return (unsigned)r; }
; DI float clamp448(float x) { return __builtin_amdgcn_fmed3f(x, -448.0f, 448.0f); }
; #define PG8_BAR __builtin_amdgcn_s_barrier()
; template <class Epi, class Sched, bool PERM, bool FP8 = false, bool GATHER = false>
; DI void gemm_phase(LAS unsigned char* lds, const unsigned char* wsb, const unsigned lda, const unsigned ldb, const int nt, const Sched& S, const Epi& E) {
;     ...
;         if (!has_next) break;
; #pragma unroll
;         for (int a = 0; a < 2; ++a)
; #pragma unroll
;             for (int b = 0; b < 2; ++b)
; #pragma unroll
;                 for (int m = 0; m < 4; ++m)
; #pragma unroll
;                     for (int n = 0; n < 2; ++n) acc[a][b][m][n] = (f32x4){0.f, 0.f, 0.f, 0.f};
;         cur = nxt; cA = nA; cB = nB; ++ui;
;         if (wr == 1) PG8_BAR;
;     DI void operator()(EPI_ARGS) const {
;     ...
; #pragma unroll
;         for (int ai = 0; ai < 2; ++ai)
; #pragma unroll
;             for (int m = 0; m < 4; ++m) {
;                 const int row = rbase + 128 * ai + 16 * m;
;                 u32x4 w;
; #pragma unroll
;                 for (int bj = 0; bj < 2; ++bj)
; #pragma unroll
;                     for (int n = 0; n < 2; ++n) { const f32x4 a = acc[ai][bj][m][n] * W8_INV + bv[bj][n]; w[2 * bj + n] = pk4_fp8(clamp448(a[0]), clamp448(a[1]), clamp448(a[2]), clamp448(a[3])); }
;                 *(u32x4*)(YB + (size_t)row * 1024 + cbase) = w;
;             }
	v_med3_f32 v22, v22, s54, v156
	v_med3_f32 v23, v23, s54, v156
	s_nop 0
	v_med3_f32 v14, v14, s54, v156
	v_med3_f32 v15, v15, s54, v156
	s_nop 0
	v_cvt_pk_fp8_f32 v31, v26, v27
	v_cvt_pk_fp8_f32 v32, v22, v23
	v_cvt_pk_fp8_f32 v33, v14, v15
	v_pk_fma_f32 v[26:27], v[28:29], s[18:19], v[140:141] op_sel_hi:[1,0,1]
	v_pk_fma_f32 v[22:23], v[24:25], s[18:19], v[136:137] op_sel_hi:[1,0,1]
	v_pk_fma_f32 v[14:15], v[16:17], s[18:19], v[132:133] op_sel_hi:[1,0,1]
	v_med3_f32 v26, v26, s54, v156
	v_med3_f32 v27, v27, s54, v156
	v_med3_f32 v22, v22, s54, v156
	v_med3_f32 v23, v23, s54, v156
	v_med3_f32 v14, v14, s54, v156
	v_med3_f32 v15, v15, s54, v156
	v_cvt_pk_fp8_f32 v31, v26, v27 op_sel:[0,0,1]
	v_cvt_pk_fp8_f32 v32, v22, v23 op_sel:[0,0,1]
	v_cvt_pk_fp8_f32 v33, v14, v15 op_sel:[0,0,1]
	v_add_co_u32_e32 v14, vcc, s56, v150
	v_pk_fma_f32 v[126:127], v[126:127], s[18:19], v[142:143] op_sel_hi:[1,0,1]
	s_nop 0
	v_addc_co_u32_e32 v15, vcc, 0, v151, vcc
	global_store_dwordx4 v[14:15], v[30:33], off
	v_pk_fma_f32 v[14:15], v[18:19], s[18:19], v[142:143] op_sel_hi:[1,0,1]
	v_pk_fma_f32 v[122:123], v[122:123], s[18:19], v[138:139] op_sel_hi:[1,0,1]
	v_med3_f32 v16, v14, s54, v156
	v_med3_f32 v15, v15, s54, v156
	s_nop 0
	v_cvt_pk_fp8_f32 v14, v16, v15
	v_pk_fma_f32 v[16:17], v[20:21], s[18:19], v[144:145] op_sel_hi:[1,0,1]
	v_pk_fma_f32 v[110:111], v[110:111], s[18:19], v[134:135] op_sel_hi:[1,0,1]
	v_pk_fma_f32 v[106:107], v[106:107], s[18:19], v[130:131] op_sel_hi:[1,0,1]
	v_med3_f32 v15, v16, s54, v156
	v_med3_f32 v16, v17, s54, v156
	v_pk_fma_f32 v[10:11], v[10:11], s[18:19], v[138:139] op_sel_hi:[1,0,1]
	v_pk_fma_f32 v[6:7], v[6:7], s[18:19], v[134:135] op_sel_hi:[1,0,1]
	v_pk_fma_f32 v[2:3], v[2:3], s[18:19], v[130:131] op_sel_hi:[1,0,1]
	v_med3_f32 v126, v126, s54, v156
	v_med3_f32 v127, v127, s54, v156
	v_med3_f32 v122, v122, s54, v156
	v_med3_f32 v123, v123, s54, v156
	v_med3_f32 v110, v110, s54, v156
	v_med3_f32 v111, v111, s54, v156
	v_med3_f32 v106, v106, s54, v156
	v_med3_f32 v107, v107, s54, v156
	v_cvt_pk_fp8_f32 v14, v15, v16 op_sel:[0,0,1]
	v_med3_f32 v10, v10, s54, v156
	v_med3_f32 v11, v11, s54, v156
	s_nop 0
	v_med3_f32 v6, v6, s54, v156
	v_med3_f32 v7, v7, s54, v156
	s_nop 0
	v_med3_f32 v2, v2, s54, v156
	v_med3_f32 v3, v3, s54, v156
	s_nop 0
	v_cvt_pk_fp8_f32 v158, v126, v127
	v_cvt_pk_fp8_f32 v159, v122, v123
	v_cvt_pk_fp8_f32 v160, v110, v111
	v_cvt_pk_fp8_f32 v161, v106, v107
	v_cvt_pk_fp8_f32 v15, v10, v11
	v_cvt_pk_fp8_f32 v16, v6, v7
	v_cvt_pk_fp8_f32 v17, v2, v3
	v_pk_fma_f32 v[128:129], v[128:129], s[18:19], v[144:145] op_sel_hi:[1,0,1]
	v_pk_fma_f32 v[124:125], v[124:125], s[18:19], v[140:141] op_sel_hi:[1,0,1]
	v_pk_fma_f32 v[112:113], v[112:113], s[18:19], v[136:137] op_sel_hi:[1,0,1]
	v_pk_fma_f32 v[108:109], v[108:109], s[18:19], v[132:133] op_sel_hi:[1,0,1]
	v_pk_fma_f32 v[10:11], v[12:13], s[18:19], v[140:141] op_sel_hi:[1,0,1]
	v_pk_fma_f32 v[6:7], v[8:9], s[18:19], v[136:137] op_sel_hi:[1,0,1]
	v_pk_fma_f32 v[2:3], v[4:5], s[18:19], v[132:133] op_sel_hi:[1,0,1]
	v_med3_f32 v128, v128, s54, v156
	v_med3_f32 v129, v129, s54, v156
	v_med3_f32 v124, v124, s54, v156
	v_med3_f32 v125, v125, s54, v156
	v_med3_f32 v112, v112, s54, v156
	v_med3_f32 v113, v113, s54, v156
	v_med3_f32 v108, v108, s54, v156
	v_med3_f32 v109, v109, s54, v156
	v_med3_f32 v10, v10, s54, v156
	v_med3_f32 v11, v11, s54, v156
	v_med3_f32 v6, v6, s54, v156
	v_med3_f32 v7, v7, s54, v156
	v_med3_f32 v2, v2, s54, v156
	v_med3_f32 v3, v3, s54, v156
	v_cvt_pk_fp8_f32 v158, v128, v129 op_sel:[0,0,1]
	v_cvt_pk_fp8_f32 v159, v124, v125 op_sel:[0,0,1]
	v_cvt_pk_fp8_f32 v160, v112, v113 op_sel:[0,0,1]
	v_cvt_pk_fp8_f32 v161, v108, v109 op_sel:[0,0,1]
	v_cvt_pk_fp8_f32 v15, v10, v11 op_sel:[0,0,1]
	v_cvt_pk_fp8_f32 v16, v6, v7 op_sel:[0,0,1]
	v_cvt_pk_fp8_f32 v17, v2, v3 op_sel:[0,0,1]
	v_add_co_u32_e32 v2, vcc, 0x2c000, v150
	global_store_dwordx4 v[150:151], v[158:161], off
	s_nop 0
	v_addc_co_u32_e32 v3, vcc, 0, v151, vcc
	s_andn2_b64 vcc, exec, s[20:21]
	s_mov_b64 s[20:21], -1
	global_store_dwordx4 v[2:3], v[14:17], off
	s_cbranch_vccnz .LBB0_2642
	s_andn2_b64 vcc, exec, s[10:11]
	s_cbranch_vccnz .LBB0_2641
	s_barrier
	s_branch .LBB0_2641
